# speedup vs baseline: 1.0047x; 1.0047x over previous
.LBB3_5:
	s_waitcnt lgkmcnt(0)
	v_cvt_f16_f32_e32 v180, s7
	v_cvt_f16_f32_e32 v182, s6
	v_cvt_f16_f32_e32 v181, s28
	s_waitcnt vmcnt(18)
	v_pk_mul_f16 v183, v182, v184 op_sel_hi:[0,1]
	v_pk_mul_f16 v190, v182, v187 op_sel_hi:[0,1]
	v_pk_mul_f16 v194, v180, v187 op_sel_hi:[0,1]
	v_pk_mul_f16 v198, v181, v187 op_sel_hi:[0,1]
	v_pk_mul_f16 v188, v182, v185 op_sel_hi:[0,1]
	v_pk_mul_f16 v189, v182, v186 op_sel_hi:[0,1]
	v_pk_mul_f16 v191, v180, v184 op_sel_hi:[0,1]
	v_pk_mul_f16 v192, v180, v185 op_sel_hi:[0,1]
	v_pk_mul_f16 v193, v180, v186 op_sel_hi:[0,1]
	v_pk_mul_f16 v195, v181, v184 op_sel_hi:[0,1]
	v_pk_mul_f16 v196, v181, v185 op_sel_hi:[0,1]
	v_pk_mul_f16 v197, v181, v186 op_sel_hi:[0,1]
	v_pk_fma_f16 v113, v113, v187, v190
	v_pk_fma_f16 v110, v110, v184, v183
	v_pk_fma_f16 v129, v129, v187, v190
	v_pk_fma_f16 v126, v126, v184, v183
	v_pk_fma_f16 v141, v141, v187, v190
	v_pk_fma_f16 v138, v138, v184, v183
	v_pk_fma_f16 v183, v89, v187, v194
	v_pk_fma_f16 v199, v109, v187, v194
	v_pk_fma_f16 v194, v125, v187, v194
	v_pk_fma_f16 v203, v53, v187, v198
	v_pk_fma_f16 v207, v69, v187, v198
	v_pk_fma_f16 v187, v97, v187, v198
	v_pk_maximum3_f16 v198, v113, v129, v141
	v_pk_fma_f16 v112, v112, v186, v189
	v_pk_fma_f16 v111, v111, v185, v188
	v_pk_fma_f16 v128, v128, v186, v189
	v_pk_fma_f16 v127, v127, v185, v188
	v_pk_fma_f16 v140, v140, v186, v189
	v_pk_fma_f16 v139, v139, v185, v188
	v_pk_fma_f16 v188, v88, v186, v193
	v_pk_fma_f16 v189, v87, v185, v192
	v_pk_fma_f16 v190, v86, v184, v191
	v_pk_fma_f16 v200, v108, v186, v193
	v_pk_fma_f16 v201, v107, v185, v192
	v_pk_fma_f16 v202, v106, v184, v191
	v_pk_fma_f16 v193, v124, v186, v193
	v_pk_fma_f16 v192, v123, v185, v192
	v_pk_fma_f16 v191, v122, v184, v191
	v_pk_fma_f16 v204, v52, v186, v197
	v_pk_fma_f16 v205, v51, v185, v196
	v_pk_fma_f16 v206, v50, v184, v195
	v_pk_fma_f16 v208, v68, v186, v197
	v_pk_fma_f16 v209, v67, v185, v196
	v_pk_fma_f16 v210, v66, v184, v195
	v_pk_fma_f16 v186, v96, v186, v197
	v_pk_fma_f16 v185, v95, v185, v196
	v_pk_fma_f16 v184, v94, v184, v195
	v_pk_maximum3_f16 v195, v110, v126, v138
	v_pk_maximum3_f16 v196, v111, v127, v139
	v_pk_maximum3_f16 v197, v112, v128, v140
	v_pk_maximum3_f16 v214, v183, v199, v194
	v_pk_maximum3_f16 v218, v203, v207, v187
	v_pk_maximum3_f16 v211, v190, v202, v191
	v_pk_maximum3_f16 v212, v189, v201, v192
	v_pk_maximum3_f16 v213, v188, v200, v193
	s_nop 0
	v_pk_maximum3_f16 v215, v206, v210, v184
	v_pk_maximum3_f16 v216, v205, v209, v185
	v_pk_maximum3_f16 v198, v198, v214, v218
	v_pk_maximum3_f16 v217, v204, v208, v186
	s_nop 0
	v_pk_maximum3_f16 v195, v195, v211, v215
	v_pk_maximum3_f16 v196, v196, v212, v216
	v_pk_maximum3_f16 v197, v197, v213, v217
	v_xor_b32_e32 v198, 0x80008000, v198
	v_xor_b32_e32 v197, 0x80008000, v197
	v_xor_b32_e32 v196, 0x80008000, v196
	v_xor_b32_e32 v195, 0x80008000, v195
	v_pk_add_f16 v113, v113, v198
	v_pk_add_f16 v110, v110, v195
	v_pk_add_f16 v111, v111, v196
	v_pk_add_f16 v112, v112, v197
	v_pk_add_f16 v126, v126, v195
	v_exp_f16_sdwa v211, v110 dst_sel:WORD_0 dst_unused:UNUSED_PAD src0_sel:WORD_0
	v_exp_f16_sdwa v212, v111 dst_sel:WORD_0 dst_unused:UNUSED_PAD src0_sel:WORD_0
	v_exp_f16_sdwa v213, v112 dst_sel:WORD_0 dst_unused:UNUSED_PAD src0_sel:WORD_0
	v_exp_f16_sdwa v214, v113 dst_sel:WORD_0 dst_unused:UNUSED_PAD src0_sel:WORD_0
	v_exp_f16_sdwa v211, v110 dst_sel:WORD_1 dst_unused:UNUSED_PRESERVE src0_sel:WORD_1
	v_exp_f16_sdwa v212, v111 dst_sel:WORD_1 dst_unused:UNUSED_PRESERVE src0_sel:WORD_1
	v_exp_f16_sdwa v213, v112 dst_sel:WORD_1 dst_unused:UNUSED_PRESERVE src0_sel:WORD_1
	v_exp_f16_sdwa v214, v113 dst_sel:WORD_1 dst_unused:UNUSED_PRESERVE src0_sel:WORD_1
	s_nop 0
	v_pk_add_f16 v127, v127, v196
	v_pk_add_f16 v113, v211, 0
	v_pk_fma_f16 v81, v81, v214, 0
	v_pk_add_f16 v110, v214, 0
	v_pk_add_f16 v111, v213, 0
	v_pk_add_f16 v112, v212, 0
	v_pk_fma_f16 v80, v80, v213, 0
	v_pk_fma_f16 v79, v79, v212, 0
	v_pk_fma_f16 v78, v78, v211, 0
	v_pk_add_f16 v128, v128, v197
	v_pk_add_f16 v129, v129, v198
	s_nop 0
	v_exp_f16_sdwa v211, v126 dst_sel:WORD_0 dst_unused:UNUSED_PAD src0_sel:WORD_0
	v_exp_f16_sdwa v212, v127 dst_sel:WORD_0 dst_unused:UNUSED_PAD src0_sel:WORD_0
	v_exp_f16_sdwa v213, v128 dst_sel:WORD_0 dst_unused:UNUSED_PAD src0_sel:WORD_0
	v_exp_f16_sdwa v214, v129 dst_sel:WORD_0 dst_unused:UNUSED_PAD src0_sel:WORD_0
	v_exp_f16_sdwa v211, v126 dst_sel:WORD_1 dst_unused:UNUSED_PRESERVE src0_sel:WORD_1
	v_exp_f16_sdwa v212, v127 dst_sel:WORD_1 dst_unused:UNUSED_PRESERVE src0_sel:WORD_1
	v_exp_f16_sdwa v213, v128 dst_sel:WORD_1 dst_unused:UNUSED_PRESERVE src0_sel:WORD_1
	v_exp_f16_sdwa v214, v129 dst_sel:WORD_1 dst_unused:UNUSED_PRESERVE src0_sel:WORD_1
	s_nop 0
	s_nop 0
	v_pk_add_f16 v113, v113, v211
	v_pk_fma_f16 v81, v105, v214, v81
	v_pk_add_f16 v105, v141, v198
	v_pk_add_f16 v112, v112, v212
	v_pk_add_f16 v111, v111, v213
	v_pk_add_f16 v110, v110, v214
	v_pk_fma_f16 v78, v102, v211, v78
	v_pk_fma_f16 v79, v103, v212, v79
	v_pk_fma_f16 v80, v104, v213, v80
	v_pk_add_f16 v102, v138, v195
	v_pk_add_f16 v103, v139, v196
	v_pk_add_f16 v104, v140, v197
	s_nop 0
	v_exp_f16_sdwa v126, v102 dst_sel:WORD_0 dst_unused:UNUSED_PAD src0_sel:WORD_0
	v_exp_f16_sdwa v127, v103 dst_sel:WORD_0 dst_unused:UNUSED_PAD src0_sel:WORD_0
	v_exp_f16_sdwa v128, v104 dst_sel:WORD_0 dst_unused:UNUSED_PAD src0_sel:WORD_0
	v_exp_f16_sdwa v129, v105 dst_sel:WORD_0 dst_unused:UNUSED_PAD src0_sel:WORD_0
	v_exp_f16_sdwa v126, v102 dst_sel:WORD_1 dst_unused:UNUSED_PRESERVE src0_sel:WORD_1
	v_exp_f16_sdwa v127, v103 dst_sel:WORD_1 dst_unused:UNUSED_PRESERVE src0_sel:WORD_1
	v_exp_f16_sdwa v128, v104 dst_sel:WORD_1 dst_unused:UNUSED_PRESERVE src0_sel:WORD_1
	v_exp_f16_sdwa v129, v105 dst_sel:WORD_1 dst_unused:UNUSED_PRESERVE src0_sel:WORD_1
	s_nop 0
	s_nop 0
	v_pk_add_f16 v105, v113, v126
	v_pk_add_f16 v102, v110, v129
	v_pk_add_f16 v103, v111, v128
	v_pk_add_f16 v104, v112, v127
	v_pk_fma_f16 v81, v121, v129, v81
	v_pk_fma_f16 v80, v120, v128, v80
	v_pk_fma_f16 v79, v119, v127, v79
	v_pk_fma_f16 v78, v118, v126, v78
	v_pk_add_f16 v110, v190, v195
	v_pk_add_f16 v111, v189, v196
	v_pk_add_f16 v112, v188, v197
	v_pk_add_f16 v113, v183, v198
	s_nop 0
	v_exp_f16_sdwa v118, v110 dst_sel:WORD_0 dst_unused:UNUSED_PAD src0_sel:WORD_0
	v_exp_f16_sdwa v119, v111 dst_sel:WORD_0 dst_unused:UNUSED_PAD src0_sel:WORD_0
	v_exp_f16_sdwa v120, v112 dst_sel:WORD_0 dst_unused:UNUSED_PAD src0_sel:WORD_0
	v_exp_f16_sdwa v121, v113 dst_sel:WORD_0 dst_unused:UNUSED_PAD src0_sel:WORD_0
	v_exp_f16_sdwa v118, v110 dst_sel:WORD_1 dst_unused:UNUSED_PRESERVE src0_sel:WORD_1
	v_exp_f16_sdwa v119, v111 dst_sel:WORD_1 dst_unused:UNUSED_PRESERVE src0_sel:WORD_1
	v_exp_f16_sdwa v120, v112 dst_sel:WORD_1 dst_unused:UNUSED_PRESERVE src0_sel:WORD_1
	v_exp_f16_sdwa v121, v113 dst_sel:WORD_1 dst_unused:UNUSED_PRESERVE src0_sel:WORD_1
	s_nop 0
	v_pk_add_f16 v110, v202, v195
	v_pk_add_f16 v105, v105, v118
	v_pk_add_f16 v104, v104, v119
	v_pk_add_f16 v103, v103, v120
	v_pk_add_f16 v102, v102, v121
	v_pk_fma_f16 v78, v46, v118, v78
	v_pk_fma_f16 v79, v47, v119, v79
	v_pk_fma_f16 v80, v48, v120, v80
	v_pk_fma_f16 v81, v49, v121, v81
	v_pk_add_f16 v111, v201, v196
	v_pk_add_f16 v112, v200, v197
	v_pk_add_f16 v113, v199, v198
	s_nop 0
	v_exp_f16_sdwa v118, v110 dst_sel:WORD_0 dst_unused:UNUSED_PAD src0_sel:WORD_0
	v_exp_f16_sdwa v119, v111 dst_sel:WORD_0 dst_unused:UNUSED_PAD src0_sel:WORD_0
	v_exp_f16_sdwa v120, v112 dst_sel:WORD_0 dst_unused:UNUSED_PAD src0_sel:WORD_0
	v_exp_f16_sdwa v121, v113 dst_sel:WORD_0 dst_unused:UNUSED_PAD src0_sel:WORD_0
	v_exp_f16_sdwa v118, v110 dst_sel:WORD_1 dst_unused:UNUSED_PRESERVE src0_sel:WORD_1
	v_exp_f16_sdwa v119, v111 dst_sel:WORD_1 dst_unused:UNUSED_PRESERVE src0_sel:WORD_1
	v_exp_f16_sdwa v120, v112 dst_sel:WORD_1 dst_unused:UNUSED_PRESERVE src0_sel:WORD_1
	v_exp_f16_sdwa v121, v113 dst_sel:WORD_1 dst_unused:UNUSED_PRESERVE src0_sel:WORD_1
	s_nop 0
	v_pk_add_f16 v110, v191, v195
	v_pk_add_f16 v105, v105, v118
	v_pk_add_f16 v102, v102, v121
	v_pk_add_f16 v103, v103, v120
	v_pk_add_f16 v104, v104, v119
	v_pk_fma_f16 v81, v65, v121, v81
	v_pk_fma_f16 v80, v64, v120, v80
	v_pk_fma_f16 v79, v63, v119, v79
	v_pk_fma_f16 v78, v62, v118, v78
	v_pk_add_f16 v111, v192, v196
	v_pk_add_f16 v112, v193, v197
	v_pk_add_f16 v113, v194, v198
	s_nop 0
	v_exp_f16_sdwa v118, v110 dst_sel:WORD_0 dst_unused:UNUSED_PAD src0_sel:WORD_0
	v_exp_f16_sdwa v119, v111 dst_sel:WORD_0 dst_unused:UNUSED_PAD src0_sel:WORD_0
	v_exp_f16_sdwa v120, v112 dst_sel:WORD_0 dst_unused:UNUSED_PAD src0_sel:WORD_0
	v_exp_f16_sdwa v121, v113 dst_sel:WORD_0 dst_unused:UNUSED_PAD src0_sel:WORD_0
	v_exp_f16_sdwa v118, v110 dst_sel:WORD_1 dst_unused:UNUSED_PRESERVE src0_sel:WORD_1
	v_exp_f16_sdwa v119, v111 dst_sel:WORD_1 dst_unused:UNUSED_PRESERVE src0_sel:WORD_1
	v_exp_f16_sdwa v120, v112 dst_sel:WORD_1 dst_unused:UNUSED_PRESERVE src0_sel:WORD_1
	v_exp_f16_sdwa v121, v113 dst_sel:WORD_1 dst_unused:UNUSED_PRESERVE src0_sel:WORD_1
	s_nop 0
	v_pk_add_f16 v110, v206, v195
	v_pk_add_f16 v105, v105, v118
	v_pk_add_f16 v104, v104, v119
	v_pk_add_f16 v103, v103, v120
	v_pk_add_f16 v102, v102, v121
	v_pk_fma_f16 v78, v82, v118, v78
	v_pk_fma_f16 v79, v83, v119, v79
	v_pk_fma_f16 v80, v84, v120, v80
	v_pk_fma_f16 v81, v85, v121, v81
	v_pk_add_f16 v111, v205, v196
	v_pk_add_f16 v112, v204, v197
	v_pk_add_f16 v113, v203, v198
	s_nop 0
	v_exp_f16_sdwa v118, v110 dst_sel:WORD_0 dst_unused:UNUSED_PAD src0_sel:WORD_0
	v_exp_f16_sdwa v119, v111 dst_sel:WORD_0 dst_unused:UNUSED_PAD src0_sel:WORD_0
	v_exp_f16_sdwa v120, v112 dst_sel:WORD_0 dst_unused:UNUSED_PAD src0_sel:WORD_0
	v_exp_f16_sdwa v121, v113 dst_sel:WORD_0 dst_unused:UNUSED_PAD src0_sel:WORD_0
	v_exp_f16_sdwa v118, v110 dst_sel:WORD_1 dst_unused:UNUSED_PRESERVE src0_sel:WORD_1
	v_exp_f16_sdwa v119, v111 dst_sel:WORD_1 dst_unused:UNUSED_PRESERVE src0_sel:WORD_1
	v_exp_f16_sdwa v120, v112 dst_sel:WORD_1 dst_unused:UNUSED_PRESERVE src0_sel:WORD_1
	v_exp_f16_sdwa v121, v113 dst_sel:WORD_1 dst_unused:UNUSED_PRESERVE src0_sel:WORD_1
	s_nop 0
	v_pk_add_f16 v110, v210, v195
	v_pk_add_f16 v105, v105, v118
	v_pk_add_f16 v102, v102, v121
	v_pk_add_f16 v103, v103, v120
	v_pk_add_f16 v104, v104, v119
	v_pk_fma_f16 v81, v25, v121, v81
	v_pk_fma_f16 v80, v24, v120, v80
	v_pk_fma_f16 v79, v23, v119, v79
	v_pk_fma_f16 v78, v22, v118, v78
	v_pk_add_f16 v111, v209, v196
	v_pk_add_f16 v112, v208, v197
	v_pk_add_f16 v113, v207, v198
	s_nop 0
	v_exp_f16_sdwa v118, v110 dst_sel:WORD_0 dst_unused:UNUSED_PAD src0_sel:WORD_0
	v_exp_f16_sdwa v119, v111 dst_sel:WORD_0 dst_unused:UNUSED_PAD src0_sel:WORD_0
	v_exp_f16_sdwa v120, v112 dst_sel:WORD_0 dst_unused:UNUSED_PAD src0_sel:WORD_0
	v_exp_f16_sdwa v121, v113 dst_sel:WORD_0 dst_unused:UNUSED_PAD src0_sel:WORD_0
	v_exp_f16_sdwa v118, v110 dst_sel:WORD_1 dst_unused:UNUSED_PRESERVE src0_sel:WORD_1
	v_exp_f16_sdwa v119, v111 dst_sel:WORD_1 dst_unused:UNUSED_PRESERVE src0_sel:WORD_1
	v_exp_f16_sdwa v120, v112 dst_sel:WORD_1 dst_unused:UNUSED_PRESERVE src0_sel:WORD_1
	v_exp_f16_sdwa v121, v113 dst_sel:WORD_1 dst_unused:UNUSED_PRESERVE src0_sel:WORD_1
	s_nop 0
	v_pk_add_f16 v110, v184, v195
	v_pk_add_f16 v105, v105, v118
	v_pk_add_f16 v104, v104, v119
	v_pk_add_f16 v103, v103, v120
	v_pk_add_f16 v102, v102, v121
	v_pk_fma_f16 v78, v34, v118, v78
	v_pk_fma_f16 v79, v35, v119, v79
	v_pk_fma_f16 v80, v36, v120, v80
	v_pk_fma_f16 v81, v37, v121, v81
	v_pk_add_f16 v111, v185, v196
	v_pk_add_f16 v112, v186, v197
	v_pk_add_f16 v113, v187, v198
	s_nop 0
	v_exp_f16_sdwa v118, v110 dst_sel:WORD_0 dst_unused:UNUSED_PAD src0_sel:WORD_0
	v_exp_f16_sdwa v119, v111 dst_sel:WORD_0 dst_unused:UNUSED_PAD src0_sel:WORD_0
	v_exp_f16_sdwa v120, v112 dst_sel:WORD_0 dst_unused:UNUSED_PAD src0_sel:WORD_0
	v_exp_f16_sdwa v121, v113 dst_sel:WORD_0 dst_unused:UNUSED_PAD src0_sel:WORD_0
	v_exp_f16_sdwa v118, v110 dst_sel:WORD_1 dst_unused:UNUSED_PRESERVE src0_sel:WORD_1
	v_exp_f16_sdwa v119, v111 dst_sel:WORD_1 dst_unused:UNUSED_PRESERVE src0_sel:WORD_1
	v_exp_f16_sdwa v120, v112 dst_sel:WORD_1 dst_unused:UNUSED_PRESERVE src0_sel:WORD_1
	v_exp_f16_sdwa v121, v113 dst_sel:WORD_1 dst_unused:UNUSED_PRESERVE src0_sel:WORD_1
	s_nop 0
	s_nop 0
	v_pk_add_f16 v105, v105, v118
	v_pk_add_f16 v104, v104, v119
	v_rcp_f16_e32 v110, v105
	v_rcp_f16_sdwa v105, v105 dst_sel:DWORD dst_unused:UNUSED_PAD src0_sel:WORD_1
	v_pk_add_f16 v103, v103, v120
	v_rcp_f16_e32 v111, v104
	v_rcp_f16_sdwa v104, v104 dst_sel:DWORD dst_unused:UNUSED_PAD src0_sel:WORD_1
	v_pk_add_f16 v102, v102, v121
	v_rcp_f16_e32 v112, v103
	v_rcp_f16_sdwa v103, v103 dst_sel:DWORD dst_unused:UNUSED_PAD src0_sel:WORD_1
	v_rcp_f16_e32 v113, v102
	v_rcp_f16_sdwa v102, v102 dst_sel:DWORD dst_unused:UNUSED_PAD src0_sel:WORD_1
	v_pk_fma_f16 v78, v42, v118, v78
	v_pack_b32_f16 v105, v110, v105
	v_pk_fma_f16 v79, v43, v119, v79
	v_pk_mul_f16 v110, v78, v105
	v_pack_b32_f16 v78, v111, v104
	v_pk_fma_f16 v80, v44, v120, v80
	v_pk_mul_f16 v111, v79, v78
	v_pack_b32_f16 v78, v112, v103
	v_pk_fma_f16 v81, v45, v121, v81
	v_pk_mul_f16 v112, v80, v78
	v_pack_b32_f16 v78, v113, v102
	v_pk_mul_f16 v113, v81, v78
	s_waitcnt vmcnt(12)
	v_pk_mul_f16 v78, v182, v154 op_sel_hi:[0,1]
	v_pk_mul_f16 v81, v182, v157 op_sel_hi:[0,1]
	v_pk_mul_f16 v105, v180, v157 op_sel_hi:[0,1]
	v_pk_mul_f16 v121, v181, v157 op_sel_hi:[0,1]
	v_pk_mul_f16 v79, v182, v155 op_sel_hi:[0,1]
	v_pk_mul_f16 v80, v182, v156 op_sel_hi:[0,1]
	v_pk_mul_f16 v102, v180, v154 op_sel_hi:[0,1]
	v_pk_mul_f16 v103, v180, v155 op_sel_hi:[0,1]
	v_pk_mul_f16 v104, v180, v156 op_sel_hi:[0,1]
	v_pk_mul_f16 v118, v181, v154 op_sel_hi:[0,1]
	v_pk_mul_f16 v119, v181, v155 op_sel_hi:[0,1]
	v_pk_mul_f16 v120, v181, v156 op_sel_hi:[0,1]
	v_pk_fma_f16 v89, v89, v157, v81
	v_pk_fma_f16 v86, v86, v154, v78
	v_pk_fma_f16 v109, v109, v157, v81
	v_pk_fma_f16 v106, v106, v154, v78
	v_pk_fma_f16 v81, v125, v157, v81
	v_pk_fma_f16 v78, v122, v154, v78
	v_pk_fma_f16 v122, v53, v157, v105
	v_pk_fma_f16 v126, v69, v157, v105
	v_pk_fma_f16 v105, v97, v157, v105
	v_pk_fma_f16 v138, v21, v157, v121
	v_pk_fma_f16 v183, v33, v157, v121
	v_pk_fma_f16 v121, v57, v157, v121
	v_pk_maximum3_f16 v157, v89, v109, v81
	v_pk_fma_f16 v88, v88, v156, v80
	v_pk_fma_f16 v87, v87, v155, v79
	v_pk_fma_f16 v108, v108, v156, v80
	v_pk_fma_f16 v107, v107, v155, v79
	v_pk_fma_f16 v80, v124, v156, v80
	v_pk_fma_f16 v79, v123, v155, v79
	v_pk_fma_f16 v123, v52, v156, v104
	v_pk_fma_f16 v124, v51, v155, v103
	v_pk_fma_f16 v125, v50, v154, v102
	v_pk_fma_f16 v127, v68, v156, v104
	v_pk_fma_f16 v128, v67, v155, v103
	v_pk_fma_f16 v129, v66, v154, v102
	v_pk_fma_f16 v104, v96, v156, v104
	v_pk_fma_f16 v103, v95, v155, v103
	v_pk_fma_f16 v102, v94, v154, v102
	v_pk_fma_f16 v139, v20, v156, v120
	v_pk_fma_f16 v140, v19, v155, v119
	v_pk_fma_f16 v141, v18, v154, v118
	v_pk_fma_f16 v184, v32, v156, v120
	v_pk_fma_f16 v185, v31, v155, v119
	v_pk_fma_f16 v186, v30, v154, v118
	v_pk_fma_f16 v120, v56, v156, v120
	v_pk_fma_f16 v119, v55, v155, v119
	v_pk_fma_f16 v118, v54, v154, v118
	v_pk_maximum3_f16 v154, v86, v106, v78
	v_pk_maximum3_f16 v155, v87, v107, v79
	v_pk_maximum3_f16 v156, v88, v108, v80
	v_pk_maximum3_f16 v190, v122, v126, v105
	v_pk_maximum3_f16 v194, v138, v183, v121
	v_pk_maximum3_f16 v187, v125, v129, v102
	v_pk_maximum3_f16 v188, v124, v128, v103
	v_pk_maximum3_f16 v189, v123, v127, v104
	s_nop 0
	v_pk_maximum3_f16 v191, v141, v186, v118
	v_pk_maximum3_f16 v192, v140, v185, v119
	v_pk_maximum3_f16 v157, v157, v190, v194
	v_pk_maximum3_f16 v193, v139, v184, v120
	s_nop 0
	v_pk_maximum3_f16 v154, v154, v187, v191
	v_pk_maximum3_f16 v155, v155, v188, v192
	v_pk_maximum3_f16 v156, v156, v189, v193
	v_xor_b32_e32 v157, 0x80008000, v157
	v_xor_b32_e32 v156, 0x80008000, v156
	v_xor_b32_e32 v155, 0x80008000, v155
	v_xor_b32_e32 v154, 0x80008000, v154
	v_pk_add_f16 v89, v89, v157
	v_pk_add_f16 v86, v86, v154
	v_pk_add_f16 v87, v87, v155
	v_pk_add_f16 v88, v88, v156
	v_pk_add_f16 v106, v106, v154
	v_exp_f16_sdwa v187, v86 dst_sel:WORD_0 dst_unused:UNUSED_PAD src0_sel:WORD_0
	v_exp_f16_sdwa v188, v87 dst_sel:WORD_0 dst_unused:UNUSED_PAD src0_sel:WORD_0
	v_exp_f16_sdwa v189, v88 dst_sel:WORD_0 dst_unused:UNUSED_PAD src0_sel:WORD_0
	v_exp_f16_sdwa v190, v89 dst_sel:WORD_0 dst_unused:UNUSED_PAD src0_sel:WORD_0
	v_exp_f16_sdwa v187, v86 dst_sel:WORD_1 dst_unused:UNUSED_PRESERVE src0_sel:WORD_1
	v_exp_f16_sdwa v188, v87 dst_sel:WORD_1 dst_unused:UNUSED_PRESERVE src0_sel:WORD_1
	v_exp_f16_sdwa v189, v88 dst_sel:WORD_1 dst_unused:UNUSED_PRESERVE src0_sel:WORD_1
	v_exp_f16_sdwa v190, v89 dst_sel:WORD_1 dst_unused:UNUSED_PRESERVE src0_sel:WORD_1
	s_nop 0
	v_pk_add_f16 v107, v107, v155
	v_pk_add_f16 v89, v187, 0
	v_pk_fma_f16 v49, v49, v190, 0
	v_pk_add_f16 v86, v190, 0
	v_pk_add_f16 v87, v189, 0
	v_pk_add_f16 v88, v188, 0
	v_pk_fma_f16 v48, v48, v189, 0
	v_pk_fma_f16 v47, v47, v188, 0
	v_pk_fma_f16 v46, v46, v187, 0
	v_pk_add_f16 v108, v108, v156
	v_pk_add_f16 v109, v109, v157
	s_nop 0
	v_exp_f16_sdwa v187, v106 dst_sel:WORD_0 dst_unused:UNUSED_PAD src0_sel:WORD_0
	v_exp_f16_sdwa v188, v107 dst_sel:WORD_0 dst_unused:UNUSED_PAD src0_sel:WORD_0
	v_exp_f16_sdwa v189, v108 dst_sel:WORD_0 dst_unused:UNUSED_PAD src0_sel:WORD_0
	v_exp_f16_sdwa v190, v109 dst_sel:WORD_0 dst_unused:UNUSED_PAD src0_sel:WORD_0
	v_exp_f16_sdwa v187, v106 dst_sel:WORD_1 dst_unused:UNUSED_PRESERVE src0_sel:WORD_1
	v_exp_f16_sdwa v188, v107 dst_sel:WORD_1 dst_unused:UNUSED_PRESERVE src0_sel:WORD_1
	v_exp_f16_sdwa v189, v108 dst_sel:WORD_1 dst_unused:UNUSED_PRESERVE src0_sel:WORD_1
	v_exp_f16_sdwa v190, v109 dst_sel:WORD_1 dst_unused:UNUSED_PRESERVE src0_sel:WORD_1
	s_nop 0
	s_nop 0
	v_pk_add_f16 v89, v89, v187
	v_pk_fma_f16 v49, v65, v190, v49
	v_pk_add_f16 v65, v81, v157
	v_pk_add_f16 v88, v88, v188
	v_pk_add_f16 v87, v87, v189
	v_pk_add_f16 v86, v86, v190
	v_pk_fma_f16 v46, v62, v187, v46
	v_pk_fma_f16 v47, v63, v188, v47
	v_pk_fma_f16 v48, v64, v189, v48
	v_pk_add_f16 v62, v78, v154
	v_pk_add_f16 v63, v79, v155
	v_pk_add_f16 v64, v80, v156
	s_nop 0
	v_exp_f16_sdwa v78, v62 dst_sel:WORD_0 dst_unused:UNUSED_PAD src0_sel:WORD_0
	v_exp_f16_sdwa v79, v63 dst_sel:WORD_0 dst_unused:UNUSED_PAD src0_sel:WORD_0
	v_exp_f16_sdwa v80, v64 dst_sel:WORD_0 dst_unused:UNUSED_PAD src0_sel:WORD_0
	v_exp_f16_sdwa v81, v65 dst_sel:WORD_0 dst_unused:UNUSED_PAD src0_sel:WORD_0
	v_exp_f16_sdwa v78, v62 dst_sel:WORD_1 dst_unused:UNUSED_PRESERVE src0_sel:WORD_1
	v_exp_f16_sdwa v79, v63 dst_sel:WORD_1 dst_unused:UNUSED_PRESERVE src0_sel:WORD_1
	v_exp_f16_sdwa v80, v64 dst_sel:WORD_1 dst_unused:UNUSED_PRESERVE src0_sel:WORD_1
	v_exp_f16_sdwa v81, v65 dst_sel:WORD_1 dst_unused:UNUSED_PRESERVE src0_sel:WORD_1
	s_nop 0
	s_nop 0
	v_pk_add_f16 v65, v89, v78
	v_pk_add_f16 v62, v86, v81
	v_pk_add_f16 v63, v87, v80
	v_pk_add_f16 v64, v88, v79
	v_pk_fma_f16 v49, v85, v81, v49
	v_pk_fma_f16 v48, v84, v80, v48
	v_pk_fma_f16 v47, v83, v79, v47
	v_pk_fma_f16 v46, v82, v78, v46
	v_pk_add_f16 v78, v125, v154
	v_pk_add_f16 v79, v124, v155
	v_pk_add_f16 v80, v123, v156
	v_pk_add_f16 v81, v122, v157
	s_nop 0
	v_exp_f16_sdwa v82, v78 dst_sel:WORD_0 dst_unused:UNUSED_PAD src0_sel:WORD_0
	v_exp_f16_sdwa v83, v79 dst_sel:WORD_0 dst_unused:UNUSED_PAD src0_sel:WORD_0
	v_exp_f16_sdwa v84, v80 dst_sel:WORD_0 dst_unused:UNUSED_PAD src0_sel:WORD_0
	v_exp_f16_sdwa v85, v81 dst_sel:WORD_0 dst_unused:UNUSED_PAD src0_sel:WORD_0
	v_exp_f16_sdwa v82, v78 dst_sel:WORD_1 dst_unused:UNUSED_PRESERVE src0_sel:WORD_1
	v_exp_f16_sdwa v83, v79 dst_sel:WORD_1 dst_unused:UNUSED_PRESERVE src0_sel:WORD_1
	v_exp_f16_sdwa v84, v80 dst_sel:WORD_1 dst_unused:UNUSED_PRESERVE src0_sel:WORD_1
	v_exp_f16_sdwa v85, v81 dst_sel:WORD_1 dst_unused:UNUSED_PRESERVE src0_sel:WORD_1
	s_nop 0
	v_pk_add_f16 v78, v129, v154
	v_pk_add_f16 v65, v65, v82
	v_pk_add_f16 v64, v64, v83
	v_pk_add_f16 v63, v63, v84
	v_pk_add_f16 v62, v62, v85
	v_pk_fma_f16 v46, v22, v82, v46
	v_pk_fma_f16 v47, v23, v83, v47
	v_pk_fma_f16 v48, v24, v84, v48
	v_pk_fma_f16 v49, v25, v85, v49
	v_pk_add_f16 v79, v128, v155
	v_pk_add_f16 v80, v127, v156
	v_pk_add_f16 v81, v126, v157
	s_nop 0
	v_exp_f16_sdwa v82, v78 dst_sel:WORD_0 dst_unused:UNUSED_PAD src0_sel:WORD_0
	v_exp_f16_sdwa v83, v79 dst_sel:WORD_0 dst_unused:UNUSED_PAD src0_sel:WORD_0
	v_exp_f16_sdwa v84, v80 dst_sel:WORD_0 dst_unused:UNUSED_PAD src0_sel:WORD_0
	v_exp_f16_sdwa v85, v81 dst_sel:WORD_0 dst_unused:UNUSED_PAD src0_sel:WORD_0
	v_exp_f16_sdwa v82, v78 dst_sel:WORD_1 dst_unused:UNUSED_PRESERVE src0_sel:WORD_1
	v_exp_f16_sdwa v83, v79 dst_sel:WORD_1 dst_unused:UNUSED_PRESERVE src0_sel:WORD_1
	v_exp_f16_sdwa v84, v80 dst_sel:WORD_1 dst_unused:UNUSED_PRESERVE src0_sel:WORD_1
	v_exp_f16_sdwa v85, v81 dst_sel:WORD_1 dst_unused:UNUSED_PRESERVE src0_sel:WORD_1
	s_nop 0
	v_pk_add_f16 v78, v102, v154
	v_pk_add_f16 v65, v65, v82
	v_pk_add_f16 v62, v62, v85
	v_pk_add_f16 v63, v63, v84
	v_pk_add_f16 v64, v64, v83
	v_pk_fma_f16 v49, v37, v85, v49
	v_pk_fma_f16 v48, v36, v84, v48
	v_pk_fma_f16 v47, v35, v83, v47
	v_pk_fma_f16 v46, v34, v82, v46
	v_pk_add_f16 v79, v103, v155
	v_pk_add_f16 v80, v104, v156
	v_pk_add_f16 v81, v105, v157
	s_nop 0
	v_exp_f16_sdwa v82, v78 dst_sel:WORD_0 dst_unused:UNUSED_PAD src0_sel:WORD_0
	v_exp_f16_sdwa v83, v79 dst_sel:WORD_0 dst_unused:UNUSED_PAD src0_sel:WORD_0
	v_exp_f16_sdwa v84, v80 dst_sel:WORD_0 dst_unused:UNUSED_PAD src0_sel:WORD_0
	v_exp_f16_sdwa v85, v81 dst_sel:WORD_0 dst_unused:UNUSED_PAD src0_sel:WORD_0
	v_exp_f16_sdwa v82, v78 dst_sel:WORD_1 dst_unused:UNUSED_PRESERVE src0_sel:WORD_1
	v_exp_f16_sdwa v83, v79 dst_sel:WORD_1 dst_unused:UNUSED_PRESERVE src0_sel:WORD_1
	v_exp_f16_sdwa v84, v80 dst_sel:WORD_1 dst_unused:UNUSED_PRESERVE src0_sel:WORD_1
	v_exp_f16_sdwa v85, v81 dst_sel:WORD_1 dst_unused:UNUSED_PRESERVE src0_sel:WORD_1
	s_nop 0
	v_pk_add_f16 v78, v141, v154
	v_pk_add_f16 v65, v65, v82
	v_pk_add_f16 v64, v64, v83
	v_pk_add_f16 v63, v63, v84
	v_pk_add_f16 v62, v62, v85
	v_pk_fma_f16 v46, v42, v82, v46
	v_pk_fma_f16 v47, v43, v83, v47
	v_pk_fma_f16 v48, v44, v84, v48
	v_pk_fma_f16 v49, v45, v85, v49
	v_pk_add_f16 v79, v140, v155
	v_pk_add_f16 v80, v139, v156
	v_pk_add_f16 v81, v138, v157
	s_nop 0
	v_exp_f16_sdwa v82, v78 dst_sel:WORD_0 dst_unused:UNUSED_PAD src0_sel:WORD_0
	v_exp_f16_sdwa v83, v79 dst_sel:WORD_0 dst_unused:UNUSED_PAD src0_sel:WORD_0
	v_exp_f16_sdwa v84, v80 dst_sel:WORD_0 dst_unused:UNUSED_PAD src0_sel:WORD_0
	v_exp_f16_sdwa v85, v81 dst_sel:WORD_0 dst_unused:UNUSED_PAD src0_sel:WORD_0
	v_exp_f16_sdwa v82, v78 dst_sel:WORD_1 dst_unused:UNUSED_PRESERVE src0_sel:WORD_1
	v_exp_f16_sdwa v83, v79 dst_sel:WORD_1 dst_unused:UNUSED_PRESERVE src0_sel:WORD_1
	v_exp_f16_sdwa v84, v80 dst_sel:WORD_1 dst_unused:UNUSED_PRESERVE src0_sel:WORD_1
	v_exp_f16_sdwa v85, v81 dst_sel:WORD_1 dst_unused:UNUSED_PRESERVE src0_sel:WORD_1
	s_nop 0
	v_pk_add_f16 v78, v186, v154
	v_pk_add_f16 v65, v65, v82
	v_pk_add_f16 v62, v62, v85
	v_pk_add_f16 v63, v63, v84
	v_pk_add_f16 v64, v64, v83
	v_pk_fma_f16 v49, v9, v85, v49
	v_pk_fma_f16 v48, v8, v84, v48
	v_pk_fma_f16 v47, v7, v83, v47
	v_pk_fma_f16 v46, v6, v82, v46
	v_pk_add_f16 v79, v185, v155
	v_pk_add_f16 v80, v184, v156
	v_pk_add_f16 v81, v183, v157
	s_nop 0
	v_exp_f16_sdwa v82, v78 dst_sel:WORD_0 dst_unused:UNUSED_PAD src0_sel:WORD_0
	v_exp_f16_sdwa v83, v79 dst_sel:WORD_0 dst_unused:UNUSED_PAD src0_sel:WORD_0
	v_exp_f16_sdwa v84, v80 dst_sel:WORD_0 dst_unused:UNUSED_PAD src0_sel:WORD_0
	v_exp_f16_sdwa v85, v81 dst_sel:WORD_0 dst_unused:UNUSED_PAD src0_sel:WORD_0
	v_exp_f16_sdwa v82, v78 dst_sel:WORD_1 dst_unused:UNUSED_PRESERVE src0_sel:WORD_1
	v_exp_f16_sdwa v83, v79 dst_sel:WORD_1 dst_unused:UNUSED_PRESERVE src0_sel:WORD_1
	v_exp_f16_sdwa v84, v80 dst_sel:WORD_1 dst_unused:UNUSED_PRESERVE src0_sel:WORD_1
	v_exp_f16_sdwa v85, v81 dst_sel:WORD_1 dst_unused:UNUSED_PRESERVE src0_sel:WORD_1
	s_nop 0
	v_pk_add_f16 v78, v118, v154
	v_pk_add_f16 v65, v65, v82
	v_pk_add_f16 v64, v64, v83
	v_pk_add_f16 v63, v63, v84
	v_pk_add_f16 v62, v62, v85
	v_pk_fma_f16 v46, v10, v82, v46
	v_pk_fma_f16 v47, v11, v83, v47
	v_pk_fma_f16 v48, v12, v84, v48
	v_pk_fma_f16 v49, v13, v85, v49
	v_pk_add_f16 v79, v119, v155
	v_pk_add_f16 v80, v120, v156
	v_pk_add_f16 v81, v121, v157
	s_nop 0
	v_exp_f16_sdwa v82, v78 dst_sel:WORD_0 dst_unused:UNUSED_PAD src0_sel:WORD_0
	v_exp_f16_sdwa v83, v79 dst_sel:WORD_0 dst_unused:UNUSED_PAD src0_sel:WORD_0
	v_exp_f16_sdwa v84, v80 dst_sel:WORD_0 dst_unused:UNUSED_PAD src0_sel:WORD_0
	v_exp_f16_sdwa v85, v81 dst_sel:WORD_0 dst_unused:UNUSED_PAD src0_sel:WORD_0
	v_exp_f16_sdwa v82, v78 dst_sel:WORD_1 dst_unused:UNUSED_PRESERVE src0_sel:WORD_1
	v_exp_f16_sdwa v83, v79 dst_sel:WORD_1 dst_unused:UNUSED_PRESERVE src0_sel:WORD_1
	v_exp_f16_sdwa v84, v80 dst_sel:WORD_1 dst_unused:UNUSED_PRESERVE src0_sel:WORD_1
	v_exp_f16_sdwa v85, v81 dst_sel:WORD_1 dst_unused:UNUSED_PRESERVE src0_sel:WORD_1
	s_nop 0
	s_nop 0
	v_pk_add_f16 v65, v65, v82
	v_pk_add_f16 v64, v64, v83
	v_rcp_f16_e32 v78, v65
	v_rcp_f16_sdwa v65, v65 dst_sel:DWORD dst_unused:UNUSED_PAD src0_sel:WORD_1
	v_pk_add_f16 v63, v63, v84
	v_rcp_f16_e32 v79, v64
	v_rcp_f16_sdwa v64, v64 dst_sel:DWORD dst_unused:UNUSED_PAD src0_sel:WORD_1
	v_pk_add_f16 v62, v62, v85
	v_rcp_f16_e32 v80, v63
	v_rcp_f16_sdwa v81, v63 dst_sel:DWORD dst_unused:UNUSED_PAD src0_sel:WORD_1
	v_pk_fma_f16 v47, v15, v83, v47
	v_pk_fma_f16 v46, v14, v82, v46
	v_rcp_f16_e32 v82, v62
	v_rcp_f16_sdwa v83, v62 dst_sel:DWORD dst_unused:UNUSED_PAD src0_sel:WORD_1
	v_pack_b32_f16 v62, v78, v65
	v_pk_mul_f16 v62, v46, v62
	v_pack_b32_f16 v46, v79, v64
	v_pk_fma_f16 v48, v16, v84, v48
	v_pk_mul_f16 v63, v47, v46
	v_pack_b32_f16 v46, v80, v81
	v_pk_fma_f16 v49, v17, v85, v49
	v_pk_mul_f16 v64, v48, v46
	v_pack_b32_f16 v46, v82, v83
	v_pk_mul_f16 v65, v49, v46
	s_waitcnt vmcnt(6)
	v_pk_mul_f16 v46, v182, v150 op_sel_hi:[0,1]
	v_pk_mul_f16 v47, v182, v151 op_sel_hi:[0,1]
	v_pk_mul_f16 v48, v182, v152 op_sel_hi:[0,1]
	v_pk_mul_f16 v49, v182, v153 op_sel_hi:[0,1]
	v_pk_mul_f16 v78, v180, v150 op_sel_hi:[0,1]
	v_pk_mul_f16 v82, v181, v150 op_sel_hi:[0,1]
	v_pk_fma_f16 v50, v50, v150, v46
	v_pk_fma_f16 v66, v66, v150, v46
	v_pk_fma_f16 v46, v94, v150, v46
	v_pk_mul_f16 v79, v180, v151 op_sel_hi:[0,1]
	v_pk_maximum3_f16 v118, v50, v66, v46
	v_pk_mul_f16 v80, v180, v152 op_sel_hi:[0,1]
	v_pk_mul_f16 v81, v180, v153 op_sel_hi:[0,1]
	v_pk_mul_f16 v83, v181, v151 op_sel_hi:[0,1]
	v_pk_mul_f16 v84, v181, v152 op_sel_hi:[0,1]
	v_pk_mul_f16 v85, v181, v153 op_sel_hi:[0,1]
	v_pk_fma_f16 v53, v53, v153, v49
	v_pk_fma_f16 v52, v52, v152, v48
	v_pk_fma_f16 v51, v51, v151, v47
	v_pk_fma_f16 v69, v69, v153, v49
	v_pk_fma_f16 v68, v68, v152, v48
	v_pk_fma_f16 v67, v67, v151, v47
	v_pk_fma_f16 v49, v97, v153, v49
	v_pk_fma_f16 v48, v96, v152, v48
	v_pk_fma_f16 v47, v95, v151, v47
	v_pk_fma_f16 v89, v18, v150, v78
	v_pk_fma_f16 v97, v30, v150, v78
	v_pk_fma_f16 v78, v54, v150, v78
	v_pk_fma_f16 v105, v74, v150, v82
	v_pk_fma_f16 v109, v98, v150, v82
	v_pk_fma_f16 v82, v114, v150, v82
	v_pk_maximum3_f16 v119, v51, v67, v47
	v_pk_maximum3_f16 v120, v52, v68, v48
	v_pk_maximum3_f16 v121, v53, v69, v49
	v_pk_maximum3_f16 v122, v89, v97, v78
	v_pk_fma_f16 v86, v21, v153, v81
	v_pk_maximum3_f16 v126, v105, v109, v82
	v_pk_fma_f16 v87, v20, v152, v80
	v_pk_maximum3_f16 v118, v118, v122, v126
	v_pk_fma_f16 v88, v19, v151, v79
	v_pk_fma_f16 v94, v33, v153, v81
	v_pk_fma_f16 v95, v32, v152, v80
	v_pk_fma_f16 v96, v31, v151, v79
	v_pk_fma_f16 v81, v57, v153, v81
	v_pk_fma_f16 v80, v56, v152, v80
	v_pk_fma_f16 v79, v55, v151, v79
	v_pk_fma_f16 v102, v77, v153, v85
	v_pk_fma_f16 v103, v76, v152, v84
	v_pk_fma_f16 v104, v75, v151, v83
	v_pk_fma_f16 v106, v101, v153, v85
	v_pk_fma_f16 v107, v100, v152, v84
	v_pk_fma_f16 v108, v99, v151, v83
	v_pk_fma_f16 v85, v117, v153, v85
	v_pk_fma_f16 v84, v116, v152, v84
	v_pk_fma_f16 v83, v115, v151, v83
	v_pk_maximum3_f16 v123, v88, v96, v79
	v_pk_maximum3_f16 v124, v87, v95, v80
	v_pk_maximum3_f16 v125, v86, v94, v81
	v_pk_maximum3_f16 v128, v103, v107, v84
	v_pk_maximum3_f16 v129, v102, v106, v85
	s_nop 0
	v_pk_maximum3_f16 v127, v104, v108, v83
	v_xor_b32_e32 v118, 0x80008000, v118
	v_pk_maximum3_f16 v119, v119, v123, v127
	v_pk_maximum3_f16 v120, v120, v124, v128
	v_pk_maximum3_f16 v121, v121, v125, v129
	v_pk_add_f16 v50, v50, v118
	v_xor_b32_e32 v121, 0x80008000, v121
	v_xor_b32_e32 v120, 0x80008000, v120
	v_xor_b32_e32 v119, 0x80008000, v119
	v_pk_add_f16 v51, v51, v119
	v_pk_add_f16 v52, v52, v120
	v_pk_add_f16 v53, v53, v121
	v_pk_add_f16 v66, v66, v118
	v_exp_f16_sdwa v122, v50 dst_sel:WORD_0 dst_unused:UNUSED_PAD src0_sel:WORD_0
	v_exp_f16_sdwa v123, v51 dst_sel:WORD_0 dst_unused:UNUSED_PAD src0_sel:WORD_0
	v_exp_f16_sdwa v124, v52 dst_sel:WORD_0 dst_unused:UNUSED_PAD src0_sel:WORD_0
	v_exp_f16_sdwa v125, v53 dst_sel:WORD_0 dst_unused:UNUSED_PAD src0_sel:WORD_0
	v_exp_f16_sdwa v122, v50 dst_sel:WORD_1 dst_unused:UNUSED_PRESERVE src0_sel:WORD_1
	v_exp_f16_sdwa v123, v51 dst_sel:WORD_1 dst_unused:UNUSED_PRESERVE src0_sel:WORD_1
	v_exp_f16_sdwa v124, v52 dst_sel:WORD_1 dst_unused:UNUSED_PRESERVE src0_sel:WORD_1
	v_exp_f16_sdwa v125, v53 dst_sel:WORD_1 dst_unused:UNUSED_PRESERVE src0_sel:WORD_1
	s_nop 0
	v_pk_add_f16 v67, v67, v119
	v_pk_add_f16 v50, v125, 0
	v_pk_fma_f16 v22, v22, v122, 0
	v_pk_add_f16 v51, v124, 0
	v_pk_add_f16 v52, v123, 0
	v_pk_add_f16 v53, v122, 0
	v_pk_fma_f16 v23, v23, v123, 0
	v_pk_fma_f16 v24, v24, v124, 0
	v_pk_fma_f16 v25, v25, v125, 0
	v_pk_add_f16 v68, v68, v120
	v_pk_add_f16 v69, v69, v121
	s_nop 0
	v_exp_f16_sdwa v122, v66 dst_sel:WORD_0 dst_unused:UNUSED_PAD src0_sel:WORD_0
	v_exp_f16_sdwa v123, v67 dst_sel:WORD_0 dst_unused:UNUSED_PAD src0_sel:WORD_0
	v_exp_f16_sdwa v124, v68 dst_sel:WORD_0 dst_unused:UNUSED_PAD src0_sel:WORD_0
	v_exp_f16_sdwa v125, v69 dst_sel:WORD_0 dst_unused:UNUSED_PAD src0_sel:WORD_0
	v_exp_f16_sdwa v122, v66 dst_sel:WORD_1 dst_unused:UNUSED_PRESERVE src0_sel:WORD_1
	v_exp_f16_sdwa v123, v67 dst_sel:WORD_1 dst_unused:UNUSED_PRESERVE src0_sel:WORD_1
	v_exp_f16_sdwa v124, v68 dst_sel:WORD_1 dst_unused:UNUSED_PRESERVE src0_sel:WORD_1
	v_exp_f16_sdwa v125, v69 dst_sel:WORD_1 dst_unused:UNUSED_PRESERVE src0_sel:WORD_1
	s_nop 0
	s_nop 0
	v_pk_add_f16 v50, v50, v125
	v_pk_fma_f16 v22, v34, v122, v22
	v_pk_add_f16 v34, v46, v118
	v_pk_add_f16 v53, v53, v122
	v_pk_add_f16 v52, v52, v123
	v_pk_add_f16 v51, v51, v124
	v_pk_fma_f16 v25, v37, v125, v25
	v_pk_fma_f16 v24, v36, v124, v24
	v_pk_fma_f16 v23, v35, v123, v23
	v_pk_add_f16 v35, v47, v119
	v_pk_add_f16 v36, v48, v120
	v_pk_add_f16 v37, v49, v121
	s_nop 0
	v_exp_f16_sdwa v46, v34 dst_sel:WORD_0 dst_unused:UNUSED_PAD src0_sel:WORD_0
	v_exp_f16_sdwa v47, v35 dst_sel:WORD_0 dst_unused:UNUSED_PAD src0_sel:WORD_0
	v_exp_f16_sdwa v48, v36 dst_sel:WORD_0 dst_unused:UNUSED_PAD src0_sel:WORD_0
	v_exp_f16_sdwa v49, v37 dst_sel:WORD_0 dst_unused:UNUSED_PAD src0_sel:WORD_0
	v_exp_f16_sdwa v46, v34 dst_sel:WORD_1 dst_unused:UNUSED_PRESERVE src0_sel:WORD_1
	v_exp_f16_sdwa v47, v35 dst_sel:WORD_1 dst_unused:UNUSED_PRESERVE src0_sel:WORD_1
	v_exp_f16_sdwa v48, v36 dst_sel:WORD_1 dst_unused:UNUSED_PRESERVE src0_sel:WORD_1
	v_exp_f16_sdwa v49, v37 dst_sel:WORD_1 dst_unused:UNUSED_PRESERVE src0_sel:WORD_1
	s_nop 0
	s_nop 0
	v_pk_add_f16 v34, v50, v49
	v_pk_add_f16 v35, v51, v48
	v_pk_add_f16 v36, v52, v47
	v_pk_add_f16 v37, v53, v46
	v_pk_fma_f16 v22, v42, v46, v22
	v_pk_fma_f16 v23, v43, v47, v23
	v_pk_fma_f16 v24, v44, v48, v24
	v_pk_fma_f16 v25, v45, v49, v25
	v_pk_add_f16 v42, v89, v118
	v_pk_add_f16 v43, v88, v119
	v_pk_add_f16 v44, v87, v120
	v_pk_add_f16 v45, v86, v121
	s_nop 0
	v_exp_f16_sdwa v46, v42 dst_sel:WORD_0 dst_unused:UNUSED_PAD src0_sel:WORD_0
	v_exp_f16_sdwa v47, v43 dst_sel:WORD_0 dst_unused:UNUSED_PAD src0_sel:WORD_0
	v_exp_f16_sdwa v48, v44 dst_sel:WORD_0 dst_unused:UNUSED_PAD src0_sel:WORD_0
	v_exp_f16_sdwa v49, v45 dst_sel:WORD_0 dst_unused:UNUSED_PAD src0_sel:WORD_0
	v_exp_f16_sdwa v46, v42 dst_sel:WORD_1 dst_unused:UNUSED_PRESERVE src0_sel:WORD_1
	v_exp_f16_sdwa v47, v43 dst_sel:WORD_1 dst_unused:UNUSED_PRESERVE src0_sel:WORD_1
	v_exp_f16_sdwa v48, v44 dst_sel:WORD_1 dst_unused:UNUSED_PRESERVE src0_sel:WORD_1
	v_exp_f16_sdwa v49, v45 dst_sel:WORD_1 dst_unused:UNUSED_PRESERVE src0_sel:WORD_1
	s_nop 0
	v_pk_add_f16 v42, v97, v118
	v_pk_add_f16 v34, v34, v49
	v_pk_add_f16 v37, v37, v46
	v_pk_add_f16 v36, v36, v47
	v_pk_add_f16 v35, v35, v48
	v_pk_fma_f16 v25, v9, v49, v25
	v_pk_fma_f16 v24, v8, v48, v24
	v_pk_fma_f16 v23, v7, v47, v23
	v_pk_fma_f16 v22, v6, v46, v22
	v_pk_add_f16 v43, v96, v119
	v_pk_add_f16 v44, v95, v120
	v_pk_add_f16 v45, v94, v121
	s_nop 0
	v_exp_f16_sdwa v46, v42 dst_sel:WORD_0 dst_unused:UNUSED_PAD src0_sel:WORD_0
	v_exp_f16_sdwa v47, v43 dst_sel:WORD_0 dst_unused:UNUSED_PAD src0_sel:WORD_0
	v_exp_f16_sdwa v48, v44 dst_sel:WORD_0 dst_unused:UNUSED_PAD src0_sel:WORD_0
	v_exp_f16_sdwa v49, v45 dst_sel:WORD_0 dst_unused:UNUSED_PAD src0_sel:WORD_0
	v_exp_f16_sdwa v46, v42 dst_sel:WORD_1 dst_unused:UNUSED_PRESERVE src0_sel:WORD_1
	v_exp_f16_sdwa v47, v43 dst_sel:WORD_1 dst_unused:UNUSED_PRESERVE src0_sel:WORD_1
	v_exp_f16_sdwa v48, v44 dst_sel:WORD_1 dst_unused:UNUSED_PRESERVE src0_sel:WORD_1
	v_exp_f16_sdwa v49, v45 dst_sel:WORD_1 dst_unused:UNUSED_PRESERVE src0_sel:WORD_1
	s_nop 0
	v_pk_add_f16 v42, v78, v118
	v_pk_add_f16 v34, v34, v49
	v_pk_add_f16 v35, v35, v48
	v_pk_add_f16 v36, v36, v47
	v_pk_add_f16 v37, v37, v46
	v_pk_fma_f16 v22, v10, v46, v22
	v_pk_fma_f16 v23, v11, v47, v23
	v_pk_fma_f16 v24, v12, v48, v24
	v_pk_fma_f16 v25, v13, v49, v25
	v_pk_add_f16 v43, v79, v119
	v_pk_add_f16 v44, v80, v120
	v_pk_add_f16 v45, v81, v121
	s_nop 0
	v_exp_f16_sdwa v46, v42 dst_sel:WORD_0 dst_unused:UNUSED_PAD src0_sel:WORD_0
	v_exp_f16_sdwa v47, v43 dst_sel:WORD_0 dst_unused:UNUSED_PAD src0_sel:WORD_0
	v_exp_f16_sdwa v48, v44 dst_sel:WORD_0 dst_unused:UNUSED_PAD src0_sel:WORD_0
	v_exp_f16_sdwa v49, v45 dst_sel:WORD_0 dst_unused:UNUSED_PAD src0_sel:WORD_0
	v_exp_f16_sdwa v46, v42 dst_sel:WORD_1 dst_unused:UNUSED_PRESERVE src0_sel:WORD_1
	v_exp_f16_sdwa v47, v43 dst_sel:WORD_1 dst_unused:UNUSED_PRESERVE src0_sel:WORD_1
	v_exp_f16_sdwa v48, v44 dst_sel:WORD_1 dst_unused:UNUSED_PRESERVE src0_sel:WORD_1
	v_exp_f16_sdwa v49, v45 dst_sel:WORD_1 dst_unused:UNUSED_PRESERVE src0_sel:WORD_1
	s_nop 0
	v_pk_add_f16 v42, v105, v118
	v_pk_add_f16 v34, v34, v49
	v_pk_add_f16 v37, v37, v46
	v_pk_add_f16 v36, v36, v47
	v_pk_add_f16 v35, v35, v48
	v_pk_fma_f16 v25, v17, v49, v25
	v_pk_fma_f16 v24, v16, v48, v24
	v_pk_fma_f16 v23, v15, v47, v23
	v_pk_fma_f16 v22, v14, v46, v22
	v_pk_add_f16 v43, v104, v119
	v_pk_add_f16 v44, v103, v120
	v_pk_add_f16 v45, v102, v121
	s_nop 0
	v_exp_f16_sdwa v46, v42 dst_sel:WORD_0 dst_unused:UNUSED_PAD src0_sel:WORD_0
	v_exp_f16_sdwa v47, v43 dst_sel:WORD_0 dst_unused:UNUSED_PAD src0_sel:WORD_0
	v_exp_f16_sdwa v48, v44 dst_sel:WORD_0 dst_unused:UNUSED_PAD src0_sel:WORD_0
	v_exp_f16_sdwa v49, v45 dst_sel:WORD_0 dst_unused:UNUSED_PAD src0_sel:WORD_0
	v_exp_f16_sdwa v46, v42 dst_sel:WORD_1 dst_unused:UNUSED_PRESERVE src0_sel:WORD_1
	v_exp_f16_sdwa v47, v43 dst_sel:WORD_1 dst_unused:UNUSED_PRESERVE src0_sel:WORD_1
	v_exp_f16_sdwa v48, v44 dst_sel:WORD_1 dst_unused:UNUSED_PRESERVE src0_sel:WORD_1
	v_exp_f16_sdwa v49, v45 dst_sel:WORD_1 dst_unused:UNUSED_PRESERVE src0_sel:WORD_1
	s_nop 0
	v_pk_add_f16 v42, v109, v118
	v_pk_add_f16 v34, v34, v49
	v_pk_add_f16 v35, v35, v48
	v_pk_add_f16 v36, v36, v47
	v_pk_add_f16 v37, v37, v46
	v_pk_fma_f16 v22, v26, v46, v22
	v_pk_fma_f16 v23, v27, v47, v23
	v_pk_fma_f16 v24, v28, v48, v24
	v_pk_fma_f16 v25, v29, v49, v25
	v_pk_add_f16 v43, v108, v119
	v_pk_add_f16 v44, v107, v120
	v_pk_add_f16 v45, v106, v121
	s_nop 0
	v_exp_f16_sdwa v46, v42 dst_sel:WORD_0 dst_unused:UNUSED_PAD src0_sel:WORD_0
	v_exp_f16_sdwa v47, v43 dst_sel:WORD_0 dst_unused:UNUSED_PAD src0_sel:WORD_0
	v_exp_f16_sdwa v48, v44 dst_sel:WORD_0 dst_unused:UNUSED_PAD src0_sel:WORD_0
	v_exp_f16_sdwa v49, v45 dst_sel:WORD_0 dst_unused:UNUSED_PAD src0_sel:WORD_0
	v_exp_f16_sdwa v46, v42 dst_sel:WORD_1 dst_unused:UNUSED_PRESERVE src0_sel:WORD_1
	v_exp_f16_sdwa v47, v43 dst_sel:WORD_1 dst_unused:UNUSED_PRESERVE src0_sel:WORD_1
	v_exp_f16_sdwa v48, v44 dst_sel:WORD_1 dst_unused:UNUSED_PRESERVE src0_sel:WORD_1
	v_exp_f16_sdwa v49, v45 dst_sel:WORD_1 dst_unused:UNUSED_PRESERVE src0_sel:WORD_1
	s_nop 0
	v_pk_add_f16 v42, v82, v118
	v_pk_add_f16 v34, v34, v49
	v_pk_add_f16 v37, v37, v46
	v_pk_add_f16 v36, v36, v47
	v_pk_add_f16 v35, v35, v48
	v_pk_fma_f16 v25, v41, v49, v25
	v_pk_fma_f16 v24, v40, v48, v24
	v_pk_fma_f16 v23, v39, v47, v23
	v_pk_fma_f16 v22, v38, v46, v22
	v_pk_add_f16 v43, v83, v119
	v_pk_add_f16 v44, v84, v120
	v_pk_add_f16 v45, v85, v121
	s_nop 0
	v_exp_f16_sdwa v46, v42 dst_sel:WORD_0 dst_unused:UNUSED_PAD src0_sel:WORD_0
	v_exp_f16_sdwa v47, v43 dst_sel:WORD_0 dst_unused:UNUSED_PAD src0_sel:WORD_0
	v_exp_f16_sdwa v48, v44 dst_sel:WORD_0 dst_unused:UNUSED_PAD src0_sel:WORD_0
	v_exp_f16_sdwa v49, v45 dst_sel:WORD_0 dst_unused:UNUSED_PAD src0_sel:WORD_0
	v_exp_f16_sdwa v46, v42 dst_sel:WORD_1 dst_unused:UNUSED_PRESERVE src0_sel:WORD_1
	v_exp_f16_sdwa v47, v43 dst_sel:WORD_1 dst_unused:UNUSED_PRESERVE src0_sel:WORD_1
	v_exp_f16_sdwa v48, v44 dst_sel:WORD_1 dst_unused:UNUSED_PRESERVE src0_sel:WORD_1
	v_exp_f16_sdwa v49, v45 dst_sel:WORD_1 dst_unused:UNUSED_PRESERVE src0_sel:WORD_1
	s_nop 0
	s_nop 0
	v_pk_add_f16 v34, v34, v49
	v_pk_add_f16 v35, v35, v48
	v_rcp_f16_e32 v44, v34
	v_rcp_f16_sdwa v34, v34 dst_sel:DWORD dst_unused:UNUSED_PAD src0_sel:WORD_1
	v_pk_add_f16 v36, v36, v47
	v_rcp_f16_e32 v45, v35
	v_rcp_f16_sdwa v35, v35 dst_sel:DWORD dst_unused:UNUSED_PAD src0_sel:WORD_1
	v_pk_add_f16 v37, v37, v46
	v_rcp_f16_e32 v43, v36
	v_rcp_f16_sdwa v36, v36 dst_sel:DWORD dst_unused:UNUSED_PAD src0_sel:WORD_1
	v_rcp_f16_e32 v42, v37
	v_rcp_f16_sdwa v37, v37 dst_sel:DWORD dst_unused:UNUSED_PAD src0_sel:WORD_1
	v_pk_fma_f16 v25, v61, v49, v25
	v_pack_b32_f16 v34, v44, v34
	v_pk_fma_f16 v24, v60, v48, v24
	v_pk_mul_f16 v25, v25, v34
	v_pack_b32_f16 v34, v45, v35
	v_pk_fma_f16 v23, v59, v47, v23
	v_pk_mul_f16 v24, v24, v34
	v_pack_b32_f16 v34, v43, v36
	v_pk_fma_f16 v22, v58, v46, v22
	v_pk_mul_f16 v23, v23, v34
	v_pack_b32_f16 v34, v42, v37
	v_pk_mul_f16 v22, v22, v34
	s_waitcnt vmcnt(0)
	v_pk_mul_f16 v34, v182, v146 op_sel_hi:[0,1]
	v_pk_mul_f16 v35, v182, v147 op_sel_hi:[0,1]
	v_pk_mul_f16 v36, v182, v148 op_sel_hi:[0,1]
	v_pk_mul_f16 v37, v182, v149 op_sel_hi:[0,1]
	v_pk_mul_f16 v42, v180, v146 op_sel_hi:[0,1]
	v_pk_mul_f16 v43, v180, v147 op_sel_hi:[0,1]
	v_pk_mul_f16 v44, v180, v148 op_sel_hi:[0,1]
	v_pk_mul_f16 v45, v180, v149 op_sel_hi:[0,1]
	v_pk_mul_f16 v46, v181, v146 op_sel_hi:[0,1]
	v_pk_mul_f16 v47, v181, v147 op_sel_hi:[0,1]
	v_pk_mul_f16 v48, v181, v148 op_sel_hi:[0,1]
	v_pk_mul_f16 v49, v181, v149 op_sel_hi:[0,1]
	v_pk_fma_f16 v21, v21, v149, v37
	v_pk_fma_f16 v20, v20, v148, v36
	v_pk_fma_f16 v19, v19, v147, v35
	v_pk_fma_f16 v18, v18, v146, v34
	v_pk_fma_f16 v33, v33, v149, v37
	v_pk_fma_f16 v32, v32, v148, v36
	v_pk_fma_f16 v31, v31, v147, v35
	v_pk_fma_f16 v30, v30, v146, v34
	v_pk_fma_f16 v37, v57, v149, v37
	v_pk_fma_f16 v36, v56, v148, v36
	v_pk_fma_f16 v35, v55, v147, v35
	v_pk_fma_f16 v34, v54, v146, v34
	v_pk_maximum3_f16 v79, v19, v31, v35
	v_pk_maximum3_f16 v80, v20, v32, v36
	v_pk_maximum3_f16 v81, v21, v33, v37
	v_pk_fma_f16 v50, v77, v149, v45
	v_pk_maximum3_f16 v78, v18, v30, v34
	v_pk_fma_f16 v51, v76, v148, v44
	v_pk_fma_f16 v52, v75, v147, v43
	v_pk_fma_f16 v53, v74, v146, v42
	v_pk_fma_f16 v54, v101, v149, v45
	v_pk_fma_f16 v55, v100, v148, v44
	v_pk_fma_f16 v56, v99, v147, v43
	v_pk_fma_f16 v57, v98, v146, v42
	v_pk_fma_f16 v45, v117, v149, v45
	v_pk_fma_f16 v44, v116, v148, v44
	v_pk_fma_f16 v43, v115, v147, v43
	v_pk_fma_f16 v42, v114, v146, v42
	v_pk_fma_f16 v66, v133, v149, v49
	v_pk_fma_f16 v67, v132, v148, v48
	v_pk_fma_f16 v68, v131, v147, v47
	v_pk_fma_f16 v69, v130, v146, v46
	v_pk_fma_f16 v74, v137, v149, v49
	v_pk_fma_f16 v75, v136, v148, v48
	v_pk_fma_f16 v76, v135, v147, v47
	v_pk_fma_f16 v77, v134, v146, v46
	v_pk_fma_f16 v49, v145, v149, v49
	v_pk_fma_f16 v48, v144, v148, v48
	v_pk_fma_f16 v47, v143, v147, v47
	v_pk_fma_f16 v46, v142, v146, v46
	v_pk_maximum3_f16 v82, v53, v57, v42
	v_pk_maximum3_f16 v83, v52, v56, v43
	v_pk_maximum3_f16 v84, v51, v55, v44
	v_pk_maximum3_f16 v85, v50, v54, v45
	v_pk_maximum3_f16 v87, v68, v76, v47
	s_nop 0
	v_pk_maximum3_f16 v86, v69, v77, v46
	v_pk_maximum3_f16 v88, v67, v75, v48
	v_pk_maximum3_f16 v89, v66, v74, v49
	s_nop 0
	v_pk_maximum3_f16 v78, v78, v82, v86
	v_pk_maximum3_f16 v79, v79, v83, v87
	v_pk_maximum3_f16 v80, v80, v84, v88
	v_pk_maximum3_f16 v81, v81, v85, v89
	s_nop 0
	v_xor_b32_e32 v81, 0x80008000, v81
	v_xor_b32_e32 v80, 0x80008000, v80
	v_xor_b32_e32 v79, 0x80008000, v79
	v_xor_b32_e32 v78, 0x80008000, v78
	v_pk_add_f16 v18, v18, v78
	v_pk_add_f16 v19, v19, v79
	v_pk_add_f16 v20, v20, v80
	v_pk_add_f16 v21, v21, v81
	v_pk_add_f16 v30, v30, v78
	v_exp_f16_sdwa v82, v18 dst_sel:WORD_0 dst_unused:UNUSED_PAD src0_sel:WORD_0
	v_exp_f16_sdwa v83, v19 dst_sel:WORD_0 dst_unused:UNUSED_PAD src0_sel:WORD_0
	v_exp_f16_sdwa v84, v20 dst_sel:WORD_0 dst_unused:UNUSED_PAD src0_sel:WORD_0
	v_exp_f16_sdwa v85, v21 dst_sel:WORD_0 dst_unused:UNUSED_PAD src0_sel:WORD_0
	v_exp_f16_sdwa v82, v18 dst_sel:WORD_1 dst_unused:UNUSED_PRESERVE src0_sel:WORD_1
	v_exp_f16_sdwa v83, v19 dst_sel:WORD_1 dst_unused:UNUSED_PRESERVE src0_sel:WORD_1
	v_exp_f16_sdwa v84, v20 dst_sel:WORD_1 dst_unused:UNUSED_PRESERVE src0_sel:WORD_1
	v_exp_f16_sdwa v85, v21 dst_sel:WORD_1 dst_unused:UNUSED_PRESERVE src0_sel:WORD_1
	s_nop 0
	v_pk_add_f16 v31, v31, v79
	v_pk_add_f16 v18, v82, 0
	v_pk_add_f16 v19, v83, 0
	v_pk_add_f16 v20, v84, 0
	v_pk_add_f16 v21, v85, 0
	v_pk_fma_f16 v6, v6, v82, 0
	v_pk_fma_f16 v7, v7, v83, 0
	v_pk_fma_f16 v8, v8, v84, 0
	v_pk_fma_f16 v9, v9, v85, 0
	v_pk_add_f16 v32, v32, v80
	v_pk_add_f16 v33, v33, v81
	s_nop 0
	v_exp_f16_sdwa v82, v30 dst_sel:WORD_0 dst_unused:UNUSED_PAD src0_sel:WORD_0
	v_exp_f16_sdwa v83, v31 dst_sel:WORD_0 dst_unused:UNUSED_PAD src0_sel:WORD_0
	v_exp_f16_sdwa v84, v32 dst_sel:WORD_0 dst_unused:UNUSED_PAD src0_sel:WORD_0
	v_exp_f16_sdwa v85, v33 dst_sel:WORD_0 dst_unused:UNUSED_PAD src0_sel:WORD_0
	v_exp_f16_sdwa v82, v30 dst_sel:WORD_1 dst_unused:UNUSED_PRESERVE src0_sel:WORD_1
	v_exp_f16_sdwa v83, v31 dst_sel:WORD_1 dst_unused:UNUSED_PRESERVE src0_sel:WORD_1
	v_exp_f16_sdwa v84, v32 dst_sel:WORD_1 dst_unused:UNUSED_PRESERVE src0_sel:WORD_1
	v_exp_f16_sdwa v85, v33 dst_sel:WORD_1 dst_unused:UNUSED_PRESERVE src0_sel:WORD_1
	s_nop 0
	s_nop 0
	v_pk_add_f16 v21, v21, v85
	v_pk_add_f16 v20, v20, v84
	v_pk_add_f16 v19, v19, v83
	v_pk_add_f16 v18, v18, v82
	v_pk_fma_f16 v9, v13, v85, v9
	v_pk_fma_f16 v8, v12, v84, v8
	v_pk_fma_f16 v7, v11, v83, v7
	v_pk_fma_f16 v6, v10, v82, v6
	v_pk_add_f16 v10, v34, v78
	v_pk_add_f16 v11, v35, v79
	v_pk_add_f16 v12, v36, v80
	v_pk_add_f16 v13, v37, v81
	s_nop 0
	v_exp_f16_sdwa v30, v10 dst_sel:WORD_0 dst_unused:UNUSED_PAD src0_sel:WORD_0
	v_exp_f16_sdwa v31, v11 dst_sel:WORD_0 dst_unused:UNUSED_PAD src0_sel:WORD_0
	v_exp_f16_sdwa v32, v12 dst_sel:WORD_0 dst_unused:UNUSED_PAD src0_sel:WORD_0
	v_exp_f16_sdwa v33, v13 dst_sel:WORD_0 dst_unused:UNUSED_PAD src0_sel:WORD_0
	v_exp_f16_sdwa v30, v10 dst_sel:WORD_1 dst_unused:UNUSED_PRESERVE src0_sel:WORD_1
	v_exp_f16_sdwa v31, v11 dst_sel:WORD_1 dst_unused:UNUSED_PRESERVE src0_sel:WORD_1
	v_exp_f16_sdwa v32, v12 dst_sel:WORD_1 dst_unused:UNUSED_PRESERVE src0_sel:WORD_1
	v_exp_f16_sdwa v33, v13 dst_sel:WORD_1 dst_unused:UNUSED_PRESERVE src0_sel:WORD_1
	s_nop 0
	s_nop 0
	v_pk_add_f16 v10, v18, v30
	v_pk_add_f16 v11, v19, v31
	v_pk_add_f16 v12, v20, v32
	v_pk_add_f16 v13, v21, v33
	v_pk_fma_f16 v6, v14, v30, v6
	v_pk_fma_f16 v7, v15, v31, v7
	v_pk_fma_f16 v8, v16, v32, v8
	v_pk_fma_f16 v9, v17, v33, v9
	v_pk_add_f16 v14, v53, v78
	v_pk_add_f16 v15, v52, v79
	v_pk_add_f16 v16, v51, v80
	v_pk_add_f16 v17, v50, v81
	s_nop 0
	v_exp_f16_sdwa v18, v14 dst_sel:WORD_0 dst_unused:UNUSED_PAD src0_sel:WORD_0
	v_exp_f16_sdwa v19, v15 dst_sel:WORD_0 dst_unused:UNUSED_PAD src0_sel:WORD_0
	v_exp_f16_sdwa v20, v16 dst_sel:WORD_0 dst_unused:UNUSED_PAD src0_sel:WORD_0
	v_exp_f16_sdwa v21, v17 dst_sel:WORD_0 dst_unused:UNUSED_PAD src0_sel:WORD_0
	v_exp_f16_sdwa v18, v14 dst_sel:WORD_1 dst_unused:UNUSED_PRESERVE src0_sel:WORD_1
	v_exp_f16_sdwa v19, v15 dst_sel:WORD_1 dst_unused:UNUSED_PRESERVE src0_sel:WORD_1
	v_exp_f16_sdwa v20, v16 dst_sel:WORD_1 dst_unused:UNUSED_PRESERVE src0_sel:WORD_1
	v_exp_f16_sdwa v21, v17 dst_sel:WORD_1 dst_unused:UNUSED_PRESERVE src0_sel:WORD_1
	s_nop 0
	v_pk_add_f16 v14, v57, v78
	v_pk_add_f16 v13, v13, v21
	v_pk_add_f16 v12, v12, v20
	v_pk_add_f16 v11, v11, v19
	v_pk_add_f16 v10, v10, v18
	v_pk_fma_f16 v9, v29, v21, v9
	v_pk_fma_f16 v8, v28, v20, v8
	v_pk_fma_f16 v7, v27, v19, v7
	v_pk_fma_f16 v6, v26, v18, v6
	v_pk_add_f16 v15, v56, v79
	v_pk_add_f16 v16, v55, v80
	v_pk_add_f16 v17, v54, v81
	s_nop 0
	v_exp_f16_sdwa v18, v14 dst_sel:WORD_0 dst_unused:UNUSED_PAD src0_sel:WORD_0
	v_exp_f16_sdwa v19, v15 dst_sel:WORD_0 dst_unused:UNUSED_PAD src0_sel:WORD_0
	v_exp_f16_sdwa v20, v16 dst_sel:WORD_0 dst_unused:UNUSED_PAD src0_sel:WORD_0
	v_exp_f16_sdwa v21, v17 dst_sel:WORD_0 dst_unused:UNUSED_PAD src0_sel:WORD_0
	v_exp_f16_sdwa v18, v14 dst_sel:WORD_1 dst_unused:UNUSED_PRESERVE src0_sel:WORD_1
	v_exp_f16_sdwa v19, v15 dst_sel:WORD_1 dst_unused:UNUSED_PRESERVE src0_sel:WORD_1
	v_exp_f16_sdwa v20, v16 dst_sel:WORD_1 dst_unused:UNUSED_PRESERVE src0_sel:WORD_1
	v_exp_f16_sdwa v21, v17 dst_sel:WORD_1 dst_unused:UNUSED_PRESERVE src0_sel:WORD_1
	s_nop 0
	v_pk_add_f16 v14, v42, v78
	v_pk_add_f16 v10, v10, v18
	v_pk_add_f16 v11, v11, v19
	v_pk_add_f16 v12, v12, v20
	v_pk_add_f16 v13, v13, v21
	v_pk_fma_f16 v6, v38, v18, v6
	v_pk_fma_f16 v7, v39, v19, v7
	v_pk_fma_f16 v8, v40, v20, v8
	v_pk_fma_f16 v9, v41, v21, v9
	v_pk_add_f16 v15, v43, v79
	v_pk_add_f16 v16, v44, v80
	v_pk_add_f16 v17, v45, v81
	s_nop 0
	v_exp_f16_sdwa v18, v14 dst_sel:WORD_0 dst_unused:UNUSED_PAD src0_sel:WORD_0
	v_exp_f16_sdwa v19, v15 dst_sel:WORD_0 dst_unused:UNUSED_PAD src0_sel:WORD_0
	v_exp_f16_sdwa v20, v16 dst_sel:WORD_0 dst_unused:UNUSED_PAD src0_sel:WORD_0
	v_exp_f16_sdwa v21, v17 dst_sel:WORD_0 dst_unused:UNUSED_PAD src0_sel:WORD_0
	v_exp_f16_sdwa v18, v14 dst_sel:WORD_1 dst_unused:UNUSED_PRESERVE src0_sel:WORD_1
	v_exp_f16_sdwa v19, v15 dst_sel:WORD_1 dst_unused:UNUSED_PRESERVE src0_sel:WORD_1
	v_exp_f16_sdwa v20, v16 dst_sel:WORD_1 dst_unused:UNUSED_PRESERVE src0_sel:WORD_1
	v_exp_f16_sdwa v21, v17 dst_sel:WORD_1 dst_unused:UNUSED_PRESERVE src0_sel:WORD_1
	s_nop 0
	v_pk_add_f16 v14, v69, v78
	v_pk_add_f16 v13, v13, v21
	v_pk_add_f16 v12, v12, v20
	v_pk_add_f16 v11, v11, v19
	v_pk_add_f16 v10, v10, v18
	v_pk_fma_f16 v9, v61, v21, v9
	v_pk_fma_f16 v8, v60, v20, v8
	v_pk_fma_f16 v7, v59, v19, v7
	v_pk_fma_f16 v6, v58, v18, v6
	v_pk_add_f16 v15, v68, v79
	v_pk_add_f16 v16, v67, v80
	v_pk_add_f16 v17, v66, v81
	s_nop 0
	v_exp_f16_sdwa v18, v14 dst_sel:WORD_0 dst_unused:UNUSED_PAD src0_sel:WORD_0
	v_exp_f16_sdwa v19, v15 dst_sel:WORD_0 dst_unused:UNUSED_PAD src0_sel:WORD_0
	v_exp_f16_sdwa v20, v16 dst_sel:WORD_0 dst_unused:UNUSED_PAD src0_sel:WORD_0
	v_exp_f16_sdwa v21, v17 dst_sel:WORD_0 dst_unused:UNUSED_PAD src0_sel:WORD_0
	v_exp_f16_sdwa v18, v14 dst_sel:WORD_1 dst_unused:UNUSED_PRESERVE src0_sel:WORD_1
	v_exp_f16_sdwa v19, v15 dst_sel:WORD_1 dst_unused:UNUSED_PRESERVE src0_sel:WORD_1
	v_exp_f16_sdwa v20, v16 dst_sel:WORD_1 dst_unused:UNUSED_PRESERVE src0_sel:WORD_1
	v_exp_f16_sdwa v21, v17 dst_sel:WORD_1 dst_unused:UNUSED_PRESERVE src0_sel:WORD_1
	s_nop 0
	s_nop 0
	v_pk_add_f16 v10, v10, v18
	v_pk_add_f16 v11, v11, v19
	v_pk_add_f16 v12, v12, v20
	v_pk_add_f16 v13, v13, v21
	v_pk_fma_f16 v14, v70, v18, v6
	v_pk_fma_f16 v15, v71, v19, v7
	v_pk_fma_f16 v16, v72, v20, v8
	v_pk_fma_f16 v17, v73, v21, v9
	v_pk_add_f16 v6, v77, v78
	v_pk_add_f16 v7, v76, v79
	v_pk_add_f16 v8, v75, v80
	v_pk_add_f16 v9, v74, v81
	s_nop 0
	v_exp_f16_sdwa v18, v6 dst_sel:WORD_0 dst_unused:UNUSED_PAD src0_sel:WORD_0
	v_exp_f16_sdwa v19, v7 dst_sel:WORD_0 dst_unused:UNUSED_PAD src0_sel:WORD_0
	v_exp_f16_sdwa v20, v8 dst_sel:WORD_0 dst_unused:UNUSED_PAD src0_sel:WORD_0
	v_exp_f16_sdwa v21, v9 dst_sel:WORD_0 dst_unused:UNUSED_PAD src0_sel:WORD_0
	v_exp_f16_sdwa v18, v6 dst_sel:WORD_1 dst_unused:UNUSED_PRESERVE src0_sel:WORD_1
	v_exp_f16_sdwa v19, v7 dst_sel:WORD_1 dst_unused:UNUSED_PRESERVE src0_sel:WORD_1
	v_exp_f16_sdwa v20, v8 dst_sel:WORD_1 dst_unused:UNUSED_PRESERVE src0_sel:WORD_1
	v_exp_f16_sdwa v21, v9 dst_sel:WORD_1 dst_unused:UNUSED_PRESERVE src0_sel:WORD_1
	s_nop 0
	s_nop 0
	v_pk_add_f16 v9, v13, v21
	v_pk_add_f16 v8, v12, v20
	v_pk_add_f16 v7, v11, v19
	v_pk_add_f16 v6, v10, v18
	v_pk_fma_f16 v13, v93, v21, v17
	v_pk_fma_f16 v12, v92, v20, v16
	v_pk_fma_f16 v11, v91, v19, v15
	v_pk_fma_f16 v10, v90, v18, v14
	v_pk_add_f16 v18, v46, v78
	v_pk_add_f16 v19, v47, v79
	v_pk_add_f16 v20, v48, v80
	v_pk_add_f16 v21, v49, v81
	s_nop 0
	v_exp_f16_sdwa v14, v18 dst_sel:WORD_0 dst_unused:UNUSED_PAD src0_sel:WORD_0
	v_exp_f16_sdwa v17, v19 dst_sel:WORD_0 dst_unused:UNUSED_PAD src0_sel:WORD_0
	v_exp_f16_sdwa v15, v20 dst_sel:WORD_0 dst_unused:UNUSED_PAD src0_sel:WORD_0
	v_exp_f16_sdwa v16, v21 dst_sel:WORD_0 dst_unused:UNUSED_PAD src0_sel:WORD_0
	v_exp_f16_sdwa v14, v18 dst_sel:WORD_1 dst_unused:UNUSED_PRESERVE src0_sel:WORD_1
	v_exp_f16_sdwa v17, v19 dst_sel:WORD_1 dst_unused:UNUSED_PRESERVE src0_sel:WORD_1
	v_exp_f16_sdwa v15, v20 dst_sel:WORD_1 dst_unused:UNUSED_PRESERVE src0_sel:WORD_1
	v_exp_f16_sdwa v16, v21 dst_sel:WORD_1 dst_unused:UNUSED_PRESERVE src0_sel:WORD_1
	s_nop 0

.LBB3_7:
	v_add_u32_e32 v182, s33, v161
	v_add_u32_e32 v181, -1, v182
	v_or_b32_e32 v2, v181, v164
	v_add_u32_e32 v180, 0x18400, v171
	v_cmp_gt_u32_e64 s[0:1], 64, v2
	s_mov_b64 s[4:5], -1
	s_and_b64 vcc, exec, s[24:25]
	s_cbranch_vccz .LBB3_45
	v_cmp_lt_u32_e64 s[64:65], 0, v182
	v_cmp_gt_u32_e64 s[66:67], 63, v182
	v_cmp_lt_u32_e64 s[68:69], 0, v162
	v_cmp_gt_u32_e64 s[70:71], 60, v162
	buffer_load_dwordx4 v[186:189], v180, s[16:19], 0 offen
	v_add_u32_e32 v250, 0x18000, v180
	buffer_load_dwordx4 v[154:157], v250, s[16:19], 0 offen
	v_add_u32_e32 v249, 0x30000, v180
	buffer_load_dwordx4 v[150:153], v249, s[16:19], 0 offen
	v_add_u32_e32 v250, 0x48000, v180
	buffer_load_dwordx4 v[146:149], v250, s[16:19], 0 offen
	s_and_b64 s[72:73], s[68:69], s[64:65]
	s_and_b64 s[74:75], s[68:69], s[66:67]
	s_and_b64 s[76:77], s[70:71], s[64:65]
	s_and_b64 s[78:79], s[70:71], s[66:67]
	v_add_u32_e32 v249, 0xfffe7c00, v180
	v_add_u32_e32 v250, 0xfffe8000, v180
	v_mov_b32_e32 v110, v172
	v_mov_b32_e32 v111, v174
	v_mov_b32_e32 v112, v176
	v_mov_b32_e32 v113, v178
	v_mov_b32_e32 v70, v173
	v_mov_b32_e32 v71, v175
	v_mov_b32_e32 v72, v177
	v_mov_b32_e32 v73, v179
	v_mov_b32_e32 v126, v172
	v_mov_b32_e32 v127, v174
	v_mov_b32_e32 v128, v176
	v_mov_b32_e32 v129, v178
	v_mov_b32_e32 v98, v173
	v_mov_b32_e32 v99, v175
	v_mov_b32_e32 v100, v177
	v_mov_b32_e32 v101, v179
	v_mov_b32_e32 v134, v172
	v_mov_b32_e32 v135, v174
	v_mov_b32_e32 v136, v176
	v_mov_b32_e32 v137, v178
	v_mov_b32_e32 v114, v173
	v_mov_b32_e32 v115, v175
	v_mov_b32_e32 v116, v177
	v_mov_b32_e32 v117, v179
	s_mov_b64 exec, s[72:73]
	buffer_load_dwordx4 v[110:113], v249, s[16:19], 0 offen
	buffer_load_dwordx4 v[70:73], v249, s[16:19], 0 offen offset:512
	s_mov_b64 exec, -1
	s_mov_b64 exec, s[68:69]
	buffer_load_dwordx4 v[126:129], v250, s[16:19], 0 offen offset:512
	buffer_load_dwordx4 v[98:101], v250, s[16:19], 0 offen offset:1024
	s_mov_b64 exec, -1
	s_mov_b64 exec, s[74:75]
	buffer_load_dwordx4 v[134:137], v250, s[16:19], 0 offen offset:2048
	buffer_load_dwordx4 v[114:117], v250, s[16:19], 0 offen offset:2560
	s_mov_b64 exec, -1
	v_add_u32_e32 v249, 0xfffffc00, v180
	v_mov_b32_e32 v82, v172
	v_mov_b32_e32 v83, v174
	v_mov_b32_e32 v84, v176
	v_mov_b32_e32 v85, v178
	v_mov_b32_e32 v42, v173
	v_mov_b32_e32 v43, v175
	v_mov_b32_e32 v44, v177
	v_mov_b32_e32 v45, v179
	v_mov_b32_e32 v122, v172
	v_mov_b32_e32 v123, v174
	v_mov_b32_e32 v124, v176
	v_mov_b32_e32 v125, v178
	v_mov_b32_e32 v86, v173
	v_mov_b32_e32 v87, v175
	v_mov_b32_e32 v88, v177
	v_mov_b32_e32 v89, v179
	s_mov_b64 exec, s[64:65]
	buffer_load_dwordx4 v[82:85], v249, s[16:19], 0 offen
	buffer_load_dwordx4 v[42:45], v249, s[16:19], 0 offen offset:512
	s_mov_b64 exec, -1
	buffer_load_dwordx4 v[106:109], v180, s[16:19], 0 offen offset:512
	buffer_load_dwordx4 v[62:65], v180, s[16:19], 0 offen offset:1024
	s_mov_b64 exec, s[66:67]
	buffer_load_dwordx4 v[122:125], v180, s[16:19], 0 offen offset:2048
	buffer_load_dwordx4 v[86:89], v180, s[16:19], 0 offen offset:2560
	s_mov_b64 exec, -1
	v_add_u32_e32 v249, 0x17c00, v180
	v_add_u32_e32 v250, 0x18000, v180
	v_mov_b32_e32 v50, v172
	v_mov_b32_e32 v51, v174
	v_mov_b32_e32 v52, v176
	v_mov_b32_e32 v53, v178
	v_mov_b32_e32 v22, v173
	v_mov_b32_e32 v23, v175
	v_mov_b32_e32 v24, v177
	v_mov_b32_e32 v25, v179
	v_mov_b32_e32 v94, v172
	v_mov_b32_e32 v95, v174
	v_mov_b32_e32 v96, v176
	v_mov_b32_e32 v97, v178
	v_mov_b32_e32 v46, v173
	v_mov_b32_e32 v47, v175
	v_mov_b32_e32 v48, v177
	v_mov_b32_e32 v49, v179
	s_mov_b64 exec, s[64:65]
	buffer_load_dwordx4 v[50:53], v249, s[16:19], 0 offen
	buffer_load_dwordx4 v[22:25], v249, s[16:19], 0 offen offset:512
	s_mov_b64 exec, -1
	buffer_load_dwordx4 v[66:69], v250, s[16:19], 0 offen offset:512
	buffer_load_dwordx4 v[30:33], v250, s[16:19], 0 offen offset:1024
	s_mov_b64 exec, s[66:67]
	buffer_load_dwordx4 v[94:97], v250, s[16:19], 0 offen offset:2048
	buffer_load_dwordx4 v[46:49], v250, s[16:19], 0 offen offset:2560
	s_mov_b64 exec, -1
	v_add_u32_e32 v249, 0x2fc00, v180
	v_add_u32_e32 v250, 0x30000, v180
	v_mov_b32_e32 v18, v172
	v_mov_b32_e32 v19, v174
	v_mov_b32_e32 v20, v176
	v_mov_b32_e32 v21, v178
	v_mov_b32_e32 v6, v173
	v_mov_b32_e32 v7, v175
	v_mov_b32_e32 v8, v177
	v_mov_b32_e32 v9, v179
	v_mov_b32_e32 v54, v172
	v_mov_b32_e32 v55, v174
	v_mov_b32_e32 v56, v176
	v_mov_b32_e32 v57, v178
	v_mov_b32_e32 v14, v173
	v_mov_b32_e32 v15, v175
	v_mov_b32_e32 v16, v177
	v_mov_b32_e32 v17, v179
	s_mov_b64 exec, s[64:65]
	buffer_load_dwordx4 v[18:21], v249, s[16:19], 0 offen
	buffer_load_dwordx4 v[6:9], v249, s[16:19], 0 offen offset:512
	s_mov_b64 exec, -1
	buffer_load_dwordx4 v[34:37], v250, s[16:19], 0 offen offset:512
	buffer_load_dwordx4 v[10:13], v250, s[16:19], 0 offen offset:1024
	s_mov_b64 exec, s[66:67]
	buffer_load_dwordx4 v[54:57], v250, s[16:19], 0 offen offset:2048
	buffer_load_dwordx4 v[14:17], v250, s[16:19], 0 offen offset:2560
	s_mov_b64 exec, -1
	v_add_u32_e32 v249, 0x47c00, v180
	v_add_u32_e32 v250, 0x48000, v180
	v_mov_b32_e32 v74, v172
	v_mov_b32_e32 v75, v174
	v_mov_b32_e32 v76, v176
	v_mov_b32_e32 v77, v178
	v_mov_b32_e32 v26, v173
	v_mov_b32_e32 v27, v175
	v_mov_b32_e32 v28, v177
	v_mov_b32_e32 v29, v179
	v_mov_b32_e32 v118, v172
	v_mov_b32_e32 v119, v174
	v_mov_b32_e32 v120, v176
	v_mov_b32_e32 v121, v178
	v_mov_b32_e32 v58, v173
	v_mov_b32_e32 v59, v175
	v_mov_b32_e32 v60, v177
	v_mov_b32_e32 v61, v179
	s_mov_b64 exec, s[64:65]
	buffer_load_dwordx4 v[74:77], v249, s[16:19], 0 offen
	buffer_load_dwordx4 v[26:29], v249, s[16:19], 0 offen offset:512
	s_mov_b64 exec, -1
	buffer_load_dwordx4 v[102:105], v250, s[16:19], 0 offen offset:512
	buffer_load_dwordx4 v[38:41], v250, s[16:19], 0 offen offset:1024
	s_mov_b64 exec, s[66:67]
	buffer_load_dwordx4 v[118:121], v250, s[16:19], 0 offen offset:2048
	buffer_load_dwordx4 v[58:61], v250, s[16:19], 0 offen offset:2560
	s_mov_b64 exec, -1
	v_add_u32_e32 v249, 0x5fc00, v180
	v_add_u32_e32 v250, 0x60000, v180
	v_mov_b32_e32 v130, v172
	v_mov_b32_e32 v131, v174
	v_mov_b32_e32 v132, v176
	v_mov_b32_e32 v133, v178
	v_mov_b32_e32 v78, v173
	v_mov_b32_e32 v79, v175
	v_mov_b32_e32 v80, v177
	v_mov_b32_e32 v81, v179
	v_mov_b32_e32 v138, v172
	v_mov_b32_e32 v139, v174
	v_mov_b32_e32 v140, v176
	v_mov_b32_e32 v141, v178
	v_mov_b32_e32 v90, v173
	v_mov_b32_e32 v91, v175
	v_mov_b32_e32 v92, v177
	v_mov_b32_e32 v93, v179
	v_mov_b32_e32 v142, v172
	v_mov_b32_e32 v143, v174
	v_mov_b32_e32 v144, v176
	v_mov_b32_e32 v145, v178
	v_mov_b32_e32 v2, v173
	v_mov_b32_e32 v3, v175
	v_mov_b32_e32 v4, v177
	v_mov_b32_e32 v5, v179
	s_mov_b64 exec, s[76:77]
	buffer_load_dwordx4 v[130:133], v249, s[16:19], 0 offen
	buffer_load_dwordx4 v[78:81], v249, s[16:19], 0 offen offset:512
	s_mov_b64 exec, -1
	s_mov_b64 exec, s[70:71]
	buffer_load_dwordx4 v[138:141], v250, s[16:19], 0 offen offset:512
	buffer_load_dwordx4 v[90:93], v250, s[16:19], 0 offen offset:1024
	s_mov_b64 exec, -1
	s_mov_b64 exec, s[78:79]
	buffer_load_dwordx4 v[142:145], v250, s[16:19], 0 offen offset:2048
	buffer_load_dwordx4 v[2:5], v250, s[16:19], 0 offen offset:2560
	s_mov_b64 exec, -1
	s_load_dwordx2 s[4:5], s[22:23], 0x20
	s_waitcnt lgkmcnt(0)
	s_load_dwordx2 s[26:27], s[4:5], 0x0
	s_load_dword s34, s[4:5], 0x8
	s_waitcnt lgkmcnt(0)
	v_cvt_f16_f32_e32 v183, s27
	v_cvt_f16_f32_e32 v185, s26
	v_cvt_f16_f32_e32 v184, s34
	s_mov_b64 s[4:5], 0
	s_waitcnt vmcnt(18)
	v_pk_mul_f16 v193, v185, v189 op_sel_hi:[0,1]
	v_pk_mul_f16 v197, v183, v189 op_sel_hi:[0,1]
	v_pk_mul_f16 v201, v184, v189 op_sel_hi:[0,1]
	v_pk_mul_f16 v190, v185, v186 op_sel_hi:[0,1]
	v_pk_mul_f16 v191, v185, v187 op_sel_hi:[0,1]
	v_pk_mul_f16 v192, v185, v188 op_sel_hi:[0,1]
	v_pk_mul_f16 v194, v183, v186 op_sel_hi:[0,1]
	v_pk_mul_f16 v195, v183, v187 op_sel_hi:[0,1]
	v_pk_mul_f16 v196, v183, v188 op_sel_hi:[0,1]
	v_pk_mul_f16 v198, v184, v186 op_sel_hi:[0,1]
	v_pk_mul_f16 v199, v184, v187 op_sel_hi:[0,1]
	v_pk_mul_f16 v200, v184, v188 op_sel_hi:[0,1]
	v_pk_fma_f16 v113, v113, v189, v193
	v_pk_fma_f16 v129, v129, v189, v197
	v_pk_fma_f16 v137, v137, v189, v201
	v_pk_fma_f16 v202, v85, v189, v193
	v_pk_fma_f16 v206, v109, v189, v197
	v_pk_fma_f16 v210, v125, v189, v201
	v_pk_fma_f16 v193, v53, v189, v193
	v_pk_fma_f16 v197, v69, v189, v197
	v_pk_fma_f16 v189, v97, v189, v201
	v_pk_maximum3_f16 v201, v113, v129, v137
	v_pk_fma_f16 v112, v112, v188, v192
	v_pk_fma_f16 v111, v111, v187, v191
	v_pk_fma_f16 v110, v110, v186, v190
	v_pk_fma_f16 v128, v128, v188, v196
	v_pk_fma_f16 v127, v127, v187, v195
	v_pk_fma_f16 v126, v126, v186, v194
	v_pk_fma_f16 v136, v136, v188, v200
	v_pk_fma_f16 v135, v135, v187, v199
	v_pk_fma_f16 v134, v134, v186, v198
	v_pk_fma_f16 v203, v84, v188, v192
	v_pk_fma_f16 v204, v83, v187, v191
	v_pk_fma_f16 v205, v82, v186, v190
	v_pk_fma_f16 v207, v108, v188, v196
	v_pk_fma_f16 v208, v107, v187, v195
	v_pk_fma_f16 v209, v106, v186, v194
	v_pk_fma_f16 v211, v124, v188, v200
	v_pk_fma_f16 v212, v123, v187, v199
	v_pk_fma_f16 v213, v122, v186, v198
	v_pk_fma_f16 v192, v52, v188, v192
	v_pk_fma_f16 v191, v51, v187, v191
	v_pk_fma_f16 v190, v50, v186, v190
	v_pk_fma_f16 v196, v68, v188, v196
	v_pk_fma_f16 v195, v67, v187, v195
	v_pk_fma_f16 v194, v66, v186, v194
	v_pk_fma_f16 v188, v96, v188, v200
	v_pk_fma_f16 v187, v95, v187, v199
	v_pk_fma_f16 v186, v94, v186, v198
	v_pk_maximum3_f16 v198, v110, v126, v134
	v_pk_maximum3_f16 v199, v111, v127, v135
	v_pk_maximum3_f16 v200, v112, v128, v136
	v_pk_maximum3_f16 v217, v202, v206, v210
	v_pk_maximum3_f16 v221, v193, v197, v189
	v_pk_maximum3_f16 v214, v205, v209, v213
	v_pk_maximum3_f16 v215, v204, v208, v212
	v_pk_maximum3_f16 v216, v203, v207, v211
	s_nop 0
	v_pk_maximum3_f16 v218, v190, v194, v186
	v_pk_maximum3_f16 v219, v191, v195, v187
	v_pk_maximum3_f16 v201, v201, v217, v221
	v_pk_maximum3_f16 v220, v192, v196, v188
	s_nop 0
	v_pk_maximum3_f16 v198, v198, v214, v218
	v_pk_maximum3_f16 v199, v199, v215, v219
	v_pk_maximum3_f16 v200, v200, v216, v220
	v_xor_b32_e32 v201, 0x80008000, v201
	v_xor_b32_e32 v200, 0x80008000, v200
	v_xor_b32_e32 v199, 0x80008000, v199
	v_xor_b32_e32 v198, 0x80008000, v198
	v_pk_add_f16 v113, v113, v201
	v_pk_add_f16 v110, v110, v198
	v_pk_add_f16 v111, v111, v199
	v_pk_add_f16 v112, v112, v200
	v_pk_add_f16 v126, v126, v198
	v_exp_f16_sdwa v214, v110 dst_sel:WORD_0 dst_unused:UNUSED_PAD src0_sel:WORD_0
	v_exp_f16_sdwa v215, v111 dst_sel:WORD_0 dst_unused:UNUSED_PAD src0_sel:WORD_0
	v_exp_f16_sdwa v216, v112 dst_sel:WORD_0 dst_unused:UNUSED_PAD src0_sel:WORD_0
	v_exp_f16_sdwa v217, v113 dst_sel:WORD_0 dst_unused:UNUSED_PAD src0_sel:WORD_0
	v_exp_f16_sdwa v214, v110 dst_sel:WORD_1 dst_unused:UNUSED_PRESERVE src0_sel:WORD_1
	v_exp_f16_sdwa v215, v111 dst_sel:WORD_1 dst_unused:UNUSED_PRESERVE src0_sel:WORD_1
	v_exp_f16_sdwa v216, v112 dst_sel:WORD_1 dst_unused:UNUSED_PRESERVE src0_sel:WORD_1
	v_exp_f16_sdwa v217, v113 dst_sel:WORD_1 dst_unused:UNUSED_PRESERVE src0_sel:WORD_1
	s_nop 0
	v_pk_add_f16 v127, v127, v199
	v_pk_add_f16 v113, v214, 0
	v_pk_fma_f16 v73, v73, v217, 0
	v_pk_add_f16 v110, v217, 0
	v_pk_add_f16 v111, v216, 0
	v_pk_add_f16 v112, v215, 0
	v_pk_fma_f16 v72, v72, v216, 0
	v_pk_fma_f16 v71, v71, v215, 0
	v_pk_fma_f16 v70, v70, v214, 0
	v_pk_add_f16 v128, v128, v200
	v_pk_add_f16 v129, v129, v201
	s_nop 0
	v_exp_f16_sdwa v214, v126 dst_sel:WORD_0 dst_unused:UNUSED_PAD src0_sel:WORD_0
	v_exp_f16_sdwa v215, v127 dst_sel:WORD_0 dst_unused:UNUSED_PAD src0_sel:WORD_0
	v_exp_f16_sdwa v216, v128 dst_sel:WORD_0 dst_unused:UNUSED_PAD src0_sel:WORD_0
	v_exp_f16_sdwa v217, v129 dst_sel:WORD_0 dst_unused:UNUSED_PAD src0_sel:WORD_0
	v_exp_f16_sdwa v214, v126 dst_sel:WORD_1 dst_unused:UNUSED_PRESERVE src0_sel:WORD_1
	v_exp_f16_sdwa v215, v127 dst_sel:WORD_1 dst_unused:UNUSED_PRESERVE src0_sel:WORD_1
	v_exp_f16_sdwa v216, v128 dst_sel:WORD_1 dst_unused:UNUSED_PRESERVE src0_sel:WORD_1
	v_exp_f16_sdwa v217, v129 dst_sel:WORD_1 dst_unused:UNUSED_PRESERVE src0_sel:WORD_1
	s_nop 0
	s_nop 0
	v_pk_add_f16 v113, v113, v214
	v_pk_fma_f16 v73, v101, v217, v73
	v_pk_add_f16 v101, v137, v201
	v_pk_add_f16 v112, v112, v215
	v_pk_add_f16 v111, v111, v216
	v_pk_add_f16 v110, v110, v217
	v_pk_fma_f16 v70, v98, v214, v70
	v_pk_fma_f16 v71, v99, v215, v71
	v_pk_fma_f16 v72, v100, v216, v72
	v_pk_add_f16 v98, v134, v198
	v_pk_add_f16 v99, v135, v199
	v_pk_add_f16 v100, v136, v200
	s_nop 0
	v_exp_f16_sdwa v126, v98 dst_sel:WORD_0 dst_unused:UNUSED_PAD src0_sel:WORD_0
	v_exp_f16_sdwa v127, v99 dst_sel:WORD_0 dst_unused:UNUSED_PAD src0_sel:WORD_0
	v_exp_f16_sdwa v128, v100 dst_sel:WORD_0 dst_unused:UNUSED_PAD src0_sel:WORD_0
	v_exp_f16_sdwa v129, v101 dst_sel:WORD_0 dst_unused:UNUSED_PAD src0_sel:WORD_0
	v_exp_f16_sdwa v126, v98 dst_sel:WORD_1 dst_unused:UNUSED_PRESERVE src0_sel:WORD_1
	v_exp_f16_sdwa v127, v99 dst_sel:WORD_1 dst_unused:UNUSED_PRESERVE src0_sel:WORD_1
	v_exp_f16_sdwa v128, v100 dst_sel:WORD_1 dst_unused:UNUSED_PRESERVE src0_sel:WORD_1
	v_exp_f16_sdwa v129, v101 dst_sel:WORD_1 dst_unused:UNUSED_PRESERVE src0_sel:WORD_1
	s_nop 0
	s_nop 0
	v_pk_add_f16 v101, v113, v126
	v_pk_add_f16 v98, v110, v129
	v_pk_add_f16 v99, v111, v128
	v_pk_add_f16 v100, v112, v127
	v_pk_fma_f16 v73, v117, v129, v73
	v_pk_fma_f16 v72, v116, v128, v72
	v_pk_fma_f16 v71, v115, v127, v71
	v_pk_fma_f16 v70, v114, v126, v70
	v_pk_add_f16 v110, v205, v198
	v_pk_add_f16 v111, v204, v199
	v_pk_add_f16 v112, v203, v200
	v_pk_add_f16 v113, v202, v201
	s_nop 0
	v_exp_f16_sdwa v114, v110 dst_sel:WORD_0 dst_unused:UNUSED_PAD src0_sel:WORD_0
	v_exp_f16_sdwa v115, v111 dst_sel:WORD_0 dst_unused:UNUSED_PAD src0_sel:WORD_0
	v_exp_f16_sdwa v116, v112 dst_sel:WORD_0 dst_unused:UNUSED_PAD src0_sel:WORD_0
	v_exp_f16_sdwa v117, v113 dst_sel:WORD_0 dst_unused:UNUSED_PAD src0_sel:WORD_0
	v_exp_f16_sdwa v114, v110 dst_sel:WORD_1 dst_unused:UNUSED_PRESERVE src0_sel:WORD_1
	v_exp_f16_sdwa v115, v111 dst_sel:WORD_1 dst_unused:UNUSED_PRESERVE src0_sel:WORD_1
	v_exp_f16_sdwa v116, v112 dst_sel:WORD_1 dst_unused:UNUSED_PRESERVE src0_sel:WORD_1
	v_exp_f16_sdwa v117, v113 dst_sel:WORD_1 dst_unused:UNUSED_PRESERVE src0_sel:WORD_1
	s_nop 0
	v_pk_add_f16 v110, v209, v198
	v_pk_add_f16 v101, v101, v114
	v_pk_add_f16 v100, v100, v115
	v_pk_add_f16 v99, v99, v116
	v_pk_add_f16 v98, v98, v117
	v_pk_fma_f16 v70, v42, v114, v70
	v_pk_fma_f16 v71, v43, v115, v71
	v_pk_fma_f16 v72, v44, v116, v72
	v_pk_fma_f16 v73, v45, v117, v73
	v_pk_add_f16 v111, v208, v199
	v_pk_add_f16 v112, v207, v200
	v_pk_add_f16 v113, v206, v201
	s_nop 0
	v_exp_f16_sdwa v114, v110 dst_sel:WORD_0 dst_unused:UNUSED_PAD src0_sel:WORD_0
	v_exp_f16_sdwa v115, v111 dst_sel:WORD_0 dst_unused:UNUSED_PAD src0_sel:WORD_0
	v_exp_f16_sdwa v116, v112 dst_sel:WORD_0 dst_unused:UNUSED_PAD src0_sel:WORD_0
	v_exp_f16_sdwa v117, v113 dst_sel:WORD_0 dst_unused:UNUSED_PAD src0_sel:WORD_0
	v_exp_f16_sdwa v114, v110 dst_sel:WORD_1 dst_unused:UNUSED_PRESERVE src0_sel:WORD_1
	v_exp_f16_sdwa v115, v111 dst_sel:WORD_1 dst_unused:UNUSED_PRESERVE src0_sel:WORD_1
	v_exp_f16_sdwa v116, v112 dst_sel:WORD_1 dst_unused:UNUSED_PRESERVE src0_sel:WORD_1
	v_exp_f16_sdwa v117, v113 dst_sel:WORD_1 dst_unused:UNUSED_PRESERVE src0_sel:WORD_1
	s_nop 0
	v_pk_add_f16 v110, v213, v198
	v_pk_add_f16 v101, v101, v114
	v_pk_add_f16 v98, v98, v117
	v_pk_add_f16 v99, v99, v116
	v_pk_add_f16 v100, v100, v115
	v_pk_fma_f16 v73, v65, v117, v73
	v_pk_fma_f16 v72, v64, v116, v72
	v_pk_fma_f16 v71, v63, v115, v71
	v_pk_fma_f16 v70, v62, v114, v70
	v_pk_add_f16 v111, v212, v199
	v_pk_add_f16 v112, v211, v200
	v_pk_add_f16 v113, v210, v201
	s_nop 0
	v_exp_f16_sdwa v114, v110 dst_sel:WORD_0 dst_unused:UNUSED_PAD src0_sel:WORD_0
	v_exp_f16_sdwa v115, v111 dst_sel:WORD_0 dst_unused:UNUSED_PAD src0_sel:WORD_0
	v_exp_f16_sdwa v116, v112 dst_sel:WORD_0 dst_unused:UNUSED_PAD src0_sel:WORD_0
	v_exp_f16_sdwa v117, v113 dst_sel:WORD_0 dst_unused:UNUSED_PAD src0_sel:WORD_0
	v_exp_f16_sdwa v114, v110 dst_sel:WORD_1 dst_unused:UNUSED_PRESERVE src0_sel:WORD_1
	v_exp_f16_sdwa v115, v111 dst_sel:WORD_1 dst_unused:UNUSED_PRESERVE src0_sel:WORD_1
	v_exp_f16_sdwa v116, v112 dst_sel:WORD_1 dst_unused:UNUSED_PRESERVE src0_sel:WORD_1
	v_exp_f16_sdwa v117, v113 dst_sel:WORD_1 dst_unused:UNUSED_PRESERVE src0_sel:WORD_1
	s_nop 0
	v_pk_add_f16 v110, v190, v198
	v_pk_add_f16 v101, v101, v114
	v_pk_add_f16 v100, v100, v115
	v_pk_add_f16 v99, v99, v116
	v_pk_add_f16 v98, v98, v117
	v_pk_fma_f16 v70, v86, v114, v70
	v_pk_fma_f16 v71, v87, v115, v71
	v_pk_fma_f16 v72, v88, v116, v72
	v_pk_fma_f16 v73, v89, v117, v73
	v_pk_add_f16 v111, v191, v199
	v_pk_add_f16 v112, v192, v200
	v_pk_add_f16 v113, v193, v201
	s_nop 0
	v_exp_f16_sdwa v114, v110 dst_sel:WORD_0 dst_unused:UNUSED_PAD src0_sel:WORD_0
	v_exp_f16_sdwa v115, v111 dst_sel:WORD_0 dst_unused:UNUSED_PAD src0_sel:WORD_0
	v_exp_f16_sdwa v116, v112 dst_sel:WORD_0 dst_unused:UNUSED_PAD src0_sel:WORD_0
	v_exp_f16_sdwa v117, v113 dst_sel:WORD_0 dst_unused:UNUSED_PAD src0_sel:WORD_0
	v_exp_f16_sdwa v114, v110 dst_sel:WORD_1 dst_unused:UNUSED_PRESERVE src0_sel:WORD_1
	v_exp_f16_sdwa v115, v111 dst_sel:WORD_1 dst_unused:UNUSED_PRESERVE src0_sel:WORD_1
	v_exp_f16_sdwa v116, v112 dst_sel:WORD_1 dst_unused:UNUSED_PRESERVE src0_sel:WORD_1
	v_exp_f16_sdwa v117, v113 dst_sel:WORD_1 dst_unused:UNUSED_PRESERVE src0_sel:WORD_1
	s_nop 0
	v_pk_add_f16 v110, v194, v198
	v_pk_add_f16 v101, v101, v114
	v_pk_add_f16 v98, v98, v117
	v_pk_add_f16 v99, v99, v116
	v_pk_add_f16 v100, v100, v115
	v_pk_fma_f16 v73, v25, v117, v73
	v_pk_fma_f16 v72, v24, v116, v72
	v_pk_fma_f16 v71, v23, v115, v71
	v_pk_fma_f16 v70, v22, v114, v70
	v_pk_add_f16 v111, v195, v199
	v_pk_add_f16 v112, v196, v200
	v_pk_add_f16 v113, v197, v201
	s_nop 0
	v_exp_f16_sdwa v114, v110 dst_sel:WORD_0 dst_unused:UNUSED_PAD src0_sel:WORD_0
	v_exp_f16_sdwa v115, v111 dst_sel:WORD_0 dst_unused:UNUSED_PAD src0_sel:WORD_0
	v_exp_f16_sdwa v116, v112 dst_sel:WORD_0 dst_unused:UNUSED_PAD src0_sel:WORD_0
	v_exp_f16_sdwa v117, v113 dst_sel:WORD_0 dst_unused:UNUSED_PAD src0_sel:WORD_0
	v_exp_f16_sdwa v114, v110 dst_sel:WORD_1 dst_unused:UNUSED_PRESERVE src0_sel:WORD_1
	v_exp_f16_sdwa v115, v111 dst_sel:WORD_1 dst_unused:UNUSED_PRESERVE src0_sel:WORD_1
	v_exp_f16_sdwa v116, v112 dst_sel:WORD_1 dst_unused:UNUSED_PRESERVE src0_sel:WORD_1
	v_exp_f16_sdwa v117, v113 dst_sel:WORD_1 dst_unused:UNUSED_PRESERVE src0_sel:WORD_1
	s_nop 0
	v_pk_add_f16 v110, v186, v198
	v_pk_add_f16 v101, v101, v114
	v_pk_add_f16 v100, v100, v115
	v_pk_add_f16 v99, v99, v116
	v_pk_add_f16 v98, v98, v117
	v_pk_fma_f16 v70, v30, v114, v70
	v_pk_fma_f16 v71, v31, v115, v71
	v_pk_fma_f16 v72, v32, v116, v72
	v_pk_fma_f16 v73, v33, v117, v73
	v_pk_add_f16 v111, v187, v199
	v_pk_add_f16 v112, v188, v200
	v_pk_add_f16 v113, v189, v201
	s_nop 0
	v_exp_f16_sdwa v114, v110 dst_sel:WORD_0 dst_unused:UNUSED_PAD src0_sel:WORD_0
	v_exp_f16_sdwa v115, v111 dst_sel:WORD_0 dst_unused:UNUSED_PAD src0_sel:WORD_0
	v_exp_f16_sdwa v116, v112 dst_sel:WORD_0 dst_unused:UNUSED_PAD src0_sel:WORD_0
	v_exp_f16_sdwa v117, v113 dst_sel:WORD_0 dst_unused:UNUSED_PAD src0_sel:WORD_0
	v_exp_f16_sdwa v114, v110 dst_sel:WORD_1 dst_unused:UNUSED_PRESERVE src0_sel:WORD_1
	v_exp_f16_sdwa v115, v111 dst_sel:WORD_1 dst_unused:UNUSED_PRESERVE src0_sel:WORD_1
	v_exp_f16_sdwa v116, v112 dst_sel:WORD_1 dst_unused:UNUSED_PRESERVE src0_sel:WORD_1
	v_exp_f16_sdwa v117, v113 dst_sel:WORD_1 dst_unused:UNUSED_PRESERVE src0_sel:WORD_1
	s_nop 0
	s_nop 0
	v_pk_add_f16 v101, v101, v114
	v_pk_add_f16 v100, v100, v115
	v_rcp_f16_e32 v110, v101
	v_rcp_f16_sdwa v101, v101 dst_sel:DWORD dst_unused:UNUSED_PAD src0_sel:WORD_1
	v_pk_add_f16 v99, v99, v116
	v_rcp_f16_e32 v111, v100
	v_rcp_f16_sdwa v100, v100 dst_sel:DWORD dst_unused:UNUSED_PAD src0_sel:WORD_1
	v_pk_add_f16 v98, v98, v117
	v_rcp_f16_e32 v112, v99
	v_rcp_f16_sdwa v99, v99 dst_sel:DWORD dst_unused:UNUSED_PAD src0_sel:WORD_1
	v_rcp_f16_e32 v113, v98
	v_rcp_f16_sdwa v98, v98 dst_sel:DWORD dst_unused:UNUSED_PAD src0_sel:WORD_1
	v_pk_fma_f16 v70, v46, v114, v70
	v_pack_b32_f16 v101, v110, v101
	v_pk_fma_f16 v71, v47, v115, v71
	v_pk_mul_f16 v110, v70, v101
	v_pack_b32_f16 v70, v111, v100
	v_pk_fma_f16 v72, v48, v116, v72
	v_pk_mul_f16 v111, v71, v70
	v_pack_b32_f16 v70, v112, v99
	v_pk_fma_f16 v73, v49, v117, v73
	v_pk_mul_f16 v112, v72, v70
	v_pack_b32_f16 v70, v113, v98
	v_pk_mul_f16 v113, v73, v70
	s_waitcnt vmcnt(12)
	v_pk_mul_f16 v73, v185, v157 op_sel_hi:[0,1]
	v_pk_mul_f16 v101, v183, v157 op_sel_hi:[0,1]
	v_pk_mul_f16 v117, v184, v157 op_sel_hi:[0,1]
	v_pk_mul_f16 v70, v185, v154 op_sel_hi:[0,1]
	v_pk_mul_f16 v71, v185, v155 op_sel_hi:[0,1]
	v_pk_mul_f16 v72, v185, v156 op_sel_hi:[0,1]
	v_pk_mul_f16 v98, v183, v154 op_sel_hi:[0,1]
	v_pk_mul_f16 v99, v183, v155 op_sel_hi:[0,1]
	v_pk_mul_f16 v100, v183, v156 op_sel_hi:[0,1]
	v_pk_mul_f16 v114, v184, v154 op_sel_hi:[0,1]
	v_pk_mul_f16 v115, v184, v155 op_sel_hi:[0,1]
	v_pk_mul_f16 v116, v184, v156 op_sel_hi:[0,1]
	v_pk_fma_f16 v85, v85, v157, v73
	v_pk_fma_f16 v109, v109, v157, v101
	v_pk_fma_f16 v125, v125, v157, v117
	v_pk_fma_f16 v126, v53, v157, v73
	v_pk_fma_f16 v134, v69, v157, v101
	v_pk_fma_f16 v186, v97, v157, v117
	v_pk_fma_f16 v73, v21, v157, v73
	v_pk_fma_f16 v101, v37, v157, v101
	v_pk_fma_f16 v117, v57, v157, v117
	v_pk_maximum3_f16 v157, v85, v109, v125
	v_pk_fma_f16 v84, v84, v156, v72
	v_pk_fma_f16 v83, v83, v155, v71
	v_pk_fma_f16 v82, v82, v154, v70
	v_pk_fma_f16 v108, v108, v156, v100
	v_pk_fma_f16 v107, v107, v155, v99
	v_pk_fma_f16 v106, v106, v154, v98
	v_pk_fma_f16 v124, v124, v156, v116
	v_pk_fma_f16 v123, v123, v155, v115
	v_pk_fma_f16 v122, v122, v154, v114
	v_pk_fma_f16 v127, v52, v156, v72
	v_pk_fma_f16 v128, v51, v155, v71
	v_pk_fma_f16 v129, v50, v154, v70
	v_pk_fma_f16 v135, v68, v156, v100
	v_pk_fma_f16 v136, v67, v155, v99
	v_pk_fma_f16 v137, v66, v154, v98
	v_pk_fma_f16 v187, v96, v156, v116
	v_pk_fma_f16 v188, v95, v155, v115
	v_pk_fma_f16 v189, v94, v154, v114
	v_pk_fma_f16 v72, v20, v156, v72
	v_pk_fma_f16 v71, v19, v155, v71
	v_pk_fma_f16 v70, v18, v154, v70
	v_pk_fma_f16 v100, v36, v156, v100
	v_pk_fma_f16 v99, v35, v155, v99
	v_pk_fma_f16 v98, v34, v154, v98
	v_pk_fma_f16 v116, v56, v156, v116
	v_pk_fma_f16 v115, v55, v155, v115
	v_pk_fma_f16 v114, v54, v154, v114
	v_pk_maximum3_f16 v154, v82, v106, v122
	v_pk_maximum3_f16 v155, v83, v107, v123
	v_pk_maximum3_f16 v156, v84, v108, v124
	v_pk_maximum3_f16 v193, v126, v134, v186
	v_pk_maximum3_f16 v197, v73, v101, v117
	v_pk_maximum3_f16 v190, v129, v137, v189
	v_pk_maximum3_f16 v191, v128, v136, v188
	v_pk_maximum3_f16 v192, v127, v135, v187
	s_nop 0
	v_pk_maximum3_f16 v194, v70, v98, v114
	v_pk_maximum3_f16 v195, v71, v99, v115
	v_pk_maximum3_f16 v157, v157, v193, v197
	v_pk_maximum3_f16 v196, v72, v100, v116
	s_nop 0
	v_pk_maximum3_f16 v154, v154, v190, v194
	v_pk_maximum3_f16 v155, v155, v191, v195
	v_pk_maximum3_f16 v156, v156, v192, v196
	v_xor_b32_e32 v157, 0x80008000, v157
	v_xor_b32_e32 v156, 0x80008000, v156
	v_xor_b32_e32 v155, 0x80008000, v155
	v_xor_b32_e32 v154, 0x80008000, v154
	v_pk_add_f16 v85, v85, v157
	v_pk_add_f16 v82, v82, v154
	v_pk_add_f16 v83, v83, v155
	v_pk_add_f16 v84, v84, v156
	v_pk_add_f16 v106, v106, v154
	v_exp_f16_sdwa v190, v82 dst_sel:WORD_0 dst_unused:UNUSED_PAD src0_sel:WORD_0
	v_exp_f16_sdwa v191, v83 dst_sel:WORD_0 dst_unused:UNUSED_PAD src0_sel:WORD_0
	v_exp_f16_sdwa v192, v84 dst_sel:WORD_0 dst_unused:UNUSED_PAD src0_sel:WORD_0
	v_exp_f16_sdwa v193, v85 dst_sel:WORD_0 dst_unused:UNUSED_PAD src0_sel:WORD_0
	v_exp_f16_sdwa v190, v82 dst_sel:WORD_1 dst_unused:UNUSED_PRESERVE src0_sel:WORD_1
	v_exp_f16_sdwa v191, v83 dst_sel:WORD_1 dst_unused:UNUSED_PRESERVE src0_sel:WORD_1
	v_exp_f16_sdwa v192, v84 dst_sel:WORD_1 dst_unused:UNUSED_PRESERVE src0_sel:WORD_1
	v_exp_f16_sdwa v193, v85 dst_sel:WORD_1 dst_unused:UNUSED_PRESERVE src0_sel:WORD_1
	s_nop 0
	v_pk_add_f16 v107, v107, v155
	v_pk_add_f16 v85, v190, 0
	v_pk_fma_f16 v45, v45, v193, 0
	v_pk_add_f16 v82, v193, 0
	v_pk_add_f16 v83, v192, 0
	v_pk_add_f16 v84, v191, 0
	v_pk_fma_f16 v44, v44, v192, 0
	v_pk_fma_f16 v43, v43, v191, 0
	v_pk_fma_f16 v42, v42, v190, 0
	v_pk_add_f16 v108, v108, v156
	v_pk_add_f16 v109, v109, v157
	v_pk_add_f16 v70, v70, v154
	v_exp_f16_sdwa v190, v106 dst_sel:WORD_0 dst_unused:UNUSED_PAD src0_sel:WORD_0
	v_exp_f16_sdwa v191, v107 dst_sel:WORD_0 dst_unused:UNUSED_PAD src0_sel:WORD_0
	v_exp_f16_sdwa v192, v108 dst_sel:WORD_0 dst_unused:UNUSED_PAD src0_sel:WORD_0
	v_exp_f16_sdwa v193, v109 dst_sel:WORD_0 dst_unused:UNUSED_PAD src0_sel:WORD_0
	v_exp_f16_sdwa v190, v106 dst_sel:WORD_1 dst_unused:UNUSED_PRESERVE src0_sel:WORD_1
	v_exp_f16_sdwa v191, v107 dst_sel:WORD_1 dst_unused:UNUSED_PRESERVE src0_sel:WORD_1
	v_exp_f16_sdwa v192, v108 dst_sel:WORD_1 dst_unused:UNUSED_PRESERVE src0_sel:WORD_1
	v_exp_f16_sdwa v193, v109 dst_sel:WORD_1 dst_unused:UNUSED_PRESERVE src0_sel:WORD_1
	s_nop 0
	v_pk_add_f16 v71, v71, v155
	v_pk_add_f16 v85, v85, v190
	v_pk_fma_f16 v45, v65, v193, v45
	v_pk_add_f16 v65, v125, v157
	v_pk_add_f16 v84, v84, v191
	v_pk_add_f16 v83, v83, v192
	v_pk_add_f16 v82, v82, v193
	v_pk_fma_f16 v42, v62, v190, v42
	v_pk_fma_f16 v43, v63, v191, v43
	v_pk_fma_f16 v44, v64, v192, v44
	v_pk_add_f16 v62, v122, v154
	v_pk_add_f16 v63, v123, v155
	v_pk_add_f16 v64, v124, v156
	v_pk_add_f16 v72, v72, v156
	v_exp_f16_sdwa v106, v62 dst_sel:WORD_0 dst_unused:UNUSED_PAD src0_sel:WORD_0
	v_exp_f16_sdwa v107, v63 dst_sel:WORD_0 dst_unused:UNUSED_PAD src0_sel:WORD_0
	v_exp_f16_sdwa v108, v64 dst_sel:WORD_0 dst_unused:UNUSED_PAD src0_sel:WORD_0
	v_exp_f16_sdwa v109, v65 dst_sel:WORD_0 dst_unused:UNUSED_PAD src0_sel:WORD_0
	v_exp_f16_sdwa v106, v62 dst_sel:WORD_1 dst_unused:UNUSED_PRESERVE src0_sel:WORD_1
	v_exp_f16_sdwa v107, v63 dst_sel:WORD_1 dst_unused:UNUSED_PRESERVE src0_sel:WORD_1
	v_exp_f16_sdwa v108, v64 dst_sel:WORD_1 dst_unused:UNUSED_PRESERVE src0_sel:WORD_1
	v_exp_f16_sdwa v109, v65 dst_sel:WORD_1 dst_unused:UNUSED_PRESERVE src0_sel:WORD_1
	s_nop 0
	v_pk_add_f16 v73, v73, v157
	v_pk_add_f16 v65, v85, v106
	v_pk_add_f16 v62, v82, v109
	v_pk_add_f16 v63, v83, v108
	v_pk_add_f16 v64, v84, v107
	v_pk_fma_f16 v45, v89, v109, v45
	v_pk_fma_f16 v44, v88, v108, v44
	v_pk_fma_f16 v43, v87, v107, v43
	v_pk_fma_f16 v42, v86, v106, v42
	v_pk_add_f16 v82, v129, v154
	v_pk_add_f16 v83, v128, v155
	v_pk_add_f16 v84, v127, v156
	v_pk_add_f16 v85, v126, v157
	s_nop 0
	v_exp_f16_sdwa v86, v82 dst_sel:WORD_0 dst_unused:UNUSED_PAD src0_sel:WORD_0
	v_exp_f16_sdwa v87, v83 dst_sel:WORD_0 dst_unused:UNUSED_PAD src0_sel:WORD_0
	v_exp_f16_sdwa v88, v84 dst_sel:WORD_0 dst_unused:UNUSED_PAD src0_sel:WORD_0
	v_exp_f16_sdwa v89, v85 dst_sel:WORD_0 dst_unused:UNUSED_PAD src0_sel:WORD_0
	v_exp_f16_sdwa v86, v82 dst_sel:WORD_1 dst_unused:UNUSED_PRESERVE src0_sel:WORD_1
	v_exp_f16_sdwa v87, v83 dst_sel:WORD_1 dst_unused:UNUSED_PRESERVE src0_sel:WORD_1
	v_exp_f16_sdwa v88, v84 dst_sel:WORD_1 dst_unused:UNUSED_PRESERVE src0_sel:WORD_1
	v_exp_f16_sdwa v89, v85 dst_sel:WORD_1 dst_unused:UNUSED_PRESERVE src0_sel:WORD_1
	s_nop 0
	v_pk_add_f16 v82, v137, v154
	v_pk_add_f16 v65, v65, v86
	v_pk_add_f16 v64, v64, v87
	v_pk_add_f16 v63, v63, v88
	v_pk_add_f16 v62, v62, v89
	v_pk_fma_f16 v42, v22, v86, v42
	v_pk_fma_f16 v43, v23, v87, v43
	v_pk_fma_f16 v44, v24, v88, v44
	v_pk_fma_f16 v45, v25, v89, v45
	v_pk_add_f16 v83, v136, v155
	v_pk_add_f16 v84, v135, v156
	v_pk_add_f16 v85, v134, v157
	s_nop 0
	v_exp_f16_sdwa v86, v82 dst_sel:WORD_0 dst_unused:UNUSED_PAD src0_sel:WORD_0
	v_exp_f16_sdwa v87, v83 dst_sel:WORD_0 dst_unused:UNUSED_PAD src0_sel:WORD_0
	v_exp_f16_sdwa v88, v84 dst_sel:WORD_0 dst_unused:UNUSED_PAD src0_sel:WORD_0
	v_exp_f16_sdwa v89, v85 dst_sel:WORD_0 dst_unused:UNUSED_PAD src0_sel:WORD_0
	v_exp_f16_sdwa v86, v82 dst_sel:WORD_1 dst_unused:UNUSED_PRESERVE src0_sel:WORD_1
	v_exp_f16_sdwa v87, v83 dst_sel:WORD_1 dst_unused:UNUSED_PRESERVE src0_sel:WORD_1
	v_exp_f16_sdwa v88, v84 dst_sel:WORD_1 dst_unused:UNUSED_PRESERVE src0_sel:WORD_1
	v_exp_f16_sdwa v89, v85 dst_sel:WORD_1 dst_unused:UNUSED_PRESERVE src0_sel:WORD_1
	s_nop 0
	v_pk_add_f16 v82, v189, v154
	v_pk_add_f16 v65, v65, v86
	v_pk_add_f16 v62, v62, v89
	v_pk_add_f16 v63, v63, v88
	v_pk_add_f16 v64, v64, v87
	v_pk_fma_f16 v45, v33, v89, v45
	v_pk_fma_f16 v44, v32, v88, v44
	v_pk_fma_f16 v43, v31, v87, v43
	v_pk_fma_f16 v42, v30, v86, v42
	v_pk_add_f16 v83, v188, v155
	v_pk_add_f16 v84, v187, v156
	v_pk_add_f16 v85, v186, v157
	s_nop 0
	v_exp_f16_sdwa v86, v82 dst_sel:WORD_0 dst_unused:UNUSED_PAD src0_sel:WORD_0
	v_exp_f16_sdwa v87, v83 dst_sel:WORD_0 dst_unused:UNUSED_PAD src0_sel:WORD_0
	v_exp_f16_sdwa v88, v84 dst_sel:WORD_0 dst_unused:UNUSED_PAD src0_sel:WORD_0
	v_exp_f16_sdwa v89, v85 dst_sel:WORD_0 dst_unused:UNUSED_PAD src0_sel:WORD_0
	v_exp_f16_sdwa v86, v82 dst_sel:WORD_1 dst_unused:UNUSED_PRESERVE src0_sel:WORD_1
	v_exp_f16_sdwa v87, v83 dst_sel:WORD_1 dst_unused:UNUSED_PRESERVE src0_sel:WORD_1
	v_exp_f16_sdwa v88, v84 dst_sel:WORD_1 dst_unused:UNUSED_PRESERVE src0_sel:WORD_1
	v_exp_f16_sdwa v89, v85 dst_sel:WORD_1 dst_unused:UNUSED_PRESERVE src0_sel:WORD_1
	s_nop 0
	v_exp_f16_sdwa v82, v70 dst_sel:WORD_0 dst_unused:UNUSED_PAD src0_sel:WORD_0
	v_exp_f16_sdwa v83, v71 dst_sel:WORD_0 dst_unused:UNUSED_PAD src0_sel:WORD_0
	v_exp_f16_sdwa v84, v72 dst_sel:WORD_0 dst_unused:UNUSED_PAD src0_sel:WORD_0
	v_exp_f16_sdwa v85, v73 dst_sel:WORD_0 dst_unused:UNUSED_PAD src0_sel:WORD_0
	v_exp_f16_sdwa v82, v70 dst_sel:WORD_1 dst_unused:UNUSED_PRESERVE src0_sel:WORD_1
	v_exp_f16_sdwa v83, v71 dst_sel:WORD_1 dst_unused:UNUSED_PRESERVE src0_sel:WORD_1
	v_exp_f16_sdwa v84, v72 dst_sel:WORD_1 dst_unused:UNUSED_PRESERVE src0_sel:WORD_1
	v_exp_f16_sdwa v85, v73 dst_sel:WORD_1 dst_unused:UNUSED_PRESERVE src0_sel:WORD_1
	s_nop 0
	v_pk_add_f16 v70, v98, v154
	v_pk_add_f16 v65, v65, v86
	v_pk_add_f16 v64, v64, v87
	v_pk_add_f16 v63, v63, v88
	v_pk_add_f16 v62, v62, v89
	v_pk_fma_f16 v42, v46, v86, v42
	v_pk_fma_f16 v43, v47, v87, v43
	v_pk_fma_f16 v44, v48, v88, v44
	v_pk_fma_f16 v45, v49, v89, v45
	v_pk_add_f16 v65, v65, v82
	v_pk_add_f16 v62, v62, v85
	v_pk_add_f16 v63, v63, v84
	v_pk_add_f16 v64, v64, v83
	v_pk_fma_f16 v45, v9, v85, v45
	v_pk_fma_f16 v44, v8, v84, v44
	v_pk_fma_f16 v43, v7, v83, v43
	v_pk_fma_f16 v42, v6, v82, v42
	v_pk_add_f16 v71, v99, v155
	v_pk_add_f16 v72, v100, v156
	v_pk_add_f16 v73, v101, v157
	s_nop 0
	v_exp_f16_sdwa v82, v70 dst_sel:WORD_0 dst_unused:UNUSED_PAD src0_sel:WORD_0
	v_exp_f16_sdwa v83, v71 dst_sel:WORD_0 dst_unused:UNUSED_PAD src0_sel:WORD_0
	v_exp_f16_sdwa v84, v72 dst_sel:WORD_0 dst_unused:UNUSED_PAD src0_sel:WORD_0
	v_exp_f16_sdwa v85, v73 dst_sel:WORD_0 dst_unused:UNUSED_PAD src0_sel:WORD_0
	v_exp_f16_sdwa v82, v70 dst_sel:WORD_1 dst_unused:UNUSED_PRESERVE src0_sel:WORD_1
	v_exp_f16_sdwa v83, v71 dst_sel:WORD_1 dst_unused:UNUSED_PRESERVE src0_sel:WORD_1
	v_exp_f16_sdwa v84, v72 dst_sel:WORD_1 dst_unused:UNUSED_PRESERVE src0_sel:WORD_1
	v_exp_f16_sdwa v85, v73 dst_sel:WORD_1 dst_unused:UNUSED_PRESERVE src0_sel:WORD_1
	s_nop 0
	v_pk_add_f16 v70, v114, v154
	v_pk_add_f16 v65, v65, v82
	v_pk_add_f16 v64, v64, v83
	v_pk_add_f16 v63, v63, v84
	v_pk_add_f16 v62, v62, v85
	v_pk_fma_f16 v42, v10, v82, v42
	v_pk_fma_f16 v43, v11, v83, v43
	v_pk_fma_f16 v44, v12, v84, v44
	v_pk_fma_f16 v45, v13, v85, v45
	v_pk_add_f16 v71, v115, v155
	v_pk_add_f16 v72, v116, v156
	v_pk_add_f16 v73, v117, v157
	s_nop 0
	v_exp_f16_sdwa v82, v70 dst_sel:WORD_0 dst_unused:UNUSED_PAD src0_sel:WORD_0
	v_exp_f16_sdwa v83, v71 dst_sel:WORD_0 dst_unused:UNUSED_PAD src0_sel:WORD_0
	v_exp_f16_sdwa v84, v72 dst_sel:WORD_0 dst_unused:UNUSED_PAD src0_sel:WORD_0
	v_exp_f16_sdwa v85, v73 dst_sel:WORD_0 dst_unused:UNUSED_PAD src0_sel:WORD_0
	v_exp_f16_sdwa v82, v70 dst_sel:WORD_1 dst_unused:UNUSED_PRESERVE src0_sel:WORD_1
	v_exp_f16_sdwa v83, v71 dst_sel:WORD_1 dst_unused:UNUSED_PRESERVE src0_sel:WORD_1
	v_exp_f16_sdwa v84, v72 dst_sel:WORD_1 dst_unused:UNUSED_PRESERVE src0_sel:WORD_1
	v_exp_f16_sdwa v85, v73 dst_sel:WORD_1 dst_unused:UNUSED_PRESERVE src0_sel:WORD_1
	s_nop 0
	s_nop 0
	v_pk_add_f16 v65, v65, v82
	v_pk_add_f16 v64, v64, v83
	v_rcp_f16_e32 v70, v65
	v_rcp_f16_sdwa v65, v65 dst_sel:DWORD dst_unused:UNUSED_PAD src0_sel:WORD_1
	v_pk_add_f16 v63, v63, v84
	v_rcp_f16_e32 v71, v64
	v_rcp_f16_sdwa v64, v64 dst_sel:DWORD dst_unused:UNUSED_PAD src0_sel:WORD_1
	v_pk_add_f16 v62, v62, v85
	v_rcp_f16_e32 v72, v63
	v_rcp_f16_sdwa v73, v63 dst_sel:DWORD dst_unused:UNUSED_PAD src0_sel:WORD_1
	v_pk_fma_f16 v43, v15, v83, v43
	v_pk_fma_f16 v42, v14, v82, v42
	v_rcp_f16_e32 v82, v62
	v_rcp_f16_sdwa v83, v62 dst_sel:DWORD dst_unused:UNUSED_PAD src0_sel:WORD_1
	v_pack_b32_f16 v62, v70, v65
	v_pk_mul_f16 v62, v42, v62
	v_pack_b32_f16 v42, v71, v64
	v_pk_fma_f16 v44, v16, v84, v44
	v_pk_mul_f16 v63, v43, v42
	v_pack_b32_f16 v42, v72, v73
	v_pk_fma_f16 v45, v17, v85, v45
	v_pk_mul_f16 v64, v44, v42
	v_pack_b32_f16 v42, v82, v83
	v_pk_mul_f16 v65, v45, v42
	s_waitcnt vmcnt(6)
	v_pk_mul_f16 v42, v185, v150 op_sel_hi:[0,1]
	v_pk_mul_f16 v70, v183, v150 op_sel_hi:[0,1]
	v_pk_mul_f16 v82, v184, v150 op_sel_hi:[0,1]
	v_pk_mul_f16 v43, v185, v151 op_sel_hi:[0,1]
	v_pk_mul_f16 v44, v185, v152 op_sel_hi:[0,1]
	v_pk_mul_f16 v45, v185, v153 op_sel_hi:[0,1]
	v_pk_mul_f16 v71, v183, v151 op_sel_hi:[0,1]
	v_pk_mul_f16 v72, v183, v152 op_sel_hi:[0,1]
	v_pk_mul_f16 v73, v183, v153 op_sel_hi:[0,1]
	v_pk_mul_f16 v83, v184, v151 op_sel_hi:[0,1]
	v_pk_mul_f16 v84, v184, v152 op_sel_hi:[0,1]
	v_pk_mul_f16 v85, v184, v153 op_sel_hi:[0,1]
	v_pk_fma_f16 v50, v50, v150, v42
	v_pk_fma_f16 v66, v66, v150, v70
	v_pk_fma_f16 v89, v94, v150, v82
	v_pk_fma_f16 v53, v53, v153, v45
	v_pk_maximum3_f16 v114, v50, v66, v89
	v_pk_fma_f16 v52, v52, v152, v44
	v_pk_fma_f16 v51, v51, v151, v43
	v_pk_fma_f16 v69, v69, v153, v73
	v_pk_fma_f16 v68, v68, v152, v72
	v_pk_fma_f16 v67, v67, v151, v71
	v_pk_fma_f16 v86, v97, v153, v85
	v_pk_fma_f16 v87, v96, v152, v84
	v_pk_fma_f16 v88, v95, v151, v83
	v_pk_fma_f16 v97, v18, v150, v42
	v_pk_fma_f16 v101, v34, v150, v70
	v_pk_fma_f16 v109, v54, v150, v82
	v_pk_fma_f16 v42, v74, v150, v42
	v_pk_fma_f16 v70, v102, v150, v70
	v_pk_fma_f16 v82, v118, v150, v82
	v_pk_maximum3_f16 v115, v51, v67, v88
	v_pk_maximum3_f16 v116, v52, v68, v87
	v_pk_maximum3_f16 v117, v53, v69, v86
	v_pk_maximum3_f16 v122, v97, v101, v109
	v_pk_fma_f16 v94, v21, v153, v45
	v_pk_maximum3_f16 v126, v42, v70, v82
	v_pk_fma_f16 v95, v20, v152, v44
	v_pk_maximum3_f16 v114, v114, v122, v126
	v_pk_fma_f16 v96, v19, v151, v43
	v_pk_fma_f16 v98, v37, v153, v73
	v_pk_fma_f16 v99, v36, v152, v72
	v_pk_fma_f16 v100, v35, v151, v71
	v_pk_fma_f16 v106, v57, v153, v85
	v_pk_fma_f16 v107, v56, v152, v84
	v_pk_fma_f16 v108, v55, v151, v83
	v_pk_fma_f16 v45, v77, v153, v45
	v_pk_fma_f16 v44, v76, v152, v44
	v_pk_fma_f16 v43, v75, v151, v43
	v_pk_fma_f16 v73, v105, v153, v73
	v_pk_fma_f16 v72, v104, v152, v72
	v_pk_fma_f16 v71, v103, v151, v71
	v_pk_fma_f16 v85, v121, v153, v85
	v_pk_fma_f16 v84, v120, v152, v84
	v_pk_fma_f16 v83, v119, v151, v83
	v_pk_maximum3_f16 v123, v96, v100, v108
	v_pk_maximum3_f16 v124, v95, v99, v107
	v_pk_maximum3_f16 v125, v94, v98, v106
	v_pk_maximum3_f16 v128, v44, v72, v84
	v_pk_maximum3_f16 v129, v45, v73, v85
	s_nop 0
	v_pk_maximum3_f16 v127, v43, v71, v83
	v_xor_b32_e32 v114, 0x80008000, v114
	v_pk_maximum3_f16 v115, v115, v123, v127
	v_pk_maximum3_f16 v116, v116, v124, v128
	v_pk_maximum3_f16 v117, v117, v125, v129
	v_pk_add_f16 v50, v50, v114
	v_xor_b32_e32 v117, 0x80008000, v117
	v_xor_b32_e32 v116, 0x80008000, v116
	v_xor_b32_e32 v115, 0x80008000, v115
	v_pk_add_f16 v51, v51, v115
	v_pk_add_f16 v52, v52, v116
	v_pk_add_f16 v53, v53, v117
	v_pk_add_f16 v66, v66, v114
	v_exp_f16_sdwa v122, v50 dst_sel:WORD_0 dst_unused:UNUSED_PAD src0_sel:WORD_0
	v_exp_f16_sdwa v123, v51 dst_sel:WORD_0 dst_unused:UNUSED_PAD src0_sel:WORD_0
	v_exp_f16_sdwa v124, v52 dst_sel:WORD_0 dst_unused:UNUSED_PAD src0_sel:WORD_0
	v_exp_f16_sdwa v125, v53 dst_sel:WORD_0 dst_unused:UNUSED_PAD src0_sel:WORD_0
	v_exp_f16_sdwa v122, v50 dst_sel:WORD_1 dst_unused:UNUSED_PRESERVE src0_sel:WORD_1
	v_exp_f16_sdwa v123, v51 dst_sel:WORD_1 dst_unused:UNUSED_PRESERVE src0_sel:WORD_1
	v_exp_f16_sdwa v124, v52 dst_sel:WORD_1 dst_unused:UNUSED_PRESERVE src0_sel:WORD_1
	v_exp_f16_sdwa v125, v53 dst_sel:WORD_1 dst_unused:UNUSED_PRESERVE src0_sel:WORD_1
	s_nop 0
	v_pk_add_f16 v67, v67, v115
	v_pk_add_f16 v50, v125, 0
	v_pk_fma_f16 v22, v22, v122, 0
	v_pk_add_f16 v51, v124, 0
	v_pk_add_f16 v52, v123, 0
	v_pk_add_f16 v53, v122, 0
	v_pk_fma_f16 v23, v23, v123, 0
	v_pk_fma_f16 v24, v24, v124, 0
	v_pk_fma_f16 v25, v25, v125, 0
	v_pk_add_f16 v68, v68, v116
	v_pk_add_f16 v69, v69, v117
	v_pk_add_f16 v42, v42, v114
	v_exp_f16_sdwa v122, v66 dst_sel:WORD_0 dst_unused:UNUSED_PAD src0_sel:WORD_0
	v_exp_f16_sdwa v123, v67 dst_sel:WORD_0 dst_unused:UNUSED_PAD src0_sel:WORD_0
	v_exp_f16_sdwa v124, v68 dst_sel:WORD_0 dst_unused:UNUSED_PAD src0_sel:WORD_0
	v_exp_f16_sdwa v125, v69 dst_sel:WORD_0 dst_unused:UNUSED_PAD src0_sel:WORD_0
	v_exp_f16_sdwa v122, v66 dst_sel:WORD_1 dst_unused:UNUSED_PRESERVE src0_sel:WORD_1
	v_exp_f16_sdwa v123, v67 dst_sel:WORD_1 dst_unused:UNUSED_PRESERVE src0_sel:WORD_1
	v_exp_f16_sdwa v124, v68 dst_sel:WORD_1 dst_unused:UNUSED_PRESERVE src0_sel:WORD_1
	v_exp_f16_sdwa v125, v69 dst_sel:WORD_1 dst_unused:UNUSED_PRESERVE src0_sel:WORD_1
	s_nop 0
	v_pk_add_f16 v43, v43, v115
	v_pk_add_f16 v50, v50, v125
	v_pk_fma_f16 v22, v30, v122, v22
	v_pk_add_f16 v30, v89, v114
	v_pk_add_f16 v53, v53, v122
	v_pk_add_f16 v52, v52, v123
	v_pk_add_f16 v51, v51, v124
	v_pk_fma_f16 v25, v33, v125, v25
	v_pk_fma_f16 v24, v32, v124, v24
	v_pk_fma_f16 v23, v31, v123, v23
	v_pk_add_f16 v31, v88, v115
	v_pk_add_f16 v32, v87, v116
	v_pk_add_f16 v33, v86, v117
	v_pk_add_f16 v44, v44, v116
	v_exp_f16_sdwa v66, v30 dst_sel:WORD_0 dst_unused:UNUSED_PAD src0_sel:WORD_0
	v_exp_f16_sdwa v67, v31 dst_sel:WORD_0 dst_unused:UNUSED_PAD src0_sel:WORD_0
	v_exp_f16_sdwa v68, v32 dst_sel:WORD_0 dst_unused:UNUSED_PAD src0_sel:WORD_0
	v_exp_f16_sdwa v69, v33 dst_sel:WORD_0 dst_unused:UNUSED_PAD src0_sel:WORD_0
	v_exp_f16_sdwa v66, v30 dst_sel:WORD_1 dst_unused:UNUSED_PRESERVE src0_sel:WORD_1
	v_exp_f16_sdwa v67, v31 dst_sel:WORD_1 dst_unused:UNUSED_PRESERVE src0_sel:WORD_1
	v_exp_f16_sdwa v68, v32 dst_sel:WORD_1 dst_unused:UNUSED_PRESERVE src0_sel:WORD_1
	v_exp_f16_sdwa v69, v33 dst_sel:WORD_1 dst_unused:UNUSED_PRESERVE src0_sel:WORD_1
	s_nop 0
	v_pk_add_f16 v45, v45, v117
	v_pk_add_f16 v30, v50, v69
	v_pk_add_f16 v31, v51, v68
	v_pk_add_f16 v32, v52, v67
	v_pk_add_f16 v33, v53, v66
	v_pk_fma_f16 v22, v46, v66, v22
	v_pk_fma_f16 v23, v47, v67, v23
	v_pk_fma_f16 v24, v48, v68, v24
	v_pk_fma_f16 v25, v49, v69, v25
	v_pk_add_f16 v46, v97, v114
	v_pk_add_f16 v47, v96, v115
	v_pk_add_f16 v48, v95, v116
	v_pk_add_f16 v49, v94, v117
	s_nop 0
	v_exp_f16_sdwa v50, v46 dst_sel:WORD_0 dst_unused:UNUSED_PAD src0_sel:WORD_0
	v_exp_f16_sdwa v51, v47 dst_sel:WORD_0 dst_unused:UNUSED_PAD src0_sel:WORD_0
	v_exp_f16_sdwa v52, v48 dst_sel:WORD_0 dst_unused:UNUSED_PAD src0_sel:WORD_0
	v_exp_f16_sdwa v53, v49 dst_sel:WORD_0 dst_unused:UNUSED_PAD src0_sel:WORD_0
	v_exp_f16_sdwa v50, v46 dst_sel:WORD_1 dst_unused:UNUSED_PRESERVE src0_sel:WORD_1
	v_exp_f16_sdwa v51, v47 dst_sel:WORD_1 dst_unused:UNUSED_PRESERVE src0_sel:WORD_1
	v_exp_f16_sdwa v52, v48 dst_sel:WORD_1 dst_unused:UNUSED_PRESERVE src0_sel:WORD_1
	v_exp_f16_sdwa v53, v49 dst_sel:WORD_1 dst_unused:UNUSED_PRESERVE src0_sel:WORD_1
	s_nop 0
	v_pk_add_f16 v46, v101, v114
	v_pk_add_f16 v30, v30, v53
	v_pk_add_f16 v33, v33, v50
	v_pk_add_f16 v32, v32, v51
	v_pk_add_f16 v31, v31, v52
	v_pk_fma_f16 v25, v9, v53, v25
	v_pk_fma_f16 v24, v8, v52, v24
	v_pk_fma_f16 v23, v7, v51, v23
	v_pk_fma_f16 v22, v6, v50, v22
	v_pk_add_f16 v47, v100, v115
	v_pk_add_f16 v48, v99, v116
	v_pk_add_f16 v49, v98, v117
	s_nop 0
	v_exp_f16_sdwa v50, v46 dst_sel:WORD_0 dst_unused:UNUSED_PAD src0_sel:WORD_0
	v_exp_f16_sdwa v51, v47 dst_sel:WORD_0 dst_unused:UNUSED_PAD src0_sel:WORD_0
	v_exp_f16_sdwa v52, v48 dst_sel:WORD_0 dst_unused:UNUSED_PAD src0_sel:WORD_0
	v_exp_f16_sdwa v53, v49 dst_sel:WORD_0 dst_unused:UNUSED_PAD src0_sel:WORD_0
	v_exp_f16_sdwa v50, v46 dst_sel:WORD_1 dst_unused:UNUSED_PRESERVE src0_sel:WORD_1
	v_exp_f16_sdwa v51, v47 dst_sel:WORD_1 dst_unused:UNUSED_PRESERVE src0_sel:WORD_1
	v_exp_f16_sdwa v52, v48 dst_sel:WORD_1 dst_unused:UNUSED_PRESERVE src0_sel:WORD_1
	v_exp_f16_sdwa v53, v49 dst_sel:WORD_1 dst_unused:UNUSED_PRESERVE src0_sel:WORD_1
	s_nop 0
	v_pk_add_f16 v46, v109, v114
	v_pk_add_f16 v30, v30, v53
	v_pk_add_f16 v31, v31, v52
	v_pk_add_f16 v32, v32, v51
	v_pk_add_f16 v33, v33, v50
	v_pk_fma_f16 v22, v10, v50, v22
	v_pk_fma_f16 v23, v11, v51, v23
	v_pk_fma_f16 v24, v12, v52, v24
	v_pk_fma_f16 v25, v13, v53, v25
	v_pk_add_f16 v47, v108, v115
	v_pk_add_f16 v48, v107, v116
	v_pk_add_f16 v49, v106, v117
	s_nop 0
	v_exp_f16_sdwa v50, v46 dst_sel:WORD_0 dst_unused:UNUSED_PAD src0_sel:WORD_0
	v_exp_f16_sdwa v51, v47 dst_sel:WORD_0 dst_unused:UNUSED_PAD src0_sel:WORD_0
	v_exp_f16_sdwa v52, v48 dst_sel:WORD_0 dst_unused:UNUSED_PAD src0_sel:WORD_0
	v_exp_f16_sdwa v53, v49 dst_sel:WORD_0 dst_unused:UNUSED_PAD src0_sel:WORD_0
	v_exp_f16_sdwa v50, v46 dst_sel:WORD_1 dst_unused:UNUSED_PRESERVE src0_sel:WORD_1
	v_exp_f16_sdwa v51, v47 dst_sel:WORD_1 dst_unused:UNUSED_PRESERVE src0_sel:WORD_1
	v_exp_f16_sdwa v52, v48 dst_sel:WORD_1 dst_unused:UNUSED_PRESERVE src0_sel:WORD_1
	v_exp_f16_sdwa v53, v49 dst_sel:WORD_1 dst_unused:UNUSED_PRESERVE src0_sel:WORD_1
	s_nop 0
	v_exp_f16_sdwa v46, v42 dst_sel:WORD_0 dst_unused:UNUSED_PAD src0_sel:WORD_0
	v_exp_f16_sdwa v47, v43 dst_sel:WORD_0 dst_unused:UNUSED_PAD src0_sel:WORD_0
	v_exp_f16_sdwa v48, v44 dst_sel:WORD_0 dst_unused:UNUSED_PAD src0_sel:WORD_0
	v_exp_f16_sdwa v49, v45 dst_sel:WORD_0 dst_unused:UNUSED_PAD src0_sel:WORD_0
	v_exp_f16_sdwa v46, v42 dst_sel:WORD_1 dst_unused:UNUSED_PRESERVE src0_sel:WORD_1
	v_exp_f16_sdwa v47, v43 dst_sel:WORD_1 dst_unused:UNUSED_PRESERVE src0_sel:WORD_1
	v_exp_f16_sdwa v48, v44 dst_sel:WORD_1 dst_unused:UNUSED_PRESERVE src0_sel:WORD_1
	v_exp_f16_sdwa v49, v45 dst_sel:WORD_1 dst_unused:UNUSED_PRESERVE src0_sel:WORD_1
	s_nop 0
	v_pk_add_f16 v42, v70, v114
	v_pk_add_f16 v30, v30, v53
	v_pk_add_f16 v33, v33, v50
	v_pk_add_f16 v32, v32, v51
	v_pk_add_f16 v31, v31, v52
	v_pk_fma_f16 v25, v17, v53, v25
	v_pk_fma_f16 v24, v16, v52, v24
	v_pk_fma_f16 v23, v15, v51, v23
	v_pk_fma_f16 v22, v14, v50, v22
	v_pk_add_f16 v30, v30, v49
	v_pk_add_f16 v31, v31, v48
	v_pk_add_f16 v32, v32, v47
	v_pk_add_f16 v33, v33, v46
	v_pk_fma_f16 v22, v26, v46, v22
	v_pk_fma_f16 v23, v27, v47, v23
	v_pk_fma_f16 v24, v28, v48, v24
	v_pk_fma_f16 v25, v29, v49, v25
	v_pk_add_f16 v43, v71, v115
	v_pk_add_f16 v44, v72, v116
	v_pk_add_f16 v45, v73, v117
	s_nop 0
	v_exp_f16_sdwa v46, v42 dst_sel:WORD_0 dst_unused:UNUSED_PAD src0_sel:WORD_0
	v_exp_f16_sdwa v47, v43 dst_sel:WORD_0 dst_unused:UNUSED_PAD src0_sel:WORD_0
	v_exp_f16_sdwa v48, v44 dst_sel:WORD_0 dst_unused:UNUSED_PAD src0_sel:WORD_0
	v_exp_f16_sdwa v49, v45 dst_sel:WORD_0 dst_unused:UNUSED_PAD src0_sel:WORD_0
	v_exp_f16_sdwa v46, v42 dst_sel:WORD_1 dst_unused:UNUSED_PRESERVE src0_sel:WORD_1
	v_exp_f16_sdwa v47, v43 dst_sel:WORD_1 dst_unused:UNUSED_PRESERVE src0_sel:WORD_1
	v_exp_f16_sdwa v48, v44 dst_sel:WORD_1 dst_unused:UNUSED_PRESERVE src0_sel:WORD_1
	v_exp_f16_sdwa v49, v45 dst_sel:WORD_1 dst_unused:UNUSED_PRESERVE src0_sel:WORD_1
	s_nop 0
	v_pk_add_f16 v42, v82, v114
	v_pk_add_f16 v30, v30, v49
	v_pk_add_f16 v33, v33, v46
	v_pk_add_f16 v32, v32, v47
	v_pk_add_f16 v31, v31, v48
	v_pk_fma_f16 v25, v41, v49, v25
	v_pk_fma_f16 v24, v40, v48, v24
	v_pk_fma_f16 v23, v39, v47, v23
	v_pk_fma_f16 v22, v38, v46, v22
	v_pk_add_f16 v43, v83, v115
	v_pk_add_f16 v44, v84, v116
	v_pk_add_f16 v45, v85, v117
	s_nop 0
	v_exp_f16_sdwa v46, v42 dst_sel:WORD_0 dst_unused:UNUSED_PAD src0_sel:WORD_0
	v_exp_f16_sdwa v47, v43 dst_sel:WORD_0 dst_unused:UNUSED_PAD src0_sel:WORD_0
	v_exp_f16_sdwa v48, v44 dst_sel:WORD_0 dst_unused:UNUSED_PAD src0_sel:WORD_0
	v_exp_f16_sdwa v49, v45 dst_sel:WORD_0 dst_unused:UNUSED_PAD src0_sel:WORD_0
	v_exp_f16_sdwa v46, v42 dst_sel:WORD_1 dst_unused:UNUSED_PRESERVE src0_sel:WORD_1
	v_exp_f16_sdwa v47, v43 dst_sel:WORD_1 dst_unused:UNUSED_PRESERVE src0_sel:WORD_1
	v_exp_f16_sdwa v48, v44 dst_sel:WORD_1 dst_unused:UNUSED_PRESERVE src0_sel:WORD_1
	v_exp_f16_sdwa v49, v45 dst_sel:WORD_1 dst_unused:UNUSED_PRESERVE src0_sel:WORD_1
	s_nop 0
	s_nop 0
	v_pk_add_f16 v30, v30, v49
	v_pk_add_f16 v31, v31, v48
	v_rcp_f16_e32 v44, v30
	v_rcp_f16_sdwa v30, v30 dst_sel:DWORD dst_unused:UNUSED_PAD src0_sel:WORD_1
	v_pk_add_f16 v32, v32, v47
	v_rcp_f16_e32 v45, v31
	v_rcp_f16_sdwa v31, v31 dst_sel:DWORD dst_unused:UNUSED_PAD src0_sel:WORD_1
	v_pk_add_f16 v33, v33, v46
	v_rcp_f16_e32 v43, v32
	v_rcp_f16_sdwa v32, v32 dst_sel:DWORD dst_unused:UNUSED_PAD src0_sel:WORD_1
	v_rcp_f16_e32 v42, v33
	v_rcp_f16_sdwa v33, v33 dst_sel:DWORD dst_unused:UNUSED_PAD src0_sel:WORD_1
	v_pk_fma_f16 v25, v61, v49, v25
	v_pack_b32_f16 v30, v44, v30
	v_pk_fma_f16 v24, v60, v48, v24
	v_pk_mul_f16 v25, v25, v30
	v_pack_b32_f16 v30, v45, v31
	v_pk_fma_f16 v23, v59, v47, v23
	v_pk_mul_f16 v24, v24, v30
	v_pack_b32_f16 v30, v43, v32
	v_pk_fma_f16 v22, v58, v46, v22
	v_pk_mul_f16 v23, v23, v30
	v_pack_b32_f16 v30, v42, v33
	v_pk_mul_f16 v22, v22, v30
	s_waitcnt vmcnt(0)
	v_pk_mul_f16 v30, v185, v146 op_sel_hi:[0,1]
	v_pk_mul_f16 v31, v185, v147 op_sel_hi:[0,1]
	v_pk_mul_f16 v32, v185, v148 op_sel_hi:[0,1]
	v_pk_mul_f16 v33, v185, v149 op_sel_hi:[0,1]
	v_pk_mul_f16 v42, v183, v146 op_sel_hi:[0,1]
	v_pk_mul_f16 v43, v183, v147 op_sel_hi:[0,1]
	v_pk_mul_f16 v44, v183, v148 op_sel_hi:[0,1]
	v_pk_mul_f16 v45, v183, v149 op_sel_hi:[0,1]
	v_pk_mul_f16 v46, v184, v146 op_sel_hi:[0,1]
	v_pk_mul_f16 v47, v184, v147 op_sel_hi:[0,1]
	v_pk_mul_f16 v48, v184, v148 op_sel_hi:[0,1]
	v_pk_mul_f16 v49, v184, v149 op_sel_hi:[0,1]
	v_pk_fma_f16 v21, v21, v149, v33
	v_pk_fma_f16 v20, v20, v148, v32
	v_pk_fma_f16 v19, v19, v147, v31
	v_pk_fma_f16 v18, v18, v146, v30
	v_pk_fma_f16 v37, v37, v149, v45
	v_pk_fma_f16 v36, v36, v148, v44
	v_pk_fma_f16 v35, v35, v147, v43
	v_pk_fma_f16 v34, v34, v146, v42
	v_pk_fma_f16 v50, v57, v149, v49
	v_pk_fma_f16 v51, v56, v148, v48
	v_pk_fma_f16 v52, v55, v147, v47
	v_pk_fma_f16 v53, v54, v146, v46
	v_pk_fma_f16 v54, v77, v149, v33
	v_pk_fma_f16 v55, v76, v148, v32
	v_pk_fma_f16 v56, v75, v147, v31
	v_pk_fma_f16 v57, v74, v146, v30
	v_pk_maximum3_f16 v74, v18, v34, v53
	v_pk_maximum3_f16 v75, v19, v35, v52
	v_pk_maximum3_f16 v76, v20, v36, v51
	v_pk_maximum3_f16 v77, v21, v37, v50
	v_pk_fma_f16 v66, v105, v149, v45
	v_pk_fma_f16 v67, v104, v148, v44
	v_pk_fma_f16 v68, v103, v147, v43
	v_pk_fma_f16 v69, v102, v146, v42
	v_pk_fma_f16 v70, v121, v149, v49
	v_pk_fma_f16 v71, v120, v148, v48
	v_pk_fma_f16 v72, v119, v147, v47
	v_pk_fma_f16 v73, v118, v146, v46
	v_pk_fma_f16 v33, v133, v149, v33
	v_pk_fma_f16 v32, v132, v148, v32
	v_pk_fma_f16 v31, v131, v147, v31
	v_pk_fma_f16 v30, v130, v146, v30
	v_pk_fma_f16 v45, v141, v149, v45
	v_pk_fma_f16 v44, v140, v148, v44
	v_pk_fma_f16 v43, v139, v147, v43
	v_pk_fma_f16 v42, v138, v146, v42
	v_pk_fma_f16 v49, v145, v149, v49
	v_pk_fma_f16 v48, v144, v148, v48
	v_pk_fma_f16 v47, v143, v147, v47
	v_pk_fma_f16 v46, v142, v146, v46
	v_pk_maximum3_f16 v82, v57, v69, v73
	v_pk_maximum3_f16 v83, v56, v68, v72
	v_pk_maximum3_f16 v84, v55, v67, v71
	v_pk_maximum3_f16 v85, v54, v66, v70
	v_pk_maximum3_f16 v87, v31, v43, v47
	s_nop 0
	v_pk_maximum3_f16 v86, v30, v42, v46
	v_pk_maximum3_f16 v88, v32, v44, v48
	v_pk_maximum3_f16 v89, v33, v45, v49
	s_nop 0
	v_pk_maximum3_f16 v74, v74, v82, v86
	v_pk_maximum3_f16 v75, v75, v83, v87
	v_pk_maximum3_f16 v76, v76, v84, v88
	v_pk_maximum3_f16 v77, v77, v85, v89
	s_nop 0
	v_xor_b32_e32 v77, 0x80008000, v77
	v_xor_b32_e32 v76, 0x80008000, v76
	v_xor_b32_e32 v75, 0x80008000, v75
	v_xor_b32_e32 v74, 0x80008000, v74
	v_pk_add_f16 v18, v18, v74
	v_pk_add_f16 v19, v19, v75
	v_pk_add_f16 v20, v20, v76
	v_pk_add_f16 v21, v21, v77
	v_pk_add_f16 v34, v34, v74
	v_exp_f16_sdwa v82, v18 dst_sel:WORD_0 dst_unused:UNUSED_PAD src0_sel:WORD_0
	v_exp_f16_sdwa v83, v19 dst_sel:WORD_0 dst_unused:UNUSED_PAD src0_sel:WORD_0
	v_exp_f16_sdwa v84, v20 dst_sel:WORD_0 dst_unused:UNUSED_PAD src0_sel:WORD_0
	v_exp_f16_sdwa v85, v21 dst_sel:WORD_0 dst_unused:UNUSED_PAD src0_sel:WORD_0
	v_exp_f16_sdwa v82, v18 dst_sel:WORD_1 dst_unused:UNUSED_PRESERVE src0_sel:WORD_1
	v_exp_f16_sdwa v83, v19 dst_sel:WORD_1 dst_unused:UNUSED_PRESERVE src0_sel:WORD_1
	v_exp_f16_sdwa v84, v20 dst_sel:WORD_1 dst_unused:UNUSED_PRESERVE src0_sel:WORD_1
	v_exp_f16_sdwa v85, v21 dst_sel:WORD_1 dst_unused:UNUSED_PRESERVE src0_sel:WORD_1
	s_nop 0
	v_pk_add_f16 v35, v35, v75
	v_pk_add_f16 v18, v82, 0
	v_pk_add_f16 v19, v83, 0
	v_pk_add_f16 v20, v84, 0
	v_pk_add_f16 v21, v85, 0
	v_pk_fma_f16 v6, v6, v82, 0
	v_pk_fma_f16 v7, v7, v83, 0
	v_pk_fma_f16 v8, v8, v84, 0
	v_pk_fma_f16 v9, v9, v85, 0
	v_pk_add_f16 v36, v36, v76
	v_pk_add_f16 v37, v37, v77
	s_nop 0
	v_exp_f16_sdwa v82, v34 dst_sel:WORD_0 dst_unused:UNUSED_PAD src0_sel:WORD_0
	v_exp_f16_sdwa v83, v35 dst_sel:WORD_0 dst_unused:UNUSED_PAD src0_sel:WORD_0
	v_exp_f16_sdwa v84, v36 dst_sel:WORD_0 dst_unused:UNUSED_PAD src0_sel:WORD_0
	v_exp_f16_sdwa v85, v37 dst_sel:WORD_0 dst_unused:UNUSED_PAD src0_sel:WORD_0
	v_exp_f16_sdwa v82, v34 dst_sel:WORD_1 dst_unused:UNUSED_PRESERVE src0_sel:WORD_1
	v_exp_f16_sdwa v83, v35 dst_sel:WORD_1 dst_unused:UNUSED_PRESERVE src0_sel:WORD_1
	v_exp_f16_sdwa v84, v36 dst_sel:WORD_1 dst_unused:UNUSED_PRESERVE src0_sel:WORD_1
	v_exp_f16_sdwa v85, v37 dst_sel:WORD_1 dst_unused:UNUSED_PRESERVE src0_sel:WORD_1
	s_nop 0
	s_nop 0
	v_pk_add_f16 v21, v21, v85
	v_pk_add_f16 v20, v20, v84
	v_pk_add_f16 v19, v19, v83
	v_pk_add_f16 v18, v18, v82
	v_pk_fma_f16 v9, v13, v85, v9
	v_pk_fma_f16 v8, v12, v84, v8
	v_pk_fma_f16 v7, v11, v83, v7
	v_pk_fma_f16 v6, v10, v82, v6
	v_pk_add_f16 v10, v53, v74
	v_pk_add_f16 v11, v52, v75
	v_pk_add_f16 v12, v51, v76
	v_pk_add_f16 v13, v50, v77
	s_nop 0
	v_exp_f16_sdwa v34, v10 dst_sel:WORD_0 dst_unused:UNUSED_PAD src0_sel:WORD_0
	v_exp_f16_sdwa v35, v11 dst_sel:WORD_0 dst_unused:UNUSED_PAD src0_sel:WORD_0
	v_exp_f16_sdwa v36, v12 dst_sel:WORD_0 dst_unused:UNUSED_PAD src0_sel:WORD_0
	v_exp_f16_sdwa v37, v13 dst_sel:WORD_0 dst_unused:UNUSED_PAD src0_sel:WORD_0
	v_exp_f16_sdwa v34, v10 dst_sel:WORD_1 dst_unused:UNUSED_PRESERVE src0_sel:WORD_1
	v_exp_f16_sdwa v35, v11 dst_sel:WORD_1 dst_unused:UNUSED_PRESERVE src0_sel:WORD_1
	v_exp_f16_sdwa v36, v12 dst_sel:WORD_1 dst_unused:UNUSED_PRESERVE src0_sel:WORD_1
	v_exp_f16_sdwa v37, v13 dst_sel:WORD_1 dst_unused:UNUSED_PRESERVE src0_sel:WORD_1
	s_nop 0
	s_nop 0
	v_pk_add_f16 v10, v18, v34
	v_pk_add_f16 v11, v19, v35
	v_pk_add_f16 v12, v20, v36
	v_pk_add_f16 v13, v21, v37
	v_pk_fma_f16 v6, v14, v34, v6
	v_pk_fma_f16 v7, v15, v35, v7
	v_pk_fma_f16 v8, v16, v36, v8
	v_pk_fma_f16 v9, v17, v37, v9
	v_pk_add_f16 v14, v57, v74
	v_pk_add_f16 v15, v56, v75
	v_pk_add_f16 v16, v55, v76
	v_pk_add_f16 v17, v54, v77
	s_nop 0
	v_exp_f16_sdwa v18, v14 dst_sel:WORD_0 dst_unused:UNUSED_PAD src0_sel:WORD_0
	v_exp_f16_sdwa v19, v15 dst_sel:WORD_0 dst_unused:UNUSED_PAD src0_sel:WORD_0
	v_exp_f16_sdwa v20, v16 dst_sel:WORD_0 dst_unused:UNUSED_PAD src0_sel:WORD_0
	v_exp_f16_sdwa v21, v17 dst_sel:WORD_0 dst_unused:UNUSED_PAD src0_sel:WORD_0
	v_exp_f16_sdwa v18, v14 dst_sel:WORD_1 dst_unused:UNUSED_PRESERVE src0_sel:WORD_1
	v_exp_f16_sdwa v19, v15 dst_sel:WORD_1 dst_unused:UNUSED_PRESERVE src0_sel:WORD_1
	v_exp_f16_sdwa v20, v16 dst_sel:WORD_1 dst_unused:UNUSED_PRESERVE src0_sel:WORD_1
	v_exp_f16_sdwa v21, v17 dst_sel:WORD_1 dst_unused:UNUSED_PRESERVE src0_sel:WORD_1
	s_nop 0
	v_pk_add_f16 v14, v69, v74
	v_pk_add_f16 v13, v13, v21
	v_pk_add_f16 v12, v12, v20
	v_pk_add_f16 v11, v11, v19
	v_pk_add_f16 v10, v10, v18
	v_pk_fma_f16 v9, v29, v21, v9
	v_pk_fma_f16 v8, v28, v20, v8
	v_pk_fma_f16 v7, v27, v19, v7
	v_pk_fma_f16 v6, v26, v18, v6
	v_pk_add_f16 v15, v68, v75
	v_pk_add_f16 v16, v67, v76
	v_pk_add_f16 v17, v66, v77
	s_nop 0
	v_exp_f16_sdwa v18, v14 dst_sel:WORD_0 dst_unused:UNUSED_PAD src0_sel:WORD_0
	v_exp_f16_sdwa v19, v15 dst_sel:WORD_0 dst_unused:UNUSED_PAD src0_sel:WORD_0
	v_exp_f16_sdwa v20, v16 dst_sel:WORD_0 dst_unused:UNUSED_PAD src0_sel:WORD_0
	v_exp_f16_sdwa v21, v17 dst_sel:WORD_0 dst_unused:UNUSED_PAD src0_sel:WORD_0
	v_exp_f16_sdwa v18, v14 dst_sel:WORD_1 dst_unused:UNUSED_PRESERVE src0_sel:WORD_1
	v_exp_f16_sdwa v19, v15 dst_sel:WORD_1 dst_unused:UNUSED_PRESERVE src0_sel:WORD_1
	v_exp_f16_sdwa v20, v16 dst_sel:WORD_1 dst_unused:UNUSED_PRESERVE src0_sel:WORD_1
	v_exp_f16_sdwa v21, v17 dst_sel:WORD_1 dst_unused:UNUSED_PRESERVE src0_sel:WORD_1
	s_nop 0
	v_pk_add_f16 v14, v73, v74
	v_pk_add_f16 v10, v10, v18
	v_pk_add_f16 v11, v11, v19
	v_pk_add_f16 v12, v12, v20
	v_pk_add_f16 v13, v13, v21
	v_pk_fma_f16 v6, v38, v18, v6
	v_pk_fma_f16 v7, v39, v19, v7
	v_pk_fma_f16 v8, v40, v20, v8
	v_pk_fma_f16 v9, v41, v21, v9
	v_pk_add_f16 v15, v72, v75
	v_pk_add_f16 v16, v71, v76
	v_pk_add_f16 v17, v70, v77
	s_nop 0
	v_exp_f16_sdwa v18, v14 dst_sel:WORD_0 dst_unused:UNUSED_PAD src0_sel:WORD_0
	v_exp_f16_sdwa v19, v15 dst_sel:WORD_0 dst_unused:UNUSED_PAD src0_sel:WORD_0
	v_exp_f16_sdwa v20, v16 dst_sel:WORD_0 dst_unused:UNUSED_PAD src0_sel:WORD_0
	v_exp_f16_sdwa v21, v17 dst_sel:WORD_0 dst_unused:UNUSED_PAD src0_sel:WORD_0
	v_exp_f16_sdwa v18, v14 dst_sel:WORD_1 dst_unused:UNUSED_PRESERVE src0_sel:WORD_1
	v_exp_f16_sdwa v19, v15 dst_sel:WORD_1 dst_unused:UNUSED_PRESERVE src0_sel:WORD_1
	v_exp_f16_sdwa v20, v16 dst_sel:WORD_1 dst_unused:UNUSED_PRESERVE src0_sel:WORD_1
	v_exp_f16_sdwa v21, v17 dst_sel:WORD_1 dst_unused:UNUSED_PRESERVE src0_sel:WORD_1
	s_nop 0
	v_pk_add_f16 v14, v30, v74
	v_pk_add_f16 v13, v13, v21
	v_pk_add_f16 v12, v12, v20
	v_pk_add_f16 v11, v11, v19
	v_pk_add_f16 v10, v10, v18
	v_pk_fma_f16 v9, v61, v21, v9
	v_pk_fma_f16 v8, v60, v20, v8
	v_pk_fma_f16 v7, v59, v19, v7
	v_pk_fma_f16 v6, v58, v18, v6
	v_pk_add_f16 v15, v31, v75
	v_pk_add_f16 v16, v32, v76
	v_pk_add_f16 v17, v33, v77
	s_nop 0
	v_exp_f16_sdwa v18, v14 dst_sel:WORD_0 dst_unused:UNUSED_PAD src0_sel:WORD_0
	v_exp_f16_sdwa v19, v15 dst_sel:WORD_0 dst_unused:UNUSED_PAD src0_sel:WORD_0
	v_exp_f16_sdwa v20, v16 dst_sel:WORD_0 dst_unused:UNUSED_PAD src0_sel:WORD_0
	v_exp_f16_sdwa v21, v17 dst_sel:WORD_0 dst_unused:UNUSED_PAD src0_sel:WORD_0
	v_exp_f16_sdwa v18, v14 dst_sel:WORD_1 dst_unused:UNUSED_PRESERVE src0_sel:WORD_1
	v_exp_f16_sdwa v19, v15 dst_sel:WORD_1 dst_unused:UNUSED_PRESERVE src0_sel:WORD_1
	v_exp_f16_sdwa v20, v16 dst_sel:WORD_1 dst_unused:UNUSED_PRESERVE src0_sel:WORD_1
	v_exp_f16_sdwa v21, v17 dst_sel:WORD_1 dst_unused:UNUSED_PRESERVE src0_sel:WORD_1
	s_nop 0
	s_nop 0
	v_pk_add_f16 v10, v10, v18
	v_pk_add_f16 v11, v11, v19
	v_pk_add_f16 v12, v12, v20
	v_pk_add_f16 v13, v13, v21
	v_pk_fma_f16 v14, v78, v18, v6
	v_pk_fma_f16 v15, v79, v19, v7
	v_pk_fma_f16 v16, v80, v20, v8
	v_pk_fma_f16 v17, v81, v21, v9
	v_pk_add_f16 v6, v42, v74
	v_pk_add_f16 v7, v43, v75
	v_pk_add_f16 v8, v44, v76
	v_pk_add_f16 v9, v45, v77
	s_nop 0
	v_exp_f16_sdwa v18, v6 dst_sel:WORD_0 dst_unused:UNUSED_PAD src0_sel:WORD_0
	v_exp_f16_sdwa v19, v7 dst_sel:WORD_0 dst_unused:UNUSED_PAD src0_sel:WORD_0
	v_exp_f16_sdwa v20, v8 dst_sel:WORD_0 dst_unused:UNUSED_PAD src0_sel:WORD_0
	v_exp_f16_sdwa v21, v9 dst_sel:WORD_0 dst_unused:UNUSED_PAD src0_sel:WORD_0
	v_exp_f16_sdwa v18, v6 dst_sel:WORD_1 dst_unused:UNUSED_PRESERVE src0_sel:WORD_1
	v_exp_f16_sdwa v19, v7 dst_sel:WORD_1 dst_unused:UNUSED_PRESERVE src0_sel:WORD_1
	v_exp_f16_sdwa v20, v8 dst_sel:WORD_1 dst_unused:UNUSED_PRESERVE src0_sel:WORD_1
	v_exp_f16_sdwa v21, v9 dst_sel:WORD_1 dst_unused:UNUSED_PRESERVE src0_sel:WORD_1
	s_nop 0
	s_nop 0
	v_pk_add_f16 v9, v13, v21
	v_pk_add_f16 v8, v12, v20
	v_pk_add_f16 v7, v11, v19
	v_pk_add_f16 v6, v10, v18
	v_pk_fma_f16 v13, v93, v21, v17
	v_pk_fma_f16 v12, v92, v20, v16
	v_pk_fma_f16 v11, v91, v19, v15
	v_pk_fma_f16 v10, v90, v18, v14
	v_pk_add_f16 v18, v46, v74
	v_pk_add_f16 v19, v47, v75
	v_pk_add_f16 v20, v48, v76
	v_pk_add_f16 v21, v49, v77
	s_nop 0
	v_exp_f16_sdwa v14, v18 dst_sel:WORD_0 dst_unused:UNUSED_PAD src0_sel:WORD_0
	v_exp_f16_sdwa v17, v19 dst_sel:WORD_0 dst_unused:UNUSED_PAD src0_sel:WORD_0
	v_exp_f16_sdwa v15, v20 dst_sel:WORD_0 dst_unused:UNUSED_PAD src0_sel:WORD_0
	v_exp_f16_sdwa v16, v21 dst_sel:WORD_0 dst_unused:UNUSED_PAD src0_sel:WORD_0
	v_exp_f16_sdwa v14, v18 dst_sel:WORD_1 dst_unused:UNUSED_PRESERVE src0_sel:WORD_1
	v_exp_f16_sdwa v17, v19 dst_sel:WORD_1 dst_unused:UNUSED_PRESERVE src0_sel:WORD_1
	v_exp_f16_sdwa v15, v20 dst_sel:WORD_1 dst_unused:UNUSED_PRESERVE src0_sel:WORD_1
	v_exp_f16_sdwa v16, v21 dst_sel:WORD_1 dst_unused:UNUSED_PRESERVE src0_sel:WORD_1
	s_nop 0
.LBB3_45:
	s_and_b64 vcc, exec, s[4:5]
	s_cbranch_vccz .LBB3_6
	v_cmp_lt_u32_e64 s[64:65], 0, v182
	v_cmp_gt_u32_e64 s[66:67], 63, v182
	v_cmp_lt_u32_e64 s[68:69], 0, v162
	v_cmp_gt_u32_e64 s[70:71], 60, v162
	buffer_load_dwordx4 v[184:187], v180, s[16:19], 0 offen
	v_add_u32_e32 v250, 0x18000, v180
	buffer_load_dwordx4 v[154:157], v250, s[16:19], 0 offen
	v_add_u32_e32 v249, 0x30000, v180
	buffer_load_dwordx4 v[150:153], v249, s[16:19], 0 offen
	v_add_u32_e32 v250, 0x48000, v180
	buffer_load_dwordx4 v[146:149], v250, s[16:19], 0 offen
	s_and_b64 s[72:73], s[68:69], s[64:65]
	s_and_b64 s[74:75], s[68:69], s[66:67]
	s_and_b64 s[76:77], s[70:71], s[64:65]
	s_and_b64 s[78:79], s[70:71], s[66:67]
	v_add_u32_e32 v249, 0xfffe7c00, v180
	v_add_u32_e32 v250, 0xfffe8000, v180
	v_mov_b32_e32 v110, v172
	v_mov_b32_e32 v111, v174
	v_mov_b32_e32 v112, v176
	v_mov_b32_e32 v113, v178
	v_mov_b32_e32 v78, v173
	v_mov_b32_e32 v79, v175
	v_mov_b32_e32 v80, v177
	v_mov_b32_e32 v81, v179
	v_mov_b32_e32 v126, v172
	v_mov_b32_e32 v127, v174
	v_mov_b32_e32 v128, v176
	v_mov_b32_e32 v129, v178
	v_mov_b32_e32 v102, v173
	v_mov_b32_e32 v103, v175
	v_mov_b32_e32 v104, v177
	v_mov_b32_e32 v105, v179
	v_mov_b32_e32 v138, v172
	v_mov_b32_e32 v139, v174
	v_mov_b32_e32 v140, v176
	v_mov_b32_e32 v141, v178
	v_mov_b32_e32 v118, v173
	v_mov_b32_e32 v119, v175
	v_mov_b32_e32 v120, v177
	v_mov_b32_e32 v121, v179
	s_mov_b64 exec, s[72:73]
	buffer_load_dwordx4 v[110:113], v249, s[16:19], 0 offen
	buffer_load_dwordx4 v[78:81], v249, s[16:19], 0 offen offset:512
	s_mov_b64 exec, -1
	s_mov_b64 exec, s[68:69]
	buffer_load_dwordx4 v[126:129], v250, s[16:19], 0 offen offset:512
	buffer_load_dwordx4 v[102:105], v250, s[16:19], 0 offen offset:1024
	s_mov_b64 exec, -1
	s_mov_b64 exec, s[74:75]
	buffer_load_dwordx4 v[138:141], v250, s[16:19], 0 offen offset:2048
	buffer_load_dwordx4 v[118:121], v250, s[16:19], 0 offen offset:2560
	s_mov_b64 exec, -1
	v_add_u32_e32 v249, 0xfffffc00, v180
	v_mov_b32_e32 v86, v172
	v_mov_b32_e32 v87, v174
	v_mov_b32_e32 v88, v176
	v_mov_b32_e32 v89, v178
	v_mov_b32_e32 v46, v173
	v_mov_b32_e32 v47, v175
	v_mov_b32_e32 v48, v177
	v_mov_b32_e32 v49, v179
	v_mov_b32_e32 v122, v172
	v_mov_b32_e32 v123, v174
	v_mov_b32_e32 v124, v176
	v_mov_b32_e32 v125, v178
	v_mov_b32_e32 v82, v173
	v_mov_b32_e32 v83, v175
	v_mov_b32_e32 v84, v177
	v_mov_b32_e32 v85, v179
	s_mov_b64 exec, s[64:65]
	buffer_load_dwordx4 v[86:89], v249, s[16:19], 0 offen
	buffer_load_dwordx4 v[46:49], v249, s[16:19], 0 offen offset:512
	s_mov_b64 exec, -1
	buffer_load_dwordx4 v[106:109], v180, s[16:19], 0 offen offset:512
	buffer_load_dwordx4 v[62:65], v180, s[16:19], 0 offen offset:1024
	s_mov_b64 exec, s[66:67]
	buffer_load_dwordx4 v[122:125], v180, s[16:19], 0 offen offset:2048
	buffer_load_dwordx4 v[82:85], v180, s[16:19], 0 offen offset:2560
	s_mov_b64 exec, -1
	v_add_u32_e32 v249, 0x17c00, v180
	v_add_u32_e32 v250, 0x18000, v180
	v_mov_b32_e32 v50, v172
	v_mov_b32_e32 v51, v174
	v_mov_b32_e32 v52, v176
	v_mov_b32_e32 v53, v178
	v_mov_b32_e32 v22, v173
	v_mov_b32_e32 v23, v175
	v_mov_b32_e32 v24, v177
	v_mov_b32_e32 v25, v179
	v_mov_b32_e32 v94, v172
	v_mov_b32_e32 v95, v174
	v_mov_b32_e32 v96, v176
	v_mov_b32_e32 v97, v178
	v_mov_b32_e32 v42, v173
	v_mov_b32_e32 v43, v175
	v_mov_b32_e32 v44, v177
	v_mov_b32_e32 v45, v179
	s_mov_b64 exec, s[64:65]
	buffer_load_dwordx4 v[50:53], v249, s[16:19], 0 offen
	buffer_load_dwordx4 v[22:25], v249, s[16:19], 0 offen offset:512
	s_mov_b64 exec, -1
	buffer_load_dwordx4 v[66:69], v250, s[16:19], 0 offen offset:512
	buffer_load_dwordx4 v[34:37], v250, s[16:19], 0 offen offset:1024
	s_mov_b64 exec, s[66:67]
	buffer_load_dwordx4 v[94:97], v250, s[16:19], 0 offen offset:2048
	buffer_load_dwordx4 v[42:45], v250, s[16:19], 0 offen offset:2560
	s_mov_b64 exec, -1
	v_add_u32_e32 v249, 0x2fc00, v180
	v_add_u32_e32 v250, 0x30000, v180
	v_mov_b32_e32 v18, v172
	v_mov_b32_e32 v19, v174
	v_mov_b32_e32 v20, v176
	v_mov_b32_e32 v21, v178
	v_mov_b32_e32 v6, v173
	v_mov_b32_e32 v7, v175
	v_mov_b32_e32 v8, v177
	v_mov_b32_e32 v9, v179
	v_mov_b32_e32 v54, v172
	v_mov_b32_e32 v55, v174
	v_mov_b32_e32 v56, v176
	v_mov_b32_e32 v57, v178
	v_mov_b32_e32 v14, v173
	v_mov_b32_e32 v15, v175
	v_mov_b32_e32 v16, v177
	v_mov_b32_e32 v17, v179
	s_mov_b64 exec, s[64:65]
	buffer_load_dwordx4 v[18:21], v249, s[16:19], 0 offen
	buffer_load_dwordx4 v[6:9], v249, s[16:19], 0 offen offset:512
	s_mov_b64 exec, -1
	buffer_load_dwordx4 v[30:33], v250, s[16:19], 0 offen offset:512
	buffer_load_dwordx4 v[10:13], v250, s[16:19], 0 offen offset:1024
	s_mov_b64 exec, s[66:67]
	buffer_load_dwordx4 v[54:57], v250, s[16:19], 0 offen offset:2048
	buffer_load_dwordx4 v[14:17], v250, s[16:19], 0 offen offset:2560
	s_mov_b64 exec, -1
	v_add_u32_e32 v249, 0x47c00, v180
	v_add_u32_e32 v250, 0x48000, v180
	v_mov_b32_e32 v74, v172
	v_mov_b32_e32 v75, v174
	v_mov_b32_e32 v76, v176
	v_mov_b32_e32 v77, v178
	v_mov_b32_e32 v26, v173
	v_mov_b32_e32 v27, v175
	v_mov_b32_e32 v28, v177
	v_mov_b32_e32 v29, v179
	v_mov_b32_e32 v114, v172
	v_mov_b32_e32 v115, v174
	v_mov_b32_e32 v116, v176
	v_mov_b32_e32 v117, v178
	v_mov_b32_e32 v58, v173
	v_mov_b32_e32 v59, v175
	v_mov_b32_e32 v60, v177
	v_mov_b32_e32 v61, v179
	s_mov_b64 exec, s[64:65]
	buffer_load_dwordx4 v[74:77], v249, s[16:19], 0 offen
	buffer_load_dwordx4 v[26:29], v249, s[16:19], 0 offen offset:512
	s_mov_b64 exec, -1
	buffer_load_dwordx4 v[98:101], v250, s[16:19], 0 offen offset:512
	buffer_load_dwordx4 v[38:41], v250, s[16:19], 0 offen offset:1024
	s_mov_b64 exec, s[66:67]
	buffer_load_dwordx4 v[114:117], v250, s[16:19], 0 offen offset:2048
	buffer_load_dwordx4 v[58:61], v250, s[16:19], 0 offen offset:2560
	s_mov_b64 exec, -1
	v_add_u32_e32 v249, 0x5fc00, v180
	v_add_u32_e32 v250, 0x60000, v180
	v_mov_b32_e32 v130, v172
	v_mov_b32_e32 v131, v174
	v_mov_b32_e32 v132, v176
	v_mov_b32_e32 v133, v178
	v_mov_b32_e32 v70, v173
	v_mov_b32_e32 v71, v175
	v_mov_b32_e32 v72, v177
	v_mov_b32_e32 v73, v179
	v_mov_b32_e32 v134, v172
	v_mov_b32_e32 v135, v174
	v_mov_b32_e32 v136, v176
	v_mov_b32_e32 v137, v178
	v_mov_b32_e32 v90, v173
	v_mov_b32_e32 v91, v175
	v_mov_b32_e32 v92, v177
	v_mov_b32_e32 v93, v179
	v_mov_b32_e32 v142, v172
	v_mov_b32_e32 v143, v174
	v_mov_b32_e32 v144, v176
	v_mov_b32_e32 v145, v178
	v_mov_b32_e32 v2, v173
	v_mov_b32_e32 v3, v175
	v_mov_b32_e32 v4, v177
	v_mov_b32_e32 v5, v179
	s_mov_b64 exec, s[76:77]
	buffer_load_dwordx4 v[130:133], v249, s[16:19], 0 offen
	buffer_load_dwordx4 v[70:73], v249, s[16:19], 0 offen offset:512
	s_mov_b64 exec, -1
	s_mov_b64 exec, s[70:71]
	buffer_load_dwordx4 v[134:137], v250, s[16:19], 0 offen offset:512
	buffer_load_dwordx4 v[90:93], v250, s[16:19], 0 offen offset:1024
	s_mov_b64 exec, -1
	s_mov_b64 exec, s[78:79]
	buffer_load_dwordx4 v[142:145], v250, s[16:19], 0 offen offset:2048
	buffer_load_dwordx4 v[2:5], v250, s[16:19], 0 offen offset:2560
	s_mov_b64 exec, -1
	s_load_dwordx2 s[0:1], s[22:23], 0x18
	s_waitcnt lgkmcnt(0)
	s_load_dwordx2 s[6:7], s[0:1], 0x0
	s_load_dword s28, s[0:1], 0x8
	s_branch .LBB3_5
.LBB3_82:
	s_mul_i32 s0, s9, s3
	s_lshl_b32 s1, s30, 6
	s_add_i32 s0, s0, s8
	s_or_b32 s1, s1, s31
	s_or_b32 s7, s1, s11
	s_mul_i32 s4, s0, 0x60000
	s_mul_hi_i32 s1, s0, 0x60000
	s_waitcnt lgkmcnt(0)
	s_add_u32 s6, s12, s4
	s_mulk_i32 s0, 0x300
	s_addc_u32 s8, s13, s1
	s_ashr_i32 s1, s0, 31
	s_lshl_b64 s[0:1], s[0:1], 2
	s_add_u32 s4, s14, s0
	s_addc_u32 s5, s15, s1
	s_mul_i32 s0, s2, 0x1800000
	s_mul_hi_u32 s1, s3, 0x1800000
	s_add_i32 s1, s1, s0
	s_mul_i32 s0, s3, 0x1800000
	s_add_u32 s0, s20, s0
	v_readfirstlane_b32 s2, v0
	s_addc_u32 s1, s21, s1
	s_lshr_b32 s9, s2, 6
	s_and_b32 s1, s1, 0xffff
	s_mul_i32 s2, s9, 0x6000
	v_and_b32_e32 v2, 63, v0
	s_mul_hi_u32 s3, s9, 0x6000
	s_add_u32 s2, s6, s2
	s_addc_u32 s3, s8, s3
	v_lshlrev_b32_e32 v82, 4, v2
	v_mov_b32_e32 v83, 0
	v_lshl_add_u64 v[118:119], s[2:3], 0, v[82:83]
	s_movk_i32 s6, 0x1000
	v_add_co_u32_e32 v50, vcc, s6, v118
	s_movk_i32 s6, 0x2000
	s_nop 0
	v_addc_co_u32_e32 v51, vcc, 0, v119, vcc
	v_add_co_u32_e32 v52, vcc, s6, v118
	global_load_dwordx4 v[2:5], v82, s[2:3] offset:1024
	global_load_dwordx4 v[6:9], v82, s[2:3] offset:2048
	v_addc_co_u32_e32 v53, vcc, 0, v119, vcc
	global_load_dwordx4 v[10:13], v82, s[2:3] offset:3072
	global_load_dwordx4 v[14:17], v[52:53], off offset:-4096
	global_load_dwordx4 v[18:21], v[50:51], off offset:1024
	global_load_dwordx4 v[22:25], v[50:51], off offset:2048
	global_load_dwordx4 v[26:29], v82, s[2:3]
	global_load_dwordx4 v[30:33], v[50:51], off offset:3072
	global_load_dwordx4 v[34:37], v[52:53], off
	global_load_dwordx4 v[38:41], v[52:53], off offset:1024
	global_load_dwordx4 v[42:45], v[52:53], off offset:2048
	global_load_dwordx4 v[46:49], v[52:53], off offset:3072
	s_movk_i32 s2, 0x3000
	v_add_co_u32_e32 v116, vcc, s2, v118
	s_movk_i32 s2, 0x4000
	s_nop 0
	v_addc_co_u32_e32 v117, vcc, 0, v119, vcc
	v_add_co_u32_e32 v156, vcc, s2, v118
	s_nop 1
	v_addc_co_u32_e32 v157, vcc, 0, v119, vcc
	s_barrier
	global_load_dwordx4 v[50:53], v[156:157], off offset:-4096
	global_load_dwordx4 v[54:57], v[116:117], off offset:1024
	global_load_dwordx4 v[58:61], v[116:117], off offset:2048
	v_mul_u32_u24_e32 v62, 0x556, v0
	v_lshlrev_b32_e32 v132, 9, v1
	v_lshrrev_b32_e32 v142, 16, v62
	v_xor_b32_e32 v62, v158, v1
	v_lshl_or_b32 v135, v62, 4, v132
	ds_read_b128 v[62:65], v135
	ds_read_b128 v[66:69], v135 offset:8192
	ds_read_b128 v[70:73], v135 offset:16384
	ds_read_b128 v[74:77], v135 offset:24576
	ds_read_b128 v[78:81], v135 offset:32768
	ds_read_b128 v[84:87], v135 offset:40960
	ds_read_b128 v[88:91], v135 offset:49152
	ds_read_b128 v[92:95], v135 offset:57344
	s_mul_i32 s6, s9, 48
	v_lshl_or_b32 v82, v158, 2, s6
	s_mul_i32 s6, s9, 0x60
	s_add_i32 s6, s6, 0x10000
	v_lshlrev_b32_e32 v96, 3, v142
	s_movk_i32 s9, 0x47
	v_lshl_or_b32 v248, v158, 3, s6
	s_or_b32 s6, s7, 8
	v_bitop3_b32 v143, v96, s9, v142 bitop3:0xc8
	s_mov_b32 s2, 0x1800000
	s_mov_b32 s3, 0x20000
	s_mov_b32 s8, 0x10000
	v_or_b32_e32 v140, s6, v143
	s_waitcnt vmcnt(8) lgkmcnt(7)
	v_mfma_f32_16x16x32_f16 v[96:99], v[26:29], v[62:65], 0
	s_waitcnt lgkmcnt(6)
	v_mfma_f32_16x16x32_f16 v[100:103], v[26:29], v[66:69], 0
	s_waitcnt lgkmcnt(5)
	v_mfma_f32_16x16x32_f16 v[104:107], v[26:29], v[70:73], 0
	s_waitcnt lgkmcnt(4)
	v_mfma_f32_16x16x32_f16 v[108:111], v[26:29], v[74:77], 0
	s_waitcnt lgkmcnt(3)
	v_mfma_f32_16x16x32_f16 v[112:115], v[26:29], v[78:81], 0
	s_waitcnt lgkmcnt(2)
	v_mfma_f32_16x16x32_f16 v[120:123], v[26:29], v[84:87], 0
	s_waitcnt lgkmcnt(1)
	v_mfma_f32_16x16x32_f16 v[124:127], v[26:29], v[88:91], 0
	s_waitcnt lgkmcnt(0)
	v_mfma_f32_16x16x32_f16 v[26:29], v[26:29], v[92:95], 0
	v_mfma_f32_16x16x32_f16 v[128:131], v[2:5], v[62:65], 0
	v_mfma_f32_16x16x32_f16 v[136:139], v[2:5], v[66:69], 0
	v_mfma_f32_16x16x32_f16 v[144:147], v[2:5], v[70:73], 0
	v_mfma_f32_16x16x32_f16 v[148:151], v[2:5], v[74:77], 0
	v_mfma_f32_16x16x32_f16 v[152:155], v[2:5], v[78:81], 0
	v_mfma_f32_16x16x32_f16 v[160:163], v[2:5], v[84:87], 0
	v_mfma_f32_16x16x32_f16 v[164:167], v[2:5], v[88:91], 0
	v_mfma_f32_16x16x32_f16 v[2:5], v[2:5], v[92:95], 0
	v_mfma_f32_16x16x32_f16 v[62:65], v[6:9], v[62:65], 0
	v_mfma_f32_16x16x32_f16 v[66:69], v[6:9], v[66:69], 0
	v_mfma_f32_16x16x32_f16 v[70:73], v[6:9], v[70:73], 0
	v_mfma_f32_16x16x32_f16 v[74:77], v[6:9], v[74:77], 0
	v_mfma_f32_16x16x32_f16 v[78:81], v[6:9], v[78:81], 0
	v_mfma_f32_16x16x32_f16 v[84:87], v[6:9], v[84:87], 0
	v_mfma_f32_16x16x32_f16 v[88:91], v[6:9], v[88:91], 0
	v_mfma_f32_16x16x32_f16 v[6:9], v[6:9], v[92:95], 0
	global_load_dwordx4 v[92:95], v[116:117], off offset:3072
	global_load_dwordx4 v[168:171], v[156:157], off
	global_load_dwordx4 v[172:175], v[156:157], off offset:1024
	v_bitop3_b32 v116, v158, v1, 4 bitop3:0x36
	v_lshl_or_b32 v133, v116, 4, v132
	ds_read_b128 v[176:179], v133
	ds_read_b128 v[180:183], v133 offset:8192
	ds_read_b128 v[184:187], v133 offset:16384
	ds_read_b128 v[188:191], v133 offset:24576
	ds_read_b128 v[192:195], v133 offset:32768
	ds_read_b128 v[196:199], v133 offset:40960
	ds_read_b128 v[200:203], v133 offset:49152
	ds_read_b128 v[204:207], v133 offset:57344
	s_waitcnt lgkmcnt(7)
	v_mfma_f32_16x16x32_f16 v[96:99], v[10:13], v[176:179], v[96:99]
	s_waitcnt lgkmcnt(6)
	v_mfma_f32_16x16x32_f16 v[100:103], v[10:13], v[180:183], v[100:103]
	s_waitcnt lgkmcnt(5)
	v_mfma_f32_16x16x32_f16 v[104:107], v[10:13], v[184:187], v[104:107]
	s_waitcnt lgkmcnt(4)
	v_mfma_f32_16x16x32_f16 v[108:111], v[10:13], v[188:191], v[108:111]
	s_waitcnt lgkmcnt(3)
	v_mfma_f32_16x16x32_f16 v[112:115], v[10:13], v[192:195], v[112:115]
	s_waitcnt lgkmcnt(2)
	v_mfma_f32_16x16x32_f16 v[120:123], v[10:13], v[196:199], v[120:123]
	s_waitcnt lgkmcnt(1)
	v_mfma_f32_16x16x32_f16 v[124:127], v[10:13], v[200:203], v[124:127]
	s_waitcnt lgkmcnt(0)
	v_mfma_f32_16x16x32_f16 v[10:13], v[10:13], v[204:207], v[26:29]
	v_mfma_f32_16x16x32_f16 v[26:29], v[14:17], v[176:179], v[128:131]
	v_mfma_f32_16x16x32_f16 v[128:131], v[14:17], v[180:183], v[136:139]
	v_mfma_f32_16x16x32_f16 v[136:139], v[14:17], v[184:187], v[144:147]
	v_mfma_f32_16x16x32_f16 v[144:147], v[14:17], v[188:191], v[148:151]
	v_mfma_f32_16x16x32_f16 v[148:151], v[14:17], v[192:195], v[152:155]
	v_mfma_f32_16x16x32_f16 v[152:155], v[14:17], v[196:199], v[160:163]
	v_mfma_f32_16x16x32_f16 v[160:163], v[14:17], v[200:203], v[164:167]
	v_mfma_f32_16x16x32_f16 v[2:5], v[14:17], v[204:207], v[2:5]
	v_mfma_f32_16x16x32_f16 v[14:17], v[18:21], v[176:179], v[62:65]
	v_mfma_f32_16x16x32_f16 v[62:65], v[18:21], v[180:183], v[66:69]
	v_mfma_f32_16x16x32_f16 v[66:69], v[18:21], v[184:187], v[70:73]
	v_mfma_f32_16x16x32_f16 v[70:73], v[18:21], v[188:191], v[74:77]
	v_mfma_f32_16x16x32_f16 v[74:77], v[18:21], v[192:195], v[78:81]
	v_mfma_f32_16x16x32_f16 v[78:81], v[18:21], v[196:199], v[84:87]
	v_mfma_f32_16x16x32_f16 v[84:87], v[18:21], v[200:203], v[88:91]
	v_mfma_f32_16x16x32_f16 v[6:9], v[18:21], v[204:207], v[6:9]
	s_movk_i32 s9, 0x5000
	v_add_co_u32_e32 v116, vcc, s9, v118
	global_load_dwordx4 v[88:91], v[156:157], off offset:2048
	global_load_dwordx4 v[164:167], v[156:157], off offset:3072
	v_addc_co_u32_e32 v117, vcc, 0, v119, vcc
	global_load_dwordx4 v[176:179], v[116:117], off
	v_bitop3_b32 v18, v158, v1, 8 bitop3:0x36
	v_lshl_or_b32 v134, v18, 4, v132
	ds_read_b128 v[18:21], v134
	ds_read_b128 v[180:183], v134 offset:8192
	ds_read_b128 v[184:187], v134 offset:16384
	ds_read_b128 v[188:191], v134 offset:24576
	ds_read_b128 v[192:195], v134 offset:32768
	ds_read_b128 v[196:199], v134 offset:40960
	ds_read_b128 v[200:203], v134 offset:49152
	ds_read_b128 v[204:207], v134 offset:57344
	s_waitcnt lgkmcnt(7)
	v_mfma_f32_16x16x32_f16 v[96:99], v[22:25], v[18:21], v[96:99]
	s_waitcnt lgkmcnt(6)
	v_mfma_f32_16x16x32_f16 v[100:103], v[22:25], v[180:183], v[100:103]
	s_waitcnt lgkmcnt(5)
	v_mfma_f32_16x16x32_f16 v[104:107], v[22:25], v[184:187], v[104:107]
	s_waitcnt lgkmcnt(4)
	v_mfma_f32_16x16x32_f16 v[108:111], v[22:25], v[188:191], v[108:111]
	s_waitcnt lgkmcnt(3)
	v_mfma_f32_16x16x32_f16 v[112:115], v[22:25], v[192:195], v[112:115]
	s_waitcnt lgkmcnt(2)
	v_mfma_f32_16x16x32_f16 v[120:123], v[22:25], v[196:199], v[120:123]
	s_waitcnt lgkmcnt(1)
	v_mfma_f32_16x16x32_f16 v[124:127], v[22:25], v[200:203], v[124:127]
	s_waitcnt lgkmcnt(0)
	v_mfma_f32_16x16x32_f16 v[10:13], v[22:25], v[204:207], v[10:13]
	s_waitcnt vmcnt(13)
	v_mfma_f32_16x16x32_f16 v[22:25], v[30:33], v[18:21], v[26:29]
	v_mfma_f32_16x16x32_f16 v[26:29], v[30:33], v[180:183], v[128:131]
	v_mfma_f32_16x16x32_f16 v[128:131], v[30:33], v[184:187], v[136:139]
	v_mfma_f32_16x16x32_f16 v[144:147], v[30:33], v[188:191], v[144:147]
	v_mfma_f32_16x16x32_f16 v[148:151], v[30:33], v[192:195], v[148:151]
	v_mfma_f32_16x16x32_f16 v[152:155], v[30:33], v[196:199], v[152:155]
	v_mfma_f32_16x16x32_f16 v[160:163], v[30:33], v[200:203], v[160:163]
	v_mfma_f32_16x16x32_f16 v[2:5], v[30:33], v[204:207], v[2:5]
	s_waitcnt vmcnt(12)
	v_mfma_f32_16x16x32_f16 v[14:17], v[34:37], v[18:21], v[14:17]
	v_mfma_f32_16x16x32_f16 v[18:21], v[34:37], v[180:183], v[62:65]
	v_mfma_f32_16x16x32_f16 v[30:33], v[34:37], v[184:187], v[66:69]
	v_mfma_f32_16x16x32_f16 v[62:65], v[34:37], v[188:191], v[70:73]
	v_mfma_f32_16x16x32_f16 v[66:69], v[34:37], v[192:195], v[74:77]
	v_mfma_f32_16x16x32_f16 v[70:73], v[34:37], v[196:199], v[78:81]
	v_mfma_f32_16x16x32_f16 v[74:77], v[34:37], v[200:203], v[84:87]
	v_mfma_f32_16x16x32_f16 v[6:9], v[34:37], v[204:207], v[6:9]
	s_nop 0
	global_load_dwordx4 v[78:81], v[116:117], off offset:1024
	global_load_dwordx4 v[180:183], v[116:117], off offset:2048
	global_load_dwordx4 v[184:187], v[116:117], off offset:3072
	v_bitop3_b32 v34, v158, v1, 12 bitop3:0x36
	v_lshl_or_b32 v136, v34, 4, v132
	ds_read_b128 v[34:37], v136
	ds_read_b128 v[84:87], v136 offset:8192
	ds_read_b128 v[188:191], v136 offset:16384
	ds_read_b128 v[192:195], v136 offset:24576
	ds_read_b128 v[196:199], v136 offset:32768
	ds_read_b128 v[200:203], v136 offset:40960
	ds_read_b128 v[204:207], v136 offset:49152
	ds_read_b128 v[208:211], v136 offset:57344
	s_waitcnt vmcnt(14) lgkmcnt(7)
	v_mfma_f32_16x16x32_f16 v[96:99], v[38:41], v[34:37], v[96:99]
	s_waitcnt lgkmcnt(6)
	v_mfma_f32_16x16x32_f16 v[100:103], v[38:41], v[84:87], v[100:103]
	s_waitcnt lgkmcnt(5)
	v_mfma_f32_16x16x32_f16 v[104:107], v[38:41], v[188:191], v[104:107]
	s_waitcnt lgkmcnt(4)
	v_mfma_f32_16x16x32_f16 v[108:111], v[38:41], v[192:195], v[108:111]
	s_waitcnt lgkmcnt(3)
	v_mfma_f32_16x16x32_f16 v[112:115], v[38:41], v[196:199], v[112:115]
	s_waitcnt lgkmcnt(2)
	v_mfma_f32_16x16x32_f16 v[120:123], v[38:41], v[200:203], v[120:123]
	s_waitcnt lgkmcnt(1)
	v_mfma_f32_16x16x32_f16 v[124:127], v[38:41], v[204:207], v[124:127]
	s_waitcnt lgkmcnt(0)
	v_mfma_f32_16x16x32_f16 v[212:215], v[38:41], v[208:211], v[10:13]
	s_waitcnt vmcnt(13)
	v_mfma_f32_16x16x32_f16 v[22:25], v[42:45], v[34:37], v[22:25]
	v_mfma_f32_16x16x32_f16 v[216:219], v[42:45], v[84:87], v[26:29]
	v_mfma_f32_16x16x32_f16 v[128:131], v[42:45], v[188:191], v[128:131]
	v_mfma_f32_16x16x32_f16 v[144:147], v[42:45], v[192:195], v[144:147]
	v_mfma_f32_16x16x32_f16 v[148:151], v[42:45], v[196:199], v[148:151]
	v_mfma_f32_16x16x32_f16 v[152:155], v[42:45], v[200:203], v[152:155]
	v_mfma_f32_16x16x32_f16 v[160:163], v[42:45], v[204:207], v[160:163]
	v_mfma_f32_16x16x32_f16 v[2:5], v[42:45], v[208:211], v[2:5]
	s_waitcnt vmcnt(12)
	v_mfma_f32_16x16x32_f16 v[14:17], v[46:49], v[34:37], v[14:17]
	v_mfma_f32_16x16x32_f16 v[18:21], v[46:49], v[84:87], v[18:21]
	v_mfma_f32_16x16x32_f16 v[30:33], v[46:49], v[188:191], v[30:33]
	v_mfma_f32_16x16x32_f16 v[34:37], v[46:49], v[192:195], v[62:65]
	v_mfma_f32_16x16x32_f16 v[42:45], v[46:49], v[196:199], v[66:69]
	v_mfma_f32_16x16x32_f16 v[62:65], v[46:49], v[200:203], v[70:73]
	v_mfma_f32_16x16x32_f16 v[66:69], v[46:49], v[204:207], v[74:77]
	v_mfma_f32_16x16x32_f16 v[6:9], v[46:49], v[208:211], v[6:9]
	s_mov_b32 s9, 0x30000
	v_add_co_u32_e32 v116, vcc, s9, v118
	s_mov_b32 s9, 0x31000
	s_nop 0
	v_addc_co_u32_e32 v117, vcc, 0, v119, vcc
	v_add_co_u32_e32 v156, vcc, s9, v118
	v_bitop3_b32 v46, v158, v1, 16 bitop3:0x36
	s_nop 0
	v_addc_co_u32_e32 v157, vcc, 0, v119, vcc
	global_load_dwordx4 v[38:41], v[156:157], off offset:-4096
	global_load_dwordx4 v[26:29], v[116:117], off offset:1024
	global_load_dwordx4 v[10:13], v[116:117], off offset:2048
	v_lshl_or_b32 v137, v46, 4, v132
	ds_read_b128 v[46:49], v137
	ds_read_b128 v[70:73], v137 offset:8192
	ds_read_b128 v[74:77], v137 offset:16384
	ds_read_b128 v[84:87], v137 offset:24576
	ds_read_b128 v[188:191], v137 offset:32768
	ds_read_b128 v[192:195], v137 offset:40960
	ds_read_b128 v[196:199], v137 offset:49152
	ds_read_b128 v[200:203], v137 offset:57344
	s_waitcnt vmcnt(14) lgkmcnt(7)
	v_mfma_f32_16x16x32_f16 v[96:99], v[50:53], v[46:49], v[96:99]
	s_waitcnt lgkmcnt(6)
	v_mfma_f32_16x16x32_f16 v[100:103], v[50:53], v[70:73], v[100:103]
	s_waitcnt lgkmcnt(5)
	v_mfma_f32_16x16x32_f16 v[104:107], v[50:53], v[74:77], v[104:107]
	s_waitcnt lgkmcnt(4)
	v_mfma_f32_16x16x32_f16 v[108:111], v[50:53], v[84:87], v[108:111]
	s_waitcnt lgkmcnt(3)
	v_mfma_f32_16x16x32_f16 v[112:115], v[50:53], v[188:191], v[112:115]
	s_waitcnt lgkmcnt(2)
	v_mfma_f32_16x16x32_f16 v[120:123], v[50:53], v[192:195], v[120:123]
	s_waitcnt lgkmcnt(1)
	v_mfma_f32_16x16x32_f16 v[124:127], v[50:53], v[196:199], v[124:127]
	s_waitcnt lgkmcnt(0)
	v_mfma_f32_16x16x32_f16 v[50:53], v[50:53], v[200:203], v[212:215]
	s_waitcnt vmcnt(13)
	v_mfma_f32_16x16x32_f16 v[204:207], v[54:57], v[46:49], v[22:25]
	v_mfma_f32_16x16x32_f16 v[208:211], v[54:57], v[70:73], v[216:219]
	v_mfma_f32_16x16x32_f16 v[128:131], v[54:57], v[74:77], v[128:131]
	v_mfma_f32_16x16x32_f16 v[144:147], v[54:57], v[84:87], v[144:147]
	v_mfma_f32_16x16x32_f16 v[148:151], v[54:57], v[188:191], v[148:151]
	v_mfma_f32_16x16x32_f16 v[152:155], v[54:57], v[192:195], v[152:155]
	v_mfma_f32_16x16x32_f16 v[160:163], v[54:57], v[196:199], v[160:163]
	v_mfma_f32_16x16x32_f16 v[54:57], v[54:57], v[200:203], v[2:5]
	s_waitcnt vmcnt(12)
	v_mfma_f32_16x16x32_f16 v[14:17], v[58:61], v[46:49], v[14:17]
	v_mfma_f32_16x16x32_f16 v[18:21], v[58:61], v[70:73], v[18:21]
	v_mfma_f32_16x16x32_f16 v[30:33], v[58:61], v[74:77], v[30:33]
	v_mfma_f32_16x16x32_f16 v[34:37], v[58:61], v[84:87], v[34:37]
	v_mfma_f32_16x16x32_f16 v[42:45], v[58:61], v[188:191], v[42:45]
	v_mfma_f32_16x16x32_f16 v[46:49], v[58:61], v[192:195], v[62:65]
	v_mfma_f32_16x16x32_f16 v[62:65], v[58:61], v[196:199], v[66:69]
	v_mfma_f32_16x16x32_f16 v[58:61], v[58:61], v[200:203], v[6:9]
	global_load_dwordx4 v[22:25], v[116:117], off offset:3072
	s_nop 1
	global_load_dwordx4 v[6:9], v[156:157], off
	global_load_dwordx4 v[2:5], v[156:157], off offset:1024
	v_bitop3_b32 v66, v158, v1, 20 bitop3:0x36
	v_lshl_or_b32 v138, v66, 4, v132
	ds_read_b128 v[66:69], v138
	ds_read_b128 v[70:73], v138 offset:8192
	ds_read_b128 v[74:77], v138 offset:16384
	ds_read_b128 v[84:87], v138 offset:24576
	ds_read_b128 v[188:191], v138 offset:32768
	ds_read_b128 v[192:195], v138 offset:40960
	ds_read_b128 v[196:199], v138 offset:49152
	ds_read_b128 v[200:203], v138 offset:57344
	s_waitcnt vmcnt(14) lgkmcnt(7)
	v_mfma_f32_16x16x32_f16 v[96:99], v[92:95], v[66:69], v[96:99]
	s_waitcnt lgkmcnt(6)
	v_mfma_f32_16x16x32_f16 v[100:103], v[92:95], v[70:73], v[100:103]
	s_waitcnt lgkmcnt(5)
	v_mfma_f32_16x16x32_f16 v[104:107], v[92:95], v[74:77], v[104:107]
	s_waitcnt lgkmcnt(4)
	v_mfma_f32_16x16x32_f16 v[108:111], v[92:95], v[84:87], v[108:111]
	s_waitcnt lgkmcnt(3)
	v_mfma_f32_16x16x32_f16 v[112:115], v[92:95], v[188:191], v[112:115]
	s_waitcnt lgkmcnt(2)
	v_mfma_f32_16x16x32_f16 v[212:215], v[92:95], v[192:195], v[120:123]
	s_waitcnt lgkmcnt(1)
	v_mfma_f32_16x16x32_f16 v[124:127], v[92:95], v[196:199], v[124:127]
	s_waitcnt lgkmcnt(0)
	v_mfma_f32_16x16x32_f16 v[50:53], v[92:95], v[200:203], v[50:53]
	s_waitcnt vmcnt(13)
	v_mfma_f32_16x16x32_f16 v[92:95], v[168:171], v[66:69], v[204:207]
	v_mfma_f32_16x16x32_f16 v[204:207], v[168:171], v[70:73], v[208:211]
	v_mfma_f32_16x16x32_f16 v[128:131], v[168:171], v[74:77], v[128:131]
	v_mfma_f32_16x16x32_f16 v[144:147], v[168:171], v[84:87], v[144:147]
	v_mfma_f32_16x16x32_f16 v[148:151], v[168:171], v[188:191], v[148:151]
	v_mfma_f32_16x16x32_f16 v[152:155], v[168:171], v[192:195], v[152:155]
	v_mfma_f32_16x16x32_f16 v[160:163], v[168:171], v[196:199], v[160:163]
	v_mfma_f32_16x16x32_f16 v[54:57], v[168:171], v[200:203], v[54:57]
	s_waitcnt vmcnt(12)
	v_mfma_f32_16x16x32_f16 v[66:69], v[172:175], v[66:69], v[14:17]
	v_mfma_f32_16x16x32_f16 v[70:73], v[172:175], v[70:73], v[18:21]
	v_mfma_f32_16x16x32_f16 v[74:77], v[172:175], v[74:77], v[30:33]
	v_mfma_f32_16x16x32_f16 v[34:37], v[172:175], v[84:87], v[34:37]
	v_mfma_f32_16x16x32_f16 v[42:45], v[172:175], v[188:191], v[42:45]
	v_mfma_f32_16x16x32_f16 v[46:49], v[172:175], v[192:195], v[46:49]
	v_mfma_f32_16x16x32_f16 v[62:65], v[172:175], v[196:199], v[62:65]
	v_mfma_f32_16x16x32_f16 v[58:61], v[172:175], v[200:203], v[58:61]
	s_mov_b32 s9, 0x33000
	v_add_co_u32_e32 v122, vcc, s9, v118
	global_load_dwordx4 v[30:33], v[156:157], off offset:2048
	global_load_dwordx4 v[14:17], v[156:157], off offset:3072
	v_addc_co_u32_e32 v123, vcc, 0, v119, vcc
	global_load_dwordx4 v[18:21], v[122:123], off offset:-4096
	v_bitop3_b32 v84, v158, v1, 24 bitop3:0x36
	v_lshl_or_b32 v139, v84, 4, v132
	ds_read_b128 v[84:87], v139
	ds_read_b128 v[168:171], v139 offset:8192
	ds_read_b128 v[172:175], v139 offset:16384
	ds_read_b128 v[188:191], v139 offset:24576
	ds_read_b128 v[192:195], v139 offset:32768
	ds_read_b128 v[196:199], v139 offset:40960
	ds_read_b128 v[200:203], v139 offset:49152
	ds_read_b128 v[208:211], v139 offset:57344
	s_mov_b32 s9, 0x32000
	v_add_co_u32_e32 v116, vcc, s9, v118
	s_nop 1
	v_addc_co_u32_e32 v117, vcc, 0, v119, vcc
	s_waitcnt vmcnt(14) lgkmcnt(7)
	v_mfma_f32_16x16x32_f16 v[96:99], v[88:91], v[84:87], v[96:99]
	s_waitcnt lgkmcnt(6)
	v_mfma_f32_16x16x32_f16 v[100:103], v[88:91], v[168:171], v[100:103]
	s_waitcnt lgkmcnt(5)
	v_mfma_f32_16x16x32_f16 v[104:107], v[88:91], v[172:175], v[104:107]
	s_waitcnt lgkmcnt(4)
	v_mfma_f32_16x16x32_f16 v[108:111], v[88:91], v[188:191], v[108:111]
	s_waitcnt lgkmcnt(3)
	v_mfma_f32_16x16x32_f16 v[112:115], v[88:91], v[192:195], v[112:115]
	s_waitcnt lgkmcnt(2)
	v_mfma_f32_16x16x32_f16 v[212:215], v[88:91], v[196:199], v[212:215]
	s_waitcnt lgkmcnt(1)
	v_mfma_f32_16x16x32_f16 v[124:127], v[88:91], v[200:203], v[124:127]
	s_waitcnt lgkmcnt(0)
	v_mfma_f32_16x16x32_f16 v[50:53], v[88:91], v[208:211], v[50:53]
	s_waitcnt vmcnt(13)
	v_mfma_f32_16x16x32_f16 v[90:93], v[164:167], v[84:87], v[92:95]
	v_mfma_f32_16x16x32_f16 v[204:207], v[164:167], v[168:171], v[204:207]
	v_mfma_f32_16x16x32_f16 v[128:131], v[164:167], v[172:175], v[128:131]
	v_mfma_f32_16x16x32_f16 v[144:147], v[164:167], v[188:191], v[144:147]
	v_mfma_f32_16x16x32_f16 v[148:151], v[164:167], v[192:195], v[148:151]
	v_mfma_f32_16x16x32_f16 v[152:155], v[164:167], v[196:199], v[152:155]
	v_mfma_f32_16x16x32_f16 v[160:163], v[164:167], v[200:203], v[160:163]
	v_mfma_f32_16x16x32_f16 v[54:57], v[164:167], v[208:211], v[54:57]
	s_waitcnt vmcnt(12)
	v_mfma_f32_16x16x32_f16 v[164:167], v[176:179], v[84:87], v[66:69]
	v_mfma_f32_16x16x32_f16 v[168:171], v[176:179], v[168:171], v[70:73]
	v_mfma_f32_16x16x32_f16 v[172:175], v[176:179], v[172:175], v[74:77]
	v_mfma_f32_16x16x32_f16 v[188:191], v[176:179], v[188:191], v[34:37]
	v_mfma_f32_16x16x32_f16 v[192:195], v[176:179], v[192:195], v[42:45]
	v_mfma_f32_16x16x32_f16 v[196:199], v[176:179], v[196:199], v[46:49]
	v_mfma_f32_16x16x32_f16 v[200:203], v[176:179], v[200:203], v[62:65]
	v_mfma_f32_16x16x32_f16 v[176:179], v[176:179], v[208:211], v[58:61]
	s_nop 0
	global_load_dwordx4 v[46:49], v[116:117], off offset:1024
	global_load_dwordx4 v[42:45], v[116:117], off offset:2048
	global_load_dwordx4 v[34:37], v[116:117], off offset:3072
	v_bitop3_b32 v58, v158, v1, 28 bitop3:0x36
	v_lshl_or_b32 v141, v58, 4, v132
	ds_read_b128 v[58:61], v141
	ds_read_b128 v[62:65], v141 offset:8192
	ds_read_b128 v[156:159], v141 offset:16384
	ds_read_b128 v[208:211], v141 offset:24576
	ds_read_b128 v[216:219], v141 offset:32768
	ds_read_b128 v[220:223], v141 offset:40960
	ds_read_b128 v[224:227], v141 offset:49152
	ds_read_b128 v[228:231], v141 offset:57344
	s_waitcnt vmcnt(14) lgkmcnt(7)
	v_mfma_f32_16x16x32_f16 v[232:235], v[78:81], v[58:61], v[96:99]
	s_waitcnt lgkmcnt(6)
	v_mfma_f32_16x16x32_f16 v[236:239], v[78:81], v[62:65], v[100:103]
	s_waitcnt lgkmcnt(5)
	v_mfma_f32_16x16x32_f16 v[240:243], v[78:81], v[156:159], v[104:107]
	s_waitcnt lgkmcnt(4)
	v_mfma_f32_16x16x32_f16 v[244:247], v[78:81], v[208:211], v[108:111]
	s_waitcnt lgkmcnt(3)
	v_mfma_f32_16x16x32_f16 v[106:109], v[78:81], v[216:219], v[112:115]
	s_waitcnt lgkmcnt(2)
	v_mfma_f32_16x16x32_f16 v[102:105], v[78:81], v[220:223], v[212:215]
	s_waitcnt lgkmcnt(1)
	v_mfma_f32_16x16x32_f16 v[94:97], v[78:81], v[224:227], v[124:127]
	s_waitcnt lgkmcnt(0)
	v_mfma_f32_16x16x32_f16 v[86:89], v[78:81], v[228:231], v[50:53]
	s_waitcnt vmcnt(13)
	v_mfma_f32_16x16x32_f16 v[124:127], v[180:183], v[58:61], v[90:93]
	v_mfma_f32_16x16x32_f16 v[204:207], v[180:183], v[62:65], v[204:207]
	v_mfma_f32_16x16x32_f16 v[212:215], v[180:183], v[156:159], v[128:131]
	v_mfma_f32_16x16x32_f16 v[144:147], v[180:183], v[208:211], v[144:147]
	v_mfma_f32_16x16x32_f16 v[78:81], v[180:183], v[216:219], v[148:151]
	v_mfma_f32_16x16x32_f16 v[74:77], v[180:183], v[220:223], v[152:155]
	v_mfma_f32_16x16x32_f16 v[70:73], v[180:183], v[224:227], v[160:163]
	v_mfma_f32_16x16x32_f16 v[66:69], v[180:183], v[228:231], v[54:57]
	s_waitcnt vmcnt(12)
	v_mfma_f32_16x16x32_f16 v[148:151], v[184:187], v[58:61], v[164:167]
	v_mfma_f32_16x16x32_f16 v[152:155], v[184:187], v[62:65], v[168:171]
	v_mfma_f32_16x16x32_f16 v[114:117], v[184:187], v[156:159], v[172:175]
	v_mfma_f32_16x16x32_f16 v[110:113], v[184:187], v[208:211], v[188:191]
	v_mfma_f32_16x16x32_f16 v[62:65], v[184:187], v[216:219], v[192:195]
	v_mfma_f32_16x16x32_f16 v[58:61], v[184:187], v[220:223], v[196:199]
	v_mfma_f32_16x16x32_f16 v[54:57], v[184:187], v[224:227], v[200:203]
	v_mfma_f32_16x16x32_f16 v[50:53], v[184:187], v[228:231], v[176:179]
	v_lshl_add_u64 v[120:121], v[82:83], 2, s[4:5]
	global_load_dwordx4 v[98:101], v[120:121], off
	global_load_dwordx4 v[90:93], v[120:121], off offset:64
	global_load_dwordx4 v[82:85], v[120:121], off offset:128
	s_movk_i32 s4, 0x310
	v_mad_u32_u24 v130, v1, s4, v248
	v_mov_b32_e32 v156, v237
	v_mov_b32_e32 v157, v238
	v_mov_b32_e32 v158, v241
	v_mov_b32_e32 v159, v242
	v_mov_b32_e32 v160, v245
	v_mov_b32_e32 v161, v246
	v_mov_b32_e32 v162, v205
	v_mov_b32_e32 v163, v206
	v_mov_b32_e32 v167, v146
	v_mov_b32_e32 v164, v213
	v_mov_b32_e32 v165, v214
	v_mov_b32_e32 v166, v145
	s_barrier
	v_add_u32_e32 v132, 0x3000, v130
	v_add_u32_e32 v131, 0x6000, v130
	s_mov_b32 s5, 0xfffffd0
	v_mul_lo_u32 v174, v142, s5
	s_movk_i32 s4, 0x600
	s_movk_i32 s9, 0xc7
	s_waitcnt vmcnt(2)
	v_pk_add_f32 v[168:169], v[232:233], v[98:99]
	v_pk_add_f32 v[170:171], v[234:235], v[100:101]
	v_add_f32_e32 v1, v236, v98
	v_pk_mov_b32 v[128:129], v[98:99], v[100:101] op_sel:[1,0]
	v_add_f32_e32 v99, v239, v101
	s_waitcnt vmcnt(1)
	v_pk_add_f32 v[124:125], v[124:125], v[90:91]
	v_pk_add_f32 v[172:173], v[126:127], v[92:93]
	v_add_f32_e32 v178, v204, v90
	v_pk_mov_b32 v[126:127], v[90:91], v[92:93] op_sel:[1,0]
	v_add_f32_e32 v91, v207, v93
	v_add_f32_e32 v100, v240, v98
	v_add_f32_e32 v175, v243, v101
	v_add_f32_e32 v92, v212, v90
	v_add_f32_e32 v179, v215, v93
	v_add_f32_e32 v181, v147, v93
	v_cvt_pk_f16_f32 v147, v170, v171
	v_cvt_f16_f32_e32 v1, v1
	v_cvt_f16_f32_e32 v99, v99
	v_cvt_f16_f32_e32 v171, v178
	v_cvt_f16_f32_e32 v91, v91
	v_cvt_pk_f16_f32 v146, v168, v169
	v_cvt_f16_f32_e32 v100, v100
	v_cvt_f16_f32_e32 v168, v175
	v_cvt_pk_f16_f32 v124, v124, v125
	v_cvt_pk_f16_f32 v125, v172, v173
	v_cvt_f16_f32_e32 v92, v92
	v_cvt_f16_f32_e32 v172, v179
	v_add_f32_e32 v180, v144, v90
	s_waitcnt vmcnt(0)
	v_pk_add_f32 v[144:145], v[148:149], v[82:83]
	v_pk_add_f32 v[148:149], v[156:157], v[128:129]
	v_pk_add_f32 v[156:157], v[158:159], v[128:129]
	v_pk_add_f32 v[158:159], v[160:161], v[128:129]
	v_pk_add_f32 v[160:161], v[162:163], v[126:127]
	v_pk_add_f32 v[162:163], v[164:165], v[126:127]
	v_cvt_pk_f16_f32 v144, v144, v145
	v_cvt_pk_f16_f32 v145, v148, v149
	v_cvt_pk_f16_f32 v148, v156, v157
	v_cvt_pk_f16_f32 v157, v160, v161
	v_cvt_pk_f16_f32 v149, v158, v159
	v_cvt_pk_f16_f32 v159, v162, v163
	ds_write2_b64 v130, v[146:147], v[124:125] offset1:4
	v_pack_b32_f16 v124, v1, v145
	v_alignbit_b32 v125, v99, v145, 16
	v_pack_b32_f16 v156, v171, v157
	v_alignbit_b32 v157, v91, v157, 16
	v_pack_b32_f16 v146, v100, v148
	v_alignbit_b32 v147, v168, v148, 16
	v_pack_b32_f16 v158, v92, v159
	v_alignbit_b32 v159, v172, v159, 16
	ds_write2_b64 v132, v[124:125], v[156:157] offset0:32 offset1:36
	ds_write2_b64 v131, v[146:147], v[158:159] offset0:64 offset1:68
	v_pk_add_f32 v[124:125], v[150:151], v[84:85]
	v_add_f32_e32 v1, v152, v82
	v_cvt_pk_f16_f32 v145, v124, v125
	v_pk_mov_b32 v[124:125], v[82:83], v[84:85] op_sel:[1,0]
	v_add_f32_e32 v83, v155, v85
	v_cvt_f16_f32_e32 v1, v1
	v_cvt_f16_f32_e32 v83, v83
	ds_write_b64 v130, v[144:145] offset:64
	v_mov_b32_e32 v144, v153
	v_mov_b32_e32 v145, v154
	v_pk_add_f32 v[144:145], v[144:145], v[124:125]
	v_add_f32_e32 v176, v244, v98
	v_cvt_pk_f16_f32 v84, v144, v145
	v_pack_b32_f16 v144, v1, v84
	v_alignbit_b32 v145, v83, v84, 16
	v_add_f32_e32 v1, v114, v82
	v_add_f32_e32 v83, v117, v85
	v_cvt_f16_f32_e32 v1, v1
	v_cvt_f16_f32_e32 v83, v83
	v_mov_b32_e32 v114, v115
	v_mov_b32_e32 v115, v116
	v_pk_add_f32 v[114:115], v[114:115], v[124:125]
	v_add_f32_e32 v177, v247, v101
	v_cvt_pk_f16_f32 v84, v114, v115
	v_pack_b32_f16 v114, v1, v84
	v_alignbit_b32 v115, v83, v84, 16
	v_add_f32_e32 v1, v110, v82
	v_add_f32_e32 v83, v113, v85
	v_cvt_f16_f32_e32 v1, v1
	v_cvt_f16_f32_e32 v83, v83
	v_mov_b32_e32 v110, v111
	v_mov_b32_e32 v111, v112
	v_cvt_f16_f32_e32 v169, v176
	v_cvt_f16_f32_e32 v170, v177
	v_cvt_f16_f32_e32 v173, v180
	v_pk_add_f32 v[164:165], v[166:167], v[126:127]
	v_cvt_f16_f32_e32 v166, v181
	v_pk_add_f32 v[110:111], v[110:111], v[124:125]
	v_cvt_pk_f16_f32 v161, v164, v165
	v_cvt_pk_f16_f32 v84, v110, v111
	v_pack_b32_f16 v110, v1, v84
	v_alignbit_b32 v111, v83, v84, 16
	ds_write_b64 v130, v[110:111] offset:37696
	v_add_lshl_u32 v111, v174, v0, 4
	v_mul_u32_u24_e32 v83, 0x310, v142
	v_pack_b32_f16 v148, v169, v149
	v_alignbit_b32 v149, v170, v149, 16
	v_pack_b32_f16 v160, v173, v161
	v_alignbit_b32 v161, v166, v161, 16
	v_add_u32_e32 v91, 0x9000, v130
	v_add3_u32 v83, v111, v83, s8
	v_or_b32_e32 v84, 0x200, v0
	ds_write2_b64 v91, v[148:149], v[160:161] offset0:96 offset1:100
	ds_write_b64 v130, v[144:145] offset:12608
	ds_write_b64 v130, v[114:115] offset:25152
	s_waitcnt lgkmcnt(0)
	s_barrier
	ds_read_b128 v[114:117], v83
	v_mul_u32_u24_e32 v92, 0x556, v84
	v_lshrrev_b32_e32 v92, 16, v92
	v_or_b32_e32 v1, s7, v143
	v_mul_lo_u32 v99, v92, s5
	v_mul_lo_u32 v112, v1, s4
	v_add_lshl_u32 v113, v99, v84, 4
	v_mul_u32_u24_e32 v84, 0x310, v92
	v_add_u32_e32 v1, v112, v111
	v_add3_u32 v84, v113, v84, s8
	ds_read_b128 v[142:145], v84
	s_waitcnt lgkmcnt(1)
	buffer_store_dwordx4 v[114:117], v1, s[0:3], 0 offen sc1
	v_lshlrev_b32_e32 v1, 3, v92
	v_bitop3_b32 v154, v1, s9, v92 bitop3:0xc8
	v_or_b32_e32 v1, s7, v154
	v_mul_lo_u32 v114, v1, s4
	v_add_u32_e32 v1, v114, v113
	s_waitcnt lgkmcnt(0)
	buffer_store_dwordx4 v[142:145], v1, s[0:3], 0 offen sc1
	v_or_b32_e32 v1, 0x400, v0
	v_mul_u32_u24_e32 v92, 0x556, v1
	v_lshrrev_b32_e32 v92, 16, v92
	v_mul_lo_u32 v99, v92, s5
	v_lshlrev_b32_e32 v100, 3, v92
	s_movk_i32 s9, 0x1c7
	v_bitop3_b32 v155, v100, s9, v92 bitop3:0xc8
	v_add_lshl_u32 v115, v99, v1, 4
	v_mul_u32_u24_e32 v92, 0x310, v92
	v_or_b32_e32 v100, s7, v155
	v_add3_u32 v92, v115, v92, s8
	v_or_b32_e32 v99, 0x600, v0
	v_mul_lo_u32 v116, v100, s4
	ds_read_b128 v[142:145], v92
	v_mul_u32_u24_e32 v100, 0x556, v99
	v_lshrrev_b32_e32 v100, 16, v100
	v_mul_lo_u32 v110, v100, s5
	v_add_lshl_u32 v117, v110, v99, 4
	v_mul_u32_u24_e32 v99, 0x310, v100
	v_add_u32_e32 v1, v116, v115
	v_add3_u32 v99, v117, v99, s8
	ds_read_b128 v[146:149], v99
	s_waitcnt lgkmcnt(1)
	buffer_store_dwordx4 v[142:145], v1, s[0:3], 0 offen sc1
	v_lshlrev_b32_e32 v1, 3, v100
	v_bitop3_b32 v156, v1, s9, v100 bitop3:0xc8
	v_add_u32_e32 v1, s7, v156
	v_mul_lo_u32 v142, v1, s4
	v_add_u32_e32 v1, v142, v117
	s_waitcnt lgkmcnt(0)
	buffer_store_dwordx4 v[146:149], v1, s[0:3], 0 offen sc1
	v_or_b32_e32 v1, 0x800, v0
	v_mul_u32_u24_e32 v100, 0xaab, v1
	v_lshrrev_b32_e32 v100, 17, v100
	v_mul_lo_u32 v110, v100, s5
	v_lshlrev_b32_e32 v143, 3, v100
	v_bitop3_b32 v157, v143, s9, v100 bitop3:0xc8
	v_add_lshl_u32 v144, v110, v1, 4
	v_mul_u32_u24_e32 v100, 0x310, v100
	v_or_b32_e32 v0, 0xa00, v0
	v_add3_u32 v100, v100, v144, s8
	v_mul_u32_u24_e32 v110, 0xaab, v0
	ds_read_b128 v[146:149], v100
	v_lshrrev_b32_e32 v158, 17, v110
	v_mul_lo_u32 v110, v158, s5
	v_or_b32_e32 v143, s7, v157
	v_add_lshl_u32 v145, v110, v0, 4
	v_mul_u32_u24_e32 v0, 0x310, v158
	v_mul_lo_u32 v143, v143, s4
	v_add3_u32 v110, v0, v145, s8
	v_add_u32_e32 v1, v143, v144
	ds_read_b128 v[150:153], v110
	v_lshlrev_b32_e32 v0, 3, v158
	s_movk_i32 s5, 0x3c7
	s_waitcnt lgkmcnt(1)
	buffer_store_dwordx4 v[146:149], v1, s[0:3], 0 offen sc1
	v_mov_b32_e32 v1, v108
	v_add_f32_e32 v102, v102, v98
	v_bitop3_b32 v147, v0, s5, v158 bitop3:0xc8
	v_add_u32_e32 v0, s7, v147
	v_mul_lo_u32 v146, v0, s4
	v_add_u32_e32 v0, v146, v145
	s_waitcnt lgkmcnt(0)
	buffer_store_dwordx4 v[150:153], v0, s[0:3], 0 offen sc1
	v_add_f32_e32 v0, v106, v98
	v_cvt_f16_f32_e32 v106, v0
	v_mov_b32_e32 v0, v107
	v_pk_add_f32 v[0:1], v[0:1], v[128:129]
	v_add_f32_e32 v94, v94, v98
	v_cvt_pk_f16_f32 v1, v0, v1
	v_pack_b32_f16 v0, v106, v1
	v_cvt_f16_f32_e32 v106, v102
	v_mov_b32_e32 v102, v103
	v_mov_b32_e32 v103, v104
	v_add_f32_e32 v104, v105, v101
	v_cvt_f16_f32_e32 v104, v104
	v_pk_add_f32 v[102:103], v[102:103], v[128:129]
	v_add_f32_e32 v86, v86, v98
	v_cvt_pk_f16_f32 v103, v102, v103
	v_pack_b32_f16 v102, v106, v103
	v_alignbit_b32 v103, v104, v103, 16
	v_cvt_f16_f32_e32 v104, v94
	v_mov_b32_e32 v94, v95
	v_mov_b32_e32 v95, v96
	v_add_f32_e32 v96, v97, v101
	v_cvt_f16_f32_e32 v96, v96
	v_pk_add_f32 v[94:95], v[94:95], v[128:129]
	v_add_f32_e32 v78, v78, v90
	v_cvt_pk_f16_f32 v95, v94, v95
	v_pack_b32_f16 v94, v104, v95
	v_alignbit_b32 v95, v96, v95, 16
	v_cvt_f16_f32_e32 v96, v86
	v_mov_b32_e32 v86, v87
	v_mov_b32_e32 v87, v88
	v_add_f32_e32 v88, v89, v101
	v_cvt_f16_f32_e32 v88, v88
	v_pk_add_f32 v[86:87], v[86:87], v[128:129]
	v_add_f32_e32 v107, v109, v101
	v_cvt_pk_f16_f32 v87, v86, v87
	v_pack_b32_f16 v86, v96, v87
	v_alignbit_b32 v87, v88, v87, 16
	v_cvt_f16_f32_e32 v88, v78
	v_mov_b32_e32 v78, v79
	v_mov_b32_e32 v79, v80
	v_add_f32_e32 v80, v81, v93
	v_cvt_f16_f32_e32 v107, v107
	v_cvt_f16_f32_e32 v80, v80
	v_pk_add_f32 v[78:79], v[78:79], v[126:127]
	s_nop 0
	v_cvt_pk_f16_f32 v79, v78, v79
	v_alignbit_b32 v1, v107, v1, 16
	v_pack_b32_f16 v78, v88, v79
	v_alignbit_b32 v79, v80, v79, 16
	s_barrier
	ds_write2_b64 v130, v[0:1], v[78:79] offset1:4
	v_add_f32_e32 v0, v74, v90
	v_cvt_f16_f32_e32 v74, v0
	v_mov_b32_e32 v0, v75
	v_add_f32_e32 v75, v77, v93
	v_cvt_f16_f32_e32 v75, v75
	v_mov_b32_e32 v1, v76
	v_pk_add_f32 v[0:1], v[0:1], v[126:127]
	s_nop 0
	v_cvt_pk_f16_f32 v1, v0, v1
	v_pack_b32_f16 v0, v74, v1
	v_alignbit_b32 v1, v75, v1, 16
	ds_write2_b64 v132, v[102:103], v[0:1] offset0:32 offset1:36
	v_add_f32_e32 v0, v70, v90
	v_cvt_f16_f32_e32 v70, v0
	v_mov_b32_e32 v0, v71
	v_add_f32_e32 v71, v73, v93
	v_cvt_f16_f32_e32 v71, v71
	v_mov_b32_e32 v1, v72
	v_pk_add_f32 v[0:1], v[0:1], v[126:127]
	s_nop 0
	v_cvt_pk_f16_f32 v1, v0, v1
	v_pack_b32_f16 v0, v70, v1
	v_alignbit_b32 v1, v71, v1, 16
	ds_write2_b64 v131, v[94:95], v[0:1] offset0:64 offset1:68
	v_add_f32_e32 v0, v66, v90
	v_cvt_f16_f32_e32 v66, v0
	v_mov_b32_e32 v0, v67
	v_add_f32_e32 v67, v69, v93
	v_cvt_f16_f32_e32 v67, v67
	v_mov_b32_e32 v1, v68
	v_pk_add_f32 v[0:1], v[0:1], v[126:127]
	v_mul_lo_u32 v68, v140, s4
	v_cvt_pk_f16_f32 v1, v0, v1
	v_pack_b32_f16 v0, v66, v1
	v_alignbit_b32 v1, v67, v1, 16
	ds_write2_b64 v91, v[86:87], v[0:1] offset0:96 offset1:100
	v_add_f32_e32 v0, v62, v82
	v_cvt_f16_f32_e32 v62, v0
	v_mov_b32_e32 v0, v63
	v_add_f32_e32 v63, v65, v85
	v_cvt_f16_f32_e32 v63, v63
	v_mov_b32_e32 v1, v64
	v_pk_add_f32 v[0:1], v[0:1], v[124:125]
	s_nop 0
	v_cvt_pk_f16_f32 v1, v0, v1
	v_pack_b32_f16 v0, v62, v1
	v_alignbit_b32 v1, v63, v1, 16
	ds_write_b64 v130, v[0:1] offset:64
	v_add_f32_e32 v0, v58, v82
	v_cvt_f16_f32_e32 v58, v0
	v_mov_b32_e32 v0, v59
	v_add_f32_e32 v59, v61, v85
	v_cvt_f16_f32_e32 v59, v59
	v_mov_b32_e32 v1, v60
	v_pk_add_f32 v[0:1], v[0:1], v[124:125]
	s_nop 0
	v_cvt_pk_f16_f32 v1, v0, v1
	v_pack_b32_f16 v0, v58, v1
	v_alignbit_b32 v1, v59, v1, 16
	ds_write_b64 v130, v[0:1] offset:12608
	v_add_f32_e32 v0, v54, v82
	v_cvt_f16_f32_e32 v54, v0
	v_mov_b32_e32 v0, v55
	v_add_f32_e32 v55, v57, v85
	v_cvt_f16_f32_e32 v55, v55
	v_mov_b32_e32 v1, v56
	v_pk_add_f32 v[0:1], v[0:1], v[124:125]
	s_nop 0
	v_cvt_pk_f16_f32 v1, v0, v1
	v_pack_b32_f16 v0, v54, v1
	v_alignbit_b32 v1, v55, v1, 16
	ds_write_b64 v130, v[0:1] offset:25152
	v_add_f32_e32 v0, v50, v82
	v_cvt_f16_f32_e32 v50, v0
	v_mov_b32_e32 v0, v51
	v_add_f32_e32 v51, v53, v85
	v_cvt_f16_f32_e32 v51, v51
	v_mov_b32_e32 v1, v52
	v_pk_add_f32 v[0:1], v[0:1], v[124:125]
	s_nop 0
	v_cvt_pk_f16_f32 v1, v0, v1
	v_pack_b32_f16 v0, v50, v1
	v_alignbit_b32 v1, v51, v1, 16
	ds_write_b64 v130, v[0:1] offset:37696
	s_waitcnt lgkmcnt(0)
	s_barrier
	global_load_dwordx4 v[50:53], v[122:123], off
	global_load_dwordx4 v[54:57], v[122:123], off offset:1024
	global_load_dwordx4 v[58:61], v[122:123], off offset:2048
	ds_read_b128 v[62:65], v83
	ds_read_b128 v[70:73], v84
	v_add_u32_e32 v0, v68, v111
	ds_read_b128 v[74:77], v99
	s_waitcnt lgkmcnt(2)
	buffer_store_dwordx4 v[62:65], v0, s[0:3], 0 offen sc1
	v_or_b32_e32 v0, s6, v154
	v_mul_lo_u32 v69, v0, s4
	ds_read_b128 v[62:65], v92
	v_add_u32_e32 v0, v69, v113
	s_waitcnt lgkmcnt(2)
	buffer_store_dwordx4 v[70:73], v0, s[0:3], 0 offen sc1
	v_or_b32_e32 v0, s6, v155
	s_nop 0
	v_mul_lo_u32 v72, v0, s4
	v_add_u32_e32 v0, v72, v115
	s_waitcnt lgkmcnt(0)
	buffer_store_dwordx4 v[62:65], v0, s[0:3], 0 offen sc1
	v_add_u32_e32 v0, s6, v156
	v_mul_lo_u32 v70, v0, s4
	ds_read_b128 v[62:65], v100
	v_add_u32_e32 v0, v70, v117
	buffer_store_dwordx4 v[74:77], v0, s[0:3], 0 offen sc1
	v_or_b32_e32 v0, s6, v157
	v_mul_lo_u32 v71, v0, s4
	v_add_u32_e32 v0, v71, v144
	ds_read_b128 v[74:77], v110
	s_waitcnt lgkmcnt(1)
	buffer_store_dwordx4 v[62:65], v0, s[0:3], 0 offen sc1
	ds_read_b128 v[62:65], v135
	ds_read_b128 v[78:81], v135 offset:8192
	ds_read_b128 v[86:89], v135 offset:16384
	ds_read_b128 v[94:97], v135 offset:24576
	ds_read_b128 v[102:105], v135 offset:32768
	ds_read_b128 v[106:109], v135 offset:40960
	ds_read_b128 v[124:127], v135 offset:49152
	ds_read_b128 v[148:151], v135 offset:57344
	v_add_u32_e32 v0, s6, v147
	v_mul_lo_u32 v73, v0, s4
	v_add_u32_e32 v0, v73, v145
	s_waitcnt lgkmcnt(8)
	buffer_store_dwordx4 v[74:77], v0, s[0:3], 0 offen sc1
	s_waitcnt lgkmcnt(7)
	s_nop 0
	v_mfma_f32_16x16x32_f16 v[74:77], v[38:41], v[62:65], 0
	s_waitcnt lgkmcnt(6)
	v_mfma_f32_16x16x32_f16 v[152:155], v[38:41], v[78:81], 0
	s_waitcnt lgkmcnt(5)
	v_mfma_f32_16x16x32_f16 v[156:159], v[38:41], v[86:89], 0
	s_waitcnt lgkmcnt(4)
	v_mfma_f32_16x16x32_f16 v[160:163], v[38:41], v[94:97], 0
	s_waitcnt lgkmcnt(3)
	v_mfma_f32_16x16x32_f16 v[164:167], v[38:41], v[102:105], 0
	s_waitcnt lgkmcnt(2)
	v_mfma_f32_16x16x32_f16 v[168:171], v[38:41], v[106:109], 0
	s_waitcnt lgkmcnt(1)
	v_mfma_f32_16x16x32_f16 v[172:175], v[38:41], v[124:127], 0
	s_waitcnt lgkmcnt(0)
	v_mfma_f32_16x16x32_f16 v[38:41], v[38:41], v[148:151], 0
	v_mfma_f32_16x16x32_f16 v[176:179], v[26:29], v[62:65], 0
	v_mfma_f32_16x16x32_f16 v[180:183], v[26:29], v[78:81], 0
	v_mfma_f32_16x16x32_f16 v[184:187], v[26:29], v[86:89], 0
	v_mfma_f32_16x16x32_f16 v[188:191], v[26:29], v[94:97], 0
	v_mfma_f32_16x16x32_f16 v[192:195], v[26:29], v[102:105], 0
	v_mfma_f32_16x16x32_f16 v[196:199], v[26:29], v[106:109], 0
	v_mfma_f32_16x16x32_f16 v[200:203], v[26:29], v[124:127], 0
	v_mfma_f32_16x16x32_f16 v[26:29], v[26:29], v[148:151], 0
	v_mfma_f32_16x16x32_f16 v[62:65], v[10:13], v[62:65], 0
	v_mfma_f32_16x16x32_f16 v[78:81], v[10:13], v[78:81], 0
	v_mfma_f32_16x16x32_f16 v[86:89], v[10:13], v[86:89], 0
	v_mfma_f32_16x16x32_f16 v[94:97], v[10:13], v[94:97], 0
	v_mfma_f32_16x16x32_f16 v[102:105], v[10:13], v[102:105], 0
	v_mfma_f32_16x16x32_f16 v[106:109], v[10:13], v[106:109], 0
	v_mfma_f32_16x16x32_f16 v[124:127], v[10:13], v[124:127], 0
	v_mfma_f32_16x16x32_f16 v[10:13], v[10:13], v[148:151], 0
	s_mov_b32 s4, 0x34000
	v_add_co_u32_e32 v66, vcc, s4, v118
	s_mov_b32 s4, 0x35000
	s_nop 0
	v_addc_co_u32_e32 v67, vcc, 0, v119, vcc
	v_add_co_u32_e32 v118, vcc, s4, v118
	s_nop 1
	v_addc_co_u32_e32 v119, vcc, 0, v119, vcc
	global_load_dwordx4 v[148:151], v[118:119], off offset:-4096
	global_load_dwordx4 v[204:207], v[122:123], off offset:3072
	global_load_dwordx4 v[208:211], v[66:67], off offset:1024
	ds_read_b128 v[212:215], v133
	ds_read_b128 v[216:219], v133 offset:8192
	ds_read_b128 v[220:223], v133 offset:16384
	ds_read_b128 v[224:227], v133 offset:24576
	ds_read_b128 v[228:231], v133 offset:32768
	ds_read_b128 v[232:235], v133 offset:40960
	ds_read_b128 v[236:239], v133 offset:49152
	ds_read_b128 v[240:243], v133 offset:57344
	s_waitcnt lgkmcnt(7)
	v_mfma_f32_16x16x32_f16 v[74:77], v[22:25], v[212:215], v[74:77]
	s_waitcnt lgkmcnt(6)
	v_mfma_f32_16x16x32_f16 v[152:155], v[22:25], v[216:219], v[152:155]
	s_waitcnt lgkmcnt(5)
	v_mfma_f32_16x16x32_f16 v[156:159], v[22:25], v[220:223], v[156:159]
	s_waitcnt lgkmcnt(4)
	v_mfma_f32_16x16x32_f16 v[160:163], v[22:25], v[224:227], v[160:163]
	s_waitcnt lgkmcnt(3)
	v_mfma_f32_16x16x32_f16 v[164:167], v[22:25], v[228:231], v[164:167]
	s_waitcnt lgkmcnt(2)
	v_mfma_f32_16x16x32_f16 v[168:171], v[22:25], v[232:235], v[168:171]
	s_waitcnt lgkmcnt(1)
	v_mfma_f32_16x16x32_f16 v[172:175], v[22:25], v[236:239], v[172:175]
	s_waitcnt lgkmcnt(0)
	v_mfma_f32_16x16x32_f16 v[22:25], v[22:25], v[240:243], v[38:41]
	v_mfma_f32_16x16x32_f16 v[38:41], v[6:9], v[212:215], v[176:179]
	v_mfma_f32_16x16x32_f16 v[176:179], v[6:9], v[216:219], v[180:183]
	v_mfma_f32_16x16x32_f16 v[180:183], v[6:9], v[220:223], v[184:187]
	v_mfma_f32_16x16x32_f16 v[184:187], v[6:9], v[224:227], v[188:191]
	v_mfma_f32_16x16x32_f16 v[188:191], v[6:9], v[228:231], v[192:195]
	v_mfma_f32_16x16x32_f16 v[192:195], v[6:9], v[232:235], v[196:199]
	v_mfma_f32_16x16x32_f16 v[196:199], v[6:9], v[236:239], v[200:203]
	v_mfma_f32_16x16x32_f16 v[6:9], v[6:9], v[240:243], v[26:29]
	v_mfma_f32_16x16x32_f16 v[26:29], v[2:5], v[212:215], v[62:65]
	v_mfma_f32_16x16x32_f16 v[62:65], v[2:5], v[216:219], v[78:81]
	v_mfma_f32_16x16x32_f16 v[78:81], v[2:5], v[220:223], v[86:89]
	v_mfma_f32_16x16x32_f16 v[86:89], v[2:5], v[224:227], v[94:97]
	v_mfma_f32_16x16x32_f16 v[94:97], v[2:5], v[228:231], v[102:105]
	v_mfma_f32_16x16x32_f16 v[102:105], v[2:5], v[232:235], v[106:109]
	v_mfma_f32_16x16x32_f16 v[106:109], v[2:5], v[236:239], v[124:127]
	v_mfma_f32_16x16x32_f16 v[0:3], v[2:5], v[240:243], v[10:13]
	s_nop 2
	global_load_dwordx4 v[10:13], v[66:67], off offset:2048
	global_load_dwordx4 v[122:125], v[66:67], off offset:3072
	global_load_dwordx4 v[126:129], v[118:119], off
	ds_read_b128 v[200:203], v134
	ds_read_b128 v[212:215], v134 offset:8192
	ds_read_b128 v[216:219], v134 offset:16384
	ds_read_b128 v[220:223], v134 offset:24576
	ds_read_b128 v[224:227], v134 offset:32768
	ds_read_b128 v[228:231], v134 offset:40960
	ds_read_b128 v[232:235], v134 offset:49152
	ds_read_b128 v[236:239], v134 offset:57344
	s_waitcnt lgkmcnt(7)
	v_mfma_f32_16x16x32_f16 v[74:77], v[30:33], v[200:203], v[74:77]
	s_waitcnt lgkmcnt(6)
	v_mfma_f32_16x16x32_f16 v[152:155], v[30:33], v[212:215], v[152:155]
	s_waitcnt lgkmcnt(5)
	v_mfma_f32_16x16x32_f16 v[156:159], v[30:33], v[216:219], v[156:159]
	s_waitcnt lgkmcnt(4)
	v_mfma_f32_16x16x32_f16 v[160:163], v[30:33], v[220:223], v[160:163]
	s_waitcnt lgkmcnt(3)
	v_mfma_f32_16x16x32_f16 v[164:167], v[30:33], v[224:227], v[164:167]
	s_waitcnt lgkmcnt(2)
	v_mfma_f32_16x16x32_f16 v[168:171], v[30:33], v[228:231], v[168:171]
	s_waitcnt lgkmcnt(1)
	v_mfma_f32_16x16x32_f16 v[172:175], v[30:33], v[232:235], v[172:175]
	s_waitcnt lgkmcnt(0)
	v_mfma_f32_16x16x32_f16 v[22:25], v[30:33], v[236:239], v[22:25]
	v_mfma_f32_16x16x32_f16 v[30:33], v[14:17], v[200:203], v[38:41]
	v_mfma_f32_16x16x32_f16 v[38:41], v[14:17], v[212:215], v[176:179]
	v_mfma_f32_16x16x32_f16 v[176:179], v[14:17], v[216:219], v[180:183]
	v_mfma_f32_16x16x32_f16 v[180:183], v[14:17], v[220:223], v[184:187]
	v_mfma_f32_16x16x32_f16 v[184:187], v[14:17], v[224:227], v[188:191]
	v_mfma_f32_16x16x32_f16 v[188:191], v[14:17], v[228:231], v[192:195]
	v_mfma_f32_16x16x32_f16 v[192:195], v[14:17], v[232:235], v[196:199]
	v_mfma_f32_16x16x32_f16 v[4:7], v[14:17], v[236:239], v[6:9]
	v_mfma_f32_16x16x32_f16 v[14:17], v[18:21], v[200:203], v[26:29]
	v_mfma_f32_16x16x32_f16 v[26:29], v[18:21], v[212:215], v[62:65]
	v_mfma_f32_16x16x32_f16 v[62:65], v[18:21], v[216:219], v[78:81]
	v_mfma_f32_16x16x32_f16 v[78:81], v[18:21], v[220:223], v[86:89]
	v_mfma_f32_16x16x32_f16 v[86:89], v[18:21], v[224:227], v[94:97]
	v_mfma_f32_16x16x32_f16 v[94:97], v[18:21], v[228:231], v[102:105]
	v_mfma_f32_16x16x32_f16 v[102:105], v[18:21], v[232:235], v[106:109]
	v_mfma_f32_16x16x32_f16 v[0:3], v[18:21], v[236:239], v[0:3]
	global_load_dwordx4 v[18:21], v[118:119], off offset:1024
	s_nop 0
	global_load_dwordx4 v[106:109], v[118:119], off offset:2048
	global_load_dwordx4 v[196:199], v[118:119], off offset:3072
	ds_read_b128 v[200:203], v136
	ds_read_b128 v[212:215], v136 offset:8192
	ds_read_b128 v[216:219], v136 offset:16384
	ds_read_b128 v[220:223], v136 offset:24576
	ds_read_b128 v[224:227], v136 offset:32768
	ds_read_b128 v[228:231], v136 offset:40960
	ds_read_b128 v[232:235], v136 offset:49152
	ds_read_b128 v[236:239], v136 offset:57344
	s_waitcnt lgkmcnt(7)
	v_mfma_f32_16x16x32_f16 v[74:77], v[46:49], v[200:203], v[74:77]
	s_waitcnt lgkmcnt(6)
	v_mfma_f32_16x16x32_f16 v[152:155], v[46:49], v[212:215], v[152:155]
	s_waitcnt lgkmcnt(5)
	v_mfma_f32_16x16x32_f16 v[156:159], v[46:49], v[216:219], v[156:159]
	s_waitcnt lgkmcnt(4)
	v_mfma_f32_16x16x32_f16 v[160:163], v[46:49], v[220:223], v[160:163]
	s_waitcnt lgkmcnt(3)
	v_mfma_f32_16x16x32_f16 v[164:167], v[46:49], v[224:227], v[164:167]
	s_waitcnt lgkmcnt(2)
	v_mfma_f32_16x16x32_f16 v[168:171], v[46:49], v[228:231], v[168:171]
	s_waitcnt lgkmcnt(1)
	v_mfma_f32_16x16x32_f16 v[172:175], v[46:49], v[232:235], v[172:175]
	s_waitcnt lgkmcnt(0)
	v_mfma_f32_16x16x32_f16 v[22:25], v[46:49], v[236:239], v[22:25]
	v_mfma_f32_16x16x32_f16 v[30:33], v[42:45], v[200:203], v[30:33]
	v_mfma_f32_16x16x32_f16 v[38:41], v[42:45], v[212:215], v[38:41]
	v_mfma_f32_16x16x32_f16 v[46:49], v[42:45], v[216:219], v[176:179]
	v_mfma_f32_16x16x32_f16 v[176:179], v[42:45], v[220:223], v[180:183]
	v_mfma_f32_16x16x32_f16 v[180:183], v[42:45], v[224:227], v[184:187]
	v_mfma_f32_16x16x32_f16 v[184:187], v[42:45], v[228:231], v[188:191]
	v_mfma_f32_16x16x32_f16 v[188:191], v[42:45], v[232:235], v[192:195]
	v_mfma_f32_16x16x32_f16 v[4:7], v[42:45], v[236:239], v[4:7]
	v_mfma_f32_16x16x32_f16 v[14:17], v[34:37], v[200:203], v[14:17]
	v_mfma_f32_16x16x32_f16 v[26:29], v[34:37], v[212:215], v[26:29]
	v_mfma_f32_16x16x32_f16 v[42:45], v[34:37], v[216:219], v[62:65]
	v_mfma_f32_16x16x32_f16 v[62:65], v[34:37], v[220:223], v[78:81]
	v_mfma_f32_16x16x32_f16 v[78:81], v[34:37], v[224:227], v[86:89]
	v_mfma_f32_16x16x32_f16 v[86:89], v[34:37], v[228:231], v[94:97]
	v_mfma_f32_16x16x32_f16 v[94:97], v[34:37], v[232:235], v[102:105]
	v_mfma_f32_16x16x32_f16 v[0:3], v[34:37], v[236:239], v[0:3]
	ds_read_b128 v[34:37], v137
	s_nop 0
	ds_read_b128 v[102:105], v137 offset:8192
	ds_read_b128 v[192:195], v137 offset:16384
	ds_read_b128 v[200:203], v137 offset:24576
	ds_read_b128 v[212:215], v137 offset:32768
	ds_read_b128 v[216:219], v137 offset:40960
	ds_read_b128 v[220:223], v137 offset:49152
	ds_read_b128 v[134:137], v137 offset:57344
	s_waitcnt vmcnt(17) lgkmcnt(7)
	v_mfma_f32_16x16x32_f16 v[74:77], v[50:53], v[34:37], v[74:77]
	s_waitcnt lgkmcnt(6)
	v_mfma_f32_16x16x32_f16 v[152:155], v[50:53], v[102:105], v[152:155]
	s_waitcnt lgkmcnt(5)
	v_mfma_f32_16x16x32_f16 v[156:159], v[50:53], v[192:195], v[156:159]
	s_waitcnt lgkmcnt(4)
	v_mfma_f32_16x16x32_f16 v[160:163], v[50:53], v[200:203], v[160:163]
	s_waitcnt lgkmcnt(3)
	v_mfma_f32_16x16x32_f16 v[164:167], v[50:53], v[212:215], v[164:167]
	s_waitcnt lgkmcnt(2)
	v_mfma_f32_16x16x32_f16 v[168:171], v[50:53], v[216:219], v[168:171]
	s_waitcnt lgkmcnt(1)
	v_mfma_f32_16x16x32_f16 v[172:175], v[50:53], v[220:223], v[172:175]
	s_waitcnt lgkmcnt(0)
	v_mfma_f32_16x16x32_f16 v[22:25], v[50:53], v[134:137], v[22:25]
	s_waitcnt vmcnt(16)
	v_mfma_f32_16x16x32_f16 v[30:33], v[54:57], v[34:37], v[30:33]
	v_mfma_f32_16x16x32_f16 v[38:41], v[54:57], v[102:105], v[38:41]
	v_mfma_f32_16x16x32_f16 v[46:49], v[54:57], v[192:195], v[46:49]
	v_mfma_f32_16x16x32_f16 v[50:53], v[54:57], v[200:203], v[176:179]
	v_mfma_f32_16x16x32_f16 v[176:179], v[54:57], v[212:215], v[180:183]
	v_mfma_f32_16x16x32_f16 v[180:183], v[54:57], v[216:219], v[184:187]
	v_mfma_f32_16x16x32_f16 v[184:187], v[54:57], v[220:223], v[188:191]
	v_mfma_f32_16x16x32_f16 v[4:7], v[54:57], v[134:137], v[4:7]
	s_waitcnt vmcnt(15)
	v_mfma_f32_16x16x32_f16 v[14:17], v[58:61], v[34:37], v[14:17]
	v_mfma_f32_16x16x32_f16 v[26:29], v[58:61], v[102:105], v[26:29]
	v_mfma_f32_16x16x32_f16 v[34:37], v[58:61], v[192:195], v[42:45]
	v_mfma_f32_16x16x32_f16 v[42:45], v[58:61], v[200:203], v[62:65]
	v_mfma_f32_16x16x32_f16 v[54:57], v[58:61], v[212:215], v[78:81]
	v_mfma_f32_16x16x32_f16 v[62:65], v[58:61], v[216:219], v[86:89]
	v_mfma_f32_16x16x32_f16 v[78:81], v[58:61], v[220:223], v[94:97]
	v_mfma_f32_16x16x32_f16 v[0:3], v[58:61], v[134:137], v[0:3]
	ds_read_b128 v[58:61], v138
	ds_read_b128 v[86:89], v138 offset:8192
	ds_read_b128 v[94:97], v138 offset:16384
	ds_read_b128 v[102:105], v138 offset:24576
	ds_read_b128 v[134:137], v138 offset:32768
	ds_read_b128 v[188:191], v138 offset:40960
	ds_read_b128 v[192:195], v138 offset:49152
	ds_read_b128 v[200:203], v138 offset:57344
	s_waitcnt vmcnt(7) lgkmcnt(7)
	v_mfma_f32_16x16x32_f16 v[74:77], v[204:207], v[58:61], v[74:77]
	s_waitcnt lgkmcnt(6)
	v_mfma_f32_16x16x32_f16 v[152:155], v[204:207], v[86:89], v[152:155]
	s_waitcnt lgkmcnt(5)
	v_mfma_f32_16x16x32_f16 v[156:159], v[204:207], v[94:97], v[156:159]
	s_waitcnt lgkmcnt(4)
	v_mfma_f32_16x16x32_f16 v[160:163], v[204:207], v[102:105], v[160:163]
	s_waitcnt lgkmcnt(3)
	v_mfma_f32_16x16x32_f16 v[164:167], v[204:207], v[134:137], v[164:167]
	s_waitcnt lgkmcnt(2)
	v_mfma_f32_16x16x32_f16 v[168:171], v[204:207], v[188:191], v[168:171]
	s_waitcnt lgkmcnt(1)
	v_mfma_f32_16x16x32_f16 v[172:175], v[204:207], v[192:195], v[172:175]
	s_waitcnt lgkmcnt(0)
	v_mfma_f32_16x16x32_f16 v[22:25], v[204:207], v[200:203], v[22:25]
	v_mfma_f32_16x16x32_f16 v[30:33], v[148:151], v[58:61], v[30:33]
	v_mfma_f32_16x16x32_f16 v[38:41], v[148:151], v[86:89], v[38:41]
	v_mfma_f32_16x16x32_f16 v[46:49], v[148:151], v[94:97], v[46:49]
	v_mfma_f32_16x16x32_f16 v[50:53], v[148:151], v[102:105], v[50:53]
	v_mfma_f32_16x16x32_f16 v[176:179], v[148:151], v[134:137], v[176:179]
	v_mfma_f32_16x16x32_f16 v[180:183], v[148:151], v[188:191], v[180:183]
	v_mfma_f32_16x16x32_f16 v[184:187], v[148:151], v[192:195], v[184:187]
	v_mfma_f32_16x16x32_f16 v[4:7], v[148:151], v[200:203], v[4:7]
	s_waitcnt vmcnt(6)
	v_mfma_f32_16x16x32_f16 v[14:17], v[208:211], v[58:61], v[14:17]
	v_mfma_f32_16x16x32_f16 v[26:29], v[208:211], v[86:89], v[26:29]
	v_mfma_f32_16x16x32_f16 v[34:37], v[208:211], v[94:97], v[34:37]
	v_mfma_f32_16x16x32_f16 v[42:45], v[208:211], v[102:105], v[42:45]
	v_mfma_f32_16x16x32_f16 v[54:57], v[208:211], v[134:137], v[54:57]
	v_mfma_f32_16x16x32_f16 v[58:61], v[208:211], v[188:191], v[62:65]
	v_mfma_f32_16x16x32_f16 v[62:65], v[208:211], v[192:195], v[78:81]
	v_mfma_f32_16x16x32_f16 v[0:3], v[208:211], v[200:203], v[0:3]
	s_nop 1
	ds_read_b128 v[78:81], v139
	ds_read_b128 v[86:89], v139 offset:8192
	ds_read_b128 v[94:97], v139 offset:16384
	ds_read_b128 v[102:105], v139 offset:24576
	ds_read_b128 v[134:137], v139 offset:32768
	ds_read_b128 v[148:151], v139 offset:40960
	ds_read_b128 v[188:191], v139 offset:49152
	ds_read_b128 v[192:195], v139 offset:57344
	s_waitcnt vmcnt(5) lgkmcnt(7)
	v_mfma_f32_16x16x32_f16 v[74:77], v[10:13], v[78:81], v[74:77]
	s_waitcnt lgkmcnt(6)
	v_mfma_f32_16x16x32_f16 v[152:155], v[10:13], v[86:89], v[152:155]
	s_waitcnt lgkmcnt(5)
	v_mfma_f32_16x16x32_f16 v[156:159], v[10:13], v[94:97], v[156:159]
	s_waitcnt lgkmcnt(4)
	v_mfma_f32_16x16x32_f16 v[160:163], v[10:13], v[102:105], v[160:163]
	s_waitcnt lgkmcnt(3)
	v_mfma_f32_16x16x32_f16 v[164:167], v[10:13], v[134:137], v[164:167]
	s_waitcnt lgkmcnt(2)
	v_mfma_f32_16x16x32_f16 v[168:171], v[10:13], v[148:151], v[168:171]
	s_waitcnt lgkmcnt(1)
	v_mfma_f32_16x16x32_f16 v[172:175], v[10:13], v[188:191], v[172:175]
	s_waitcnt lgkmcnt(0)
	v_mfma_f32_16x16x32_f16 v[8:11], v[10:13], v[192:195], v[22:25]
	s_waitcnt vmcnt(4)
	v_mfma_f32_16x16x32_f16 v[22:25], v[122:125], v[78:81], v[30:33]
	v_mfma_f32_16x16x32_f16 v[30:33], v[122:125], v[86:89], v[38:41]
	v_mfma_f32_16x16x32_f16 v[200:203], v[122:125], v[94:97], v[46:49]
	v_mfma_f32_16x16x32_f16 v[48:51], v[122:125], v[102:105], v[50:53]
	v_mfma_f32_16x16x32_f16 v[176:179], v[122:125], v[134:137], v[176:179]
	v_mfma_f32_16x16x32_f16 v[180:183], v[122:125], v[148:151], v[180:183]
	v_mfma_f32_16x16x32_f16 v[184:187], v[122:125], v[188:191], v[184:187]
	v_mfma_f32_16x16x32_f16 v[4:7], v[122:125], v[192:195], v[4:7]
	s_waitcnt vmcnt(3)
	v_mfma_f32_16x16x32_f16 v[12:15], v[126:129], v[78:81], v[14:17]
	v_mfma_f32_16x16x32_f16 v[78:81], v[126:129], v[86:89], v[26:29]
	v_mfma_f32_16x16x32_f16 v[86:89], v[126:129], v[94:97], v[34:37]
	v_mfma_f32_16x16x32_f16 v[40:43], v[126:129], v[102:105], v[42:45]
	v_mfma_f32_16x16x32_f16 v[94:97], v[126:129], v[134:137], v[54:57]
	v_mfma_f32_16x16x32_f16 v[102:105], v[126:129], v[148:151], v[58:61]
	v_mfma_f32_16x16x32_f16 v[64:67], v[126:129], v[188:191], v[62:65]
	v_mfma_f32_16x16x32_f16 v[0:3], v[126:129], v[192:195], v[0:3]
	s_nop 1
	ds_read_b128 v[60:63], v141
	ds_read_b128 v[122:125], v141 offset:8192
	ds_read_b128 v[126:129], v141 offset:16384
	ds_read_b128 v[134:137], v141 offset:24576
	ds_read_b128 v[148:151], v141 offset:32768
	ds_read_b128 v[188:191], v141 offset:40960
	ds_read_b128 v[192:195], v141 offset:49152
	ds_read_b128 v[138:141], v141 offset:57344
	s_waitcnt vmcnt(2) lgkmcnt(7)
	v_mfma_f32_16x16x32_f16 v[74:77], v[18:21], v[60:63], v[74:77]
	s_waitcnt lgkmcnt(6)
	v_mfma_f32_16x16x32_f16 v[152:155], v[18:21], v[122:125], v[152:155]
	s_waitcnt lgkmcnt(5)
	v_mfma_f32_16x16x32_f16 v[156:159], v[18:21], v[126:129], v[156:159]
	s_waitcnt lgkmcnt(4)
	v_mfma_f32_16x16x32_f16 v[160:163], v[18:21], v[134:137], v[160:163]
	s_waitcnt lgkmcnt(3)
	v_mfma_f32_16x16x32_f16 v[56:59], v[18:21], v[148:151], v[164:167]
	s_waitcnt lgkmcnt(2)
	v_mfma_f32_16x16x32_f16 v[52:55], v[18:21], v[188:191], v[168:171]
	s_waitcnt lgkmcnt(1)
	v_mfma_f32_16x16x32_f16 v[44:47], v[18:21], v[192:195], v[172:175]
	s_waitcnt lgkmcnt(0)
	v_mfma_f32_16x16x32_f16 v[36:39], v[18:21], v[138:141], v[8:11]
	s_waitcnt vmcnt(1)
	v_mfma_f32_16x16x32_f16 v[164:167], v[106:109], v[60:63], v[22:25]
	v_mfma_f32_16x16x32_f16 v[168:171], v[106:109], v[122:125], v[30:33]
	v_mfma_f32_16x16x32_f16 v[172:175], v[106:109], v[126:129], v[200:203]
	v_mfma_f32_16x16x32_f16 v[200:203], v[106:109], v[134:137], v[48:51]
	v_mfma_f32_16x16x32_f16 v[32:35], v[106:109], v[148:151], v[176:179]
	v_mfma_f32_16x16x32_f16 v[24:27], v[106:109], v[188:191], v[180:183]
	v_mfma_f32_16x16x32_f16 v[20:23], v[106:109], v[192:195], v[184:187]
	v_mfma_f32_16x16x32_f16 v[16:19], v[106:109], v[138:141], v[4:7]
	s_waitcnt vmcnt(0)
	v_mfma_f32_16x16x32_f16 v[106:109], v[196:199], v[60:63], v[12:15]
	v_mfma_f32_16x16x32_f16 v[78:81], v[196:199], v[122:125], v[78:81]
	v_mfma_f32_16x16x32_f16 v[86:89], v[196:199], v[126:129], v[86:89]
	v_mfma_f32_16x16x32_f16 v[60:63], v[196:199], v[134:137], v[40:43]
	v_mfma_f32_16x16x32_f16 v[12:15], v[196:199], v[148:151], v[94:97]
	v_mfma_f32_16x16x32_f16 v[8:11], v[196:199], v[188:191], v[102:105]
	v_mfma_f32_16x16x32_f16 v[4:7], v[196:199], v[192:195], v[64:67]
	v_mfma_f32_16x16x32_f16 v[0:3], v[196:199], v[138:141], v[0:3]
	global_load_dwordx4 v[48:51], v[120:121], off offset:1536
	global_load_dwordx4 v[40:43], v[120:121], off offset:1600
	global_load_dwordx4 v[28:31], v[120:121], off offset:1664
	v_mov_b32_e32 v94, v157
	v_mov_b32_e32 v95, v158
	v_mov_b32_e32 v96, v161
	v_mov_b32_e32 v97, v162
	v_mov_b32_e32 v64, v153
	v_mov_b32_e32 v65, v154
	v_mov_b32_e32 v102, v169
	v_mov_b32_e32 v103, v170
	v_mov_b32_e32 v104, v173
	v_mov_b32_e32 v105, v174
	v_mov_b32_e32 v118, v201
	v_mov_b32_e32 v119, v202
	s_barrier
	s_waitcnt vmcnt(2)
	v_pk_add_f32 v[74:75], v[74:75], v[48:49]
	v_add_f32_e32 v82, v152, v48
	v_pk_mov_b32 v[120:121], v[48:49], v[50:51] op_sel:[1,0]
	v_add_f32_e32 v49, v155, v51
	s_waitcnt vmcnt(1)
	v_pk_add_f32 v[122:123], v[164:165], v[40:41]
	v_add_f32_e32 v98, v168, v40
	v_pk_mov_b32 v[66:67], v[40:41], v[42:43] op_sel:[1,0]
	v_add_f32_e32 v41, v171, v43
	v_pk_add_f32 v[76:77], v[76:77], v[50:51]
	v_add_f32_e32 v50, v156, v48
	v_add_f32_e32 v85, v159, v51
	v_add_f32_e32 v90, v160, v48
	v_add_f32_e32 v93, v163, v51
	v_pk_add_f32 v[124:125], v[166:167], v[42:43]
	v_add_f32_e32 v42, v172, v40
	v_add_f32_e32 v101, v175, v43
	v_add_f32_e32 v126, v200, v40
	v_add_f32_e32 v127, v203, v43
	v_cvt_f16_f32_e32 v82, v82
	v_cvt_f16_f32_e32 v49, v49
	v_cvt_f16_f32_e32 v98, v98
	v_cvt_f16_f32_e32 v41, v41
	v_cvt_pk_f16_f32 v74, v74, v75
	v_cvt_pk_f16_f32 v75, v76, v77
	v_cvt_f16_f32_e32 v50, v50
	v_pk_add_f32 v[76:77], v[94:95], v[120:121]
	v_cvt_f16_f32_e32 v85, v85
	v_cvt_f16_f32_e32 v90, v90
	v_pk_add_f32 v[94:95], v[96:97], v[120:121]
	v_cvt_f16_f32_e32 v93, v93
	v_cvt_pk_f16_f32 v96, v122, v123
	v_cvt_f16_f32_e32 v42, v42
	v_cvt_f16_f32_e32 v101, v101
	v_cvt_f16_f32_e32 v122, v126
	v_cvt_f16_f32_e32 v123, v127
	v_pk_add_f32 v[64:65], v[64:65], v[120:121]
	v_pk_add_f32 v[102:103], v[102:103], v[66:67]
	v_pk_add_f32 v[104:105], v[104:105], v[66:67]
	v_pk_add_f32 v[118:119], v[118:119], v[66:67]
	v_cvt_pk_f16_f32 v65, v64, v65
	v_cvt_pk_f16_f32 v76, v76, v77
	v_cvt_pk_f16_f32 v77, v94, v95
	v_cvt_pk_f16_f32 v95, v102, v103
	s_waitcnt vmcnt(0)
	v_pk_add_f32 v[106:107], v[106:107], v[28:29]
	v_pk_add_f32 v[108:109], v[108:109], v[30:31]
	v_cvt_pk_f16_f32 v97, v124, v125
	v_cvt_pk_f16_f32 v102, v104, v105
	v_cvt_pk_f16_f32 v103, v118, v119
	v_pack_b32_f16 v64, v82, v65
	v_alignbit_b32 v65, v49, v65, 16
	v_pack_b32_f16 v94, v98, v95
	v_alignbit_b32 v95, v41, v95, 16
	v_add_f32_e32 v78, v78, v28
	v_cvt_pk_f16_f32 v106, v106, v107
	v_cvt_pk_f16_f32 v107, v108, v109
	ds_write2_b64 v130, v[74:75], v[96:97] offset1:4
	ds_write_b64 v130, v[106:107] offset:64
	v_pack_b32_f16 v74, v50, v76
	v_alignbit_b32 v75, v85, v76, 16
	v_pack_b32_f16 v76, v90, v77
	v_alignbit_b32 v77, v93, v77, 16
	v_pack_b32_f16 v96, v42, v102
	v_alignbit_b32 v97, v101, v102, 16
	v_pack_b32_f16 v102, v122, v103
	v_alignbit_b32 v103, v123, v103, 16
	ds_write2_b64 v132, v[64:65], v[94:95] offset0:32 offset1:36
	ds_write2_b64 v131, v[74:75], v[96:97] offset0:64 offset1:68
	ds_write2_b64 v91, v[76:77], v[102:103] offset0:96 offset1:100
	v_pk_mov_b32 v[64:65], v[28:29], v[30:31] op_sel:[1,0]
	v_add_f32_e32 v29, v81, v31
	v_cvt_f16_f32_e32 v78, v78
	v_cvt_f16_f32_e32 v29, v29
	v_mov_b32_e32 v74, v79
	v_mov_b32_e32 v75, v80
	v_pk_add_f32 v[74:75], v[74:75], v[64:65]
	v_add_f32_e32 v56, v56, v48
	v_cvt_pk_f16_f32 v30, v74, v75
	v_pack_b32_f16 v74, v78, v30
	v_alignbit_b32 v75, v29, v30, 16
	v_add_f32_e32 v29, v86, v28
	v_add_f32_e32 v30, v89, v31
	v_cvt_f16_f32_e32 v29, v29
	v_cvt_f16_f32_e32 v30, v30
	ds_write_b64 v130, v[74:75] offset:12608
	v_mov_b32_e32 v74, v87
	v_mov_b32_e32 v75, v88
	v_pk_add_f32 v[74:75], v[74:75], v[64:65]
	v_add_f32_e32 v52, v52, v48
	v_cvt_pk_f16_f32 v41, v74, v75
	v_pack_b32_f16 v74, v29, v41
	v_alignbit_b32 v75, v30, v41, 16
	v_add_f32_e32 v29, v60, v28
	v_add_f32_e32 v30, v63, v31
	v_cvt_f16_f32_e32 v29, v29
	v_cvt_f16_f32_e32 v30, v30
	v_mov_b32_e32 v60, v61
	v_mov_b32_e32 v61, v62
	v_pk_add_f32 v[60:61], v[60:61], v[64:65]
	ds_write_b64 v130, v[74:75] offset:25152
	v_cvt_pk_f16_f32 v41, v60, v61
	v_pack_b32_f16 v60, v29, v41
	v_alignbit_b32 v61, v30, v41, 16
	ds_write_b64 v130, v[60:61] offset:37696
	s_waitcnt lgkmcnt(0)
	s_barrier
	ds_read_b128 v[60:63], v83
	ds_read_b128 v[74:77], v84
	v_add_u32_e32 v29, 0x300, v111
	v_add_u32_e32 v30, v29, v112
	v_add_f32_e32 v44, v44, v48
	s_waitcnt lgkmcnt(1)
	buffer_store_dwordx4 v[60:63], v30, s[0:3], 0 offen sc1
	v_add_u32_e32 v30, 0x300, v113
	ds_read_b128 v[60:63], v92
	v_add_u32_e32 v41, v30, v114
	s_waitcnt lgkmcnt(1)
	buffer_store_dwordx4 v[74:77], v41, s[0:3], 0 offen sc1
	ds_read_b128 v[74:77], v99
	v_add_u32_e32 v41, 0x300, v115
	v_add_u32_e32 v42, v41, v116
	s_waitcnt lgkmcnt(1)
	buffer_store_dwordx4 v[60:63], v42, s[0:3], 0 offen sc1
	v_add_u32_e32 v42, 0x300, v117
	ds_read_b128 v[60:63], v100
	v_add_u32_e32 v49, v42, v142
	s_waitcnt lgkmcnt(1)
	buffer_store_dwordx4 v[74:77], v49, s[0:3], 0 offen sc1
	ds_read_b128 v[74:77], v110
	v_add_u32_e32 v49, 0x300, v144
	v_add_u32_e32 v50, v49, v143
	s_waitcnt lgkmcnt(1)
	buffer_store_dwordx4 v[60:63], v50, s[0:3], 0 offen sc1
	v_add_u32_e32 v50, 0x300, v145
	v_add_f32_e32 v36, v36, v48
	v_add_u32_e32 v60, v50, v146
	s_waitcnt lgkmcnt(0)
	buffer_store_dwordx4 v[74:77], v60, s[0:3], 0 offen sc1
	v_cvt_f16_f32_e32 v60, v56
	v_mov_b32_e32 v56, v57
	v_mov_b32_e32 v57, v58
	v_add_f32_e32 v58, v59, v51
	v_cvt_f16_f32_e32 v58, v58
	v_pk_add_f32 v[56:57], v[56:57], v[120:121]
	v_add_f32_e32 v32, v32, v40
	v_cvt_pk_f16_f32 v57, v56, v57
	v_pack_b32_f16 v56, v60, v57
	v_alignbit_b32 v57, v58, v57, 16
	v_cvt_f16_f32_e32 v58, v52
	v_mov_b32_e32 v52, v53
	v_mov_b32_e32 v53, v54
	v_add_f32_e32 v54, v55, v51
	v_cvt_f16_f32_e32 v54, v54
	v_pk_add_f32 v[52:53], v[52:53], v[120:121]
	v_add_f32_e32 v24, v24, v40
	v_cvt_pk_f16_f32 v53, v52, v53
	v_pack_b32_f16 v52, v58, v53
	v_alignbit_b32 v53, v54, v53, 16
	v_cvt_f16_f32_e32 v54, v44
	v_mov_b32_e32 v44, v45
	v_mov_b32_e32 v45, v46
	v_add_f32_e32 v46, v47, v51
	v_cvt_f16_f32_e32 v46, v46
	v_pk_add_f32 v[44:45], v[44:45], v[120:121]
	s_nop 0
	v_cvt_pk_f16_f32 v45, v44, v45
	v_pack_b32_f16 v44, v54, v45
	v_alignbit_b32 v45, v46, v45, 16
	v_cvt_f16_f32_e32 v46, v36
	v_mov_b32_e32 v36, v37
	v_mov_b32_e32 v37, v38
	v_add_f32_e32 v38, v39, v51
	v_cvt_f16_f32_e32 v38, v38
	v_pk_add_f32 v[36:37], v[36:37], v[120:121]
	s_barrier
	v_cvt_pk_f16_f32 v37, v36, v37
	v_pack_b32_f16 v36, v46, v37
	v_alignbit_b32 v37, v38, v37, 16
	v_cvt_f16_f32_e32 v38, v32
	v_mov_b32_e32 v32, v33
	v_mov_b32_e32 v33, v34
	v_add_f32_e32 v34, v35, v43
	v_cvt_f16_f32_e32 v34, v34
	v_pk_add_f32 v[32:33], v[32:33], v[66:67]
	s_nop 0
	v_cvt_pk_f16_f32 v33, v32, v33
	v_pack_b32_f16 v32, v38, v33
	v_alignbit_b32 v33, v34, v33, 16
	ds_write2_b64 v130, v[56:57], v[32:33] offset1:4
	v_cvt_f16_f32_e32 v32, v24
	v_mov_b32_e32 v24, v25
	v_mov_b32_e32 v25, v26
	v_add_f32_e32 v26, v27, v43
	v_cvt_f16_f32_e32 v26, v26
	v_pk_add_f32 v[24:25], v[24:25], v[66:67]
	v_add_f32_e32 v20, v20, v40
	v_cvt_pk_f16_f32 v25, v24, v25
	v_pack_b32_f16 v24, v32, v25
	v_alignbit_b32 v25, v26, v25, 16
	ds_write2_b64 v132, v[52:53], v[24:25] offset0:32 offset1:36
	v_cvt_f16_f32_e32 v24, v20
	v_mov_b32_e32 v20, v21
	v_mov_b32_e32 v21, v22
	v_add_f32_e32 v22, v23, v43
	v_cvt_f16_f32_e32 v22, v22
	v_pk_add_f32 v[20:21], v[20:21], v[66:67]
	v_add_f32_e32 v16, v16, v40
	v_cvt_pk_f16_f32 v21, v20, v21
	v_pack_b32_f16 v20, v24, v21
	v_alignbit_b32 v21, v22, v21, 16
	ds_write2_b64 v131, v[44:45], v[20:21] offset0:64 offset1:68
	v_cvt_f16_f32_e32 v20, v16
	v_mov_b32_e32 v16, v17
	v_mov_b32_e32 v17, v18
	v_add_f32_e32 v18, v19, v43
	v_cvt_f16_f32_e32 v18, v18
	v_pk_add_f32 v[16:17], v[16:17], v[66:67]
	v_add_f32_e32 v12, v12, v28
	v_cvt_pk_f16_f32 v17, v16, v17
	v_pack_b32_f16 v16, v20, v17
	v_alignbit_b32 v17, v18, v17, 16
	ds_write2_b64 v91, v[36:37], v[16:17] offset0:96 offset1:100
	v_cvt_f16_f32_e32 v16, v12
	v_mov_b32_e32 v12, v13
	v_mov_b32_e32 v13, v14
	v_add_f32_e32 v14, v15, v31
	v_cvt_f16_f32_e32 v14, v14
	v_pk_add_f32 v[12:13], v[12:13], v[64:65]
	v_add_f32_e32 v8, v8, v28
	v_cvt_pk_f16_f32 v13, v12, v13
	v_pack_b32_f16 v12, v16, v13
	v_alignbit_b32 v13, v14, v13, 16
	ds_write_b64 v130, v[12:13] offset:64
	v_cvt_f16_f32_e32 v12, v8
	v_mov_b32_e32 v8, v9
	v_mov_b32_e32 v9, v10
	v_add_f32_e32 v10, v11, v31
	v_cvt_f16_f32_e32 v10, v10
	v_pk_add_f32 v[8:9], v[8:9], v[64:65]
	v_add_f32_e32 v4, v4, v28
	v_cvt_pk_f16_f32 v9, v8, v9
	v_pack_b32_f16 v8, v12, v9
	v_alignbit_b32 v9, v10, v9, 16
	ds_write_b64 v130, v[8:9] offset:12608
	v_cvt_f16_f32_e32 v8, v4
	v_mov_b32_e32 v4, v5
	v_mov_b32_e32 v5, v6
	v_add_f32_e32 v6, v7, v31
	v_cvt_f16_f32_e32 v6, v6
	v_pk_add_f32 v[4:5], v[4:5], v[64:65]
	v_add_f32_e32 v0, v0, v28
	v_cvt_pk_f16_f32 v5, v4, v5
	v_pack_b32_f16 v4, v8, v5
	v_alignbit_b32 v5, v6, v5, 16
	ds_write_b64 v130, v[4:5] offset:25152
	v_cvt_f16_f32_e32 v4, v0
	v_mov_b32_e32 v0, v1
	v_mov_b32_e32 v1, v2
	v_add_f32_e32 v2, v3, v31
	v_cvt_f16_f32_e32 v2, v2
	v_pk_add_f32 v[0:1], v[0:1], v[64:65]
	v_add_u32_e32 v8, v29, v68
	v_cvt_pk_f16_f32 v1, v0, v1
	v_pack_b32_f16 v0, v4, v1
	v_alignbit_b32 v1, v2, v1, 16
	ds_write_b64 v130, v[0:1] offset:37696
	s_waitcnt lgkmcnt(0)
	s_barrier
	ds_read_b128 v[0:3], v83
	ds_read_b128 v[4:7], v84
	v_add_u32_e32 v12, v42, v70
	s_waitcnt lgkmcnt(1)
	buffer_store_dwordx4 v[0:3], v8, s[0:3], 0 offen sc1
	ds_read_b128 v[0:3], v92
	v_add_u32_e32 v8, v30, v69
	s_waitcnt lgkmcnt(1)
	buffer_store_dwordx4 v[4:7], v8, s[0:3], 0 offen sc1
	v_add_u32_e32 v8, v41, v72
	ds_read_b128 v[4:7], v99
	s_waitcnt lgkmcnt(1)
	buffer_store_dwordx4 v[0:3], v8, s[0:3], 0 offen sc1
	ds_read_b128 v[0:3], v100
	ds_read_b128 v[8:11], v110
	s_waitcnt lgkmcnt(2)
	buffer_store_dwordx4 v[4:7], v12, s[0:3], 0 offen sc1
	s_nop 1
	v_add_u32_e32 v4, v49, v71
	s_waitcnt lgkmcnt(1)
	buffer_store_dwordx4 v[0:3], v4, s[0:3], 0 offen sc1
	s_nop 1
	v_add_u32_e32 v0, v50, v73
	s_waitcnt lgkmcnt(0)
	buffer_store_dwordx4 v[8:11], v0, s[0:3], 0 offen sc1
	s_endpgm
	.p2alignl 8, 3212836864

	.amdhsa_kernel _Z7k_stageILi0ELi8EEv8AttnArgsPKDF16_PKfPDF16_iii
		.amdhsa_group_segment_fixed_size 115712
		.amdhsa_private_segment_fixed_size 0
		.amdhsa_kernarg_size 148
		.amdhsa_user_sgpr_count 2
		.amdhsa_user_sgpr_dispatch_ptr 0
		.amdhsa_user_sgpr_queue_ptr 0
		.amdhsa_user_sgpr_kernarg_segment_ptr 1
		.amdhsa_user_sgpr_dispatch_id 0
		.amdhsa_user_sgpr_kernarg_preload_length 0
		.amdhsa_user_sgpr_kernarg_preload_offset 0
		.amdhsa_user_sgpr_private_segment_size 0
		.amdhsa_uses_dynamic_stack 0
		.amdhsa_enable_private_segment 0
		.amdhsa_system_sgpr_workgroup_id_x 1
		.amdhsa_system_sgpr_workgroup_id_y 1
		.amdhsa_system_sgpr_workgroup_id_z 0
		.amdhsa_system_sgpr_workgroup_info 0
		.amdhsa_system_vgpr_workitem_id 0
		.amdhsa_next_free_vgpr 251
		.amdhsa_next_free_sgpr 96
		.amdhsa_accum_offset 252
		.amdhsa_reserve_vcc 1
		.amdhsa_float_round_mode_32 0
		.amdhsa_float_round_mode_16_64 0
		.amdhsa_float_denorm_mode_32 3
		.amdhsa_float_denorm_mode_16_64 3
		.amdhsa_dx10_clamp 1
		.amdhsa_ieee_mode 1
		.amdhsa_fp16_overflow 0
		.amdhsa_tg_split 0
		.amdhsa_exception_fp_ieee_invalid_op 0
		.amdhsa_exception_fp_denorm_src 0
		.amdhsa_exception_fp_ieee_div_zero 0
		.amdhsa_exception_fp_ieee_overflow 0
		.amdhsa_exception_fp_ieee_underflow 0
		.amdhsa_exception_fp_ieee_inexact 0
		.amdhsa_exception_int_div_zero 0
	.end_amdhsa_kernel

.LBB4_2:
	s_waitcnt vmcnt(19)
	v_pk_mul_f16 v161, v160, v162 op_sel_hi:[0,1]
	v_pk_mul_f16 v206, v160, v165 op_sel_hi:[0,1]
	v_pk_mul_f16 v210, v158, v165 op_sel_hi:[0,1]
	v_pk_mul_f16 v214, v159, v165 op_sel_hi:[0,1]
	v_pk_mul_f16 v200, v160, v163 op_sel_hi:[0,1]
	v_pk_mul_f16 v201, v160, v164 op_sel_hi:[0,1]
	v_pk_mul_f16 v207, v158, v162 op_sel_hi:[0,1]
	v_pk_mul_f16 v208, v158, v163 op_sel_hi:[0,1]
	v_pk_mul_f16 v209, v158, v164 op_sel_hi:[0,1]
	v_pk_mul_f16 v211, v159, v162 op_sel_hi:[0,1]
	v_pk_mul_f16 v212, v159, v163 op_sel_hi:[0,1]
	v_pk_mul_f16 v213, v159, v164 op_sel_hi:[0,1]
	v_pk_fma_f16 v117, v117, v165, v206
	v_pk_fma_f16 v114, v114, v162, v161
	v_pk_fma_f16 v133, v133, v165, v206
	v_pk_fma_f16 v130, v130, v162, v161
	v_pk_fma_f16 v141, v141, v165, v206
	v_pk_fma_f16 v138, v138, v162, v161
	v_pk_fma_f16 v161, v89, v165, v210
	v_pk_fma_f16 v215, v113, v165, v210
	v_pk_fma_f16 v210, v129, v165, v210
	v_pk_fma_f16 v219, v57, v165, v214
	v_pk_fma_f16 v223, v77, v165, v214
	v_pk_fma_f16 v165, v101, v165, v214
	v_pk_maximum3_f16 v214, v117, v133, v141
	v_pk_fma_f16 v116, v116, v164, v201
	v_pk_fma_f16 v115, v115, v163, v200
	v_pk_fma_f16 v132, v132, v164, v201
	v_pk_fma_f16 v131, v131, v163, v200
	v_pk_fma_f16 v140, v140, v164, v201
	v_pk_fma_f16 v139, v139, v163, v200
	v_pk_fma_f16 v200, v88, v164, v209
	v_pk_fma_f16 v201, v87, v163, v208
	v_pk_fma_f16 v206, v86, v162, v207
	v_pk_fma_f16 v216, v112, v164, v209
	v_pk_fma_f16 v217, v111, v163, v208
	v_pk_fma_f16 v218, v110, v162, v207
	v_pk_fma_f16 v209, v128, v164, v209
	v_pk_fma_f16 v208, v127, v163, v208
	v_pk_fma_f16 v207, v126, v162, v207
	v_pk_fma_f16 v220, v56, v164, v213
	v_pk_fma_f16 v221, v55, v163, v212
	v_pk_fma_f16 v222, v54, v162, v211
	v_pk_fma_f16 v224, v76, v164, v213
	v_pk_fma_f16 v225, v75, v163, v212
	v_pk_fma_f16 v226, v74, v162, v211
	v_pk_fma_f16 v164, v100, v164, v213
	v_pk_fma_f16 v163, v99, v163, v212
	v_pk_fma_f16 v162, v98, v162, v211
	v_pk_maximum3_f16 v211, v114, v130, v138
	v_pk_maximum3_f16 v212, v115, v131, v139
	v_pk_maximum3_f16 v213, v116, v132, v140
	v_pk_maximum3_f16 v230, v161, v215, v210
	v_pk_maximum3_f16 v234, v219, v223, v165
	v_pk_maximum3_f16 v227, v206, v218, v207
	v_pk_maximum3_f16 v228, v201, v217, v208
	v_pk_maximum3_f16 v229, v200, v216, v209
	s_nop 0
	v_pk_maximum3_f16 v231, v222, v226, v162
	v_pk_maximum3_f16 v232, v221, v225, v163
	v_pk_maximum3_f16 v214, v214, v230, v234
	v_pk_maximum3_f16 v233, v220, v224, v164
	s_nop 0
	v_pk_maximum3_f16 v211, v211, v227, v231
	v_pk_maximum3_f16 v212, v212, v228, v232
	v_pk_maximum3_f16 v213, v213, v229, v233
	v_xor_b32_e32 v214, 0x80008000, v214
	v_xor_b32_e32 v213, 0x80008000, v213
	v_xor_b32_e32 v212, 0x80008000, v212
	v_xor_b32_e32 v211, 0x80008000, v211
	v_pk_add_f16 v117, v117, v214
	v_pk_add_f16 v114, v114, v211
	v_pk_add_f16 v115, v115, v212
	v_pk_add_f16 v116, v116, v213
	v_pk_add_f16 v130, v130, v211
	v_exp_f16_sdwa v227, v114 dst_sel:WORD_0 dst_unused:UNUSED_PAD src0_sel:WORD_0
	v_exp_f16_sdwa v228, v115 dst_sel:WORD_0 dst_unused:UNUSED_PAD src0_sel:WORD_0
	v_exp_f16_sdwa v229, v116 dst_sel:WORD_0 dst_unused:UNUSED_PAD src0_sel:WORD_0
	v_exp_f16_sdwa v230, v117 dst_sel:WORD_0 dst_unused:UNUSED_PAD src0_sel:WORD_0
	v_exp_f16_sdwa v227, v114 dst_sel:WORD_1 dst_unused:UNUSED_PRESERVE src0_sel:WORD_1
	v_exp_f16_sdwa v228, v115 dst_sel:WORD_1 dst_unused:UNUSED_PRESERVE src0_sel:WORD_1
	v_exp_f16_sdwa v229, v116 dst_sel:WORD_1 dst_unused:UNUSED_PRESERVE src0_sel:WORD_1
	v_exp_f16_sdwa v230, v117 dst_sel:WORD_1 dst_unused:UNUSED_PRESERVE src0_sel:WORD_1
	s_nop 0
	v_pk_add_f16 v131, v131, v212
	v_pk_add_f16 v117, v227, 0
	v_pk_fma_f16 v73, v73, v230, 0
	v_pk_add_f16 v114, v230, 0
	v_pk_add_f16 v115, v229, 0
	v_pk_add_f16 v116, v228, 0
	v_pk_fma_f16 v72, v72, v229, 0
	v_pk_fma_f16 v71, v71, v228, 0
	v_pk_fma_f16 v70, v70, v227, 0
	v_pk_add_f16 v132, v132, v213
	v_pk_add_f16 v133, v133, v214
	s_nop 0
	v_exp_f16_sdwa v227, v130 dst_sel:WORD_0 dst_unused:UNUSED_PAD src0_sel:WORD_0
	v_exp_f16_sdwa v228, v131 dst_sel:WORD_0 dst_unused:UNUSED_PAD src0_sel:WORD_0
	v_exp_f16_sdwa v229, v132 dst_sel:WORD_0 dst_unused:UNUSED_PAD src0_sel:WORD_0
	v_exp_f16_sdwa v230, v133 dst_sel:WORD_0 dst_unused:UNUSED_PAD src0_sel:WORD_0
	v_exp_f16_sdwa v227, v130 dst_sel:WORD_1 dst_unused:UNUSED_PRESERVE src0_sel:WORD_1
	v_exp_f16_sdwa v228, v131 dst_sel:WORD_1 dst_unused:UNUSED_PRESERVE src0_sel:WORD_1
	v_exp_f16_sdwa v229, v132 dst_sel:WORD_1 dst_unused:UNUSED_PRESERVE src0_sel:WORD_1
	v_exp_f16_sdwa v230, v133 dst_sel:WORD_1 dst_unused:UNUSED_PRESERVE src0_sel:WORD_1
	s_nop 0
	s_nop 0
	v_pk_add_f16 v117, v117, v227
	v_pk_fma_f16 v73, v97, v230, v73
	v_pk_add_f16 v97, v141, v214
	v_pk_add_f16 v116, v116, v228
	v_pk_add_f16 v115, v115, v229
	v_pk_add_f16 v114, v114, v230
	v_pk_fma_f16 v70, v94, v227, v70
	v_pk_fma_f16 v71, v95, v228, v71
	v_pk_fma_f16 v72, v96, v229, v72
	v_pk_add_f16 v94, v138, v211
	v_pk_add_f16 v95, v139, v212
	v_pk_add_f16 v96, v140, v213
	s_nop 0
	v_exp_f16_sdwa v130, v94 dst_sel:WORD_0 dst_unused:UNUSED_PAD src0_sel:WORD_0
	v_exp_f16_sdwa v131, v95 dst_sel:WORD_0 dst_unused:UNUSED_PAD src0_sel:WORD_0
	v_exp_f16_sdwa v132, v96 dst_sel:WORD_0 dst_unused:UNUSED_PAD src0_sel:WORD_0
	v_exp_f16_sdwa v133, v97 dst_sel:WORD_0 dst_unused:UNUSED_PAD src0_sel:WORD_0
	v_exp_f16_sdwa v130, v94 dst_sel:WORD_1 dst_unused:UNUSED_PRESERVE src0_sel:WORD_1
	v_exp_f16_sdwa v131, v95 dst_sel:WORD_1 dst_unused:UNUSED_PRESERVE src0_sel:WORD_1
	v_exp_f16_sdwa v132, v96 dst_sel:WORD_1 dst_unused:UNUSED_PRESERVE src0_sel:WORD_1
	v_exp_f16_sdwa v133, v97 dst_sel:WORD_1 dst_unused:UNUSED_PRESERVE src0_sel:WORD_1
	s_nop 0
	s_nop 0
	v_pk_add_f16 v97, v117, v130
	v_pk_add_f16 v94, v114, v133
	v_pk_add_f16 v95, v115, v132
	v_pk_add_f16 v96, v116, v131
	v_pk_fma_f16 v73, v121, v133, v73
	v_pk_fma_f16 v72, v120, v132, v72
	v_pk_fma_f16 v71, v119, v131, v71
	v_pk_fma_f16 v70, v118, v130, v70
	v_pk_add_f16 v114, v206, v211
	v_pk_add_f16 v115, v201, v212
	v_pk_add_f16 v116, v200, v213
	v_pk_add_f16 v117, v161, v214
	s_nop 0
	v_exp_f16_sdwa v118, v114 dst_sel:WORD_0 dst_unused:UNUSED_PAD src0_sel:WORD_0
	v_exp_f16_sdwa v119, v115 dst_sel:WORD_0 dst_unused:UNUSED_PAD src0_sel:WORD_0
	v_exp_f16_sdwa v120, v116 dst_sel:WORD_0 dst_unused:UNUSED_PAD src0_sel:WORD_0
	v_exp_f16_sdwa v121, v117 dst_sel:WORD_0 dst_unused:UNUSED_PAD src0_sel:WORD_0
	v_exp_f16_sdwa v118, v114 dst_sel:WORD_1 dst_unused:UNUSED_PRESERVE src0_sel:WORD_1
	v_exp_f16_sdwa v119, v115 dst_sel:WORD_1 dst_unused:UNUSED_PRESERVE src0_sel:WORD_1
	v_exp_f16_sdwa v120, v116 dst_sel:WORD_1 dst_unused:UNUSED_PRESERVE src0_sel:WORD_1
	v_exp_f16_sdwa v121, v117 dst_sel:WORD_1 dst_unused:UNUSED_PRESERVE src0_sel:WORD_1
	s_nop 0
	v_pk_add_f16 v114, v218, v211
	v_pk_add_f16 v97, v97, v118
	v_pk_add_f16 v96, v96, v119
	v_pk_add_f16 v95, v95, v120
	v_pk_add_f16 v94, v94, v121
	v_pk_fma_f16 v70, v42, v118, v70
	v_pk_fma_f16 v71, v43, v119, v71
	v_pk_fma_f16 v72, v44, v120, v72
	v_pk_fma_f16 v73, v45, v121, v73
	v_pk_add_f16 v115, v217, v212
	v_pk_add_f16 v116, v216, v213
	v_pk_add_f16 v117, v215, v214
	s_nop 0
	v_exp_f16_sdwa v118, v114 dst_sel:WORD_0 dst_unused:UNUSED_PAD src0_sel:WORD_0
	v_exp_f16_sdwa v119, v115 dst_sel:WORD_0 dst_unused:UNUSED_PAD src0_sel:WORD_0
	v_exp_f16_sdwa v120, v116 dst_sel:WORD_0 dst_unused:UNUSED_PAD src0_sel:WORD_0
	v_exp_f16_sdwa v121, v117 dst_sel:WORD_0 dst_unused:UNUSED_PAD src0_sel:WORD_0
	v_exp_f16_sdwa v118, v114 dst_sel:WORD_1 dst_unused:UNUSED_PRESERVE src0_sel:WORD_1
	v_exp_f16_sdwa v119, v115 dst_sel:WORD_1 dst_unused:UNUSED_PRESERVE src0_sel:WORD_1
	v_exp_f16_sdwa v120, v116 dst_sel:WORD_1 dst_unused:UNUSED_PRESERVE src0_sel:WORD_1
	v_exp_f16_sdwa v121, v117 dst_sel:WORD_1 dst_unused:UNUSED_PRESERVE src0_sel:WORD_1
	s_nop 0
	v_pk_add_f16 v114, v207, v211
	v_pk_add_f16 v97, v97, v118
	v_pk_add_f16 v94, v94, v121
	v_pk_add_f16 v95, v95, v120
	v_pk_add_f16 v96, v96, v119
	v_pk_fma_f16 v73, v69, v121, v73
	v_pk_fma_f16 v72, v68, v120, v72
	v_pk_fma_f16 v71, v67, v119, v71
	v_pk_fma_f16 v70, v66, v118, v70
	v_pk_add_f16 v115, v208, v212
	v_pk_add_f16 v116, v209, v213
	v_pk_add_f16 v117, v210, v214
	s_nop 0
	v_exp_f16_sdwa v118, v114 dst_sel:WORD_0 dst_unused:UNUSED_PAD src0_sel:WORD_0
	v_exp_f16_sdwa v119, v115 dst_sel:WORD_0 dst_unused:UNUSED_PAD src0_sel:WORD_0
	v_exp_f16_sdwa v120, v116 dst_sel:WORD_0 dst_unused:UNUSED_PAD src0_sel:WORD_0
	v_exp_f16_sdwa v121, v117 dst_sel:WORD_0 dst_unused:UNUSED_PAD src0_sel:WORD_0
	v_exp_f16_sdwa v118, v114 dst_sel:WORD_1 dst_unused:UNUSED_PRESERVE src0_sel:WORD_1
	v_exp_f16_sdwa v119, v115 dst_sel:WORD_1 dst_unused:UNUSED_PRESERVE src0_sel:WORD_1
	v_exp_f16_sdwa v120, v116 dst_sel:WORD_1 dst_unused:UNUSED_PRESERVE src0_sel:WORD_1
	v_exp_f16_sdwa v121, v117 dst_sel:WORD_1 dst_unused:UNUSED_PRESERVE src0_sel:WORD_1
	s_nop 0
	v_pk_add_f16 v114, v222, v211
	v_pk_add_f16 v97, v97, v118
	v_pk_add_f16 v96, v96, v119
	v_pk_add_f16 v95, v95, v120
	v_pk_add_f16 v94, v94, v121
	v_pk_fma_f16 v70, v90, v118, v70
	v_pk_fma_f16 v71, v91, v119, v71
	v_pk_fma_f16 v72, v92, v120, v72
	v_pk_fma_f16 v73, v93, v121, v73
	v_pk_add_f16 v115, v221, v212
	v_pk_add_f16 v116, v220, v213
	v_pk_add_f16 v117, v219, v214
	s_nop 0
	v_exp_f16_sdwa v118, v114 dst_sel:WORD_0 dst_unused:UNUSED_PAD src0_sel:WORD_0
	v_exp_f16_sdwa v119, v115 dst_sel:WORD_0 dst_unused:UNUSED_PAD src0_sel:WORD_0
	v_exp_f16_sdwa v120, v116 dst_sel:WORD_0 dst_unused:UNUSED_PAD src0_sel:WORD_0
	v_exp_f16_sdwa v121, v117 dst_sel:WORD_0 dst_unused:UNUSED_PAD src0_sel:WORD_0
	v_exp_f16_sdwa v118, v114 dst_sel:WORD_1 dst_unused:UNUSED_PRESERVE src0_sel:WORD_1
	v_exp_f16_sdwa v119, v115 dst_sel:WORD_1 dst_unused:UNUSED_PRESERVE src0_sel:WORD_1
	v_exp_f16_sdwa v120, v116 dst_sel:WORD_1 dst_unused:UNUSED_PRESERVE src0_sel:WORD_1
	v_exp_f16_sdwa v121, v117 dst_sel:WORD_1 dst_unused:UNUSED_PRESERVE src0_sel:WORD_1
	s_nop 0
	v_pk_add_f16 v114, v226, v211
	v_pk_add_f16 v97, v97, v118
	v_pk_add_f16 v94, v94, v121
	v_pk_add_f16 v95, v95, v120
	v_pk_add_f16 v96, v96, v119
	v_pk_fma_f16 v73, v25, v121, v73
	v_pk_fma_f16 v72, v24, v120, v72
	v_pk_fma_f16 v71, v23, v119, v71
	v_pk_fma_f16 v70, v22, v118, v70
	v_pk_add_f16 v115, v225, v212
	v_pk_add_f16 v116, v224, v213
	v_pk_add_f16 v117, v223, v214
	s_nop 0
	v_exp_f16_sdwa v118, v114 dst_sel:WORD_0 dst_unused:UNUSED_PAD src0_sel:WORD_0
	v_exp_f16_sdwa v119, v115 dst_sel:WORD_0 dst_unused:UNUSED_PAD src0_sel:WORD_0
	v_exp_f16_sdwa v120, v116 dst_sel:WORD_0 dst_unused:UNUSED_PAD src0_sel:WORD_0
	v_exp_f16_sdwa v121, v117 dst_sel:WORD_0 dst_unused:UNUSED_PAD src0_sel:WORD_0
	v_exp_f16_sdwa v118, v114 dst_sel:WORD_1 dst_unused:UNUSED_PRESERVE src0_sel:WORD_1
	v_exp_f16_sdwa v119, v115 dst_sel:WORD_1 dst_unused:UNUSED_PRESERVE src0_sel:WORD_1
	v_exp_f16_sdwa v120, v116 dst_sel:WORD_1 dst_unused:UNUSED_PRESERVE src0_sel:WORD_1
	v_exp_f16_sdwa v121, v117 dst_sel:WORD_1 dst_unused:UNUSED_PRESERVE src0_sel:WORD_1
	s_nop 0
	v_pk_add_f16 v114, v162, v211
	v_pk_add_f16 v97, v97, v118
	v_pk_add_f16 v96, v96, v119
	v_pk_add_f16 v95, v95, v120
	v_pk_add_f16 v94, v94, v121
	v_pk_fma_f16 v70, v34, v118, v70
	v_pk_fma_f16 v71, v35, v119, v71
	v_pk_fma_f16 v72, v36, v120, v72
	v_pk_fma_f16 v73, v37, v121, v73
	v_pk_add_f16 v115, v163, v212
	v_pk_add_f16 v116, v164, v213
	v_pk_add_f16 v117, v165, v214
	s_nop 0
	v_exp_f16_sdwa v118, v114 dst_sel:WORD_0 dst_unused:UNUSED_PAD src0_sel:WORD_0
	v_exp_f16_sdwa v119, v115 dst_sel:WORD_0 dst_unused:UNUSED_PAD src0_sel:WORD_0
	v_exp_f16_sdwa v120, v116 dst_sel:WORD_0 dst_unused:UNUSED_PAD src0_sel:WORD_0
	v_exp_f16_sdwa v121, v117 dst_sel:WORD_0 dst_unused:UNUSED_PAD src0_sel:WORD_0
	v_exp_f16_sdwa v118, v114 dst_sel:WORD_1 dst_unused:UNUSED_PRESERVE src0_sel:WORD_1
	v_exp_f16_sdwa v119, v115 dst_sel:WORD_1 dst_unused:UNUSED_PRESERVE src0_sel:WORD_1
	v_exp_f16_sdwa v120, v116 dst_sel:WORD_1 dst_unused:UNUSED_PRESERVE src0_sel:WORD_1
	v_exp_f16_sdwa v121, v117 dst_sel:WORD_1 dst_unused:UNUSED_PRESERVE src0_sel:WORD_1
	s_nop 0
	s_nop 0
	v_pk_add_f16 v97, v97, v118
	v_pk_add_f16 v96, v96, v119
	v_rcp_f16_e32 v114, v97
	v_rcp_f16_sdwa v97, v97 dst_sel:DWORD dst_unused:UNUSED_PAD src0_sel:WORD_1
	v_pk_add_f16 v95, v95, v120
	v_rcp_f16_e32 v115, v96
	v_rcp_f16_sdwa v96, v96 dst_sel:DWORD dst_unused:UNUSED_PAD src0_sel:WORD_1
	v_pk_add_f16 v94, v94, v121
	v_rcp_f16_e32 v116, v95
	v_rcp_f16_sdwa v95, v95 dst_sel:DWORD dst_unused:UNUSED_PAD src0_sel:WORD_1
	v_rcp_f16_e32 v117, v94
	v_rcp_f16_sdwa v94, v94 dst_sel:DWORD dst_unused:UNUSED_PAD src0_sel:WORD_1
	v_pk_fma_f16 v70, v50, v118, v70
	v_pack_b32_f16 v97, v114, v97
	v_pk_fma_f16 v71, v51, v119, v71
	v_pk_mul_f16 v141, v70, v97
	v_pack_b32_f16 v70, v115, v96
	v_pk_fma_f16 v72, v52, v120, v72
	v_pk_mul_f16 v140, v71, v70
	v_pack_b32_f16 v70, v116, v95
	v_pk_fma_f16 v73, v53, v121, v73
	v_pk_mul_f16 v139, v72, v70
	v_pack_b32_f16 v70, v117, v94
	v_pk_mul_f16 v138, v73, v70
	s_waitcnt vmcnt(13)
	v_pk_mul_f16 v70, v160, v154 op_sel_hi:[0,1]
	v_pk_mul_f16 v73, v160, v157 op_sel_hi:[0,1]
	v_pk_mul_f16 v97, v158, v157 op_sel_hi:[0,1]
	v_pk_mul_f16 v117, v159, v157 op_sel_hi:[0,1]
	v_pk_mul_f16 v71, v160, v155 op_sel_hi:[0,1]
	v_pk_mul_f16 v72, v160, v156 op_sel_hi:[0,1]
	v_pk_mul_f16 v94, v158, v154 op_sel_hi:[0,1]
	v_pk_mul_f16 v95, v158, v155 op_sel_hi:[0,1]
	v_pk_mul_f16 v96, v158, v156 op_sel_hi:[0,1]
	v_pk_mul_f16 v114, v159, v154 op_sel_hi:[0,1]
	v_pk_mul_f16 v115, v159, v155 op_sel_hi:[0,1]
	v_pk_mul_f16 v116, v159, v156 op_sel_hi:[0,1]
	v_pk_fma_f16 v89, v89, v157, v73
	v_pk_fma_f16 v86, v86, v154, v70
	v_pk_fma_f16 v113, v113, v157, v73
	v_pk_fma_f16 v110, v110, v154, v70
	v_pk_fma_f16 v73, v129, v157, v73
	v_pk_fma_f16 v70, v126, v154, v70
	v_pk_fma_f16 v118, v57, v157, v97
	v_pk_fma_f16 v126, v77, v157, v97
	v_pk_fma_f16 v97, v101, v157, v97
	v_pk_fma_f16 v130, v29, v157, v117
	v_pk_fma_f16 v161, v41, v157, v117
	v_pk_fma_f16 v117, v61, v157, v117
	v_pk_maximum3_f16 v157, v89, v113, v73
	v_pk_fma_f16 v88, v88, v156, v72
	v_pk_fma_f16 v87, v87, v155, v71
	v_pk_fma_f16 v112, v112, v156, v72
	v_pk_fma_f16 v111, v111, v155, v71
	v_pk_fma_f16 v72, v128, v156, v72
	v_pk_fma_f16 v71, v127, v155, v71
	v_pk_fma_f16 v119, v56, v156, v96
	v_pk_fma_f16 v120, v55, v155, v95
	v_pk_fma_f16 v121, v54, v154, v94
	v_pk_fma_f16 v127, v76, v156, v96
	v_pk_fma_f16 v128, v75, v155, v95
	v_pk_fma_f16 v129, v74, v154, v94
	v_pk_fma_f16 v96, v100, v156, v96
	v_pk_fma_f16 v95, v99, v155, v95
	v_pk_fma_f16 v94, v98, v154, v94
	v_pk_fma_f16 v131, v28, v156, v116
	v_pk_fma_f16 v132, v27, v155, v115
	v_pk_fma_f16 v133, v26, v154, v114
	v_pk_fma_f16 v162, v40, v156, v116
	v_pk_fma_f16 v163, v39, v155, v115
	v_pk_fma_f16 v164, v38, v154, v114
	v_pk_fma_f16 v116, v60, v156, v116
	v_pk_fma_f16 v115, v59, v155, v115
	v_pk_fma_f16 v114, v58, v154, v114
	v_pk_maximum3_f16 v154, v86, v110, v70
	v_pk_maximum3_f16 v155, v87, v111, v71
	v_pk_maximum3_f16 v156, v88, v112, v72
	v_pk_maximum3_f16 v206, v118, v126, v97
	v_pk_maximum3_f16 v210, v130, v161, v117
	v_pk_maximum3_f16 v165, v121, v129, v94
	v_pk_maximum3_f16 v200, v120, v128, v95
	v_pk_maximum3_f16 v201, v119, v127, v96
	s_nop 0
	v_pk_maximum3_f16 v207, v133, v164, v114
	v_pk_maximum3_f16 v208, v132, v163, v115
	v_pk_maximum3_f16 v157, v157, v206, v210
	v_pk_maximum3_f16 v209, v131, v162, v116
	s_nop 0
	v_pk_maximum3_f16 v154, v154, v165, v207
	v_pk_maximum3_f16 v155, v155, v200, v208
	v_pk_maximum3_f16 v156, v156, v201, v209
	v_xor_b32_e32 v157, 0x80008000, v157
	v_xor_b32_e32 v156, 0x80008000, v156
	v_xor_b32_e32 v155, 0x80008000, v155
	v_xor_b32_e32 v154, 0x80008000, v154
	v_pk_add_f16 v89, v89, v157
	v_pk_add_f16 v86, v86, v154
	v_pk_add_f16 v87, v87, v155
	v_pk_add_f16 v88, v88, v156
	v_pk_add_f16 v110, v110, v154
	v_exp_f16_sdwa v165, v86 dst_sel:WORD_0 dst_unused:UNUSED_PAD src0_sel:WORD_0
	v_exp_f16_sdwa v200, v87 dst_sel:WORD_0 dst_unused:UNUSED_PAD src0_sel:WORD_0
	v_exp_f16_sdwa v201, v88 dst_sel:WORD_0 dst_unused:UNUSED_PAD src0_sel:WORD_0
	v_exp_f16_sdwa v206, v89 dst_sel:WORD_0 dst_unused:UNUSED_PAD src0_sel:WORD_0
	v_exp_f16_sdwa v165, v86 dst_sel:WORD_1 dst_unused:UNUSED_PRESERVE src0_sel:WORD_1
	v_exp_f16_sdwa v200, v87 dst_sel:WORD_1 dst_unused:UNUSED_PRESERVE src0_sel:WORD_1
	v_exp_f16_sdwa v201, v88 dst_sel:WORD_1 dst_unused:UNUSED_PRESERVE src0_sel:WORD_1
	v_exp_f16_sdwa v206, v89 dst_sel:WORD_1 dst_unused:UNUSED_PRESERVE src0_sel:WORD_1
	s_nop 0
	v_pk_add_f16 v111, v111, v155
	v_pk_add_f16 v89, v165, 0
	v_pk_fma_f16 v45, v45, v206, 0
	v_pk_add_f16 v86, v206, 0
	v_pk_add_f16 v87, v201, 0
	v_pk_add_f16 v88, v200, 0
	v_pk_fma_f16 v44, v44, v201, 0
	v_pk_fma_f16 v43, v43, v200, 0
	v_pk_fma_f16 v42, v42, v165, 0
	v_pk_add_f16 v112, v112, v156
	v_pk_add_f16 v113, v113, v157
	s_nop 0
	v_exp_f16_sdwa v165, v110 dst_sel:WORD_0 dst_unused:UNUSED_PAD src0_sel:WORD_0
	v_exp_f16_sdwa v200, v111 dst_sel:WORD_0 dst_unused:UNUSED_PAD src0_sel:WORD_0
	v_exp_f16_sdwa v201, v112 dst_sel:WORD_0 dst_unused:UNUSED_PAD src0_sel:WORD_0
	v_exp_f16_sdwa v206, v113 dst_sel:WORD_0 dst_unused:UNUSED_PAD src0_sel:WORD_0
	v_exp_f16_sdwa v165, v110 dst_sel:WORD_1 dst_unused:UNUSED_PRESERVE src0_sel:WORD_1
	v_exp_f16_sdwa v200, v111 dst_sel:WORD_1 dst_unused:UNUSED_PRESERVE src0_sel:WORD_1
	v_exp_f16_sdwa v201, v112 dst_sel:WORD_1 dst_unused:UNUSED_PRESERVE src0_sel:WORD_1
	v_exp_f16_sdwa v206, v113 dst_sel:WORD_1 dst_unused:UNUSED_PRESERVE src0_sel:WORD_1
	s_nop 0
	s_nop 0
	v_pk_add_f16 v89, v89, v165
	v_pk_fma_f16 v45, v69, v206, v45
	v_pk_add_f16 v69, v73, v157
	v_pk_add_f16 v88, v88, v200
	v_pk_add_f16 v87, v87, v201
	v_pk_add_f16 v86, v86, v206
	v_pk_fma_f16 v42, v66, v165, v42
	v_pk_fma_f16 v43, v67, v200, v43
	v_pk_fma_f16 v44, v68, v201, v44
	v_pk_add_f16 v66, v70, v154
	v_pk_add_f16 v67, v71, v155
	v_pk_add_f16 v68, v72, v156
	s_nop 0
	v_exp_f16_sdwa v70, v66 dst_sel:WORD_0 dst_unused:UNUSED_PAD src0_sel:WORD_0
	v_exp_f16_sdwa v71, v67 dst_sel:WORD_0 dst_unused:UNUSED_PAD src0_sel:WORD_0
	v_exp_f16_sdwa v72, v68 dst_sel:WORD_0 dst_unused:UNUSED_PAD src0_sel:WORD_0
	v_exp_f16_sdwa v73, v69 dst_sel:WORD_0 dst_unused:UNUSED_PAD src0_sel:WORD_0
	v_exp_f16_sdwa v70, v66 dst_sel:WORD_1 dst_unused:UNUSED_PRESERVE src0_sel:WORD_1
	v_exp_f16_sdwa v71, v67 dst_sel:WORD_1 dst_unused:UNUSED_PRESERVE src0_sel:WORD_1
	v_exp_f16_sdwa v72, v68 dst_sel:WORD_1 dst_unused:UNUSED_PRESERVE src0_sel:WORD_1
	v_exp_f16_sdwa v73, v69 dst_sel:WORD_1 dst_unused:UNUSED_PRESERVE src0_sel:WORD_1
	s_nop 0
	s_nop 0
	v_pk_add_f16 v69, v89, v70
	v_pk_add_f16 v66, v86, v73
	v_pk_add_f16 v67, v87, v72
	v_pk_add_f16 v68, v88, v71
	v_pk_fma_f16 v45, v93, v73, v45
	v_pk_fma_f16 v44, v92, v72, v44
	v_pk_fma_f16 v43, v91, v71, v43
	v_pk_fma_f16 v42, v90, v70, v42
	v_pk_add_f16 v70, v121, v154
	v_pk_add_f16 v71, v120, v155
	v_pk_add_f16 v72, v119, v156
	v_pk_add_f16 v73, v118, v157
	s_nop 0
	v_exp_f16_sdwa v86, v70 dst_sel:WORD_0 dst_unused:UNUSED_PAD src0_sel:WORD_0
	v_exp_f16_sdwa v87, v71 dst_sel:WORD_0 dst_unused:UNUSED_PAD src0_sel:WORD_0
	v_exp_f16_sdwa v88, v72 dst_sel:WORD_0 dst_unused:UNUSED_PAD src0_sel:WORD_0
	v_exp_f16_sdwa v89, v73 dst_sel:WORD_0 dst_unused:UNUSED_PAD src0_sel:WORD_0
	v_exp_f16_sdwa v86, v70 dst_sel:WORD_1 dst_unused:UNUSED_PRESERVE src0_sel:WORD_1
	v_exp_f16_sdwa v87, v71 dst_sel:WORD_1 dst_unused:UNUSED_PRESERVE src0_sel:WORD_1
	v_exp_f16_sdwa v88, v72 dst_sel:WORD_1 dst_unused:UNUSED_PRESERVE src0_sel:WORD_1
	v_exp_f16_sdwa v89, v73 dst_sel:WORD_1 dst_unused:UNUSED_PRESERVE src0_sel:WORD_1
	s_nop 0
	v_pk_add_f16 v70, v129, v154
	v_pk_add_f16 v69, v69, v86
	v_pk_add_f16 v68, v68, v87
	v_pk_add_f16 v67, v67, v88
	v_pk_add_f16 v66, v66, v89
	v_pk_fma_f16 v42, v22, v86, v42
	v_pk_fma_f16 v43, v23, v87, v43
	v_pk_fma_f16 v44, v24, v88, v44
	v_pk_fma_f16 v45, v25, v89, v45
	v_pk_add_f16 v71, v128, v155
	v_pk_add_f16 v72, v127, v156
	v_pk_add_f16 v73, v126, v157
	s_nop 0
	v_exp_f16_sdwa v86, v70 dst_sel:WORD_0 dst_unused:UNUSED_PAD src0_sel:WORD_0
	v_exp_f16_sdwa v87, v71 dst_sel:WORD_0 dst_unused:UNUSED_PAD src0_sel:WORD_0
	v_exp_f16_sdwa v88, v72 dst_sel:WORD_0 dst_unused:UNUSED_PAD src0_sel:WORD_0
	v_exp_f16_sdwa v89, v73 dst_sel:WORD_0 dst_unused:UNUSED_PAD src0_sel:WORD_0
	v_exp_f16_sdwa v86, v70 dst_sel:WORD_1 dst_unused:UNUSED_PRESERVE src0_sel:WORD_1
	v_exp_f16_sdwa v87, v71 dst_sel:WORD_1 dst_unused:UNUSED_PRESERVE src0_sel:WORD_1
	v_exp_f16_sdwa v88, v72 dst_sel:WORD_1 dst_unused:UNUSED_PRESERVE src0_sel:WORD_1
	v_exp_f16_sdwa v89, v73 dst_sel:WORD_1 dst_unused:UNUSED_PRESERVE src0_sel:WORD_1
	s_nop 0
	v_pk_add_f16 v70, v94, v154
	v_pk_add_f16 v69, v69, v86
	v_pk_add_f16 v66, v66, v89
	v_pk_add_f16 v67, v67, v88
	v_pk_add_f16 v68, v68, v87
	v_pk_fma_f16 v45, v37, v89, v45
	v_pk_fma_f16 v44, v36, v88, v44
	v_pk_fma_f16 v43, v35, v87, v43
	v_pk_fma_f16 v42, v34, v86, v42
	v_pk_add_f16 v71, v95, v155
	v_pk_add_f16 v72, v96, v156
	v_pk_add_f16 v73, v97, v157
	s_nop 0
	v_exp_f16_sdwa v86, v70 dst_sel:WORD_0 dst_unused:UNUSED_PAD src0_sel:WORD_0
	v_exp_f16_sdwa v87, v71 dst_sel:WORD_0 dst_unused:UNUSED_PAD src0_sel:WORD_0
	v_exp_f16_sdwa v88, v72 dst_sel:WORD_0 dst_unused:UNUSED_PAD src0_sel:WORD_0
	v_exp_f16_sdwa v89, v73 dst_sel:WORD_0 dst_unused:UNUSED_PAD src0_sel:WORD_0
	v_exp_f16_sdwa v86, v70 dst_sel:WORD_1 dst_unused:UNUSED_PRESERVE src0_sel:WORD_1
	v_exp_f16_sdwa v87, v71 dst_sel:WORD_1 dst_unused:UNUSED_PRESERVE src0_sel:WORD_1
	v_exp_f16_sdwa v88, v72 dst_sel:WORD_1 dst_unused:UNUSED_PRESERVE src0_sel:WORD_1
	v_exp_f16_sdwa v89, v73 dst_sel:WORD_1 dst_unused:UNUSED_PRESERVE src0_sel:WORD_1
	s_nop 0
	v_pk_add_f16 v70, v133, v154
	v_pk_add_f16 v69, v69, v86
	v_pk_add_f16 v68, v68, v87
	v_pk_add_f16 v67, v67, v88
	v_pk_add_f16 v66, v66, v89
	v_pk_fma_f16 v42, v50, v86, v42
	v_pk_fma_f16 v43, v51, v87, v43
	v_pk_fma_f16 v44, v52, v88, v44
	v_pk_fma_f16 v45, v53, v89, v45
	v_pk_add_f16 v71, v132, v155
	v_pk_add_f16 v72, v131, v156
	v_pk_add_f16 v73, v130, v157
	s_nop 0
	v_exp_f16_sdwa v86, v70 dst_sel:WORD_0 dst_unused:UNUSED_PAD src0_sel:WORD_0
	v_exp_f16_sdwa v87, v71 dst_sel:WORD_0 dst_unused:UNUSED_PAD src0_sel:WORD_0
	v_exp_f16_sdwa v88, v72 dst_sel:WORD_0 dst_unused:UNUSED_PAD src0_sel:WORD_0
	v_exp_f16_sdwa v89, v73 dst_sel:WORD_0 dst_unused:UNUSED_PAD src0_sel:WORD_0
	v_exp_f16_sdwa v86, v70 dst_sel:WORD_1 dst_unused:UNUSED_PRESERVE src0_sel:WORD_1
	v_exp_f16_sdwa v87, v71 dst_sel:WORD_1 dst_unused:UNUSED_PRESERVE src0_sel:WORD_1
	v_exp_f16_sdwa v88, v72 dst_sel:WORD_1 dst_unused:UNUSED_PRESERVE src0_sel:WORD_1
	v_exp_f16_sdwa v89, v73 dst_sel:WORD_1 dst_unused:UNUSED_PRESERVE src0_sel:WORD_1
	s_nop 0
	v_pk_add_f16 v70, v164, v154
	v_pk_add_f16 v69, v69, v86
	v_pk_add_f16 v66, v66, v89
	v_pk_add_f16 v67, v67, v88
	v_pk_add_f16 v68, v68, v87
	v_pk_fma_f16 v45, v13, v89, v45
	v_pk_fma_f16 v44, v12, v88, v44
	v_pk_fma_f16 v43, v11, v87, v43
	v_pk_fma_f16 v42, v10, v86, v42
	v_pk_add_f16 v71, v163, v155
	v_pk_add_f16 v72, v162, v156
	v_pk_add_f16 v73, v161, v157
	s_nop 0
	v_exp_f16_sdwa v86, v70 dst_sel:WORD_0 dst_unused:UNUSED_PAD src0_sel:WORD_0
	v_exp_f16_sdwa v87, v71 dst_sel:WORD_0 dst_unused:UNUSED_PAD src0_sel:WORD_0
	v_exp_f16_sdwa v88, v72 dst_sel:WORD_0 dst_unused:UNUSED_PAD src0_sel:WORD_0
	v_exp_f16_sdwa v89, v73 dst_sel:WORD_0 dst_unused:UNUSED_PAD src0_sel:WORD_0
	v_exp_f16_sdwa v86, v70 dst_sel:WORD_1 dst_unused:UNUSED_PRESERVE src0_sel:WORD_1
	v_exp_f16_sdwa v87, v71 dst_sel:WORD_1 dst_unused:UNUSED_PRESERVE src0_sel:WORD_1
	v_exp_f16_sdwa v88, v72 dst_sel:WORD_1 dst_unused:UNUSED_PRESERVE src0_sel:WORD_1
	v_exp_f16_sdwa v89, v73 dst_sel:WORD_1 dst_unused:UNUSED_PRESERVE src0_sel:WORD_1
	s_nop 0
	v_pk_add_f16 v70, v114, v154
	v_pk_add_f16 v69, v69, v86
	v_pk_add_f16 v68, v68, v87
	v_pk_add_f16 v67, v67, v88
	v_pk_add_f16 v66, v66, v89
	v_pk_fma_f16 v42, v14, v86, v42
	v_pk_fma_f16 v43, v15, v87, v43
	v_pk_fma_f16 v44, v16, v88, v44
	v_pk_fma_f16 v45, v17, v89, v45
	v_pk_add_f16 v71, v115, v155
	v_pk_add_f16 v72, v116, v156
	v_pk_add_f16 v73, v117, v157
	s_nop 0
	v_exp_f16_sdwa v86, v70 dst_sel:WORD_0 dst_unused:UNUSED_PAD src0_sel:WORD_0
	v_exp_f16_sdwa v87, v71 dst_sel:WORD_0 dst_unused:UNUSED_PAD src0_sel:WORD_0
	v_exp_f16_sdwa v88, v72 dst_sel:WORD_0 dst_unused:UNUSED_PAD src0_sel:WORD_0
	v_exp_f16_sdwa v89, v73 dst_sel:WORD_0 dst_unused:UNUSED_PAD src0_sel:WORD_0
	v_exp_f16_sdwa v86, v70 dst_sel:WORD_1 dst_unused:UNUSED_PRESERVE src0_sel:WORD_1
	v_exp_f16_sdwa v87, v71 dst_sel:WORD_1 dst_unused:UNUSED_PRESERVE src0_sel:WORD_1
	v_exp_f16_sdwa v88, v72 dst_sel:WORD_1 dst_unused:UNUSED_PRESERVE src0_sel:WORD_1
	v_exp_f16_sdwa v89, v73 dst_sel:WORD_1 dst_unused:UNUSED_PRESERVE src0_sel:WORD_1
	s_nop 0
	s_nop 0
	v_pk_add_f16 v69, v69, v86
	v_pk_add_f16 v68, v68, v87
	v_rcp_f16_e32 v70, v69
	v_rcp_f16_sdwa v69, v69 dst_sel:DWORD dst_unused:UNUSED_PAD src0_sel:WORD_1
	v_pk_add_f16 v67, v67, v88
	v_rcp_f16_e32 v71, v68
	v_rcp_f16_sdwa v68, v68 dst_sel:DWORD dst_unused:UNUSED_PAD src0_sel:WORD_1
	v_pk_add_f16 v66, v66, v89
	v_rcp_f16_e32 v72, v67
	v_rcp_f16_sdwa v67, v67 dst_sel:DWORD dst_unused:UNUSED_PAD src0_sel:WORD_1
	v_rcp_f16_e32 v73, v66
	v_rcp_f16_sdwa v66, v66 dst_sel:DWORD dst_unused:UNUSED_PAD src0_sel:WORD_1
	v_pk_fma_f16 v42, v18, v86, v42
	v_pack_b32_f16 v69, v70, v69
	v_pk_fma_f16 v43, v19, v87, v43
	v_pk_mul_f16 v97, v42, v69
	v_pack_b32_f16 v42, v71, v68
	v_pk_fma_f16 v44, v20, v88, v44
	v_pk_mul_f16 v96, v43, v42
	v_pack_b32_f16 v42, v72, v67
	v_pk_fma_f16 v45, v21, v89, v45
	v_pk_mul_f16 v95, v44, v42
	v_pack_b32_f16 v42, v73, v66
	v_pk_mul_f16 v94, v45, v42
	s_waitcnt vmcnt(7)
	v_pk_mul_f16 v45, v160, v153 op_sel_hi:[0,1]
	v_pk_mul_f16 v42, v160, v150 op_sel_hi:[0,1]
	v_pk_mul_f16 v43, v160, v151 op_sel_hi:[0,1]
	v_pk_mul_f16 v44, v160, v152 op_sel_hi:[0,1]
	v_pk_mul_f16 v69, v158, v153 op_sel_hi:[0,1]
	v_pk_mul_f16 v73, v159, v153 op_sel_hi:[0,1]
	v_pk_fma_f16 v57, v57, v153, v45
	v_pk_fma_f16 v77, v77, v153, v45
	v_pk_fma_f16 v45, v101, v153, v45
	v_pk_mul_f16 v66, v158, v150 op_sel_hi:[0,1]
	v_pk_maximum3_f16 v117, v57, v77, v45
	v_pk_mul_f16 v67, v158, v151 op_sel_hi:[0,1]
	v_pk_mul_f16 v68, v158, v152 op_sel_hi:[0,1]
	v_pk_mul_f16 v70, v159, v150 op_sel_hi:[0,1]
	v_pk_mul_f16 v71, v159, v151 op_sel_hi:[0,1]
	v_pk_mul_f16 v72, v159, v152 op_sel_hi:[0,1]
	v_pk_fma_f16 v56, v56, v152, v44
	v_pk_fma_f16 v55, v55, v151, v43
	v_pk_fma_f16 v54, v54, v150, v42
	v_pk_fma_f16 v76, v76, v152, v44
	v_pk_fma_f16 v75, v75, v151, v43
	v_pk_fma_f16 v74, v74, v150, v42
	v_pk_fma_f16 v44, v100, v152, v44
	v_pk_fma_f16 v43, v99, v151, v43
	v_pk_fma_f16 v42, v98, v150, v42
	v_pk_fma_f16 v86, v29, v153, v69
	v_pk_fma_f16 v90, v41, v153, v69
	v_pk_fma_f16 v69, v61, v153, v69
	v_pk_fma_f16 v98, v81, v153, v73
	v_pk_fma_f16 v110, v109, v153, v73
	v_pk_fma_f16 v73, v125, v153, v73
	v_pk_maximum3_f16 v114, v54, v74, v42
	v_pk_maximum3_f16 v115, v55, v75, v43
	v_pk_maximum3_f16 v116, v56, v76, v44
	v_pk_maximum3_f16 v121, v86, v90, v69
	v_pk_fma_f16 v87, v28, v152, v68
	v_pk_maximum3_f16 v129, v98, v110, v73
	v_pk_fma_f16 v88, v27, v151, v67
	v_pk_maximum3_f16 v117, v117, v121, v129
	v_pk_fma_f16 v89, v26, v150, v66
	v_pk_fma_f16 v91, v40, v152, v68
	v_pk_fma_f16 v92, v39, v151, v67
	v_pk_fma_f16 v93, v38, v150, v66
	v_pk_fma_f16 v68, v60, v152, v68
	v_pk_fma_f16 v67, v59, v151, v67
	v_pk_fma_f16 v66, v58, v150, v66
	v_pk_fma_f16 v99, v80, v152, v72
	v_pk_fma_f16 v100, v79, v151, v71
	v_pk_fma_f16 v101, v78, v150, v70
	v_pk_fma_f16 v111, v108, v152, v72
	v_pk_fma_f16 v112, v107, v151, v71
	v_pk_fma_f16 v113, v106, v150, v70
	v_pk_fma_f16 v72, v124, v152, v72
	v_pk_fma_f16 v71, v123, v151, v71
	v_pk_fma_f16 v70, v122, v150, v70
	v_pk_maximum3_f16 v118, v89, v93, v66
	v_pk_maximum3_f16 v119, v88, v92, v67
	v_pk_maximum3_f16 v120, v87, v91, v68
	v_pk_maximum3_f16 v127, v100, v112, v71
	v_pk_maximum3_f16 v128, v99, v111, v72
	s_nop 0
	v_pk_maximum3_f16 v126, v101, v113, v70
	v_xor_b32_e32 v117, 0x80008000, v117
	v_pk_maximum3_f16 v114, v114, v118, v126
	v_pk_maximum3_f16 v115, v115, v119, v127
	v_pk_maximum3_f16 v116, v116, v120, v128
	v_pk_add_f16 v57, v57, v117
	v_xor_b32_e32 v116, 0x80008000, v116
	v_xor_b32_e32 v115, 0x80008000, v115
	v_xor_b32_e32 v114, 0x80008000, v114
	v_pk_add_f16 v54, v54, v114
	v_pk_add_f16 v55, v55, v115
	v_pk_add_f16 v56, v56, v116
	v_pk_add_f16 v74, v74, v114
	v_exp_f16_sdwa v118, v54 dst_sel:WORD_0 dst_unused:UNUSED_PAD src0_sel:WORD_0
	v_exp_f16_sdwa v119, v55 dst_sel:WORD_0 dst_unused:UNUSED_PAD src0_sel:WORD_0
	v_exp_f16_sdwa v120, v56 dst_sel:WORD_0 dst_unused:UNUSED_PAD src0_sel:WORD_0
	v_exp_f16_sdwa v121, v57 dst_sel:WORD_0 dst_unused:UNUSED_PAD src0_sel:WORD_0
	v_exp_f16_sdwa v118, v54 dst_sel:WORD_1 dst_unused:UNUSED_PRESERVE src0_sel:WORD_1
	v_exp_f16_sdwa v119, v55 dst_sel:WORD_1 dst_unused:UNUSED_PRESERVE src0_sel:WORD_1
	v_exp_f16_sdwa v120, v56 dst_sel:WORD_1 dst_unused:UNUSED_PRESERVE src0_sel:WORD_1
	v_exp_f16_sdwa v121, v57 dst_sel:WORD_1 dst_unused:UNUSED_PRESERVE src0_sel:WORD_1
	s_nop 0
	v_pk_add_f16 v75, v75, v115
	v_pk_add_f16 v57, v118, 0
	v_pk_fma_f16 v25, v25, v121, 0
	v_pk_add_f16 v54, v121, 0
	v_pk_add_f16 v55, v120, 0
	v_pk_add_f16 v56, v119, 0
	v_pk_fma_f16 v24, v24, v120, 0
	v_pk_fma_f16 v23, v23, v119, 0
	v_pk_fma_f16 v22, v22, v118, 0
	v_pk_add_f16 v76, v76, v116
	v_pk_add_f16 v77, v77, v117
	s_nop 0
	v_exp_f16_sdwa v118, v74 dst_sel:WORD_0 dst_unused:UNUSED_PAD src0_sel:WORD_0
	v_exp_f16_sdwa v119, v75 dst_sel:WORD_0 dst_unused:UNUSED_PAD src0_sel:WORD_0
	v_exp_f16_sdwa v120, v76 dst_sel:WORD_0 dst_unused:UNUSED_PAD src0_sel:WORD_0
	v_exp_f16_sdwa v121, v77 dst_sel:WORD_0 dst_unused:UNUSED_PAD src0_sel:WORD_0
	v_exp_f16_sdwa v118, v74 dst_sel:WORD_1 dst_unused:UNUSED_PRESERVE src0_sel:WORD_1
	v_exp_f16_sdwa v119, v75 dst_sel:WORD_1 dst_unused:UNUSED_PRESERVE src0_sel:WORD_1
	v_exp_f16_sdwa v120, v76 dst_sel:WORD_1 dst_unused:UNUSED_PRESERVE src0_sel:WORD_1
	v_exp_f16_sdwa v121, v77 dst_sel:WORD_1 dst_unused:UNUSED_PRESERVE src0_sel:WORD_1
	s_nop 0
	s_nop 0
	v_pk_add_f16 v57, v57, v118
	v_pk_fma_f16 v25, v37, v121, v25
	v_pk_add_f16 v37, v45, v117
	v_pk_add_f16 v56, v56, v119
	v_pk_add_f16 v55, v55, v120
	v_pk_add_f16 v54, v54, v121
	v_pk_fma_f16 v22, v34, v118, v22
	v_pk_fma_f16 v23, v35, v119, v23
	v_pk_fma_f16 v24, v36, v120, v24
	v_pk_add_f16 v34, v42, v114
	v_pk_add_f16 v35, v43, v115
	v_pk_add_f16 v36, v44, v116
	s_nop 0
	v_exp_f16_sdwa v42, v34 dst_sel:WORD_0 dst_unused:UNUSED_PAD src0_sel:WORD_0
	v_exp_f16_sdwa v43, v35 dst_sel:WORD_0 dst_unused:UNUSED_PAD src0_sel:WORD_0
	v_exp_f16_sdwa v44, v36 dst_sel:WORD_0 dst_unused:UNUSED_PAD src0_sel:WORD_0
	v_exp_f16_sdwa v45, v37 dst_sel:WORD_0 dst_unused:UNUSED_PAD src0_sel:WORD_0
	v_exp_f16_sdwa v42, v34 dst_sel:WORD_1 dst_unused:UNUSED_PRESERVE src0_sel:WORD_1
	v_exp_f16_sdwa v43, v35 dst_sel:WORD_1 dst_unused:UNUSED_PRESERVE src0_sel:WORD_1
	v_exp_f16_sdwa v44, v36 dst_sel:WORD_1 dst_unused:UNUSED_PRESERVE src0_sel:WORD_1
	v_exp_f16_sdwa v45, v37 dst_sel:WORD_1 dst_unused:UNUSED_PRESERVE src0_sel:WORD_1
	s_nop 0
	s_nop 0
	v_pk_add_f16 v37, v57, v42
	v_pk_add_f16 v34, v54, v45
	v_pk_add_f16 v35, v55, v44
	v_pk_add_f16 v36, v56, v43
	v_pk_fma_f16 v25, v53, v45, v25
	v_pk_fma_f16 v24, v52, v44, v24
	v_pk_fma_f16 v23, v51, v43, v23
	v_pk_fma_f16 v22, v50, v42, v22
	v_pk_add_f16 v42, v89, v114
	v_pk_add_f16 v43, v88, v115
	v_pk_add_f16 v44, v87, v116
	v_pk_add_f16 v45, v86, v117
	s_nop 0
	v_exp_f16_sdwa v50, v42 dst_sel:WORD_0 dst_unused:UNUSED_PAD src0_sel:WORD_0
	v_exp_f16_sdwa v51, v43 dst_sel:WORD_0 dst_unused:UNUSED_PAD src0_sel:WORD_0
	v_exp_f16_sdwa v52, v44 dst_sel:WORD_0 dst_unused:UNUSED_PAD src0_sel:WORD_0
	v_exp_f16_sdwa v53, v45 dst_sel:WORD_0 dst_unused:UNUSED_PAD src0_sel:WORD_0
	v_exp_f16_sdwa v50, v42 dst_sel:WORD_1 dst_unused:UNUSED_PRESERVE src0_sel:WORD_1
	v_exp_f16_sdwa v51, v43 dst_sel:WORD_1 dst_unused:UNUSED_PRESERVE src0_sel:WORD_1
	v_exp_f16_sdwa v52, v44 dst_sel:WORD_1 dst_unused:UNUSED_PRESERVE src0_sel:WORD_1
	v_exp_f16_sdwa v53, v45 dst_sel:WORD_1 dst_unused:UNUSED_PRESERVE src0_sel:WORD_1
	s_nop 0
	v_pk_add_f16 v42, v93, v114
	v_pk_add_f16 v37, v37, v50
	v_pk_add_f16 v36, v36, v51
	v_pk_add_f16 v35, v35, v52
	v_pk_add_f16 v34, v34, v53
	v_pk_fma_f16 v22, v10, v50, v22
	v_pk_fma_f16 v23, v11, v51, v23
	v_pk_fma_f16 v24, v12, v52, v24
	v_pk_fma_f16 v25, v13, v53, v25
	v_pk_add_f16 v43, v92, v115
	v_pk_add_f16 v44, v91, v116
	v_pk_add_f16 v45, v90, v117
	s_nop 0
	v_exp_f16_sdwa v50, v42 dst_sel:WORD_0 dst_unused:UNUSED_PAD src0_sel:WORD_0
	v_exp_f16_sdwa v51, v43 dst_sel:WORD_0 dst_unused:UNUSED_PAD src0_sel:WORD_0
	v_exp_f16_sdwa v52, v44 dst_sel:WORD_0 dst_unused:UNUSED_PAD src0_sel:WORD_0
	v_exp_f16_sdwa v53, v45 dst_sel:WORD_0 dst_unused:UNUSED_PAD src0_sel:WORD_0
	v_exp_f16_sdwa v50, v42 dst_sel:WORD_1 dst_unused:UNUSED_PRESERVE src0_sel:WORD_1
	v_exp_f16_sdwa v51, v43 dst_sel:WORD_1 dst_unused:UNUSED_PRESERVE src0_sel:WORD_1
	v_exp_f16_sdwa v52, v44 dst_sel:WORD_1 dst_unused:UNUSED_PRESERVE src0_sel:WORD_1
	v_exp_f16_sdwa v53, v45 dst_sel:WORD_1 dst_unused:UNUSED_PRESERVE src0_sel:WORD_1
	s_nop 0
	v_pk_add_f16 v42, v66, v114
	v_pk_add_f16 v37, v37, v50
	v_pk_add_f16 v34, v34, v53
	v_pk_add_f16 v35, v35, v52
	v_pk_add_f16 v36, v36, v51
	v_pk_fma_f16 v25, v17, v53, v25
	v_pk_fma_f16 v24, v16, v52, v24
	v_pk_fma_f16 v23, v15, v51, v23
	v_pk_fma_f16 v22, v14, v50, v22
	v_pk_add_f16 v43, v67, v115
	v_pk_add_f16 v44, v68, v116
	v_pk_add_f16 v45, v69, v117
	s_nop 0
	v_exp_f16_sdwa v50, v42 dst_sel:WORD_0 dst_unused:UNUSED_PAD src0_sel:WORD_0
	v_exp_f16_sdwa v51, v43 dst_sel:WORD_0 dst_unused:UNUSED_PAD src0_sel:WORD_0
	v_exp_f16_sdwa v52, v44 dst_sel:WORD_0 dst_unused:UNUSED_PAD src0_sel:WORD_0
	v_exp_f16_sdwa v53, v45 dst_sel:WORD_0 dst_unused:UNUSED_PAD src0_sel:WORD_0
	v_exp_f16_sdwa v50, v42 dst_sel:WORD_1 dst_unused:UNUSED_PRESERVE src0_sel:WORD_1
	v_exp_f16_sdwa v51, v43 dst_sel:WORD_1 dst_unused:UNUSED_PRESERVE src0_sel:WORD_1
	v_exp_f16_sdwa v52, v44 dst_sel:WORD_1 dst_unused:UNUSED_PRESERVE src0_sel:WORD_1
	v_exp_f16_sdwa v53, v45 dst_sel:WORD_1 dst_unused:UNUSED_PRESERVE src0_sel:WORD_1
	s_nop 0
	v_pk_add_f16 v42, v101, v114
	v_pk_add_f16 v37, v37, v50
	v_pk_add_f16 v36, v36, v51
	v_pk_add_f16 v35, v35, v52
	v_pk_add_f16 v34, v34, v53
	v_pk_fma_f16 v22, v18, v50, v22
	v_pk_fma_f16 v23, v19, v51, v23
	v_pk_fma_f16 v24, v20, v52, v24
	v_pk_fma_f16 v25, v21, v53, v25
	v_pk_add_f16 v43, v100, v115
	v_pk_add_f16 v44, v99, v116
	v_pk_add_f16 v45, v98, v117
	s_nop 0
	v_exp_f16_sdwa v50, v42 dst_sel:WORD_0 dst_unused:UNUSED_PAD src0_sel:WORD_0
	v_exp_f16_sdwa v51, v43 dst_sel:WORD_0 dst_unused:UNUSED_PAD src0_sel:WORD_0
	v_exp_f16_sdwa v52, v44 dst_sel:WORD_0 dst_unused:UNUSED_PAD src0_sel:WORD_0
	v_exp_f16_sdwa v53, v45 dst_sel:WORD_0 dst_unused:UNUSED_PAD src0_sel:WORD_0
	v_exp_f16_sdwa v50, v42 dst_sel:WORD_1 dst_unused:UNUSED_PRESERVE src0_sel:WORD_1
	v_exp_f16_sdwa v51, v43 dst_sel:WORD_1 dst_unused:UNUSED_PRESERVE src0_sel:WORD_1
	v_exp_f16_sdwa v52, v44 dst_sel:WORD_1 dst_unused:UNUSED_PRESERVE src0_sel:WORD_1
	v_exp_f16_sdwa v53, v45 dst_sel:WORD_1 dst_unused:UNUSED_PRESERVE src0_sel:WORD_1
	s_nop 0
	v_pk_add_f16 v42, v113, v114
	v_pk_add_f16 v37, v37, v50
	v_pk_add_f16 v34, v34, v53
	v_pk_add_f16 v35, v35, v52
	v_pk_add_f16 v36, v36, v51
	v_pk_fma_f16 v25, v33, v53, v25
	v_pk_fma_f16 v24, v32, v52, v24
	v_pk_fma_f16 v23, v31, v51, v23
	v_pk_fma_f16 v22, v30, v50, v22
	v_pk_add_f16 v43, v112, v115
	v_pk_add_f16 v44, v111, v116
	v_pk_add_f16 v45, v110, v117
	s_nop 0
	v_exp_f16_sdwa v50, v42 dst_sel:WORD_0 dst_unused:UNUSED_PAD src0_sel:WORD_0
	v_exp_f16_sdwa v51, v43 dst_sel:WORD_0 dst_unused:UNUSED_PAD src0_sel:WORD_0
	v_exp_f16_sdwa v52, v44 dst_sel:WORD_0 dst_unused:UNUSED_PAD src0_sel:WORD_0
	v_exp_f16_sdwa v53, v45 dst_sel:WORD_0 dst_unused:UNUSED_PAD src0_sel:WORD_0
	v_exp_f16_sdwa v50, v42 dst_sel:WORD_1 dst_unused:UNUSED_PRESERVE src0_sel:WORD_1
	v_exp_f16_sdwa v51, v43 dst_sel:WORD_1 dst_unused:UNUSED_PRESERVE src0_sel:WORD_1
	v_exp_f16_sdwa v52, v44 dst_sel:WORD_1 dst_unused:UNUSED_PRESERVE src0_sel:WORD_1
	v_exp_f16_sdwa v53, v45 dst_sel:WORD_1 dst_unused:UNUSED_PRESERVE src0_sel:WORD_1
	s_nop 0
	v_pk_add_f16 v42, v70, v114
	v_pk_add_f16 v37, v37, v50
	v_pk_add_f16 v36, v36, v51
	v_pk_add_f16 v35, v35, v52
	v_pk_add_f16 v34, v34, v53
	v_pk_fma_f16 v22, v46, v50, v22
	v_pk_fma_f16 v23, v47, v51, v23
	v_pk_fma_f16 v24, v48, v52, v24
	v_pk_fma_f16 v25, v49, v53, v25
	v_pk_add_f16 v43, v71, v115
	v_pk_add_f16 v44, v72, v116
	v_pk_add_f16 v45, v73, v117
	s_nop 0
	v_exp_f16_sdwa v50, v42 dst_sel:WORD_0 dst_unused:UNUSED_PAD src0_sel:WORD_0
	v_exp_f16_sdwa v51, v43 dst_sel:WORD_0 dst_unused:UNUSED_PAD src0_sel:WORD_0
	v_exp_f16_sdwa v52, v44 dst_sel:WORD_0 dst_unused:UNUSED_PAD src0_sel:WORD_0
	v_exp_f16_sdwa v53, v45 dst_sel:WORD_0 dst_unused:UNUSED_PAD src0_sel:WORD_0
	v_exp_f16_sdwa v50, v42 dst_sel:WORD_1 dst_unused:UNUSED_PRESERVE src0_sel:WORD_1
	v_exp_f16_sdwa v51, v43 dst_sel:WORD_1 dst_unused:UNUSED_PRESERVE src0_sel:WORD_1
	v_exp_f16_sdwa v52, v44 dst_sel:WORD_1 dst_unused:UNUSED_PRESERVE src0_sel:WORD_1
	v_exp_f16_sdwa v53, v45 dst_sel:WORD_1 dst_unused:UNUSED_PRESERVE src0_sel:WORD_1
	s_nop 0
	s_nop 0
	v_pk_add_f16 v37, v37, v50
	v_pk_add_f16 v36, v36, v51
	v_rcp_f16_e32 v42, v37
	v_rcp_f16_sdwa v37, v37 dst_sel:DWORD dst_unused:UNUSED_PAD src0_sel:WORD_1
	v_pk_add_f16 v35, v35, v52
	v_rcp_f16_e32 v43, v36
	v_rcp_f16_sdwa v36, v36 dst_sel:DWORD dst_unused:UNUSED_PAD src0_sel:WORD_1
	v_pk_add_f16 v34, v34, v53
	v_pk_fma_f16 v22, v62, v50, v22
	v_rcp_f16_e32 v50, v35
	v_rcp_f16_sdwa v35, v35 dst_sel:DWORD dst_unused:UNUSED_PAD src0_sel:WORD_1
	v_pk_fma_f16 v23, v63, v51, v23
	v_rcp_f16_e32 v51, v34
	v_rcp_f16_sdwa v34, v34 dst_sel:DWORD dst_unused:UNUSED_PAD src0_sel:WORD_1
	v_pack_b32_f16 v37, v42, v37
	v_pk_mul_f16 v45, v22, v37
	v_pack_b32_f16 v22, v43, v36
	v_pk_fma_f16 v24, v64, v52, v24
	v_pk_mul_f16 v44, v23, v22
	v_pack_b32_f16 v22, v50, v35
	v_pk_fma_f16 v25, v65, v53, v25
	v_pk_mul_f16 v43, v24, v22
	v_pack_b32_f16 v22, v51, v34
	v_pk_mul_f16 v42, v25, v22
	s_waitcnt vmcnt(0)
	v_pk_mul_f16 v22, v160, v146 op_sel_hi:[0,1]
	v_pk_mul_f16 v23, v160, v147 op_sel_hi:[0,1]
	v_pk_mul_f16 v24, v160, v148 op_sel_hi:[0,1]
	v_pk_mul_f16 v25, v160, v149 op_sel_hi:[0,1]
	v_pk_mul_f16 v50, v159, v146 op_sel_hi:[0,1]
	v_pk_mul_f16 v51, v159, v147 op_sel_hi:[0,1]
	v_pk_mul_f16 v52, v159, v148 op_sel_hi:[0,1]
	v_pk_mul_f16 v53, v159, v149 op_sel_hi:[0,1]
	v_pk_mul_f16 v34, v158, v146 op_sel_hi:[0,1]
	v_pk_mul_f16 v35, v158, v147 op_sel_hi:[0,1]
	v_pk_mul_f16 v36, v158, v148 op_sel_hi:[0,1]
	v_pk_mul_f16 v37, v158, v149 op_sel_hi:[0,1]
	v_pk_fma_f16 v29, v29, v149, v25
	v_pk_fma_f16 v28, v28, v148, v24
	v_pk_fma_f16 v27, v27, v147, v23
	v_pk_fma_f16 v26, v26, v146, v22
	v_pk_fma_f16 v41, v41, v149, v25
	v_pk_fma_f16 v40, v40, v148, v24
	v_pk_fma_f16 v39, v39, v147, v23
	v_pk_fma_f16 v38, v38, v146, v22
	v_pk_fma_f16 v25, v61, v149, v25
	v_pk_fma_f16 v24, v60, v148, v24
	v_pk_fma_f16 v23, v59, v147, v23
	v_pk_fma_f16 v22, v58, v146, v22
	v_pk_fma_f16 v66, v137, v149, v53
	v_pk_fma_f16 v67, v136, v148, v52
	v_pk_fma_f16 v68, v135, v147, v51
	v_pk_fma_f16 v69, v134, v146, v50
	v_pk_fma_f16 v70, v145, v149, v53
	v_pk_fma_f16 v71, v144, v148, v52
	v_pk_fma_f16 v72, v143, v147, v51
	v_pk_fma_f16 v73, v142, v146, v50
	v_pk_fma_f16 v9, v9, v149, v53
	v_pk_fma_f16 v8, v8, v148, v52
	v_pk_fma_f16 v7, v7, v147, v51
	v_pk_fma_f16 v6, v6, v146, v50
	v_pk_maximum3_f16 v50, v26, v38, v22
	v_pk_maximum3_f16 v51, v27, v39, v23
	v_pk_maximum3_f16 v52, v28, v40, v24
	v_pk_maximum3_f16 v53, v29, v41, v25
	v_pk_fma_f16 v54, v81, v149, v37
	v_pk_fma_f16 v55, v80, v148, v36
	v_pk_fma_f16 v56, v79, v147, v35
	v_pk_fma_f16 v57, v78, v146, v34
	v_pk_fma_f16 v58, v109, v149, v37
	v_pk_fma_f16 v59, v108, v148, v36
	v_pk_fma_f16 v60, v107, v147, v35
	v_pk_fma_f16 v61, v106, v146, v34
	v_pk_fma_f16 v37, v125, v149, v37
	v_pk_fma_f16 v36, v124, v148, v36
	v_pk_fma_f16 v35, v123, v147, v35
	v_pk_fma_f16 v34, v122, v146, v34
	v_pk_maximum3_f16 v75, v56, v60, v35
	v_pk_maximum3_f16 v76, v55, v59, v36
	v_pk_maximum3_f16 v77, v54, v58, v37
	v_pk_maximum3_f16 v78, v69, v73, v6
	v_pk_maximum3_f16 v79, v68, v72, v7
	s_nop 0
	v_pk_maximum3_f16 v74, v57, v61, v34
	v_pk_maximum3_f16 v80, v67, v71, v8
	v_pk_maximum3_f16 v81, v66, v70, v9
	s_nop 0
	v_pk_maximum3_f16 v50, v50, v74, v78
	v_pk_maximum3_f16 v51, v51, v75, v79
	v_pk_maximum3_f16 v52, v52, v76, v80
	v_pk_maximum3_f16 v53, v53, v77, v81
	s_nop 0
	v_xor_b32_e32 v53, 0x80008000, v53
	v_xor_b32_e32 v52, 0x80008000, v52
	v_xor_b32_e32 v51, 0x80008000, v51
	v_xor_b32_e32 v50, 0x80008000, v50
	v_pk_add_f16 v26, v26, v50
	v_pk_add_f16 v27, v27, v51
	v_pk_add_f16 v28, v28, v52
	v_pk_add_f16 v29, v29, v53
	v_pk_add_f16 v38, v38, v50
	v_exp_f16_sdwa v74, v26 dst_sel:WORD_0 dst_unused:UNUSED_PAD src0_sel:WORD_0
	v_exp_f16_sdwa v75, v27 dst_sel:WORD_0 dst_unused:UNUSED_PAD src0_sel:WORD_0
	v_exp_f16_sdwa v76, v28 dst_sel:WORD_0 dst_unused:UNUSED_PAD src0_sel:WORD_0
	v_exp_f16_sdwa v77, v29 dst_sel:WORD_0 dst_unused:UNUSED_PAD src0_sel:WORD_0
	v_exp_f16_sdwa v74, v26 dst_sel:WORD_1 dst_unused:UNUSED_PRESERVE src0_sel:WORD_1
	v_exp_f16_sdwa v75, v27 dst_sel:WORD_1 dst_unused:UNUSED_PRESERVE src0_sel:WORD_1
	v_exp_f16_sdwa v76, v28 dst_sel:WORD_1 dst_unused:UNUSED_PRESERVE src0_sel:WORD_1
	v_exp_f16_sdwa v77, v29 dst_sel:WORD_1 dst_unused:UNUSED_PRESERVE src0_sel:WORD_1
	s_nop 0
	v_pk_add_f16 v39, v39, v51
	v_pk_add_f16 v26, v74, 0
	v_pk_add_f16 v27, v75, 0
	v_pk_add_f16 v28, v76, 0
	v_pk_add_f16 v29, v77, 0
	v_pk_fma_f16 v10, v10, v74, 0
	v_pk_fma_f16 v11, v11, v75, 0
	v_pk_fma_f16 v12, v12, v76, 0
	v_pk_fma_f16 v13, v13, v77, 0
	v_pk_add_f16 v40, v40, v52
	v_pk_add_f16 v41, v41, v53
	v_pk_add_f16 v6, v6, v50
	v_exp_f16_sdwa v74, v38 dst_sel:WORD_0 dst_unused:UNUSED_PAD src0_sel:WORD_0
	v_exp_f16_sdwa v75, v39 dst_sel:WORD_0 dst_unused:UNUSED_PAD src0_sel:WORD_0
	v_exp_f16_sdwa v76, v40 dst_sel:WORD_0 dst_unused:UNUSED_PAD src0_sel:WORD_0
	v_exp_f16_sdwa v77, v41 dst_sel:WORD_0 dst_unused:UNUSED_PAD src0_sel:WORD_0
	v_exp_f16_sdwa v74, v38 dst_sel:WORD_1 dst_unused:UNUSED_PRESERVE src0_sel:WORD_1
	v_exp_f16_sdwa v75, v39 dst_sel:WORD_1 dst_unused:UNUSED_PRESERVE src0_sel:WORD_1
	v_exp_f16_sdwa v76, v40 dst_sel:WORD_1 dst_unused:UNUSED_PRESERVE src0_sel:WORD_1
	v_exp_f16_sdwa v77, v41 dst_sel:WORD_1 dst_unused:UNUSED_PRESERVE src0_sel:WORD_1
	s_nop 0
	v_pk_add_f16 v7, v7, v51
	v_pk_add_f16 v29, v29, v77
	v_pk_add_f16 v28, v28, v76
	v_pk_add_f16 v27, v27, v75
	v_pk_add_f16 v26, v26, v74
	v_pk_fma_f16 v13, v17, v77, v13
	v_pk_fma_f16 v12, v16, v76, v12
	v_pk_fma_f16 v11, v15, v75, v11
	v_pk_fma_f16 v10, v14, v74, v10
	v_pk_add_f16 v14, v22, v50
	v_pk_add_f16 v15, v23, v51
	v_pk_add_f16 v16, v24, v52
	v_pk_add_f16 v17, v25, v53
	v_pk_add_f16 v8, v8, v52
	v_exp_f16_sdwa v22, v14 dst_sel:WORD_0 dst_unused:UNUSED_PAD src0_sel:WORD_0
	v_exp_f16_sdwa v23, v15 dst_sel:WORD_0 dst_unused:UNUSED_PAD src0_sel:WORD_0
	v_exp_f16_sdwa v24, v16 dst_sel:WORD_0 dst_unused:UNUSED_PAD src0_sel:WORD_0
	v_exp_f16_sdwa v25, v17 dst_sel:WORD_0 dst_unused:UNUSED_PAD src0_sel:WORD_0
	v_exp_f16_sdwa v22, v14 dst_sel:WORD_1 dst_unused:UNUSED_PRESERVE src0_sel:WORD_1
	v_exp_f16_sdwa v23, v15 dst_sel:WORD_1 dst_unused:UNUSED_PRESERVE src0_sel:WORD_1
	v_exp_f16_sdwa v24, v16 dst_sel:WORD_1 dst_unused:UNUSED_PRESERVE src0_sel:WORD_1
	v_exp_f16_sdwa v25, v17 dst_sel:WORD_1 dst_unused:UNUSED_PRESERVE src0_sel:WORD_1
	s_nop 0
	v_pk_add_f16 v9, v9, v53
	v_pk_add_f16 v14, v26, v22
	v_pk_add_f16 v15, v27, v23
	v_pk_add_f16 v16, v28, v24
	v_pk_add_f16 v17, v29, v25
	v_pk_fma_f16 v10, v18, v22, v10
	v_pk_fma_f16 v11, v19, v23, v11
	v_pk_fma_f16 v12, v20, v24, v12
	v_pk_fma_f16 v13, v21, v25, v13
	v_pk_add_f16 v18, v57, v50
	v_pk_add_f16 v19, v56, v51
	v_pk_add_f16 v20, v55, v52
	v_pk_add_f16 v21, v54, v53
	s_nop 0
	v_exp_f16_sdwa v22, v18 dst_sel:WORD_0 dst_unused:UNUSED_PAD src0_sel:WORD_0
	v_exp_f16_sdwa v23, v19 dst_sel:WORD_0 dst_unused:UNUSED_PAD src0_sel:WORD_0
	v_exp_f16_sdwa v24, v20 dst_sel:WORD_0 dst_unused:UNUSED_PAD src0_sel:WORD_0
	v_exp_f16_sdwa v25, v21 dst_sel:WORD_0 dst_unused:UNUSED_PAD src0_sel:WORD_0
	v_exp_f16_sdwa v22, v18 dst_sel:WORD_1 dst_unused:UNUSED_PRESERVE src0_sel:WORD_1
	v_exp_f16_sdwa v23, v19 dst_sel:WORD_1 dst_unused:UNUSED_PRESERVE src0_sel:WORD_1
	v_exp_f16_sdwa v24, v20 dst_sel:WORD_1 dst_unused:UNUSED_PRESERVE src0_sel:WORD_1
	v_exp_f16_sdwa v25, v21 dst_sel:WORD_1 dst_unused:UNUSED_PRESERVE src0_sel:WORD_1
	s_nop 0
	v_pk_add_f16 v18, v61, v50
	v_pk_add_f16 v17, v17, v25
	v_pk_add_f16 v16, v16, v24
	v_pk_add_f16 v15, v15, v23
	v_pk_add_f16 v14, v14, v22
	v_pk_fma_f16 v13, v33, v25, v13
	v_pk_fma_f16 v12, v32, v24, v12
	v_pk_fma_f16 v11, v31, v23, v11
	v_pk_fma_f16 v10, v30, v22, v10
	v_pk_add_f16 v19, v60, v51
	v_pk_add_f16 v20, v59, v52
	v_pk_add_f16 v21, v58, v53
	s_nop 0
	v_exp_f16_sdwa v22, v18 dst_sel:WORD_0 dst_unused:UNUSED_PAD src0_sel:WORD_0
	v_exp_f16_sdwa v23, v19 dst_sel:WORD_0 dst_unused:UNUSED_PAD src0_sel:WORD_0
	v_exp_f16_sdwa v24, v20 dst_sel:WORD_0 dst_unused:UNUSED_PAD src0_sel:WORD_0
	v_exp_f16_sdwa v25, v21 dst_sel:WORD_0 dst_unused:UNUSED_PAD src0_sel:WORD_0
	v_exp_f16_sdwa v22, v18 dst_sel:WORD_1 dst_unused:UNUSED_PRESERVE src0_sel:WORD_1
	v_exp_f16_sdwa v23, v19 dst_sel:WORD_1 dst_unused:UNUSED_PRESERVE src0_sel:WORD_1
	v_exp_f16_sdwa v24, v20 dst_sel:WORD_1 dst_unused:UNUSED_PRESERVE src0_sel:WORD_1
	v_exp_f16_sdwa v25, v21 dst_sel:WORD_1 dst_unused:UNUSED_PRESERVE src0_sel:WORD_1
	s_nop 0
	v_pk_add_f16 v18, v34, v50
	v_pk_add_f16 v14, v14, v22
	v_pk_add_f16 v15, v15, v23
	v_pk_add_f16 v16, v16, v24
	v_pk_add_f16 v17, v17, v25
	v_pk_fma_f16 v10, v46, v22, v10
	v_pk_fma_f16 v11, v47, v23, v11
	v_pk_fma_f16 v12, v48, v24, v12
	v_pk_fma_f16 v13, v49, v25, v13
	v_pk_add_f16 v19, v35, v51
	v_pk_add_f16 v20, v36, v52
	v_pk_add_f16 v21, v37, v53
	s_nop 0
	v_exp_f16_sdwa v22, v18 dst_sel:WORD_0 dst_unused:UNUSED_PAD src0_sel:WORD_0
	v_exp_f16_sdwa v23, v19 dst_sel:WORD_0 dst_unused:UNUSED_PAD src0_sel:WORD_0
	v_exp_f16_sdwa v24, v20 dst_sel:WORD_0 dst_unused:UNUSED_PAD src0_sel:WORD_0
	v_exp_f16_sdwa v25, v21 dst_sel:WORD_0 dst_unused:UNUSED_PAD src0_sel:WORD_0
	v_exp_f16_sdwa v22, v18 dst_sel:WORD_1 dst_unused:UNUSED_PRESERVE src0_sel:WORD_1
	v_exp_f16_sdwa v23, v19 dst_sel:WORD_1 dst_unused:UNUSED_PRESERVE src0_sel:WORD_1
	v_exp_f16_sdwa v24, v20 dst_sel:WORD_1 dst_unused:UNUSED_PRESERVE src0_sel:WORD_1
	v_exp_f16_sdwa v25, v21 dst_sel:WORD_1 dst_unused:UNUSED_PRESERVE src0_sel:WORD_1
	s_nop 0
	v_pk_add_f16 v18, v69, v50
	v_pk_add_f16 v17, v17, v25
	v_pk_add_f16 v16, v16, v24
	v_pk_add_f16 v15, v15, v23
	v_pk_add_f16 v14, v14, v22
	v_pk_fma_f16 v13, v65, v25, v13
	v_pk_fma_f16 v12, v64, v24, v12
	v_pk_fma_f16 v11, v63, v23, v11
	v_pk_fma_f16 v10, v62, v22, v10
	v_pk_add_f16 v19, v68, v51
	v_pk_add_f16 v20, v67, v52
	v_pk_add_f16 v21, v66, v53
	s_nop 0
	v_exp_f16_sdwa v22, v18 dst_sel:WORD_0 dst_unused:UNUSED_PAD src0_sel:WORD_0
	v_exp_f16_sdwa v23, v19 dst_sel:WORD_0 dst_unused:UNUSED_PAD src0_sel:WORD_0
	v_exp_f16_sdwa v24, v20 dst_sel:WORD_0 dst_unused:UNUSED_PAD src0_sel:WORD_0
	v_exp_f16_sdwa v25, v21 dst_sel:WORD_0 dst_unused:UNUSED_PAD src0_sel:WORD_0
	v_exp_f16_sdwa v22, v18 dst_sel:WORD_1 dst_unused:UNUSED_PRESERVE src0_sel:WORD_1
	v_exp_f16_sdwa v23, v19 dst_sel:WORD_1 dst_unused:UNUSED_PRESERVE src0_sel:WORD_1
	v_exp_f16_sdwa v24, v20 dst_sel:WORD_1 dst_unused:UNUSED_PRESERVE src0_sel:WORD_1
	v_exp_f16_sdwa v25, v21 dst_sel:WORD_1 dst_unused:UNUSED_PRESERVE src0_sel:WORD_1
	s_nop 0
	v_pk_add_f16 v18, v73, v50
	v_pk_add_f16 v14, v14, v22
	v_pk_add_f16 v15, v15, v23
	v_pk_add_f16 v16, v16, v24
	v_pk_add_f16 v17, v17, v25
	v_pk_fma_f16 v10, v82, v22, v10
	v_pk_fma_f16 v11, v83, v23, v11
	v_pk_fma_f16 v12, v84, v24, v12
	v_pk_fma_f16 v13, v85, v25, v13
	v_pk_add_f16 v19, v72, v51
	v_pk_add_f16 v20, v71, v52
	v_pk_add_f16 v21, v70, v53
	s_nop 0
	v_exp_f16_sdwa v22, v18 dst_sel:WORD_0 dst_unused:UNUSED_PAD src0_sel:WORD_0
	v_exp_f16_sdwa v23, v19 dst_sel:WORD_0 dst_unused:UNUSED_PAD src0_sel:WORD_0
	v_exp_f16_sdwa v24, v20 dst_sel:WORD_0 dst_unused:UNUSED_PAD src0_sel:WORD_0
	v_exp_f16_sdwa v25, v21 dst_sel:WORD_0 dst_unused:UNUSED_PAD src0_sel:WORD_0
	v_exp_f16_sdwa v22, v18 dst_sel:WORD_1 dst_unused:UNUSED_PRESERVE src0_sel:WORD_1
	v_exp_f16_sdwa v23, v19 dst_sel:WORD_1 dst_unused:UNUSED_PRESERVE src0_sel:WORD_1
	v_exp_f16_sdwa v24, v20 dst_sel:WORD_1 dst_unused:UNUSED_PRESERVE src0_sel:WORD_1
	v_exp_f16_sdwa v25, v21 dst_sel:WORD_1 dst_unused:UNUSED_PRESERVE src0_sel:WORD_1
	s_nop 0
	s_nop 0
	v_pk_add_f16 v17, v17, v25
	v_pk_add_f16 v16, v16, v24
	v_pk_add_f16 v15, v15, v23
	v_pk_add_f16 v14, v14, v22
	v_pk_fma_f16 v21, v105, v25, v13
	v_pk_fma_f16 v20, v104, v24, v12
	v_pk_fma_f16 v19, v103, v23, v11
	v_pk_fma_f16 v18, v102, v22, v10
	v_mov_b32_e32 v13, v5
	v_mov_b32_e32 v12, v4
	v_mov_b32_e32 v11, v3
	v_mov_b32_e32 v10, v2
	v_exp_f16_sdwa v22, v6 dst_sel:WORD_0 dst_unused:UNUSED_PAD src0_sel:WORD_0
	v_exp_f16_sdwa v23, v7 dst_sel:WORD_0 dst_unused:UNUSED_PAD src0_sel:WORD_0
	v_exp_f16_sdwa v24, v8 dst_sel:WORD_0 dst_unused:UNUSED_PAD src0_sel:WORD_0
	v_exp_f16_sdwa v25, v9 dst_sel:WORD_0 dst_unused:UNUSED_PAD src0_sel:WORD_0
	v_exp_f16_sdwa v22, v6 dst_sel:WORD_1 dst_unused:UNUSED_PRESERVE src0_sel:WORD_1
	v_exp_f16_sdwa v23, v7 dst_sel:WORD_1 dst_unused:UNUSED_PRESERVE src0_sel:WORD_1
	v_exp_f16_sdwa v24, v8 dst_sel:WORD_1 dst_unused:UNUSED_PRESERVE src0_sel:WORD_1
	v_exp_f16_sdwa v25, v9 dst_sel:WORD_1 dst_unused:UNUSED_PRESERVE src0_sel:WORD_1
	s_nop 0

.LBB4_4:
	global_load_dwordx4 v[2:5], v[170:171], off
	global_load_dwordx4 v[8:11], v[172:173], off
	global_load_dwordx4 v[22:25], v[170:171], off offset:16
	global_load_dwordx4 v[26:29], v[172:173], off offset:16
	s_lshl_b32 s48, s46, 3
	s_add_i32 s48, s48, s44
	v_or_b32_e32 v199, s48, v178
	v_add_u32_e32 v168, v199, v181
	v_add_u32_e32 v201, -1, v199
	v_mul_lo_u32 v6, v168, s47
	v_or_b32_e32 v7, v201, v182
	v_or_b32_e32 v6, v6, v166
	s_mov_b64 s[4:5], -1
	s_and_b64 vcc, exec, s[26:27]
	v_cmp_gt_u32_e64 s[2:3], 64, v7
	v_lshlrev_b32_e32 v200, 1, v6
	s_waitcnt vmcnt(3)
	v_cvt_pk_f16_f32 v6, v2, v3
	s_waitcnt vmcnt(2)
	v_cvt_pk_f16_f32 v2, v8, v9
	v_cvt_pk_f16_f32 v7, v4, v5
	v_cvt_pk_f16_f32 v3, v10, v11
	s_waitcnt vmcnt(1)
	v_cvt_pk_f16_f32 v8, v22, v23
	s_waitcnt vmcnt(0)
	v_cvt_pk_f16_f32 v4, v26, v27
	v_cvt_pk_f16_f32 v9, v24, v25
	v_cvt_pk_f16_f32 v5, v28, v29
	s_cbranch_vccz .LBB4_42
	global_load_dwordx3 v[154:156], v169, s[10:11]
	v_cmp_lt_u32_e64 s[64:65], 0, v199
	v_cmp_gt_u32_e64 s[66:67], 63, v199
	v_cmp_lt_u32_e64 s[68:69], 0, v180
	v_cmp_gt_u32_e64 s[70:71], 60, v180
	buffer_load_dwordx4 v[206:209], v200, s[36:39], 0 offen
	v_add_u32_e32 v246, 0x18000, v200
	buffer_load_dwordx4 v[162:165], v246, s[36:39], 0 offen
	v_add_u32_e32 v245, 0x30000, v200
	buffer_load_dwordx4 v[158:161], v245, s[36:39], 0 offen
	s_and_b64 s[72:73], s[68:69], s[64:65]
	s_and_b64 s[74:75], s[68:69], s[66:67]
	s_and_b64 s[76:77], s[70:71], s[64:65]
	s_and_b64 s[78:79], s[70:71], s[66:67]
	v_add_u32_e32 v245, 0xfffe7c00, v200
	v_add_u32_e32 v246, 0xfffe8000, v200
	v_mov_b32_e32 v122, v6
	v_mov_b32_e32 v123, v7
	v_mov_b32_e32 v124, v8
	v_mov_b32_e32 v125, v9
	v_mov_b32_e32 v82, v2
	v_mov_b32_e32 v83, v3
	v_mov_b32_e32 v84, v4
	v_mov_b32_e32 v85, v5
	v_mov_b32_e32 v138, v6
	v_mov_b32_e32 v139, v7
	v_mov_b32_e32 v140, v8
	v_mov_b32_e32 v141, v9
	v_mov_b32_e32 v106, v2
	v_mov_b32_e32 v107, v3
	v_mov_b32_e32 v108, v4
	v_mov_b32_e32 v109, v5
	v_mov_b32_e32 v146, v6
	v_mov_b32_e32 v147, v7
	v_mov_b32_e32 v148, v8
	v_mov_b32_e32 v149, v9
	v_mov_b32_e32 v126, v2
	v_mov_b32_e32 v127, v3
	v_mov_b32_e32 v128, v4
	v_mov_b32_e32 v129, v5
	s_mov_b64 exec, s[72:73]
	buffer_load_dwordx4 v[122:125], v245, s[36:39], 0 offen
	buffer_load_dwordx4 v[82:85], v245, s[36:39], 0 offen offset:512
	s_mov_b64 exec, -1
	s_mov_b64 exec, s[68:69]
	buffer_load_dwordx4 v[138:141], v246, s[36:39], 0 offen offset:512
	buffer_load_dwordx4 v[106:109], v246, s[36:39], 0 offen offset:1024
	s_mov_b64 exec, -1
	s_mov_b64 exec, s[74:75]
	buffer_load_dwordx4 v[146:149], v246, s[36:39], 0 offen offset:2048
	buffer_load_dwordx4 v[126:129], v246, s[36:39], 0 offen offset:2560
	s_mov_b64 exec, -1
	v_add_u32_e32 v245, 0xfffffc00, v200
	v_mov_b32_e32 v94, v6
	v_mov_b32_e32 v95, v7
	v_mov_b32_e32 v96, v8
	v_mov_b32_e32 v97, v9
	v_mov_b32_e32 v54, v2
	v_mov_b32_e32 v55, v3
	v_mov_b32_e32 v56, v4
	v_mov_b32_e32 v57, v5
	v_mov_b32_e32 v134, v6
	v_mov_b32_e32 v135, v7
	v_mov_b32_e32 v136, v8
	v_mov_b32_e32 v137, v9
	v_mov_b32_e32 v98, v2
	v_mov_b32_e32 v99, v3
	v_mov_b32_e32 v100, v4
	v_mov_b32_e32 v101, v5
	s_mov_b64 exec, s[64:65]
	buffer_load_dwordx4 v[94:97], v245, s[36:39], 0 offen
	buffer_load_dwordx4 v[54:57], v245, s[36:39], 0 offen offset:512
	s_mov_b64 exec, -1
	buffer_load_dwordx4 v[118:121], v200, s[36:39], 0 offen offset:512
	buffer_load_dwordx4 v[74:77], v200, s[36:39], 0 offen offset:1024
	s_mov_b64 exec, s[66:67]
	buffer_load_dwordx4 v[134:137], v200, s[36:39], 0 offen offset:2048
	buffer_load_dwordx4 v[98:101], v200, s[36:39], 0 offen offset:2560
	s_mov_b64 exec, -1
	v_add_u32_e32 v245, 0x17c00, v200
	v_add_u32_e32 v246, 0x18000, v200
	v_mov_b32_e32 v62, v6
	v_mov_b32_e32 v63, v7
	v_mov_b32_e32 v64, v8
	v_mov_b32_e32 v65, v9
	v_mov_b32_e32 v30, v2
	v_mov_b32_e32 v31, v3
	v_mov_b32_e32 v32, v4
	v_mov_b32_e32 v33, v5
	v_mov_b32_e32 v102, v6
	v_mov_b32_e32 v103, v7
	v_mov_b32_e32 v104, v8
	v_mov_b32_e32 v105, v9
	v_mov_b32_e32 v58, v2
	v_mov_b32_e32 v59, v3
	v_mov_b32_e32 v60, v4
	v_mov_b32_e32 v61, v5
	s_mov_b64 exec, s[64:65]
	buffer_load_dwordx4 v[62:65], v245, s[36:39], 0 offen
	buffer_load_dwordx4 v[30:33], v245, s[36:39], 0 offen offset:512
	s_mov_b64 exec, -1
	buffer_load_dwordx4 v[78:81], v246, s[36:39], 0 offen offset:512
	buffer_load_dwordx4 v[42:45], v246, s[36:39], 0 offen offset:1024
	s_mov_b64 exec, s[66:67]
	buffer_load_dwordx4 v[102:105], v246, s[36:39], 0 offen offset:2048
	buffer_load_dwordx4 v[58:61], v246, s[36:39], 0 offen offset:2560
	s_mov_b64 exec, -1
	v_add_u32_e32 v245, 0x2fc00, v200
	v_add_u32_e32 v246, 0x30000, v200
	v_mov_b32_e32 v34, v6
	v_mov_b32_e32 v35, v7
	v_mov_b32_e32 v36, v8
	v_mov_b32_e32 v37, v9
	v_mov_b32_e32 v18, v2
	v_mov_b32_e32 v19, v3
	v_mov_b32_e32 v20, v4
	v_mov_b32_e32 v21, v5
	v_mov_b32_e32 v66, v6
	v_mov_b32_e32 v67, v7
	v_mov_b32_e32 v68, v8
	v_mov_b32_e32 v69, v9
	v_mov_b32_e32 v26, v2
	v_mov_b32_e32 v27, v3
	v_mov_b32_e32 v28, v4
	v_mov_b32_e32 v29, v5
	s_mov_b64 exec, s[64:65]
	buffer_load_dwordx4 v[34:37], v245, s[36:39], 0 offen
	buffer_load_dwordx4 v[18:21], v245, s[36:39], 0 offen offset:512
	s_mov_b64 exec, -1
	buffer_load_dwordx4 v[46:49], v246, s[36:39], 0 offen offset:512
	buffer_load_dwordx4 v[22:25], v246, s[36:39], 0 offen offset:1024
	s_mov_b64 exec, s[66:67]
	buffer_load_dwordx4 v[66:69], v246, s[36:39], 0 offen offset:2048
	buffer_load_dwordx4 v[26:29], v246, s[36:39], 0 offen offset:2560
	s_mov_b64 exec, -1
	v_add_u32_e32 v245, 0x47c00, v200
	v_add_u32_e32 v246, 0x48000, v200
	v_mov_b32_e32 v86, v6
	v_mov_b32_e32 v87, v7
	v_mov_b32_e32 v88, v8
	v_mov_b32_e32 v89, v9
	v_mov_b32_e32 v38, v2
	v_mov_b32_e32 v39, v3
	v_mov_b32_e32 v40, v4
	v_mov_b32_e32 v41, v5
	v_mov_b32_e32 v130, v6
	v_mov_b32_e32 v131, v7
	v_mov_b32_e32 v132, v8
	v_mov_b32_e32 v133, v9
	v_mov_b32_e32 v70, v2
	v_mov_b32_e32 v71, v3
	v_mov_b32_e32 v72, v4
	v_mov_b32_e32 v73, v5
	s_mov_b64 exec, s[64:65]
	buffer_load_dwordx4 v[86:89], v245, s[36:39], 0 offen
	buffer_load_dwordx4 v[38:41], v245, s[36:39], 0 offen offset:512
	s_mov_b64 exec, -1
	buffer_load_dwordx4 v[114:117], v246, s[36:39], 0 offen offset:512
	buffer_load_dwordx4 v[50:53], v246, s[36:39], 0 offen offset:1024
	s_mov_b64 exec, s[66:67]
	buffer_load_dwordx4 v[130:133], v246, s[36:39], 0 offen offset:2048
	buffer_load_dwordx4 v[70:73], v246, s[36:39], 0 offen offset:2560
	s_mov_b64 exec, -1
	v_add_u32_e32 v245, 0x5fc00, v200
	v_add_u32_e32 v246, 0x60000, v200
	v_mov_b32_e32 v142, v6
	v_mov_b32_e32 v143, v7
	v_mov_b32_e32 v144, v8
	v_mov_b32_e32 v145, v9
	v_mov_b32_e32 v90, v2
	v_mov_b32_e32 v91, v3
	v_mov_b32_e32 v92, v4
	v_mov_b32_e32 v93, v5
	v_mov_b32_e32 v150, v6
	v_mov_b32_e32 v151, v7
	v_mov_b32_e32 v152, v8
	v_mov_b32_e32 v153, v9
	v_mov_b32_e32 v110, v2
	v_mov_b32_e32 v111, v3
	v_mov_b32_e32 v112, v4
	v_mov_b32_e32 v113, v5
	v_mov_b32_e32 v14, v6
	v_mov_b32_e32 v15, v7
	v_mov_b32_e32 v16, v8
	v_mov_b32_e32 v17, v9
	v_mov_b32_e32 v10, v2
	v_mov_b32_e32 v11, v3
	v_mov_b32_e32 v12, v4
	v_mov_b32_e32 v13, v5
	s_mov_b64 exec, s[76:77]
	buffer_load_dwordx4 v[142:145], v245, s[36:39], 0 offen
	buffer_load_dwordx4 v[90:93], v245, s[36:39], 0 offen offset:512
	s_mov_b64 exec, -1
	s_mov_b64 exec, s[70:71]
	buffer_load_dwordx4 v[150:153], v246, s[36:39], 0 offen offset:512
	buffer_load_dwordx4 v[110:113], v246, s[36:39], 0 offen offset:1024
	s_mov_b64 exec, -1
	s_mov_b64 exec, s[78:79]
	buffer_load_dwordx4 v[14:17], v246, s[36:39], 0 offen offset:2048
	buffer_load_dwordx4 v[10:13], v246, s[36:39], 0 offen offset:2560
	s_mov_b64 exec, -1
	s_waitcnt vmcnt(39)
	v_cvt_f16_f32_e32 v202, v155
	v_cvt_f16_f32_e32 v204, v154
	v_cvt_f16_f32_e32 v203, v156
	v_add_u32_e32 v245, 0x48000, v200
	buffer_load_dwordx4 v[154:157], v245, s[36:39], 0 offen
	s_mov_b64 s[4:5], 0
	s_waitcnt vmcnt(19)
	v_pk_mul_f16 v212, v204, v209 op_sel_hi:[0,1]
	v_pk_mul_f16 v216, v202, v209 op_sel_hi:[0,1]
	v_pk_mul_f16 v220, v203, v209 op_sel_hi:[0,1]
	v_pk_mul_f16 v205, v204, v206 op_sel_hi:[0,1]
	v_pk_mul_f16 v210, v204, v207 op_sel_hi:[0,1]
	v_pk_mul_f16 v211, v204, v208 op_sel_hi:[0,1]
	v_pk_mul_f16 v213, v202, v206 op_sel_hi:[0,1]
	v_pk_mul_f16 v214, v202, v207 op_sel_hi:[0,1]
	v_pk_mul_f16 v215, v202, v208 op_sel_hi:[0,1]
	v_pk_mul_f16 v217, v203, v206 op_sel_hi:[0,1]
	v_pk_mul_f16 v218, v203, v207 op_sel_hi:[0,1]
	v_pk_mul_f16 v219, v203, v208 op_sel_hi:[0,1]
	v_pk_fma_f16 v125, v125, v209, v212
	v_pk_fma_f16 v141, v141, v209, v216
	v_pk_fma_f16 v149, v149, v209, v220
	v_pk_fma_f16 v221, v97, v209, v212
	v_pk_fma_f16 v225, v121, v209, v216
	v_pk_fma_f16 v229, v137, v209, v220
	v_pk_fma_f16 v212, v65, v209, v212
	v_pk_fma_f16 v216, v81, v209, v216
	v_pk_fma_f16 v209, v105, v209, v220
	v_pk_maximum3_f16 v220, v125, v141, v149
	v_pk_fma_f16 v124, v124, v208, v211
	v_pk_fma_f16 v123, v123, v207, v210
	v_pk_fma_f16 v122, v122, v206, v205
	v_pk_fma_f16 v140, v140, v208, v215
	v_pk_fma_f16 v139, v139, v207, v214
	v_pk_fma_f16 v138, v138, v206, v213
	v_pk_fma_f16 v148, v148, v208, v219
	v_pk_fma_f16 v147, v147, v207, v218
	v_pk_fma_f16 v146, v146, v206, v217
	v_pk_fma_f16 v222, v96, v208, v211
	v_pk_fma_f16 v223, v95, v207, v210
	v_pk_fma_f16 v224, v94, v206, v205
	v_pk_fma_f16 v226, v120, v208, v215
	v_pk_fma_f16 v227, v119, v207, v214
	v_pk_fma_f16 v228, v118, v206, v213
	v_pk_fma_f16 v230, v136, v208, v219
	v_pk_fma_f16 v231, v135, v207, v218
	v_pk_fma_f16 v232, v134, v206, v217
	v_pk_fma_f16 v211, v64, v208, v211
	v_pk_fma_f16 v210, v63, v207, v210
	v_pk_fma_f16 v205, v62, v206, v205
	v_pk_fma_f16 v215, v80, v208, v215
	v_pk_fma_f16 v214, v79, v207, v214
	v_pk_fma_f16 v213, v78, v206, v213
	v_pk_fma_f16 v208, v104, v208, v219
	v_pk_fma_f16 v207, v103, v207, v218
	v_pk_fma_f16 v206, v102, v206, v217
	v_pk_maximum3_f16 v217, v122, v138, v146
	v_pk_maximum3_f16 v218, v123, v139, v147
	v_pk_maximum3_f16 v219, v124, v140, v148
	v_pk_maximum3_f16 v236, v221, v225, v229
	v_pk_maximum3_f16 v240, v212, v216, v209
	v_pk_maximum3_f16 v233, v224, v228, v232
	v_pk_maximum3_f16 v234, v223, v227, v231
	v_pk_maximum3_f16 v235, v222, v226, v230
	s_nop 0
	v_pk_maximum3_f16 v237, v205, v213, v206
	v_pk_maximum3_f16 v238, v210, v214, v207
	v_pk_maximum3_f16 v220, v220, v236, v240
	v_pk_maximum3_f16 v239, v211, v215, v208
	s_nop 0
	v_pk_maximum3_f16 v217, v217, v233, v237
	v_pk_maximum3_f16 v218, v218, v234, v238
	v_pk_maximum3_f16 v219, v219, v235, v239
	v_xor_b32_e32 v220, 0x80008000, v220
	v_xor_b32_e32 v219, 0x80008000, v219
	v_xor_b32_e32 v218, 0x80008000, v218
	v_xor_b32_e32 v217, 0x80008000, v217
	v_pk_add_f16 v125, v125, v220
	v_pk_add_f16 v122, v122, v217
	v_pk_add_f16 v123, v123, v218
	v_pk_add_f16 v124, v124, v219
	v_pk_add_f16 v138, v138, v217
	v_exp_f16_sdwa v233, v122 dst_sel:WORD_0 dst_unused:UNUSED_PAD src0_sel:WORD_0
	v_exp_f16_sdwa v234, v123 dst_sel:WORD_0 dst_unused:UNUSED_PAD src0_sel:WORD_0
	v_exp_f16_sdwa v235, v124 dst_sel:WORD_0 dst_unused:UNUSED_PAD src0_sel:WORD_0
	v_exp_f16_sdwa v236, v125 dst_sel:WORD_0 dst_unused:UNUSED_PAD src0_sel:WORD_0
	v_exp_f16_sdwa v233, v122 dst_sel:WORD_1 dst_unused:UNUSED_PRESERVE src0_sel:WORD_1
	v_exp_f16_sdwa v234, v123 dst_sel:WORD_1 dst_unused:UNUSED_PRESERVE src0_sel:WORD_1
	v_exp_f16_sdwa v235, v124 dst_sel:WORD_1 dst_unused:UNUSED_PRESERVE src0_sel:WORD_1
	v_exp_f16_sdwa v236, v125 dst_sel:WORD_1 dst_unused:UNUSED_PRESERVE src0_sel:WORD_1
	s_nop 0
	v_pk_add_f16 v139, v139, v218
	v_pk_add_f16 v125, v233, 0
	v_pk_fma_f16 v85, v85, v236, 0
	v_pk_add_f16 v122, v236, 0
	v_pk_add_f16 v123, v235, 0
	v_pk_add_f16 v124, v234, 0
	v_pk_fma_f16 v84, v84, v235, 0
	v_pk_fma_f16 v83, v83, v234, 0
	v_pk_fma_f16 v82, v82, v233, 0
	v_pk_add_f16 v140, v140, v219
	v_pk_add_f16 v141, v141, v220
	s_nop 0
	v_exp_f16_sdwa v233, v138 dst_sel:WORD_0 dst_unused:UNUSED_PAD src0_sel:WORD_0
	v_exp_f16_sdwa v234, v139 dst_sel:WORD_0 dst_unused:UNUSED_PAD src0_sel:WORD_0
	v_exp_f16_sdwa v235, v140 dst_sel:WORD_0 dst_unused:UNUSED_PAD src0_sel:WORD_0
	v_exp_f16_sdwa v236, v141 dst_sel:WORD_0 dst_unused:UNUSED_PAD src0_sel:WORD_0
	v_exp_f16_sdwa v233, v138 dst_sel:WORD_1 dst_unused:UNUSED_PRESERVE src0_sel:WORD_1
	v_exp_f16_sdwa v234, v139 dst_sel:WORD_1 dst_unused:UNUSED_PRESERVE src0_sel:WORD_1
	v_exp_f16_sdwa v235, v140 dst_sel:WORD_1 dst_unused:UNUSED_PRESERVE src0_sel:WORD_1
	v_exp_f16_sdwa v236, v141 dst_sel:WORD_1 dst_unused:UNUSED_PRESERVE src0_sel:WORD_1
	s_nop 0
	s_nop 0
	v_pk_add_f16 v125, v125, v233
	v_pk_fma_f16 v85, v109, v236, v85
	v_pk_add_f16 v109, v149, v220
	v_pk_add_f16 v124, v124, v234
	v_pk_add_f16 v123, v123, v235
	v_pk_add_f16 v122, v122, v236
	v_pk_fma_f16 v82, v106, v233, v82
	v_pk_fma_f16 v83, v107, v234, v83
	v_pk_fma_f16 v84, v108, v235, v84
	v_pk_add_f16 v106, v146, v217
	v_pk_add_f16 v107, v147, v218
	v_pk_add_f16 v108, v148, v219
	s_nop 0
	v_exp_f16_sdwa v138, v106 dst_sel:WORD_0 dst_unused:UNUSED_PAD src0_sel:WORD_0
	v_exp_f16_sdwa v139, v107 dst_sel:WORD_0 dst_unused:UNUSED_PAD src0_sel:WORD_0
	v_exp_f16_sdwa v140, v108 dst_sel:WORD_0 dst_unused:UNUSED_PAD src0_sel:WORD_0
	v_exp_f16_sdwa v141, v109 dst_sel:WORD_0 dst_unused:UNUSED_PAD src0_sel:WORD_0
	v_exp_f16_sdwa v138, v106 dst_sel:WORD_1 dst_unused:UNUSED_PRESERVE src0_sel:WORD_1
	v_exp_f16_sdwa v139, v107 dst_sel:WORD_1 dst_unused:UNUSED_PRESERVE src0_sel:WORD_1
	v_exp_f16_sdwa v140, v108 dst_sel:WORD_1 dst_unused:UNUSED_PRESERVE src0_sel:WORD_1
	v_exp_f16_sdwa v141, v109 dst_sel:WORD_1 dst_unused:UNUSED_PRESERVE src0_sel:WORD_1
	s_nop 0
	s_nop 0
	v_pk_add_f16 v109, v125, v138
	v_pk_add_f16 v106, v122, v141
	v_pk_add_f16 v107, v123, v140
	v_pk_add_f16 v108, v124, v139
	v_pk_fma_f16 v85, v129, v141, v85
	v_pk_fma_f16 v84, v128, v140, v84
	v_pk_fma_f16 v83, v127, v139, v83
	v_pk_fma_f16 v82, v126, v138, v82
	v_pk_add_f16 v122, v224, v217
	v_pk_add_f16 v123, v223, v218
	v_pk_add_f16 v124, v222, v219
	v_pk_add_f16 v125, v221, v220
	s_nop 0
	v_exp_f16_sdwa v126, v122 dst_sel:WORD_0 dst_unused:UNUSED_PAD src0_sel:WORD_0
	v_exp_f16_sdwa v127, v123 dst_sel:WORD_0 dst_unused:UNUSED_PAD src0_sel:WORD_0
	v_exp_f16_sdwa v128, v124 dst_sel:WORD_0 dst_unused:UNUSED_PAD src0_sel:WORD_0
	v_exp_f16_sdwa v129, v125 dst_sel:WORD_0 dst_unused:UNUSED_PAD src0_sel:WORD_0
	v_exp_f16_sdwa v126, v122 dst_sel:WORD_1 dst_unused:UNUSED_PRESERVE src0_sel:WORD_1
	v_exp_f16_sdwa v127, v123 dst_sel:WORD_1 dst_unused:UNUSED_PRESERVE src0_sel:WORD_1
	v_exp_f16_sdwa v128, v124 dst_sel:WORD_1 dst_unused:UNUSED_PRESERVE src0_sel:WORD_1
	v_exp_f16_sdwa v129, v125 dst_sel:WORD_1 dst_unused:UNUSED_PRESERVE src0_sel:WORD_1
	s_nop 0
	v_pk_add_f16 v122, v228, v217
	v_pk_add_f16 v109, v109, v126
	v_pk_add_f16 v108, v108, v127
	v_pk_add_f16 v107, v107, v128
	v_pk_add_f16 v106, v106, v129
	v_pk_fma_f16 v82, v54, v126, v82
	v_pk_fma_f16 v83, v55, v127, v83
	v_pk_fma_f16 v84, v56, v128, v84
	v_pk_fma_f16 v85, v57, v129, v85
	v_pk_add_f16 v123, v227, v218
	v_pk_add_f16 v124, v226, v219
	v_pk_add_f16 v125, v225, v220
	s_nop 0
	v_exp_f16_sdwa v126, v122 dst_sel:WORD_0 dst_unused:UNUSED_PAD src0_sel:WORD_0
	v_exp_f16_sdwa v127, v123 dst_sel:WORD_0 dst_unused:UNUSED_PAD src0_sel:WORD_0
	v_exp_f16_sdwa v128, v124 dst_sel:WORD_0 dst_unused:UNUSED_PAD src0_sel:WORD_0
	v_exp_f16_sdwa v129, v125 dst_sel:WORD_0 dst_unused:UNUSED_PAD src0_sel:WORD_0
	v_exp_f16_sdwa v126, v122 dst_sel:WORD_1 dst_unused:UNUSED_PRESERVE src0_sel:WORD_1
	v_exp_f16_sdwa v127, v123 dst_sel:WORD_1 dst_unused:UNUSED_PRESERVE src0_sel:WORD_1
	v_exp_f16_sdwa v128, v124 dst_sel:WORD_1 dst_unused:UNUSED_PRESERVE src0_sel:WORD_1
	v_exp_f16_sdwa v129, v125 dst_sel:WORD_1 dst_unused:UNUSED_PRESERVE src0_sel:WORD_1
	s_nop 0
	v_pk_add_f16 v122, v232, v217
	v_pk_add_f16 v109, v109, v126
	v_pk_add_f16 v106, v106, v129
	v_pk_add_f16 v107, v107, v128
	v_pk_add_f16 v108, v108, v127
	v_pk_fma_f16 v85, v77, v129, v85
	v_pk_fma_f16 v84, v76, v128, v84
	v_pk_fma_f16 v83, v75, v127, v83
	v_pk_fma_f16 v82, v74, v126, v82
	v_pk_add_f16 v123, v231, v218
	v_pk_add_f16 v124, v230, v219
	v_pk_add_f16 v125, v229, v220
	s_nop 0
	v_exp_f16_sdwa v126, v122 dst_sel:WORD_0 dst_unused:UNUSED_PAD src0_sel:WORD_0
	v_exp_f16_sdwa v127, v123 dst_sel:WORD_0 dst_unused:UNUSED_PAD src0_sel:WORD_0
	v_exp_f16_sdwa v128, v124 dst_sel:WORD_0 dst_unused:UNUSED_PAD src0_sel:WORD_0
	v_exp_f16_sdwa v129, v125 dst_sel:WORD_0 dst_unused:UNUSED_PAD src0_sel:WORD_0
	v_exp_f16_sdwa v126, v122 dst_sel:WORD_1 dst_unused:UNUSED_PRESERVE src0_sel:WORD_1
	v_exp_f16_sdwa v127, v123 dst_sel:WORD_1 dst_unused:UNUSED_PRESERVE src0_sel:WORD_1
	v_exp_f16_sdwa v128, v124 dst_sel:WORD_1 dst_unused:UNUSED_PRESERVE src0_sel:WORD_1
	v_exp_f16_sdwa v129, v125 dst_sel:WORD_1 dst_unused:UNUSED_PRESERVE src0_sel:WORD_1
	s_nop 0
	v_pk_add_f16 v122, v205, v217
	v_pk_add_f16 v109, v109, v126
	v_pk_add_f16 v108, v108, v127
	v_pk_add_f16 v107, v107, v128
	v_pk_add_f16 v106, v106, v129
	v_pk_fma_f16 v82, v98, v126, v82
	v_pk_fma_f16 v83, v99, v127, v83
	v_pk_fma_f16 v84, v100, v128, v84
	v_pk_fma_f16 v85, v101, v129, v85
	v_pk_add_f16 v123, v210, v218
	v_pk_add_f16 v124, v211, v219
	v_pk_add_f16 v125, v212, v220
	s_nop 0
	v_exp_f16_sdwa v126, v122 dst_sel:WORD_0 dst_unused:UNUSED_PAD src0_sel:WORD_0
	v_exp_f16_sdwa v127, v123 dst_sel:WORD_0 dst_unused:UNUSED_PAD src0_sel:WORD_0
	v_exp_f16_sdwa v128, v124 dst_sel:WORD_0 dst_unused:UNUSED_PAD src0_sel:WORD_0
	v_exp_f16_sdwa v129, v125 dst_sel:WORD_0 dst_unused:UNUSED_PAD src0_sel:WORD_0
	v_exp_f16_sdwa v126, v122 dst_sel:WORD_1 dst_unused:UNUSED_PRESERVE src0_sel:WORD_1
	v_exp_f16_sdwa v127, v123 dst_sel:WORD_1 dst_unused:UNUSED_PRESERVE src0_sel:WORD_1
	v_exp_f16_sdwa v128, v124 dst_sel:WORD_1 dst_unused:UNUSED_PRESERVE src0_sel:WORD_1
	v_exp_f16_sdwa v129, v125 dst_sel:WORD_1 dst_unused:UNUSED_PRESERVE src0_sel:WORD_1
	s_nop 0
	v_pk_add_f16 v122, v213, v217
	v_pk_add_f16 v109, v109, v126
	v_pk_add_f16 v106, v106, v129
	v_pk_add_f16 v107, v107, v128
	v_pk_add_f16 v108, v108, v127
	v_pk_fma_f16 v85, v33, v129, v85
	v_pk_fma_f16 v84, v32, v128, v84
	v_pk_fma_f16 v83, v31, v127, v83
	v_pk_fma_f16 v82, v30, v126, v82
	v_pk_add_f16 v123, v214, v218
	v_pk_add_f16 v124, v215, v219
	v_pk_add_f16 v125, v216, v220
	s_nop 0
	v_exp_f16_sdwa v126, v122 dst_sel:WORD_0 dst_unused:UNUSED_PAD src0_sel:WORD_0
	v_exp_f16_sdwa v127, v123 dst_sel:WORD_0 dst_unused:UNUSED_PAD src0_sel:WORD_0
	v_exp_f16_sdwa v128, v124 dst_sel:WORD_0 dst_unused:UNUSED_PAD src0_sel:WORD_0
	v_exp_f16_sdwa v129, v125 dst_sel:WORD_0 dst_unused:UNUSED_PAD src0_sel:WORD_0
	v_exp_f16_sdwa v126, v122 dst_sel:WORD_1 dst_unused:UNUSED_PRESERVE src0_sel:WORD_1
	v_exp_f16_sdwa v127, v123 dst_sel:WORD_1 dst_unused:UNUSED_PRESERVE src0_sel:WORD_1
	v_exp_f16_sdwa v128, v124 dst_sel:WORD_1 dst_unused:UNUSED_PRESERVE src0_sel:WORD_1
	v_exp_f16_sdwa v129, v125 dst_sel:WORD_1 dst_unused:UNUSED_PRESERVE src0_sel:WORD_1
	s_nop 0
	v_pk_add_f16 v122, v206, v217
	v_pk_add_f16 v109, v109, v126
	v_pk_add_f16 v108, v108, v127
	v_pk_add_f16 v107, v107, v128
	v_pk_add_f16 v106, v106, v129
	v_pk_fma_f16 v82, v42, v126, v82
	v_pk_fma_f16 v83, v43, v127, v83
	v_pk_fma_f16 v84, v44, v128, v84
	v_pk_fma_f16 v85, v45, v129, v85
	v_pk_add_f16 v123, v207, v218
	v_pk_add_f16 v124, v208, v219
	v_pk_add_f16 v125, v209, v220
	s_nop 0
	v_exp_f16_sdwa v126, v122 dst_sel:WORD_0 dst_unused:UNUSED_PAD src0_sel:WORD_0
	v_exp_f16_sdwa v127, v123 dst_sel:WORD_0 dst_unused:UNUSED_PAD src0_sel:WORD_0
	v_exp_f16_sdwa v128, v124 dst_sel:WORD_0 dst_unused:UNUSED_PAD src0_sel:WORD_0
	v_exp_f16_sdwa v129, v125 dst_sel:WORD_0 dst_unused:UNUSED_PAD src0_sel:WORD_0
	v_exp_f16_sdwa v126, v122 dst_sel:WORD_1 dst_unused:UNUSED_PRESERVE src0_sel:WORD_1
	v_exp_f16_sdwa v127, v123 dst_sel:WORD_1 dst_unused:UNUSED_PRESERVE src0_sel:WORD_1
	v_exp_f16_sdwa v128, v124 dst_sel:WORD_1 dst_unused:UNUSED_PRESERVE src0_sel:WORD_1
	v_exp_f16_sdwa v129, v125 dst_sel:WORD_1 dst_unused:UNUSED_PRESERVE src0_sel:WORD_1
	s_nop 0
	s_nop 0
	v_pk_add_f16 v109, v109, v126
	v_pk_add_f16 v108, v108, v127
	v_rcp_f16_e32 v122, v109
	v_rcp_f16_sdwa v109, v109 dst_sel:DWORD dst_unused:UNUSED_PAD src0_sel:WORD_1
	v_pk_add_f16 v107, v107, v128
	v_rcp_f16_e32 v123, v108
	v_rcp_f16_sdwa v108, v108 dst_sel:DWORD dst_unused:UNUSED_PAD src0_sel:WORD_1
	v_pk_add_f16 v106, v106, v129
	v_rcp_f16_e32 v124, v107
	v_rcp_f16_sdwa v107, v107 dst_sel:DWORD dst_unused:UNUSED_PAD src0_sel:WORD_1
	v_rcp_f16_e32 v125, v106
	v_rcp_f16_sdwa v106, v106 dst_sel:DWORD dst_unused:UNUSED_PAD src0_sel:WORD_1
	v_pk_fma_f16 v82, v58, v126, v82
	v_pack_b32_f16 v109, v122, v109
	v_pk_fma_f16 v83, v59, v127, v83
	v_pk_mul_f16 v138, v82, v109
	v_pack_b32_f16 v82, v123, v108
	v_pk_fma_f16 v84, v60, v128, v84
	v_pk_mul_f16 v139, v83, v82
	v_pack_b32_f16 v82, v124, v107
	v_pk_fma_f16 v85, v61, v129, v85
	v_pk_mul_f16 v140, v84, v82
	v_pack_b32_f16 v82, v125, v106
	v_pk_mul_f16 v141, v85, v82
	s_waitcnt vmcnt(13)
	v_pk_mul_f16 v85, v204, v165 op_sel_hi:[0,1]
	v_pk_mul_f16 v109, v202, v165 op_sel_hi:[0,1]
	v_pk_mul_f16 v122, v203, v162 op_sel_hi:[0,1]
	v_pk_mul_f16 v125, v203, v165 op_sel_hi:[0,1]
	v_pk_mul_f16 v82, v204, v162 op_sel_hi:[0,1]
	v_pk_mul_f16 v83, v204, v163 op_sel_hi:[0,1]
	v_pk_mul_f16 v84, v204, v164 op_sel_hi:[0,1]
	v_pk_mul_f16 v106, v202, v162 op_sel_hi:[0,1]
	v_pk_mul_f16 v107, v202, v163 op_sel_hi:[0,1]
	v_pk_mul_f16 v108, v202, v164 op_sel_hi:[0,1]
	v_pk_mul_f16 v123, v203, v163 op_sel_hi:[0,1]
	v_pk_mul_f16 v124, v203, v164 op_sel_hi:[0,1]
	v_pk_fma_f16 v97, v97, v165, v85
	v_pk_fma_f16 v121, v121, v165, v109
	v_pk_fma_f16 v126, v137, v165, v125
	v_pk_fma_f16 v129, v134, v162, v122
	v_pk_fma_f16 v134, v65, v165, v85
	v_pk_fma_f16 v146, v81, v165, v109
	v_pk_fma_f16 v205, v105, v165, v125
	v_pk_fma_f16 v85, v37, v165, v85
	v_pk_fma_f16 v109, v49, v165, v109
	v_pk_fma_f16 v125, v69, v165, v125
	v_pk_maximum3_f16 v165, v97, v121, v126
	v_pk_fma_f16 v96, v96, v164, v84
	v_pk_fma_f16 v95, v95, v163, v83
	v_pk_fma_f16 v94, v94, v162, v82
	v_pk_fma_f16 v120, v120, v164, v108
	v_pk_fma_f16 v119, v119, v163, v107
	v_pk_fma_f16 v118, v118, v162, v106
	v_pk_fma_f16 v127, v136, v164, v124
	v_pk_fma_f16 v128, v135, v163, v123
	v_pk_fma_f16 v135, v64, v164, v84
	v_pk_fma_f16 v136, v63, v163, v83
	v_pk_fma_f16 v137, v62, v162, v82
	v_pk_fma_f16 v147, v80, v164, v108
	v_pk_fma_f16 v148, v79, v163, v107
	v_pk_fma_f16 v149, v78, v162, v106
	v_pk_fma_f16 v206, v104, v164, v124
	v_pk_fma_f16 v207, v103, v163, v123
	v_pk_fma_f16 v208, v102, v162, v122
	v_pk_fma_f16 v84, v36, v164, v84
	v_pk_fma_f16 v83, v35, v163, v83
	v_pk_fma_f16 v82, v34, v162, v82
	v_pk_fma_f16 v108, v48, v164, v108
	v_pk_fma_f16 v107, v47, v163, v107
	v_pk_fma_f16 v106, v46, v162, v106
	v_pk_fma_f16 v124, v68, v164, v124
	v_pk_fma_f16 v123, v67, v163, v123
	v_pk_fma_f16 v122, v66, v162, v122
	v_pk_maximum3_f16 v162, v94, v118, v129
	v_pk_maximum3_f16 v163, v95, v119, v128
	v_pk_maximum3_f16 v164, v96, v120, v127
	v_pk_maximum3_f16 v212, v134, v146, v205
	v_pk_maximum3_f16 v216, v85, v109, v125
	v_pk_maximum3_f16 v209, v137, v149, v208
	v_pk_maximum3_f16 v210, v136, v148, v207
	v_pk_maximum3_f16 v211, v135, v147, v206
	s_nop 0
	v_pk_maximum3_f16 v213, v82, v106, v122
	v_pk_maximum3_f16 v214, v83, v107, v123
	v_pk_maximum3_f16 v165, v165, v212, v216
	v_pk_maximum3_f16 v215, v84, v108, v124
	s_nop 0
	v_pk_maximum3_f16 v162, v162, v209, v213
	v_pk_maximum3_f16 v163, v163, v210, v214
	v_pk_maximum3_f16 v164, v164, v211, v215
	v_xor_b32_e32 v165, 0x80008000, v165
	v_xor_b32_e32 v164, 0x80008000, v164
	v_xor_b32_e32 v163, 0x80008000, v163
	v_xor_b32_e32 v162, 0x80008000, v162
	v_pk_add_f16 v97, v97, v165
	v_pk_add_f16 v94, v94, v162
	v_pk_add_f16 v95, v95, v163
	v_pk_add_f16 v96, v96, v164
	v_pk_add_f16 v118, v118, v162
	v_exp_f16_sdwa v209, v94 dst_sel:WORD_0 dst_unused:UNUSED_PAD src0_sel:WORD_0
	v_exp_f16_sdwa v210, v95 dst_sel:WORD_0 dst_unused:UNUSED_PAD src0_sel:WORD_0
	v_exp_f16_sdwa v211, v96 dst_sel:WORD_0 dst_unused:UNUSED_PAD src0_sel:WORD_0
	v_exp_f16_sdwa v212, v97 dst_sel:WORD_0 dst_unused:UNUSED_PAD src0_sel:WORD_0
	v_exp_f16_sdwa v209, v94 dst_sel:WORD_1 dst_unused:UNUSED_PRESERVE src0_sel:WORD_1
	v_exp_f16_sdwa v210, v95 dst_sel:WORD_1 dst_unused:UNUSED_PRESERVE src0_sel:WORD_1
	v_exp_f16_sdwa v211, v96 dst_sel:WORD_1 dst_unused:UNUSED_PRESERVE src0_sel:WORD_1
	v_exp_f16_sdwa v212, v97 dst_sel:WORD_1 dst_unused:UNUSED_PRESERVE src0_sel:WORD_1
	s_nop 0
	v_pk_add_f16 v119, v119, v163
	v_pk_add_f16 v97, v209, 0
	v_pk_fma_f16 v57, v57, v212, 0
	v_pk_add_f16 v94, v212, 0
	v_pk_add_f16 v95, v211, 0
	v_pk_add_f16 v96, v210, 0
	v_pk_fma_f16 v56, v56, v211, 0
	v_pk_fma_f16 v55, v55, v210, 0
	v_pk_fma_f16 v54, v54, v209, 0
	v_pk_add_f16 v120, v120, v164
	v_pk_add_f16 v121, v121, v165
	v_pk_add_f16 v82, v82, v162
	v_exp_f16_sdwa v209, v118 dst_sel:WORD_0 dst_unused:UNUSED_PAD src0_sel:WORD_0
	v_exp_f16_sdwa v210, v119 dst_sel:WORD_0 dst_unused:UNUSED_PAD src0_sel:WORD_0
	v_exp_f16_sdwa v211, v120 dst_sel:WORD_0 dst_unused:UNUSED_PAD src0_sel:WORD_0
	v_exp_f16_sdwa v212, v121 dst_sel:WORD_0 dst_unused:UNUSED_PAD src0_sel:WORD_0
	v_exp_f16_sdwa v209, v118 dst_sel:WORD_1 dst_unused:UNUSED_PRESERVE src0_sel:WORD_1
	v_exp_f16_sdwa v210, v119 dst_sel:WORD_1 dst_unused:UNUSED_PRESERVE src0_sel:WORD_1
	v_exp_f16_sdwa v211, v120 dst_sel:WORD_1 dst_unused:UNUSED_PRESERVE src0_sel:WORD_1
	v_exp_f16_sdwa v212, v121 dst_sel:WORD_1 dst_unused:UNUSED_PRESERVE src0_sel:WORD_1
	s_nop 0
	v_pk_add_f16 v83, v83, v163
	v_pk_add_f16 v97, v97, v209
	v_pk_fma_f16 v57, v77, v212, v57
	v_pk_add_f16 v77, v126, v165
	v_pk_add_f16 v96, v96, v210
	v_pk_add_f16 v95, v95, v211
	v_pk_add_f16 v94, v94, v212
	v_pk_fma_f16 v54, v74, v209, v54
	v_pk_fma_f16 v55, v75, v210, v55
	v_pk_fma_f16 v56, v76, v211, v56
	v_pk_add_f16 v74, v129, v162
	v_pk_add_f16 v75, v128, v163
	v_pk_add_f16 v76, v127, v164
	v_pk_add_f16 v84, v84, v164
	v_exp_f16_sdwa v118, v74 dst_sel:WORD_0 dst_unused:UNUSED_PAD src0_sel:WORD_0
	v_exp_f16_sdwa v119, v75 dst_sel:WORD_0 dst_unused:UNUSED_PAD src0_sel:WORD_0
	v_exp_f16_sdwa v120, v76 dst_sel:WORD_0 dst_unused:UNUSED_PAD src0_sel:WORD_0
	v_exp_f16_sdwa v121, v77 dst_sel:WORD_0 dst_unused:UNUSED_PAD src0_sel:WORD_0
	v_exp_f16_sdwa v118, v74 dst_sel:WORD_1 dst_unused:UNUSED_PRESERVE src0_sel:WORD_1
	v_exp_f16_sdwa v119, v75 dst_sel:WORD_1 dst_unused:UNUSED_PRESERVE src0_sel:WORD_1
	v_exp_f16_sdwa v120, v76 dst_sel:WORD_1 dst_unused:UNUSED_PRESERVE src0_sel:WORD_1
	v_exp_f16_sdwa v121, v77 dst_sel:WORD_1 dst_unused:UNUSED_PRESERVE src0_sel:WORD_1
	s_nop 0
	v_pk_add_f16 v85, v85, v165
	v_pk_add_f16 v77, v97, v118
	v_pk_add_f16 v74, v94, v121
	v_pk_add_f16 v75, v95, v120
	v_pk_add_f16 v76, v96, v119
	v_pk_fma_f16 v57, v101, v121, v57
	v_pk_fma_f16 v56, v100, v120, v56
	v_pk_fma_f16 v55, v99, v119, v55
	v_pk_fma_f16 v54, v98, v118, v54
	v_pk_add_f16 v94, v137, v162
	v_pk_add_f16 v95, v136, v163
	v_pk_add_f16 v96, v135, v164
	v_pk_add_f16 v97, v134, v165
	s_nop 0
	v_exp_f16_sdwa v98, v94 dst_sel:WORD_0 dst_unused:UNUSED_PAD src0_sel:WORD_0
	v_exp_f16_sdwa v99, v95 dst_sel:WORD_0 dst_unused:UNUSED_PAD src0_sel:WORD_0
	v_exp_f16_sdwa v100, v96 dst_sel:WORD_0 dst_unused:UNUSED_PAD src0_sel:WORD_0
	v_exp_f16_sdwa v101, v97 dst_sel:WORD_0 dst_unused:UNUSED_PAD src0_sel:WORD_0
	v_exp_f16_sdwa v98, v94 dst_sel:WORD_1 dst_unused:UNUSED_PRESERVE src0_sel:WORD_1
	v_exp_f16_sdwa v99, v95 dst_sel:WORD_1 dst_unused:UNUSED_PRESERVE src0_sel:WORD_1
	v_exp_f16_sdwa v100, v96 dst_sel:WORD_1 dst_unused:UNUSED_PRESERVE src0_sel:WORD_1
	v_exp_f16_sdwa v101, v97 dst_sel:WORD_1 dst_unused:UNUSED_PRESERVE src0_sel:WORD_1
	s_nop 0
	v_pk_add_f16 v94, v149, v162
	v_pk_add_f16 v77, v77, v98
	v_pk_add_f16 v76, v76, v99
	v_pk_add_f16 v75, v75, v100
	v_pk_add_f16 v74, v74, v101
	v_pk_fma_f16 v54, v30, v98, v54
	v_pk_fma_f16 v55, v31, v99, v55
	v_pk_fma_f16 v56, v32, v100, v56
	v_pk_fma_f16 v57, v33, v101, v57
	v_pk_add_f16 v95, v148, v163
	v_pk_add_f16 v96, v147, v164
	v_pk_add_f16 v97, v146, v165
	s_nop 0
	v_exp_f16_sdwa v98, v94 dst_sel:WORD_0 dst_unused:UNUSED_PAD src0_sel:WORD_0
	v_exp_f16_sdwa v99, v95 dst_sel:WORD_0 dst_unused:UNUSED_PAD src0_sel:WORD_0
	v_exp_f16_sdwa v100, v96 dst_sel:WORD_0 dst_unused:UNUSED_PAD src0_sel:WORD_0
	v_exp_f16_sdwa v101, v97 dst_sel:WORD_0 dst_unused:UNUSED_PAD src0_sel:WORD_0
	v_exp_f16_sdwa v98, v94 dst_sel:WORD_1 dst_unused:UNUSED_PRESERVE src0_sel:WORD_1
	v_exp_f16_sdwa v99, v95 dst_sel:WORD_1 dst_unused:UNUSED_PRESERVE src0_sel:WORD_1
	v_exp_f16_sdwa v100, v96 dst_sel:WORD_1 dst_unused:UNUSED_PRESERVE src0_sel:WORD_1
	v_exp_f16_sdwa v101, v97 dst_sel:WORD_1 dst_unused:UNUSED_PRESERVE src0_sel:WORD_1
	s_nop 0
	v_pk_add_f16 v94, v208, v162
	v_pk_add_f16 v77, v77, v98
	v_pk_add_f16 v74, v74, v101
	v_pk_add_f16 v75, v75, v100
	v_pk_add_f16 v76, v76, v99
	v_pk_fma_f16 v57, v45, v101, v57
	v_pk_fma_f16 v56, v44, v100, v56
	v_pk_fma_f16 v55, v43, v99, v55
	v_pk_fma_f16 v54, v42, v98, v54
	v_pk_add_f16 v95, v207, v163
	v_pk_add_f16 v96, v206, v164
	v_pk_add_f16 v97, v205, v165
	s_nop 0
	v_exp_f16_sdwa v98, v94 dst_sel:WORD_0 dst_unused:UNUSED_PAD src0_sel:WORD_0
	v_exp_f16_sdwa v99, v95 dst_sel:WORD_0 dst_unused:UNUSED_PAD src0_sel:WORD_0
	v_exp_f16_sdwa v100, v96 dst_sel:WORD_0 dst_unused:UNUSED_PAD src0_sel:WORD_0
	v_exp_f16_sdwa v101, v97 dst_sel:WORD_0 dst_unused:UNUSED_PAD src0_sel:WORD_0
	v_exp_f16_sdwa v98, v94 dst_sel:WORD_1 dst_unused:UNUSED_PRESERVE src0_sel:WORD_1
	v_exp_f16_sdwa v99, v95 dst_sel:WORD_1 dst_unused:UNUSED_PRESERVE src0_sel:WORD_1
	v_exp_f16_sdwa v100, v96 dst_sel:WORD_1 dst_unused:UNUSED_PRESERVE src0_sel:WORD_1
	v_exp_f16_sdwa v101, v97 dst_sel:WORD_1 dst_unused:UNUSED_PRESERVE src0_sel:WORD_1
	s_nop 0
	v_exp_f16_sdwa v94, v82 dst_sel:WORD_0 dst_unused:UNUSED_PAD src0_sel:WORD_0
	v_exp_f16_sdwa v95, v83 dst_sel:WORD_0 dst_unused:UNUSED_PAD src0_sel:WORD_0
	v_exp_f16_sdwa v96, v84 dst_sel:WORD_0 dst_unused:UNUSED_PAD src0_sel:WORD_0
	v_exp_f16_sdwa v97, v85 dst_sel:WORD_0 dst_unused:UNUSED_PAD src0_sel:WORD_0
	v_exp_f16_sdwa v94, v82 dst_sel:WORD_1 dst_unused:UNUSED_PRESERVE src0_sel:WORD_1
	v_exp_f16_sdwa v95, v83 dst_sel:WORD_1 dst_unused:UNUSED_PRESERVE src0_sel:WORD_1
	v_exp_f16_sdwa v96, v84 dst_sel:WORD_1 dst_unused:UNUSED_PRESERVE src0_sel:WORD_1
	v_exp_f16_sdwa v97, v85 dst_sel:WORD_1 dst_unused:UNUSED_PRESERVE src0_sel:WORD_1
	s_nop 0
	v_pk_add_f16 v82, v106, v162
	v_pk_add_f16 v77, v77, v98
	v_pk_add_f16 v76, v76, v99
	v_pk_add_f16 v75, v75, v100
	v_pk_add_f16 v74, v74, v101
	v_pk_fma_f16 v54, v58, v98, v54
	v_pk_fma_f16 v55, v59, v99, v55
	v_pk_fma_f16 v56, v60, v100, v56
	v_pk_fma_f16 v57, v61, v101, v57
	v_pk_add_f16 v77, v77, v94
	v_pk_add_f16 v74, v74, v97
	v_pk_add_f16 v75, v75, v96
	v_pk_add_f16 v76, v76, v95
	v_pk_fma_f16 v57, v21, v97, v57
	v_pk_fma_f16 v56, v20, v96, v56
	v_pk_fma_f16 v55, v19, v95, v55
	v_pk_fma_f16 v54, v18, v94, v54
	v_pk_add_f16 v83, v107, v163
	v_pk_add_f16 v84, v108, v164
	v_pk_add_f16 v85, v109, v165
	s_nop 0
	v_exp_f16_sdwa v94, v82 dst_sel:WORD_0 dst_unused:UNUSED_PAD src0_sel:WORD_0
	v_exp_f16_sdwa v95, v83 dst_sel:WORD_0 dst_unused:UNUSED_PAD src0_sel:WORD_0
	v_exp_f16_sdwa v96, v84 dst_sel:WORD_0 dst_unused:UNUSED_PAD src0_sel:WORD_0
	v_exp_f16_sdwa v97, v85 dst_sel:WORD_0 dst_unused:UNUSED_PAD src0_sel:WORD_0
	v_exp_f16_sdwa v94, v82 dst_sel:WORD_1 dst_unused:UNUSED_PRESERVE src0_sel:WORD_1
	v_exp_f16_sdwa v95, v83 dst_sel:WORD_1 dst_unused:UNUSED_PRESERVE src0_sel:WORD_1
	v_exp_f16_sdwa v96, v84 dst_sel:WORD_1 dst_unused:UNUSED_PRESERVE src0_sel:WORD_1
	v_exp_f16_sdwa v97, v85 dst_sel:WORD_1 dst_unused:UNUSED_PRESERVE src0_sel:WORD_1
	s_nop 0
	v_pk_add_f16 v82, v122, v162
	v_pk_add_f16 v77, v77, v94
	v_pk_add_f16 v76, v76, v95
	v_pk_add_f16 v75, v75, v96
	v_pk_add_f16 v74, v74, v97
	v_pk_fma_f16 v54, v22, v94, v54
	v_pk_fma_f16 v55, v23, v95, v55
	v_pk_fma_f16 v56, v24, v96, v56
	v_pk_fma_f16 v57, v25, v97, v57
	v_pk_add_f16 v83, v123, v163
	v_pk_add_f16 v84, v124, v164
	v_pk_add_f16 v85, v125, v165
	s_nop 0
	v_exp_f16_sdwa v94, v82 dst_sel:WORD_0 dst_unused:UNUSED_PAD src0_sel:WORD_0
	v_exp_f16_sdwa v95, v83 dst_sel:WORD_0 dst_unused:UNUSED_PAD src0_sel:WORD_0
	v_exp_f16_sdwa v96, v84 dst_sel:WORD_0 dst_unused:UNUSED_PAD src0_sel:WORD_0
	v_exp_f16_sdwa v97, v85 dst_sel:WORD_0 dst_unused:UNUSED_PAD src0_sel:WORD_0
	v_exp_f16_sdwa v94, v82 dst_sel:WORD_1 dst_unused:UNUSED_PRESERVE src0_sel:WORD_1
	v_exp_f16_sdwa v95, v83 dst_sel:WORD_1 dst_unused:UNUSED_PRESERVE src0_sel:WORD_1
	v_exp_f16_sdwa v96, v84 dst_sel:WORD_1 dst_unused:UNUSED_PRESERVE src0_sel:WORD_1
	v_exp_f16_sdwa v97, v85 dst_sel:WORD_1 dst_unused:UNUSED_PRESERVE src0_sel:WORD_1
	s_nop 0
	s_nop 0
	v_pk_add_f16 v77, v77, v94
	v_pk_add_f16 v76, v76, v95
	v_rcp_f16_e32 v82, v77
	v_rcp_f16_sdwa v77, v77 dst_sel:DWORD dst_unused:UNUSED_PAD src0_sel:WORD_1
	v_pk_add_f16 v75, v75, v96
	v_rcp_f16_e32 v83, v76
	v_rcp_f16_sdwa v76, v76 dst_sel:DWORD dst_unused:UNUSED_PAD src0_sel:WORD_1
	v_pk_add_f16 v74, v74, v97
	v_rcp_f16_e32 v84, v75
	v_rcp_f16_sdwa v75, v75 dst_sel:DWORD dst_unused:UNUSED_PAD src0_sel:WORD_1
	v_rcp_f16_e32 v85, v74
	v_rcp_f16_sdwa v74, v74 dst_sel:DWORD dst_unused:UNUSED_PAD src0_sel:WORD_1
	v_pk_fma_f16 v54, v26, v94, v54
	v_pack_b32_f16 v77, v82, v77
	v_pk_fma_f16 v55, v27, v95, v55
	v_pk_mul_f16 v77, v54, v77
	v_pack_b32_f16 v54, v83, v76
	v_pk_fma_f16 v56, v28, v96, v56
	v_pk_mul_f16 v76, v55, v54
	v_pack_b32_f16 v54, v84, v75
	v_pk_fma_f16 v57, v29, v97, v57
	v_pk_mul_f16 v75, v56, v54
	v_pack_b32_f16 v54, v85, v74
	v_pk_mul_f16 v74, v57, v54
	s_waitcnt vmcnt(7)
	v_pk_mul_f16 v57, v204, v161 op_sel_hi:[0,1]
	v_pk_mul_f16 v85, v202, v161 op_sel_hi:[0,1]
	v_pk_mul_f16 v97, v203, v161 op_sel_hi:[0,1]
	v_pk_mul_f16 v54, v204, v158 op_sel_hi:[0,1]
	v_pk_mul_f16 v55, v204, v159 op_sel_hi:[0,1]
	v_pk_mul_f16 v56, v204, v160 op_sel_hi:[0,1]
	v_pk_mul_f16 v82, v202, v158 op_sel_hi:[0,1]
	v_pk_mul_f16 v83, v202, v159 op_sel_hi:[0,1]
	v_pk_mul_f16 v84, v202, v160 op_sel_hi:[0,1]
	v_pk_mul_f16 v94, v203, v158 op_sel_hi:[0,1]
	v_pk_mul_f16 v95, v203, v159 op_sel_hi:[0,1]
	v_pk_mul_f16 v96, v203, v160 op_sel_hi:[0,1]
	v_pk_fma_f16 v65, v65, v161, v57
	v_pk_fma_f16 v81, v81, v161, v85
	v_pk_fma_f16 v98, v105, v161, v97
	v_pk_fma_f16 v64, v64, v160, v56
	v_pk_maximum3_f16 v125, v65, v81, v98
	v_pk_fma_f16 v63, v63, v159, v55
	v_pk_fma_f16 v62, v62, v158, v54
	v_pk_fma_f16 v80, v80, v160, v84
	v_pk_fma_f16 v79, v79, v159, v83
	v_pk_fma_f16 v78, v78, v158, v82
	v_pk_fma_f16 v99, v104, v160, v96
	v_pk_fma_f16 v100, v103, v159, v95
	v_pk_fma_f16 v101, v102, v158, v94
	v_pk_fma_f16 v102, v37, v161, v57
	v_pk_fma_f16 v106, v49, v161, v85
	v_pk_fma_f16 v118, v69, v161, v97
	v_pk_fma_f16 v57, v89, v161, v57
	v_pk_fma_f16 v85, v117, v161, v85
	v_pk_fma_f16 v97, v133, v161, v97
	v_pk_maximum3_f16 v122, v62, v78, v101
	v_pk_maximum3_f16 v123, v63, v79, v100
	v_pk_maximum3_f16 v124, v64, v80, v99
	v_pk_maximum3_f16 v129, v102, v106, v118
	v_pk_fma_f16 v103, v36, v160, v56
	v_pk_maximum3_f16 v137, v57, v85, v97
	v_pk_fma_f16 v104, v35, v159, v55
	v_pk_maximum3_f16 v125, v125, v129, v137
	v_pk_fma_f16 v105, v34, v158, v54
	v_pk_fma_f16 v107, v48, v160, v84
	v_pk_fma_f16 v108, v47, v159, v83
	v_pk_fma_f16 v109, v46, v158, v82
	v_pk_fma_f16 v119, v68, v160, v96
	v_pk_fma_f16 v120, v67, v159, v95
	v_pk_fma_f16 v121, v66, v158, v94
	v_pk_fma_f16 v56, v88, v160, v56
	v_pk_fma_f16 v55, v87, v159, v55
	v_pk_fma_f16 v54, v86, v158, v54
	v_pk_fma_f16 v84, v116, v160, v84
	v_pk_fma_f16 v83, v115, v159, v83
	v_pk_fma_f16 v82, v114, v158, v82
	v_pk_fma_f16 v96, v132, v160, v96
	v_pk_fma_f16 v95, v131, v159, v95
	v_pk_fma_f16 v94, v130, v158, v94
	v_pk_maximum3_f16 v126, v105, v109, v121
	v_pk_maximum3_f16 v127, v104, v108, v120
	v_pk_maximum3_f16 v128, v103, v107, v119
	v_pk_maximum3_f16 v135, v55, v83, v95
	v_pk_maximum3_f16 v136, v56, v84, v96
	s_nop 0
	v_pk_maximum3_f16 v134, v54, v82, v94
	v_xor_b32_e32 v125, 0x80008000, v125
	v_pk_maximum3_f16 v122, v122, v126, v134
	v_pk_maximum3_f16 v123, v123, v127, v135
	v_pk_maximum3_f16 v124, v124, v128, v136
	v_pk_add_f16 v65, v65, v125
	v_xor_b32_e32 v124, 0x80008000, v124
	v_xor_b32_e32 v123, 0x80008000, v123
	v_xor_b32_e32 v122, 0x80008000, v122
	v_pk_add_f16 v62, v62, v122
	v_pk_add_f16 v63, v63, v123
	v_pk_add_f16 v64, v64, v124
	v_pk_add_f16 v78, v78, v122
	v_exp_f16_sdwa v126, v62 dst_sel:WORD_0 dst_unused:UNUSED_PAD src0_sel:WORD_0
	v_exp_f16_sdwa v127, v63 dst_sel:WORD_0 dst_unused:UNUSED_PAD src0_sel:WORD_0
	v_exp_f16_sdwa v128, v64 dst_sel:WORD_0 dst_unused:UNUSED_PAD src0_sel:WORD_0
	v_exp_f16_sdwa v129, v65 dst_sel:WORD_0 dst_unused:UNUSED_PAD src0_sel:WORD_0
	v_exp_f16_sdwa v126, v62 dst_sel:WORD_1 dst_unused:UNUSED_PRESERVE src0_sel:WORD_1
	v_exp_f16_sdwa v127, v63 dst_sel:WORD_1 dst_unused:UNUSED_PRESERVE src0_sel:WORD_1
	v_exp_f16_sdwa v128, v64 dst_sel:WORD_1 dst_unused:UNUSED_PRESERVE src0_sel:WORD_1
	v_exp_f16_sdwa v129, v65 dst_sel:WORD_1 dst_unused:UNUSED_PRESERVE src0_sel:WORD_1
	s_nop 0
	v_pk_add_f16 v79, v79, v123
	v_pk_add_f16 v65, v126, 0
	v_pk_fma_f16 v33, v33, v129, 0
	v_pk_add_f16 v62, v129, 0
	v_pk_add_f16 v63, v128, 0
	v_pk_add_f16 v64, v127, 0
	v_pk_fma_f16 v32, v32, v128, 0
	v_pk_fma_f16 v31, v31, v127, 0
	v_pk_fma_f16 v30, v30, v126, 0
	v_pk_add_f16 v80, v80, v124
	v_pk_add_f16 v81, v81, v125
	v_pk_add_f16 v54, v54, v122
	v_exp_f16_sdwa v126, v78 dst_sel:WORD_0 dst_unused:UNUSED_PAD src0_sel:WORD_0
	v_exp_f16_sdwa v127, v79 dst_sel:WORD_0 dst_unused:UNUSED_PAD src0_sel:WORD_0
	v_exp_f16_sdwa v128, v80 dst_sel:WORD_0 dst_unused:UNUSED_PAD src0_sel:WORD_0
	v_exp_f16_sdwa v129, v81 dst_sel:WORD_0 dst_unused:UNUSED_PAD src0_sel:WORD_0
	v_exp_f16_sdwa v126, v78 dst_sel:WORD_1 dst_unused:UNUSED_PRESERVE src0_sel:WORD_1
	v_exp_f16_sdwa v127, v79 dst_sel:WORD_1 dst_unused:UNUSED_PRESERVE src0_sel:WORD_1
	v_exp_f16_sdwa v128, v80 dst_sel:WORD_1 dst_unused:UNUSED_PRESERVE src0_sel:WORD_1
	v_exp_f16_sdwa v129, v81 dst_sel:WORD_1 dst_unused:UNUSED_PRESERVE src0_sel:WORD_1
	s_nop 0
	v_pk_add_f16 v55, v55, v123
	v_pk_add_f16 v65, v65, v126
	v_pk_fma_f16 v33, v45, v129, v33
	v_pk_add_f16 v45, v98, v125
	v_pk_add_f16 v64, v64, v127
	v_pk_add_f16 v63, v63, v128
	v_pk_add_f16 v62, v62, v129
	v_pk_fma_f16 v30, v42, v126, v30
	v_pk_fma_f16 v31, v43, v127, v31
	v_pk_fma_f16 v32, v44, v128, v32
	v_pk_add_f16 v42, v101, v122
	v_pk_add_f16 v43, v100, v123
	v_pk_add_f16 v44, v99, v124
	v_pk_add_f16 v56, v56, v124
	v_exp_f16_sdwa v78, v42 dst_sel:WORD_0 dst_unused:UNUSED_PAD src0_sel:WORD_0
	v_exp_f16_sdwa v79, v43 dst_sel:WORD_0 dst_unused:UNUSED_PAD src0_sel:WORD_0
	v_exp_f16_sdwa v80, v44 dst_sel:WORD_0 dst_unused:UNUSED_PAD src0_sel:WORD_0
	v_exp_f16_sdwa v81, v45 dst_sel:WORD_0 dst_unused:UNUSED_PAD src0_sel:WORD_0
	v_exp_f16_sdwa v78, v42 dst_sel:WORD_1 dst_unused:UNUSED_PRESERVE src0_sel:WORD_1
	v_exp_f16_sdwa v79, v43 dst_sel:WORD_1 dst_unused:UNUSED_PRESERVE src0_sel:WORD_1
	v_exp_f16_sdwa v80, v44 dst_sel:WORD_1 dst_unused:UNUSED_PRESERVE src0_sel:WORD_1
	v_exp_f16_sdwa v81, v45 dst_sel:WORD_1 dst_unused:UNUSED_PRESERVE src0_sel:WORD_1
	s_nop 0
	v_pk_add_f16 v57, v57, v125
	v_pk_add_f16 v45, v65, v78
	v_pk_add_f16 v42, v62, v81
	v_pk_add_f16 v43, v63, v80
	v_pk_add_f16 v44, v64, v79
	v_pk_fma_f16 v33, v61, v81, v33
	v_pk_fma_f16 v32, v60, v80, v32
	v_pk_fma_f16 v31, v59, v79, v31
	v_pk_fma_f16 v30, v58, v78, v30
	v_pk_add_f16 v58, v105, v122
	v_pk_add_f16 v59, v104, v123
	v_pk_add_f16 v60, v103, v124
	v_pk_add_f16 v61, v102, v125
	s_nop 0
	v_exp_f16_sdwa v62, v58 dst_sel:WORD_0 dst_unused:UNUSED_PAD src0_sel:WORD_0
	v_exp_f16_sdwa v63, v59 dst_sel:WORD_0 dst_unused:UNUSED_PAD src0_sel:WORD_0
	v_exp_f16_sdwa v64, v60 dst_sel:WORD_0 dst_unused:UNUSED_PAD src0_sel:WORD_0
	v_exp_f16_sdwa v65, v61 dst_sel:WORD_0 dst_unused:UNUSED_PAD src0_sel:WORD_0
	v_exp_f16_sdwa v62, v58 dst_sel:WORD_1 dst_unused:UNUSED_PRESERVE src0_sel:WORD_1
	v_exp_f16_sdwa v63, v59 dst_sel:WORD_1 dst_unused:UNUSED_PRESERVE src0_sel:WORD_1
	v_exp_f16_sdwa v64, v60 dst_sel:WORD_1 dst_unused:UNUSED_PRESERVE src0_sel:WORD_1
	v_exp_f16_sdwa v65, v61 dst_sel:WORD_1 dst_unused:UNUSED_PRESERVE src0_sel:WORD_1
	s_nop 0
	v_pk_add_f16 v58, v109, v122
	v_pk_add_f16 v45, v45, v62
	v_pk_add_f16 v44, v44, v63
	v_pk_add_f16 v43, v43, v64
	v_pk_add_f16 v42, v42, v65
	v_pk_fma_f16 v30, v18, v62, v30
	v_pk_fma_f16 v31, v19, v63, v31
	v_pk_fma_f16 v32, v20, v64, v32
	v_pk_fma_f16 v33, v21, v65, v33
	v_pk_add_f16 v59, v108, v123
	v_pk_add_f16 v60, v107, v124
	v_pk_add_f16 v61, v106, v125
	s_nop 0
	v_exp_f16_sdwa v62, v58 dst_sel:WORD_0 dst_unused:UNUSED_PAD src0_sel:WORD_0
	v_exp_f16_sdwa v63, v59 dst_sel:WORD_0 dst_unused:UNUSED_PAD src0_sel:WORD_0
	v_exp_f16_sdwa v64, v60 dst_sel:WORD_0 dst_unused:UNUSED_PAD src0_sel:WORD_0
	v_exp_f16_sdwa v65, v61 dst_sel:WORD_0 dst_unused:UNUSED_PAD src0_sel:WORD_0
	v_exp_f16_sdwa v62, v58 dst_sel:WORD_1 dst_unused:UNUSED_PRESERVE src0_sel:WORD_1
	v_exp_f16_sdwa v63, v59 dst_sel:WORD_1 dst_unused:UNUSED_PRESERVE src0_sel:WORD_1
	v_exp_f16_sdwa v64, v60 dst_sel:WORD_1 dst_unused:UNUSED_PRESERVE src0_sel:WORD_1
	v_exp_f16_sdwa v65, v61 dst_sel:WORD_1 dst_unused:UNUSED_PRESERVE src0_sel:WORD_1
	s_nop 0
	v_pk_add_f16 v58, v121, v122
	v_pk_add_f16 v45, v45, v62
	v_pk_add_f16 v42, v42, v65
	v_pk_add_f16 v43, v43, v64
	v_pk_add_f16 v44, v44, v63
	v_pk_fma_f16 v33, v25, v65, v33
	v_pk_fma_f16 v32, v24, v64, v32
	v_pk_fma_f16 v31, v23, v63, v31
	v_pk_fma_f16 v30, v22, v62, v30
	v_pk_add_f16 v59, v120, v123
	v_pk_add_f16 v60, v119, v124
	v_pk_add_f16 v61, v118, v125
	s_nop 0
	v_exp_f16_sdwa v62, v58 dst_sel:WORD_0 dst_unused:UNUSED_PAD src0_sel:WORD_0
	v_exp_f16_sdwa v63, v59 dst_sel:WORD_0 dst_unused:UNUSED_PAD src0_sel:WORD_0
	v_exp_f16_sdwa v64, v60 dst_sel:WORD_0 dst_unused:UNUSED_PAD src0_sel:WORD_0
	v_exp_f16_sdwa v65, v61 dst_sel:WORD_0 dst_unused:UNUSED_PAD src0_sel:WORD_0
	v_exp_f16_sdwa v62, v58 dst_sel:WORD_1 dst_unused:UNUSED_PRESERVE src0_sel:WORD_1
	v_exp_f16_sdwa v63, v59 dst_sel:WORD_1 dst_unused:UNUSED_PRESERVE src0_sel:WORD_1
	v_exp_f16_sdwa v64, v60 dst_sel:WORD_1 dst_unused:UNUSED_PRESERVE src0_sel:WORD_1
	v_exp_f16_sdwa v65, v61 dst_sel:WORD_1 dst_unused:UNUSED_PRESERVE src0_sel:WORD_1
	s_nop 0
	v_exp_f16_sdwa v58, v54 dst_sel:WORD_0 dst_unused:UNUSED_PAD src0_sel:WORD_0
	v_exp_f16_sdwa v59, v55 dst_sel:WORD_0 dst_unused:UNUSED_PAD src0_sel:WORD_0
	v_exp_f16_sdwa v60, v56 dst_sel:WORD_0 dst_unused:UNUSED_PAD src0_sel:WORD_0
	v_exp_f16_sdwa v61, v57 dst_sel:WORD_0 dst_unused:UNUSED_PAD src0_sel:WORD_0
	v_exp_f16_sdwa v58, v54 dst_sel:WORD_1 dst_unused:UNUSED_PRESERVE src0_sel:WORD_1
	v_exp_f16_sdwa v59, v55 dst_sel:WORD_1 dst_unused:UNUSED_PRESERVE src0_sel:WORD_1
	v_exp_f16_sdwa v60, v56 dst_sel:WORD_1 dst_unused:UNUSED_PRESERVE src0_sel:WORD_1
	v_exp_f16_sdwa v61, v57 dst_sel:WORD_1 dst_unused:UNUSED_PRESERVE src0_sel:WORD_1
	s_nop 0
	v_pk_add_f16 v54, v82, v122
	v_pk_add_f16 v45, v45, v62
	v_pk_add_f16 v44, v44, v63
	v_pk_add_f16 v43, v43, v64
	v_pk_add_f16 v42, v42, v65
	v_pk_fma_f16 v30, v26, v62, v30
	v_pk_fma_f16 v31, v27, v63, v31
	v_pk_fma_f16 v32, v28, v64, v32
	v_pk_fma_f16 v33, v29, v65, v33
	v_pk_add_f16 v45, v45, v58
	v_pk_add_f16 v42, v42, v61
	v_pk_add_f16 v43, v43, v60
	v_pk_add_f16 v44, v44, v59
	v_pk_fma_f16 v33, v41, v61, v33
	v_pk_fma_f16 v32, v40, v60, v32
	v_pk_fma_f16 v31, v39, v59, v31
	v_pk_fma_f16 v30, v38, v58, v30
	v_pk_add_f16 v55, v83, v123
	v_pk_add_f16 v56, v84, v124
	v_pk_add_f16 v57, v85, v125
	s_nop 0
	v_exp_f16_sdwa v58, v54 dst_sel:WORD_0 dst_unused:UNUSED_PAD src0_sel:WORD_0
	v_exp_f16_sdwa v59, v55 dst_sel:WORD_0 dst_unused:UNUSED_PAD src0_sel:WORD_0
	v_exp_f16_sdwa v60, v56 dst_sel:WORD_0 dst_unused:UNUSED_PAD src0_sel:WORD_0
	v_exp_f16_sdwa v61, v57 dst_sel:WORD_0 dst_unused:UNUSED_PAD src0_sel:WORD_0
	v_exp_f16_sdwa v58, v54 dst_sel:WORD_1 dst_unused:UNUSED_PRESERVE src0_sel:WORD_1
	v_exp_f16_sdwa v59, v55 dst_sel:WORD_1 dst_unused:UNUSED_PRESERVE src0_sel:WORD_1
	v_exp_f16_sdwa v60, v56 dst_sel:WORD_1 dst_unused:UNUSED_PRESERVE src0_sel:WORD_1
	v_exp_f16_sdwa v61, v57 dst_sel:WORD_1 dst_unused:UNUSED_PRESERVE src0_sel:WORD_1
	s_nop 0
	v_pk_add_f16 v54, v94, v122
	v_pk_add_f16 v45, v45, v58
	v_pk_add_f16 v44, v44, v59
	v_pk_add_f16 v43, v43, v60
	v_pk_add_f16 v42, v42, v61
	v_pk_fma_f16 v30, v50, v58, v30
	v_pk_fma_f16 v31, v51, v59, v31
	v_pk_fma_f16 v32, v52, v60, v32
	v_pk_fma_f16 v33, v53, v61, v33
	v_pk_add_f16 v55, v95, v123
	v_pk_add_f16 v56, v96, v124
	v_pk_add_f16 v57, v97, v125
	s_nop 0
	v_exp_f16_sdwa v58, v54 dst_sel:WORD_0 dst_unused:UNUSED_PAD src0_sel:WORD_0
	v_exp_f16_sdwa v59, v55 dst_sel:WORD_0 dst_unused:UNUSED_PAD src0_sel:WORD_0
	v_exp_f16_sdwa v60, v56 dst_sel:WORD_0 dst_unused:UNUSED_PAD src0_sel:WORD_0
	v_exp_f16_sdwa v61, v57 dst_sel:WORD_0 dst_unused:UNUSED_PAD src0_sel:WORD_0
	v_exp_f16_sdwa v58, v54 dst_sel:WORD_1 dst_unused:UNUSED_PRESERVE src0_sel:WORD_1
	v_exp_f16_sdwa v59, v55 dst_sel:WORD_1 dst_unused:UNUSED_PRESERVE src0_sel:WORD_1
	v_exp_f16_sdwa v60, v56 dst_sel:WORD_1 dst_unused:UNUSED_PRESERVE src0_sel:WORD_1
	v_exp_f16_sdwa v61, v57 dst_sel:WORD_1 dst_unused:UNUSED_PRESERVE src0_sel:WORD_1
	s_nop 0
	s_nop 0
	v_pk_add_f16 v45, v45, v58
	v_pk_add_f16 v44, v44, v59
	v_rcp_f16_e32 v54, v45
	v_rcp_f16_sdwa v45, v45 dst_sel:DWORD dst_unused:UNUSED_PAD src0_sel:WORD_1
	v_pk_add_f16 v43, v43, v60
	v_rcp_f16_e32 v55, v44
	v_rcp_f16_sdwa v44, v44 dst_sel:DWORD dst_unused:UNUSED_PAD src0_sel:WORD_1
	v_pk_add_f16 v42, v42, v61
	v_pk_fma_f16 v30, v70, v58, v30
	v_rcp_f16_e32 v58, v43
	v_rcp_f16_sdwa v43, v43 dst_sel:DWORD dst_unused:UNUSED_PAD src0_sel:WORD_1
	v_pk_fma_f16 v31, v71, v59, v31
	v_rcp_f16_e32 v59, v42
	v_rcp_f16_sdwa v42, v42 dst_sel:DWORD dst_unused:UNUSED_PAD src0_sel:WORD_1
	v_pack_b32_f16 v45, v54, v45
	v_pk_mul_f16 v57, v30, v45
	v_pack_b32_f16 v30, v55, v44
	v_pk_fma_f16 v32, v72, v60, v32
	v_pk_mul_f16 v56, v31, v30
	v_pack_b32_f16 v30, v58, v43
	v_pk_fma_f16 v33, v73, v61, v33
	v_pk_mul_f16 v55, v32, v30
	v_pack_b32_f16 v30, v59, v42
	v_pk_mul_f16 v54, v33, v30
	s_waitcnt vmcnt(0)
	v_pk_mul_f16 v30, v204, v154 op_sel_hi:[0,1]
	v_pk_mul_f16 v31, v204, v155 op_sel_hi:[0,1]
	v_pk_mul_f16 v32, v204, v156 op_sel_hi:[0,1]
	v_pk_mul_f16 v33, v204, v157 op_sel_hi:[0,1]
	v_pk_mul_f16 v42, v202, v154 op_sel_hi:[0,1]
	v_pk_mul_f16 v43, v202, v155 op_sel_hi:[0,1]
	v_pk_mul_f16 v44, v202, v156 op_sel_hi:[0,1]
	v_pk_mul_f16 v45, v202, v157 op_sel_hi:[0,1]
	v_pk_mul_f16 v58, v203, v154 op_sel_hi:[0,1]
	v_pk_mul_f16 v59, v203, v155 op_sel_hi:[0,1]
	v_pk_mul_f16 v60, v203, v156 op_sel_hi:[0,1]
	v_pk_mul_f16 v61, v203, v157 op_sel_hi:[0,1]
	v_pk_fma_f16 v37, v37, v157, v33
	v_pk_fma_f16 v36, v36, v156, v32
	v_pk_fma_f16 v35, v35, v155, v31
	v_pk_fma_f16 v34, v34, v154, v30
	v_pk_fma_f16 v49, v49, v157, v45
	v_pk_fma_f16 v48, v48, v156, v44
	v_pk_fma_f16 v47, v47, v155, v43
	v_pk_fma_f16 v46, v46, v154, v42
	v_pk_fma_f16 v62, v69, v157, v61
	v_pk_fma_f16 v63, v68, v156, v60
	v_pk_fma_f16 v64, v67, v155, v59
	v_pk_fma_f16 v65, v66, v154, v58
	v_pk_fma_f16 v66, v89, v157, v33
	v_pk_fma_f16 v67, v88, v156, v32
	v_pk_fma_f16 v68, v87, v155, v31
	v_pk_fma_f16 v69, v86, v154, v30
	v_pk_fma_f16 v78, v117, v157, v45
	v_pk_fma_f16 v79, v116, v156, v44
	v_pk_fma_f16 v80, v115, v155, v43
	v_pk_fma_f16 v81, v114, v154, v42
	v_pk_fma_f16 v82, v133, v157, v61
	v_pk_fma_f16 v83, v132, v156, v60
	v_pk_fma_f16 v84, v131, v155, v59
	v_pk_fma_f16 v85, v130, v154, v58
	v_pk_fma_f16 v61, v17, v157, v61
	v_pk_fma_f16 v60, v16, v156, v60
	v_pk_fma_f16 v59, v15, v155, v59
	v_pk_fma_f16 v58, v14, v154, v58
	v_pk_maximum3_f16 v14, v34, v46, v65
	v_pk_maximum3_f16 v15, v35, v47, v64
	v_pk_maximum3_f16 v16, v36, v48, v63
	v_pk_maximum3_f16 v17, v37, v49, v62
	v_pk_maximum3_f16 v86, v69, v81, v85
	v_pk_maximum3_f16 v87, v68, v80, v84
	v_pk_maximum3_f16 v88, v67, v79, v83
	v_pk_maximum3_f16 v89, v66, v78, v82
	v_pk_fma_f16 v33, v145, v157, v33
	v_pk_fma_f16 v32, v144, v156, v32
	v_pk_fma_f16 v31, v143, v155, v31
	v_pk_fma_f16 v30, v142, v154, v30
	v_pk_fma_f16 v45, v153, v157, v45
	v_pk_fma_f16 v44, v152, v156, v44
	v_pk_fma_f16 v43, v151, v155, v43
	v_pk_fma_f16 v42, v150, v154, v42
	v_pk_maximum3_f16 v95, v31, v43, v59
	v_pk_maximum3_f16 v96, v32, v44, v60
	v_pk_maximum3_f16 v97, v33, v45, v61
	s_nop 0
	v_pk_maximum3_f16 v94, v30, v42, v58
	v_pk_maximum3_f16 v15, v15, v87, v95
	v_pk_maximum3_f16 v16, v16, v88, v96
	v_pk_maximum3_f16 v17, v17, v89, v97
	s_nop 0
	v_pk_maximum3_f16 v14, v14, v86, v94
	v_xor_b32_e32 v86, 0x80008000, v17
	v_xor_b32_e32 v87, 0x80008000, v16
	v_xor_b32_e32 v88, 0x80008000, v15
	v_xor_b32_e32 v89, 0x80008000, v14
	v_pk_add_f16 v14, v34, v89
	v_pk_add_f16 v15, v35, v88
	v_pk_add_f16 v16, v36, v87
	v_pk_add_f16 v17, v37, v86
	s_nop 0
	v_exp_f16_sdwa v34, v14 dst_sel:WORD_0 dst_unused:UNUSED_PAD src0_sel:WORD_0
	v_exp_f16_sdwa v35, v15 dst_sel:WORD_0 dst_unused:UNUSED_PAD src0_sel:WORD_0
	v_exp_f16_sdwa v36, v16 dst_sel:WORD_0 dst_unused:UNUSED_PAD src0_sel:WORD_0
	v_exp_f16_sdwa v37, v17 dst_sel:WORD_0 dst_unused:UNUSED_PAD src0_sel:WORD_0
	v_exp_f16_sdwa v34, v14 dst_sel:WORD_1 dst_unused:UNUSED_PRESERVE src0_sel:WORD_1
	v_exp_f16_sdwa v35, v15 dst_sel:WORD_1 dst_unused:UNUSED_PRESERVE src0_sel:WORD_1
	v_exp_f16_sdwa v36, v16 dst_sel:WORD_1 dst_unused:UNUSED_PRESERVE src0_sel:WORD_1
	v_exp_f16_sdwa v37, v17 dst_sel:WORD_1 dst_unused:UNUSED_PRESERVE src0_sel:WORD_1
	s_nop 0
	s_nop 0
	v_pk_add_f16 v14, v34, 0
	v_pk_add_f16 v15, v35, 0
	v_pk_add_f16 v16, v36, 0
	v_pk_add_f16 v17, v37, 0
	v_pk_fma_f16 v18, v18, v34, 0
	v_pk_fma_f16 v19, v19, v35, 0
	v_pk_fma_f16 v20, v20, v36, 0
	v_pk_fma_f16 v21, v21, v37, 0
	v_pk_add_f16 v34, v46, v89
	v_pk_add_f16 v35, v47, v88
	v_pk_add_f16 v36, v48, v87
	v_pk_add_f16 v37, v49, v86
	s_nop 0
	v_exp_f16_sdwa v46, v34 dst_sel:WORD_0 dst_unused:UNUSED_PAD src0_sel:WORD_0
	v_exp_f16_sdwa v47, v35 dst_sel:WORD_0 dst_unused:UNUSED_PAD src0_sel:WORD_0
	v_exp_f16_sdwa v48, v36 dst_sel:WORD_0 dst_unused:UNUSED_PAD src0_sel:WORD_0
	v_exp_f16_sdwa v49, v37 dst_sel:WORD_0 dst_unused:UNUSED_PAD src0_sel:WORD_0
	v_exp_f16_sdwa v46, v34 dst_sel:WORD_1 dst_unused:UNUSED_PRESERVE src0_sel:WORD_1
	v_exp_f16_sdwa v47, v35 dst_sel:WORD_1 dst_unused:UNUSED_PRESERVE src0_sel:WORD_1
	v_exp_f16_sdwa v48, v36 dst_sel:WORD_1 dst_unused:UNUSED_PRESERVE src0_sel:WORD_1
	v_exp_f16_sdwa v49, v37 dst_sel:WORD_1 dst_unused:UNUSED_PRESERVE src0_sel:WORD_1
	s_nop 0
	s_nop 0
	v_pk_add_f16 v17, v17, v49
	v_pk_add_f16 v16, v16, v48
	v_pk_add_f16 v15, v15, v47
	v_pk_add_f16 v14, v14, v46
	v_pk_fma_f16 v21, v25, v49, v21
	v_pk_fma_f16 v20, v24, v48, v20
	v_pk_fma_f16 v19, v23, v47, v19
	v_pk_fma_f16 v18, v22, v46, v18
	v_pk_add_f16 v22, v65, v89
	v_pk_add_f16 v23, v64, v88
	v_pk_add_f16 v24, v63, v87
	v_pk_add_f16 v25, v62, v86
	s_nop 0
	v_exp_f16_sdwa v34, v22 dst_sel:WORD_0 dst_unused:UNUSED_PAD src0_sel:WORD_0
	v_exp_f16_sdwa v35, v23 dst_sel:WORD_0 dst_unused:UNUSED_PAD src0_sel:WORD_0
	v_exp_f16_sdwa v36, v24 dst_sel:WORD_0 dst_unused:UNUSED_PAD src0_sel:WORD_0
	v_exp_f16_sdwa v37, v25 dst_sel:WORD_0 dst_unused:UNUSED_PAD src0_sel:WORD_0
	v_exp_f16_sdwa v34, v22 dst_sel:WORD_1 dst_unused:UNUSED_PRESERVE src0_sel:WORD_1
	v_exp_f16_sdwa v35, v23 dst_sel:WORD_1 dst_unused:UNUSED_PRESERVE src0_sel:WORD_1
	v_exp_f16_sdwa v36, v24 dst_sel:WORD_1 dst_unused:UNUSED_PRESERVE src0_sel:WORD_1
	v_exp_f16_sdwa v37, v25 dst_sel:WORD_1 dst_unused:UNUSED_PRESERVE src0_sel:WORD_1
	s_nop 0
	v_pk_add_f16 v22, v69, v89
	v_pk_add_f16 v14, v14, v34
	v_pk_add_f16 v15, v15, v35
	v_pk_add_f16 v16, v16, v36
	v_pk_add_f16 v17, v17, v37
	v_pk_fma_f16 v18, v26, v34, v18
	v_pk_fma_f16 v19, v27, v35, v19
	v_pk_fma_f16 v20, v28, v36, v20
	v_pk_fma_f16 v21, v29, v37, v21
	v_pk_add_f16 v23, v68, v88
	v_pk_add_f16 v24, v67, v87
	v_pk_add_f16 v25, v66, v86
	s_nop 0
	v_exp_f16_sdwa v26, v22 dst_sel:WORD_0 dst_unused:UNUSED_PAD src0_sel:WORD_0
	v_exp_f16_sdwa v27, v23 dst_sel:WORD_0 dst_unused:UNUSED_PAD src0_sel:WORD_0
	v_exp_f16_sdwa v28, v24 dst_sel:WORD_0 dst_unused:UNUSED_PAD src0_sel:WORD_0
	v_exp_f16_sdwa v29, v25 dst_sel:WORD_0 dst_unused:UNUSED_PAD src0_sel:WORD_0
	v_exp_f16_sdwa v26, v22 dst_sel:WORD_1 dst_unused:UNUSED_PRESERVE src0_sel:WORD_1
	v_exp_f16_sdwa v27, v23 dst_sel:WORD_1 dst_unused:UNUSED_PRESERVE src0_sel:WORD_1
	v_exp_f16_sdwa v28, v24 dst_sel:WORD_1 dst_unused:UNUSED_PRESERVE src0_sel:WORD_1
	v_exp_f16_sdwa v29, v25 dst_sel:WORD_1 dst_unused:UNUSED_PRESERVE src0_sel:WORD_1
	s_nop 0
	v_pk_add_f16 v22, v81, v89
	v_pk_add_f16 v17, v17, v29
	v_pk_add_f16 v16, v16, v28
	v_pk_add_f16 v15, v15, v27
	v_pk_add_f16 v14, v14, v26
	v_pk_fma_f16 v21, v41, v29, v21
	v_pk_fma_f16 v20, v40, v28, v20
	v_pk_fma_f16 v19, v39, v27, v19
	v_pk_fma_f16 v18, v38, v26, v18
	v_pk_add_f16 v23, v80, v88
	v_pk_add_f16 v24, v79, v87
	v_pk_add_f16 v25, v78, v86
	s_nop 0
	v_exp_f16_sdwa v26, v22 dst_sel:WORD_0 dst_unused:UNUSED_PAD src0_sel:WORD_0
	v_exp_f16_sdwa v27, v23 dst_sel:WORD_0 dst_unused:UNUSED_PAD src0_sel:WORD_0
	v_exp_f16_sdwa v28, v24 dst_sel:WORD_0 dst_unused:UNUSED_PAD src0_sel:WORD_0
	v_exp_f16_sdwa v29, v25 dst_sel:WORD_0 dst_unused:UNUSED_PAD src0_sel:WORD_0
	v_exp_f16_sdwa v26, v22 dst_sel:WORD_1 dst_unused:UNUSED_PRESERVE src0_sel:WORD_1
	v_exp_f16_sdwa v27, v23 dst_sel:WORD_1 dst_unused:UNUSED_PRESERVE src0_sel:WORD_1
	v_exp_f16_sdwa v28, v24 dst_sel:WORD_1 dst_unused:UNUSED_PRESERVE src0_sel:WORD_1
	v_exp_f16_sdwa v29, v25 dst_sel:WORD_1 dst_unused:UNUSED_PRESERVE src0_sel:WORD_1
	s_nop 0
	v_pk_add_f16 v22, v85, v89
	v_pk_add_f16 v14, v14, v26
	v_pk_add_f16 v15, v15, v27
	v_pk_add_f16 v16, v16, v28
	v_pk_add_f16 v17, v17, v29
	v_pk_fma_f16 v18, v50, v26, v18
	v_pk_fma_f16 v19, v51, v27, v19
	v_pk_fma_f16 v20, v52, v28, v20
	v_pk_fma_f16 v21, v53, v29, v21
	v_pk_add_f16 v23, v84, v88
	v_pk_add_f16 v24, v83, v87
	v_pk_add_f16 v25, v82, v86
	s_nop 0
	v_exp_f16_sdwa v26, v22 dst_sel:WORD_0 dst_unused:UNUSED_PAD src0_sel:WORD_0
	v_exp_f16_sdwa v27, v23 dst_sel:WORD_0 dst_unused:UNUSED_PAD src0_sel:WORD_0
	v_exp_f16_sdwa v28, v24 dst_sel:WORD_0 dst_unused:UNUSED_PAD src0_sel:WORD_0
	v_exp_f16_sdwa v29, v25 dst_sel:WORD_0 dst_unused:UNUSED_PAD src0_sel:WORD_0
	v_exp_f16_sdwa v26, v22 dst_sel:WORD_1 dst_unused:UNUSED_PRESERVE src0_sel:WORD_1
	v_exp_f16_sdwa v27, v23 dst_sel:WORD_1 dst_unused:UNUSED_PRESERVE src0_sel:WORD_1
	v_exp_f16_sdwa v28, v24 dst_sel:WORD_1 dst_unused:UNUSED_PRESERVE src0_sel:WORD_1
	v_exp_f16_sdwa v29, v25 dst_sel:WORD_1 dst_unused:UNUSED_PRESERVE src0_sel:WORD_1
	s_nop 0
	v_pk_add_f16 v22, v30, v89
	v_pk_add_f16 v17, v17, v29
	v_pk_add_f16 v16, v16, v28
	v_pk_add_f16 v15, v15, v27
	v_pk_add_f16 v14, v14, v26
	v_pk_fma_f16 v21, v73, v29, v21
	v_pk_fma_f16 v20, v72, v28, v20
	v_pk_fma_f16 v19, v71, v27, v19
	v_pk_fma_f16 v18, v70, v26, v18
	v_pk_add_f16 v23, v31, v88
	v_pk_add_f16 v24, v32, v87
	v_pk_add_f16 v25, v33, v86
	s_nop 0
	v_exp_f16_sdwa v26, v22 dst_sel:WORD_0 dst_unused:UNUSED_PAD src0_sel:WORD_0
	v_exp_f16_sdwa v27, v23 dst_sel:WORD_0 dst_unused:UNUSED_PAD src0_sel:WORD_0
	v_exp_f16_sdwa v28, v24 dst_sel:WORD_0 dst_unused:UNUSED_PAD src0_sel:WORD_0
	v_exp_f16_sdwa v29, v25 dst_sel:WORD_0 dst_unused:UNUSED_PAD src0_sel:WORD_0
	v_exp_f16_sdwa v26, v22 dst_sel:WORD_1 dst_unused:UNUSED_PRESERVE src0_sel:WORD_1
	v_exp_f16_sdwa v27, v23 dst_sel:WORD_1 dst_unused:UNUSED_PRESERVE src0_sel:WORD_1
	v_exp_f16_sdwa v28, v24 dst_sel:WORD_1 dst_unused:UNUSED_PRESERVE src0_sel:WORD_1
	v_exp_f16_sdwa v29, v25 dst_sel:WORD_1 dst_unused:UNUSED_PRESERVE src0_sel:WORD_1
	s_nop 0
	v_pk_add_f16 v22, v42, v89
	v_pk_add_f16 v14, v14, v26
	v_pk_add_f16 v15, v15, v27
	v_pk_add_f16 v16, v16, v28
	v_pk_add_f16 v17, v17, v29
	v_pk_fma_f16 v18, v90, v26, v18
	v_pk_fma_f16 v19, v91, v27, v19
	v_pk_fma_f16 v20, v92, v28, v20
	v_pk_fma_f16 v21, v93, v29, v21
	v_pk_add_f16 v23, v43, v88
	v_pk_add_f16 v24, v44, v87
	v_pk_add_f16 v25, v45, v86
	s_nop 0
	v_exp_f16_sdwa v26, v22 dst_sel:WORD_0 dst_unused:UNUSED_PAD src0_sel:WORD_0
	v_exp_f16_sdwa v27, v23 dst_sel:WORD_0 dst_unused:UNUSED_PAD src0_sel:WORD_0
	v_exp_f16_sdwa v28, v24 dst_sel:WORD_0 dst_unused:UNUSED_PAD src0_sel:WORD_0
	v_exp_f16_sdwa v29, v25 dst_sel:WORD_0 dst_unused:UNUSED_PAD src0_sel:WORD_0
	v_exp_f16_sdwa v26, v22 dst_sel:WORD_1 dst_unused:UNUSED_PRESERVE src0_sel:WORD_1
	v_exp_f16_sdwa v27, v23 dst_sel:WORD_1 dst_unused:UNUSED_PRESERVE src0_sel:WORD_1
	v_exp_f16_sdwa v28, v24 dst_sel:WORD_1 dst_unused:UNUSED_PRESERVE src0_sel:WORD_1
	v_exp_f16_sdwa v29, v25 dst_sel:WORD_1 dst_unused:UNUSED_PRESERVE src0_sel:WORD_1
	s_nop 0
	v_pk_add_f16 v22, v58, v89
	v_pk_add_f16 v17, v17, v29
	v_pk_add_f16 v16, v16, v28
	v_pk_add_f16 v15, v15, v27
	v_pk_add_f16 v14, v14, v26
	v_pk_fma_f16 v21, v113, v29, v21
	v_pk_fma_f16 v20, v112, v28, v20
	v_pk_fma_f16 v19, v111, v27, v19
	v_pk_fma_f16 v18, v110, v26, v18
	v_pk_add_f16 v23, v59, v88
	v_pk_add_f16 v24, v60, v87
	v_pk_add_f16 v25, v61, v86
	s_nop 0
	v_exp_f16_sdwa v30, v22 dst_sel:WORD_0 dst_unused:UNUSED_PAD src0_sel:WORD_0
	v_exp_f16_sdwa v31, v23 dst_sel:WORD_0 dst_unused:UNUSED_PAD src0_sel:WORD_0
	v_exp_f16_sdwa v32, v24 dst_sel:WORD_0 dst_unused:UNUSED_PAD src0_sel:WORD_0
	v_exp_f16_sdwa v33, v25 dst_sel:WORD_0 dst_unused:UNUSED_PAD src0_sel:WORD_0
	v_exp_f16_sdwa v30, v22 dst_sel:WORD_1 dst_unused:UNUSED_PRESERVE src0_sel:WORD_1
	v_exp_f16_sdwa v31, v23 dst_sel:WORD_1 dst_unused:UNUSED_PRESERVE src0_sel:WORD_1
	v_exp_f16_sdwa v32, v24 dst_sel:WORD_1 dst_unused:UNUSED_PRESERVE src0_sel:WORD_1
	v_exp_f16_sdwa v33, v25 dst_sel:WORD_1 dst_unused:UNUSED_PRESERVE src0_sel:WORD_1
	s_nop 0
.LBB4_42:
	s_and_b64 vcc, exec, s[4:5]
	s_cbranch_vccz .LBB4_80
	global_load_dwordx3 v[146:148], v169, s[8:9]
	v_cmp_lt_u32_e64 s[64:65], 0, v199
	v_cmp_gt_u32_e64 s[66:67], 63, v199
	v_cmp_lt_u32_e64 s[68:69], 0, v180
	v_cmp_gt_u32_e64 s[70:71], 60, v180
	buffer_load_dwordx4 v[162:165], v200, s[36:39], 0 offen
	v_add_u32_e32 v246, 0x18000, v200
	buffer_load_dwordx4 v[154:157], v246, s[36:39], 0 offen
	v_add_u32_e32 v245, 0x30000, v200
	buffer_load_dwordx4 v[150:153], v245, s[36:39], 0 offen
	s_and_b64 s[72:73], s[68:69], s[64:65]
	s_and_b64 s[74:75], s[68:69], s[66:67]
	s_and_b64 s[76:77], s[70:71], s[64:65]
	s_and_b64 s[78:79], s[70:71], s[66:67]
	v_add_u32_e32 v245, 0xfffe7c00, v200
	v_add_u32_e32 v246, 0xfffe8000, v200
	v_mov_b32_e32 v114, v6
	v_mov_b32_e32 v115, v7
	v_mov_b32_e32 v116, v8
	v_mov_b32_e32 v117, v9
	v_mov_b32_e32 v74, v2
	v_mov_b32_e32 v75, v3
	v_mov_b32_e32 v76, v4
	v_mov_b32_e32 v77, v5
	v_mov_b32_e32 v130, v6
	v_mov_b32_e32 v131, v7
	v_mov_b32_e32 v132, v8
	v_mov_b32_e32 v133, v9
	v_mov_b32_e32 v98, v2
	v_mov_b32_e32 v99, v3
	v_mov_b32_e32 v100, v4
	v_mov_b32_e32 v101, v5
	v_mov_b32_e32 v138, v6
	v_mov_b32_e32 v139, v7
	v_mov_b32_e32 v140, v8
	v_mov_b32_e32 v141, v9
	v_mov_b32_e32 v118, v2
	v_mov_b32_e32 v119, v3
	v_mov_b32_e32 v120, v4
	v_mov_b32_e32 v121, v5
	s_mov_b64 exec, s[72:73]
	buffer_load_dwordx4 v[114:117], v245, s[36:39], 0 offen
	buffer_load_dwordx4 v[74:77], v245, s[36:39], 0 offen offset:512
	s_mov_b64 exec, -1
	s_mov_b64 exec, s[68:69]
	buffer_load_dwordx4 v[130:133], v246, s[36:39], 0 offen offset:512
	buffer_load_dwordx4 v[98:101], v246, s[36:39], 0 offen offset:1024
	s_mov_b64 exec, -1
	s_mov_b64 exec, s[74:75]
	buffer_load_dwordx4 v[138:141], v246, s[36:39], 0 offen offset:2048
	buffer_load_dwordx4 v[118:121], v246, s[36:39], 0 offen offset:2560
	s_mov_b64 exec, -1
	v_add_u32_e32 v245, 0xfffffc00, v200
	v_mov_b32_e32 v86, v6
	v_mov_b32_e32 v87, v7
	v_mov_b32_e32 v88, v8
	v_mov_b32_e32 v89, v9
	v_mov_b32_e32 v46, v2
	v_mov_b32_e32 v47, v3
	v_mov_b32_e32 v48, v4
	v_mov_b32_e32 v49, v5
	v_mov_b32_e32 v126, v6
	v_mov_b32_e32 v127, v7
	v_mov_b32_e32 v128, v8
	v_mov_b32_e32 v129, v9
	v_mov_b32_e32 v90, v2
	v_mov_b32_e32 v91, v3
	v_mov_b32_e32 v92, v4
	v_mov_b32_e32 v93, v5
	s_mov_b64 exec, s[64:65]
	buffer_load_dwordx4 v[86:89], v245, s[36:39], 0 offen
	buffer_load_dwordx4 v[46:49], v245, s[36:39], 0 offen offset:512
	s_mov_b64 exec, -1
	buffer_load_dwordx4 v[110:113], v200, s[36:39], 0 offen offset:512
	buffer_load_dwordx4 v[66:69], v200, s[36:39], 0 offen offset:1024
	s_mov_b64 exec, s[66:67]
	buffer_load_dwordx4 v[126:129], v200, s[36:39], 0 offen offset:2048
	buffer_load_dwordx4 v[90:93], v200, s[36:39], 0 offen offset:2560
	s_mov_b64 exec, -1
	v_add_u32_e32 v245, 0x17c00, v200
	v_add_u32_e32 v246, 0x18000, v200
	v_mov_b32_e32 v54, v6
	v_mov_b32_e32 v55, v7
	v_mov_b32_e32 v56, v8
	v_mov_b32_e32 v57, v9
	v_mov_b32_e32 v22, v2
	v_mov_b32_e32 v23, v3
	v_mov_b32_e32 v24, v4
	v_mov_b32_e32 v25, v5
	v_mov_b32_e32 v94, v6
	v_mov_b32_e32 v95, v7
	v_mov_b32_e32 v96, v8
	v_mov_b32_e32 v97, v9
	v_mov_b32_e32 v50, v2
	v_mov_b32_e32 v51, v3
	v_mov_b32_e32 v52, v4
	v_mov_b32_e32 v53, v5
	s_mov_b64 exec, s[64:65]
	buffer_load_dwordx4 v[54:57], v245, s[36:39], 0 offen
	buffer_load_dwordx4 v[22:25], v245, s[36:39], 0 offen offset:512
	s_mov_b64 exec, -1
	buffer_load_dwordx4 v[70:73], v246, s[36:39], 0 offen offset:512
	buffer_load_dwordx4 v[34:37], v246, s[36:39], 0 offen offset:1024
	s_mov_b64 exec, s[66:67]
	buffer_load_dwordx4 v[94:97], v246, s[36:39], 0 offen offset:2048
	buffer_load_dwordx4 v[50:53], v246, s[36:39], 0 offen offset:2560
	s_mov_b64 exec, -1
	v_add_u32_e32 v245, 0x2fc00, v200
	v_add_u32_e32 v246, 0x30000, v200
	v_mov_b32_e32 v26, v6
	v_mov_b32_e32 v27, v7
	v_mov_b32_e32 v28, v8
	v_mov_b32_e32 v29, v9
	v_mov_b32_e32 v10, v2
	v_mov_b32_e32 v11, v3
	v_mov_b32_e32 v12, v4
	v_mov_b32_e32 v13, v5
	v_mov_b32_e32 v58, v6
	v_mov_b32_e32 v59, v7
	v_mov_b32_e32 v60, v8
	v_mov_b32_e32 v61, v9
	v_mov_b32_e32 v18, v2
	v_mov_b32_e32 v19, v3
	v_mov_b32_e32 v20, v4
	v_mov_b32_e32 v21, v5
	s_mov_b64 exec, s[64:65]
	buffer_load_dwordx4 v[26:29], v245, s[36:39], 0 offen
	buffer_load_dwordx4 v[10:13], v245, s[36:39], 0 offen offset:512
	s_mov_b64 exec, -1
	buffer_load_dwordx4 v[38:41], v246, s[36:39], 0 offen offset:512
	buffer_load_dwordx4 v[14:17], v246, s[36:39], 0 offen offset:1024
	s_mov_b64 exec, s[66:67]
	buffer_load_dwordx4 v[58:61], v246, s[36:39], 0 offen offset:2048
	buffer_load_dwordx4 v[18:21], v246, s[36:39], 0 offen offset:2560
	s_mov_b64 exec, -1
	v_add_u32_e32 v245, 0x47c00, v200
	v_add_u32_e32 v246, 0x48000, v200
	v_mov_b32_e32 v78, v6
	v_mov_b32_e32 v79, v7
	v_mov_b32_e32 v80, v8
	v_mov_b32_e32 v81, v9
	v_mov_b32_e32 v30, v2
	v_mov_b32_e32 v31, v3
	v_mov_b32_e32 v32, v4
	v_mov_b32_e32 v33, v5
	v_mov_b32_e32 v122, v6
	v_mov_b32_e32 v123, v7
	v_mov_b32_e32 v124, v8
	v_mov_b32_e32 v125, v9
	v_mov_b32_e32 v62, v2
	v_mov_b32_e32 v63, v3
	v_mov_b32_e32 v64, v4
	v_mov_b32_e32 v65, v5
	s_mov_b64 exec, s[64:65]
	buffer_load_dwordx4 v[78:81], v245, s[36:39], 0 offen
	buffer_load_dwordx4 v[30:33], v245, s[36:39], 0 offen offset:512
	s_mov_b64 exec, -1
	buffer_load_dwordx4 v[106:109], v246, s[36:39], 0 offen offset:512
	buffer_load_dwordx4 v[42:45], v246, s[36:39], 0 offen offset:1024
	s_mov_b64 exec, s[66:67]
	buffer_load_dwordx4 v[122:125], v246, s[36:39], 0 offen offset:2048
	buffer_load_dwordx4 v[62:65], v246, s[36:39], 0 offen offset:2560
	s_mov_b64 exec, -1
	v_add_u32_e32 v245, 0x5fc00, v200
	v_add_u32_e32 v246, 0x60000, v200
	v_mov_b32_e32 v134, v6
	v_mov_b32_e32 v135, v7
	v_mov_b32_e32 v136, v8
	v_mov_b32_e32 v137, v9
	v_mov_b32_e32 v82, v2
	v_mov_b32_e32 v83, v3
	v_mov_b32_e32 v84, v4
	v_mov_b32_e32 v85, v5
	v_mov_b32_e32 v142, v6
	v_mov_b32_e32 v143, v7
	v_mov_b32_e32 v144, v8
	v_mov_b32_e32 v145, v9
	v_mov_b32_e32 v102, v2
	v_mov_b32_e32 v103, v3
	v_mov_b32_e32 v104, v4
	v_mov_b32_e32 v105, v5
	s_mov_b64 exec, s[76:77]
	buffer_load_dwordx4 v[134:137], v245, s[36:39], 0 offen
	buffer_load_dwordx4 v[82:85], v245, s[36:39], 0 offen offset:512
	s_mov_b64 exec, -1
	s_mov_b64 exec, s[70:71]
	buffer_load_dwordx4 v[142:145], v246, s[36:39], 0 offen offset:512
	buffer_load_dwordx4 v[102:105], v246, s[36:39], 0 offen offset:1024
	s_mov_b64 exec, -1
	s_mov_b64 exec, s[78:79]
	buffer_load_dwordx4 v[6:9], v246, s[36:39], 0 offen offset:2048
	buffer_load_dwordx4 v[2:5], v246, s[36:39], 0 offen offset:2560
	s_mov_b64 exec, -1
	s_waitcnt vmcnt(39)
	v_cvt_f16_f32_e32 v158, v147
	v_cvt_f16_f32_e32 v160, v146
	v_cvt_f16_f32_e32 v159, v148
	v_add_u32_e32 v245, 0x48000, v200
	buffer_load_dwordx4 v[146:149], v245, s[36:39], 0 offen
	s_waitcnt vmcnt(19)
	v_pk_mul_f16 v161, v160, v162 op_sel_hi:[0,1]
	v_pk_mul_f16 v204, v160, v165 op_sel_hi:[0,1]
	v_pk_mul_f16 v208, v158, v165 op_sel_hi:[0,1]
	v_pk_mul_f16 v212, v159, v165 op_sel_hi:[0,1]
	v_pk_mul_f16 v202, v160, v163 op_sel_hi:[0,1]
	v_pk_mul_f16 v203, v160, v164 op_sel_hi:[0,1]
	v_pk_mul_f16 v205, v158, v162 op_sel_hi:[0,1]
	v_pk_mul_f16 v206, v158, v163 op_sel_hi:[0,1]
	v_pk_mul_f16 v207, v158, v164 op_sel_hi:[0,1]
	v_pk_mul_f16 v209, v159, v162 op_sel_hi:[0,1]
	v_pk_mul_f16 v210, v159, v163 op_sel_hi:[0,1]
	v_pk_mul_f16 v211, v159, v164 op_sel_hi:[0,1]
	v_pk_fma_f16 v117, v117, v165, v204
	v_pk_fma_f16 v114, v114, v162, v161
	v_pk_fma_f16 v133, v133, v165, v204
	v_pk_fma_f16 v130, v130, v162, v161
	v_pk_fma_f16 v141, v141, v165, v204
	v_pk_fma_f16 v138, v138, v162, v161
	v_pk_fma_f16 v161, v89, v165, v208
	v_pk_fma_f16 v213, v113, v165, v208
	v_pk_fma_f16 v208, v129, v165, v208
	v_pk_fma_f16 v217, v57, v165, v212
	v_pk_fma_f16 v221, v73, v165, v212
	v_pk_fma_f16 v165, v97, v165, v212
	v_pk_maximum3_f16 v212, v117, v133, v141
	v_pk_fma_f16 v116, v116, v164, v203
	v_pk_fma_f16 v115, v115, v163, v202
	v_pk_fma_f16 v132, v132, v164, v203
	v_pk_fma_f16 v131, v131, v163, v202
	v_pk_fma_f16 v140, v140, v164, v203
	v_pk_fma_f16 v139, v139, v163, v202
	v_pk_fma_f16 v202, v88, v164, v207
	v_pk_fma_f16 v203, v87, v163, v206
	v_pk_fma_f16 v204, v86, v162, v205
	v_pk_fma_f16 v214, v112, v164, v207
	v_pk_fma_f16 v215, v111, v163, v206
	v_pk_fma_f16 v216, v110, v162, v205
	v_pk_fma_f16 v207, v128, v164, v207
	v_pk_fma_f16 v206, v127, v163, v206
	v_pk_fma_f16 v205, v126, v162, v205
	v_pk_fma_f16 v218, v56, v164, v211
	v_pk_fma_f16 v219, v55, v163, v210
	v_pk_fma_f16 v220, v54, v162, v209
	v_pk_fma_f16 v222, v72, v164, v211
	v_pk_fma_f16 v223, v71, v163, v210
	v_pk_fma_f16 v224, v70, v162, v209
	v_pk_fma_f16 v164, v96, v164, v211
	v_pk_fma_f16 v163, v95, v163, v210
	v_pk_fma_f16 v162, v94, v162, v209
	v_pk_maximum3_f16 v209, v114, v130, v138
	v_pk_maximum3_f16 v210, v115, v131, v139
	v_pk_maximum3_f16 v211, v116, v132, v140
	v_pk_maximum3_f16 v228, v161, v213, v208
	v_pk_maximum3_f16 v232, v217, v221, v165
	v_pk_maximum3_f16 v225, v204, v216, v205
	v_pk_maximum3_f16 v226, v203, v215, v206
	v_pk_maximum3_f16 v227, v202, v214, v207
	s_nop 0
	v_pk_maximum3_f16 v229, v220, v224, v162
	v_pk_maximum3_f16 v230, v219, v223, v163
	v_pk_maximum3_f16 v212, v212, v228, v232
	v_pk_maximum3_f16 v231, v218, v222, v164
	s_nop 0
	v_pk_maximum3_f16 v209, v209, v225, v229
	v_pk_maximum3_f16 v210, v210, v226, v230
	v_pk_maximum3_f16 v211, v211, v227, v231
	v_xor_b32_e32 v212, 0x80008000, v212
	v_xor_b32_e32 v211, 0x80008000, v211
	v_xor_b32_e32 v210, 0x80008000, v210
	v_xor_b32_e32 v209, 0x80008000, v209
	v_pk_add_f16 v117, v117, v212
	v_pk_add_f16 v114, v114, v209
	v_pk_add_f16 v115, v115, v210
	v_pk_add_f16 v116, v116, v211
	v_pk_add_f16 v130, v130, v209
	v_exp_f16_sdwa v225, v114 dst_sel:WORD_0 dst_unused:UNUSED_PAD src0_sel:WORD_0
	v_exp_f16_sdwa v226, v115 dst_sel:WORD_0 dst_unused:UNUSED_PAD src0_sel:WORD_0
	v_exp_f16_sdwa v227, v116 dst_sel:WORD_0 dst_unused:UNUSED_PAD src0_sel:WORD_0
	v_exp_f16_sdwa v228, v117 dst_sel:WORD_0 dst_unused:UNUSED_PAD src0_sel:WORD_0
	v_exp_f16_sdwa v225, v114 dst_sel:WORD_1 dst_unused:UNUSED_PRESERVE src0_sel:WORD_1
	v_exp_f16_sdwa v226, v115 dst_sel:WORD_1 dst_unused:UNUSED_PRESERVE src0_sel:WORD_1
	v_exp_f16_sdwa v227, v116 dst_sel:WORD_1 dst_unused:UNUSED_PRESERVE src0_sel:WORD_1
	v_exp_f16_sdwa v228, v117 dst_sel:WORD_1 dst_unused:UNUSED_PRESERVE src0_sel:WORD_1
	s_nop 0
	v_pk_add_f16 v131, v131, v210
	v_pk_add_f16 v117, v225, 0
	v_pk_fma_f16 v77, v77, v228, 0
	v_pk_add_f16 v114, v228, 0
	v_pk_add_f16 v115, v227, 0
	v_pk_add_f16 v116, v226, 0
	v_pk_fma_f16 v76, v76, v227, 0
	v_pk_fma_f16 v75, v75, v226, 0
	v_pk_fma_f16 v74, v74, v225, 0
	v_pk_add_f16 v132, v132, v211
	v_pk_add_f16 v133, v133, v212
	s_nop 0
	v_exp_f16_sdwa v225, v130 dst_sel:WORD_0 dst_unused:UNUSED_PAD src0_sel:WORD_0
	v_exp_f16_sdwa v226, v131 dst_sel:WORD_0 dst_unused:UNUSED_PAD src0_sel:WORD_0
	v_exp_f16_sdwa v227, v132 dst_sel:WORD_0 dst_unused:UNUSED_PAD src0_sel:WORD_0
	v_exp_f16_sdwa v228, v133 dst_sel:WORD_0 dst_unused:UNUSED_PAD src0_sel:WORD_0
	v_exp_f16_sdwa v225, v130 dst_sel:WORD_1 dst_unused:UNUSED_PRESERVE src0_sel:WORD_1
	v_exp_f16_sdwa v226, v131 dst_sel:WORD_1 dst_unused:UNUSED_PRESERVE src0_sel:WORD_1
	v_exp_f16_sdwa v227, v132 dst_sel:WORD_1 dst_unused:UNUSED_PRESERVE src0_sel:WORD_1
	v_exp_f16_sdwa v228, v133 dst_sel:WORD_1 dst_unused:UNUSED_PRESERVE src0_sel:WORD_1
	s_nop 0
	s_nop 0
	v_pk_add_f16 v117, v117, v225
	v_pk_fma_f16 v77, v101, v228, v77
	v_pk_add_f16 v101, v141, v212
	v_pk_add_f16 v116, v116, v226
	v_pk_add_f16 v115, v115, v227
	v_pk_add_f16 v114, v114, v228
	v_pk_fma_f16 v74, v98, v225, v74
	v_pk_fma_f16 v75, v99, v226, v75
	v_pk_fma_f16 v76, v100, v227, v76
	v_pk_add_f16 v98, v138, v209
	v_pk_add_f16 v99, v139, v210
	v_pk_add_f16 v100, v140, v211
	s_nop 0
	v_exp_f16_sdwa v130, v98 dst_sel:WORD_0 dst_unused:UNUSED_PAD src0_sel:WORD_0
	v_exp_f16_sdwa v131, v99 dst_sel:WORD_0 dst_unused:UNUSED_PAD src0_sel:WORD_0
	v_exp_f16_sdwa v132, v100 dst_sel:WORD_0 dst_unused:UNUSED_PAD src0_sel:WORD_0
	v_exp_f16_sdwa v133, v101 dst_sel:WORD_0 dst_unused:UNUSED_PAD src0_sel:WORD_0
	v_exp_f16_sdwa v130, v98 dst_sel:WORD_1 dst_unused:UNUSED_PRESERVE src0_sel:WORD_1
	v_exp_f16_sdwa v131, v99 dst_sel:WORD_1 dst_unused:UNUSED_PRESERVE src0_sel:WORD_1
	v_exp_f16_sdwa v132, v100 dst_sel:WORD_1 dst_unused:UNUSED_PRESERVE src0_sel:WORD_1
	v_exp_f16_sdwa v133, v101 dst_sel:WORD_1 dst_unused:UNUSED_PRESERVE src0_sel:WORD_1
	s_nop 0
	s_nop 0
	v_pk_add_f16 v101, v117, v130
	v_pk_add_f16 v98, v114, v133
	v_pk_add_f16 v99, v115, v132
	v_pk_add_f16 v100, v116, v131
	v_pk_fma_f16 v77, v121, v133, v77
	v_pk_fma_f16 v76, v120, v132, v76
	v_pk_fma_f16 v75, v119, v131, v75
	v_pk_fma_f16 v74, v118, v130, v74
	v_pk_add_f16 v114, v204, v209
	v_pk_add_f16 v115, v203, v210
	v_pk_add_f16 v116, v202, v211
	v_pk_add_f16 v117, v161, v212
	s_nop 0
	v_exp_f16_sdwa v118, v114 dst_sel:WORD_0 dst_unused:UNUSED_PAD src0_sel:WORD_0
	v_exp_f16_sdwa v119, v115 dst_sel:WORD_0 dst_unused:UNUSED_PAD src0_sel:WORD_0
	v_exp_f16_sdwa v120, v116 dst_sel:WORD_0 dst_unused:UNUSED_PAD src0_sel:WORD_0
	v_exp_f16_sdwa v121, v117 dst_sel:WORD_0 dst_unused:UNUSED_PAD src0_sel:WORD_0
	v_exp_f16_sdwa v118, v114 dst_sel:WORD_1 dst_unused:UNUSED_PRESERVE src0_sel:WORD_1
	v_exp_f16_sdwa v119, v115 dst_sel:WORD_1 dst_unused:UNUSED_PRESERVE src0_sel:WORD_1
	v_exp_f16_sdwa v120, v116 dst_sel:WORD_1 dst_unused:UNUSED_PRESERVE src0_sel:WORD_1
	v_exp_f16_sdwa v121, v117 dst_sel:WORD_1 dst_unused:UNUSED_PRESERVE src0_sel:WORD_1
	s_nop 0
	v_pk_add_f16 v114, v216, v209
	v_pk_add_f16 v101, v101, v118
	v_pk_add_f16 v100, v100, v119
	v_pk_add_f16 v99, v99, v120
	v_pk_add_f16 v98, v98, v121
	v_pk_fma_f16 v74, v46, v118, v74
	v_pk_fma_f16 v75, v47, v119, v75
	v_pk_fma_f16 v76, v48, v120, v76
	v_pk_fma_f16 v77, v49, v121, v77
	v_pk_add_f16 v115, v215, v210
	v_pk_add_f16 v116, v214, v211
	v_pk_add_f16 v117, v213, v212
	s_nop 0
	v_exp_f16_sdwa v118, v114 dst_sel:WORD_0 dst_unused:UNUSED_PAD src0_sel:WORD_0
	v_exp_f16_sdwa v119, v115 dst_sel:WORD_0 dst_unused:UNUSED_PAD src0_sel:WORD_0
	v_exp_f16_sdwa v120, v116 dst_sel:WORD_0 dst_unused:UNUSED_PAD src0_sel:WORD_0
	v_exp_f16_sdwa v121, v117 dst_sel:WORD_0 dst_unused:UNUSED_PAD src0_sel:WORD_0
	v_exp_f16_sdwa v118, v114 dst_sel:WORD_1 dst_unused:UNUSED_PRESERVE src0_sel:WORD_1
	v_exp_f16_sdwa v119, v115 dst_sel:WORD_1 dst_unused:UNUSED_PRESERVE src0_sel:WORD_1
	v_exp_f16_sdwa v120, v116 dst_sel:WORD_1 dst_unused:UNUSED_PRESERVE src0_sel:WORD_1
	v_exp_f16_sdwa v121, v117 dst_sel:WORD_1 dst_unused:UNUSED_PRESERVE src0_sel:WORD_1
	s_nop 0
	v_pk_add_f16 v114, v205, v209
	v_pk_add_f16 v101, v101, v118
	v_pk_add_f16 v98, v98, v121
	v_pk_add_f16 v99, v99, v120
	v_pk_add_f16 v100, v100, v119
	v_pk_fma_f16 v77, v69, v121, v77
	v_pk_fma_f16 v76, v68, v120, v76
	v_pk_fma_f16 v75, v67, v119, v75
	v_pk_fma_f16 v74, v66, v118, v74
	v_pk_add_f16 v115, v206, v210
	v_pk_add_f16 v116, v207, v211
	v_pk_add_f16 v117, v208, v212
	s_nop 0
	v_exp_f16_sdwa v118, v114 dst_sel:WORD_0 dst_unused:UNUSED_PAD src0_sel:WORD_0
	v_exp_f16_sdwa v119, v115 dst_sel:WORD_0 dst_unused:UNUSED_PAD src0_sel:WORD_0
	v_exp_f16_sdwa v120, v116 dst_sel:WORD_0 dst_unused:UNUSED_PAD src0_sel:WORD_0
	v_exp_f16_sdwa v121, v117 dst_sel:WORD_0 dst_unused:UNUSED_PAD src0_sel:WORD_0
	v_exp_f16_sdwa v118, v114 dst_sel:WORD_1 dst_unused:UNUSED_PRESERVE src0_sel:WORD_1
	v_exp_f16_sdwa v119, v115 dst_sel:WORD_1 dst_unused:UNUSED_PRESERVE src0_sel:WORD_1
	v_exp_f16_sdwa v120, v116 dst_sel:WORD_1 dst_unused:UNUSED_PRESERVE src0_sel:WORD_1
	v_exp_f16_sdwa v121, v117 dst_sel:WORD_1 dst_unused:UNUSED_PRESERVE src0_sel:WORD_1
	s_nop 0
	v_pk_add_f16 v114, v220, v209
	v_pk_add_f16 v101, v101, v118
	v_pk_add_f16 v100, v100, v119
	v_pk_add_f16 v99, v99, v120
	v_pk_add_f16 v98, v98, v121
	v_pk_fma_f16 v74, v90, v118, v74
	v_pk_fma_f16 v75, v91, v119, v75
	v_pk_fma_f16 v76, v92, v120, v76
	v_pk_fma_f16 v77, v93, v121, v77
	v_pk_add_f16 v115, v219, v210
	v_pk_add_f16 v116, v218, v211
	v_pk_add_f16 v117, v217, v212
	s_nop 0
	v_exp_f16_sdwa v118, v114 dst_sel:WORD_0 dst_unused:UNUSED_PAD src0_sel:WORD_0
	v_exp_f16_sdwa v119, v115 dst_sel:WORD_0 dst_unused:UNUSED_PAD src0_sel:WORD_0
	v_exp_f16_sdwa v120, v116 dst_sel:WORD_0 dst_unused:UNUSED_PAD src0_sel:WORD_0
	v_exp_f16_sdwa v121, v117 dst_sel:WORD_0 dst_unused:UNUSED_PAD src0_sel:WORD_0
	v_exp_f16_sdwa v118, v114 dst_sel:WORD_1 dst_unused:UNUSED_PRESERVE src0_sel:WORD_1
	v_exp_f16_sdwa v119, v115 dst_sel:WORD_1 dst_unused:UNUSED_PRESERVE src0_sel:WORD_1
	v_exp_f16_sdwa v120, v116 dst_sel:WORD_1 dst_unused:UNUSED_PRESERVE src0_sel:WORD_1
	v_exp_f16_sdwa v121, v117 dst_sel:WORD_1 dst_unused:UNUSED_PRESERVE src0_sel:WORD_1
	s_nop 0
	v_pk_add_f16 v114, v224, v209
	v_pk_add_f16 v101, v101, v118
	v_pk_add_f16 v98, v98, v121
	v_pk_add_f16 v99, v99, v120
	v_pk_add_f16 v100, v100, v119
	v_pk_fma_f16 v77, v25, v121, v77
	v_pk_fma_f16 v76, v24, v120, v76
	v_pk_fma_f16 v75, v23, v119, v75
	v_pk_fma_f16 v74, v22, v118, v74
	v_pk_add_f16 v115, v223, v210
	v_pk_add_f16 v116, v222, v211
	v_pk_add_f16 v117, v221, v212
	s_nop 0
	v_exp_f16_sdwa v118, v114 dst_sel:WORD_0 dst_unused:UNUSED_PAD src0_sel:WORD_0
	v_exp_f16_sdwa v119, v115 dst_sel:WORD_0 dst_unused:UNUSED_PAD src0_sel:WORD_0
	v_exp_f16_sdwa v120, v116 dst_sel:WORD_0 dst_unused:UNUSED_PAD src0_sel:WORD_0
	v_exp_f16_sdwa v121, v117 dst_sel:WORD_0 dst_unused:UNUSED_PAD src0_sel:WORD_0
	v_exp_f16_sdwa v118, v114 dst_sel:WORD_1 dst_unused:UNUSED_PRESERVE src0_sel:WORD_1
	v_exp_f16_sdwa v119, v115 dst_sel:WORD_1 dst_unused:UNUSED_PRESERVE src0_sel:WORD_1
	v_exp_f16_sdwa v120, v116 dst_sel:WORD_1 dst_unused:UNUSED_PRESERVE src0_sel:WORD_1
	v_exp_f16_sdwa v121, v117 dst_sel:WORD_1 dst_unused:UNUSED_PRESERVE src0_sel:WORD_1
	s_nop 0
	v_pk_add_f16 v114, v162, v209
	v_pk_add_f16 v101, v101, v118
	v_pk_add_f16 v100, v100, v119
	v_pk_add_f16 v99, v99, v120
	v_pk_add_f16 v98, v98, v121
	v_pk_fma_f16 v74, v34, v118, v74
	v_pk_fma_f16 v75, v35, v119, v75
	v_pk_fma_f16 v76, v36, v120, v76
	v_pk_fma_f16 v77, v37, v121, v77
	v_pk_add_f16 v115, v163, v210
	v_pk_add_f16 v116, v164, v211
	v_pk_add_f16 v117, v165, v212
	s_nop 0
	v_exp_f16_sdwa v118, v114 dst_sel:WORD_0 dst_unused:UNUSED_PAD src0_sel:WORD_0
	v_exp_f16_sdwa v119, v115 dst_sel:WORD_0 dst_unused:UNUSED_PAD src0_sel:WORD_0
	v_exp_f16_sdwa v120, v116 dst_sel:WORD_0 dst_unused:UNUSED_PAD src0_sel:WORD_0
	v_exp_f16_sdwa v121, v117 dst_sel:WORD_0 dst_unused:UNUSED_PAD src0_sel:WORD_0
	v_exp_f16_sdwa v118, v114 dst_sel:WORD_1 dst_unused:UNUSED_PRESERVE src0_sel:WORD_1
	v_exp_f16_sdwa v119, v115 dst_sel:WORD_1 dst_unused:UNUSED_PRESERVE src0_sel:WORD_1
	v_exp_f16_sdwa v120, v116 dst_sel:WORD_1 dst_unused:UNUSED_PRESERVE src0_sel:WORD_1
	v_exp_f16_sdwa v121, v117 dst_sel:WORD_1 dst_unused:UNUSED_PRESERVE src0_sel:WORD_1
	s_nop 0
	s_nop 0
	v_pk_add_f16 v101, v101, v118
	v_pk_add_f16 v100, v100, v119
	v_rcp_f16_e32 v114, v101
	v_rcp_f16_sdwa v101, v101 dst_sel:DWORD dst_unused:UNUSED_PAD src0_sel:WORD_1
	v_pk_add_f16 v99, v99, v120
	v_rcp_f16_e32 v115, v100
	v_rcp_f16_sdwa v100, v100 dst_sel:DWORD dst_unused:UNUSED_PAD src0_sel:WORD_1
	v_pk_add_f16 v98, v98, v121
	v_rcp_f16_e32 v116, v99
	v_rcp_f16_sdwa v99, v99 dst_sel:DWORD dst_unused:UNUSED_PAD src0_sel:WORD_1
	v_rcp_f16_e32 v117, v98
	v_rcp_f16_sdwa v98, v98 dst_sel:DWORD dst_unused:UNUSED_PAD src0_sel:WORD_1
	v_pk_fma_f16 v74, v50, v118, v74
	v_pack_b32_f16 v101, v114, v101
	v_pk_fma_f16 v75, v51, v119, v75
	v_pk_mul_f16 v138, v74, v101
	v_pack_b32_f16 v74, v115, v100
	v_pk_fma_f16 v76, v52, v120, v76
	v_pk_mul_f16 v139, v75, v74
	v_pack_b32_f16 v74, v116, v99
	v_pk_fma_f16 v77, v53, v121, v77
	v_pk_mul_f16 v140, v76, v74
	v_pack_b32_f16 v74, v117, v98
	v_pk_mul_f16 v141, v77, v74
	s_waitcnt vmcnt(13)
	v_pk_mul_f16 v74, v160, v154 op_sel_hi:[0,1]
	v_pk_mul_f16 v77, v160, v157 op_sel_hi:[0,1]
	v_pk_mul_f16 v101, v158, v157 op_sel_hi:[0,1]
	v_pk_mul_f16 v117, v159, v157 op_sel_hi:[0,1]
	v_pk_mul_f16 v75, v160, v155 op_sel_hi:[0,1]
	v_pk_mul_f16 v76, v160, v156 op_sel_hi:[0,1]
	v_pk_mul_f16 v98, v158, v154 op_sel_hi:[0,1]
	v_pk_mul_f16 v99, v158, v155 op_sel_hi:[0,1]
	v_pk_mul_f16 v100, v158, v156 op_sel_hi:[0,1]
	v_pk_mul_f16 v114, v159, v154 op_sel_hi:[0,1]
	v_pk_mul_f16 v115, v159, v155 op_sel_hi:[0,1]
	v_pk_mul_f16 v116, v159, v156 op_sel_hi:[0,1]
	v_pk_fma_f16 v89, v89, v157, v77
	v_pk_fma_f16 v86, v86, v154, v74
	v_pk_fma_f16 v113, v113, v157, v77
	v_pk_fma_f16 v110, v110, v154, v74
	v_pk_fma_f16 v77, v129, v157, v77
	v_pk_fma_f16 v74, v126, v154, v74
	v_pk_fma_f16 v118, v57, v157, v101
	v_pk_fma_f16 v126, v73, v157, v101
	v_pk_fma_f16 v101, v97, v157, v101
	v_pk_fma_f16 v130, v29, v157, v117
	v_pk_fma_f16 v161, v41, v157, v117
	v_pk_fma_f16 v117, v61, v157, v117
	v_pk_maximum3_f16 v157, v89, v113, v77
	v_pk_fma_f16 v88, v88, v156, v76
	v_pk_fma_f16 v87, v87, v155, v75
	v_pk_fma_f16 v112, v112, v156, v76
	v_pk_fma_f16 v111, v111, v155, v75
	v_pk_fma_f16 v76, v128, v156, v76
	v_pk_fma_f16 v75, v127, v155, v75
	v_pk_fma_f16 v119, v56, v156, v100
	v_pk_fma_f16 v120, v55, v155, v99
	v_pk_fma_f16 v121, v54, v154, v98
	v_pk_fma_f16 v127, v72, v156, v100
	v_pk_fma_f16 v128, v71, v155, v99
	v_pk_fma_f16 v129, v70, v154, v98
	v_pk_fma_f16 v100, v96, v156, v100
	v_pk_fma_f16 v99, v95, v155, v99
	v_pk_fma_f16 v98, v94, v154, v98
	v_pk_fma_f16 v131, v28, v156, v116
	v_pk_fma_f16 v132, v27, v155, v115
	v_pk_fma_f16 v133, v26, v154, v114
	v_pk_fma_f16 v162, v40, v156, v116
	v_pk_fma_f16 v163, v39, v155, v115
	v_pk_fma_f16 v164, v38, v154, v114
	v_pk_fma_f16 v116, v60, v156, v116
	v_pk_fma_f16 v115, v59, v155, v115
	v_pk_fma_f16 v114, v58, v154, v114
	v_pk_maximum3_f16 v154, v86, v110, v74
	v_pk_maximum3_f16 v155, v87, v111, v75
	v_pk_maximum3_f16 v156, v88, v112, v76
	v_pk_maximum3_f16 v204, v118, v126, v101
	v_pk_maximum3_f16 v208, v130, v161, v117
	v_pk_maximum3_f16 v165, v121, v129, v98
	v_pk_maximum3_f16 v202, v120, v128, v99
	v_pk_maximum3_f16 v203, v119, v127, v100
	s_nop 0
	v_pk_maximum3_f16 v205, v133, v164, v114
	v_pk_maximum3_f16 v206, v132, v163, v115
	v_pk_maximum3_f16 v157, v157, v204, v208
	v_pk_maximum3_f16 v207, v131, v162, v116
	s_nop 0
	v_pk_maximum3_f16 v154, v154, v165, v205
	v_pk_maximum3_f16 v155, v155, v202, v206
	v_pk_maximum3_f16 v156, v156, v203, v207
	v_xor_b32_e32 v157, 0x80008000, v157
	v_xor_b32_e32 v156, 0x80008000, v156
	v_xor_b32_e32 v155, 0x80008000, v155
	v_xor_b32_e32 v154, 0x80008000, v154
	v_pk_add_f16 v89, v89, v157
	v_pk_add_f16 v86, v86, v154
	v_pk_add_f16 v87, v87, v155
	v_pk_add_f16 v88, v88, v156
	v_pk_add_f16 v110, v110, v154
	v_exp_f16_sdwa v165, v86 dst_sel:WORD_0 dst_unused:UNUSED_PAD src0_sel:WORD_0
	v_exp_f16_sdwa v202, v87 dst_sel:WORD_0 dst_unused:UNUSED_PAD src0_sel:WORD_0
	v_exp_f16_sdwa v203, v88 dst_sel:WORD_0 dst_unused:UNUSED_PAD src0_sel:WORD_0
	v_exp_f16_sdwa v204, v89 dst_sel:WORD_0 dst_unused:UNUSED_PAD src0_sel:WORD_0
	v_exp_f16_sdwa v165, v86 dst_sel:WORD_1 dst_unused:UNUSED_PRESERVE src0_sel:WORD_1
	v_exp_f16_sdwa v202, v87 dst_sel:WORD_1 dst_unused:UNUSED_PRESERVE src0_sel:WORD_1
	v_exp_f16_sdwa v203, v88 dst_sel:WORD_1 dst_unused:UNUSED_PRESERVE src0_sel:WORD_1
	v_exp_f16_sdwa v204, v89 dst_sel:WORD_1 dst_unused:UNUSED_PRESERVE src0_sel:WORD_1
	s_nop 0
	v_pk_add_f16 v111, v111, v155
	v_pk_add_f16 v89, v165, 0
	v_pk_fma_f16 v49, v49, v204, 0
	v_pk_add_f16 v86, v204, 0
	v_pk_add_f16 v87, v203, 0
	v_pk_add_f16 v88, v202, 0
	v_pk_fma_f16 v48, v48, v203, 0
	v_pk_fma_f16 v47, v47, v202, 0
	v_pk_fma_f16 v46, v46, v165, 0
	v_pk_add_f16 v112, v112, v156
	v_pk_add_f16 v113, v113, v157
	s_nop 0
	v_exp_f16_sdwa v165, v110 dst_sel:WORD_0 dst_unused:UNUSED_PAD src0_sel:WORD_0
	v_exp_f16_sdwa v202, v111 dst_sel:WORD_0 dst_unused:UNUSED_PAD src0_sel:WORD_0
	v_exp_f16_sdwa v203, v112 dst_sel:WORD_0 dst_unused:UNUSED_PAD src0_sel:WORD_0
	v_exp_f16_sdwa v204, v113 dst_sel:WORD_0 dst_unused:UNUSED_PAD src0_sel:WORD_0
	v_exp_f16_sdwa v165, v110 dst_sel:WORD_1 dst_unused:UNUSED_PRESERVE src0_sel:WORD_1
	v_exp_f16_sdwa v202, v111 dst_sel:WORD_1 dst_unused:UNUSED_PRESERVE src0_sel:WORD_1
	v_exp_f16_sdwa v203, v112 dst_sel:WORD_1 dst_unused:UNUSED_PRESERVE src0_sel:WORD_1
	v_exp_f16_sdwa v204, v113 dst_sel:WORD_1 dst_unused:UNUSED_PRESERVE src0_sel:WORD_1
	s_nop 0
	s_nop 0
	v_pk_add_f16 v89, v89, v165
	v_pk_fma_f16 v49, v69, v204, v49
	v_pk_add_f16 v69, v77, v157
	v_pk_add_f16 v88, v88, v202
	v_pk_add_f16 v87, v87, v203
	v_pk_add_f16 v86, v86, v204
	v_pk_fma_f16 v46, v66, v165, v46
	v_pk_fma_f16 v47, v67, v202, v47
	v_pk_fma_f16 v48, v68, v203, v48
	v_pk_add_f16 v66, v74, v154
	v_pk_add_f16 v67, v75, v155
	v_pk_add_f16 v68, v76, v156
	s_nop 0
	v_exp_f16_sdwa v74, v66 dst_sel:WORD_0 dst_unused:UNUSED_PAD src0_sel:WORD_0
	v_exp_f16_sdwa v75, v67 dst_sel:WORD_0 dst_unused:UNUSED_PAD src0_sel:WORD_0
	v_exp_f16_sdwa v76, v68 dst_sel:WORD_0 dst_unused:UNUSED_PAD src0_sel:WORD_0
	v_exp_f16_sdwa v77, v69 dst_sel:WORD_0 dst_unused:UNUSED_PAD src0_sel:WORD_0
	v_exp_f16_sdwa v74, v66 dst_sel:WORD_1 dst_unused:UNUSED_PRESERVE src0_sel:WORD_1
	v_exp_f16_sdwa v75, v67 dst_sel:WORD_1 dst_unused:UNUSED_PRESERVE src0_sel:WORD_1
	v_exp_f16_sdwa v76, v68 dst_sel:WORD_1 dst_unused:UNUSED_PRESERVE src0_sel:WORD_1
	v_exp_f16_sdwa v77, v69 dst_sel:WORD_1 dst_unused:UNUSED_PRESERVE src0_sel:WORD_1
	s_nop 0
	s_nop 0
	v_pk_add_f16 v69, v89, v74
	v_pk_add_f16 v66, v86, v77
	v_pk_add_f16 v67, v87, v76
	v_pk_add_f16 v68, v88, v75
	v_pk_fma_f16 v49, v93, v77, v49
	v_pk_fma_f16 v48, v92, v76, v48
	v_pk_fma_f16 v47, v91, v75, v47
	v_pk_fma_f16 v46, v90, v74, v46
	v_pk_add_f16 v74, v121, v154
	v_pk_add_f16 v75, v120, v155
	v_pk_add_f16 v76, v119, v156
	v_pk_add_f16 v77, v118, v157
	s_nop 0
	v_exp_f16_sdwa v86, v74 dst_sel:WORD_0 dst_unused:UNUSED_PAD src0_sel:WORD_0
	v_exp_f16_sdwa v87, v75 dst_sel:WORD_0 dst_unused:UNUSED_PAD src0_sel:WORD_0
	v_exp_f16_sdwa v88, v76 dst_sel:WORD_0 dst_unused:UNUSED_PAD src0_sel:WORD_0
	v_exp_f16_sdwa v89, v77 dst_sel:WORD_0 dst_unused:UNUSED_PAD src0_sel:WORD_0
	v_exp_f16_sdwa v86, v74 dst_sel:WORD_1 dst_unused:UNUSED_PRESERVE src0_sel:WORD_1
	v_exp_f16_sdwa v87, v75 dst_sel:WORD_1 dst_unused:UNUSED_PRESERVE src0_sel:WORD_1
	v_exp_f16_sdwa v88, v76 dst_sel:WORD_1 dst_unused:UNUSED_PRESERVE src0_sel:WORD_1
	v_exp_f16_sdwa v89, v77 dst_sel:WORD_1 dst_unused:UNUSED_PRESERVE src0_sel:WORD_1
	s_nop 0
	v_pk_add_f16 v74, v129, v154
	v_pk_add_f16 v69, v69, v86
	v_pk_add_f16 v68, v68, v87
	v_pk_add_f16 v67, v67, v88
	v_pk_add_f16 v66, v66, v89
	v_pk_fma_f16 v46, v22, v86, v46
	v_pk_fma_f16 v47, v23, v87, v47
	v_pk_fma_f16 v48, v24, v88, v48
	v_pk_fma_f16 v49, v25, v89, v49
	v_pk_add_f16 v75, v128, v155
	v_pk_add_f16 v76, v127, v156
	v_pk_add_f16 v77, v126, v157
	s_nop 0
	v_exp_f16_sdwa v86, v74 dst_sel:WORD_0 dst_unused:UNUSED_PAD src0_sel:WORD_0
	v_exp_f16_sdwa v87, v75 dst_sel:WORD_0 dst_unused:UNUSED_PAD src0_sel:WORD_0
	v_exp_f16_sdwa v88, v76 dst_sel:WORD_0 dst_unused:UNUSED_PAD src0_sel:WORD_0
	v_exp_f16_sdwa v89, v77 dst_sel:WORD_0 dst_unused:UNUSED_PAD src0_sel:WORD_0
	v_exp_f16_sdwa v86, v74 dst_sel:WORD_1 dst_unused:UNUSED_PRESERVE src0_sel:WORD_1
	v_exp_f16_sdwa v87, v75 dst_sel:WORD_1 dst_unused:UNUSED_PRESERVE src0_sel:WORD_1
	v_exp_f16_sdwa v88, v76 dst_sel:WORD_1 dst_unused:UNUSED_PRESERVE src0_sel:WORD_1
	v_exp_f16_sdwa v89, v77 dst_sel:WORD_1 dst_unused:UNUSED_PRESERVE src0_sel:WORD_1
	s_nop 0
	v_pk_add_f16 v74, v98, v154
	v_pk_add_f16 v69, v69, v86
	v_pk_add_f16 v66, v66, v89
	v_pk_add_f16 v67, v67, v88
	v_pk_add_f16 v68, v68, v87
	v_pk_fma_f16 v49, v37, v89, v49
	v_pk_fma_f16 v48, v36, v88, v48
	v_pk_fma_f16 v47, v35, v87, v47
	v_pk_fma_f16 v46, v34, v86, v46
	v_pk_add_f16 v75, v99, v155
	v_pk_add_f16 v76, v100, v156
	v_pk_add_f16 v77, v101, v157
	s_nop 0
	v_exp_f16_sdwa v86, v74 dst_sel:WORD_0 dst_unused:UNUSED_PAD src0_sel:WORD_0
	v_exp_f16_sdwa v87, v75 dst_sel:WORD_0 dst_unused:UNUSED_PAD src0_sel:WORD_0
	v_exp_f16_sdwa v88, v76 dst_sel:WORD_0 dst_unused:UNUSED_PAD src0_sel:WORD_0
	v_exp_f16_sdwa v89, v77 dst_sel:WORD_0 dst_unused:UNUSED_PAD src0_sel:WORD_0
	v_exp_f16_sdwa v86, v74 dst_sel:WORD_1 dst_unused:UNUSED_PRESERVE src0_sel:WORD_1
	v_exp_f16_sdwa v87, v75 dst_sel:WORD_1 dst_unused:UNUSED_PRESERVE src0_sel:WORD_1
	v_exp_f16_sdwa v88, v76 dst_sel:WORD_1 dst_unused:UNUSED_PRESERVE src0_sel:WORD_1
	v_exp_f16_sdwa v89, v77 dst_sel:WORD_1 dst_unused:UNUSED_PRESERVE src0_sel:WORD_1
	s_nop 0
	v_pk_add_f16 v74, v133, v154
	v_pk_add_f16 v69, v69, v86
	v_pk_add_f16 v68, v68, v87
	v_pk_add_f16 v67, v67, v88
	v_pk_add_f16 v66, v66, v89
	v_pk_fma_f16 v46, v50, v86, v46
	v_pk_fma_f16 v47, v51, v87, v47
	v_pk_fma_f16 v48, v52, v88, v48
	v_pk_fma_f16 v49, v53, v89, v49
	v_pk_add_f16 v75, v132, v155
	v_pk_add_f16 v76, v131, v156
	v_pk_add_f16 v77, v130, v157
	s_nop 0
	v_exp_f16_sdwa v86, v74 dst_sel:WORD_0 dst_unused:UNUSED_PAD src0_sel:WORD_0
	v_exp_f16_sdwa v87, v75 dst_sel:WORD_0 dst_unused:UNUSED_PAD src0_sel:WORD_0
	v_exp_f16_sdwa v88, v76 dst_sel:WORD_0 dst_unused:UNUSED_PAD src0_sel:WORD_0
	v_exp_f16_sdwa v89, v77 dst_sel:WORD_0 dst_unused:UNUSED_PAD src0_sel:WORD_0
	v_exp_f16_sdwa v86, v74 dst_sel:WORD_1 dst_unused:UNUSED_PRESERVE src0_sel:WORD_1
	v_exp_f16_sdwa v87, v75 dst_sel:WORD_1 dst_unused:UNUSED_PRESERVE src0_sel:WORD_1
	v_exp_f16_sdwa v88, v76 dst_sel:WORD_1 dst_unused:UNUSED_PRESERVE src0_sel:WORD_1
	v_exp_f16_sdwa v89, v77 dst_sel:WORD_1 dst_unused:UNUSED_PRESERVE src0_sel:WORD_1
	s_nop 0
	v_pk_add_f16 v74, v164, v154
	v_pk_add_f16 v69, v69, v86
	v_pk_add_f16 v66, v66, v89
	v_pk_add_f16 v67, v67, v88
	v_pk_add_f16 v68, v68, v87
	v_pk_fma_f16 v49, v13, v89, v49
	v_pk_fma_f16 v48, v12, v88, v48
	v_pk_fma_f16 v47, v11, v87, v47
	v_pk_fma_f16 v46, v10, v86, v46
	v_pk_add_f16 v75, v163, v155
	v_pk_add_f16 v76, v162, v156
	v_pk_add_f16 v77, v161, v157
	s_nop 0
	v_exp_f16_sdwa v86, v74 dst_sel:WORD_0 dst_unused:UNUSED_PAD src0_sel:WORD_0
	v_exp_f16_sdwa v87, v75 dst_sel:WORD_0 dst_unused:UNUSED_PAD src0_sel:WORD_0
	v_exp_f16_sdwa v88, v76 dst_sel:WORD_0 dst_unused:UNUSED_PAD src0_sel:WORD_0
	v_exp_f16_sdwa v89, v77 dst_sel:WORD_0 dst_unused:UNUSED_PAD src0_sel:WORD_0
	v_exp_f16_sdwa v86, v74 dst_sel:WORD_1 dst_unused:UNUSED_PRESERVE src0_sel:WORD_1
	v_exp_f16_sdwa v87, v75 dst_sel:WORD_1 dst_unused:UNUSED_PRESERVE src0_sel:WORD_1
	v_exp_f16_sdwa v88, v76 dst_sel:WORD_1 dst_unused:UNUSED_PRESERVE src0_sel:WORD_1
	v_exp_f16_sdwa v89, v77 dst_sel:WORD_1 dst_unused:UNUSED_PRESERVE src0_sel:WORD_1
	s_nop 0
	v_pk_add_f16 v74, v114, v154
	v_pk_add_f16 v69, v69, v86
	v_pk_add_f16 v68, v68, v87
	v_pk_add_f16 v67, v67, v88
	v_pk_add_f16 v66, v66, v89
	v_pk_fma_f16 v46, v14, v86, v46
	v_pk_fma_f16 v47, v15, v87, v47
	v_pk_fma_f16 v48, v16, v88, v48
	v_pk_fma_f16 v49, v17, v89, v49
	v_pk_add_f16 v75, v115, v155
	v_pk_add_f16 v76, v116, v156
	v_pk_add_f16 v77, v117, v157
	s_nop 0
	v_exp_f16_sdwa v86, v74 dst_sel:WORD_0 dst_unused:UNUSED_PAD src0_sel:WORD_0
	v_exp_f16_sdwa v87, v75 dst_sel:WORD_0 dst_unused:UNUSED_PAD src0_sel:WORD_0
	v_exp_f16_sdwa v88, v76 dst_sel:WORD_0 dst_unused:UNUSED_PAD src0_sel:WORD_0
	v_exp_f16_sdwa v89, v77 dst_sel:WORD_0 dst_unused:UNUSED_PAD src0_sel:WORD_0
	v_exp_f16_sdwa v86, v74 dst_sel:WORD_1 dst_unused:UNUSED_PRESERVE src0_sel:WORD_1
	v_exp_f16_sdwa v87, v75 dst_sel:WORD_1 dst_unused:UNUSED_PRESERVE src0_sel:WORD_1
	v_exp_f16_sdwa v88, v76 dst_sel:WORD_1 dst_unused:UNUSED_PRESERVE src0_sel:WORD_1
	v_exp_f16_sdwa v89, v77 dst_sel:WORD_1 dst_unused:UNUSED_PRESERVE src0_sel:WORD_1
	s_nop 0
	s_nop 0
	v_pk_add_f16 v69, v69, v86
	v_pk_add_f16 v68, v68, v87
	v_rcp_f16_e32 v74, v69
	v_rcp_f16_sdwa v69, v69 dst_sel:DWORD dst_unused:UNUSED_PAD src0_sel:WORD_1
	v_pk_add_f16 v67, v67, v88
	v_rcp_f16_e32 v75, v68
	v_rcp_f16_sdwa v68, v68 dst_sel:DWORD dst_unused:UNUSED_PAD src0_sel:WORD_1
	v_pk_add_f16 v66, v66, v89
	v_pk_fma_f16 v46, v18, v86, v46
	v_rcp_f16_e32 v86, v67
	v_rcp_f16_sdwa v67, v67 dst_sel:DWORD dst_unused:UNUSED_PAD src0_sel:WORD_1
	v_pk_fma_f16 v47, v19, v87, v47
	v_rcp_f16_e32 v87, v66
	v_rcp_f16_sdwa v66, v66 dst_sel:DWORD dst_unused:UNUSED_PAD src0_sel:WORD_1
	v_pack_b32_f16 v69, v74, v69
	v_pk_mul_f16 v77, v46, v69
	v_pack_b32_f16 v46, v75, v68
	v_pk_fma_f16 v48, v20, v88, v48
	v_pk_mul_f16 v76, v47, v46
	v_pack_b32_f16 v46, v86, v67
	v_pk_fma_f16 v49, v21, v89, v49
	v_pk_mul_f16 v75, v48, v46
	v_pack_b32_f16 v46, v87, v66
	v_pk_mul_f16 v74, v49, v46
	s_waitcnt vmcnt(7)
	v_pk_mul_f16 v49, v160, v153 op_sel_hi:[0,1]
	v_pk_mul_f16 v46, v160, v150 op_sel_hi:[0,1]
	v_pk_mul_f16 v47, v160, v151 op_sel_hi:[0,1]
	v_pk_mul_f16 v48, v160, v152 op_sel_hi:[0,1]
	v_pk_mul_f16 v69, v158, v153 op_sel_hi:[0,1]
	v_pk_mul_f16 v89, v159, v153 op_sel_hi:[0,1]
	v_pk_fma_f16 v57, v57, v153, v49
	v_pk_fma_f16 v73, v73, v153, v49
	v_pk_fma_f16 v49, v97, v153, v49
	v_pk_mul_f16 v66, v158, v150 op_sel_hi:[0,1]
	v_pk_maximum3_f16 v117, v57, v73, v49
	v_pk_mul_f16 v67, v158, v151 op_sel_hi:[0,1]
	v_pk_mul_f16 v68, v158, v152 op_sel_hi:[0,1]
	v_pk_mul_f16 v86, v159, v150 op_sel_hi:[0,1]
	v_pk_mul_f16 v87, v159, v151 op_sel_hi:[0,1]
	v_pk_mul_f16 v88, v159, v152 op_sel_hi:[0,1]
	v_pk_fma_f16 v56, v56, v152, v48
	v_pk_fma_f16 v55, v55, v151, v47
	v_pk_fma_f16 v54, v54, v150, v46
	v_pk_fma_f16 v72, v72, v152, v48
	v_pk_fma_f16 v71, v71, v151, v47
	v_pk_fma_f16 v70, v70, v150, v46
	v_pk_fma_f16 v48, v96, v152, v48
	v_pk_fma_f16 v47, v95, v151, v47
	v_pk_fma_f16 v46, v94, v150, v46
	v_pk_fma_f16 v90, v29, v153, v69
	v_pk_fma_f16 v94, v41, v153, v69
	v_pk_fma_f16 v69, v61, v153, v69
	v_pk_fma_f16 v98, v81, v153, v89
	v_pk_fma_f16 v110, v109, v153, v89
	v_pk_fma_f16 v89, v125, v153, v89
	v_pk_maximum3_f16 v114, v54, v70, v46
	v_pk_maximum3_f16 v115, v55, v71, v47
	v_pk_maximum3_f16 v116, v56, v72, v48
	v_pk_maximum3_f16 v121, v90, v94, v69
	v_pk_fma_f16 v91, v28, v152, v68
	v_pk_maximum3_f16 v129, v98, v110, v89
	v_pk_fma_f16 v92, v27, v151, v67
	v_pk_maximum3_f16 v117, v117, v121, v129
	v_pk_fma_f16 v93, v26, v150, v66
	v_pk_fma_f16 v95, v40, v152, v68
	v_pk_fma_f16 v96, v39, v151, v67
	v_pk_fma_f16 v97, v38, v150, v66
	v_pk_fma_f16 v68, v60, v152, v68
	v_pk_fma_f16 v67, v59, v151, v67
	v_pk_fma_f16 v66, v58, v150, v66
	v_pk_fma_f16 v99, v80, v152, v88
	v_pk_fma_f16 v100, v79, v151, v87
	v_pk_fma_f16 v101, v78, v150, v86
	v_pk_fma_f16 v111, v108, v152, v88
	v_pk_fma_f16 v112, v107, v151, v87
	v_pk_fma_f16 v113, v106, v150, v86
	v_pk_fma_f16 v88, v124, v152, v88
	v_pk_fma_f16 v87, v123, v151, v87
	v_pk_fma_f16 v86, v122, v150, v86
	v_pk_maximum3_f16 v118, v93, v97, v66
	v_pk_maximum3_f16 v119, v92, v96, v67
	v_pk_maximum3_f16 v120, v91, v95, v68
	v_pk_maximum3_f16 v127, v100, v112, v87
	v_pk_maximum3_f16 v128, v99, v111, v88
	s_nop 0
	v_pk_maximum3_f16 v126, v101, v113, v86
	v_xor_b32_e32 v117, 0x80008000, v117
	v_pk_maximum3_f16 v114, v114, v118, v126
	v_pk_maximum3_f16 v115, v115, v119, v127
	v_pk_maximum3_f16 v116, v116, v120, v128
	v_pk_add_f16 v57, v57, v117
	v_xor_b32_e32 v116, 0x80008000, v116
	v_xor_b32_e32 v115, 0x80008000, v115
	v_xor_b32_e32 v114, 0x80008000, v114
	v_pk_add_f16 v54, v54, v114
	v_pk_add_f16 v55, v55, v115
	v_pk_add_f16 v56, v56, v116
	v_pk_add_f16 v70, v70, v114
	v_exp_f16_sdwa v118, v54 dst_sel:WORD_0 dst_unused:UNUSED_PAD src0_sel:WORD_0
	v_exp_f16_sdwa v119, v55 dst_sel:WORD_0 dst_unused:UNUSED_PAD src0_sel:WORD_0
	v_exp_f16_sdwa v120, v56 dst_sel:WORD_0 dst_unused:UNUSED_PAD src0_sel:WORD_0
	v_exp_f16_sdwa v121, v57 dst_sel:WORD_0 dst_unused:UNUSED_PAD src0_sel:WORD_0
	v_exp_f16_sdwa v118, v54 dst_sel:WORD_1 dst_unused:UNUSED_PRESERVE src0_sel:WORD_1
	v_exp_f16_sdwa v119, v55 dst_sel:WORD_1 dst_unused:UNUSED_PRESERVE src0_sel:WORD_1
	v_exp_f16_sdwa v120, v56 dst_sel:WORD_1 dst_unused:UNUSED_PRESERVE src0_sel:WORD_1
	v_exp_f16_sdwa v121, v57 dst_sel:WORD_1 dst_unused:UNUSED_PRESERVE src0_sel:WORD_1
	s_nop 0
	v_pk_add_f16 v71, v71, v115
	v_pk_add_f16 v57, v118, 0
	v_pk_fma_f16 v25, v25, v121, 0
	v_pk_add_f16 v54, v121, 0
	v_pk_add_f16 v55, v120, 0
	v_pk_add_f16 v56, v119, 0
	v_pk_fma_f16 v24, v24, v120, 0
	v_pk_fma_f16 v23, v23, v119, 0
	v_pk_fma_f16 v22, v22, v118, 0
	v_pk_add_f16 v72, v72, v116
	v_pk_add_f16 v73, v73, v117
	s_nop 0
	v_exp_f16_sdwa v118, v70 dst_sel:WORD_0 dst_unused:UNUSED_PAD src0_sel:WORD_0
	v_exp_f16_sdwa v119, v71 dst_sel:WORD_0 dst_unused:UNUSED_PAD src0_sel:WORD_0
	v_exp_f16_sdwa v120, v72 dst_sel:WORD_0 dst_unused:UNUSED_PAD src0_sel:WORD_0
	v_exp_f16_sdwa v121, v73 dst_sel:WORD_0 dst_unused:UNUSED_PAD src0_sel:WORD_0
	v_exp_f16_sdwa v118, v70 dst_sel:WORD_1 dst_unused:UNUSED_PRESERVE src0_sel:WORD_1
	v_exp_f16_sdwa v119, v71 dst_sel:WORD_1 dst_unused:UNUSED_PRESERVE src0_sel:WORD_1
	v_exp_f16_sdwa v120, v72 dst_sel:WORD_1 dst_unused:UNUSED_PRESERVE src0_sel:WORD_1
	v_exp_f16_sdwa v121, v73 dst_sel:WORD_1 dst_unused:UNUSED_PRESERVE src0_sel:WORD_1
	s_nop 0
	s_nop 0
	v_pk_add_f16 v57, v57, v118
	v_pk_fma_f16 v25, v37, v121, v25
	v_pk_add_f16 v37, v49, v117
	v_pk_add_f16 v56, v56, v119
	v_pk_add_f16 v55, v55, v120
	v_pk_add_f16 v54, v54, v121
	v_pk_fma_f16 v22, v34, v118, v22
	v_pk_fma_f16 v23, v35, v119, v23
	v_pk_fma_f16 v24, v36, v120, v24
	v_pk_add_f16 v34, v46, v114
	v_pk_add_f16 v35, v47, v115
	v_pk_add_f16 v36, v48, v116
	s_nop 0
	v_exp_f16_sdwa v46, v34 dst_sel:WORD_0 dst_unused:UNUSED_PAD src0_sel:WORD_0
	v_exp_f16_sdwa v47, v35 dst_sel:WORD_0 dst_unused:UNUSED_PAD src0_sel:WORD_0
	v_exp_f16_sdwa v48, v36 dst_sel:WORD_0 dst_unused:UNUSED_PAD src0_sel:WORD_0
	v_exp_f16_sdwa v49, v37 dst_sel:WORD_0 dst_unused:UNUSED_PAD src0_sel:WORD_0
	v_exp_f16_sdwa v46, v34 dst_sel:WORD_1 dst_unused:UNUSED_PRESERVE src0_sel:WORD_1
	v_exp_f16_sdwa v47, v35 dst_sel:WORD_1 dst_unused:UNUSED_PRESERVE src0_sel:WORD_1
	v_exp_f16_sdwa v48, v36 dst_sel:WORD_1 dst_unused:UNUSED_PRESERVE src0_sel:WORD_1
	v_exp_f16_sdwa v49, v37 dst_sel:WORD_1 dst_unused:UNUSED_PRESERVE src0_sel:WORD_1
	s_nop 0
	s_nop 0
	v_pk_add_f16 v37, v57, v46
	v_pk_add_f16 v34, v54, v49
	v_pk_add_f16 v35, v55, v48
	v_pk_add_f16 v36, v56, v47
	v_pk_fma_f16 v25, v53, v49, v25
	v_pk_fma_f16 v24, v52, v48, v24
	v_pk_fma_f16 v23, v51, v47, v23
	v_pk_fma_f16 v22, v50, v46, v22
	v_pk_add_f16 v46, v93, v114
	v_pk_add_f16 v47, v92, v115
	v_pk_add_f16 v48, v91, v116
	v_pk_add_f16 v49, v90, v117
	s_nop 0
	v_exp_f16_sdwa v50, v46 dst_sel:WORD_0 dst_unused:UNUSED_PAD src0_sel:WORD_0
	v_exp_f16_sdwa v51, v47 dst_sel:WORD_0 dst_unused:UNUSED_PAD src0_sel:WORD_0
	v_exp_f16_sdwa v52, v48 dst_sel:WORD_0 dst_unused:UNUSED_PAD src0_sel:WORD_0
	v_exp_f16_sdwa v53, v49 dst_sel:WORD_0 dst_unused:UNUSED_PAD src0_sel:WORD_0
	v_exp_f16_sdwa v50, v46 dst_sel:WORD_1 dst_unused:UNUSED_PRESERVE src0_sel:WORD_1
	v_exp_f16_sdwa v51, v47 dst_sel:WORD_1 dst_unused:UNUSED_PRESERVE src0_sel:WORD_1
	v_exp_f16_sdwa v52, v48 dst_sel:WORD_1 dst_unused:UNUSED_PRESERVE src0_sel:WORD_1
	v_exp_f16_sdwa v53, v49 dst_sel:WORD_1 dst_unused:UNUSED_PRESERVE src0_sel:WORD_1
	s_nop 0
	v_pk_add_f16 v46, v97, v114
	v_pk_add_f16 v37, v37, v50
	v_pk_add_f16 v36, v36, v51
	v_pk_add_f16 v35, v35, v52
	v_pk_add_f16 v34, v34, v53
	v_pk_fma_f16 v22, v10, v50, v22
	v_pk_fma_f16 v23, v11, v51, v23
	v_pk_fma_f16 v24, v12, v52, v24
	v_pk_fma_f16 v25, v13, v53, v25
	v_pk_add_f16 v47, v96, v115
	v_pk_add_f16 v48, v95, v116
	v_pk_add_f16 v49, v94, v117
	s_nop 0
	v_exp_f16_sdwa v50, v46 dst_sel:WORD_0 dst_unused:UNUSED_PAD src0_sel:WORD_0
	v_exp_f16_sdwa v51, v47 dst_sel:WORD_0 dst_unused:UNUSED_PAD src0_sel:WORD_0
	v_exp_f16_sdwa v52, v48 dst_sel:WORD_0 dst_unused:UNUSED_PAD src0_sel:WORD_0
	v_exp_f16_sdwa v53, v49 dst_sel:WORD_0 dst_unused:UNUSED_PAD src0_sel:WORD_0
	v_exp_f16_sdwa v50, v46 dst_sel:WORD_1 dst_unused:UNUSED_PRESERVE src0_sel:WORD_1
	v_exp_f16_sdwa v51, v47 dst_sel:WORD_1 dst_unused:UNUSED_PRESERVE src0_sel:WORD_1
	v_exp_f16_sdwa v52, v48 dst_sel:WORD_1 dst_unused:UNUSED_PRESERVE src0_sel:WORD_1
	v_exp_f16_sdwa v53, v49 dst_sel:WORD_1 dst_unused:UNUSED_PRESERVE src0_sel:WORD_1
	s_nop 0
	v_pk_add_f16 v46, v66, v114
	v_pk_add_f16 v37, v37, v50
	v_pk_add_f16 v34, v34, v53
	v_pk_add_f16 v35, v35, v52
	v_pk_add_f16 v36, v36, v51
	v_pk_fma_f16 v25, v17, v53, v25
	v_pk_fma_f16 v24, v16, v52, v24
	v_pk_fma_f16 v23, v15, v51, v23
	v_pk_fma_f16 v22, v14, v50, v22
	v_pk_add_f16 v47, v67, v115
	v_pk_add_f16 v48, v68, v116
	v_pk_add_f16 v49, v69, v117
	s_nop 0
	v_exp_f16_sdwa v50, v46 dst_sel:WORD_0 dst_unused:UNUSED_PAD src0_sel:WORD_0
	v_exp_f16_sdwa v51, v47 dst_sel:WORD_0 dst_unused:UNUSED_PAD src0_sel:WORD_0
	v_exp_f16_sdwa v52, v48 dst_sel:WORD_0 dst_unused:UNUSED_PAD src0_sel:WORD_0
	v_exp_f16_sdwa v53, v49 dst_sel:WORD_0 dst_unused:UNUSED_PAD src0_sel:WORD_0
	v_exp_f16_sdwa v50, v46 dst_sel:WORD_1 dst_unused:UNUSED_PRESERVE src0_sel:WORD_1
	v_exp_f16_sdwa v51, v47 dst_sel:WORD_1 dst_unused:UNUSED_PRESERVE src0_sel:WORD_1
	v_exp_f16_sdwa v52, v48 dst_sel:WORD_1 dst_unused:UNUSED_PRESERVE src0_sel:WORD_1
	v_exp_f16_sdwa v53, v49 dst_sel:WORD_1 dst_unused:UNUSED_PRESERVE src0_sel:WORD_1
	s_nop 0
	v_pk_add_f16 v46, v101, v114
	v_pk_add_f16 v37, v37, v50
	v_pk_add_f16 v36, v36, v51
	v_pk_add_f16 v35, v35, v52
	v_pk_add_f16 v34, v34, v53
	v_pk_fma_f16 v22, v18, v50, v22
	v_pk_fma_f16 v23, v19, v51, v23
	v_pk_fma_f16 v24, v20, v52, v24
	v_pk_fma_f16 v25, v21, v53, v25
	v_pk_add_f16 v47, v100, v115
	v_pk_add_f16 v48, v99, v116
	v_pk_add_f16 v49, v98, v117
	s_nop 0
	v_exp_f16_sdwa v50, v46 dst_sel:WORD_0 dst_unused:UNUSED_PAD src0_sel:WORD_0
	v_exp_f16_sdwa v51, v47 dst_sel:WORD_0 dst_unused:UNUSED_PAD src0_sel:WORD_0
	v_exp_f16_sdwa v52, v48 dst_sel:WORD_0 dst_unused:UNUSED_PAD src0_sel:WORD_0
	v_exp_f16_sdwa v53, v49 dst_sel:WORD_0 dst_unused:UNUSED_PAD src0_sel:WORD_0
	v_exp_f16_sdwa v50, v46 dst_sel:WORD_1 dst_unused:UNUSED_PRESERVE src0_sel:WORD_1
	v_exp_f16_sdwa v51, v47 dst_sel:WORD_1 dst_unused:UNUSED_PRESERVE src0_sel:WORD_1
	v_exp_f16_sdwa v52, v48 dst_sel:WORD_1 dst_unused:UNUSED_PRESERVE src0_sel:WORD_1
	v_exp_f16_sdwa v53, v49 dst_sel:WORD_1 dst_unused:UNUSED_PRESERVE src0_sel:WORD_1
	s_nop 0
	v_pk_add_f16 v46, v113, v114
	v_pk_add_f16 v37, v37, v50
	v_pk_add_f16 v34, v34, v53
	v_pk_add_f16 v35, v35, v52
	v_pk_add_f16 v36, v36, v51
	v_pk_fma_f16 v25, v33, v53, v25
	v_pk_fma_f16 v24, v32, v52, v24
	v_pk_fma_f16 v23, v31, v51, v23
	v_pk_fma_f16 v22, v30, v50, v22
	v_pk_add_f16 v47, v112, v115
	v_pk_add_f16 v48, v111, v116
	v_pk_add_f16 v49, v110, v117
	s_nop 0
	v_exp_f16_sdwa v50, v46 dst_sel:WORD_0 dst_unused:UNUSED_PAD src0_sel:WORD_0
	v_exp_f16_sdwa v51, v47 dst_sel:WORD_0 dst_unused:UNUSED_PAD src0_sel:WORD_0
	v_exp_f16_sdwa v52, v48 dst_sel:WORD_0 dst_unused:UNUSED_PAD src0_sel:WORD_0
	v_exp_f16_sdwa v53, v49 dst_sel:WORD_0 dst_unused:UNUSED_PAD src0_sel:WORD_0
	v_exp_f16_sdwa v50, v46 dst_sel:WORD_1 dst_unused:UNUSED_PRESERVE src0_sel:WORD_1
	v_exp_f16_sdwa v51, v47 dst_sel:WORD_1 dst_unused:UNUSED_PRESERVE src0_sel:WORD_1
	v_exp_f16_sdwa v52, v48 dst_sel:WORD_1 dst_unused:UNUSED_PRESERVE src0_sel:WORD_1
	v_exp_f16_sdwa v53, v49 dst_sel:WORD_1 dst_unused:UNUSED_PRESERVE src0_sel:WORD_1
	s_nop 0
	v_pk_add_f16 v46, v86, v114
	v_pk_add_f16 v37, v37, v50
	v_pk_add_f16 v36, v36, v51
	v_pk_add_f16 v35, v35, v52
	v_pk_add_f16 v34, v34, v53
	v_pk_fma_f16 v22, v42, v50, v22
	v_pk_fma_f16 v23, v43, v51, v23
	v_pk_fma_f16 v24, v44, v52, v24
	v_pk_fma_f16 v25, v45, v53, v25
	v_pk_add_f16 v47, v87, v115
	v_pk_add_f16 v48, v88, v116
	v_pk_add_f16 v49, v89, v117
	s_nop 0
	v_exp_f16_sdwa v50, v46 dst_sel:WORD_0 dst_unused:UNUSED_PAD src0_sel:WORD_0
	v_exp_f16_sdwa v51, v47 dst_sel:WORD_0 dst_unused:UNUSED_PAD src0_sel:WORD_0
	v_exp_f16_sdwa v52, v48 dst_sel:WORD_0 dst_unused:UNUSED_PAD src0_sel:WORD_0
	v_exp_f16_sdwa v53, v49 dst_sel:WORD_0 dst_unused:UNUSED_PAD src0_sel:WORD_0
	v_exp_f16_sdwa v50, v46 dst_sel:WORD_1 dst_unused:UNUSED_PRESERVE src0_sel:WORD_1
	v_exp_f16_sdwa v51, v47 dst_sel:WORD_1 dst_unused:UNUSED_PRESERVE src0_sel:WORD_1
	v_exp_f16_sdwa v52, v48 dst_sel:WORD_1 dst_unused:UNUSED_PRESERVE src0_sel:WORD_1
	v_exp_f16_sdwa v53, v49 dst_sel:WORD_1 dst_unused:UNUSED_PRESERVE src0_sel:WORD_1
	s_nop 0
	s_nop 0
	v_pk_add_f16 v37, v37, v50
	v_pk_add_f16 v36, v36, v51
	v_rcp_f16_e32 v46, v37
	v_rcp_f16_sdwa v37, v37 dst_sel:DWORD dst_unused:UNUSED_PAD src0_sel:WORD_1
	v_pk_add_f16 v35, v35, v52
	v_rcp_f16_e32 v47, v36
	v_rcp_f16_sdwa v36, v36 dst_sel:DWORD dst_unused:UNUSED_PAD src0_sel:WORD_1
	v_pk_add_f16 v34, v34, v53
	v_rcp_f16_e32 v48, v35
	v_rcp_f16_sdwa v35, v35 dst_sel:DWORD dst_unused:UNUSED_PAD src0_sel:WORD_1
	v_rcp_f16_e32 v49, v34
	v_rcp_f16_sdwa v34, v34 dst_sel:DWORD dst_unused:UNUSED_PAD src0_sel:WORD_1
	v_pk_fma_f16 v22, v62, v50, v22
	v_pack_b32_f16 v37, v46, v37
	v_pk_fma_f16 v23, v63, v51, v23
	v_pk_mul_f16 v57, v22, v37
	v_pack_b32_f16 v22, v47, v36
	v_pk_fma_f16 v24, v64, v52, v24
	v_pk_mul_f16 v56, v23, v22
	v_pack_b32_f16 v22, v48, v35
	v_pk_fma_f16 v25, v65, v53, v25
	v_pk_mul_f16 v55, v24, v22
	v_pack_b32_f16 v22, v49, v34
	v_pk_mul_f16 v54, v25, v22
	s_waitcnt vmcnt(0)
	v_pk_mul_f16 v22, v160, v146 op_sel_hi:[0,1]
	v_pk_mul_f16 v23, v160, v147 op_sel_hi:[0,1]
	v_pk_mul_f16 v24, v160, v148 op_sel_hi:[0,1]
	v_pk_mul_f16 v25, v160, v149 op_sel_hi:[0,1]
	v_pk_mul_f16 v46, v159, v146 op_sel_hi:[0,1]
	v_pk_mul_f16 v47, v159, v147 op_sel_hi:[0,1]
	v_pk_mul_f16 v48, v159, v148 op_sel_hi:[0,1]
	v_pk_mul_f16 v49, v159, v149 op_sel_hi:[0,1]
	v_pk_mul_f16 v34, v158, v146 op_sel_hi:[0,1]
	v_pk_mul_f16 v35, v158, v147 op_sel_hi:[0,1]
	v_pk_mul_f16 v36, v158, v148 op_sel_hi:[0,1]
	v_pk_mul_f16 v37, v158, v149 op_sel_hi:[0,1]
	v_pk_fma_f16 v29, v29, v149, v25
	v_pk_fma_f16 v28, v28, v148, v24
	v_pk_fma_f16 v27, v27, v147, v23
	v_pk_fma_f16 v26, v26, v146, v22
	v_pk_fma_f16 v41, v41, v149, v25
	v_pk_fma_f16 v40, v40, v148, v24
	v_pk_fma_f16 v39, v39, v147, v23
	v_pk_fma_f16 v38, v38, v146, v22
	v_pk_fma_f16 v25, v61, v149, v25
	v_pk_fma_f16 v24, v60, v148, v24
	v_pk_fma_f16 v23, v59, v147, v23
	v_pk_fma_f16 v22, v58, v146, v22
	v_pk_fma_f16 v66, v137, v149, v49
	v_pk_fma_f16 v67, v136, v148, v48
	v_pk_fma_f16 v68, v135, v147, v47
	v_pk_fma_f16 v69, v134, v146, v46
	v_pk_fma_f16 v70, v145, v149, v49
	v_pk_fma_f16 v71, v144, v148, v48
	v_pk_fma_f16 v72, v143, v147, v47
	v_pk_fma_f16 v73, v142, v146, v46
	v_pk_fma_f16 v9, v9, v149, v49
	v_pk_fma_f16 v8, v8, v148, v48
	v_pk_fma_f16 v7, v7, v147, v47
	v_pk_fma_f16 v6, v6, v146, v46
	v_pk_maximum3_f16 v46, v26, v38, v22
	v_pk_maximum3_f16 v47, v27, v39, v23
	v_pk_maximum3_f16 v48, v28, v40, v24
	v_pk_maximum3_f16 v49, v29, v41, v25
	v_pk_fma_f16 v50, v81, v149, v37
	v_pk_fma_f16 v51, v80, v148, v36
	v_pk_fma_f16 v52, v79, v147, v35
	v_pk_fma_f16 v53, v78, v146, v34
	v_pk_fma_f16 v58, v109, v149, v37
	v_pk_fma_f16 v59, v108, v148, v36
	v_pk_fma_f16 v60, v107, v147, v35
	v_pk_fma_f16 v61, v106, v146, v34
	v_pk_fma_f16 v37, v125, v149, v37
	v_pk_fma_f16 v36, v124, v148, v36
	v_pk_fma_f16 v35, v123, v147, v35
	v_pk_fma_f16 v34, v122, v146, v34
	v_pk_maximum3_f16 v79, v52, v60, v35
	v_pk_maximum3_f16 v80, v51, v59, v36
	v_pk_maximum3_f16 v81, v50, v58, v37
	v_pk_maximum3_f16 v86, v69, v73, v6
	v_pk_maximum3_f16 v87, v68, v72, v7
	s_nop 0
	v_pk_maximum3_f16 v78, v53, v61, v34
	v_pk_maximum3_f16 v88, v67, v71, v8
	v_pk_maximum3_f16 v89, v66, v70, v9
	s_nop 0
	v_pk_maximum3_f16 v46, v46, v78, v86
	v_pk_maximum3_f16 v47, v47, v79, v87
	v_pk_maximum3_f16 v48, v48, v80, v88
	v_pk_maximum3_f16 v49, v49, v81, v89
	s_nop 0
	v_xor_b32_e32 v49, 0x80008000, v49
	v_xor_b32_e32 v48, 0x80008000, v48
	v_xor_b32_e32 v47, 0x80008000, v47
	v_xor_b32_e32 v46, 0x80008000, v46
	v_pk_add_f16 v26, v26, v46
	v_pk_add_f16 v27, v27, v47
	v_pk_add_f16 v28, v28, v48
	v_pk_add_f16 v29, v29, v49
	v_pk_add_f16 v38, v38, v46
	v_exp_f16_sdwa v78, v26 dst_sel:WORD_0 dst_unused:UNUSED_PAD src0_sel:WORD_0
	v_exp_f16_sdwa v79, v27 dst_sel:WORD_0 dst_unused:UNUSED_PAD src0_sel:WORD_0
	v_exp_f16_sdwa v80, v28 dst_sel:WORD_0 dst_unused:UNUSED_PAD src0_sel:WORD_0
	v_exp_f16_sdwa v81, v29 dst_sel:WORD_0 dst_unused:UNUSED_PAD src0_sel:WORD_0
	v_exp_f16_sdwa v78, v26 dst_sel:WORD_1 dst_unused:UNUSED_PRESERVE src0_sel:WORD_1
	v_exp_f16_sdwa v79, v27 dst_sel:WORD_1 dst_unused:UNUSED_PRESERVE src0_sel:WORD_1
	v_exp_f16_sdwa v80, v28 dst_sel:WORD_1 dst_unused:UNUSED_PRESERVE src0_sel:WORD_1
	v_exp_f16_sdwa v81, v29 dst_sel:WORD_1 dst_unused:UNUSED_PRESERVE src0_sel:WORD_1
	s_nop 0
	v_pk_add_f16 v39, v39, v47
	v_pk_add_f16 v26, v78, 0
	v_pk_add_f16 v27, v79, 0
	v_pk_add_f16 v28, v80, 0
	v_pk_add_f16 v29, v81, 0
	v_pk_fma_f16 v10, v10, v78, 0
	v_pk_fma_f16 v11, v11, v79, 0
	v_pk_fma_f16 v12, v12, v80, 0
	v_pk_fma_f16 v13, v13, v81, 0
	v_pk_add_f16 v40, v40, v48
	v_pk_add_f16 v41, v41, v49
	v_pk_add_f16 v6, v6, v46
	v_exp_f16_sdwa v78, v38 dst_sel:WORD_0 dst_unused:UNUSED_PAD src0_sel:WORD_0
	v_exp_f16_sdwa v79, v39 dst_sel:WORD_0 dst_unused:UNUSED_PAD src0_sel:WORD_0
	v_exp_f16_sdwa v80, v40 dst_sel:WORD_0 dst_unused:UNUSED_PAD src0_sel:WORD_0
	v_exp_f16_sdwa v81, v41 dst_sel:WORD_0 dst_unused:UNUSED_PAD src0_sel:WORD_0
	v_exp_f16_sdwa v78, v38 dst_sel:WORD_1 dst_unused:UNUSED_PRESERVE src0_sel:WORD_1
	v_exp_f16_sdwa v79, v39 dst_sel:WORD_1 dst_unused:UNUSED_PRESERVE src0_sel:WORD_1
	v_exp_f16_sdwa v80, v40 dst_sel:WORD_1 dst_unused:UNUSED_PRESERVE src0_sel:WORD_1
	v_exp_f16_sdwa v81, v41 dst_sel:WORD_1 dst_unused:UNUSED_PRESERVE src0_sel:WORD_1
	s_nop 0
	v_pk_add_f16 v7, v7, v47
	v_pk_add_f16 v29, v29, v81
	v_pk_add_f16 v28, v28, v80
	v_pk_add_f16 v27, v27, v79
	v_pk_add_f16 v26, v26, v78
	v_pk_fma_f16 v13, v17, v81, v13
	v_pk_fma_f16 v12, v16, v80, v12
	v_pk_fma_f16 v11, v15, v79, v11
	v_pk_fma_f16 v10, v14, v78, v10
	v_pk_add_f16 v14, v22, v46
	v_pk_add_f16 v15, v23, v47
	v_pk_add_f16 v16, v24, v48
	v_pk_add_f16 v17, v25, v49
	v_pk_add_f16 v8, v8, v48
	v_exp_f16_sdwa v22, v14 dst_sel:WORD_0 dst_unused:UNUSED_PAD src0_sel:WORD_0
	v_exp_f16_sdwa v23, v15 dst_sel:WORD_0 dst_unused:UNUSED_PAD src0_sel:WORD_0
	v_exp_f16_sdwa v24, v16 dst_sel:WORD_0 dst_unused:UNUSED_PAD src0_sel:WORD_0
	v_exp_f16_sdwa v25, v17 dst_sel:WORD_0 dst_unused:UNUSED_PAD src0_sel:WORD_0
	v_exp_f16_sdwa v22, v14 dst_sel:WORD_1 dst_unused:UNUSED_PRESERVE src0_sel:WORD_1
	v_exp_f16_sdwa v23, v15 dst_sel:WORD_1 dst_unused:UNUSED_PRESERVE src0_sel:WORD_1
	v_exp_f16_sdwa v24, v16 dst_sel:WORD_1 dst_unused:UNUSED_PRESERVE src0_sel:WORD_1
	v_exp_f16_sdwa v25, v17 dst_sel:WORD_1 dst_unused:UNUSED_PRESERVE src0_sel:WORD_1
	s_nop 0
	v_pk_add_f16 v9, v9, v49
	v_pk_add_f16 v14, v26, v22
	v_pk_add_f16 v15, v27, v23
	v_pk_add_f16 v16, v28, v24
	v_pk_add_f16 v17, v29, v25
	v_pk_fma_f16 v10, v18, v22, v10
	v_pk_fma_f16 v11, v19, v23, v11
	v_pk_fma_f16 v12, v20, v24, v12
	v_pk_fma_f16 v13, v21, v25, v13
	v_pk_add_f16 v18, v53, v46
	v_pk_add_f16 v19, v52, v47
	v_pk_add_f16 v20, v51, v48
	v_pk_add_f16 v21, v50, v49
	s_nop 0
	v_exp_f16_sdwa v22, v18 dst_sel:WORD_0 dst_unused:UNUSED_PAD src0_sel:WORD_0
	v_exp_f16_sdwa v23, v19 dst_sel:WORD_0 dst_unused:UNUSED_PAD src0_sel:WORD_0
	v_exp_f16_sdwa v24, v20 dst_sel:WORD_0 dst_unused:UNUSED_PAD src0_sel:WORD_0
	v_exp_f16_sdwa v25, v21 dst_sel:WORD_0 dst_unused:UNUSED_PAD src0_sel:WORD_0
	v_exp_f16_sdwa v22, v18 dst_sel:WORD_1 dst_unused:UNUSED_PRESERVE src0_sel:WORD_1
	v_exp_f16_sdwa v23, v19 dst_sel:WORD_1 dst_unused:UNUSED_PRESERVE src0_sel:WORD_1
	v_exp_f16_sdwa v24, v20 dst_sel:WORD_1 dst_unused:UNUSED_PRESERVE src0_sel:WORD_1
	v_exp_f16_sdwa v25, v21 dst_sel:WORD_1 dst_unused:UNUSED_PRESERVE src0_sel:WORD_1
	s_nop 0
	v_pk_add_f16 v18, v61, v46
	v_pk_add_f16 v17, v17, v25
	v_pk_add_f16 v16, v16, v24
	v_pk_add_f16 v15, v15, v23
	v_pk_add_f16 v14, v14, v22
	v_pk_fma_f16 v13, v33, v25, v13
	v_pk_fma_f16 v12, v32, v24, v12
	v_pk_fma_f16 v11, v31, v23, v11
	v_pk_fma_f16 v10, v30, v22, v10
	v_pk_add_f16 v19, v60, v47
	v_pk_add_f16 v20, v59, v48
	v_pk_add_f16 v21, v58, v49
	v_exp_f16_sdwa v30, v6 dst_sel:WORD_0 dst_unused:UNUSED_PAD src0_sel:WORD_0
	v_exp_f16_sdwa v31, v7 dst_sel:WORD_0 dst_unused:UNUSED_PAD src0_sel:WORD_0
	v_exp_f16_sdwa v32, v8 dst_sel:WORD_0 dst_unused:UNUSED_PAD src0_sel:WORD_0
	v_exp_f16_sdwa v33, v9 dst_sel:WORD_0 dst_unused:UNUSED_PAD src0_sel:WORD_0
	v_exp_f16_sdwa v30, v6 dst_sel:WORD_1 dst_unused:UNUSED_PRESERVE src0_sel:WORD_1
	v_exp_f16_sdwa v31, v7 dst_sel:WORD_1 dst_unused:UNUSED_PRESERVE src0_sel:WORD_1
	v_exp_f16_sdwa v32, v8 dst_sel:WORD_1 dst_unused:UNUSED_PRESERVE src0_sel:WORD_1
	v_exp_f16_sdwa v33, v9 dst_sel:WORD_1 dst_unused:UNUSED_PRESERVE src0_sel:WORD_1
	s_nop 0
	s_nop 0
	v_exp_f16_sdwa v22, v18 dst_sel:WORD_0 dst_unused:UNUSED_PAD src0_sel:WORD_0
	v_exp_f16_sdwa v23, v19 dst_sel:WORD_0 dst_unused:UNUSED_PAD src0_sel:WORD_0
	v_exp_f16_sdwa v24, v20 dst_sel:WORD_0 dst_unused:UNUSED_PAD src0_sel:WORD_0
	v_exp_f16_sdwa v25, v21 dst_sel:WORD_0 dst_unused:UNUSED_PAD src0_sel:WORD_0
	v_exp_f16_sdwa v22, v18 dst_sel:WORD_1 dst_unused:UNUSED_PRESERVE src0_sel:WORD_1
	v_exp_f16_sdwa v23, v19 dst_sel:WORD_1 dst_unused:UNUSED_PRESERVE src0_sel:WORD_1
	v_exp_f16_sdwa v24, v20 dst_sel:WORD_1 dst_unused:UNUSED_PRESERVE src0_sel:WORD_1
	v_exp_f16_sdwa v25, v21 dst_sel:WORD_1 dst_unused:UNUSED_PRESERVE src0_sel:WORD_1
	s_nop 0
	v_pk_add_f16 v18, v34, v46
	v_pk_add_f16 v14, v14, v22
	v_pk_add_f16 v15, v15, v23
	v_pk_add_f16 v16, v16, v24
	v_pk_add_f16 v17, v17, v25
	v_pk_fma_f16 v10, v42, v22, v10
	v_pk_fma_f16 v11, v43, v23, v11
	v_pk_fma_f16 v12, v44, v24, v12
	v_pk_fma_f16 v13, v45, v25, v13
	v_pk_add_f16 v19, v35, v47
	v_pk_add_f16 v20, v36, v48
	v_pk_add_f16 v21, v37, v49
	s_nop 0
	v_exp_f16_sdwa v22, v18 dst_sel:WORD_0 dst_unused:UNUSED_PAD src0_sel:WORD_0
	v_exp_f16_sdwa v23, v19 dst_sel:WORD_0 dst_unused:UNUSED_PAD src0_sel:WORD_0
	v_exp_f16_sdwa v24, v20 dst_sel:WORD_0 dst_unused:UNUSED_PAD src0_sel:WORD_0
	v_exp_f16_sdwa v25, v21 dst_sel:WORD_0 dst_unused:UNUSED_PAD src0_sel:WORD_0
	v_exp_f16_sdwa v22, v18 dst_sel:WORD_1 dst_unused:UNUSED_PRESERVE src0_sel:WORD_1
	v_exp_f16_sdwa v23, v19 dst_sel:WORD_1 dst_unused:UNUSED_PRESERVE src0_sel:WORD_1
	v_exp_f16_sdwa v24, v20 dst_sel:WORD_1 dst_unused:UNUSED_PRESERVE src0_sel:WORD_1
	v_exp_f16_sdwa v25, v21 dst_sel:WORD_1 dst_unused:UNUSED_PRESERVE src0_sel:WORD_1
	s_nop 0
	v_pk_add_f16 v18, v69, v46
	v_pk_add_f16 v17, v17, v25
	v_pk_add_f16 v16, v16, v24
	v_pk_add_f16 v15, v15, v23
	v_pk_add_f16 v14, v14, v22
	v_pk_fma_f16 v13, v65, v25, v13
	v_pk_fma_f16 v12, v64, v24, v12
	v_pk_fma_f16 v11, v63, v23, v11
	v_pk_fma_f16 v10, v62, v22, v10
	v_pk_add_f16 v19, v68, v47
	v_pk_add_f16 v20, v67, v48
	v_pk_add_f16 v21, v66, v49
	s_nop 0
	v_exp_f16_sdwa v22, v18 dst_sel:WORD_0 dst_unused:UNUSED_PAD src0_sel:WORD_0
	v_exp_f16_sdwa v23, v19 dst_sel:WORD_0 dst_unused:UNUSED_PAD src0_sel:WORD_0
	v_exp_f16_sdwa v24, v20 dst_sel:WORD_0 dst_unused:UNUSED_PAD src0_sel:WORD_0
	v_exp_f16_sdwa v25, v21 dst_sel:WORD_0 dst_unused:UNUSED_PAD src0_sel:WORD_0
	v_exp_f16_sdwa v22, v18 dst_sel:WORD_1 dst_unused:UNUSED_PRESERVE src0_sel:WORD_1
	v_exp_f16_sdwa v23, v19 dst_sel:WORD_1 dst_unused:UNUSED_PRESERVE src0_sel:WORD_1
	v_exp_f16_sdwa v24, v20 dst_sel:WORD_1 dst_unused:UNUSED_PRESERVE src0_sel:WORD_1
	v_exp_f16_sdwa v25, v21 dst_sel:WORD_1 dst_unused:UNUSED_PRESERVE src0_sel:WORD_1
	s_nop 0
	v_pk_add_f16 v18, v73, v46
	v_pk_add_f16 v14, v14, v22
	v_pk_add_f16 v15, v15, v23
	v_pk_add_f16 v16, v16, v24
	v_pk_add_f16 v17, v17, v25
	v_pk_fma_f16 v10, v82, v22, v10
	v_pk_fma_f16 v11, v83, v23, v11
	v_pk_fma_f16 v12, v84, v24, v12
	v_pk_fma_f16 v13, v85, v25, v13
	v_pk_add_f16 v19, v72, v47
	v_pk_add_f16 v20, v71, v48
	v_pk_add_f16 v21, v70, v49
	s_nop 0
	v_exp_f16_sdwa v22, v18 dst_sel:WORD_0 dst_unused:UNUSED_PAD src0_sel:WORD_0
	v_exp_f16_sdwa v23, v19 dst_sel:WORD_0 dst_unused:UNUSED_PAD src0_sel:WORD_0
	v_exp_f16_sdwa v24, v20 dst_sel:WORD_0 dst_unused:UNUSED_PAD src0_sel:WORD_0
	v_exp_f16_sdwa v25, v21 dst_sel:WORD_0 dst_unused:UNUSED_PAD src0_sel:WORD_0
	v_exp_f16_sdwa v22, v18 dst_sel:WORD_1 dst_unused:UNUSED_PRESERVE src0_sel:WORD_1
	v_exp_f16_sdwa v23, v19 dst_sel:WORD_1 dst_unused:UNUSED_PRESERVE src0_sel:WORD_1
	v_exp_f16_sdwa v24, v20 dst_sel:WORD_1 dst_unused:UNUSED_PRESERVE src0_sel:WORD_1
	v_exp_f16_sdwa v25, v21 dst_sel:WORD_1 dst_unused:UNUSED_PRESERVE src0_sel:WORD_1
	s_nop 0
	s_nop 0
	v_pk_add_f16 v17, v17, v25
	v_pk_add_f16 v16, v16, v24
	v_pk_add_f16 v15, v15, v23
	v_pk_add_f16 v14, v14, v22
	v_pk_fma_f16 v21, v105, v25, v13
	v_pk_fma_f16 v20, v104, v24, v12
	v_pk_fma_f16 v19, v103, v23, v11
	v_pk_fma_f16 v18, v102, v22, v10
	v_mov_b32_e32 v13, v5
	v_mov_b32_e32 v12, v4
	v_mov_b32_e32 v11, v3
	v_mov_b32_e32 v10, v2
.LBB4_80:
	v_lshlrev_b64 v[6:7], 9, v[168:169]
	v_or_b32_e32 v6, v6, v198
	v_lshl_add_u64 v[2:3], s[20:21], 0, v[6:7]
	global_load_dwordx4 v[2:5], v[2:3], off nt
	v_lshl_add_u64 v[6:7], s[22:23], 0, v[6:7]
	global_load_dwordx4 v[6:9], v[6:7], off nt
	v_add_u32_e32 v168, v185, v199
	v_lshlrev_b64 v[26:27], 9, v[168:169]
	v_or_b32_e32 v26, v26, v198
	v_lshl_add_u64 v[22:23], s[20:21], 0, v[26:27]
	global_load_dwordx4 v[22:25], v[22:23], off nt
	v_lshl_add_u64 v[26:27], s[22:23], 0, v[26:27]
	global_load_dwordx4 v[26:29], v[26:27], off nt
	v_pk_add_f16 v17, v17, v33
	v_pk_add_f16 v16, v16, v32
	v_pk_add_f16 v15, v15, v31
	v_pk_add_f16 v14, v14, v30
	v_pk_fma_f16 v42, v13, v33, v21
	v_pk_fma_f16 v43, v12, v32, v20
	v_rcp_f16_e32 v12, v14
	v_rcp_f16_sdwa v13, v14 dst_sel:DWORD dst_unused:UNUSED_PAD src0_sel:WORD_1
	v_rcp_f16_e32 v14, v15
	v_rcp_f16_sdwa v15, v15 dst_sel:DWORD dst_unused:UNUSED_PAD src0_sel:WORD_1
	v_rcp_f16_e32 v46, v16
	v_rcp_f16_sdwa v16, v16 dst_sel:DWORD dst_unused:UNUSED_PAD src0_sel:WORD_1
	v_rcp_f16_e32 v47, v17
	v_rcp_f16_sdwa v17, v17 dst_sel:DWORD dst_unused:UNUSED_PAD src0_sel:WORD_1
	v_add_u32_e32 v168, v187, v199
	v_pk_fma_f16 v44, v10, v30, v18
	v_pk_fma_f16 v45, v11, v31, v19
	v_lshlrev_b64 v[10:11], 9, v[168:169]
	v_or_b32_e32 v10, v10, v198
	v_lshl_add_u64 v[38:39], s[20:21], 0, v[10:11]
	v_lshl_add_u64 v[40:41], s[22:23], 0, v[10:11]
	v_pack_b32_f16 v48, v14, v15
	v_pack_b32_f16 v49, v12, v13
	v_pack_b32_f16 v46, v46, v16
	v_pack_b32_f16 v47, v47, v17
	global_load_dwordx4 v[10:13], v[38:39], off nt
	global_load_dwordx4 v[14:17], v[40:41], off nt
	v_cvt_f32_f16_sdwa v21, v139 dst_sel:DWORD dst_unused:UNUSED_PAD src0_sel:WORD_1
	v_cvt_f32_f16_e32 v20, v139
	v_cvt_f32_f16_sdwa v19, v138 dst_sel:DWORD dst_unused:UNUSED_PAD src0_sel:WORD_1
	v_cvt_f32_f16_e32 v18, v138
	v_cvt_f32_f16_sdwa v33, v141 dst_sel:DWORD dst_unused:UNUSED_PAD src0_sel:WORD_1
	v_cvt_f32_f16_e32 v32, v141
	v_pk_mul_f16 v58, v43, v46
	v_pk_mul_f16 v59, v42, v47
	v_cvt_f32_f16_sdwa v31, v140 dst_sel:DWORD dst_unused:UNUSED_PAD src0_sel:WORD_1
	v_cvt_f32_f16_e32 v30, v140
	v_pk_mul_f16 v52, v45, v48
	v_pk_mul_f16 v53, v44, v49
	v_add_u32_e32 v168, v190, v199
	v_lshlrev_b64 v[36:37], 9, v[168:169]
	v_or_b32_e32 v36, v36, v198
	v_lshl_or_b32 v50, s46, 6, v178
	v_lshlrev_b32_e32 v51, 9, v50
	v_add_u32_e32 v203, v184, v51
	v_cvt_f32_f16_sdwa v35, v77 dst_sel:DWORD dst_unused:UNUSED_PAD src0_sel:WORD_1
	v_cvt_f32_f16_e32 v34, v77
	v_add_lshl_u32 v202, v188, v50, 9
	s_mov_b64 s[4:5], -1
	s_and_b64 vcc, exec, s[26:27]
	s_waitcnt vmcnt(5)
	v_cvt_f32_f16_e32 v38, v2
	v_cvt_f32_f16_sdwa v39, v2 dst_sel:DWORD dst_unused:UNUSED_PAD src0_sel:WORD_1
	v_cvt_f32_f16_e32 v2, v3
	v_cvt_f32_f16_sdwa v3, v3 dst_sel:DWORD dst_unused:UNUSED_PAD src0_sel:WORD_1
	s_waitcnt vmcnt(4)
	v_cvt_f32_f16_e32 v40, v6
	v_cvt_f32_f16_sdwa v41, v6 dst_sel:DWORD dst_unused:UNUSED_PAD src0_sel:WORD_1
	v_cvt_f32_f16_e32 v6, v7
	v_cvt_f32_f16_sdwa v7, v7 dst_sel:DWORD dst_unused:UNUSED_PAD src0_sel:WORD_1
	v_cvt_f32_f16_e32 v42, v4
	v_cvt_f32_f16_sdwa v43, v4 dst_sel:DWORD dst_unused:UNUSED_PAD src0_sel:WORD_1
	v_cvt_f32_f16_e32 v4, v5
	v_cvt_f32_f16_sdwa v5, v5 dst_sel:DWORD dst_unused:UNUSED_PAD src0_sel:WORD_1
	v_cvt_f32_f16_e32 v44, v8
	v_cvt_f32_f16_sdwa v45, v8 dst_sel:DWORD dst_unused:UNUSED_PAD src0_sel:WORD_1
	v_cvt_f32_f16_e32 v8, v9
	v_cvt_f32_f16_sdwa v9, v9 dst_sel:DWORD dst_unused:UNUSED_PAD src0_sel:WORD_1
	v_pk_add_f32 v[2:3], v[20:21], v[2:3]
	v_pk_add_f32 v[18:19], v[18:19], v[38:39]
	v_pk_add_f32 v[4:5], v[32:33], v[4:5]
	v_pk_add_f32 v[6:7], v[2:3], v[6:7]
	v_pk_add_f32 v[20:21], v[30:31], v[42:43]
	v_pk_add_f32 v[18:19], v[18:19], v[40:41]
	v_pk_add_f32 v[8:9], v[4:5], v[8:9]
	v_cvt_pk_f16_f32 v3, v6, v7
	v_lshl_add_u64 v[6:7], s[20:21], 0, v[36:37]
	v_pk_add_f32 v[20:21], v[20:21], v[44:45]
	v_cvt_pk_f16_f32 v2, v18, v19
	v_cvt_pk_f16_f32 v5, v8, v9
	global_load_dwordx4 v[6:9], v[6:7], off nt
	v_lshl_add_u64 v[18:19], s[22:23], 0, v[36:37]
	v_cvt_pk_f16_f32 v4, v20, v21
	global_load_dwordx4 v[18:21], v[18:19], off nt
	s_waitcnt vmcnt(5)
	v_cvt_f32_f16_e32 v46, v22
	v_cvt_f32_f16_sdwa v47, v22 dst_sel:DWORD dst_unused:UNUSED_PAD src0_sel:WORD_1
	ds_write_b128 v203, v[2:5]
	v_cvt_f32_f16_sdwa v5, v76 dst_sel:DWORD dst_unused:UNUSED_PAD src0_sel:WORD_1
	v_cvt_f32_f16_e32 v4, v76
	v_cvt_f32_f16_e32 v22, v23
	v_cvt_f32_f16_sdwa v23, v23 dst_sel:DWORD dst_unused:UNUSED_PAD src0_sel:WORD_1
	s_waitcnt vmcnt(4)
	v_cvt_f32_f16_e32 v48, v26
	v_cvt_f32_f16_sdwa v49, v26 dst_sel:DWORD dst_unused:UNUSED_PAD src0_sel:WORD_1
	v_cvt_f32_f16_e32 v26, v27
	v_cvt_f32_f16_sdwa v27, v27 dst_sel:DWORD dst_unused:UNUSED_PAD src0_sel:WORD_1
	v_cvt_f32_f16_sdwa v31, v75 dst_sel:DWORD dst_unused:UNUSED_PAD src0_sel:WORD_1
	v_cvt_f32_f16_e32 v30, v75
	v_cvt_f32_f16_e32 v32, v24
	v_cvt_f32_f16_sdwa v33, v24 dst_sel:DWORD dst_unused:UNUSED_PAD src0_sel:WORD_1
	v_pk_add_f32 v[4:5], v[4:5], v[22:23]
	v_cvt_f32_f16_e32 v22, v28
	v_pk_add_f32 v[4:5], v[4:5], v[26:27]
	v_cvt_f32_f16_sdwa v23, v28 dst_sel:DWORD dst_unused:UNUSED_PAD src0_sel:WORD_1
	v_cvt_f32_f16_sdwa v27, v74 dst_sel:DWORD dst_unused:UNUSED_PAD src0_sel:WORD_1
	v_cvt_f32_f16_e32 v26, v74
	v_cvt_f32_f16_e32 v24, v25
	v_cvt_f32_f16_sdwa v25, v25 dst_sel:DWORD dst_unused:UNUSED_PAD src0_sel:WORD_1
	v_pk_add_f32 v[2:3], v[34:35], v[46:47]
	v_cvt_f32_f16_e32 v28, v29
	v_cvt_f32_f16_sdwa v29, v29 dst_sel:DWORD dst_unused:UNUSED_PAD src0_sel:WORD_1
	v_pk_add_f32 v[2:3], v[2:3], v[48:49]
	s_nop 0
	v_cvt_pk_f16_f32 v2, v2, v3
	v_cvt_pk_f16_f32 v3, v4, v5
	v_pk_add_f32 v[4:5], v[30:31], v[32:33]
	s_nop 0
	v_pk_add_f32 v[4:5], v[4:5], v[22:23]
	v_pk_add_f32 v[22:23], v[26:27], v[24:25]
	v_cvt_pk_f16_f32 v4, v4, v5
	v_pk_add_f32 v[22:23], v[22:23], v[28:29]
	s_waitcnt vmcnt(3)
	v_cvt_f32_f16_e32 v24, v10
	v_cvt_pk_f16_f32 v5, v22, v23
	v_add_u32_e32 v22, v186, v50
	v_lshlrev_b32_e32 v204, 9, v22
	v_bitop3_b32 v22, v22, v179, 15 bitop3:0x6c
	v_lshlrev_b32_e32 v205, 4, v22
	v_cvt_f32_f16_sdwa v25, v10 dst_sel:DWORD dst_unused:UNUSED_PAD src0_sel:WORD_1
	v_or_b32_e32 v10, v205, v204
	v_cvt_f32_f16_sdwa v23, v57 dst_sel:DWORD dst_unused:UNUSED_PAD src0_sel:WORD_1
	v_cvt_f32_f16_e32 v22, v57
	ds_write_b128 v10, v[2:5]
	v_cvt_f32_f16_sdwa v5, v56 dst_sel:DWORD dst_unused:UNUSED_PAD src0_sel:WORD_1
	v_cvt_f32_f16_e32 v4, v56
	v_cvt_f32_f16_e32 v10, v11
	v_cvt_f32_f16_sdwa v11, v11 dst_sel:DWORD dst_unused:UNUSED_PAD src0_sel:WORD_1
	s_waitcnt vmcnt(2)
	v_cvt_f32_f16_e32 v26, v14
	v_cvt_f32_f16_sdwa v27, v14 dst_sel:DWORD dst_unused:UNUSED_PAD src0_sel:WORD_1
	v_cvt_f32_f16_e32 v14, v15
	v_cvt_f32_f16_sdwa v15, v15 dst_sel:DWORD dst_unused:UNUSED_PAD src0_sel:WORD_1
	v_pk_add_f32 v[2:3], v[22:23], v[24:25]
	v_cvt_f32_f16_sdwa v23, v55 dst_sel:DWORD dst_unused:UNUSED_PAD src0_sel:WORD_1
	v_cvt_f32_f16_e32 v22, v55
	v_cvt_f32_f16_e32 v24, v12
	v_cvt_f32_f16_sdwa v25, v12 dst_sel:DWORD dst_unused:UNUSED_PAD src0_sel:WORD_1
	v_pk_add_f32 v[4:5], v[4:5], v[10:11]
	v_cvt_f32_f16_e32 v10, v16
	v_pk_add_f32 v[4:5], v[4:5], v[14:15]
	v_cvt_f32_f16_sdwa v11, v16 dst_sel:DWORD dst_unused:UNUSED_PAD src0_sel:WORD_1
	v_cvt_f32_f16_sdwa v15, v54 dst_sel:DWORD dst_unused:UNUSED_PAD src0_sel:WORD_1
	v_cvt_f32_f16_e32 v14, v54
	v_cvt_f32_f16_e32 v12, v13
	v_cvt_f32_f16_sdwa v13, v13 dst_sel:DWORD dst_unused:UNUSED_PAD src0_sel:WORD_1
	v_cvt_f32_f16_e32 v16, v17
	v_cvt_f32_f16_sdwa v17, v17 dst_sel:DWORD dst_unused:UNUSED_PAD src0_sel:WORD_1
	v_pk_add_f32 v[2:3], v[2:3], v[26:27]
	s_nop 0
	v_cvt_pk_f16_f32 v2, v2, v3
	v_cvt_pk_f16_f32 v3, v4, v5
	v_pk_add_f32 v[4:5], v[22:23], v[24:25]
	s_nop 0
	v_pk_add_f32 v[4:5], v[4:5], v[10:11]
	v_pk_add_f32 v[10:11], v[14:15], v[12:13]
	v_cvt_pk_f16_f32 v4, v4, v5
	v_pk_add_f32 v[10:11], v[10:11], v[16:17]
	s_waitcnt vmcnt(1)
	v_cvt_f32_f16_e32 v12, v6
	v_cvt_pk_f16_f32 v5, v10, v11
	v_cvt_f32_f16_e32 v10, v53
	v_cvt_f32_f16_sdwa v11, v53 dst_sel:DWORD dst_unused:UNUSED_PAD src0_sel:WORD_1
	v_cvt_f32_f16_sdwa v13, v6 dst_sel:DWORD dst_unused:UNUSED_PAD src0_sel:WORD_1
	s_waitcnt vmcnt(0)
	v_cvt_f32_f16_e32 v14, v18
	v_cvt_f32_f16_sdwa v15, v18 dst_sel:DWORD dst_unused:UNUSED_PAD src0_sel:WORD_1
	v_or_b32_e32 v6, v189, v202
	ds_write_b128 v6, v[2:5]
	v_cvt_f32_f16_e32 v4, v52
	v_cvt_f32_f16_sdwa v5, v52 dst_sel:DWORD dst_unused:UNUSED_PAD src0_sel:WORD_1
	v_cvt_f32_f16_e32 v6, v7
	v_cvt_f32_f16_sdwa v7, v7 dst_sel:DWORD dst_unused:UNUSED_PAD src0_sel:WORD_1
	v_pk_add_f32 v[2:3], v[10:11], v[12:13]
	v_cvt_f32_f16_e32 v10, v19
	v_cvt_f32_f16_sdwa v11, v19 dst_sel:DWORD dst_unused:UNUSED_PAD src0_sel:WORD_1
	v_pk_add_f32 v[2:3], v[2:3], v[14:15]
	v_cvt_f32_f16_e32 v12, v58
	v_cvt_f32_f16_sdwa v13, v58 dst_sel:DWORD dst_unused:UNUSED_PAD src0_sel:WORD_1
	v_cvt_f32_f16_e32 v14, v8
	v_cvt_f32_f16_sdwa v15, v8 dst_sel:DWORD dst_unused:UNUSED_PAD src0_sel:WORD_1
	v_pk_add_f32 v[4:5], v[4:5], v[6:7]
	v_cvt_f32_f16_e32 v6, v20
	v_pk_add_f32 v[4:5], v[4:5], v[10:11]
	v_cvt_f32_f16_sdwa v7, v20 dst_sel:DWORD dst_unused:UNUSED_PAD src0_sel:WORD_1
	v_cvt_f32_f16_e32 v10, v59
	v_cvt_f32_f16_sdwa v11, v59 dst_sel:DWORD dst_unused:UNUSED_PAD src0_sel:WORD_1
	v_cvt_f32_f16_e32 v8, v9
	v_cvt_f32_f16_sdwa v9, v9 dst_sel:DWORD dst_unused:UNUSED_PAD src0_sel:WORD_1
	v_cvt_pk_f16_f32 v2, v2, v3
	v_cvt_pk_f16_f32 v3, v4, v5
	v_pk_add_f32 v[4:5], v[12:13], v[14:15]
	v_cvt_f32_f16_e32 v12, v21
	v_cvt_f32_f16_sdwa v13, v21 dst_sel:DWORD dst_unused:UNUSED_PAD src0_sel:WORD_1
	v_pk_add_f32 v[4:5], v[4:5], v[6:7]
	v_pk_add_f32 v[6:7], v[10:11], v[8:9]
	v_cvt_pk_f16_f32 v4, v4, v5
	v_pk_add_f32 v[6:7], v[6:7], v[12:13]
	s_nop 0
	v_cvt_pk_f16_f32 v5, v6, v7
	v_add_lshl_u32 v6, v191, v50, 9
	v_add_u32_e32 v168, v192, v6
	ds_write_b128 v168, v[2:5]
	global_load_dwordx4 v[2:5], v[174:175], off
	global_load_dwordx4 v[8:11], v[176:177], off
	global_load_dwordx4 v[12:15], v[174:175], off offset:16
	global_load_dwordx4 v[16:19], v[176:177], off offset:16
	s_waitcnt vmcnt(3)
	v_cvt_pk_f16_f32 v6, v2, v3
	s_waitcnt vmcnt(2)
	v_cvt_pk_f16_f32 v2, v8, v9
	v_cvt_pk_f16_f32 v7, v4, v5
	v_cvt_pk_f16_f32 v3, v10, v11
	s_waitcnt vmcnt(1)
	v_cvt_pk_f16_f32 v8, v12, v13
	s_waitcnt vmcnt(0)
	v_cvt_pk_f16_f32 v4, v16, v17
	v_cvt_pk_f16_f32 v9, v14, v15
	v_cvt_pk_f16_f32 v5, v18, v19
	s_cbranch_vccz .LBB4_118
	global_load_dwordx3 v[154:156], v169, s[18:19]
	s_mov_b32 s14, s38
	s_mov_b32 s15, s39
	v_cmp_lt_u32_e64 s[64:65], 0, v199
	v_cmp_gt_u32_e64 s[66:67], 63, v199
	v_cmp_lt_u32_e64 s[68:69], 0, v180
	v_cmp_gt_u32_e64 s[70:71], 60, v180
	buffer_load_dwordx4 v[210:213], v200, s[12:15], 0 offen
	v_add_u32_e32 v246, 0x18000, v200
	buffer_load_dwordx4 v[162:165], v246, s[12:15], 0 offen
	v_add_u32_e32 v245, 0x30000, v200
	buffer_load_dwordx4 v[158:161], v245, s[12:15], 0 offen
	s_and_b64 s[72:73], s[68:69], s[64:65]
	s_and_b64 s[74:75], s[68:69], s[66:67]
	s_and_b64 s[76:77], s[70:71], s[64:65]
	s_and_b64 s[78:79], s[70:71], s[66:67]
	v_add_u32_e32 v245, 0xfffe7c00, v200
	v_add_u32_e32 v246, 0xfffe8000, v200
	v_mov_b32_e32 v122, v6
	v_mov_b32_e32 v123, v7
	v_mov_b32_e32 v124, v8
	v_mov_b32_e32 v125, v9
	v_mov_b32_e32 v82, v2
	v_mov_b32_e32 v83, v3
	v_mov_b32_e32 v84, v4
	v_mov_b32_e32 v85, v5
	v_mov_b32_e32 v138, v6
	v_mov_b32_e32 v139, v7
	v_mov_b32_e32 v140, v8
	v_mov_b32_e32 v141, v9
	v_mov_b32_e32 v106, v2
	v_mov_b32_e32 v107, v3
	v_mov_b32_e32 v108, v4
	v_mov_b32_e32 v109, v5
	v_mov_b32_e32 v146, v6
	v_mov_b32_e32 v147, v7
	v_mov_b32_e32 v148, v8
	v_mov_b32_e32 v149, v9
	v_mov_b32_e32 v126, v2
	v_mov_b32_e32 v127, v3
	v_mov_b32_e32 v128, v4
	v_mov_b32_e32 v129, v5
	s_mov_b64 exec, s[72:73]
	buffer_load_dwordx4 v[122:125], v245, s[12:15], 0 offen
	buffer_load_dwordx4 v[82:85], v245, s[12:15], 0 offen offset:512
	s_mov_b64 exec, -1
	s_mov_b64 exec, s[68:69]
	buffer_load_dwordx4 v[138:141], v246, s[12:15], 0 offen offset:512
	buffer_load_dwordx4 v[106:109], v246, s[12:15], 0 offen offset:1024
	s_mov_b64 exec, -1
	s_mov_b64 exec, s[74:75]
	buffer_load_dwordx4 v[146:149], v246, s[12:15], 0 offen offset:2048
	buffer_load_dwordx4 v[126:129], v246, s[12:15], 0 offen offset:2560
	s_mov_b64 exec, -1
	v_add_u32_e32 v245, 0xfffffc00, v200
	v_mov_b32_e32 v94, v6
	v_mov_b32_e32 v95, v7
	v_mov_b32_e32 v96, v8
	v_mov_b32_e32 v97, v9
	v_mov_b32_e32 v54, v2
	v_mov_b32_e32 v55, v3
	v_mov_b32_e32 v56, v4
	v_mov_b32_e32 v57, v5
	v_mov_b32_e32 v134, v6
	v_mov_b32_e32 v135, v7
	v_mov_b32_e32 v136, v8
	v_mov_b32_e32 v137, v9
	v_mov_b32_e32 v98, v2
	v_mov_b32_e32 v99, v3
	v_mov_b32_e32 v100, v4
	v_mov_b32_e32 v101, v5
	s_mov_b64 exec, s[64:65]
	buffer_load_dwordx4 v[94:97], v245, s[12:15], 0 offen
	buffer_load_dwordx4 v[54:57], v245, s[12:15], 0 offen offset:512
	s_mov_b64 exec, -1
	buffer_load_dwordx4 v[118:121], v200, s[12:15], 0 offen offset:512
	buffer_load_dwordx4 v[74:77], v200, s[12:15], 0 offen offset:1024
	s_mov_b64 exec, s[66:67]
	buffer_load_dwordx4 v[134:137], v200, s[12:15], 0 offen offset:2048
	buffer_load_dwordx4 v[98:101], v200, s[12:15], 0 offen offset:2560
	s_mov_b64 exec, -1
	v_add_u32_e32 v245, 0x17c00, v200
	v_add_u32_e32 v246, 0x18000, v200
	v_mov_b32_e32 v62, v6
	v_mov_b32_e32 v63, v7
	v_mov_b32_e32 v64, v8
	v_mov_b32_e32 v65, v9
	v_mov_b32_e32 v30, v2
	v_mov_b32_e32 v31, v3
	v_mov_b32_e32 v32, v4
	v_mov_b32_e32 v33, v5
	v_mov_b32_e32 v102, v6
	v_mov_b32_e32 v103, v7
	v_mov_b32_e32 v104, v8
	v_mov_b32_e32 v105, v9
	v_mov_b32_e32 v58, v2
	v_mov_b32_e32 v59, v3
	v_mov_b32_e32 v60, v4
	v_mov_b32_e32 v61, v5
	s_mov_b64 exec, s[64:65]
	buffer_load_dwordx4 v[62:65], v245, s[12:15], 0 offen
	buffer_load_dwordx4 v[30:33], v245, s[12:15], 0 offen offset:512
	s_mov_b64 exec, -1
	buffer_load_dwordx4 v[78:81], v246, s[12:15], 0 offen offset:512
	buffer_load_dwordx4 v[42:45], v246, s[12:15], 0 offen offset:1024
	s_mov_b64 exec, s[66:67]
	buffer_load_dwordx4 v[102:105], v246, s[12:15], 0 offen offset:2048
	buffer_load_dwordx4 v[58:61], v246, s[12:15], 0 offen offset:2560
	s_mov_b64 exec, -1
	v_add_u32_e32 v245, 0x2fc00, v200
	v_add_u32_e32 v246, 0x30000, v200
	v_mov_b32_e32 v34, v6
	v_mov_b32_e32 v35, v7
	v_mov_b32_e32 v36, v8
	v_mov_b32_e32 v37, v9
	v_mov_b32_e32 v18, v2
	v_mov_b32_e32 v19, v3
	v_mov_b32_e32 v20, v4
	v_mov_b32_e32 v21, v5
	v_mov_b32_e32 v66, v6
	v_mov_b32_e32 v67, v7
	v_mov_b32_e32 v68, v8
	v_mov_b32_e32 v69, v9
	v_mov_b32_e32 v26, v2
	v_mov_b32_e32 v27, v3
	v_mov_b32_e32 v28, v4
	v_mov_b32_e32 v29, v5
	s_mov_b64 exec, s[64:65]
	buffer_load_dwordx4 v[34:37], v245, s[12:15], 0 offen
	buffer_load_dwordx4 v[18:21], v245, s[12:15], 0 offen offset:512
	s_mov_b64 exec, -1
	buffer_load_dwordx4 v[46:49], v246, s[12:15], 0 offen offset:512
	buffer_load_dwordx4 v[22:25], v246, s[12:15], 0 offen offset:1024
	s_mov_b64 exec, s[66:67]
	buffer_load_dwordx4 v[66:69], v246, s[12:15], 0 offen offset:2048
	buffer_load_dwordx4 v[26:29], v246, s[12:15], 0 offen offset:2560
	s_mov_b64 exec, -1
	v_add_u32_e32 v245, 0x47c00, v200
	v_add_u32_e32 v246, 0x48000, v200
	v_mov_b32_e32 v86, v6
	v_mov_b32_e32 v87, v7
	v_mov_b32_e32 v88, v8
	v_mov_b32_e32 v89, v9
	v_mov_b32_e32 v38, v2
	v_mov_b32_e32 v39, v3
	v_mov_b32_e32 v40, v4
	v_mov_b32_e32 v41, v5
	v_mov_b32_e32 v130, v6
	v_mov_b32_e32 v131, v7
	v_mov_b32_e32 v132, v8
	v_mov_b32_e32 v133, v9
	v_mov_b32_e32 v70, v2
	v_mov_b32_e32 v71, v3
	v_mov_b32_e32 v72, v4
	v_mov_b32_e32 v73, v5
	s_mov_b64 exec, s[64:65]
	buffer_load_dwordx4 v[86:89], v245, s[12:15], 0 offen
	buffer_load_dwordx4 v[38:41], v245, s[12:15], 0 offen offset:512
	s_mov_b64 exec, -1
	buffer_load_dwordx4 v[114:117], v246, s[12:15], 0 offen offset:512
	buffer_load_dwordx4 v[50:53], v246, s[12:15], 0 offen offset:1024
	s_mov_b64 exec, s[66:67]
	buffer_load_dwordx4 v[130:133], v246, s[12:15], 0 offen offset:2048
	buffer_load_dwordx4 v[70:73], v246, s[12:15], 0 offen offset:2560
	s_mov_b64 exec, -1
	v_add_u32_e32 v245, 0x5fc00, v200
	v_add_u32_e32 v246, 0x60000, v200
	v_mov_b32_e32 v142, v6
	v_mov_b32_e32 v143, v7
	v_mov_b32_e32 v144, v8
	v_mov_b32_e32 v145, v9
	v_mov_b32_e32 v90, v2
	v_mov_b32_e32 v91, v3
	v_mov_b32_e32 v92, v4
	v_mov_b32_e32 v93, v5
	v_mov_b32_e32 v150, v6
	v_mov_b32_e32 v151, v7
	v_mov_b32_e32 v152, v8
	v_mov_b32_e32 v153, v9
	v_mov_b32_e32 v110, v2
	v_mov_b32_e32 v111, v3
	v_mov_b32_e32 v112, v4
	v_mov_b32_e32 v113, v5
	v_mov_b32_e32 v14, v6
	v_mov_b32_e32 v15, v7
	v_mov_b32_e32 v16, v8
	v_mov_b32_e32 v17, v9
	v_mov_b32_e32 v10, v2
	v_mov_b32_e32 v11, v3
	v_mov_b32_e32 v12, v4
	v_mov_b32_e32 v13, v5
	s_mov_b64 exec, s[76:77]
	buffer_load_dwordx4 v[142:145], v245, s[12:15], 0 offen
	buffer_load_dwordx4 v[90:93], v245, s[12:15], 0 offen offset:512
	s_mov_b64 exec, -1
	s_mov_b64 exec, s[70:71]
	buffer_load_dwordx4 v[150:153], v246, s[12:15], 0 offen offset:512
	buffer_load_dwordx4 v[110:113], v246, s[12:15], 0 offen offset:1024
	s_mov_b64 exec, -1
	s_mov_b64 exec, s[78:79]
	buffer_load_dwordx4 v[14:17], v246, s[12:15], 0 offen offset:2048
	buffer_load_dwordx4 v[10:13], v246, s[12:15], 0 offen offset:2560
	s_mov_b64 exec, -1
	s_waitcnt vmcnt(39)
	v_cvt_f16_f32_e32 v206, v155
	v_cvt_f16_f32_e32 v208, v154
	v_cvt_f16_f32_e32 v207, v156
	v_add_u32_e32 v245, 0x48000, v200
	buffer_load_dwordx4 v[154:157], v245, s[12:15], 0 offen
	s_mov_b64 s[4:5], 0
	s_waitcnt vmcnt(19)
	v_pk_mul_f16 v216, v208, v213 op_sel_hi:[0,1]
	v_pk_mul_f16 v220, v206, v213 op_sel_hi:[0,1]
	v_pk_mul_f16 v224, v207, v213 op_sel_hi:[0,1]
	v_pk_mul_f16 v209, v208, v210 op_sel_hi:[0,1]
	v_pk_mul_f16 v214, v208, v211 op_sel_hi:[0,1]
	v_pk_mul_f16 v215, v208, v212 op_sel_hi:[0,1]
	v_pk_mul_f16 v217, v206, v210 op_sel_hi:[0,1]
	v_pk_mul_f16 v218, v206, v211 op_sel_hi:[0,1]
	v_pk_mul_f16 v219, v206, v212 op_sel_hi:[0,1]
	v_pk_mul_f16 v221, v207, v210 op_sel_hi:[0,1]
	v_pk_mul_f16 v222, v207, v211 op_sel_hi:[0,1]
	v_pk_mul_f16 v223, v207, v212 op_sel_hi:[0,1]
	v_pk_fma_f16 v125, v125, v213, v216
	v_pk_fma_f16 v141, v141, v213, v220
	v_pk_fma_f16 v149, v149, v213, v224
	v_pk_fma_f16 v225, v97, v213, v216
	v_pk_fma_f16 v229, v121, v213, v220
	v_pk_fma_f16 v233, v137, v213, v224
	v_pk_fma_f16 v216, v65, v213, v216
	v_pk_fma_f16 v220, v81, v213, v220
	v_pk_fma_f16 v213, v105, v213, v224
	v_pk_maximum3_f16 v224, v125, v141, v149
	v_pk_fma_f16 v124, v124, v212, v215
	v_pk_fma_f16 v123, v123, v211, v214
	v_pk_fma_f16 v122, v122, v210, v209
	v_pk_fma_f16 v140, v140, v212, v219
	v_pk_fma_f16 v139, v139, v211, v218
	v_pk_fma_f16 v138, v138, v210, v217
	v_pk_fma_f16 v148, v148, v212, v223
	v_pk_fma_f16 v147, v147, v211, v222
	v_pk_fma_f16 v146, v146, v210, v221
	v_pk_fma_f16 v226, v96, v212, v215
	v_pk_fma_f16 v227, v95, v211, v214
	v_pk_fma_f16 v228, v94, v210, v209
	v_pk_fma_f16 v230, v120, v212, v219
	v_pk_fma_f16 v231, v119, v211, v218
	v_pk_fma_f16 v232, v118, v210, v217
	v_pk_fma_f16 v234, v136, v212, v223
	v_pk_fma_f16 v235, v135, v211, v222
	v_pk_fma_f16 v236, v134, v210, v221
	v_pk_fma_f16 v215, v64, v212, v215
	v_pk_fma_f16 v214, v63, v211, v214
	v_pk_fma_f16 v209, v62, v210, v209
	v_pk_fma_f16 v219, v80, v212, v219
	v_pk_fma_f16 v218, v79, v211, v218
	v_pk_fma_f16 v217, v78, v210, v217
	v_pk_fma_f16 v212, v104, v212, v223
	v_pk_fma_f16 v211, v103, v211, v222
	v_pk_fma_f16 v210, v102, v210, v221
	v_pk_maximum3_f16 v221, v122, v138, v146
	v_pk_maximum3_f16 v222, v123, v139, v147
	v_pk_maximum3_f16 v223, v124, v140, v148
	v_pk_maximum3_f16 v240, v225, v229, v233
	v_pk_maximum3_f16 v244, v216, v220, v213
	v_pk_maximum3_f16 v237, v228, v232, v236
	v_pk_maximum3_f16 v238, v227, v231, v235
	v_pk_maximum3_f16 v239, v226, v230, v234
	s_nop 0
	v_pk_maximum3_f16 v241, v209, v217, v210
	v_pk_maximum3_f16 v242, v214, v218, v211
	v_pk_maximum3_f16 v224, v224, v240, v244
	v_pk_maximum3_f16 v243, v215, v219, v212
	s_nop 0
	v_pk_maximum3_f16 v221, v221, v237, v241
	v_pk_maximum3_f16 v222, v222, v238, v242
	v_pk_maximum3_f16 v223, v223, v239, v243
	v_xor_b32_e32 v224, 0x80008000, v224
	v_xor_b32_e32 v223, 0x80008000, v223
	v_xor_b32_e32 v222, 0x80008000, v222
	v_xor_b32_e32 v221, 0x80008000, v221
	v_pk_add_f16 v125, v125, v224
	v_pk_add_f16 v122, v122, v221
	v_pk_add_f16 v123, v123, v222
	v_pk_add_f16 v124, v124, v223
	v_pk_add_f16 v138, v138, v221
	v_exp_f16_sdwa v237, v122 dst_sel:WORD_0 dst_unused:UNUSED_PAD src0_sel:WORD_0
	v_exp_f16_sdwa v238, v123 dst_sel:WORD_0 dst_unused:UNUSED_PAD src0_sel:WORD_0
	v_exp_f16_sdwa v239, v124 dst_sel:WORD_0 dst_unused:UNUSED_PAD src0_sel:WORD_0
	v_exp_f16_sdwa v240, v125 dst_sel:WORD_0 dst_unused:UNUSED_PAD src0_sel:WORD_0
	v_exp_f16_sdwa v237, v122 dst_sel:WORD_1 dst_unused:UNUSED_PRESERVE src0_sel:WORD_1
	v_exp_f16_sdwa v238, v123 dst_sel:WORD_1 dst_unused:UNUSED_PRESERVE src0_sel:WORD_1
	v_exp_f16_sdwa v239, v124 dst_sel:WORD_1 dst_unused:UNUSED_PRESERVE src0_sel:WORD_1
	v_exp_f16_sdwa v240, v125 dst_sel:WORD_1 dst_unused:UNUSED_PRESERVE src0_sel:WORD_1
	s_nop 0
	v_pk_add_f16 v139, v139, v222
	v_pk_add_f16 v125, v237, 0
	v_pk_fma_f16 v85, v85, v240, 0
	v_pk_add_f16 v122, v240, 0
	v_pk_add_f16 v123, v239, 0
	v_pk_add_f16 v124, v238, 0
	v_pk_fma_f16 v84, v84, v239, 0
	v_pk_fma_f16 v83, v83, v238, 0
	v_pk_fma_f16 v82, v82, v237, 0
	v_pk_add_f16 v140, v140, v223
	v_pk_add_f16 v141, v141, v224
	s_nop 0
	v_exp_f16_sdwa v237, v138 dst_sel:WORD_0 dst_unused:UNUSED_PAD src0_sel:WORD_0
	v_exp_f16_sdwa v238, v139 dst_sel:WORD_0 dst_unused:UNUSED_PAD src0_sel:WORD_0
	v_exp_f16_sdwa v239, v140 dst_sel:WORD_0 dst_unused:UNUSED_PAD src0_sel:WORD_0
	v_exp_f16_sdwa v240, v141 dst_sel:WORD_0 dst_unused:UNUSED_PAD src0_sel:WORD_0
	v_exp_f16_sdwa v237, v138 dst_sel:WORD_1 dst_unused:UNUSED_PRESERVE src0_sel:WORD_1
	v_exp_f16_sdwa v238, v139 dst_sel:WORD_1 dst_unused:UNUSED_PRESERVE src0_sel:WORD_1
	v_exp_f16_sdwa v239, v140 dst_sel:WORD_1 dst_unused:UNUSED_PRESERVE src0_sel:WORD_1
	v_exp_f16_sdwa v240, v141 dst_sel:WORD_1 dst_unused:UNUSED_PRESERVE src0_sel:WORD_1
	s_nop 0
	s_nop 0
	v_pk_add_f16 v125, v125, v237
	v_pk_fma_f16 v85, v109, v240, v85
	v_pk_add_f16 v109, v149, v224
	v_pk_add_f16 v124, v124, v238
	v_pk_add_f16 v123, v123, v239
	v_pk_add_f16 v122, v122, v240
	v_pk_fma_f16 v82, v106, v237, v82
	v_pk_fma_f16 v83, v107, v238, v83
	v_pk_fma_f16 v84, v108, v239, v84
	v_pk_add_f16 v106, v146, v221
	v_pk_add_f16 v107, v147, v222
	v_pk_add_f16 v108, v148, v223
	s_nop 0
	v_exp_f16_sdwa v138, v106 dst_sel:WORD_0 dst_unused:UNUSED_PAD src0_sel:WORD_0
	v_exp_f16_sdwa v139, v107 dst_sel:WORD_0 dst_unused:UNUSED_PAD src0_sel:WORD_0
	v_exp_f16_sdwa v140, v108 dst_sel:WORD_0 dst_unused:UNUSED_PAD src0_sel:WORD_0
	v_exp_f16_sdwa v141, v109 dst_sel:WORD_0 dst_unused:UNUSED_PAD src0_sel:WORD_0
	v_exp_f16_sdwa v138, v106 dst_sel:WORD_1 dst_unused:UNUSED_PRESERVE src0_sel:WORD_1
	v_exp_f16_sdwa v139, v107 dst_sel:WORD_1 dst_unused:UNUSED_PRESERVE src0_sel:WORD_1
	v_exp_f16_sdwa v140, v108 dst_sel:WORD_1 dst_unused:UNUSED_PRESERVE src0_sel:WORD_1
	v_exp_f16_sdwa v141, v109 dst_sel:WORD_1 dst_unused:UNUSED_PRESERVE src0_sel:WORD_1
	s_nop 0
	s_nop 0
	v_pk_add_f16 v109, v125, v138
	v_pk_add_f16 v106, v122, v141
	v_pk_add_f16 v107, v123, v140
	v_pk_add_f16 v108, v124, v139
	v_pk_fma_f16 v85, v129, v141, v85
	v_pk_fma_f16 v84, v128, v140, v84
	v_pk_fma_f16 v83, v127, v139, v83
	v_pk_fma_f16 v82, v126, v138, v82
	v_pk_add_f16 v122, v228, v221
	v_pk_add_f16 v123, v227, v222
	v_pk_add_f16 v124, v226, v223
	v_pk_add_f16 v125, v225, v224
	s_nop 0
	v_exp_f16_sdwa v126, v122 dst_sel:WORD_0 dst_unused:UNUSED_PAD src0_sel:WORD_0
	v_exp_f16_sdwa v127, v123 dst_sel:WORD_0 dst_unused:UNUSED_PAD src0_sel:WORD_0
	v_exp_f16_sdwa v128, v124 dst_sel:WORD_0 dst_unused:UNUSED_PAD src0_sel:WORD_0
	v_exp_f16_sdwa v129, v125 dst_sel:WORD_0 dst_unused:UNUSED_PAD src0_sel:WORD_0
	v_exp_f16_sdwa v126, v122 dst_sel:WORD_1 dst_unused:UNUSED_PRESERVE src0_sel:WORD_1
	v_exp_f16_sdwa v127, v123 dst_sel:WORD_1 dst_unused:UNUSED_PRESERVE src0_sel:WORD_1
	v_exp_f16_sdwa v128, v124 dst_sel:WORD_1 dst_unused:UNUSED_PRESERVE src0_sel:WORD_1
	v_exp_f16_sdwa v129, v125 dst_sel:WORD_1 dst_unused:UNUSED_PRESERVE src0_sel:WORD_1
	s_nop 0
	v_pk_add_f16 v122, v232, v221
	v_pk_add_f16 v109, v109, v126
	v_pk_add_f16 v108, v108, v127
	v_pk_add_f16 v107, v107, v128
	v_pk_add_f16 v106, v106, v129
	v_pk_fma_f16 v82, v54, v126, v82
	v_pk_fma_f16 v83, v55, v127, v83
	v_pk_fma_f16 v84, v56, v128, v84
	v_pk_fma_f16 v85, v57, v129, v85
	v_pk_add_f16 v123, v231, v222
	v_pk_add_f16 v124, v230, v223
	v_pk_add_f16 v125, v229, v224
	s_nop 0
	v_exp_f16_sdwa v126, v122 dst_sel:WORD_0 dst_unused:UNUSED_PAD src0_sel:WORD_0
	v_exp_f16_sdwa v127, v123 dst_sel:WORD_0 dst_unused:UNUSED_PAD src0_sel:WORD_0
	v_exp_f16_sdwa v128, v124 dst_sel:WORD_0 dst_unused:UNUSED_PAD src0_sel:WORD_0
	v_exp_f16_sdwa v129, v125 dst_sel:WORD_0 dst_unused:UNUSED_PAD src0_sel:WORD_0
	v_exp_f16_sdwa v126, v122 dst_sel:WORD_1 dst_unused:UNUSED_PRESERVE src0_sel:WORD_1
	v_exp_f16_sdwa v127, v123 dst_sel:WORD_1 dst_unused:UNUSED_PRESERVE src0_sel:WORD_1
	v_exp_f16_sdwa v128, v124 dst_sel:WORD_1 dst_unused:UNUSED_PRESERVE src0_sel:WORD_1
	v_exp_f16_sdwa v129, v125 dst_sel:WORD_1 dst_unused:UNUSED_PRESERVE src0_sel:WORD_1
	s_nop 0
	v_pk_add_f16 v122, v236, v221
	v_pk_add_f16 v109, v109, v126
	v_pk_add_f16 v106, v106, v129
	v_pk_add_f16 v107, v107, v128
	v_pk_add_f16 v108, v108, v127
	v_pk_fma_f16 v85, v77, v129, v85
	v_pk_fma_f16 v84, v76, v128, v84
	v_pk_fma_f16 v83, v75, v127, v83
	v_pk_fma_f16 v82, v74, v126, v82
	v_pk_add_f16 v123, v235, v222
	v_pk_add_f16 v124, v234, v223
	v_pk_add_f16 v125, v233, v224
	s_nop 0
	v_exp_f16_sdwa v126, v122 dst_sel:WORD_0 dst_unused:UNUSED_PAD src0_sel:WORD_0
	v_exp_f16_sdwa v127, v123 dst_sel:WORD_0 dst_unused:UNUSED_PAD src0_sel:WORD_0
	v_exp_f16_sdwa v128, v124 dst_sel:WORD_0 dst_unused:UNUSED_PAD src0_sel:WORD_0
	v_exp_f16_sdwa v129, v125 dst_sel:WORD_0 dst_unused:UNUSED_PAD src0_sel:WORD_0
	v_exp_f16_sdwa v126, v122 dst_sel:WORD_1 dst_unused:UNUSED_PRESERVE src0_sel:WORD_1
	v_exp_f16_sdwa v127, v123 dst_sel:WORD_1 dst_unused:UNUSED_PRESERVE src0_sel:WORD_1
	v_exp_f16_sdwa v128, v124 dst_sel:WORD_1 dst_unused:UNUSED_PRESERVE src0_sel:WORD_1
	v_exp_f16_sdwa v129, v125 dst_sel:WORD_1 dst_unused:UNUSED_PRESERVE src0_sel:WORD_1
	s_nop 0
	v_pk_add_f16 v122, v209, v221
	v_pk_add_f16 v109, v109, v126
	v_pk_add_f16 v108, v108, v127
	v_pk_add_f16 v107, v107, v128
	v_pk_add_f16 v106, v106, v129
	v_pk_fma_f16 v82, v98, v126, v82
	v_pk_fma_f16 v83, v99, v127, v83
	v_pk_fma_f16 v84, v100, v128, v84
	v_pk_fma_f16 v85, v101, v129, v85
	v_pk_add_f16 v123, v214, v222
	v_pk_add_f16 v124, v215, v223
	v_pk_add_f16 v125, v216, v224
	s_nop 0
	v_exp_f16_sdwa v126, v122 dst_sel:WORD_0 dst_unused:UNUSED_PAD src0_sel:WORD_0
	v_exp_f16_sdwa v127, v123 dst_sel:WORD_0 dst_unused:UNUSED_PAD src0_sel:WORD_0
	v_exp_f16_sdwa v128, v124 dst_sel:WORD_0 dst_unused:UNUSED_PAD src0_sel:WORD_0
	v_exp_f16_sdwa v129, v125 dst_sel:WORD_0 dst_unused:UNUSED_PAD src0_sel:WORD_0
	v_exp_f16_sdwa v126, v122 dst_sel:WORD_1 dst_unused:UNUSED_PRESERVE src0_sel:WORD_1
	v_exp_f16_sdwa v127, v123 dst_sel:WORD_1 dst_unused:UNUSED_PRESERVE src0_sel:WORD_1
	v_exp_f16_sdwa v128, v124 dst_sel:WORD_1 dst_unused:UNUSED_PRESERVE src0_sel:WORD_1
	v_exp_f16_sdwa v129, v125 dst_sel:WORD_1 dst_unused:UNUSED_PRESERVE src0_sel:WORD_1
	s_nop 0
	v_pk_add_f16 v122, v217, v221
	v_pk_add_f16 v109, v109, v126
	v_pk_add_f16 v106, v106, v129
	v_pk_add_f16 v107, v107, v128
	v_pk_add_f16 v108, v108, v127
	v_pk_fma_f16 v85, v33, v129, v85
	v_pk_fma_f16 v84, v32, v128, v84
	v_pk_fma_f16 v83, v31, v127, v83
	v_pk_fma_f16 v82, v30, v126, v82
	v_pk_add_f16 v123, v218, v222
	v_pk_add_f16 v124, v219, v223
	v_pk_add_f16 v125, v220, v224
	s_nop 0
	v_exp_f16_sdwa v126, v122 dst_sel:WORD_0 dst_unused:UNUSED_PAD src0_sel:WORD_0
	v_exp_f16_sdwa v127, v123 dst_sel:WORD_0 dst_unused:UNUSED_PAD src0_sel:WORD_0
	v_exp_f16_sdwa v128, v124 dst_sel:WORD_0 dst_unused:UNUSED_PAD src0_sel:WORD_0
	v_exp_f16_sdwa v129, v125 dst_sel:WORD_0 dst_unused:UNUSED_PAD src0_sel:WORD_0
	v_exp_f16_sdwa v126, v122 dst_sel:WORD_1 dst_unused:UNUSED_PRESERVE src0_sel:WORD_1
	v_exp_f16_sdwa v127, v123 dst_sel:WORD_1 dst_unused:UNUSED_PRESERVE src0_sel:WORD_1
	v_exp_f16_sdwa v128, v124 dst_sel:WORD_1 dst_unused:UNUSED_PRESERVE src0_sel:WORD_1
	v_exp_f16_sdwa v129, v125 dst_sel:WORD_1 dst_unused:UNUSED_PRESERVE src0_sel:WORD_1
	s_nop 0
	v_pk_add_f16 v122, v210, v221
	v_pk_add_f16 v109, v109, v126
	v_pk_add_f16 v108, v108, v127
	v_pk_add_f16 v107, v107, v128
	v_pk_add_f16 v106, v106, v129
	v_pk_fma_f16 v82, v42, v126, v82
	v_pk_fma_f16 v83, v43, v127, v83
	v_pk_fma_f16 v84, v44, v128, v84
	v_pk_fma_f16 v85, v45, v129, v85
	v_pk_add_f16 v123, v211, v222
	v_pk_add_f16 v124, v212, v223
	v_pk_add_f16 v125, v213, v224
	s_nop 0
	v_exp_f16_sdwa v126, v122 dst_sel:WORD_0 dst_unused:UNUSED_PAD src0_sel:WORD_0
	v_exp_f16_sdwa v127, v123 dst_sel:WORD_0 dst_unused:UNUSED_PAD src0_sel:WORD_0
	v_exp_f16_sdwa v128, v124 dst_sel:WORD_0 dst_unused:UNUSED_PAD src0_sel:WORD_0
	v_exp_f16_sdwa v129, v125 dst_sel:WORD_0 dst_unused:UNUSED_PAD src0_sel:WORD_0
	v_exp_f16_sdwa v126, v122 dst_sel:WORD_1 dst_unused:UNUSED_PRESERVE src0_sel:WORD_1
	v_exp_f16_sdwa v127, v123 dst_sel:WORD_1 dst_unused:UNUSED_PRESERVE src0_sel:WORD_1
	v_exp_f16_sdwa v128, v124 dst_sel:WORD_1 dst_unused:UNUSED_PRESERVE src0_sel:WORD_1
	v_exp_f16_sdwa v129, v125 dst_sel:WORD_1 dst_unused:UNUSED_PRESERVE src0_sel:WORD_1
	s_nop 0
	s_nop 0
	v_pk_add_f16 v109, v109, v126
	v_pk_add_f16 v108, v108, v127
	v_rcp_f16_e32 v122, v109
	v_rcp_f16_sdwa v109, v109 dst_sel:DWORD dst_unused:UNUSED_PAD src0_sel:WORD_1
	v_pk_add_f16 v107, v107, v128
	v_rcp_f16_e32 v123, v108
	v_rcp_f16_sdwa v108, v108 dst_sel:DWORD dst_unused:UNUSED_PAD src0_sel:WORD_1
	v_pk_add_f16 v106, v106, v129
	v_rcp_f16_e32 v124, v107
	v_rcp_f16_sdwa v107, v107 dst_sel:DWORD dst_unused:UNUSED_PAD src0_sel:WORD_1
	v_rcp_f16_e32 v125, v106
	v_rcp_f16_sdwa v106, v106 dst_sel:DWORD dst_unused:UNUSED_PAD src0_sel:WORD_1
	v_pk_fma_f16 v82, v58, v126, v82
	v_pack_b32_f16 v109, v122, v109
	v_pk_fma_f16 v83, v59, v127, v83
	v_pk_mul_f16 v141, v82, v109
	v_pack_b32_f16 v82, v123, v108
	v_pk_fma_f16 v84, v60, v128, v84
	v_pk_mul_f16 v140, v83, v82
	v_pack_b32_f16 v82, v124, v107
	v_pk_fma_f16 v85, v61, v129, v85
	v_pk_mul_f16 v139, v84, v82
	v_pack_b32_f16 v82, v125, v106
	v_pk_mul_f16 v138, v85, v82
	s_waitcnt vmcnt(13)
	v_pk_mul_f16 v85, v208, v165 op_sel_hi:[0,1]
	v_pk_mul_f16 v109, v206, v165 op_sel_hi:[0,1]
	v_pk_mul_f16 v122, v207, v162 op_sel_hi:[0,1]
	v_pk_mul_f16 v125, v207, v165 op_sel_hi:[0,1]
	v_pk_mul_f16 v82, v208, v162 op_sel_hi:[0,1]
	v_pk_mul_f16 v83, v208, v163 op_sel_hi:[0,1]
	v_pk_mul_f16 v84, v208, v164 op_sel_hi:[0,1]
	v_pk_mul_f16 v106, v206, v162 op_sel_hi:[0,1]
	v_pk_mul_f16 v107, v206, v163 op_sel_hi:[0,1]
	v_pk_mul_f16 v108, v206, v164 op_sel_hi:[0,1]
	v_pk_mul_f16 v123, v207, v163 op_sel_hi:[0,1]
	v_pk_mul_f16 v124, v207, v164 op_sel_hi:[0,1]
	v_pk_fma_f16 v97, v97, v165, v85
	v_pk_fma_f16 v121, v121, v165, v109
	v_pk_fma_f16 v126, v137, v165, v125
	v_pk_fma_f16 v129, v134, v162, v122
	v_pk_fma_f16 v134, v65, v165, v85
	v_pk_fma_f16 v146, v81, v165, v109
	v_pk_fma_f16 v209, v105, v165, v125
	v_pk_fma_f16 v85, v37, v165, v85
	v_pk_fma_f16 v109, v49, v165, v109
	v_pk_fma_f16 v125, v69, v165, v125
	v_pk_maximum3_f16 v165, v97, v121, v126
	v_pk_fma_f16 v96, v96, v164, v84
	v_pk_fma_f16 v95, v95, v163, v83
	v_pk_fma_f16 v94, v94, v162, v82
	v_pk_fma_f16 v120, v120, v164, v108
	v_pk_fma_f16 v119, v119, v163, v107
	v_pk_fma_f16 v118, v118, v162, v106
	v_pk_fma_f16 v127, v136, v164, v124
	v_pk_fma_f16 v128, v135, v163, v123
	v_pk_fma_f16 v135, v64, v164, v84
	v_pk_fma_f16 v136, v63, v163, v83
	v_pk_fma_f16 v137, v62, v162, v82
	v_pk_fma_f16 v147, v80, v164, v108
	v_pk_fma_f16 v148, v79, v163, v107
	v_pk_fma_f16 v149, v78, v162, v106
	v_pk_fma_f16 v210, v104, v164, v124
	v_pk_fma_f16 v211, v103, v163, v123
	v_pk_fma_f16 v212, v102, v162, v122
	v_pk_fma_f16 v84, v36, v164, v84
	v_pk_fma_f16 v83, v35, v163, v83
	v_pk_fma_f16 v82, v34, v162, v82
	v_pk_fma_f16 v108, v48, v164, v108
	v_pk_fma_f16 v107, v47, v163, v107
	v_pk_fma_f16 v106, v46, v162, v106
	v_pk_fma_f16 v124, v68, v164, v124
	v_pk_fma_f16 v123, v67, v163, v123
	v_pk_fma_f16 v122, v66, v162, v122
	v_pk_maximum3_f16 v162, v94, v118, v129
	v_pk_maximum3_f16 v163, v95, v119, v128
	v_pk_maximum3_f16 v164, v96, v120, v127
	v_pk_maximum3_f16 v216, v134, v146, v209
	v_pk_maximum3_f16 v220, v85, v109, v125
	v_pk_maximum3_f16 v213, v137, v149, v212
	v_pk_maximum3_f16 v214, v136, v148, v211
	v_pk_maximum3_f16 v215, v135, v147, v210
	s_nop 0
	v_pk_maximum3_f16 v217, v82, v106, v122
	v_pk_maximum3_f16 v218, v83, v107, v123
	v_pk_maximum3_f16 v165, v165, v216, v220
	v_pk_maximum3_f16 v219, v84, v108, v124
	s_nop 0
	v_pk_maximum3_f16 v162, v162, v213, v217
	v_pk_maximum3_f16 v163, v163, v214, v218
	v_pk_maximum3_f16 v164, v164, v215, v219
	v_xor_b32_e32 v165, 0x80008000, v165
	v_xor_b32_e32 v164, 0x80008000, v164
	v_xor_b32_e32 v163, 0x80008000, v163
	v_xor_b32_e32 v162, 0x80008000, v162
	v_pk_add_f16 v97, v97, v165
	v_pk_add_f16 v94, v94, v162
	v_pk_add_f16 v95, v95, v163
	v_pk_add_f16 v96, v96, v164
	v_pk_add_f16 v118, v118, v162
	v_exp_f16_sdwa v213, v94 dst_sel:WORD_0 dst_unused:UNUSED_PAD src0_sel:WORD_0
	v_exp_f16_sdwa v214, v95 dst_sel:WORD_0 dst_unused:UNUSED_PAD src0_sel:WORD_0
	v_exp_f16_sdwa v215, v96 dst_sel:WORD_0 dst_unused:UNUSED_PAD src0_sel:WORD_0
	v_exp_f16_sdwa v216, v97 dst_sel:WORD_0 dst_unused:UNUSED_PAD src0_sel:WORD_0
	v_exp_f16_sdwa v213, v94 dst_sel:WORD_1 dst_unused:UNUSED_PRESERVE src0_sel:WORD_1
	v_exp_f16_sdwa v214, v95 dst_sel:WORD_1 dst_unused:UNUSED_PRESERVE src0_sel:WORD_1
	v_exp_f16_sdwa v215, v96 dst_sel:WORD_1 dst_unused:UNUSED_PRESERVE src0_sel:WORD_1
	v_exp_f16_sdwa v216, v97 dst_sel:WORD_1 dst_unused:UNUSED_PRESERVE src0_sel:WORD_1
	s_nop 0
	v_pk_add_f16 v119, v119, v163
	v_pk_add_f16 v97, v213, 0
	v_pk_fma_f16 v57, v57, v216, 0
	v_pk_add_f16 v94, v216, 0
	v_pk_add_f16 v95, v215, 0
	v_pk_add_f16 v96, v214, 0
	v_pk_fma_f16 v56, v56, v215, 0
	v_pk_fma_f16 v55, v55, v214, 0
	v_pk_fma_f16 v54, v54, v213, 0
	v_pk_add_f16 v120, v120, v164
	v_pk_add_f16 v121, v121, v165
	v_pk_add_f16 v82, v82, v162
	v_exp_f16_sdwa v213, v118 dst_sel:WORD_0 dst_unused:UNUSED_PAD src0_sel:WORD_0
	v_exp_f16_sdwa v214, v119 dst_sel:WORD_0 dst_unused:UNUSED_PAD src0_sel:WORD_0
	v_exp_f16_sdwa v215, v120 dst_sel:WORD_0 dst_unused:UNUSED_PAD src0_sel:WORD_0
	v_exp_f16_sdwa v216, v121 dst_sel:WORD_0 dst_unused:UNUSED_PAD src0_sel:WORD_0
	v_exp_f16_sdwa v213, v118 dst_sel:WORD_1 dst_unused:UNUSED_PRESERVE src0_sel:WORD_1
	v_exp_f16_sdwa v214, v119 dst_sel:WORD_1 dst_unused:UNUSED_PRESERVE src0_sel:WORD_1
	v_exp_f16_sdwa v215, v120 dst_sel:WORD_1 dst_unused:UNUSED_PRESERVE src0_sel:WORD_1
	v_exp_f16_sdwa v216, v121 dst_sel:WORD_1 dst_unused:UNUSED_PRESERVE src0_sel:WORD_1
	s_nop 0
	v_pk_add_f16 v83, v83, v163
	v_pk_add_f16 v97, v97, v213
	v_pk_fma_f16 v57, v77, v216, v57
	v_pk_add_f16 v77, v126, v165
	v_pk_add_f16 v96, v96, v214
	v_pk_add_f16 v95, v95, v215
	v_pk_add_f16 v94, v94, v216
	v_pk_fma_f16 v54, v74, v213, v54
	v_pk_fma_f16 v55, v75, v214, v55
	v_pk_fma_f16 v56, v76, v215, v56
	v_pk_add_f16 v74, v129, v162
	v_pk_add_f16 v75, v128, v163
	v_pk_add_f16 v76, v127, v164
	v_pk_add_f16 v84, v84, v164
	v_exp_f16_sdwa v118, v74 dst_sel:WORD_0 dst_unused:UNUSED_PAD src0_sel:WORD_0
	v_exp_f16_sdwa v119, v75 dst_sel:WORD_0 dst_unused:UNUSED_PAD src0_sel:WORD_0
	v_exp_f16_sdwa v120, v76 dst_sel:WORD_0 dst_unused:UNUSED_PAD src0_sel:WORD_0
	v_exp_f16_sdwa v121, v77 dst_sel:WORD_0 dst_unused:UNUSED_PAD src0_sel:WORD_0
	v_exp_f16_sdwa v118, v74 dst_sel:WORD_1 dst_unused:UNUSED_PRESERVE src0_sel:WORD_1
	v_exp_f16_sdwa v119, v75 dst_sel:WORD_1 dst_unused:UNUSED_PRESERVE src0_sel:WORD_1
	v_exp_f16_sdwa v120, v76 dst_sel:WORD_1 dst_unused:UNUSED_PRESERVE src0_sel:WORD_1
	v_exp_f16_sdwa v121, v77 dst_sel:WORD_1 dst_unused:UNUSED_PRESERVE src0_sel:WORD_1
	s_nop 0
	v_pk_add_f16 v85, v85, v165
	v_pk_add_f16 v77, v97, v118
	v_pk_add_f16 v74, v94, v121
	v_pk_add_f16 v75, v95, v120
	v_pk_add_f16 v76, v96, v119
	v_pk_fma_f16 v57, v101, v121, v57
	v_pk_fma_f16 v56, v100, v120, v56
	v_pk_fma_f16 v55, v99, v119, v55
	v_pk_fma_f16 v54, v98, v118, v54
	v_pk_add_f16 v94, v137, v162
	v_pk_add_f16 v95, v136, v163
	v_pk_add_f16 v96, v135, v164
	v_pk_add_f16 v97, v134, v165
	s_nop 0
	v_exp_f16_sdwa v98, v94 dst_sel:WORD_0 dst_unused:UNUSED_PAD src0_sel:WORD_0
	v_exp_f16_sdwa v99, v95 dst_sel:WORD_0 dst_unused:UNUSED_PAD src0_sel:WORD_0
	v_exp_f16_sdwa v100, v96 dst_sel:WORD_0 dst_unused:UNUSED_PAD src0_sel:WORD_0
	v_exp_f16_sdwa v101, v97 dst_sel:WORD_0 dst_unused:UNUSED_PAD src0_sel:WORD_0
	v_exp_f16_sdwa v98, v94 dst_sel:WORD_1 dst_unused:UNUSED_PRESERVE src0_sel:WORD_1
	v_exp_f16_sdwa v99, v95 dst_sel:WORD_1 dst_unused:UNUSED_PRESERVE src0_sel:WORD_1
	v_exp_f16_sdwa v100, v96 dst_sel:WORD_1 dst_unused:UNUSED_PRESERVE src0_sel:WORD_1
	v_exp_f16_sdwa v101, v97 dst_sel:WORD_1 dst_unused:UNUSED_PRESERVE src0_sel:WORD_1
	s_nop 0
	v_pk_add_f16 v94, v149, v162
	v_pk_add_f16 v77, v77, v98
	v_pk_add_f16 v76, v76, v99
	v_pk_add_f16 v75, v75, v100
	v_pk_add_f16 v74, v74, v101
	v_pk_fma_f16 v54, v30, v98, v54
	v_pk_fma_f16 v55, v31, v99, v55
	v_pk_fma_f16 v56, v32, v100, v56
	v_pk_fma_f16 v57, v33, v101, v57
	v_pk_add_f16 v95, v148, v163
	v_pk_add_f16 v96, v147, v164
	v_pk_add_f16 v97, v146, v165
	s_nop 0
	v_exp_f16_sdwa v98, v94 dst_sel:WORD_0 dst_unused:UNUSED_PAD src0_sel:WORD_0
	v_exp_f16_sdwa v99, v95 dst_sel:WORD_0 dst_unused:UNUSED_PAD src0_sel:WORD_0
	v_exp_f16_sdwa v100, v96 dst_sel:WORD_0 dst_unused:UNUSED_PAD src0_sel:WORD_0
	v_exp_f16_sdwa v101, v97 dst_sel:WORD_0 dst_unused:UNUSED_PAD src0_sel:WORD_0
	v_exp_f16_sdwa v98, v94 dst_sel:WORD_1 dst_unused:UNUSED_PRESERVE src0_sel:WORD_1
	v_exp_f16_sdwa v99, v95 dst_sel:WORD_1 dst_unused:UNUSED_PRESERVE src0_sel:WORD_1
	v_exp_f16_sdwa v100, v96 dst_sel:WORD_1 dst_unused:UNUSED_PRESERVE src0_sel:WORD_1
	v_exp_f16_sdwa v101, v97 dst_sel:WORD_1 dst_unused:UNUSED_PRESERVE src0_sel:WORD_1
	s_nop 0
	v_pk_add_f16 v94, v212, v162
	v_pk_add_f16 v77, v77, v98
	v_pk_add_f16 v74, v74, v101
	v_pk_add_f16 v75, v75, v100
	v_pk_add_f16 v76, v76, v99
	v_pk_fma_f16 v57, v45, v101, v57
	v_pk_fma_f16 v56, v44, v100, v56
	v_pk_fma_f16 v55, v43, v99, v55
	v_pk_fma_f16 v54, v42, v98, v54
	v_pk_add_f16 v95, v211, v163
	v_pk_add_f16 v96, v210, v164
	v_pk_add_f16 v97, v209, v165
	s_nop 0
	v_exp_f16_sdwa v98, v94 dst_sel:WORD_0 dst_unused:UNUSED_PAD src0_sel:WORD_0
	v_exp_f16_sdwa v99, v95 dst_sel:WORD_0 dst_unused:UNUSED_PAD src0_sel:WORD_0
	v_exp_f16_sdwa v100, v96 dst_sel:WORD_0 dst_unused:UNUSED_PAD src0_sel:WORD_0
	v_exp_f16_sdwa v101, v97 dst_sel:WORD_0 dst_unused:UNUSED_PAD src0_sel:WORD_0
	v_exp_f16_sdwa v98, v94 dst_sel:WORD_1 dst_unused:UNUSED_PRESERVE src0_sel:WORD_1
	v_exp_f16_sdwa v99, v95 dst_sel:WORD_1 dst_unused:UNUSED_PRESERVE src0_sel:WORD_1
	v_exp_f16_sdwa v100, v96 dst_sel:WORD_1 dst_unused:UNUSED_PRESERVE src0_sel:WORD_1
	v_exp_f16_sdwa v101, v97 dst_sel:WORD_1 dst_unused:UNUSED_PRESERVE src0_sel:WORD_1
	s_nop 0
	v_exp_f16_sdwa v94, v82 dst_sel:WORD_0 dst_unused:UNUSED_PAD src0_sel:WORD_0
	v_exp_f16_sdwa v95, v83 dst_sel:WORD_0 dst_unused:UNUSED_PAD src0_sel:WORD_0
	v_exp_f16_sdwa v96, v84 dst_sel:WORD_0 dst_unused:UNUSED_PAD src0_sel:WORD_0
	v_exp_f16_sdwa v97, v85 dst_sel:WORD_0 dst_unused:UNUSED_PAD src0_sel:WORD_0
	v_exp_f16_sdwa v94, v82 dst_sel:WORD_1 dst_unused:UNUSED_PRESERVE src0_sel:WORD_1
	v_exp_f16_sdwa v95, v83 dst_sel:WORD_1 dst_unused:UNUSED_PRESERVE src0_sel:WORD_1
	v_exp_f16_sdwa v96, v84 dst_sel:WORD_1 dst_unused:UNUSED_PRESERVE src0_sel:WORD_1
	v_exp_f16_sdwa v97, v85 dst_sel:WORD_1 dst_unused:UNUSED_PRESERVE src0_sel:WORD_1
	s_nop 0
	v_pk_add_f16 v82, v106, v162
	v_pk_add_f16 v77, v77, v98
	v_pk_add_f16 v76, v76, v99
	v_pk_add_f16 v75, v75, v100
	v_pk_add_f16 v74, v74, v101
	v_pk_fma_f16 v54, v58, v98, v54
	v_pk_fma_f16 v55, v59, v99, v55
	v_pk_fma_f16 v56, v60, v100, v56
	v_pk_fma_f16 v57, v61, v101, v57
	v_pk_add_f16 v77, v77, v94
	v_pk_add_f16 v74, v74, v97
	v_pk_add_f16 v75, v75, v96
	v_pk_add_f16 v76, v76, v95
	v_pk_fma_f16 v57, v21, v97, v57
	v_pk_fma_f16 v56, v20, v96, v56
	v_pk_fma_f16 v55, v19, v95, v55
	v_pk_fma_f16 v54, v18, v94, v54
	v_pk_add_f16 v83, v107, v163
	v_pk_add_f16 v84, v108, v164
	v_pk_add_f16 v85, v109, v165
	s_nop 0
	v_exp_f16_sdwa v94, v82 dst_sel:WORD_0 dst_unused:UNUSED_PAD src0_sel:WORD_0
	v_exp_f16_sdwa v95, v83 dst_sel:WORD_0 dst_unused:UNUSED_PAD src0_sel:WORD_0
	v_exp_f16_sdwa v96, v84 dst_sel:WORD_0 dst_unused:UNUSED_PAD src0_sel:WORD_0
	v_exp_f16_sdwa v97, v85 dst_sel:WORD_0 dst_unused:UNUSED_PAD src0_sel:WORD_0
	v_exp_f16_sdwa v94, v82 dst_sel:WORD_1 dst_unused:UNUSED_PRESERVE src0_sel:WORD_1
	v_exp_f16_sdwa v95, v83 dst_sel:WORD_1 dst_unused:UNUSED_PRESERVE src0_sel:WORD_1
	v_exp_f16_sdwa v96, v84 dst_sel:WORD_1 dst_unused:UNUSED_PRESERVE src0_sel:WORD_1
	v_exp_f16_sdwa v97, v85 dst_sel:WORD_1 dst_unused:UNUSED_PRESERVE src0_sel:WORD_1
	s_nop 0
	v_pk_add_f16 v82, v122, v162
	v_pk_add_f16 v77, v77, v94
	v_pk_add_f16 v76, v76, v95
	v_pk_add_f16 v75, v75, v96
	v_pk_add_f16 v74, v74, v97
	v_pk_fma_f16 v54, v22, v94, v54
	v_pk_fma_f16 v55, v23, v95, v55
	v_pk_fma_f16 v56, v24, v96, v56
	v_pk_fma_f16 v57, v25, v97, v57
	v_pk_add_f16 v83, v123, v163
	v_pk_add_f16 v84, v124, v164
	v_pk_add_f16 v85, v125, v165
	s_nop 0
	v_exp_f16_sdwa v94, v82 dst_sel:WORD_0 dst_unused:UNUSED_PAD src0_sel:WORD_0
	v_exp_f16_sdwa v95, v83 dst_sel:WORD_0 dst_unused:UNUSED_PAD src0_sel:WORD_0
	v_exp_f16_sdwa v96, v84 dst_sel:WORD_0 dst_unused:UNUSED_PAD src0_sel:WORD_0
	v_exp_f16_sdwa v97, v85 dst_sel:WORD_0 dst_unused:UNUSED_PAD src0_sel:WORD_0
	v_exp_f16_sdwa v94, v82 dst_sel:WORD_1 dst_unused:UNUSED_PRESERVE src0_sel:WORD_1
	v_exp_f16_sdwa v95, v83 dst_sel:WORD_1 dst_unused:UNUSED_PRESERVE src0_sel:WORD_1
	v_exp_f16_sdwa v96, v84 dst_sel:WORD_1 dst_unused:UNUSED_PRESERVE src0_sel:WORD_1
	v_exp_f16_sdwa v97, v85 dst_sel:WORD_1 dst_unused:UNUSED_PRESERVE src0_sel:WORD_1
	s_nop 0
	s_nop 0
	v_pk_add_f16 v77, v77, v94
	v_pk_add_f16 v76, v76, v95
	v_rcp_f16_e32 v82, v77
	v_rcp_f16_sdwa v77, v77 dst_sel:DWORD dst_unused:UNUSED_PAD src0_sel:WORD_1
	v_pk_add_f16 v75, v75, v96
	v_rcp_f16_e32 v83, v76
	v_rcp_f16_sdwa v76, v76 dst_sel:DWORD dst_unused:UNUSED_PAD src0_sel:WORD_1
	v_pk_add_f16 v74, v74, v97
	v_rcp_f16_e32 v84, v75
	v_rcp_f16_sdwa v75, v75 dst_sel:DWORD dst_unused:UNUSED_PAD src0_sel:WORD_1
	v_rcp_f16_e32 v85, v74
	v_rcp_f16_sdwa v74, v74 dst_sel:DWORD dst_unused:UNUSED_PAD src0_sel:WORD_1
	v_pk_fma_f16 v54, v26, v94, v54
	v_pack_b32_f16 v77, v82, v77
	v_pk_fma_f16 v57, v29, v97, v57
	v_pk_fma_f16 v55, v27, v95, v55
	v_pk_mul_f16 v97, v54, v77
	v_pack_b32_f16 v54, v83, v76
	v_pk_fma_f16 v56, v28, v96, v56
	v_pk_mul_f16 v96, v55, v54
	v_pack_b32_f16 v54, v84, v75
	v_pk_mul_f16 v95, v56, v54
	v_pack_b32_f16 v54, v85, v74
	v_pk_mul_f16 v94, v57, v54
	s_waitcnt vmcnt(7)
	v_pk_mul_f16 v57, v208, v161 op_sel_hi:[0,1]
	v_pk_mul_f16 v77, v206, v161 op_sel_hi:[0,1]
	v_pk_mul_f16 v85, v207, v161 op_sel_hi:[0,1]
	v_pk_mul_f16 v54, v208, v158 op_sel_hi:[0,1]
	v_pk_mul_f16 v55, v208, v159 op_sel_hi:[0,1]
	v_pk_mul_f16 v56, v208, v160 op_sel_hi:[0,1]
	v_pk_mul_f16 v74, v206, v158 op_sel_hi:[0,1]
	v_pk_mul_f16 v75, v206, v159 op_sel_hi:[0,1]
	v_pk_mul_f16 v76, v206, v160 op_sel_hi:[0,1]
	v_pk_mul_f16 v82, v207, v158 op_sel_hi:[0,1]
	v_pk_mul_f16 v83, v207, v159 op_sel_hi:[0,1]
	v_pk_mul_f16 v84, v207, v160 op_sel_hi:[0,1]
	v_pk_fma_f16 v65, v65, v161, v57
	v_pk_fma_f16 v81, v81, v161, v77
	v_pk_fma_f16 v98, v105, v161, v85
	v_pk_fma_f16 v64, v64, v160, v56
	v_pk_maximum3_f16 v125, v65, v81, v98
	v_pk_fma_f16 v63, v63, v159, v55
	v_pk_fma_f16 v62, v62, v158, v54
	v_pk_fma_f16 v80, v80, v160, v76
	v_pk_fma_f16 v79, v79, v159, v75
	v_pk_fma_f16 v78, v78, v158, v74
	v_pk_fma_f16 v99, v104, v160, v84
	v_pk_fma_f16 v100, v103, v159, v83
	v_pk_fma_f16 v101, v102, v158, v82
	v_pk_fma_f16 v102, v37, v161, v57
	v_pk_fma_f16 v106, v49, v161, v77
	v_pk_fma_f16 v118, v69, v161, v85
	v_pk_fma_f16 v57, v89, v161, v57
	v_pk_fma_f16 v77, v117, v161, v77
	v_pk_fma_f16 v85, v133, v161, v85
	v_pk_maximum3_f16 v122, v62, v78, v101
	v_pk_maximum3_f16 v123, v63, v79, v100
	v_pk_maximum3_f16 v124, v64, v80, v99
	v_pk_maximum3_f16 v129, v102, v106, v118
	v_pk_fma_f16 v103, v36, v160, v56
	v_pk_maximum3_f16 v137, v57, v77, v85
	v_pk_fma_f16 v104, v35, v159, v55
	v_pk_maximum3_f16 v125, v125, v129, v137
	v_pk_fma_f16 v105, v34, v158, v54
	v_pk_fma_f16 v107, v48, v160, v76
	v_pk_fma_f16 v108, v47, v159, v75
	v_pk_fma_f16 v109, v46, v158, v74
	v_pk_fma_f16 v119, v68, v160, v84
	v_pk_fma_f16 v120, v67, v159, v83
	v_pk_fma_f16 v121, v66, v158, v82
	v_pk_fma_f16 v56, v88, v160, v56
	v_pk_fma_f16 v55, v87, v159, v55
	v_pk_fma_f16 v54, v86, v158, v54
	v_pk_fma_f16 v76, v116, v160, v76
	v_pk_fma_f16 v75, v115, v159, v75
	v_pk_fma_f16 v74, v114, v158, v74
	v_pk_fma_f16 v84, v132, v160, v84
	v_pk_fma_f16 v83, v131, v159, v83
	v_pk_fma_f16 v82, v130, v158, v82
	v_pk_maximum3_f16 v126, v105, v109, v121
	v_pk_maximum3_f16 v127, v104, v108, v120
	v_pk_maximum3_f16 v128, v103, v107, v119
	v_pk_maximum3_f16 v135, v55, v75, v83
	v_pk_maximum3_f16 v136, v56, v76, v84
	s_nop 0
	v_pk_maximum3_f16 v134, v54, v74, v82
	v_xor_b32_e32 v125, 0x80008000, v125
	v_pk_maximum3_f16 v122, v122, v126, v134
	v_pk_maximum3_f16 v123, v123, v127, v135
	v_pk_maximum3_f16 v124, v124, v128, v136
	v_pk_add_f16 v65, v65, v125
	v_xor_b32_e32 v124, 0x80008000, v124
	v_xor_b32_e32 v123, 0x80008000, v123
	v_xor_b32_e32 v122, 0x80008000, v122
	v_pk_add_f16 v62, v62, v122
	v_pk_add_f16 v63, v63, v123
	v_pk_add_f16 v64, v64, v124
	v_pk_add_f16 v78, v78, v122
	v_exp_f16_sdwa v126, v62 dst_sel:WORD_0 dst_unused:UNUSED_PAD src0_sel:WORD_0
	v_exp_f16_sdwa v127, v63 dst_sel:WORD_0 dst_unused:UNUSED_PAD src0_sel:WORD_0
	v_exp_f16_sdwa v128, v64 dst_sel:WORD_0 dst_unused:UNUSED_PAD src0_sel:WORD_0
	v_exp_f16_sdwa v129, v65 dst_sel:WORD_0 dst_unused:UNUSED_PAD src0_sel:WORD_0
	v_exp_f16_sdwa v126, v62 dst_sel:WORD_1 dst_unused:UNUSED_PRESERVE src0_sel:WORD_1
	v_exp_f16_sdwa v127, v63 dst_sel:WORD_1 dst_unused:UNUSED_PRESERVE src0_sel:WORD_1
	v_exp_f16_sdwa v128, v64 dst_sel:WORD_1 dst_unused:UNUSED_PRESERVE src0_sel:WORD_1
	v_exp_f16_sdwa v129, v65 dst_sel:WORD_1 dst_unused:UNUSED_PRESERVE src0_sel:WORD_1
	s_nop 0
	v_pk_add_f16 v79, v79, v123
	v_pk_add_f16 v65, v126, 0
	v_pk_fma_f16 v33, v33, v129, 0
	v_pk_add_f16 v62, v129, 0
	v_pk_add_f16 v63, v128, 0
	v_pk_add_f16 v64, v127, 0
	v_pk_fma_f16 v32, v32, v128, 0
	v_pk_fma_f16 v31, v31, v127, 0
	v_pk_fma_f16 v30, v30, v126, 0
	v_pk_add_f16 v80, v80, v124
	v_pk_add_f16 v81, v81, v125
	v_pk_add_f16 v54, v54, v122
	v_exp_f16_sdwa v126, v78 dst_sel:WORD_0 dst_unused:UNUSED_PAD src0_sel:WORD_0
	v_exp_f16_sdwa v127, v79 dst_sel:WORD_0 dst_unused:UNUSED_PAD src0_sel:WORD_0
	v_exp_f16_sdwa v128, v80 dst_sel:WORD_0 dst_unused:UNUSED_PAD src0_sel:WORD_0
	v_exp_f16_sdwa v129, v81 dst_sel:WORD_0 dst_unused:UNUSED_PAD src0_sel:WORD_0
	v_exp_f16_sdwa v126, v78 dst_sel:WORD_1 dst_unused:UNUSED_PRESERVE src0_sel:WORD_1
	v_exp_f16_sdwa v127, v79 dst_sel:WORD_1 dst_unused:UNUSED_PRESERVE src0_sel:WORD_1
	v_exp_f16_sdwa v128, v80 dst_sel:WORD_1 dst_unused:UNUSED_PRESERVE src0_sel:WORD_1
	v_exp_f16_sdwa v129, v81 dst_sel:WORD_1 dst_unused:UNUSED_PRESERVE src0_sel:WORD_1
	s_nop 0
	v_pk_add_f16 v55, v55, v123
	v_pk_add_f16 v65, v65, v126
	v_pk_fma_f16 v33, v45, v129, v33
	v_pk_add_f16 v45, v98, v125
	v_pk_add_f16 v64, v64, v127
	v_pk_add_f16 v63, v63, v128
	v_pk_add_f16 v62, v62, v129
	v_pk_fma_f16 v30, v42, v126, v30
	v_pk_fma_f16 v31, v43, v127, v31
	v_pk_fma_f16 v32, v44, v128, v32
	v_pk_add_f16 v42, v101, v122
	v_pk_add_f16 v43, v100, v123
	v_pk_add_f16 v44, v99, v124
	v_pk_add_f16 v56, v56, v124
	v_exp_f16_sdwa v78, v42 dst_sel:WORD_0 dst_unused:UNUSED_PAD src0_sel:WORD_0
	v_exp_f16_sdwa v79, v43 dst_sel:WORD_0 dst_unused:UNUSED_PAD src0_sel:WORD_0
	v_exp_f16_sdwa v80, v44 dst_sel:WORD_0 dst_unused:UNUSED_PAD src0_sel:WORD_0
	v_exp_f16_sdwa v81, v45 dst_sel:WORD_0 dst_unused:UNUSED_PAD src0_sel:WORD_0
	v_exp_f16_sdwa v78, v42 dst_sel:WORD_1 dst_unused:UNUSED_PRESERVE src0_sel:WORD_1
	v_exp_f16_sdwa v79, v43 dst_sel:WORD_1 dst_unused:UNUSED_PRESERVE src0_sel:WORD_1
	v_exp_f16_sdwa v80, v44 dst_sel:WORD_1 dst_unused:UNUSED_PRESERVE src0_sel:WORD_1
	v_exp_f16_sdwa v81, v45 dst_sel:WORD_1 dst_unused:UNUSED_PRESERVE src0_sel:WORD_1
	s_nop 0
	v_pk_add_f16 v57, v57, v125
	v_pk_add_f16 v45, v65, v78
	v_pk_add_f16 v42, v62, v81
	v_pk_add_f16 v43, v63, v80
	v_pk_add_f16 v44, v64, v79
	v_pk_fma_f16 v33, v61, v81, v33
	v_pk_fma_f16 v32, v60, v80, v32
	v_pk_fma_f16 v31, v59, v79, v31
	v_pk_fma_f16 v30, v58, v78, v30
	v_pk_add_f16 v58, v105, v122
	v_pk_add_f16 v59, v104, v123
	v_pk_add_f16 v60, v103, v124
	v_pk_add_f16 v61, v102, v125
	s_nop 0
	v_exp_f16_sdwa v62, v58 dst_sel:WORD_0 dst_unused:UNUSED_PAD src0_sel:WORD_0
	v_exp_f16_sdwa v63, v59 dst_sel:WORD_0 dst_unused:UNUSED_PAD src0_sel:WORD_0
	v_exp_f16_sdwa v64, v60 dst_sel:WORD_0 dst_unused:UNUSED_PAD src0_sel:WORD_0
	v_exp_f16_sdwa v65, v61 dst_sel:WORD_0 dst_unused:UNUSED_PAD src0_sel:WORD_0
	v_exp_f16_sdwa v62, v58 dst_sel:WORD_1 dst_unused:UNUSED_PRESERVE src0_sel:WORD_1
	v_exp_f16_sdwa v63, v59 dst_sel:WORD_1 dst_unused:UNUSED_PRESERVE src0_sel:WORD_1
	v_exp_f16_sdwa v64, v60 dst_sel:WORD_1 dst_unused:UNUSED_PRESERVE src0_sel:WORD_1
	v_exp_f16_sdwa v65, v61 dst_sel:WORD_1 dst_unused:UNUSED_PRESERVE src0_sel:WORD_1
	s_nop 0
	v_pk_add_f16 v58, v109, v122
	v_pk_add_f16 v45, v45, v62
	v_pk_add_f16 v44, v44, v63
	v_pk_add_f16 v43, v43, v64
	v_pk_add_f16 v42, v42, v65
	v_pk_fma_f16 v30, v18, v62, v30
	v_pk_fma_f16 v31, v19, v63, v31
	v_pk_fma_f16 v32, v20, v64, v32
	v_pk_fma_f16 v33, v21, v65, v33
	v_pk_add_f16 v59, v108, v123
	v_pk_add_f16 v60, v107, v124
	v_pk_add_f16 v61, v106, v125
	s_nop 0
	v_exp_f16_sdwa v62, v58 dst_sel:WORD_0 dst_unused:UNUSED_PAD src0_sel:WORD_0
	v_exp_f16_sdwa v63, v59 dst_sel:WORD_0 dst_unused:UNUSED_PAD src0_sel:WORD_0
	v_exp_f16_sdwa v64, v60 dst_sel:WORD_0 dst_unused:UNUSED_PAD src0_sel:WORD_0
	v_exp_f16_sdwa v65, v61 dst_sel:WORD_0 dst_unused:UNUSED_PAD src0_sel:WORD_0
	v_exp_f16_sdwa v62, v58 dst_sel:WORD_1 dst_unused:UNUSED_PRESERVE src0_sel:WORD_1
	v_exp_f16_sdwa v63, v59 dst_sel:WORD_1 dst_unused:UNUSED_PRESERVE src0_sel:WORD_1
	v_exp_f16_sdwa v64, v60 dst_sel:WORD_1 dst_unused:UNUSED_PRESERVE src0_sel:WORD_1
	v_exp_f16_sdwa v65, v61 dst_sel:WORD_1 dst_unused:UNUSED_PRESERVE src0_sel:WORD_1
	s_nop 0
	v_pk_add_f16 v58, v121, v122
	v_pk_add_f16 v45, v45, v62
	v_pk_add_f16 v42, v42, v65
	v_pk_add_f16 v43, v43, v64
	v_pk_add_f16 v44, v44, v63
	v_pk_fma_f16 v33, v25, v65, v33
	v_pk_fma_f16 v32, v24, v64, v32
	v_pk_fma_f16 v31, v23, v63, v31
	v_pk_fma_f16 v30, v22, v62, v30
	v_pk_add_f16 v59, v120, v123
	v_pk_add_f16 v60, v119, v124
	v_pk_add_f16 v61, v118, v125
	s_nop 0
	v_exp_f16_sdwa v62, v58 dst_sel:WORD_0 dst_unused:UNUSED_PAD src0_sel:WORD_0
	v_exp_f16_sdwa v63, v59 dst_sel:WORD_0 dst_unused:UNUSED_PAD src0_sel:WORD_0
	v_exp_f16_sdwa v64, v60 dst_sel:WORD_0 dst_unused:UNUSED_PAD src0_sel:WORD_0
	v_exp_f16_sdwa v65, v61 dst_sel:WORD_0 dst_unused:UNUSED_PAD src0_sel:WORD_0
	v_exp_f16_sdwa v62, v58 dst_sel:WORD_1 dst_unused:UNUSED_PRESERVE src0_sel:WORD_1
	v_exp_f16_sdwa v63, v59 dst_sel:WORD_1 dst_unused:UNUSED_PRESERVE src0_sel:WORD_1
	v_exp_f16_sdwa v64, v60 dst_sel:WORD_1 dst_unused:UNUSED_PRESERVE src0_sel:WORD_1
	v_exp_f16_sdwa v65, v61 dst_sel:WORD_1 dst_unused:UNUSED_PRESERVE src0_sel:WORD_1
	s_nop 0
	v_exp_f16_sdwa v58, v54 dst_sel:WORD_0 dst_unused:UNUSED_PAD src0_sel:WORD_0
	v_exp_f16_sdwa v59, v55 dst_sel:WORD_0 dst_unused:UNUSED_PAD src0_sel:WORD_0
	v_exp_f16_sdwa v60, v56 dst_sel:WORD_0 dst_unused:UNUSED_PAD src0_sel:WORD_0
	v_exp_f16_sdwa v61, v57 dst_sel:WORD_0 dst_unused:UNUSED_PAD src0_sel:WORD_0
	v_exp_f16_sdwa v58, v54 dst_sel:WORD_1 dst_unused:UNUSED_PRESERVE src0_sel:WORD_1
	v_exp_f16_sdwa v59, v55 dst_sel:WORD_1 dst_unused:UNUSED_PRESERVE src0_sel:WORD_1
	v_exp_f16_sdwa v60, v56 dst_sel:WORD_1 dst_unused:UNUSED_PRESERVE src0_sel:WORD_1
	v_exp_f16_sdwa v61, v57 dst_sel:WORD_1 dst_unused:UNUSED_PRESERVE src0_sel:WORD_1
	s_nop 0
	v_pk_add_f16 v54, v74, v122
	v_pk_add_f16 v45, v45, v62
	v_pk_add_f16 v44, v44, v63
	v_pk_add_f16 v43, v43, v64
	v_pk_add_f16 v42, v42, v65
	v_pk_fma_f16 v30, v26, v62, v30
	v_pk_fma_f16 v31, v27, v63, v31
	v_pk_fma_f16 v32, v28, v64, v32
	v_pk_fma_f16 v33, v29, v65, v33
	v_pk_add_f16 v45, v45, v58
	v_pk_add_f16 v42, v42, v61
	v_pk_add_f16 v43, v43, v60
	v_pk_add_f16 v44, v44, v59
	v_pk_fma_f16 v33, v41, v61, v33
	v_pk_fma_f16 v32, v40, v60, v32
	v_pk_fma_f16 v31, v39, v59, v31
	v_pk_fma_f16 v30, v38, v58, v30
	v_pk_add_f16 v55, v75, v123
	v_pk_add_f16 v56, v76, v124
	v_pk_add_f16 v57, v77, v125
	s_nop 0
	v_exp_f16_sdwa v58, v54 dst_sel:WORD_0 dst_unused:UNUSED_PAD src0_sel:WORD_0
	v_exp_f16_sdwa v59, v55 dst_sel:WORD_0 dst_unused:UNUSED_PAD src0_sel:WORD_0
	v_exp_f16_sdwa v60, v56 dst_sel:WORD_0 dst_unused:UNUSED_PAD src0_sel:WORD_0
	v_exp_f16_sdwa v61, v57 dst_sel:WORD_0 dst_unused:UNUSED_PAD src0_sel:WORD_0
	v_exp_f16_sdwa v58, v54 dst_sel:WORD_1 dst_unused:UNUSED_PRESERVE src0_sel:WORD_1
	v_exp_f16_sdwa v59, v55 dst_sel:WORD_1 dst_unused:UNUSED_PRESERVE src0_sel:WORD_1
	v_exp_f16_sdwa v60, v56 dst_sel:WORD_1 dst_unused:UNUSED_PRESERVE src0_sel:WORD_1
	v_exp_f16_sdwa v61, v57 dst_sel:WORD_1 dst_unused:UNUSED_PRESERVE src0_sel:WORD_1
	s_nop 0
	v_pk_add_f16 v54, v82, v122
	v_pk_add_f16 v45, v45, v58
	v_pk_add_f16 v44, v44, v59
	v_pk_add_f16 v43, v43, v60
	v_pk_add_f16 v42, v42, v61
	v_pk_fma_f16 v30, v50, v58, v30
	v_pk_fma_f16 v31, v51, v59, v31
	v_pk_fma_f16 v32, v52, v60, v32
	v_pk_fma_f16 v33, v53, v61, v33
	v_pk_add_f16 v55, v83, v123
	v_pk_add_f16 v56, v84, v124
	v_pk_add_f16 v57, v85, v125
	s_nop 0
	v_exp_f16_sdwa v58, v54 dst_sel:WORD_0 dst_unused:UNUSED_PAD src0_sel:WORD_0
	v_exp_f16_sdwa v59, v55 dst_sel:WORD_0 dst_unused:UNUSED_PAD src0_sel:WORD_0
	v_exp_f16_sdwa v60, v56 dst_sel:WORD_0 dst_unused:UNUSED_PAD src0_sel:WORD_0
	v_exp_f16_sdwa v61, v57 dst_sel:WORD_0 dst_unused:UNUSED_PAD src0_sel:WORD_0
	v_exp_f16_sdwa v58, v54 dst_sel:WORD_1 dst_unused:UNUSED_PRESERVE src0_sel:WORD_1
	v_exp_f16_sdwa v59, v55 dst_sel:WORD_1 dst_unused:UNUSED_PRESERVE src0_sel:WORD_1
	v_exp_f16_sdwa v60, v56 dst_sel:WORD_1 dst_unused:UNUSED_PRESERVE src0_sel:WORD_1
	v_exp_f16_sdwa v61, v57 dst_sel:WORD_1 dst_unused:UNUSED_PRESERVE src0_sel:WORD_1
	s_nop 0
	s_nop 0
	v_pk_add_f16 v45, v45, v58
	v_pk_add_f16 v44, v44, v59
	v_rcp_f16_e32 v54, v45
	v_rcp_f16_sdwa v45, v45 dst_sel:DWORD dst_unused:UNUSED_PAD src0_sel:WORD_1
	v_pk_add_f16 v43, v43, v60
	v_rcp_f16_e32 v55, v44
	v_rcp_f16_sdwa v44, v44 dst_sel:DWORD dst_unused:UNUSED_PAD src0_sel:WORD_1
	v_pk_add_f16 v42, v42, v61
	v_rcp_f16_e32 v56, v43
	v_rcp_f16_sdwa v43, v43 dst_sel:DWORD dst_unused:UNUSED_PAD src0_sel:WORD_1
	v_rcp_f16_e32 v57, v42
	v_rcp_f16_sdwa v42, v42 dst_sel:DWORD dst_unused:UNUSED_PAD src0_sel:WORD_1
	v_pk_fma_f16 v30, v70, v58, v30
	v_pack_b32_f16 v45, v54, v45
	v_pk_fma_f16 v31, v71, v59, v31
	v_pk_mul_f16 v45, v30, v45
	v_pack_b32_f16 v30, v55, v44
	v_pk_fma_f16 v32, v72, v60, v32
	v_pk_mul_f16 v44, v31, v30
	v_pack_b32_f16 v30, v56, v43
	v_pk_fma_f16 v33, v73, v61, v33
	v_pk_mul_f16 v43, v32, v30
	v_pack_b32_f16 v30, v57, v42
	v_pk_mul_f16 v42, v33, v30
	s_waitcnt vmcnt(0)
	v_pk_mul_f16 v30, v208, v154 op_sel_hi:[0,1]
	v_pk_mul_f16 v31, v208, v155 op_sel_hi:[0,1]
	v_pk_mul_f16 v32, v208, v156 op_sel_hi:[0,1]
	v_pk_mul_f16 v33, v208, v157 op_sel_hi:[0,1]
	v_pk_mul_f16 v54, v206, v154 op_sel_hi:[0,1]
	v_pk_mul_f16 v55, v206, v155 op_sel_hi:[0,1]
	v_pk_mul_f16 v56, v206, v156 op_sel_hi:[0,1]
	v_pk_mul_f16 v57, v206, v157 op_sel_hi:[0,1]
	v_pk_mul_f16 v58, v207, v154 op_sel_hi:[0,1]
	v_pk_mul_f16 v59, v207, v155 op_sel_hi:[0,1]
	v_pk_mul_f16 v60, v207, v156 op_sel_hi:[0,1]
	v_pk_mul_f16 v61, v207, v157 op_sel_hi:[0,1]
	v_pk_fma_f16 v37, v37, v157, v33
	v_pk_fma_f16 v36, v36, v156, v32
	v_pk_fma_f16 v35, v35, v155, v31
	v_pk_fma_f16 v34, v34, v154, v30
	v_pk_fma_f16 v49, v49, v157, v57
	v_pk_fma_f16 v48, v48, v156, v56
	v_pk_fma_f16 v47, v47, v155, v55
	v_pk_fma_f16 v46, v46, v154, v54
	v_pk_fma_f16 v62, v69, v157, v61
	v_pk_fma_f16 v63, v68, v156, v60
	v_pk_fma_f16 v64, v67, v155, v59
	v_pk_fma_f16 v65, v66, v154, v58
	v_pk_fma_f16 v66, v89, v157, v33
	v_pk_fma_f16 v67, v88, v156, v32
	v_pk_fma_f16 v68, v87, v155, v31
	v_pk_fma_f16 v69, v86, v154, v30
	v_pk_fma_f16 v74, v117, v157, v57
	v_pk_fma_f16 v75, v116, v156, v56
	v_pk_fma_f16 v76, v115, v155, v55
	v_pk_fma_f16 v77, v114, v154, v54
	v_pk_fma_f16 v78, v133, v157, v61
	v_pk_fma_f16 v79, v132, v156, v60
	v_pk_fma_f16 v80, v131, v155, v59
	v_pk_fma_f16 v81, v130, v154, v58
	v_pk_fma_f16 v61, v17, v157, v61
	v_pk_fma_f16 v60, v16, v156, v60
	v_pk_fma_f16 v59, v15, v155, v59
	v_pk_fma_f16 v58, v14, v154, v58
	v_pk_maximum3_f16 v14, v34, v46, v65
	v_pk_maximum3_f16 v15, v35, v47, v64
	v_pk_maximum3_f16 v16, v36, v48, v63
	v_pk_maximum3_f16 v17, v37, v49, v62
	v_pk_maximum3_f16 v82, v69, v77, v81
	v_pk_maximum3_f16 v83, v68, v76, v80
	v_pk_maximum3_f16 v84, v67, v75, v79
	v_pk_maximum3_f16 v85, v66, v74, v78
	v_pk_fma_f16 v33, v145, v157, v33
	v_pk_fma_f16 v32, v144, v156, v32
	v_pk_fma_f16 v31, v143, v155, v31
	v_pk_fma_f16 v30, v142, v154, v30
	v_pk_fma_f16 v57, v153, v157, v57
	v_pk_fma_f16 v56, v152, v156, v56
	v_pk_fma_f16 v55, v151, v155, v55
	v_pk_fma_f16 v54, v150, v154, v54
	v_pk_maximum3_f16 v87, v31, v55, v59
	v_pk_maximum3_f16 v88, v32, v56, v60
	v_pk_maximum3_f16 v89, v33, v57, v61
	s_nop 0
	v_pk_maximum3_f16 v86, v30, v54, v58
	v_pk_maximum3_f16 v15, v15, v83, v87
	v_pk_maximum3_f16 v16, v16, v84, v88
	v_pk_maximum3_f16 v17, v17, v85, v89
	s_nop 0
	v_pk_maximum3_f16 v14, v14, v82, v86
	v_xor_b32_e32 v82, 0x80008000, v17
	v_xor_b32_e32 v83, 0x80008000, v16
	v_xor_b32_e32 v84, 0x80008000, v15
	v_xor_b32_e32 v85, 0x80008000, v14
	v_pk_add_f16 v14, v34, v85
	v_pk_add_f16 v15, v35, v84
	v_pk_add_f16 v16, v36, v83
	v_pk_add_f16 v17, v37, v82
	s_nop 0
	v_exp_f16_sdwa v34, v14 dst_sel:WORD_0 dst_unused:UNUSED_PAD src0_sel:WORD_0
	v_exp_f16_sdwa v35, v15 dst_sel:WORD_0 dst_unused:UNUSED_PAD src0_sel:WORD_0
	v_exp_f16_sdwa v36, v16 dst_sel:WORD_0 dst_unused:UNUSED_PAD src0_sel:WORD_0
	v_exp_f16_sdwa v37, v17 dst_sel:WORD_0 dst_unused:UNUSED_PAD src0_sel:WORD_0
	v_exp_f16_sdwa v34, v14 dst_sel:WORD_1 dst_unused:UNUSED_PRESERVE src0_sel:WORD_1
	v_exp_f16_sdwa v35, v15 dst_sel:WORD_1 dst_unused:UNUSED_PRESERVE src0_sel:WORD_1
	v_exp_f16_sdwa v36, v16 dst_sel:WORD_1 dst_unused:UNUSED_PRESERVE src0_sel:WORD_1
	v_exp_f16_sdwa v37, v17 dst_sel:WORD_1 dst_unused:UNUSED_PRESERVE src0_sel:WORD_1
	s_nop 0
	s_nop 0
	v_pk_add_f16 v14, v34, 0
	v_pk_add_f16 v15, v35, 0
	v_pk_add_f16 v16, v36, 0
	v_pk_add_f16 v17, v37, 0
	v_pk_fma_f16 v18, v18, v34, 0
	v_pk_fma_f16 v19, v19, v35, 0
	v_pk_fma_f16 v20, v20, v36, 0
	v_pk_fma_f16 v21, v21, v37, 0
	v_pk_add_f16 v34, v46, v85
	v_pk_add_f16 v35, v47, v84
	v_pk_add_f16 v36, v48, v83
	v_pk_add_f16 v37, v49, v82
	s_nop 0
	v_exp_f16_sdwa v46, v34 dst_sel:WORD_0 dst_unused:UNUSED_PAD src0_sel:WORD_0
	v_exp_f16_sdwa v47, v35 dst_sel:WORD_0 dst_unused:UNUSED_PAD src0_sel:WORD_0
	v_exp_f16_sdwa v48, v36 dst_sel:WORD_0 dst_unused:UNUSED_PAD src0_sel:WORD_0
	v_exp_f16_sdwa v49, v37 dst_sel:WORD_0 dst_unused:UNUSED_PAD src0_sel:WORD_0
	v_exp_f16_sdwa v46, v34 dst_sel:WORD_1 dst_unused:UNUSED_PRESERVE src0_sel:WORD_1
	v_exp_f16_sdwa v47, v35 dst_sel:WORD_1 dst_unused:UNUSED_PRESERVE src0_sel:WORD_1
	v_exp_f16_sdwa v48, v36 dst_sel:WORD_1 dst_unused:UNUSED_PRESERVE src0_sel:WORD_1
	v_exp_f16_sdwa v49, v37 dst_sel:WORD_1 dst_unused:UNUSED_PRESERVE src0_sel:WORD_1
	s_nop 0
	s_nop 0
	v_pk_add_f16 v17, v17, v49
	v_pk_add_f16 v16, v16, v48
	v_pk_add_f16 v15, v15, v47
	v_pk_add_f16 v14, v14, v46
	v_pk_fma_f16 v21, v25, v49, v21
	v_pk_fma_f16 v20, v24, v48, v20
	v_pk_fma_f16 v19, v23, v47, v19
	v_pk_fma_f16 v18, v22, v46, v18
	v_pk_add_f16 v22, v65, v85
	v_pk_add_f16 v23, v64, v84
	v_pk_add_f16 v24, v63, v83
	v_pk_add_f16 v25, v62, v82
	s_nop 0
	v_exp_f16_sdwa v34, v22 dst_sel:WORD_0 dst_unused:UNUSED_PAD src0_sel:WORD_0
	v_exp_f16_sdwa v35, v23 dst_sel:WORD_0 dst_unused:UNUSED_PAD src0_sel:WORD_0
	v_exp_f16_sdwa v36, v24 dst_sel:WORD_0 dst_unused:UNUSED_PAD src0_sel:WORD_0
	v_exp_f16_sdwa v37, v25 dst_sel:WORD_0 dst_unused:UNUSED_PAD src0_sel:WORD_0
	v_exp_f16_sdwa v34, v22 dst_sel:WORD_1 dst_unused:UNUSED_PRESERVE src0_sel:WORD_1
	v_exp_f16_sdwa v35, v23 dst_sel:WORD_1 dst_unused:UNUSED_PRESERVE src0_sel:WORD_1
	v_exp_f16_sdwa v36, v24 dst_sel:WORD_1 dst_unused:UNUSED_PRESERVE src0_sel:WORD_1
	v_exp_f16_sdwa v37, v25 dst_sel:WORD_1 dst_unused:UNUSED_PRESERVE src0_sel:WORD_1
	s_nop 0
	v_pk_add_f16 v22, v69, v85
	v_pk_add_f16 v14, v14, v34
	v_pk_add_f16 v15, v15, v35
	v_pk_add_f16 v16, v16, v36
	v_pk_add_f16 v17, v17, v37
	v_pk_fma_f16 v18, v26, v34, v18
	v_pk_fma_f16 v19, v27, v35, v19
	v_pk_fma_f16 v20, v28, v36, v20
	v_pk_fma_f16 v21, v29, v37, v21
	v_pk_add_f16 v23, v68, v84
	v_pk_add_f16 v24, v67, v83
	v_pk_add_f16 v25, v66, v82
	s_nop 0
	v_exp_f16_sdwa v26, v22 dst_sel:WORD_0 dst_unused:UNUSED_PAD src0_sel:WORD_0
	v_exp_f16_sdwa v27, v23 dst_sel:WORD_0 dst_unused:UNUSED_PAD src0_sel:WORD_0
	v_exp_f16_sdwa v28, v24 dst_sel:WORD_0 dst_unused:UNUSED_PAD src0_sel:WORD_0
	v_exp_f16_sdwa v29, v25 dst_sel:WORD_0 dst_unused:UNUSED_PAD src0_sel:WORD_0
	v_exp_f16_sdwa v26, v22 dst_sel:WORD_1 dst_unused:UNUSED_PRESERVE src0_sel:WORD_1
	v_exp_f16_sdwa v27, v23 dst_sel:WORD_1 dst_unused:UNUSED_PRESERVE src0_sel:WORD_1
	v_exp_f16_sdwa v28, v24 dst_sel:WORD_1 dst_unused:UNUSED_PRESERVE src0_sel:WORD_1
	v_exp_f16_sdwa v29, v25 dst_sel:WORD_1 dst_unused:UNUSED_PRESERVE src0_sel:WORD_1
	s_nop 0
	v_pk_add_f16 v22, v77, v85
	v_pk_add_f16 v17, v17, v29
	v_pk_add_f16 v16, v16, v28
	v_pk_add_f16 v15, v15, v27
	v_pk_add_f16 v14, v14, v26
	v_pk_fma_f16 v21, v41, v29, v21
	v_pk_fma_f16 v20, v40, v28, v20
	v_pk_fma_f16 v19, v39, v27, v19
	v_pk_fma_f16 v18, v38, v26, v18
	v_pk_add_f16 v23, v76, v84
	v_pk_add_f16 v24, v75, v83
	v_pk_add_f16 v25, v74, v82
	s_nop 0
	v_exp_f16_sdwa v26, v22 dst_sel:WORD_0 dst_unused:UNUSED_PAD src0_sel:WORD_0
	v_exp_f16_sdwa v27, v23 dst_sel:WORD_0 dst_unused:UNUSED_PAD src0_sel:WORD_0
	v_exp_f16_sdwa v28, v24 dst_sel:WORD_0 dst_unused:UNUSED_PAD src0_sel:WORD_0
	v_exp_f16_sdwa v29, v25 dst_sel:WORD_0 dst_unused:UNUSED_PAD src0_sel:WORD_0
	v_exp_f16_sdwa v26, v22 dst_sel:WORD_1 dst_unused:UNUSED_PRESERVE src0_sel:WORD_1
	v_exp_f16_sdwa v27, v23 dst_sel:WORD_1 dst_unused:UNUSED_PRESERVE src0_sel:WORD_1
	v_exp_f16_sdwa v28, v24 dst_sel:WORD_1 dst_unused:UNUSED_PRESERVE src0_sel:WORD_1
	v_exp_f16_sdwa v29, v25 dst_sel:WORD_1 dst_unused:UNUSED_PRESERVE src0_sel:WORD_1
	s_nop 0
	v_pk_add_f16 v22, v81, v85
	v_pk_add_f16 v14, v14, v26
	v_pk_add_f16 v15, v15, v27
	v_pk_add_f16 v16, v16, v28
	v_pk_add_f16 v17, v17, v29
	v_pk_fma_f16 v18, v50, v26, v18
	v_pk_fma_f16 v19, v51, v27, v19
	v_pk_fma_f16 v20, v52, v28, v20
	v_pk_fma_f16 v21, v53, v29, v21
	v_pk_add_f16 v23, v80, v84
	v_pk_add_f16 v24, v79, v83
	v_pk_add_f16 v25, v78, v82
	s_nop 0
	v_exp_f16_sdwa v26, v22 dst_sel:WORD_0 dst_unused:UNUSED_PAD src0_sel:WORD_0
	v_exp_f16_sdwa v27, v23 dst_sel:WORD_0 dst_unused:UNUSED_PAD src0_sel:WORD_0
	v_exp_f16_sdwa v28, v24 dst_sel:WORD_0 dst_unused:UNUSED_PAD src0_sel:WORD_0
	v_exp_f16_sdwa v29, v25 dst_sel:WORD_0 dst_unused:UNUSED_PAD src0_sel:WORD_0
	v_exp_f16_sdwa v26, v22 dst_sel:WORD_1 dst_unused:UNUSED_PRESERVE src0_sel:WORD_1
	v_exp_f16_sdwa v27, v23 dst_sel:WORD_1 dst_unused:UNUSED_PRESERVE src0_sel:WORD_1
	v_exp_f16_sdwa v28, v24 dst_sel:WORD_1 dst_unused:UNUSED_PRESERVE src0_sel:WORD_1
	v_exp_f16_sdwa v29, v25 dst_sel:WORD_1 dst_unused:UNUSED_PRESERVE src0_sel:WORD_1
	s_nop 0
	v_pk_add_f16 v22, v30, v85
	v_pk_add_f16 v17, v17, v29
	v_pk_add_f16 v16, v16, v28
	v_pk_add_f16 v15, v15, v27
	v_pk_add_f16 v14, v14, v26
	v_pk_fma_f16 v21, v73, v29, v21
	v_pk_fma_f16 v20, v72, v28, v20
	v_pk_fma_f16 v19, v71, v27, v19
	v_pk_fma_f16 v18, v70, v26, v18
	v_pk_add_f16 v23, v31, v84
	v_pk_add_f16 v24, v32, v83
	v_pk_add_f16 v25, v33, v82
	s_nop 0
	v_exp_f16_sdwa v26, v22 dst_sel:WORD_0 dst_unused:UNUSED_PAD src0_sel:WORD_0
	v_exp_f16_sdwa v27, v23 dst_sel:WORD_0 dst_unused:UNUSED_PAD src0_sel:WORD_0
	v_exp_f16_sdwa v28, v24 dst_sel:WORD_0 dst_unused:UNUSED_PAD src0_sel:WORD_0
	v_exp_f16_sdwa v29, v25 dst_sel:WORD_0 dst_unused:UNUSED_PAD src0_sel:WORD_0
	v_exp_f16_sdwa v26, v22 dst_sel:WORD_1 dst_unused:UNUSED_PRESERVE src0_sel:WORD_1
	v_exp_f16_sdwa v27, v23 dst_sel:WORD_1 dst_unused:UNUSED_PRESERVE src0_sel:WORD_1
	v_exp_f16_sdwa v28, v24 dst_sel:WORD_1 dst_unused:UNUSED_PRESERVE src0_sel:WORD_1
	v_exp_f16_sdwa v29, v25 dst_sel:WORD_1 dst_unused:UNUSED_PRESERVE src0_sel:WORD_1
	s_nop 0
	v_pk_add_f16 v22, v54, v85
	v_pk_add_f16 v14, v14, v26
	v_pk_add_f16 v15, v15, v27
	v_pk_add_f16 v16, v16, v28
	v_pk_add_f16 v17, v17, v29
	v_pk_fma_f16 v18, v90, v26, v18
	v_pk_fma_f16 v19, v91, v27, v19
	v_pk_fma_f16 v20, v92, v28, v20
	v_pk_fma_f16 v21, v93, v29, v21
	v_pk_add_f16 v23, v55, v84
	v_pk_add_f16 v24, v56, v83
	v_pk_add_f16 v25, v57, v82
	s_nop 0
	v_exp_f16_sdwa v26, v22 dst_sel:WORD_0 dst_unused:UNUSED_PAD src0_sel:WORD_0
	v_exp_f16_sdwa v27, v23 dst_sel:WORD_0 dst_unused:UNUSED_PAD src0_sel:WORD_0
	v_exp_f16_sdwa v28, v24 dst_sel:WORD_0 dst_unused:UNUSED_PAD src0_sel:WORD_0
	v_exp_f16_sdwa v29, v25 dst_sel:WORD_0 dst_unused:UNUSED_PAD src0_sel:WORD_0
	v_exp_f16_sdwa v26, v22 dst_sel:WORD_1 dst_unused:UNUSED_PRESERVE src0_sel:WORD_1
	v_exp_f16_sdwa v27, v23 dst_sel:WORD_1 dst_unused:UNUSED_PRESERVE src0_sel:WORD_1
	v_exp_f16_sdwa v28, v24 dst_sel:WORD_1 dst_unused:UNUSED_PRESERVE src0_sel:WORD_1
	v_exp_f16_sdwa v29, v25 dst_sel:WORD_1 dst_unused:UNUSED_PRESERVE src0_sel:WORD_1
	s_nop 0
	s_nop 0
	v_pk_add_f16 v17, v17, v29
	v_pk_add_f16 v16, v16, v28
	v_pk_add_f16 v15, v15, v27
	v_pk_add_f16 v14, v14, v26
	v_pk_fma_f16 v21, v113, v29, v21
	v_pk_fma_f16 v20, v112, v28, v20
	v_pk_fma_f16 v19, v111, v27, v19
	v_pk_fma_f16 v18, v110, v26, v18
	v_pk_add_f16 v26, v58, v85
	v_pk_add_f16 v27, v59, v84
	v_pk_add_f16 v28, v60, v83
	v_pk_add_f16 v29, v61, v82
	s_nop 0
	v_exp_f16_sdwa v22, v26 dst_sel:WORD_0 dst_unused:UNUSED_PAD src0_sel:WORD_0
	v_exp_f16_sdwa v23, v27 dst_sel:WORD_0 dst_unused:UNUSED_PAD src0_sel:WORD_0
	v_exp_f16_sdwa v24, v28 dst_sel:WORD_0 dst_unused:UNUSED_PAD src0_sel:WORD_0
	v_exp_f16_sdwa v25, v29 dst_sel:WORD_0 dst_unused:UNUSED_PAD src0_sel:WORD_0
	v_exp_f16_sdwa v22, v26 dst_sel:WORD_1 dst_unused:UNUSED_PRESERVE src0_sel:WORD_1
	v_exp_f16_sdwa v23, v27 dst_sel:WORD_1 dst_unused:UNUSED_PRESERVE src0_sel:WORD_1
	v_exp_f16_sdwa v24, v28 dst_sel:WORD_1 dst_unused:UNUSED_PRESERVE src0_sel:WORD_1
	v_exp_f16_sdwa v25, v29 dst_sel:WORD_1 dst_unused:UNUSED_PRESERVE src0_sel:WORD_1
	s_nop 0
.LBB4_118:
	s_and_b64 vcc, exec, s[4:5]
	s_cbranch_vccz .LBB4_3
	global_load_dwordx3 v[146:148], v169, s[16:17]
	s_mov_b32 s14, s38
	s_mov_b32 s15, s39
	v_cmp_lt_u32_e64 s[64:65], 0, v199
	v_cmp_gt_u32_e64 s[66:67], 63, v199
	v_cmp_lt_u32_e64 s[68:69], 0, v180
	v_cmp_gt_u32_e64 s[70:71], 60, v180
	buffer_load_dwordx4 v[162:165], v200, s[12:15], 0 offen
	v_add_u32_e32 v246, 0x18000, v200
	buffer_load_dwordx4 v[154:157], v246, s[12:15], 0 offen
	v_add_u32_e32 v245, 0x30000, v200
	buffer_load_dwordx4 v[150:153], v245, s[12:15], 0 offen
	s_and_b64 s[72:73], s[68:69], s[64:65]
	s_and_b64 s[74:75], s[68:69], s[66:67]
	s_and_b64 s[76:77], s[70:71], s[64:65]
	s_and_b64 s[78:79], s[70:71], s[66:67]
	v_add_u32_e32 v245, 0xfffe7c00, v200
	v_add_u32_e32 v246, 0xfffe8000, v200
	v_mov_b32_e32 v114, v6
	v_mov_b32_e32 v115, v7
	v_mov_b32_e32 v116, v8
	v_mov_b32_e32 v117, v9
	v_mov_b32_e32 v70, v2
	v_mov_b32_e32 v71, v3
	v_mov_b32_e32 v72, v4
	v_mov_b32_e32 v73, v5
	v_mov_b32_e32 v130, v6
	v_mov_b32_e32 v131, v7
	v_mov_b32_e32 v132, v8
	v_mov_b32_e32 v133, v9
	v_mov_b32_e32 v94, v2
	v_mov_b32_e32 v95, v3
	v_mov_b32_e32 v96, v4
	v_mov_b32_e32 v97, v5
	v_mov_b32_e32 v138, v6
	v_mov_b32_e32 v139, v7
	v_mov_b32_e32 v140, v8
	v_mov_b32_e32 v141, v9
	v_mov_b32_e32 v118, v2
	v_mov_b32_e32 v119, v3
	v_mov_b32_e32 v120, v4
	v_mov_b32_e32 v121, v5
	s_mov_b64 exec, s[72:73]
	buffer_load_dwordx4 v[114:117], v245, s[12:15], 0 offen
	buffer_load_dwordx4 v[70:73], v245, s[12:15], 0 offen offset:512
	s_mov_b64 exec, -1
	s_mov_b64 exec, s[68:69]
	buffer_load_dwordx4 v[130:133], v246, s[12:15], 0 offen offset:512
	buffer_load_dwordx4 v[94:97], v246, s[12:15], 0 offen offset:1024
	s_mov_b64 exec, -1
	s_mov_b64 exec, s[74:75]
	buffer_load_dwordx4 v[138:141], v246, s[12:15], 0 offen offset:2048
	buffer_load_dwordx4 v[118:121], v246, s[12:15], 0 offen offset:2560
	s_mov_b64 exec, -1
	v_add_u32_e32 v245, 0xfffffc00, v200
	v_mov_b32_e32 v86, v6
	v_mov_b32_e32 v87, v7
	v_mov_b32_e32 v88, v8
	v_mov_b32_e32 v89, v9
	v_mov_b32_e32 v42, v2
	v_mov_b32_e32 v43, v3
	v_mov_b32_e32 v44, v4
	v_mov_b32_e32 v45, v5
	v_mov_b32_e32 v126, v6
	v_mov_b32_e32 v127, v7
	v_mov_b32_e32 v128, v8
	v_mov_b32_e32 v129, v9
	v_mov_b32_e32 v90, v2
	v_mov_b32_e32 v91, v3
	v_mov_b32_e32 v92, v4
	v_mov_b32_e32 v93, v5
	s_mov_b64 exec, s[64:65]
	buffer_load_dwordx4 v[86:89], v245, s[12:15], 0 offen
	buffer_load_dwordx4 v[42:45], v245, s[12:15], 0 offen offset:512
	s_mov_b64 exec, -1
	buffer_load_dwordx4 v[110:113], v200, s[12:15], 0 offen offset:512
	buffer_load_dwordx4 v[66:69], v200, s[12:15], 0 offen offset:1024
	s_mov_b64 exec, s[66:67]
	buffer_load_dwordx4 v[126:129], v200, s[12:15], 0 offen offset:2048
	buffer_load_dwordx4 v[90:93], v200, s[12:15], 0 offen offset:2560
	s_mov_b64 exec, -1
	v_add_u32_e32 v245, 0x17c00, v200
	v_add_u32_e32 v246, 0x18000, v200
	v_mov_b32_e32 v54, v6
	v_mov_b32_e32 v55, v7
	v_mov_b32_e32 v56, v8
	v_mov_b32_e32 v57, v9
	v_mov_b32_e32 v22, v2
	v_mov_b32_e32 v23, v3
	v_mov_b32_e32 v24, v4
	v_mov_b32_e32 v25, v5
	v_mov_b32_e32 v98, v6
	v_mov_b32_e32 v99, v7
	v_mov_b32_e32 v100, v8
	v_mov_b32_e32 v101, v9
	v_mov_b32_e32 v50, v2
	v_mov_b32_e32 v51, v3
	v_mov_b32_e32 v52, v4
	v_mov_b32_e32 v53, v5
	s_mov_b64 exec, s[64:65]
	buffer_load_dwordx4 v[54:57], v245, s[12:15], 0 offen
	buffer_load_dwordx4 v[22:25], v245, s[12:15], 0 offen offset:512
	s_mov_b64 exec, -1
	buffer_load_dwordx4 v[74:77], v246, s[12:15], 0 offen offset:512
	buffer_load_dwordx4 v[34:37], v246, s[12:15], 0 offen offset:1024
	s_mov_b64 exec, s[66:67]
	buffer_load_dwordx4 v[98:101], v246, s[12:15], 0 offen offset:2048
	buffer_load_dwordx4 v[50:53], v246, s[12:15], 0 offen offset:2560
	s_mov_b64 exec, -1
	v_add_u32_e32 v245, 0x2fc00, v200
	v_add_u32_e32 v246, 0x30000, v200
	v_mov_b32_e32 v26, v6
	v_mov_b32_e32 v27, v7
	v_mov_b32_e32 v28, v8
	v_mov_b32_e32 v29, v9
	v_mov_b32_e32 v10, v2
	v_mov_b32_e32 v11, v3
	v_mov_b32_e32 v12, v4
	v_mov_b32_e32 v13, v5
	v_mov_b32_e32 v58, v6
	v_mov_b32_e32 v59, v7
	v_mov_b32_e32 v60, v8
	v_mov_b32_e32 v61, v9
	v_mov_b32_e32 v18, v2
	v_mov_b32_e32 v19, v3
	v_mov_b32_e32 v20, v4
	v_mov_b32_e32 v21, v5
	s_mov_b64 exec, s[64:65]
	buffer_load_dwordx4 v[26:29], v245, s[12:15], 0 offen
	buffer_load_dwordx4 v[10:13], v245, s[12:15], 0 offen offset:512
	s_mov_b64 exec, -1
	buffer_load_dwordx4 v[38:41], v246, s[12:15], 0 offen offset:512
	buffer_load_dwordx4 v[14:17], v246, s[12:15], 0 offen offset:1024
	s_mov_b64 exec, s[66:67]
	buffer_load_dwordx4 v[58:61], v246, s[12:15], 0 offen offset:2048
	buffer_load_dwordx4 v[18:21], v246, s[12:15], 0 offen offset:2560
	s_mov_b64 exec, -1
	v_add_u32_e32 v245, 0x47c00, v200
	v_add_u32_e32 v246, 0x48000, v200
	v_mov_b32_e32 v78, v6
	v_mov_b32_e32 v79, v7
	v_mov_b32_e32 v80, v8
	v_mov_b32_e32 v81, v9
	v_mov_b32_e32 v30, v2
	v_mov_b32_e32 v31, v3
	v_mov_b32_e32 v32, v4
	v_mov_b32_e32 v33, v5
	v_mov_b32_e32 v122, v6
	v_mov_b32_e32 v123, v7
	v_mov_b32_e32 v124, v8
	v_mov_b32_e32 v125, v9
	v_mov_b32_e32 v62, v2
	v_mov_b32_e32 v63, v3
	v_mov_b32_e32 v64, v4
	v_mov_b32_e32 v65, v5
	s_mov_b64 exec, s[64:65]
	buffer_load_dwordx4 v[78:81], v245, s[12:15], 0 offen
	buffer_load_dwordx4 v[30:33], v245, s[12:15], 0 offen offset:512
	s_mov_b64 exec, -1
	buffer_load_dwordx4 v[106:109], v246, s[12:15], 0 offen offset:512
	buffer_load_dwordx4 v[46:49], v246, s[12:15], 0 offen offset:1024
	s_mov_b64 exec, s[66:67]
	buffer_load_dwordx4 v[122:125], v246, s[12:15], 0 offen offset:2048
	buffer_load_dwordx4 v[62:65], v246, s[12:15], 0 offen offset:2560
	s_mov_b64 exec, -1
	v_add_u32_e32 v245, 0x5fc00, v200
	v_add_u32_e32 v246, 0x60000, v200
	v_mov_b32_e32 v134, v6
	v_mov_b32_e32 v135, v7
	v_mov_b32_e32 v136, v8
	v_mov_b32_e32 v137, v9
	v_mov_b32_e32 v82, v2
	v_mov_b32_e32 v83, v3
	v_mov_b32_e32 v84, v4
	v_mov_b32_e32 v85, v5
	v_mov_b32_e32 v142, v6
	v_mov_b32_e32 v143, v7
	v_mov_b32_e32 v144, v8
	v_mov_b32_e32 v145, v9
	v_mov_b32_e32 v102, v2
	v_mov_b32_e32 v103, v3
	v_mov_b32_e32 v104, v4
	v_mov_b32_e32 v105, v5
	s_mov_b64 exec, s[76:77]
	buffer_load_dwordx4 v[134:137], v245, s[12:15], 0 offen
	buffer_load_dwordx4 v[82:85], v245, s[12:15], 0 offen offset:512
	s_mov_b64 exec, -1
	s_mov_b64 exec, s[70:71]
	buffer_load_dwordx4 v[142:145], v246, s[12:15], 0 offen offset:512
	buffer_load_dwordx4 v[102:105], v246, s[12:15], 0 offen offset:1024
	s_mov_b64 exec, -1
	s_mov_b64 exec, s[78:79]
	buffer_load_dwordx4 v[6:9], v246, s[12:15], 0 offen offset:2048
	buffer_load_dwordx4 v[2:5], v246, s[12:15], 0 offen offset:2560
	s_mov_b64 exec, -1
	s_waitcnt vmcnt(39)
	v_cvt_f16_f32_e32 v158, v147
	v_cvt_f16_f32_e32 v160, v146
	v_cvt_f16_f32_e32 v159, v148
	v_add_u32_e32 v245, 0x48000, v200
	buffer_load_dwordx4 v[146:149], v245, s[12:15], 0 offen
	s_branch .LBB4_2
.LBB4_155:
	s_load_dword s0, s[0:1], 0x88
	s_lshl_b32 s1, s45, 6
	s_and_b32 s1, s1, 0xfffffe00
	s_or_b32 s2, s1, s44
	v_readfirstlane_b32 s4, v0
	s_waitcnt lgkmcnt(0)
	s_mul_i32 s3, s0, 0x60000
	s_mul_hi_i32 s1, s0, 0x60000
	s_add_u32 s3, s28, s3
	s_mulk_i32 s0, 0x300
	s_addc_u32 s5, s29, s1
	s_ashr_i32 s1, s0, 31
	s_lshl_b64 s[0:1], s[0:1], 2
	s_add_u32 s0, s30, s0
	s_addc_u32 s1, s31, s1
	s_lshr_b32 s6, s4, 6
	s_and_b32 s25, s25, 0xffff
	s_mul_i32 s4, s6, 0x6000
	v_and_b32_e32 v2, 63, v0
	s_mul_hi_u32 s7, s6, 0x6000
	s_add_u32 s4, s3, s4
	s_addc_u32 s5, s5, s7
	v_lshlrev_b32_e32 v56, 4, v2
	v_mov_b32_e32 v57, 0
	v_lshl_add_u64 v[54:55], s[4:5], 0, v[56:57]
	s_movk_i32 s3, 0x1000
	v_add_co_u32_e32 v50, vcc, s3, v54
	s_movk_i32 s3, 0x2000
	s_nop 0
	v_addc_co_u32_e32 v51, vcc, 0, v55, vcc
	v_add_co_u32_e32 v52, vcc, s3, v54
	global_load_dwordx4 v[2:5], v56, s[4:5] offset:1024
	global_load_dwordx4 v[6:9], v56, s[4:5] offset:2048
	v_addc_co_u32_e32 v53, vcc, 0, v55, vcc
	global_load_dwordx4 v[10:13], v56, s[4:5] offset:3072
	global_load_dwordx4 v[14:17], v[52:53], off offset:-4096
	global_load_dwordx4 v[18:21], v[50:51], off offset:1024
	global_load_dwordx4 v[22:25], v[50:51], off offset:2048
	global_load_dwordx4 v[26:29], v56, s[4:5]
	global_load_dwordx4 v[30:33], v[50:51], off offset:3072
	global_load_dwordx4 v[34:37], v[52:53], off
	global_load_dwordx4 v[38:41], v[52:53], off offset:1024
	global_load_dwordx4 v[42:45], v[52:53], off offset:2048
	global_load_dwordx4 v[46:49], v[52:53], off offset:3072
	s_movk_i32 s3, 0x3000
	v_add_co_u32_e32 v58, vcc, s3, v54
	s_movk_i32 s3, 0x4000
	s_nop 0
	v_addc_co_u32_e32 v59, vcc, 0, v55, vcc
	v_add_co_u32_e32 v140, vcc, s3, v54
	s_nop 1
	v_addc_co_u32_e32 v141, vcc, 0, v55, vcc
	s_barrier
	global_load_dwordx4 v[50:53], v[140:141], off offset:-4096
	global_load_dwordx4 v[62:65], v[58:59], off offset:1024
	global_load_dwordx4 v[68:71], v[58:59], off offset:2048
	v_lshlrev_b32_e32 v67, 9, v1
	v_xor_b32_e32 v61, v167, v1
	v_lshl_or_b32 v66, v61, 4, v67
	ds_read_b128 v[72:75], v66
	ds_read_b128 v[76:79], v66 offset:8192
	ds_read_b128 v[80:83], v66 offset:16384
	ds_read_b128 v[84:87], v66 offset:24576
	v_mul_u32_u24_e32 v60, 0x556, v0
	v_lshrrev_b32_e32 v60, 16, v60
	s_mul_i32 s3, s6, 48
	v_lshlrev_b32_e32 v61, 3, v60
	s_movk_i32 s5, 0x47
	v_lshl_or_b32 v56, v167, 2, s3
	s_mov_b32 s3, 0xfffffd0
	v_bitop3_b32 v61, v61, s5, v60 bitop3:0xc8
	s_mov_b32 s27, 0x20000
	s_mov_b32 s26, 0x1800000
	s_mul_i32 s4, s6, 0x60
	v_mul_lo_u32 v150, v60, s3
	v_or_b32_e32 v61, s2, v61
	s_waitcnt vmcnt(8) lgkmcnt(3)
	v_mfma_f32_16x16x32_f16 v[88:91], v[26:29], v[72:75], 0
	s_waitcnt lgkmcnt(2)
	v_mfma_f32_16x16x32_f16 v[92:95], v[26:29], v[76:79], 0
	s_waitcnt lgkmcnt(1)
	v_mfma_f32_16x16x32_f16 v[96:99], v[26:29], v[80:83], 0
	s_waitcnt lgkmcnt(0)
	v_mfma_f32_16x16x32_f16 v[26:29], v[26:29], v[84:87], 0
	v_mfma_f32_16x16x32_f16 v[100:103], v[2:5], v[72:75], 0
	v_mfma_f32_16x16x32_f16 v[104:107], v[2:5], v[76:79], 0
	v_mfma_f32_16x16x32_f16 v[108:111], v[2:5], v[80:83], 0
	v_mfma_f32_16x16x32_f16 v[2:5], v[2:5], v[84:87], 0
	v_mfma_f32_16x16x32_f16 v[112:115], v[6:9], v[72:75], 0
	v_mfma_f32_16x16x32_f16 v[74:77], v[6:9], v[76:79], 0
	v_mfma_f32_16x16x32_f16 v[78:81], v[6:9], v[80:83], 0
	v_mfma_f32_16x16x32_f16 v[6:9], v[6:9], v[84:87], 0
	global_load_dwordx4 v[82:85], v[58:59], off offset:3072
	global_load_dwordx4 v[116:119], v[140:141], off
	global_load_dwordx4 v[120:123], v[140:141], off offset:1024
	v_bitop3_b32 v58, v167, v1, 4 bitop3:0x36
	v_lshl_or_b32 v72, v58, 4, v67
	ds_read_b128 v[124:127], v72
	ds_read_b128 v[128:131], v72 offset:8192
	ds_read_b128 v[132:135], v72 offset:16384
	ds_read_b128 v[136:139], v72 offset:24576
	s_waitcnt lgkmcnt(3)
	v_mfma_f32_16x16x32_f16 v[86:89], v[10:13], v[124:127], v[88:91]
	s_waitcnt lgkmcnt(2)
	v_mfma_f32_16x16x32_f16 v[90:93], v[10:13], v[128:131], v[92:95]
	s_waitcnt lgkmcnt(1)
	v_mfma_f32_16x16x32_f16 v[94:97], v[10:13], v[132:135], v[96:99]
	s_waitcnt lgkmcnt(0)
	v_mfma_f32_16x16x32_f16 v[10:13], v[10:13], v[136:139], v[26:29]
	v_mfma_f32_16x16x32_f16 v[26:29], v[14:17], v[124:127], v[100:103]
	v_mfma_f32_16x16x32_f16 v[98:101], v[14:17], v[128:131], v[104:107]
	v_mfma_f32_16x16x32_f16 v[102:105], v[14:17], v[132:135], v[108:111]
	v_mfma_f32_16x16x32_f16 v[2:5], v[14:17], v[136:139], v[2:5]
	v_mfma_f32_16x16x32_f16 v[14:17], v[18:21], v[124:127], v[112:115]
	v_mfma_f32_16x16x32_f16 v[106:109], v[18:21], v[128:131], v[74:77]
	v_mfma_f32_16x16x32_f16 v[76:79], v[18:21], v[132:135], v[78:81]
	v_mfma_f32_16x16x32_f16 v[6:9], v[18:21], v[136:139], v[6:9]
	s_movk_i32 s5, 0x5000
	v_add_co_u32_e32 v58, vcc, s5, v54
	global_load_dwordx4 v[110:113], v[140:141], off offset:2048
	global_load_dwordx4 v[124:127], v[140:141], off offset:3072
	v_addc_co_u32_e32 v59, vcc, 0, v55, vcc
	global_load_dwordx4 v[128:131], v[58:59], off
	v_bitop3_b32 v18, v167, v1, 8 bitop3:0x36
	v_lshl_or_b32 v74, v18, 4, v67
	ds_read_b128 v[18:21], v74
	ds_read_b128 v[132:135], v74 offset:8192
	ds_read_b128 v[136:139], v74 offset:16384
	ds_read_b128 v[140:143], v74 offset:24576
	s_waitcnt lgkmcnt(3)
	v_mfma_f32_16x16x32_f16 v[86:89], v[22:25], v[18:21], v[86:89]
	s_waitcnt lgkmcnt(2)
	v_mfma_f32_16x16x32_f16 v[90:93], v[22:25], v[132:135], v[90:93]
	s_waitcnt lgkmcnt(1)
	v_mfma_f32_16x16x32_f16 v[94:97], v[22:25], v[136:139], v[94:97]
	s_waitcnt lgkmcnt(0)
	v_mfma_f32_16x16x32_f16 v[10:13], v[22:25], v[140:143], v[10:13]
	s_waitcnt vmcnt(13)
	v_mfma_f32_16x16x32_f16 v[22:25], v[30:33], v[18:21], v[26:29]
	v_mfma_f32_16x16x32_f16 v[26:29], v[30:33], v[132:135], v[98:101]
	v_mfma_f32_16x16x32_f16 v[98:101], v[30:33], v[136:139], v[102:105]
	v_mfma_f32_16x16x32_f16 v[2:5], v[30:33], v[140:143], v[2:5]
	s_waitcnt vmcnt(12)
	v_mfma_f32_16x16x32_f16 v[14:17], v[34:37], v[18:21], v[14:17]
	v_mfma_f32_16x16x32_f16 v[18:21], v[34:37], v[132:135], v[106:109]
	v_mfma_f32_16x16x32_f16 v[30:33], v[34:37], v[136:139], v[76:79]
	v_mfma_f32_16x16x32_f16 v[6:9], v[34:37], v[140:143], v[6:9]
	global_load_dwordx4 v[102:105], v[58:59], off offset:1024
	global_load_dwordx4 v[106:109], v[58:59], off offset:2048
	global_load_dwordx4 v[132:135], v[58:59], off offset:3072
	v_bitop3_b32 v34, v167, v1, 12 bitop3:0x36
	v_lshl_or_b32 v75, v34, 4, v67
	ds_read_b128 v[34:37], v75
	ds_read_b128 v[76:79], v75 offset:8192
	ds_read_b128 v[136:139], v75 offset:16384
	ds_read_b128 v[140:143], v75 offset:24576
	s_waitcnt vmcnt(14) lgkmcnt(3)
	v_mfma_f32_16x16x32_f16 v[86:89], v[38:41], v[34:37], v[86:89]
	s_waitcnt lgkmcnt(2)
	v_mfma_f32_16x16x32_f16 v[90:93], v[38:41], v[76:79], v[90:93]
	s_waitcnt lgkmcnt(1)
	v_mfma_f32_16x16x32_f16 v[94:97], v[38:41], v[136:139], v[94:97]
	s_waitcnt lgkmcnt(0)
	v_mfma_f32_16x16x32_f16 v[10:13], v[38:41], v[140:143], v[10:13]
	s_waitcnt vmcnt(13)
	v_mfma_f32_16x16x32_f16 v[38:41], v[42:45], v[34:37], v[22:25]
	v_mfma_f32_16x16x32_f16 v[144:147], v[42:45], v[76:79], v[26:29]
	v_mfma_f32_16x16x32_f16 v[98:101], v[42:45], v[136:139], v[98:101]
	v_mfma_f32_16x16x32_f16 v[2:5], v[42:45], v[140:143], v[2:5]
	s_waitcnt vmcnt(12)
	v_mfma_f32_16x16x32_f16 v[14:17], v[46:49], v[34:37], v[14:17]
	v_mfma_f32_16x16x32_f16 v[18:21], v[46:49], v[76:79], v[18:21]
	v_mfma_f32_16x16x32_f16 v[30:33], v[46:49], v[136:139], v[30:33]
	v_mfma_f32_16x16x32_f16 v[6:9], v[46:49], v[140:143], v[6:9]
	s_mov_b32 s5, 0x30000
	v_add_co_u32_e32 v58, vcc, s5, v54
	s_mov_b32 s5, 0x31000
	s_nop 0
	v_addc_co_u32_e32 v59, vcc, 0, v55, vcc
	v_add_co_u32_e32 v148, vcc, s5, v54
	v_bitop3_b32 v42, v167, v1, 16 bitop3:0x36
	s_nop 0
	v_addc_co_u32_e32 v149, vcc, 0, v55, vcc
	global_load_dwordx4 v[34:37], v[148:149], off offset:-4096
	global_load_dwordx4 v[26:29], v[58:59], off offset:1024
	global_load_dwordx4 v[22:25], v[58:59], off offset:2048
	v_lshl_or_b32 v76, v42, 4, v67
	ds_read_b128 v[42:45], v76
	ds_read_b128 v[46:49], v76 offset:8192
	ds_read_b128 v[78:81], v76 offset:16384
	ds_read_b128 v[136:139], v76 offset:24576
	s_waitcnt vmcnt(14) lgkmcnt(3)
	v_mfma_f32_16x16x32_f16 v[86:89], v[50:53], v[42:45], v[86:89]
	s_waitcnt lgkmcnt(2)
	v_mfma_f32_16x16x32_f16 v[90:93], v[50:53], v[46:49], v[90:93]
	s_waitcnt lgkmcnt(1)
	v_mfma_f32_16x16x32_f16 v[94:97], v[50:53], v[78:81], v[94:97]
	s_waitcnt lgkmcnt(0)
	v_mfma_f32_16x16x32_f16 v[10:13], v[50:53], v[136:139], v[10:13]
	s_waitcnt vmcnt(13)
	v_mfma_f32_16x16x32_f16 v[38:41], v[62:65], v[42:45], v[38:41]
	v_mfma_f32_16x16x32_f16 v[50:53], v[62:65], v[46:49], v[144:147]
	v_mfma_f32_16x16x32_f16 v[98:101], v[62:65], v[78:81], v[98:101]
	v_mfma_f32_16x16x32_f16 v[62:65], v[62:65], v[136:139], v[2:5]
	s_waitcnt vmcnt(12)
	v_mfma_f32_16x16x32_f16 v[42:45], v[68:71], v[42:45], v[14:17]
	v_mfma_f32_16x16x32_f16 v[18:21], v[68:71], v[46:49], v[18:21]
	v_mfma_f32_16x16x32_f16 v[30:33], v[68:71], v[78:81], v[30:33]
	v_mfma_f32_16x16x32_f16 v[46:49], v[68:71], v[136:139], v[6:9]
	global_load_dwordx4 v[14:17], v[58:59], off offset:3072
	s_nop 1
	global_load_dwordx4 v[6:9], v[148:149], off
	global_load_dwordx4 v[2:5], v[148:149], off offset:1024
	v_bitop3_b32 v58, v167, v1, 20 bitop3:0x36
	v_lshl_or_b32 v77, v58, 4, v67
	ds_read_b128 v[68:71], v77
	ds_read_b128 v[78:81], v77 offset:8192
	ds_read_b128 v[136:139], v77 offset:16384
	ds_read_b128 v[140:143], v77 offset:24576
	s_waitcnt vmcnt(14) lgkmcnt(3)
	v_mfma_f32_16x16x32_f16 v[86:89], v[82:85], v[68:71], v[86:89]
	s_waitcnt lgkmcnt(2)
	v_mfma_f32_16x16x32_f16 v[90:93], v[82:85], v[78:81], v[90:93]
	s_waitcnt lgkmcnt(1)
	v_mfma_f32_16x16x32_f16 v[94:97], v[82:85], v[136:139], v[94:97]
	s_waitcnt lgkmcnt(0)
	v_mfma_f32_16x16x32_f16 v[82:85], v[82:85], v[140:143], v[10:13]
	s_waitcnt vmcnt(13)
	v_mfma_f32_16x16x32_f16 v[38:41], v[116:119], v[68:71], v[38:41]
	v_mfma_f32_16x16x32_f16 v[50:53], v[116:119], v[78:81], v[50:53]
	v_mfma_f32_16x16x32_f16 v[98:101], v[116:119], v[136:139], v[98:101]
	v_mfma_f32_16x16x32_f16 v[62:65], v[116:119], v[140:143], v[62:65]
	s_waitcnt vmcnt(12)
	v_mfma_f32_16x16x32_f16 v[42:45], v[120:123], v[68:71], v[42:45]
	v_mfma_f32_16x16x32_f16 v[68:71], v[120:123], v[78:81], v[18:21]
	v_mfma_f32_16x16x32_f16 v[114:117], v[120:123], v[136:139], v[30:33]
	v_mfma_f32_16x16x32_f16 v[46:49], v[120:123], v[140:143], v[46:49]
	s_mov_b32 s5, 0x33000
	v_add_co_u32_e32 v58, vcc, s5, v54
	global_load_dwordx4 v[18:21], v[148:149], off offset:2048
	global_load_dwordx4 v[10:13], v[148:149], off offset:3072
	v_addc_co_u32_e32 v59, vcc, 0, v55, vcc
	global_load_dwordx4 v[30:33], v[58:59], off offset:-4096
	v_bitop3_b32 v73, v167, v1, 24 bitop3:0x36
	v_lshl_or_b32 v78, v73, 4, v67
	ds_read_b128 v[118:121], v78
	ds_read_b128 v[136:139], v78 offset:8192
	ds_read_b128 v[140:143], v78 offset:16384
	ds_read_b128 v[144:147], v78 offset:24576
	s_mov_b32 s5, 0x32000
	v_add_co_u32_e32 v148, vcc, s5, v54
	s_nop 1
	v_addc_co_u32_e32 v149, vcc, 0, v55, vcc
	s_waitcnt vmcnt(14) lgkmcnt(3)
	v_mfma_f32_16x16x32_f16 v[86:89], v[110:113], v[118:121], v[86:89]
	s_waitcnt lgkmcnt(2)
	v_mfma_f32_16x16x32_f16 v[90:93], v[110:113], v[136:139], v[90:93]
	s_waitcnt lgkmcnt(1)
	v_mfma_f32_16x16x32_f16 v[94:97], v[110:113], v[140:143], v[94:97]
	s_waitcnt lgkmcnt(0)
	v_mfma_f32_16x16x32_f16 v[80:83], v[110:113], v[144:147], v[82:85]
	s_waitcnt vmcnt(13)
	v_mfma_f32_16x16x32_f16 v[110:113], v[124:127], v[118:121], v[38:41]
	v_mfma_f32_16x16x32_f16 v[50:53], v[124:127], v[136:139], v[50:53]
	v_mfma_f32_16x16x32_f16 v[98:101], v[124:127], v[140:143], v[98:101]
	v_mfma_f32_16x16x32_f16 v[62:65], v[124:127], v[144:147], v[62:65]
	s_waitcnt vmcnt(12)
	v_mfma_f32_16x16x32_f16 v[118:121], v[128:131], v[118:121], v[42:45]
	v_mfma_f32_16x16x32_f16 v[68:71], v[128:131], v[136:139], v[68:71]
	v_mfma_f32_16x16x32_f16 v[114:117], v[128:131], v[140:143], v[114:117]
	v_mfma_f32_16x16x32_f16 v[122:125], v[128:131], v[144:147], v[46:49]
	s_nop 2
	global_load_dwordx4 v[46:49], v[148:149], off offset:1024
	global_load_dwordx4 v[42:45], v[148:149], off offset:2048
	global_load_dwordx4 v[38:41], v[148:149], off offset:3072
	v_bitop3_b32 v73, v167, v1, 28 bitop3:0x36
	v_lshl_or_b32 v79, v73, 4, v67
	ds_read_b128 v[126:129], v79
	ds_read_b128 v[136:139], v79 offset:8192
	ds_read_b128 v[140:143], v79 offset:16384
	ds_read_b128 v[144:147], v79 offset:24576
	s_waitcnt vmcnt(14) lgkmcnt(3)
	v_mfma_f32_16x16x32_f16 v[84:87], v[102:105], v[126:129], v[86:89]
	s_waitcnt lgkmcnt(2)
	v_mfma_f32_16x16x32_f16 v[88:91], v[102:105], v[136:139], v[90:93]
	s_waitcnt lgkmcnt(1)
	v_mfma_f32_16x16x32_f16 v[92:95], v[102:105], v[140:143], v[94:97]
	s_waitcnt lgkmcnt(0)
	v_mfma_f32_16x16x32_f16 v[80:83], v[102:105], v[144:147], v[80:83]
	s_waitcnt vmcnt(13)
	v_mfma_f32_16x16x32_f16 v[102:105], v[106:109], v[126:129], v[110:113]
	v_mfma_f32_16x16x32_f16 v[110:113], v[106:109], v[136:139], v[50:53]
	v_mfma_f32_16x16x32_f16 v[96:99], v[106:109], v[140:143], v[98:101]
	v_mfma_f32_16x16x32_f16 v[62:65], v[106:109], v[144:147], v[62:65]
	s_waitcnt vmcnt(12)
	v_mfma_f32_16x16x32_f16 v[106:109], v[132:135], v[126:129], v[118:121]
	v_mfma_f32_16x16x32_f16 v[118:121], v[132:135], v[136:139], v[68:71]
	v_mfma_f32_16x16x32_f16 v[114:117], v[132:135], v[140:143], v[114:117]
	v_mfma_f32_16x16x32_f16 v[50:53], v[132:135], v[144:147], v[122:125]
	v_lshl_add_u64 v[56:57], v[56:57], 2, s[0:1]
	s_nop 1
	global_load_dwordx4 v[122:125], v[56:57], off
	global_load_dwordx4 v[126:129], v[56:57], off offset:64
	global_load_dwordx4 v[130:133], v[56:57], off offset:128
	v_lshl_or_b32 v67, v167, 3, s4
	s_movk_i32 s0, 0x310
	v_mov_b32_e32 v100, v89
	v_mov_b32_e32 v101, v90
	v_mov_b32_e32 v134, v93
	v_mov_b32_e32 v135, v94
	v_mov_b32_e32 v140, v97
	v_mov_b32_e32 v141, v98
	v_mad_u32_u24 v69, v1, s0, v67
	v_mov_b32_e32 v143, v64
	v_mov_b32_e32 v136, v81
	v_mov_b32_e32 v137, v82
	v_mov_b32_e32 v138, v111
	v_mov_b32_e32 v139, v112
	v_mov_b32_e32 v142, v63
	v_add_u32_e32 v73, 0x8000, v69
	s_barrier
	v_add_u32_e32 v70, 0xb000, v69
	v_add_u32_e32 v71, 0xe000, v69
	v_add_u32_e32 v68, 0x9300, v69
	s_movk_i32 s1, 0x600
	s_movk_i32 s6, 0x1c7
	s_waitcnt vmcnt(2)
	v_pk_add_f32 v[84:85], v[84:85], v[122:123]
	v_add_f32_e32 v1, v88, v122
	v_pk_mov_b32 v[88:89], v[122:123], v[124:125] op_sel:[1,0]
	v_add_f32_e32 v67, v91, v125
	v_add_f32_e32 v92, v92, v122
	v_add_f32_e32 v93, v95, v125
	v_add_f32_e32 v94, v80, v122
	v_add_f32_e32 v95, v83, v125
	s_waitcnt vmcnt(1)
	v_add_f32_e32 v97, v110, v126
	v_add_f32_e32 v98, v113, v129
	v_add_f32_e32 v96, v96, v126
	v_add_f32_e32 v99, v99, v129
	v_cvt_pk_f16_f32 v64, v84, v85
	v_cvt_f16_f32_e32 v1, v1
	v_pk_add_f32 v[84:85], v[100:101], v[88:89]
	v_cvt_f16_f32_e32 v67, v67
	v_cvt_f16_f32_e32 v100, v92
	v_cvt_f16_f32_e32 v101, v93
	v_cvt_f16_f32_e32 v94, v94
	v_cvt_f16_f32_e32 v95, v95
	v_cvt_f16_f32_e32 v97, v97
	v_cvt_f16_f32_e32 v98, v98
	v_pk_add_f32 v[86:87], v[86:87], v[124:125]
	v_pk_add_f32 v[80:81], v[102:103], v[126:127]
	v_pk_add_f32 v[82:83], v[104:105], v[128:129]
	v_pk_mov_b32 v[90:91], v[126:127], v[128:129] op_sel:[1,0]
	v_cvt_f16_f32_e32 v96, v96
	v_cvt_f16_f32_e32 v99, v99
	v_add_f32_e32 v102, v62, v126
	v_add_f32_e32 v103, v65, v129
	s_waitcnt vmcnt(0)
	v_pk_add_f32 v[62:63], v[106:107], v[130:131]
	v_cvt_pk_f16_f32 v65, v86, v87
	v_pk_add_f32 v[86:87], v[134:135], v[88:89]
	v_pk_add_f32 v[88:89], v[136:137], v[88:89]
	v_cvt_pk_f16_f32 v80, v80, v81
	v_cvt_pk_f16_f32 v81, v82, v83
	v_pk_add_f32 v[82:83], v[138:139], v[90:91]
	v_pk_add_f32 v[92:93], v[140:141], v[90:91]
	v_cvt_pk_f16_f32 v62, v62, v63
	v_cvt_pk_f16_f32 v63, v84, v85
	v_cvt_pk_f16_f32 v84, v86, v87
	v_cvt_pk_f16_f32 v85, v88, v89
	v_cvt_pk_f16_f32 v86, v82, v83
	v_cvt_pk_f16_f32 v87, v92, v93
	ds_write2_b64 v73, v[64:65], v[80:81] offset1:4
	v_pack_b32_f16 v64, v1, v63
	v_alignbit_b32 v65, v67, v63, 16
	v_pack_b32_f16 v80, v100, v84
	v_alignbit_b32 v81, v101, v84, 16
	v_pack_b32_f16 v82, v94, v85
	v_alignbit_b32 v83, v95, v85, 16
	v_pack_b32_f16 v84, v97, v86
	v_alignbit_b32 v85, v98, v86, 16
	v_pack_b32_f16 v86, v96, v87
	v_alignbit_b32 v87, v99, v87, 16
	ds_write2_b64 v70, v[64:65], v[84:85] offset0:32 offset1:36
	ds_write2_b64 v71, v[80:81], v[86:87] offset0:64 offset1:68
	v_pk_add_f32 v[64:65], v[108:109], v[132:133]
	v_add_f32_e32 v1, v118, v130
	v_cvt_pk_f16_f32 v63, v64, v65
	v_cvt_f16_f32_e32 v1, v1
	v_add_f32_e32 v67, v121, v133
	ds_write_b64 v69, v[62:63] offset:32832
	v_mov_b32_e32 v62, v119
	v_mov_b32_e32 v63, v120
	v_pk_mov_b32 v[64:65], v[130:131], v[132:133] op_sel:[1,0]
	v_cvt_f16_f32_e32 v67, v67
	v_pk_add_f32 v[62:63], v[62:63], v[64:65]
	v_cvt_f16_f32_e32 v102, v102
	v_cvt_pk_f16_f32 v63, v62, v63
	v_pack_b32_f16 v62, v1, v63
	v_add_f32_e32 v1, v114, v130
	v_alignbit_b32 v63, v67, v63, 16
	v_cvt_f16_f32_e32 v1, v1
	ds_write_b64 v69, v[62:63] offset:45376
	v_mov_b32_e32 v62, v115
	v_mov_b32_e32 v63, v116
	v_pk_add_f32 v[62:63], v[62:63], v[64:65]
	v_add_f32_e32 v67, v117, v133
	v_cvt_pk_f16_f32 v63, v62, v63
	v_pack_b32_f16 v62, v1, v63
	v_add_f32_e32 v1, v50, v130
	v_mov_b32_e32 v50, v51
	v_mov_b32_e32 v51, v52
	v_add_f32_e32 v52, v53, v133
	v_cvt_f16_f32_e32 v103, v103
	v_cvt_f16_f32_e32 v67, v67
	v_cvt_f16_f32_e32 v1, v1
	v_cvt_f16_f32_e32 v52, v52
	v_pk_add_f32 v[90:91], v[142:143], v[90:91]
	v_pk_add_f32 v[50:51], v[50:51], v[64:65]
	v_cvt_pk_f16_f32 v89, v90, v91
	v_cvt_pk_f16_f32 v51, v50, v51
	v_pack_b32_f16 v88, v102, v89
	v_alignbit_b32 v89, v103, v89, 16
	v_add_u32_e32 v80, 0x8000, v68
	v_alignbit_b32 v63, v67, v63, 16
	v_pack_b32_f16 v50, v1, v51
	v_alignbit_b32 v51, v52, v51, 16
	ds_write2_b64 v80, v[82:83], v[88:89] offset1:4
	ds_write_b64 v69, v[62:63] offset:57920
	ds_write_b64 v68, v[50:51] offset:32832
	s_waitcnt lgkmcnt(0)
	s_barrier
	global_load_dwordx4 v[82:85], v[58:59], off
	global_load_dwordx4 v[86:89], v[58:59], off offset:1024
	global_load_dwordx4 v[90:93], v[58:59], off offset:2048
	v_add_lshl_u32 v52, v150, v0, 4
	v_mad_u64_u32 v[50:51], s[4:5], v61, s1, v[52:53]
	v_or_b32_e32 v1, 0x200, v0
	v_mad_u32_u24 v51, v60, s0, v52
	v_mul_u32_u24_e32 v52, 0x556, v1
	v_lshrrev_b32_e32 v53, 16, v52
	v_mul_lo_u32 v52, v53, s3
	v_add_lshl_u32 v52, v52, v1, 4
	v_lshlrev_b32_e32 v1, 3, v53
	s_movk_i32 s4, 0xc7
	ds_read_b128 v[60:63], v51 offset:32768
	v_bitop3_b32 v1, v1, s4, v53 bitop3:0xc8
	v_or_b32_e32 v1, s2, v1
	v_mad_u32_u24 v81, v53, s0, v52
	v_mad_u64_u32 v[52:53], s[4:5], v1, s1, v[52:53]
	v_or_b32_e32 v1, 0x400, v0
	v_mul_u32_u24_e32 v53, 0x556, v1
	v_lshrrev_b32_e32 v53, 16, v53
	ds_read_b128 v[94:97], v81 offset:32768
	s_waitcnt lgkmcnt(1)
	buffer_store_dwordx4 v[60:63], v50, s[24:27], 0 offen sc1
	s_waitcnt lgkmcnt(0)
	buffer_store_dwordx4 v[94:97], v52, s[24:27], 0 offen sc1
	v_lshlrev_b32_e32 v61, 3, v53
	v_mul_lo_u32 v60, v53, s3
	v_bitop3_b32 v61, v61, s6, v53 bitop3:0xc8
	v_or_b32_e32 v61, s2, v61
	v_add_lshl_u32 v62, v60, v1, 4
	v_mad_u64_u32 v[60:61], s[4:5], v61, s1, v[62:63]
	v_or_b32_e32 v1, 0x600, v0
	v_mad_u32_u24 v53, v53, s0, v62
	v_mul_u32_u24_e32 v61, 0x556, v1
	ds_read_b128 v[62:65], v53 offset:32768
	v_lshrrev_b32_e32 v67, 16, v61
	v_mul_lo_u32 v94, v67, s3
	v_add_lshl_u32 v98, v94, v1, 4
	v_lshrrev_b32_e32 v1, 13, v61
	v_mad_u32_u24 v160, v67, s0, v98
	v_and_b32_e32 v1, 0x1c0, v1
	v_bfe_u32 v61, v61, 16, 3
	ds_read_b128 v[94:97], v160 offset:32768
	v_or3_b32 v1, s2, v61, v1
	s_waitcnt lgkmcnt(1)
	buffer_store_dwordx4 v[62:65], v60, s[24:27], 0 offen sc1
	s_nop 1
	v_mad_u64_u32 v[62:63], s[4:5], v1, s1, v[98:99]
	v_or_b32_e32 v1, 0x800, v0
	v_mul_u32_u24_e32 v61, 0xaab, v1
	v_lshrrev_b32_e32 v61, 17, v61
	v_mul_lo_u32 v63, v61, s3
	v_lshlrev_b32_e32 v64, 3, v61
	s_waitcnt lgkmcnt(0)
	buffer_store_dwordx4 v[94:97], v62, s[24:27], 0 offen sc1
	v_bitop3_b32 v64, v64, s6, v61 bitop3:0xc8
	v_or_b32_e32 v64, s2, v64
	v_add_lshl_u32 v94, v63, v1, 4
	v_mad_u32_u24 v61, v61, s0, v94
	v_or_b32_e32 v0, 0xa00, v0
	v_mad_u64_u32 v[64:65], s[4:5], v64, s1, v[94:95]
	ds_read_b128 v[94:97], v61 offset:32768
	v_mul_u32_u24_e32 v1, 0xaab, v0
	v_lshrrev_b32_e32 v63, 17, v1
	v_mul_lo_u32 v65, v63, s3
	v_add_lshl_u32 v0, v65, v0, 4
	v_mad_u32_u24 v63, v63, s0, v0
	ds_read_b128 v[98:101], v63 offset:32768
	s_waitcnt lgkmcnt(1)
	buffer_store_dwordx4 v[94:97], v64, s[24:27], 0 offen sc1
	ds_read_b128 v[94:97], v66
	ds_read_b128 v[102:105], v66 offset:8192
	ds_read_b128 v[106:109], v66 offset:16384
	ds_read_b128 v[110:113], v66 offset:24576
	v_lshrrev_b32_e32 v65, 14, v1
	v_and_b32_e32 v65, 0x1c0, v65
	v_bfe_u32 v1, v1, 17, 3
	v_or3_b32 v1, s2, v1, v65
	v_mad_u64_u32 v[66:67], s[0:1], v1, s1, v[0:1]
	s_waitcnt lgkmcnt(4)
	buffer_store_dwordx4 v[98:101], v66, s[24:27], 0 offen sc1
	s_waitcnt lgkmcnt(3)
	s_nop 0
	v_mfma_f32_16x16x32_f16 v[98:101], v[34:37], v[94:97], 0
	s_waitcnt lgkmcnt(2)
	v_mfma_f32_16x16x32_f16 v[114:117], v[34:37], v[102:105], 0
	s_waitcnt lgkmcnt(1)
	v_mfma_f32_16x16x32_f16 v[118:121], v[34:37], v[106:109], 0
	s_waitcnt lgkmcnt(0)
	v_mfma_f32_16x16x32_f16 v[34:37], v[34:37], v[110:113], 0
	v_mfma_f32_16x16x32_f16 v[122:125], v[26:29], v[94:97], 0
	v_mfma_f32_16x16x32_f16 v[126:129], v[26:29], v[102:105], 0
	v_mfma_f32_16x16x32_f16 v[130:133], v[26:29], v[106:109], 0
	v_mfma_f32_16x16x32_f16 v[26:29], v[26:29], v[110:113], 0
	v_mfma_f32_16x16x32_f16 v[94:97], v[22:25], v[94:97], 0
	v_mfma_f32_16x16x32_f16 v[102:105], v[22:25], v[102:105], 0
	v_mfma_f32_16x16x32_f16 v[106:109], v[22:25], v[106:109], 0
	v_mfma_f32_16x16x32_f16 v[22:25], v[22:25], v[110:113], 0
	s_mov_b32 s0, 0x34000
	v_add_co_u32_e32 v158, vcc, s0, v54
	s_mov_b32 s0, 0x35000
	s_nop 0
	v_addc_co_u32_e32 v159, vcc, 0, v55, vcc
	v_add_co_u32_e32 v54, vcc, s0, v54
	s_nop 1
	v_addc_co_u32_e32 v55, vcc, 0, v55, vcc
	global_load_dwordx4 v[110:113], v[54:55], off offset:-4096
	global_load_dwordx4 v[134:137], v[58:59], off offset:3072
	global_load_dwordx4 v[138:141], v[158:159], off offset:1024
	ds_read_b128 v[142:145], v72
	ds_read_b128 v[146:149], v72 offset:8192
	ds_read_b128 v[150:153], v72 offset:16384
	ds_read_b128 v[154:157], v72 offset:24576
	s_waitcnt lgkmcnt(3)
	v_mfma_f32_16x16x32_f16 v[98:101], v[14:17], v[142:145], v[98:101]
	s_waitcnt lgkmcnt(2)
	v_mfma_f32_16x16x32_f16 v[114:117], v[14:17], v[146:149], v[114:117]
	s_waitcnt lgkmcnt(1)
	v_mfma_f32_16x16x32_f16 v[118:121], v[14:17], v[150:153], v[118:121]
	s_waitcnt lgkmcnt(0)
	v_mfma_f32_16x16x32_f16 v[14:17], v[14:17], v[154:157], v[34:37]
	v_mfma_f32_16x16x32_f16 v[34:37], v[6:9], v[142:145], v[122:125]
	v_mfma_f32_16x16x32_f16 v[122:125], v[6:9], v[146:149], v[126:129]
	v_mfma_f32_16x16x32_f16 v[126:129], v[6:9], v[150:153], v[130:133]
	v_mfma_f32_16x16x32_f16 v[6:9], v[6:9], v[154:157], v[26:29]
	v_mfma_f32_16x16x32_f16 v[26:29], v[2:5], v[142:145], v[94:97]
	v_mfma_f32_16x16x32_f16 v[94:97], v[2:5], v[146:149], v[102:105]
	v_mfma_f32_16x16x32_f16 v[102:105], v[2:5], v[150:153], v[106:109]
	v_mfma_f32_16x16x32_f16 v[0:3], v[2:5], v[154:157], v[22:25]
	s_nop 2
	global_load_dwordx4 v[22:25], v[158:159], off offset:2048
	global_load_dwordx4 v[106:109], v[158:159], off offset:3072
	global_load_dwordx4 v[130:133], v[54:55], off
	ds_read_b128 v[142:145], v74
	ds_read_b128 v[146:149], v74 offset:8192
	ds_read_b128 v[150:153], v74 offset:16384
	ds_read_b128 v[154:157], v74 offset:24576
	s_waitcnt lgkmcnt(3)
	v_mfma_f32_16x16x32_f16 v[98:101], v[18:21], v[142:145], v[98:101]
	s_waitcnt lgkmcnt(2)
	v_mfma_f32_16x16x32_f16 v[114:117], v[18:21], v[146:149], v[114:117]
	s_waitcnt lgkmcnt(1)
	v_mfma_f32_16x16x32_f16 v[118:121], v[18:21], v[150:153], v[118:121]
	s_waitcnt lgkmcnt(0)
	v_mfma_f32_16x16x32_f16 v[14:17], v[18:21], v[154:157], v[14:17]
	v_mfma_f32_16x16x32_f16 v[18:21], v[10:13], v[142:145], v[34:37]
	v_mfma_f32_16x16x32_f16 v[34:37], v[10:13], v[146:149], v[122:125]
	v_mfma_f32_16x16x32_f16 v[122:125], v[10:13], v[150:153], v[126:129]
	v_mfma_f32_16x16x32_f16 v[4:7], v[10:13], v[154:157], v[6:9]
	v_mfma_f32_16x16x32_f16 v[8:11], v[30:33], v[142:145], v[26:29]
	v_mfma_f32_16x16x32_f16 v[26:29], v[30:33], v[146:149], v[94:97]
	v_mfma_f32_16x16x32_f16 v[94:97], v[30:33], v[150:153], v[102:105]
	v_mfma_f32_16x16x32_f16 v[0:3], v[30:33], v[154:157], v[0:3]
	global_load_dwordx4 v[30:33], v[54:55], off offset:1024
	s_nop 0
	global_load_dwordx4 v[102:105], v[54:55], off offset:2048
	global_load_dwordx4 v[126:129], v[54:55], off offset:3072
	ds_read_b128 v[142:145], v75
	ds_read_b128 v[146:149], v75 offset:8192
	ds_read_b128 v[150:153], v75 offset:16384
	ds_read_b128 v[154:157], v75 offset:24576
	s_waitcnt lgkmcnt(3)
	v_mfma_f32_16x16x32_f16 v[98:101], v[46:49], v[142:145], v[98:101]
	s_waitcnt lgkmcnt(2)
	v_mfma_f32_16x16x32_f16 v[114:117], v[46:49], v[146:149], v[114:117]
	s_waitcnt lgkmcnt(1)
	v_mfma_f32_16x16x32_f16 v[118:121], v[46:49], v[150:153], v[118:121]
	s_waitcnt lgkmcnt(0)
	v_mfma_f32_16x16x32_f16 v[12:15], v[46:49], v[154:157], v[14:17]
	v_mfma_f32_16x16x32_f16 v[16:19], v[42:45], v[142:145], v[18:21]
	v_mfma_f32_16x16x32_f16 v[34:37], v[42:45], v[146:149], v[34:37]
	v_mfma_f32_16x16x32_f16 v[46:49], v[42:45], v[150:153], v[122:125]
	v_mfma_f32_16x16x32_f16 v[4:7], v[42:45], v[154:157], v[4:7]
	v_mfma_f32_16x16x32_f16 v[8:11], v[38:41], v[142:145], v[8:11]
	v_mfma_f32_16x16x32_f16 v[26:29], v[38:41], v[146:149], v[26:29]
	v_mfma_f32_16x16x32_f16 v[42:45], v[38:41], v[150:153], v[94:97]
	v_mfma_f32_16x16x32_f16 v[0:3], v[38:41], v[154:157], v[0:3]
	ds_read_b128 v[38:41], v76
	s_nop 0
	ds_read_b128 v[94:97], v76 offset:8192
	ds_read_b128 v[122:125], v76 offset:16384
	ds_read_b128 v[142:145], v76 offset:24576
	s_waitcnt vmcnt(17) lgkmcnt(3)
	v_mfma_f32_16x16x32_f16 v[98:101], v[82:85], v[38:41], v[98:101]
	s_waitcnt lgkmcnt(2)
	v_mfma_f32_16x16x32_f16 v[114:117], v[82:85], v[94:97], v[114:117]
	s_waitcnt lgkmcnt(1)
	v_mfma_f32_16x16x32_f16 v[118:121], v[82:85], v[122:125], v[118:121]
	s_waitcnt lgkmcnt(0)
	v_mfma_f32_16x16x32_f16 v[12:15], v[82:85], v[142:145], v[12:15]
	s_waitcnt vmcnt(16)
	v_mfma_f32_16x16x32_f16 v[16:19], v[86:89], v[38:41], v[16:19]
	v_mfma_f32_16x16x32_f16 v[34:37], v[86:89], v[94:97], v[34:37]
	v_mfma_f32_16x16x32_f16 v[46:49], v[86:89], v[122:125], v[46:49]
	v_mfma_f32_16x16x32_f16 v[4:7], v[86:89], v[142:145], v[4:7]
	s_waitcnt vmcnt(15)
	v_mfma_f32_16x16x32_f16 v[8:11], v[90:93], v[38:41], v[8:11]
	v_mfma_f32_16x16x32_f16 v[26:29], v[90:93], v[94:97], v[26:29]
	v_mfma_f32_16x16x32_f16 v[38:41], v[90:93], v[122:125], v[42:45]
	v_mfma_f32_16x16x32_f16 v[0:3], v[90:93], v[142:145], v[0:3]
	s_nop 1
	ds_read_b128 v[42:45], v77
	ds_read_b128 v[82:85], v77 offset:8192
	ds_read_b128 v[86:89], v77 offset:16384
	ds_read_b128 v[74:77], v77 offset:24576
	s_waitcnt vmcnt(7) lgkmcnt(3)
	v_mfma_f32_16x16x32_f16 v[90:93], v[134:137], v[42:45], v[98:101]
	s_waitcnt lgkmcnt(2)
	v_mfma_f32_16x16x32_f16 v[94:97], v[134:137], v[82:85], v[114:117]
	s_waitcnt lgkmcnt(1)
	v_mfma_f32_16x16x32_f16 v[98:101], v[134:137], v[86:89], v[118:121]
	s_waitcnt lgkmcnt(0)
	v_mfma_f32_16x16x32_f16 v[12:15], v[134:137], v[74:77], v[12:15]
	v_mfma_f32_16x16x32_f16 v[16:19], v[110:113], v[42:45], v[16:19]
	v_mfma_f32_16x16x32_f16 v[34:37], v[110:113], v[82:85], v[34:37]
	v_mfma_f32_16x16x32_f16 v[46:49], v[110:113], v[86:89], v[46:49]
	v_mfma_f32_16x16x32_f16 v[4:7], v[110:113], v[74:77], v[4:7]
	s_waitcnt vmcnt(6)
	v_mfma_f32_16x16x32_f16 v[8:11], v[138:141], v[42:45], v[8:11]
	v_mfma_f32_16x16x32_f16 v[26:29], v[138:141], v[82:85], v[26:29]
	v_mfma_f32_16x16x32_f16 v[38:41], v[138:141], v[86:89], v[38:41]
	v_mfma_f32_16x16x32_f16 v[0:3], v[138:141], v[74:77], v[0:3]
	ds_read_b128 v[42:45], v78
	ds_read_b128 v[74:77], v78 offset:8192
	ds_read_b128 v[82:85], v78 offset:16384
	ds_read_b128 v[86:89], v78 offset:24576
	s_waitcnt vmcnt(5) lgkmcnt(3)
	v_mfma_f32_16x16x32_f16 v[90:93], v[22:25], v[42:45], v[90:93]
	s_waitcnt lgkmcnt(2)
	v_mfma_f32_16x16x32_f16 v[94:97], v[22:25], v[74:77], v[94:97]
	s_waitcnt lgkmcnt(1)
	v_mfma_f32_16x16x32_f16 v[98:101], v[22:25], v[82:85], v[98:101]
	s_waitcnt lgkmcnt(0)
	v_mfma_f32_16x16x32_f16 v[12:15], v[22:25], v[86:89], v[12:15]
	s_waitcnt vmcnt(4)
	v_mfma_f32_16x16x32_f16 v[16:19], v[106:109], v[42:45], v[16:19]
	v_mfma_f32_16x16x32_f16 v[20:23], v[106:109], v[74:77], v[34:37]
	v_mfma_f32_16x16x32_f16 v[34:37], v[106:109], v[82:85], v[46:49]
	v_mfma_f32_16x16x32_f16 v[4:7], v[106:109], v[86:89], v[4:7]
	s_waitcnt vmcnt(3)
	v_mfma_f32_16x16x32_f16 v[8:11], v[130:133], v[42:45], v[8:11]
	v_mfma_f32_16x16x32_f16 v[24:27], v[130:133], v[74:77], v[26:29]
	v_mfma_f32_16x16x32_f16 v[38:41], v[130:133], v[82:85], v[38:41]
	v_mfma_f32_16x16x32_f16 v[0:3], v[130:133], v[86:89], v[0:3]
	ds_read_b128 v[42:45], v79
	ds_read_b128 v[46:49], v79 offset:8192
	ds_read_b128 v[74:77], v79 offset:16384
	ds_read_b128 v[82:85], v79 offset:24576
	s_waitcnt vmcnt(2) lgkmcnt(3)
	v_mfma_f32_16x16x32_f16 v[86:89], v[30:33], v[42:45], v[90:93]
	s_waitcnt lgkmcnt(2)
	v_mfma_f32_16x16x32_f16 v[90:93], v[30:33], v[46:49], v[94:97]
	s_waitcnt lgkmcnt(1)
	v_mfma_f32_16x16x32_f16 v[94:97], v[30:33], v[74:77], v[98:101]
	s_waitcnt lgkmcnt(0)
	v_mfma_f32_16x16x32_f16 v[12:15], v[30:33], v[82:85], v[12:15]
	s_waitcnt vmcnt(1)
	v_mfma_f32_16x16x32_f16 v[16:19], v[102:105], v[42:45], v[16:19]
	v_mfma_f32_16x16x32_f16 v[20:23], v[102:105], v[46:49], v[20:23]
	v_mfma_f32_16x16x32_f16 v[28:31], v[102:105], v[74:77], v[34:37]
	v_mfma_f32_16x16x32_f16 v[4:7], v[102:105], v[82:85], v[4:7]
	s_waitcnt vmcnt(0)
	v_mfma_f32_16x16x32_f16 v[8:11], v[126:129], v[42:45], v[8:11]
	v_mfma_f32_16x16x32_f16 v[24:27], v[126:129], v[46:49], v[24:27]
	v_mfma_f32_16x16x32_f16 v[32:35], v[126:129], v[74:77], v[38:41]
	v_mfma_f32_16x16x32_f16 v[0:3], v[126:129], v[82:85], v[0:3]
	s_nop 1
	global_load_dwordx4 v[36:39], v[56:57], off offset:1536
	global_load_dwordx4 v[40:43], v[56:57], off offset:1600
	global_load_dwordx4 v[44:47], v[56:57], off offset:1664
	v_mov_b32_e32 v58, v21
	v_mov_b32_e32 v59, v22
	v_mov_b32_e32 v74, v29
	v_mov_b32_e32 v56, v13
	v_mov_b32_e32 v57, v14
	v_mov_b32_e32 v75, v30
	v_mov_b32_e32 v48, v91
	v_mov_b32_e32 v49, v92
	v_mov_b32_e32 v54, v95
	v_mov_b32_e32 v55, v96
	v_mov_b32_e32 v76, v5
	v_mov_b32_e32 v77, v6
	s_barrier
	s_waitcnt vmcnt(2)
	v_pk_add_f32 v[78:79], v[86:87], v[36:37]
	v_pk_add_f32 v[82:83], v[88:89], v[38:39]
	v_add_f32_e32 v21, v90, v36
	v_pk_mov_b32 v[84:85], v[36:37], v[38:39] op_sel:[1,0]
	v_add_f32_e32 v22, v93, v39
	v_add_f32_e32 v29, v94, v36
	v_add_f32_e32 v36, v12, v36
	v_add_f32_e32 v37, v15, v39
	s_waitcnt vmcnt(1)
	v_add_f32_e32 v38, v20, v40
	v_add_f32_e32 v23, v23, v43
	v_add_f32_e32 v30, v97, v39
	v_pk_add_f32 v[12:13], v[16:17], v[40:41]
	v_pk_add_f32 v[14:15], v[18:19], v[42:43]
	v_pk_mov_b32 v[16:17], v[40:41], v[42:43] op_sel:[1,0]
	v_add_f32_e32 v28, v28, v40
	v_add_f32_e32 v31, v31, v43
	v_add_f32_e32 v39, v4, v40
	v_add_f32_e32 v40, v7, v43
	v_cvt_f16_f32_e32 v41, v21
	v_cvt_f16_f32_e32 v42, v22
	v_cvt_f16_f32_e32 v36, v36
	v_cvt_f16_f32_e32 v37, v37
	v_cvt_f16_f32_e32 v38, v38
	v_cvt_f16_f32_e32 v43, v23
	v_cvt_f16_f32_e32 v29, v29
	v_cvt_f16_f32_e32 v30, v30
	v_cvt_f16_f32_e32 v28, v28
	v_cvt_f16_f32_e32 v31, v31
	v_cvt_f16_f32_e32 v39, v39
	v_cvt_f16_f32_e32 v40, v40
	s_waitcnt vmcnt(0)
	v_pk_add_f32 v[4:5], v[8:9], v[44:45]
	v_pk_add_f32 v[6:7], v[10:11], v[46:47]
	v_pk_add_f32 v[10:11], v[48:49], v[84:85]
	v_pk_add_f32 v[20:21], v[56:57], v[84:85]
	v_cvt_pk_f16_f32 v12, v12, v13
	v_cvt_pk_f16_f32 v13, v14, v15
	v_pk_add_f32 v[14:15], v[58:59], v[16:17]
	v_cvt_pk_f16_f32 v8, v78, v79
	v_cvt_pk_f16_f32 v9, v82, v83
	v_pk_add_f32 v[18:19], v[54:55], v[84:85]
	v_pk_add_f32 v[22:23], v[74:75], v[16:17]
	v_pk_add_f32 v[16:17], v[76:77], v[16:17]
	v_cvt_pk_f16_f32 v4, v4, v5
	v_cvt_pk_f16_f32 v5, v6, v7
	v_cvt_pk_f16_f32 v6, v10, v11
	v_cvt_pk_f16_f32 v10, v20, v21
	v_cvt_pk_f16_f32 v11, v14, v15
	v_cvt_pk_f16_f32 v7, v18, v19
	v_cvt_pk_f16_f32 v14, v22, v23
	v_cvt_pk_f16_f32 v15, v16, v17
	ds_write2_b64 v73, v[8:9], v[12:13] offset1:4
	ds_write_b64 v69, v[4:5] offset:32832
	v_pack_b32_f16 v4, v41, v6
	v_alignbit_b32 v5, v42, v6, 16
	v_pack_b32_f16 v8, v36, v10
	v_alignbit_b32 v9, v37, v10, 16
	v_pack_b32_f16 v10, v38, v11
	v_alignbit_b32 v11, v43, v11, 16
	v_add_f32_e32 v24, v24, v44
	v_pack_b32_f16 v6, v29, v7
	v_alignbit_b32 v7, v30, v7, 16
	v_pack_b32_f16 v12, v28, v14
	v_alignbit_b32 v13, v31, v14, 16
	v_pack_b32_f16 v14, v39, v15
	v_alignbit_b32 v15, v40, v15, 16
	ds_write2_b64 v70, v[4:5], v[10:11] offset0:32 offset1:36
	ds_write2_b64 v71, v[6:7], v[12:13] offset0:64 offset1:68
	ds_write2_b64 v80, v[8:9], v[14:15] offset1:4
	v_add_f32_e32 v8, v27, v47
	v_cvt_f16_f32_e32 v24, v24
	v_cvt_f16_f32_e32 v8, v8
	v_mov_b32_e32 v4, v25
	v_mov_b32_e32 v5, v26
	v_pk_mov_b32 v[6:7], v[44:45], v[46:47] op_sel:[1,0]
	v_add_f32_e32 v9, v35, v47
	v_pk_add_f32 v[4:5], v[4:5], v[6:7]
	v_cvt_f16_f32_e32 v9, v9
	v_cvt_pk_f16_f32 v5, v4, v5
	v_pack_b32_f16 v4, v24, v5
	v_alignbit_b32 v5, v8, v5, 16
	ds_write_b64 v69, v[4:5] offset:45376
	v_add_f32_e32 v4, v32, v44
	v_cvt_f16_f32_e32 v8, v4
	v_mov_b32_e32 v4, v33
	v_mov_b32_e32 v5, v34
	v_pk_add_f32 v[4:5], v[4:5], v[6:7]
	v_add_f32_e32 v0, v0, v44
	v_cvt_pk_f16_f32 v5, v4, v5
	v_pack_b32_f16 v4, v8, v5
	v_alignbit_b32 v5, v9, v5, 16
	ds_write_b64 v69, v[4:5] offset:57920
	v_cvt_f16_f32_e32 v4, v0
	v_mov_b32_e32 v0, v1
	v_mov_b32_e32 v1, v2
	v_add_f32_e32 v2, v3, v47
	v_cvt_f16_f32_e32 v2, v2
	v_pk_add_f32 v[0:1], v[0:1], v[6:7]
	s_nop 0
	v_cvt_pk_f16_f32 v1, v0, v1
	v_pack_b32_f16 v0, v4, v1
	v_alignbit_b32 v1, v2, v1, 16
	ds_write_b64 v68, v[0:1] offset:32832
	s_waitcnt lgkmcnt(0)
	s_barrier
	ds_read_b128 v[0:3], v51 offset:32768
	ds_read_b128 v[4:7], v81 offset:32768
	s_waitcnt lgkmcnt(1)
	buffer_store_dwordx4 v[0:3], v50, s[24:27], 0 offen offset:768 sc1
	ds_read_b128 v[0:3], v53 offset:32768
	ds_read_b128 v[8:11], v160 offset:32768
	ds_read_b128 v[12:15], v61 offset:32768
	ds_read_b128 v[16:19], v63 offset:32768
	s_waitcnt lgkmcnt(4)
	buffer_store_dwordx4 v[4:7], v52, s[24:27], 0 offen offset:768 sc1
	s_waitcnt lgkmcnt(3)
	buffer_store_dwordx4 v[0:3], v60, s[24:27], 0 offen offset:768 sc1
	s_waitcnt lgkmcnt(2)
	buffer_store_dwordx4 v[8:11], v62, s[24:27], 0 offen offset:768 sc1
	s_waitcnt lgkmcnt(1)
	buffer_store_dwordx4 v[12:15], v64, s[24:27], 0 offen offset:768 sc1
	s_waitcnt lgkmcnt(0)
	buffer_store_dwordx4 v[16:19], v66, s[24:27], 0 offen offset:768 sc1
	s_endpgm
	.p2alignl 8, 3212836864

	.amdhsa_kernel _Z7k_stageILi1ELi4EEv8AttnArgsPKDF16_PKfPDF16_iii
		.amdhsa_group_segment_fixed_size 82944
		.amdhsa_private_segment_fixed_size 0
		.amdhsa_kernarg_size 148
		.amdhsa_user_sgpr_count 2
		.amdhsa_user_sgpr_dispatch_ptr 0
		.amdhsa_user_sgpr_queue_ptr 0
		.amdhsa_user_sgpr_kernarg_segment_ptr 1
		.amdhsa_user_sgpr_dispatch_id 0
		.amdhsa_user_sgpr_kernarg_preload_length 0
		.amdhsa_user_sgpr_kernarg_preload_offset 0
		.amdhsa_user_sgpr_private_segment_size 0
		.amdhsa_uses_dynamic_stack 0
		.amdhsa_enable_private_segment 0
		.amdhsa_system_sgpr_workgroup_id_x 1
		.amdhsa_system_sgpr_workgroup_id_y 0
		.amdhsa_system_sgpr_workgroup_id_z 0
		.amdhsa_system_sgpr_workgroup_info 0
		.amdhsa_system_vgpr_workitem_id 0
		.amdhsa_next_free_vgpr 247
		.amdhsa_next_free_sgpr 96
		.amdhsa_accum_offset 248
		.amdhsa_reserve_vcc 1
		.amdhsa_float_round_mode_32 0
		.amdhsa_float_round_mode_16_64 0
		.amdhsa_float_denorm_mode_32 3
		.amdhsa_float_denorm_mode_16_64 3
		.amdhsa_dx10_clamp 1
		.amdhsa_ieee_mode 1
		.amdhsa_fp16_overflow 0
		.amdhsa_tg_split 0
		.amdhsa_exception_fp_ieee_invalid_op 0
		.amdhsa_exception_fp_denorm_src 0
		.amdhsa_exception_fp_ieee_div_zero 0
		.amdhsa_exception_fp_ieee_overflow 0
		.amdhsa_exception_fp_ieee_underflow 0
		.amdhsa_exception_fp_ieee_inexact 0
		.amdhsa_exception_int_div_zero 0
	.end_amdhsa_kernel

.LBB5_2:
	s_waitcnt lgkmcnt(0)
	v_cvt_f16_f32_e32 v180, s7
	v_cvt_f16_f32_e32 v182, s6
	v_cvt_f16_f32_e32 v181, s28
	s_waitcnt vmcnt(18)
	v_pk_mul_f16 v183, v182, v184 op_sel_hi:[0,1]
	v_pk_mul_f16 v190, v182, v187 op_sel_hi:[0,1]
	v_pk_mul_f16 v194, v180, v187 op_sel_hi:[0,1]
	v_pk_mul_f16 v198, v181, v187 op_sel_hi:[0,1]
	v_pk_mul_f16 v188, v182, v185 op_sel_hi:[0,1]
	v_pk_mul_f16 v189, v182, v186 op_sel_hi:[0,1]
	v_pk_mul_f16 v191, v180, v184 op_sel_hi:[0,1]
	v_pk_mul_f16 v192, v180, v185 op_sel_hi:[0,1]
	v_pk_mul_f16 v193, v180, v186 op_sel_hi:[0,1]
	v_pk_mul_f16 v195, v181, v184 op_sel_hi:[0,1]
	v_pk_mul_f16 v196, v181, v185 op_sel_hi:[0,1]
	v_pk_mul_f16 v197, v181, v186 op_sel_hi:[0,1]
	v_pk_fma_f16 v113, v113, v187, v190
	v_pk_fma_f16 v110, v110, v184, v183
	v_pk_fma_f16 v129, v129, v187, v190
	v_pk_fma_f16 v126, v126, v184, v183
	v_pk_fma_f16 v137, v137, v187, v190
	v_pk_fma_f16 v134, v134, v184, v183
	v_pk_fma_f16 v183, v85, v187, v194
	v_pk_fma_f16 v199, v109, v187, v194
	v_pk_fma_f16 v194, v125, v187, v194
	v_pk_fma_f16 v203, v53, v187, v198
	v_pk_fma_f16 v207, v69, v187, v198
	v_pk_fma_f16 v187, v97, v187, v198
	v_pk_maximum3_f16 v198, v113, v129, v137
	v_pk_fma_f16 v112, v112, v186, v189
	v_pk_fma_f16 v111, v111, v185, v188
	v_pk_fma_f16 v128, v128, v186, v189
	v_pk_fma_f16 v127, v127, v185, v188
	v_pk_fma_f16 v136, v136, v186, v189
	v_pk_fma_f16 v135, v135, v185, v188
	v_pk_fma_f16 v188, v84, v186, v193
	v_pk_fma_f16 v189, v83, v185, v192
	v_pk_fma_f16 v190, v82, v184, v191
	v_pk_fma_f16 v200, v108, v186, v193
	v_pk_fma_f16 v201, v107, v185, v192
	v_pk_fma_f16 v202, v106, v184, v191
	v_pk_fma_f16 v193, v124, v186, v193
	v_pk_fma_f16 v192, v123, v185, v192
	v_pk_fma_f16 v191, v122, v184, v191
	v_pk_fma_f16 v204, v52, v186, v197
	v_pk_fma_f16 v205, v51, v185, v196
	v_pk_fma_f16 v206, v50, v184, v195
	v_pk_fma_f16 v208, v68, v186, v197
	v_pk_fma_f16 v209, v67, v185, v196
	v_pk_fma_f16 v210, v66, v184, v195
	v_pk_fma_f16 v186, v96, v186, v197
	v_pk_fma_f16 v185, v95, v185, v196
	v_pk_fma_f16 v184, v94, v184, v195
	v_pk_maximum3_f16 v195, v110, v126, v134
	v_pk_maximum3_f16 v196, v111, v127, v135
	v_pk_maximum3_f16 v197, v112, v128, v136
	v_pk_maximum3_f16 v214, v183, v199, v194
	v_pk_maximum3_f16 v218, v203, v207, v187
	v_pk_maximum3_f16 v211, v190, v202, v191
	v_pk_maximum3_f16 v212, v189, v201, v192
	v_pk_maximum3_f16 v213, v188, v200, v193
	s_nop 0
	v_pk_maximum3_f16 v215, v206, v210, v184
	v_pk_maximum3_f16 v216, v205, v209, v185
	v_pk_maximum3_f16 v198, v198, v214, v218
	v_pk_maximum3_f16 v217, v204, v208, v186
	s_nop 0
	v_pk_maximum3_f16 v195, v195, v211, v215
	v_pk_maximum3_f16 v196, v196, v212, v216
	v_pk_maximum3_f16 v197, v197, v213, v217
	v_xor_b32_e32 v198, 0x80008000, v198
	v_xor_b32_e32 v197, 0x80008000, v197
	v_xor_b32_e32 v196, 0x80008000, v196
	v_xor_b32_e32 v195, 0x80008000, v195
	v_pk_add_f16 v113, v113, v198
	v_pk_add_f16 v110, v110, v195
	v_pk_add_f16 v111, v111, v196
	v_pk_add_f16 v112, v112, v197
	v_pk_add_f16 v126, v126, v195
	v_exp_f16_sdwa v211, v110 dst_sel:WORD_0 dst_unused:UNUSED_PAD src0_sel:WORD_0
	v_exp_f16_sdwa v212, v111 dst_sel:WORD_0 dst_unused:UNUSED_PAD src0_sel:WORD_0
	v_exp_f16_sdwa v213, v112 dst_sel:WORD_0 dst_unused:UNUSED_PAD src0_sel:WORD_0
	v_exp_f16_sdwa v214, v113 dst_sel:WORD_0 dst_unused:UNUSED_PAD src0_sel:WORD_0
	v_exp_f16_sdwa v211, v110 dst_sel:WORD_1 dst_unused:UNUSED_PRESERVE src0_sel:WORD_1
	v_exp_f16_sdwa v212, v111 dst_sel:WORD_1 dst_unused:UNUSED_PRESERVE src0_sel:WORD_1
	v_exp_f16_sdwa v213, v112 dst_sel:WORD_1 dst_unused:UNUSED_PRESERVE src0_sel:WORD_1
	v_exp_f16_sdwa v214, v113 dst_sel:WORD_1 dst_unused:UNUSED_PRESERVE src0_sel:WORD_1
	s_nop 0
	v_pk_add_f16 v127, v127, v196
	v_pk_add_f16 v113, v211, 0
	v_pk_fma_f16 v81, v81, v214, 0
	v_pk_add_f16 v110, v214, 0
	v_pk_add_f16 v111, v213, 0
	v_pk_add_f16 v112, v212, 0
	v_pk_fma_f16 v80, v80, v213, 0
	v_pk_fma_f16 v79, v79, v212, 0
	v_pk_fma_f16 v78, v78, v211, 0
	v_pk_add_f16 v128, v128, v197
	v_pk_add_f16 v129, v129, v198
	s_nop 0
	v_exp_f16_sdwa v211, v126 dst_sel:WORD_0 dst_unused:UNUSED_PAD src0_sel:WORD_0
	v_exp_f16_sdwa v212, v127 dst_sel:WORD_0 dst_unused:UNUSED_PAD src0_sel:WORD_0
	v_exp_f16_sdwa v213, v128 dst_sel:WORD_0 dst_unused:UNUSED_PAD src0_sel:WORD_0
	v_exp_f16_sdwa v214, v129 dst_sel:WORD_0 dst_unused:UNUSED_PAD src0_sel:WORD_0
	v_exp_f16_sdwa v211, v126 dst_sel:WORD_1 dst_unused:UNUSED_PRESERVE src0_sel:WORD_1
	v_exp_f16_sdwa v212, v127 dst_sel:WORD_1 dst_unused:UNUSED_PRESERVE src0_sel:WORD_1
	v_exp_f16_sdwa v213, v128 dst_sel:WORD_1 dst_unused:UNUSED_PRESERVE src0_sel:WORD_1
	v_exp_f16_sdwa v214, v129 dst_sel:WORD_1 dst_unused:UNUSED_PRESERVE src0_sel:WORD_1
	s_nop 0
	s_nop 0
	v_pk_add_f16 v113, v113, v211
	v_pk_fma_f16 v81, v105, v214, v81
	v_pk_add_f16 v105, v137, v198
	v_pk_add_f16 v112, v112, v212
	v_pk_add_f16 v111, v111, v213
	v_pk_add_f16 v110, v110, v214
	v_pk_fma_f16 v78, v102, v211, v78
	v_pk_fma_f16 v79, v103, v212, v79
	v_pk_fma_f16 v80, v104, v213, v80
	v_pk_add_f16 v102, v134, v195
	v_pk_add_f16 v103, v135, v196
	v_pk_add_f16 v104, v136, v197
	s_nop 0
	v_exp_f16_sdwa v126, v102 dst_sel:WORD_0 dst_unused:UNUSED_PAD src0_sel:WORD_0
	v_exp_f16_sdwa v127, v103 dst_sel:WORD_0 dst_unused:UNUSED_PAD src0_sel:WORD_0
	v_exp_f16_sdwa v128, v104 dst_sel:WORD_0 dst_unused:UNUSED_PAD src0_sel:WORD_0
	v_exp_f16_sdwa v129, v105 dst_sel:WORD_0 dst_unused:UNUSED_PAD src0_sel:WORD_0
	v_exp_f16_sdwa v126, v102 dst_sel:WORD_1 dst_unused:UNUSED_PRESERVE src0_sel:WORD_1
	v_exp_f16_sdwa v127, v103 dst_sel:WORD_1 dst_unused:UNUSED_PRESERVE src0_sel:WORD_1
	v_exp_f16_sdwa v128, v104 dst_sel:WORD_1 dst_unused:UNUSED_PRESERVE src0_sel:WORD_1
	v_exp_f16_sdwa v129, v105 dst_sel:WORD_1 dst_unused:UNUSED_PRESERVE src0_sel:WORD_1
	s_nop 0
	s_nop 0
	v_pk_add_f16 v105, v113, v126
	v_pk_add_f16 v102, v110, v129
	v_pk_add_f16 v103, v111, v128
	v_pk_add_f16 v104, v112, v127
	v_pk_fma_f16 v81, v117, v129, v81
	v_pk_fma_f16 v80, v116, v128, v80
	v_pk_fma_f16 v79, v115, v127, v79
	v_pk_fma_f16 v78, v114, v126, v78
	v_pk_add_f16 v110, v190, v195
	v_pk_add_f16 v111, v189, v196
	v_pk_add_f16 v112, v188, v197
	v_pk_add_f16 v113, v183, v198
	s_nop 0
	v_exp_f16_sdwa v114, v110 dst_sel:WORD_0 dst_unused:UNUSED_PAD src0_sel:WORD_0
	v_exp_f16_sdwa v115, v111 dst_sel:WORD_0 dst_unused:UNUSED_PAD src0_sel:WORD_0
	v_exp_f16_sdwa v116, v112 dst_sel:WORD_0 dst_unused:UNUSED_PAD src0_sel:WORD_0
	v_exp_f16_sdwa v117, v113 dst_sel:WORD_0 dst_unused:UNUSED_PAD src0_sel:WORD_0
	v_exp_f16_sdwa v114, v110 dst_sel:WORD_1 dst_unused:UNUSED_PRESERVE src0_sel:WORD_1
	v_exp_f16_sdwa v115, v111 dst_sel:WORD_1 dst_unused:UNUSED_PRESERVE src0_sel:WORD_1
	v_exp_f16_sdwa v116, v112 dst_sel:WORD_1 dst_unused:UNUSED_PRESERVE src0_sel:WORD_1
	v_exp_f16_sdwa v117, v113 dst_sel:WORD_1 dst_unused:UNUSED_PRESERVE src0_sel:WORD_1
	s_nop 0
	v_pk_add_f16 v110, v202, v195
	v_pk_add_f16 v105, v105, v114
	v_pk_add_f16 v104, v104, v115
	v_pk_add_f16 v103, v103, v116
	v_pk_add_f16 v102, v102, v117
	v_pk_fma_f16 v78, v42, v114, v78
	v_pk_fma_f16 v79, v43, v115, v79
	v_pk_fma_f16 v80, v44, v116, v80
	v_pk_fma_f16 v81, v45, v117, v81
	v_pk_add_f16 v111, v201, v196
	v_pk_add_f16 v112, v200, v197
	v_pk_add_f16 v113, v199, v198
	s_nop 0
	v_exp_f16_sdwa v114, v110 dst_sel:WORD_0 dst_unused:UNUSED_PAD src0_sel:WORD_0
	v_exp_f16_sdwa v115, v111 dst_sel:WORD_0 dst_unused:UNUSED_PAD src0_sel:WORD_0
	v_exp_f16_sdwa v116, v112 dst_sel:WORD_0 dst_unused:UNUSED_PAD src0_sel:WORD_0
	v_exp_f16_sdwa v117, v113 dst_sel:WORD_0 dst_unused:UNUSED_PAD src0_sel:WORD_0
	v_exp_f16_sdwa v114, v110 dst_sel:WORD_1 dst_unused:UNUSED_PRESERVE src0_sel:WORD_1
	v_exp_f16_sdwa v115, v111 dst_sel:WORD_1 dst_unused:UNUSED_PRESERVE src0_sel:WORD_1
	v_exp_f16_sdwa v116, v112 dst_sel:WORD_1 dst_unused:UNUSED_PRESERVE src0_sel:WORD_1
	v_exp_f16_sdwa v117, v113 dst_sel:WORD_1 dst_unused:UNUSED_PRESERVE src0_sel:WORD_1
	s_nop 0
	v_pk_add_f16 v110, v191, v195
	v_pk_add_f16 v105, v105, v114
	v_pk_add_f16 v102, v102, v117
	v_pk_add_f16 v103, v103, v116
	v_pk_add_f16 v104, v104, v115
	v_pk_fma_f16 v81, v65, v117, v81
	v_pk_fma_f16 v80, v64, v116, v80
	v_pk_fma_f16 v79, v63, v115, v79
	v_pk_fma_f16 v78, v62, v114, v78
	v_pk_add_f16 v111, v192, v196
	v_pk_add_f16 v112, v193, v197
	v_pk_add_f16 v113, v194, v198
	s_nop 0
	v_exp_f16_sdwa v114, v110 dst_sel:WORD_0 dst_unused:UNUSED_PAD src0_sel:WORD_0
	v_exp_f16_sdwa v115, v111 dst_sel:WORD_0 dst_unused:UNUSED_PAD src0_sel:WORD_0
	v_exp_f16_sdwa v116, v112 dst_sel:WORD_0 dst_unused:UNUSED_PAD src0_sel:WORD_0
	v_exp_f16_sdwa v117, v113 dst_sel:WORD_0 dst_unused:UNUSED_PAD src0_sel:WORD_0
	v_exp_f16_sdwa v114, v110 dst_sel:WORD_1 dst_unused:UNUSED_PRESERVE src0_sel:WORD_1
	v_exp_f16_sdwa v115, v111 dst_sel:WORD_1 dst_unused:UNUSED_PRESERVE src0_sel:WORD_1
	v_exp_f16_sdwa v116, v112 dst_sel:WORD_1 dst_unused:UNUSED_PRESERVE src0_sel:WORD_1
	v_exp_f16_sdwa v117, v113 dst_sel:WORD_1 dst_unused:UNUSED_PRESERVE src0_sel:WORD_1
	s_nop 0
	v_pk_add_f16 v110, v206, v195
	v_pk_add_f16 v105, v105, v114
	v_pk_add_f16 v104, v104, v115
	v_pk_add_f16 v103, v103, v116
	v_pk_add_f16 v102, v102, v117
	v_pk_fma_f16 v78, v86, v114, v78
	v_pk_fma_f16 v79, v87, v115, v79
	v_pk_fma_f16 v80, v88, v116, v80
	v_pk_fma_f16 v81, v89, v117, v81
	v_pk_add_f16 v111, v205, v196
	v_pk_add_f16 v112, v204, v197
	v_pk_add_f16 v113, v203, v198
	s_nop 0
	v_exp_f16_sdwa v114, v110 dst_sel:WORD_0 dst_unused:UNUSED_PAD src0_sel:WORD_0
	v_exp_f16_sdwa v115, v111 dst_sel:WORD_0 dst_unused:UNUSED_PAD src0_sel:WORD_0
	v_exp_f16_sdwa v116, v112 dst_sel:WORD_0 dst_unused:UNUSED_PAD src0_sel:WORD_0
	v_exp_f16_sdwa v117, v113 dst_sel:WORD_0 dst_unused:UNUSED_PAD src0_sel:WORD_0
	v_exp_f16_sdwa v114, v110 dst_sel:WORD_1 dst_unused:UNUSED_PRESERVE src0_sel:WORD_1
	v_exp_f16_sdwa v115, v111 dst_sel:WORD_1 dst_unused:UNUSED_PRESERVE src0_sel:WORD_1
	v_exp_f16_sdwa v116, v112 dst_sel:WORD_1 dst_unused:UNUSED_PRESERVE src0_sel:WORD_1
	v_exp_f16_sdwa v117, v113 dst_sel:WORD_1 dst_unused:UNUSED_PRESERVE src0_sel:WORD_1
	s_nop 0
	v_pk_add_f16 v110, v210, v195
	v_pk_add_f16 v105, v105, v114
	v_pk_add_f16 v102, v102, v117
	v_pk_add_f16 v103, v103, v116
	v_pk_add_f16 v104, v104, v115
	v_pk_fma_f16 v81, v25, v117, v81
	v_pk_fma_f16 v80, v24, v116, v80
	v_pk_fma_f16 v79, v23, v115, v79
	v_pk_fma_f16 v78, v22, v114, v78
	v_pk_add_f16 v111, v209, v196
	v_pk_add_f16 v112, v208, v197
	v_pk_add_f16 v113, v207, v198
	s_nop 0
	v_exp_f16_sdwa v114, v110 dst_sel:WORD_0 dst_unused:UNUSED_PAD src0_sel:WORD_0
	v_exp_f16_sdwa v115, v111 dst_sel:WORD_0 dst_unused:UNUSED_PAD src0_sel:WORD_0
	v_exp_f16_sdwa v116, v112 dst_sel:WORD_0 dst_unused:UNUSED_PAD src0_sel:WORD_0
	v_exp_f16_sdwa v117, v113 dst_sel:WORD_0 dst_unused:UNUSED_PAD src0_sel:WORD_0
	v_exp_f16_sdwa v114, v110 dst_sel:WORD_1 dst_unused:UNUSED_PRESERVE src0_sel:WORD_1
	v_exp_f16_sdwa v115, v111 dst_sel:WORD_1 dst_unused:UNUSED_PRESERVE src0_sel:WORD_1
	v_exp_f16_sdwa v116, v112 dst_sel:WORD_1 dst_unused:UNUSED_PRESERVE src0_sel:WORD_1
	v_exp_f16_sdwa v117, v113 dst_sel:WORD_1 dst_unused:UNUSED_PRESERVE src0_sel:WORD_1
	s_nop 0
	v_pk_add_f16 v110, v184, v195
	v_pk_add_f16 v105, v105, v114
	v_pk_add_f16 v104, v104, v115
	v_pk_add_f16 v103, v103, v116
	v_pk_add_f16 v102, v102, v117
	v_pk_fma_f16 v78, v34, v114, v78
	v_pk_fma_f16 v79, v35, v115, v79
	v_pk_fma_f16 v80, v36, v116, v80
	v_pk_fma_f16 v81, v37, v117, v81
	v_pk_add_f16 v111, v185, v196
	v_pk_add_f16 v112, v186, v197
	v_pk_add_f16 v113, v187, v198
	s_nop 0
	v_exp_f16_sdwa v114, v110 dst_sel:WORD_0 dst_unused:UNUSED_PAD src0_sel:WORD_0
	v_exp_f16_sdwa v115, v111 dst_sel:WORD_0 dst_unused:UNUSED_PAD src0_sel:WORD_0
	v_exp_f16_sdwa v116, v112 dst_sel:WORD_0 dst_unused:UNUSED_PAD src0_sel:WORD_0
	v_exp_f16_sdwa v117, v113 dst_sel:WORD_0 dst_unused:UNUSED_PAD src0_sel:WORD_0
	v_exp_f16_sdwa v114, v110 dst_sel:WORD_1 dst_unused:UNUSED_PRESERVE src0_sel:WORD_1
	v_exp_f16_sdwa v115, v111 dst_sel:WORD_1 dst_unused:UNUSED_PRESERVE src0_sel:WORD_1
	v_exp_f16_sdwa v116, v112 dst_sel:WORD_1 dst_unused:UNUSED_PRESERVE src0_sel:WORD_1
	v_exp_f16_sdwa v117, v113 dst_sel:WORD_1 dst_unused:UNUSED_PRESERVE src0_sel:WORD_1
	s_nop 0
	s_nop 0
	v_pk_add_f16 v105, v105, v114
	v_pk_add_f16 v104, v104, v115
	v_rcp_f16_e32 v110, v105
	v_rcp_f16_sdwa v105, v105 dst_sel:DWORD dst_unused:UNUSED_PAD src0_sel:WORD_1
	v_pk_add_f16 v103, v103, v116
	v_rcp_f16_e32 v111, v104
	v_rcp_f16_sdwa v104, v104 dst_sel:DWORD dst_unused:UNUSED_PAD src0_sel:WORD_1
	v_pk_add_f16 v102, v102, v117
	v_rcp_f16_e32 v112, v103
	v_rcp_f16_sdwa v103, v103 dst_sel:DWORD dst_unused:UNUSED_PAD src0_sel:WORD_1
	v_rcp_f16_e32 v113, v102
	v_rcp_f16_sdwa v102, v102 dst_sel:DWORD dst_unused:UNUSED_PAD src0_sel:WORD_1
	v_pk_fma_f16 v78, v46, v114, v78
	v_pack_b32_f16 v105, v110, v105
	v_pk_fma_f16 v79, v47, v115, v79
	v_pk_mul_f16 v110, v78, v105
	v_pack_b32_f16 v78, v111, v104
	v_pk_fma_f16 v80, v48, v116, v80
	v_pk_mul_f16 v111, v79, v78
	v_pack_b32_f16 v78, v112, v103
	v_pk_fma_f16 v81, v49, v117, v81
	v_pk_mul_f16 v112, v80, v78
	v_pack_b32_f16 v78, v113, v102
	v_pk_mul_f16 v113, v81, v78
	s_waitcnt vmcnt(12)
	v_pk_mul_f16 v78, v182, v154 op_sel_hi:[0,1]
	v_pk_mul_f16 v81, v182, v157 op_sel_hi:[0,1]
	v_pk_mul_f16 v102, v180, v154 op_sel_hi:[0,1]
	v_pk_mul_f16 v114, v181, v154 op_sel_hi:[0,1]
	v_pk_mul_f16 v79, v182, v155 op_sel_hi:[0,1]
	v_pk_mul_f16 v80, v182, v156 op_sel_hi:[0,1]
	v_pk_mul_f16 v103, v180, v155 op_sel_hi:[0,1]
	v_pk_mul_f16 v104, v180, v156 op_sel_hi:[0,1]
	v_pk_mul_f16 v105, v180, v157 op_sel_hi:[0,1]
	v_pk_mul_f16 v115, v181, v155 op_sel_hi:[0,1]
	v_pk_mul_f16 v116, v181, v156 op_sel_hi:[0,1]
	v_pk_mul_f16 v117, v181, v157 op_sel_hi:[0,1]
	v_pk_fma_f16 v85, v85, v157, v81
	v_pk_fma_f16 v82, v82, v154, v78
	v_pk_fma_f16 v109, v109, v157, v81
	v_pk_fma_f16 v106, v106, v154, v78
	v_pk_fma_f16 v81, v125, v157, v81
	v_pk_fma_f16 v78, v122, v154, v78
	v_pk_fma_f16 v125, v50, v154, v102
	v_pk_fma_f16 v129, v66, v154, v102
	v_pk_fma_f16 v102, v94, v154, v102
	v_pk_fma_f16 v137, v18, v154, v114
	v_pk_fma_f16 v186, v30, v154, v114
	v_pk_fma_f16 v114, v54, v154, v114
	v_pk_maximum3_f16 v154, v82, v106, v78
	v_pk_fma_f16 v84, v84, v156, v80
	v_pk_fma_f16 v83, v83, v155, v79
	v_pk_fma_f16 v108, v108, v156, v80
	v_pk_fma_f16 v107, v107, v155, v79
	v_pk_fma_f16 v80, v124, v156, v80
	v_pk_fma_f16 v79, v123, v155, v79
	v_pk_fma_f16 v122, v53, v157, v105
	v_pk_fma_f16 v123, v52, v156, v104
	v_pk_fma_f16 v124, v51, v155, v103
	v_pk_fma_f16 v126, v69, v157, v105
	v_pk_fma_f16 v127, v68, v156, v104
	v_pk_fma_f16 v128, v67, v155, v103
	v_pk_fma_f16 v105, v97, v157, v105
	v_pk_fma_f16 v104, v96, v156, v104
	v_pk_fma_f16 v103, v95, v155, v103
	v_pk_fma_f16 v134, v21, v157, v117
	v_pk_fma_f16 v135, v20, v156, v116
	v_pk_fma_f16 v136, v19, v155, v115
	v_pk_fma_f16 v183, v33, v157, v117
	v_pk_fma_f16 v184, v32, v156, v116
	v_pk_fma_f16 v185, v31, v155, v115
	v_pk_fma_f16 v117, v57, v157, v117
	v_pk_fma_f16 v116, v56, v156, v116
	v_pk_fma_f16 v115, v55, v155, v115
	v_pk_maximum3_f16 v155, v83, v107, v79
	v_pk_maximum3_f16 v156, v84, v108, v80
	v_pk_maximum3_f16 v157, v85, v109, v81
	v_pk_maximum3_f16 v187, v125, v129, v102
	v_pk_maximum3_f16 v191, v137, v186, v114
	v_pk_maximum3_f16 v188, v124, v128, v103
	v_pk_maximum3_f16 v189, v123, v127, v104
	v_pk_maximum3_f16 v190, v122, v126, v105
	s_nop 0
	v_pk_maximum3_f16 v192, v136, v185, v115
	v_pk_maximum3_f16 v193, v135, v184, v116
	v_pk_maximum3_f16 v154, v154, v187, v191
	v_pk_maximum3_f16 v194, v134, v183, v117
	s_nop 0
	v_pk_maximum3_f16 v155, v155, v188, v192
	v_pk_maximum3_f16 v156, v156, v189, v193
	v_pk_maximum3_f16 v157, v157, v190, v194
	v_xor_b32_e32 v154, 0x80008000, v154
	v_xor_b32_e32 v157, 0x80008000, v157
	v_xor_b32_e32 v156, 0x80008000, v156
	v_xor_b32_e32 v155, 0x80008000, v155
	v_pk_add_f16 v82, v82, v154
	v_pk_add_f16 v83, v83, v155
	v_pk_add_f16 v84, v84, v156
	v_pk_add_f16 v85, v85, v157
	v_pk_add_f16 v106, v106, v154
	v_exp_f16_sdwa v187, v82 dst_sel:WORD_0 dst_unused:UNUSED_PAD src0_sel:WORD_0
	v_exp_f16_sdwa v188, v83 dst_sel:WORD_0 dst_unused:UNUSED_PAD src0_sel:WORD_0
	v_exp_f16_sdwa v189, v84 dst_sel:WORD_0 dst_unused:UNUSED_PAD src0_sel:WORD_0
	v_exp_f16_sdwa v190, v85 dst_sel:WORD_0 dst_unused:UNUSED_PAD src0_sel:WORD_0
	v_exp_f16_sdwa v187, v82 dst_sel:WORD_1 dst_unused:UNUSED_PRESERVE src0_sel:WORD_1
	v_exp_f16_sdwa v188, v83 dst_sel:WORD_1 dst_unused:UNUSED_PRESERVE src0_sel:WORD_1
	v_exp_f16_sdwa v189, v84 dst_sel:WORD_1 dst_unused:UNUSED_PRESERVE src0_sel:WORD_1
	v_exp_f16_sdwa v190, v85 dst_sel:WORD_1 dst_unused:UNUSED_PRESERVE src0_sel:WORD_1
	s_nop 0
	v_pk_add_f16 v107, v107, v155
	v_pk_add_f16 v82, v190, 0
	v_pk_fma_f16 v42, v42, v187, 0
	v_pk_add_f16 v83, v189, 0
	v_pk_add_f16 v84, v188, 0
	v_pk_add_f16 v85, v187, 0
	v_pk_fma_f16 v45, v45, v190, 0
	v_pk_fma_f16 v44, v44, v189, 0
	v_pk_fma_f16 v43, v43, v188, 0
	v_pk_add_f16 v108, v108, v156
	v_pk_add_f16 v109, v109, v157
	s_nop 0
	v_exp_f16_sdwa v187, v106 dst_sel:WORD_0 dst_unused:UNUSED_PAD src0_sel:WORD_0
	v_exp_f16_sdwa v188, v107 dst_sel:WORD_0 dst_unused:UNUSED_PAD src0_sel:WORD_0
	v_exp_f16_sdwa v189, v108 dst_sel:WORD_0 dst_unused:UNUSED_PAD src0_sel:WORD_0
	v_exp_f16_sdwa v190, v109 dst_sel:WORD_0 dst_unused:UNUSED_PAD src0_sel:WORD_0
	v_exp_f16_sdwa v187, v106 dst_sel:WORD_1 dst_unused:UNUSED_PRESERVE src0_sel:WORD_1
	v_exp_f16_sdwa v188, v107 dst_sel:WORD_1 dst_unused:UNUSED_PRESERVE src0_sel:WORD_1
	v_exp_f16_sdwa v189, v108 dst_sel:WORD_1 dst_unused:UNUSED_PRESERVE src0_sel:WORD_1
	v_exp_f16_sdwa v190, v109 dst_sel:WORD_1 dst_unused:UNUSED_PRESERVE src0_sel:WORD_1
	s_nop 0
	s_nop 0
	v_pk_add_f16 v82, v82, v190
	v_pk_fma_f16 v42, v62, v187, v42
	v_pk_add_f16 v62, v78, v154
	v_pk_add_f16 v85, v85, v187
	v_pk_add_f16 v84, v84, v188
	v_pk_add_f16 v83, v83, v189
	v_pk_fma_f16 v43, v63, v188, v43
	v_pk_fma_f16 v44, v64, v189, v44
	v_pk_fma_f16 v45, v65, v190, v45
	v_pk_add_f16 v63, v79, v155
	v_pk_add_f16 v64, v80, v156
	v_pk_add_f16 v65, v81, v157
	s_nop 0
	v_exp_f16_sdwa v78, v62 dst_sel:WORD_0 dst_unused:UNUSED_PAD src0_sel:WORD_0
	v_exp_f16_sdwa v79, v63 dst_sel:WORD_0 dst_unused:UNUSED_PAD src0_sel:WORD_0
	v_exp_f16_sdwa v80, v64 dst_sel:WORD_0 dst_unused:UNUSED_PAD src0_sel:WORD_0
	v_exp_f16_sdwa v81, v65 dst_sel:WORD_0 dst_unused:UNUSED_PAD src0_sel:WORD_0
	v_exp_f16_sdwa v78, v62 dst_sel:WORD_1 dst_unused:UNUSED_PRESERVE src0_sel:WORD_1
	v_exp_f16_sdwa v79, v63 dst_sel:WORD_1 dst_unused:UNUSED_PRESERVE src0_sel:WORD_1
	v_exp_f16_sdwa v80, v64 dst_sel:WORD_1 dst_unused:UNUSED_PRESERVE src0_sel:WORD_1
	v_exp_f16_sdwa v81, v65 dst_sel:WORD_1 dst_unused:UNUSED_PRESERVE src0_sel:WORD_1
	s_nop 0
	s_nop 0
	v_pk_add_f16 v62, v82, v81
	v_pk_add_f16 v63, v83, v80
	v_pk_add_f16 v64, v84, v79
	v_pk_add_f16 v65, v85, v78
	v_pk_fma_f16 v45, v89, v81, v45
	v_pk_fma_f16 v44, v88, v80, v44
	v_pk_fma_f16 v43, v87, v79, v43
	v_pk_fma_f16 v42, v86, v78, v42
	v_pk_add_f16 v78, v125, v154
	v_pk_add_f16 v79, v124, v155
	v_pk_add_f16 v80, v123, v156
	v_pk_add_f16 v81, v122, v157
	s_nop 0
	v_exp_f16_sdwa v82, v78 dst_sel:WORD_0 dst_unused:UNUSED_PAD src0_sel:WORD_0
	v_exp_f16_sdwa v83, v79 dst_sel:WORD_0 dst_unused:UNUSED_PAD src0_sel:WORD_0
	v_exp_f16_sdwa v84, v80 dst_sel:WORD_0 dst_unused:UNUSED_PAD src0_sel:WORD_0
	v_exp_f16_sdwa v85, v81 dst_sel:WORD_0 dst_unused:UNUSED_PAD src0_sel:WORD_0
	v_exp_f16_sdwa v82, v78 dst_sel:WORD_1 dst_unused:UNUSED_PRESERVE src0_sel:WORD_1
	v_exp_f16_sdwa v83, v79 dst_sel:WORD_1 dst_unused:UNUSED_PRESERVE src0_sel:WORD_1
	v_exp_f16_sdwa v84, v80 dst_sel:WORD_1 dst_unused:UNUSED_PRESERVE src0_sel:WORD_1
	v_exp_f16_sdwa v85, v81 dst_sel:WORD_1 dst_unused:UNUSED_PRESERVE src0_sel:WORD_1
	s_nop 0
	v_pk_add_f16 v78, v129, v154
	v_pk_add_f16 v62, v62, v85
	v_pk_add_f16 v65, v65, v82
	v_pk_add_f16 v64, v64, v83
	v_pk_add_f16 v63, v63, v84
	v_pk_fma_f16 v42, v22, v82, v42
	v_pk_fma_f16 v43, v23, v83, v43
	v_pk_fma_f16 v44, v24, v84, v44
	v_pk_fma_f16 v45, v25, v85, v45
	v_pk_add_f16 v79, v128, v155
	v_pk_add_f16 v80, v127, v156
	v_pk_add_f16 v81, v126, v157
	s_nop 0
	v_exp_f16_sdwa v82, v78 dst_sel:WORD_0 dst_unused:UNUSED_PAD src0_sel:WORD_0
	v_exp_f16_sdwa v83, v79 dst_sel:WORD_0 dst_unused:UNUSED_PAD src0_sel:WORD_0
	v_exp_f16_sdwa v84, v80 dst_sel:WORD_0 dst_unused:UNUSED_PAD src0_sel:WORD_0
	v_exp_f16_sdwa v85, v81 dst_sel:WORD_0 dst_unused:UNUSED_PAD src0_sel:WORD_0
	v_exp_f16_sdwa v82, v78 dst_sel:WORD_1 dst_unused:UNUSED_PRESERVE src0_sel:WORD_1
	v_exp_f16_sdwa v83, v79 dst_sel:WORD_1 dst_unused:UNUSED_PRESERVE src0_sel:WORD_1
	v_exp_f16_sdwa v84, v80 dst_sel:WORD_1 dst_unused:UNUSED_PRESERVE src0_sel:WORD_1
	v_exp_f16_sdwa v85, v81 dst_sel:WORD_1 dst_unused:UNUSED_PRESERVE src0_sel:WORD_1
	s_nop 0
	v_pk_add_f16 v78, v102, v154
	v_pk_add_f16 v62, v62, v85
	v_pk_add_f16 v63, v63, v84
	v_pk_add_f16 v64, v64, v83
	v_pk_add_f16 v65, v65, v82
	v_pk_fma_f16 v45, v37, v85, v45
	v_pk_fma_f16 v44, v36, v84, v44
	v_pk_fma_f16 v43, v35, v83, v43
	v_pk_fma_f16 v42, v34, v82, v42
	v_pk_add_f16 v79, v103, v155
	v_pk_add_f16 v80, v104, v156
	v_pk_add_f16 v81, v105, v157
	s_nop 0
	v_exp_f16_sdwa v82, v78 dst_sel:WORD_0 dst_unused:UNUSED_PAD src0_sel:WORD_0
	v_exp_f16_sdwa v83, v79 dst_sel:WORD_0 dst_unused:UNUSED_PAD src0_sel:WORD_0
	v_exp_f16_sdwa v84, v80 dst_sel:WORD_0 dst_unused:UNUSED_PAD src0_sel:WORD_0
	v_exp_f16_sdwa v85, v81 dst_sel:WORD_0 dst_unused:UNUSED_PAD src0_sel:WORD_0
	v_exp_f16_sdwa v82, v78 dst_sel:WORD_1 dst_unused:UNUSED_PRESERVE src0_sel:WORD_1
	v_exp_f16_sdwa v83, v79 dst_sel:WORD_1 dst_unused:UNUSED_PRESERVE src0_sel:WORD_1
	v_exp_f16_sdwa v84, v80 dst_sel:WORD_1 dst_unused:UNUSED_PRESERVE src0_sel:WORD_1
	v_exp_f16_sdwa v85, v81 dst_sel:WORD_1 dst_unused:UNUSED_PRESERVE src0_sel:WORD_1
	s_nop 0
	v_pk_add_f16 v78, v137, v154
	v_pk_add_f16 v62, v62, v85
	v_pk_add_f16 v65, v65, v82
	v_pk_add_f16 v64, v64, v83
	v_pk_add_f16 v63, v63, v84
	v_pk_fma_f16 v42, v46, v82, v42
	v_pk_fma_f16 v43, v47, v83, v43
	v_pk_fma_f16 v44, v48, v84, v44
	v_pk_fma_f16 v45, v49, v85, v45
	v_pk_add_f16 v79, v136, v155
	v_pk_add_f16 v80, v135, v156
	v_pk_add_f16 v81, v134, v157
	s_nop 0
	v_exp_f16_sdwa v82, v78 dst_sel:WORD_0 dst_unused:UNUSED_PAD src0_sel:WORD_0
	v_exp_f16_sdwa v83, v79 dst_sel:WORD_0 dst_unused:UNUSED_PAD src0_sel:WORD_0
	v_exp_f16_sdwa v84, v80 dst_sel:WORD_0 dst_unused:UNUSED_PAD src0_sel:WORD_0
	v_exp_f16_sdwa v85, v81 dst_sel:WORD_0 dst_unused:UNUSED_PAD src0_sel:WORD_0
	v_exp_f16_sdwa v82, v78 dst_sel:WORD_1 dst_unused:UNUSED_PRESERVE src0_sel:WORD_1
	v_exp_f16_sdwa v83, v79 dst_sel:WORD_1 dst_unused:UNUSED_PRESERVE src0_sel:WORD_1
	v_exp_f16_sdwa v84, v80 dst_sel:WORD_1 dst_unused:UNUSED_PRESERVE src0_sel:WORD_1
	v_exp_f16_sdwa v85, v81 dst_sel:WORD_1 dst_unused:UNUSED_PRESERVE src0_sel:WORD_1
	s_nop 0
	v_pk_add_f16 v78, v186, v154
	v_pk_add_f16 v62, v62, v85
	v_pk_add_f16 v63, v63, v84
	v_pk_add_f16 v64, v64, v83
	v_pk_add_f16 v65, v65, v82
	v_pk_fma_f16 v45, v9, v85, v45
	v_pk_fma_f16 v44, v8, v84, v44
	v_pk_fma_f16 v43, v7, v83, v43
	v_pk_fma_f16 v42, v6, v82, v42
	v_pk_add_f16 v79, v185, v155
	v_pk_add_f16 v80, v184, v156
	v_pk_add_f16 v81, v183, v157
	s_nop 0
	v_exp_f16_sdwa v82, v78 dst_sel:WORD_0 dst_unused:UNUSED_PAD src0_sel:WORD_0
	v_exp_f16_sdwa v83, v79 dst_sel:WORD_0 dst_unused:UNUSED_PAD src0_sel:WORD_0
	v_exp_f16_sdwa v84, v80 dst_sel:WORD_0 dst_unused:UNUSED_PAD src0_sel:WORD_0
	v_exp_f16_sdwa v85, v81 dst_sel:WORD_0 dst_unused:UNUSED_PAD src0_sel:WORD_0
	v_exp_f16_sdwa v82, v78 dst_sel:WORD_1 dst_unused:UNUSED_PRESERVE src0_sel:WORD_1
	v_exp_f16_sdwa v83, v79 dst_sel:WORD_1 dst_unused:UNUSED_PRESERVE src0_sel:WORD_1
	v_exp_f16_sdwa v84, v80 dst_sel:WORD_1 dst_unused:UNUSED_PRESERVE src0_sel:WORD_1
	v_exp_f16_sdwa v85, v81 dst_sel:WORD_1 dst_unused:UNUSED_PRESERVE src0_sel:WORD_1
	s_nop 0
	v_pk_add_f16 v78, v114, v154
	v_pk_add_f16 v62, v62, v85
	v_pk_add_f16 v65, v65, v82
	v_pk_add_f16 v64, v64, v83
	v_pk_add_f16 v63, v63, v84
	v_pk_fma_f16 v42, v10, v82, v42
	v_pk_fma_f16 v43, v11, v83, v43
	v_pk_fma_f16 v44, v12, v84, v44
	v_pk_fma_f16 v45, v13, v85, v45
	v_pk_add_f16 v79, v115, v155
	v_pk_add_f16 v80, v116, v156
	v_pk_add_f16 v81, v117, v157
	s_nop 0
	v_exp_f16_sdwa v82, v78 dst_sel:WORD_0 dst_unused:UNUSED_PAD src0_sel:WORD_0
	v_exp_f16_sdwa v83, v79 dst_sel:WORD_0 dst_unused:UNUSED_PAD src0_sel:WORD_0
	v_exp_f16_sdwa v84, v80 dst_sel:WORD_0 dst_unused:UNUSED_PAD src0_sel:WORD_0
	v_exp_f16_sdwa v85, v81 dst_sel:WORD_0 dst_unused:UNUSED_PAD src0_sel:WORD_0
	v_exp_f16_sdwa v82, v78 dst_sel:WORD_1 dst_unused:UNUSED_PRESERVE src0_sel:WORD_1
	v_exp_f16_sdwa v83, v79 dst_sel:WORD_1 dst_unused:UNUSED_PRESERVE src0_sel:WORD_1
	v_exp_f16_sdwa v84, v80 dst_sel:WORD_1 dst_unused:UNUSED_PRESERVE src0_sel:WORD_1
	v_exp_f16_sdwa v85, v81 dst_sel:WORD_1 dst_unused:UNUSED_PRESERVE src0_sel:WORD_1
	s_nop 0
	s_nop 0
	v_pk_add_f16 v62, v62, v85
	v_pk_add_f16 v63, v63, v84
	v_pk_add_f16 v64, v64, v83
	v_pk_add_f16 v65, v65, v82
	v_rcp_f16_e32 v81, v62
	v_rcp_f16_sdwa v62, v62 dst_sel:DWORD dst_unused:UNUSED_PAD src0_sel:WORD_1
	v_rcp_f16_e32 v78, v65
	v_rcp_f16_sdwa v65, v65 dst_sel:DWORD dst_unused:UNUSED_PAD src0_sel:WORD_1
	v_rcp_f16_e32 v79, v64
	v_rcp_f16_sdwa v64, v64 dst_sel:DWORD dst_unused:UNUSED_PAD src0_sel:WORD_1
	v_rcp_f16_e32 v80, v63
	v_rcp_f16_sdwa v63, v63 dst_sel:DWORD dst_unused:UNUSED_PAD src0_sel:WORD_1
	v_pk_fma_f16 v45, v17, v85, v45
	v_pack_b32_f16 v62, v81, v62
	v_pk_fma_f16 v44, v16, v84, v44
	v_pk_fma_f16 v43, v15, v83, v43
	v_pk_fma_f16 v42, v14, v82, v42
	v_pack_b32_f16 v65, v78, v65
	v_pack_b32_f16 v64, v79, v64
	v_pack_b32_f16 v63, v80, v63
	v_pk_mul_f16 v45, v45, v62
	s_waitcnt vmcnt(6)
	v_pk_mul_f16 v62, v182, v150 op_sel_hi:[0,1]
	v_pk_mul_f16 v42, v42, v65
	v_pk_mul_f16 v43, v43, v64
	v_pk_mul_f16 v44, v44, v63
	v_pk_mul_f16 v63, v182, v151 op_sel_hi:[0,1]
	v_pk_mul_f16 v64, v182, v152 op_sel_hi:[0,1]
	v_pk_mul_f16 v65, v182, v153 op_sel_hi:[0,1]
	v_pk_mul_f16 v78, v180, v150 op_sel_hi:[0,1]
	v_pk_mul_f16 v82, v181, v150 op_sel_hi:[0,1]
	v_pk_fma_f16 v50, v50, v150, v62
	v_pk_fma_f16 v66, v66, v150, v62
	v_pk_fma_f16 v62, v94, v150, v62
	v_pk_mul_f16 v79, v180, v151 op_sel_hi:[0,1]
	v_pk_maximum3_f16 v114, v50, v66, v62
	v_pk_mul_f16 v80, v180, v152 op_sel_hi:[0,1]
	v_pk_mul_f16 v81, v180, v153 op_sel_hi:[0,1]
	v_pk_mul_f16 v83, v181, v151 op_sel_hi:[0,1]
	v_pk_mul_f16 v84, v181, v152 op_sel_hi:[0,1]
	v_pk_mul_f16 v85, v181, v153 op_sel_hi:[0,1]
	v_pk_fma_f16 v53, v53, v153, v65
	v_pk_fma_f16 v52, v52, v152, v64
	v_pk_fma_f16 v51, v51, v151, v63
	v_pk_fma_f16 v69, v69, v153, v65
	v_pk_fma_f16 v68, v68, v152, v64
	v_pk_fma_f16 v67, v67, v151, v63
	v_pk_fma_f16 v65, v97, v153, v65
	v_pk_fma_f16 v64, v96, v152, v64
	v_pk_fma_f16 v63, v95, v151, v63
	v_pk_fma_f16 v89, v18, v150, v78
	v_pk_fma_f16 v97, v30, v150, v78
	v_pk_fma_f16 v78, v54, v150, v78
	v_pk_fma_f16 v105, v74, v150, v82
	v_pk_fma_f16 v109, v98, v150, v82
	v_pk_fma_f16 v82, v118, v150, v82
	v_pk_maximum3_f16 v115, v51, v67, v63
	v_pk_maximum3_f16 v116, v52, v68, v64
	v_pk_maximum3_f16 v117, v53, v69, v65
	v_pk_maximum3_f16 v122, v89, v97, v78
	v_pk_fma_f16 v86, v21, v153, v81
	v_pk_maximum3_f16 v126, v105, v109, v82
	v_pk_fma_f16 v87, v20, v152, v80
	v_pk_maximum3_f16 v114, v114, v122, v126
	v_pk_fma_f16 v88, v19, v151, v79
	v_pk_fma_f16 v94, v33, v153, v81
	v_pk_fma_f16 v95, v32, v152, v80
	v_pk_fma_f16 v96, v31, v151, v79
	v_pk_fma_f16 v81, v57, v153, v81
	v_pk_fma_f16 v80, v56, v152, v80
	v_pk_fma_f16 v79, v55, v151, v79
	v_pk_fma_f16 v102, v77, v153, v85
	v_pk_fma_f16 v103, v76, v152, v84
	v_pk_fma_f16 v104, v75, v151, v83
	v_pk_fma_f16 v106, v101, v153, v85
	v_pk_fma_f16 v107, v100, v152, v84
	v_pk_fma_f16 v108, v99, v151, v83
	v_pk_fma_f16 v85, v121, v153, v85
	v_pk_fma_f16 v84, v120, v152, v84
	v_pk_fma_f16 v83, v119, v151, v83
	v_pk_maximum3_f16 v123, v88, v96, v79
	v_pk_maximum3_f16 v124, v87, v95, v80
	v_pk_maximum3_f16 v125, v86, v94, v81
	v_pk_maximum3_f16 v128, v103, v107, v84
	v_pk_maximum3_f16 v129, v102, v106, v85
	s_nop 0
	v_pk_maximum3_f16 v127, v104, v108, v83
	v_xor_b32_e32 v114, 0x80008000, v114
	v_pk_maximum3_f16 v115, v115, v123, v127
	v_pk_maximum3_f16 v116, v116, v124, v128
	v_pk_maximum3_f16 v117, v117, v125, v129
	v_pk_add_f16 v50, v50, v114
	v_xor_b32_e32 v117, 0x80008000, v117
	v_xor_b32_e32 v116, 0x80008000, v116
	v_xor_b32_e32 v115, 0x80008000, v115
	v_pk_add_f16 v51, v51, v115
	v_pk_add_f16 v52, v52, v116
	v_pk_add_f16 v53, v53, v117
	v_pk_add_f16 v66, v66, v114
	v_exp_f16_sdwa v122, v50 dst_sel:WORD_0 dst_unused:UNUSED_PAD src0_sel:WORD_0
	v_exp_f16_sdwa v123, v51 dst_sel:WORD_0 dst_unused:UNUSED_PAD src0_sel:WORD_0
	v_exp_f16_sdwa v124, v52 dst_sel:WORD_0 dst_unused:UNUSED_PAD src0_sel:WORD_0
	v_exp_f16_sdwa v125, v53 dst_sel:WORD_0 dst_unused:UNUSED_PAD src0_sel:WORD_0
	v_exp_f16_sdwa v122, v50 dst_sel:WORD_1 dst_unused:UNUSED_PRESERVE src0_sel:WORD_1
	v_exp_f16_sdwa v123, v51 dst_sel:WORD_1 dst_unused:UNUSED_PRESERVE src0_sel:WORD_1
	v_exp_f16_sdwa v124, v52 dst_sel:WORD_1 dst_unused:UNUSED_PRESERVE src0_sel:WORD_1
	v_exp_f16_sdwa v125, v53 dst_sel:WORD_1 dst_unused:UNUSED_PRESERVE src0_sel:WORD_1
	s_nop 0
	v_pk_add_f16 v67, v67, v115
	v_pk_add_f16 v50, v125, 0
	v_pk_fma_f16 v22, v22, v122, 0
	v_pk_add_f16 v51, v124, 0
	v_pk_add_f16 v52, v123, 0
	v_pk_add_f16 v53, v122, 0
	v_pk_fma_f16 v23, v23, v123, 0
	v_pk_fma_f16 v24, v24, v124, 0
	v_pk_fma_f16 v25, v25, v125, 0
	v_pk_add_f16 v68, v68, v116
	v_pk_add_f16 v69, v69, v117
	s_nop 0
	v_exp_f16_sdwa v122, v66 dst_sel:WORD_0 dst_unused:UNUSED_PAD src0_sel:WORD_0
	v_exp_f16_sdwa v123, v67 dst_sel:WORD_0 dst_unused:UNUSED_PAD src0_sel:WORD_0
	v_exp_f16_sdwa v124, v68 dst_sel:WORD_0 dst_unused:UNUSED_PAD src0_sel:WORD_0
	v_exp_f16_sdwa v125, v69 dst_sel:WORD_0 dst_unused:UNUSED_PAD src0_sel:WORD_0
	v_exp_f16_sdwa v122, v66 dst_sel:WORD_1 dst_unused:UNUSED_PRESERVE src0_sel:WORD_1
	v_exp_f16_sdwa v123, v67 dst_sel:WORD_1 dst_unused:UNUSED_PRESERVE src0_sel:WORD_1
	v_exp_f16_sdwa v124, v68 dst_sel:WORD_1 dst_unused:UNUSED_PRESERVE src0_sel:WORD_1
	v_exp_f16_sdwa v125, v69 dst_sel:WORD_1 dst_unused:UNUSED_PRESERVE src0_sel:WORD_1
	s_nop 0
	s_nop 0
	v_pk_add_f16 v50, v50, v125
	v_pk_fma_f16 v22, v34, v122, v22
	v_pk_add_f16 v34, v62, v114
	v_pk_add_f16 v53, v53, v122
	v_pk_add_f16 v52, v52, v123
	v_pk_add_f16 v51, v51, v124
	v_pk_fma_f16 v25, v37, v125, v25
	v_pk_fma_f16 v24, v36, v124, v24
	v_pk_fma_f16 v23, v35, v123, v23
	v_pk_add_f16 v35, v63, v115
	v_pk_add_f16 v36, v64, v116
	v_pk_add_f16 v37, v65, v117
	s_nop 0
	v_exp_f16_sdwa v62, v34 dst_sel:WORD_0 dst_unused:UNUSED_PAD src0_sel:WORD_0
	v_exp_f16_sdwa v63, v35 dst_sel:WORD_0 dst_unused:UNUSED_PAD src0_sel:WORD_0
	v_exp_f16_sdwa v64, v36 dst_sel:WORD_0 dst_unused:UNUSED_PAD src0_sel:WORD_0
	v_exp_f16_sdwa v65, v37 dst_sel:WORD_0 dst_unused:UNUSED_PAD src0_sel:WORD_0
	v_exp_f16_sdwa v62, v34 dst_sel:WORD_1 dst_unused:UNUSED_PRESERVE src0_sel:WORD_1
	v_exp_f16_sdwa v63, v35 dst_sel:WORD_1 dst_unused:UNUSED_PRESERVE src0_sel:WORD_1
	v_exp_f16_sdwa v64, v36 dst_sel:WORD_1 dst_unused:UNUSED_PRESERVE src0_sel:WORD_1
	v_exp_f16_sdwa v65, v37 dst_sel:WORD_1 dst_unused:UNUSED_PRESERVE src0_sel:WORD_1
	s_nop 0
	s_nop 0
	v_pk_add_f16 v34, v50, v65
	v_pk_add_f16 v35, v51, v64
	v_pk_add_f16 v36, v52, v63
	v_pk_add_f16 v37, v53, v62
	v_pk_fma_f16 v22, v46, v62, v22
	v_pk_fma_f16 v23, v47, v63, v23
	v_pk_fma_f16 v24, v48, v64, v24
	v_pk_fma_f16 v25, v49, v65, v25
	v_pk_add_f16 v46, v89, v114
	v_pk_add_f16 v47, v88, v115
	v_pk_add_f16 v48, v87, v116
	v_pk_add_f16 v49, v86, v117
	s_nop 0
	v_exp_f16_sdwa v50, v46 dst_sel:WORD_0 dst_unused:UNUSED_PAD src0_sel:WORD_0
	v_exp_f16_sdwa v51, v47 dst_sel:WORD_0 dst_unused:UNUSED_PAD src0_sel:WORD_0
	v_exp_f16_sdwa v52, v48 dst_sel:WORD_0 dst_unused:UNUSED_PAD src0_sel:WORD_0
	v_exp_f16_sdwa v53, v49 dst_sel:WORD_0 dst_unused:UNUSED_PAD src0_sel:WORD_0
	v_exp_f16_sdwa v50, v46 dst_sel:WORD_1 dst_unused:UNUSED_PRESERVE src0_sel:WORD_1
	v_exp_f16_sdwa v51, v47 dst_sel:WORD_1 dst_unused:UNUSED_PRESERVE src0_sel:WORD_1
	v_exp_f16_sdwa v52, v48 dst_sel:WORD_1 dst_unused:UNUSED_PRESERVE src0_sel:WORD_1
	v_exp_f16_sdwa v53, v49 dst_sel:WORD_1 dst_unused:UNUSED_PRESERVE src0_sel:WORD_1
	s_nop 0
	v_pk_add_f16 v46, v97, v114
	v_pk_add_f16 v34, v34, v53
	v_pk_add_f16 v37, v37, v50
	v_pk_add_f16 v36, v36, v51
	v_pk_add_f16 v35, v35, v52
	v_pk_fma_f16 v25, v9, v53, v25
	v_pk_fma_f16 v24, v8, v52, v24
	v_pk_fma_f16 v23, v7, v51, v23
	v_pk_fma_f16 v22, v6, v50, v22
	v_pk_add_f16 v47, v96, v115
	v_pk_add_f16 v48, v95, v116
	v_pk_add_f16 v49, v94, v117
	s_nop 0
	v_exp_f16_sdwa v50, v46 dst_sel:WORD_0 dst_unused:UNUSED_PAD src0_sel:WORD_0
	v_exp_f16_sdwa v51, v47 dst_sel:WORD_0 dst_unused:UNUSED_PAD src0_sel:WORD_0
	v_exp_f16_sdwa v52, v48 dst_sel:WORD_0 dst_unused:UNUSED_PAD src0_sel:WORD_0
	v_exp_f16_sdwa v53, v49 dst_sel:WORD_0 dst_unused:UNUSED_PAD src0_sel:WORD_0
	v_exp_f16_sdwa v50, v46 dst_sel:WORD_1 dst_unused:UNUSED_PRESERVE src0_sel:WORD_1
	v_exp_f16_sdwa v51, v47 dst_sel:WORD_1 dst_unused:UNUSED_PRESERVE src0_sel:WORD_1
	v_exp_f16_sdwa v52, v48 dst_sel:WORD_1 dst_unused:UNUSED_PRESERVE src0_sel:WORD_1
	v_exp_f16_sdwa v53, v49 dst_sel:WORD_1 dst_unused:UNUSED_PRESERVE src0_sel:WORD_1
	s_nop 0
	v_pk_add_f16 v46, v78, v114
	v_pk_add_f16 v34, v34, v53
	v_pk_add_f16 v35, v35, v52
	v_pk_add_f16 v36, v36, v51
	v_pk_add_f16 v37, v37, v50
	v_pk_fma_f16 v22, v10, v50, v22
	v_pk_fma_f16 v23, v11, v51, v23
	v_pk_fma_f16 v24, v12, v52, v24
	v_pk_fma_f16 v25, v13, v53, v25
	v_pk_add_f16 v47, v79, v115
	v_pk_add_f16 v48, v80, v116
	v_pk_add_f16 v49, v81, v117
	s_nop 0
	v_exp_f16_sdwa v50, v46 dst_sel:WORD_0 dst_unused:UNUSED_PAD src0_sel:WORD_0
	v_exp_f16_sdwa v51, v47 dst_sel:WORD_0 dst_unused:UNUSED_PAD src0_sel:WORD_0
	v_exp_f16_sdwa v52, v48 dst_sel:WORD_0 dst_unused:UNUSED_PAD src0_sel:WORD_0
	v_exp_f16_sdwa v53, v49 dst_sel:WORD_0 dst_unused:UNUSED_PAD src0_sel:WORD_0
	v_exp_f16_sdwa v50, v46 dst_sel:WORD_1 dst_unused:UNUSED_PRESERVE src0_sel:WORD_1
	v_exp_f16_sdwa v51, v47 dst_sel:WORD_1 dst_unused:UNUSED_PRESERVE src0_sel:WORD_1
	v_exp_f16_sdwa v52, v48 dst_sel:WORD_1 dst_unused:UNUSED_PRESERVE src0_sel:WORD_1
	v_exp_f16_sdwa v53, v49 dst_sel:WORD_1 dst_unused:UNUSED_PRESERVE src0_sel:WORD_1
	s_nop 0
	v_pk_add_f16 v46, v105, v114
	v_pk_add_f16 v34, v34, v53
	v_pk_add_f16 v37, v37, v50
	v_pk_add_f16 v36, v36, v51
	v_pk_add_f16 v35, v35, v52
	v_pk_fma_f16 v25, v17, v53, v25
	v_pk_fma_f16 v24, v16, v52, v24
	v_pk_fma_f16 v23, v15, v51, v23
	v_pk_fma_f16 v22, v14, v50, v22
	v_pk_add_f16 v47, v104, v115
	v_pk_add_f16 v48, v103, v116
	v_pk_add_f16 v49, v102, v117
	s_nop 0
	v_exp_f16_sdwa v50, v46 dst_sel:WORD_0 dst_unused:UNUSED_PAD src0_sel:WORD_0
	v_exp_f16_sdwa v51, v47 dst_sel:WORD_0 dst_unused:UNUSED_PAD src0_sel:WORD_0
	v_exp_f16_sdwa v52, v48 dst_sel:WORD_0 dst_unused:UNUSED_PAD src0_sel:WORD_0
	v_exp_f16_sdwa v53, v49 dst_sel:WORD_0 dst_unused:UNUSED_PAD src0_sel:WORD_0
	v_exp_f16_sdwa v50, v46 dst_sel:WORD_1 dst_unused:UNUSED_PRESERVE src0_sel:WORD_1
	v_exp_f16_sdwa v51, v47 dst_sel:WORD_1 dst_unused:UNUSED_PRESERVE src0_sel:WORD_1
	v_exp_f16_sdwa v52, v48 dst_sel:WORD_1 dst_unused:UNUSED_PRESERVE src0_sel:WORD_1
	v_exp_f16_sdwa v53, v49 dst_sel:WORD_1 dst_unused:UNUSED_PRESERVE src0_sel:WORD_1
	s_nop 0
	v_pk_add_f16 v46, v109, v114
	v_pk_add_f16 v34, v34, v53
	v_pk_add_f16 v35, v35, v52
	v_pk_add_f16 v36, v36, v51
	v_pk_add_f16 v37, v37, v50
	v_pk_fma_f16 v22, v26, v50, v22
	v_pk_fma_f16 v23, v27, v51, v23
	v_pk_fma_f16 v24, v28, v52, v24
	v_pk_fma_f16 v25, v29, v53, v25
	v_pk_add_f16 v47, v108, v115
	v_pk_add_f16 v48, v107, v116
	v_pk_add_f16 v49, v106, v117
	s_nop 0
	v_exp_f16_sdwa v50, v46 dst_sel:WORD_0 dst_unused:UNUSED_PAD src0_sel:WORD_0
	v_exp_f16_sdwa v51, v47 dst_sel:WORD_0 dst_unused:UNUSED_PAD src0_sel:WORD_0
	v_exp_f16_sdwa v52, v48 dst_sel:WORD_0 dst_unused:UNUSED_PAD src0_sel:WORD_0
	v_exp_f16_sdwa v53, v49 dst_sel:WORD_0 dst_unused:UNUSED_PAD src0_sel:WORD_0
	v_exp_f16_sdwa v50, v46 dst_sel:WORD_1 dst_unused:UNUSED_PRESERVE src0_sel:WORD_1
	v_exp_f16_sdwa v51, v47 dst_sel:WORD_1 dst_unused:UNUSED_PRESERVE src0_sel:WORD_1
	v_exp_f16_sdwa v52, v48 dst_sel:WORD_1 dst_unused:UNUSED_PRESERVE src0_sel:WORD_1
	v_exp_f16_sdwa v53, v49 dst_sel:WORD_1 dst_unused:UNUSED_PRESERVE src0_sel:WORD_1
	s_nop 0
	v_pk_add_f16 v46, v82, v114
	v_pk_add_f16 v34, v34, v53
	v_pk_add_f16 v37, v37, v50
	v_pk_add_f16 v36, v36, v51
	v_pk_add_f16 v35, v35, v52
	v_pk_fma_f16 v25, v41, v53, v25
	v_pk_fma_f16 v24, v40, v52, v24
	v_pk_fma_f16 v23, v39, v51, v23
	v_pk_fma_f16 v22, v38, v50, v22
	v_pk_add_f16 v47, v83, v115
	v_pk_add_f16 v48, v84, v116
	v_pk_add_f16 v49, v85, v117
	s_nop 0
	v_exp_f16_sdwa v50, v46 dst_sel:WORD_0 dst_unused:UNUSED_PAD src0_sel:WORD_0
	v_exp_f16_sdwa v51, v47 dst_sel:WORD_0 dst_unused:UNUSED_PAD src0_sel:WORD_0
	v_exp_f16_sdwa v52, v48 dst_sel:WORD_0 dst_unused:UNUSED_PAD src0_sel:WORD_0
	v_exp_f16_sdwa v53, v49 dst_sel:WORD_0 dst_unused:UNUSED_PAD src0_sel:WORD_0
	v_exp_f16_sdwa v50, v46 dst_sel:WORD_1 dst_unused:UNUSED_PRESERVE src0_sel:WORD_1
	v_exp_f16_sdwa v51, v47 dst_sel:WORD_1 dst_unused:UNUSED_PRESERVE src0_sel:WORD_1
	v_exp_f16_sdwa v52, v48 dst_sel:WORD_1 dst_unused:UNUSED_PRESERVE src0_sel:WORD_1
	v_exp_f16_sdwa v53, v49 dst_sel:WORD_1 dst_unused:UNUSED_PRESERVE src0_sel:WORD_1
	s_nop 0
	s_nop 0
	v_pk_add_f16 v34, v34, v53
	v_pk_add_f16 v35, v35, v52
	v_rcp_f16_e32 v48, v34
	v_rcp_f16_sdwa v34, v34 dst_sel:DWORD dst_unused:UNUSED_PAD src0_sel:WORD_1
	v_pk_add_f16 v36, v36, v51
	v_rcp_f16_e32 v49, v35
	v_rcp_f16_sdwa v35, v35 dst_sel:DWORD dst_unused:UNUSED_PAD src0_sel:WORD_1
	v_pk_add_f16 v37, v37, v50
	v_rcp_f16_e32 v47, v36
	v_rcp_f16_sdwa v36, v36 dst_sel:DWORD dst_unused:UNUSED_PAD src0_sel:WORD_1
	v_rcp_f16_e32 v46, v37
	v_rcp_f16_sdwa v37, v37 dst_sel:DWORD dst_unused:UNUSED_PAD src0_sel:WORD_1
	v_pk_fma_f16 v25, v61, v53, v25
	v_pack_b32_f16 v34, v48, v34
	v_pk_fma_f16 v24, v60, v52, v24
	v_pk_mul_f16 v25, v25, v34
	v_pack_b32_f16 v34, v49, v35
	v_pk_fma_f16 v23, v59, v51, v23
	v_pk_mul_f16 v24, v24, v34
	v_pack_b32_f16 v34, v47, v36
	v_pk_fma_f16 v22, v58, v50, v22
	v_pk_mul_f16 v23, v23, v34
	v_pack_b32_f16 v34, v46, v37
	v_pk_mul_f16 v22, v22, v34
	s_waitcnt vmcnt(0)
	v_pk_mul_f16 v34, v182, v146 op_sel_hi:[0,1]
	v_pk_mul_f16 v35, v182, v147 op_sel_hi:[0,1]
	v_pk_mul_f16 v36, v182, v148 op_sel_hi:[0,1]
	v_pk_mul_f16 v37, v182, v149 op_sel_hi:[0,1]
	v_pk_mul_f16 v46, v180, v146 op_sel_hi:[0,1]
	v_pk_mul_f16 v47, v180, v147 op_sel_hi:[0,1]
	v_pk_mul_f16 v48, v180, v148 op_sel_hi:[0,1]
	v_pk_mul_f16 v49, v180, v149 op_sel_hi:[0,1]
	v_pk_mul_f16 v50, v181, v146 op_sel_hi:[0,1]
	v_pk_mul_f16 v51, v181, v147 op_sel_hi:[0,1]
	v_pk_mul_f16 v52, v181, v148 op_sel_hi:[0,1]
	v_pk_mul_f16 v53, v181, v149 op_sel_hi:[0,1]
	v_pk_fma_f16 v21, v21, v149, v37
	v_pk_fma_f16 v20, v20, v148, v36
	v_pk_fma_f16 v19, v19, v147, v35
	v_pk_fma_f16 v18, v18, v146, v34
	v_pk_fma_f16 v33, v33, v149, v37
	v_pk_fma_f16 v32, v32, v148, v36
	v_pk_fma_f16 v31, v31, v147, v35
	v_pk_fma_f16 v30, v30, v146, v34
	v_pk_fma_f16 v37, v57, v149, v37
	v_pk_fma_f16 v36, v56, v148, v36
	v_pk_fma_f16 v35, v55, v147, v35
	v_pk_fma_f16 v34, v54, v146, v34
	v_pk_maximum3_f16 v79, v19, v31, v35
	v_pk_maximum3_f16 v80, v20, v32, v36
	v_pk_maximum3_f16 v81, v21, v33, v37
	v_pk_fma_f16 v54, v77, v149, v49
	v_pk_maximum3_f16 v78, v18, v30, v34
	v_pk_fma_f16 v55, v76, v148, v48
	v_pk_fma_f16 v56, v75, v147, v47
	v_pk_fma_f16 v57, v74, v146, v46
	v_pk_fma_f16 v62, v101, v149, v49
	v_pk_fma_f16 v63, v100, v148, v48
	v_pk_fma_f16 v64, v99, v147, v47
	v_pk_fma_f16 v65, v98, v146, v46
	v_pk_fma_f16 v49, v121, v149, v49
	v_pk_fma_f16 v48, v120, v148, v48
	v_pk_fma_f16 v47, v119, v147, v47
	v_pk_fma_f16 v46, v118, v146, v46
	v_pk_fma_f16 v66, v133, v149, v53
	v_pk_fma_f16 v67, v132, v148, v52
	v_pk_fma_f16 v68, v131, v147, v51
	v_pk_fma_f16 v69, v130, v146, v50
	v_pk_fma_f16 v74, v141, v149, v53
	v_pk_fma_f16 v75, v140, v148, v52
	v_pk_fma_f16 v76, v139, v147, v51
	v_pk_fma_f16 v77, v138, v146, v50
	v_pk_fma_f16 v53, v145, v149, v53
	v_pk_fma_f16 v52, v144, v148, v52
	v_pk_fma_f16 v51, v143, v147, v51
	v_pk_fma_f16 v50, v142, v146, v50
	v_pk_maximum3_f16 v82, v57, v65, v46
	v_pk_maximum3_f16 v83, v56, v64, v47
	v_pk_maximum3_f16 v84, v55, v63, v48
	v_pk_maximum3_f16 v85, v54, v62, v49
	v_pk_maximum3_f16 v87, v68, v76, v51
	s_nop 0
	v_pk_maximum3_f16 v86, v69, v77, v50
	v_pk_maximum3_f16 v88, v67, v75, v52
	v_pk_maximum3_f16 v89, v66, v74, v53
	s_nop 0
	v_pk_maximum3_f16 v78, v78, v82, v86
	v_pk_maximum3_f16 v79, v79, v83, v87
	v_pk_maximum3_f16 v80, v80, v84, v88
	v_pk_maximum3_f16 v81, v81, v85, v89
	s_nop 0
	v_xor_b32_e32 v81, 0x80008000, v81
	v_xor_b32_e32 v80, 0x80008000, v80
	v_xor_b32_e32 v79, 0x80008000, v79
	v_xor_b32_e32 v78, 0x80008000, v78
	v_pk_add_f16 v18, v18, v78
	v_pk_add_f16 v19, v19, v79
	v_pk_add_f16 v20, v20, v80
	v_pk_add_f16 v21, v21, v81
	v_pk_add_f16 v30, v30, v78
	v_exp_f16_sdwa v82, v18 dst_sel:WORD_0 dst_unused:UNUSED_PAD src0_sel:WORD_0
	v_exp_f16_sdwa v83, v19 dst_sel:WORD_0 dst_unused:UNUSED_PAD src0_sel:WORD_0
	v_exp_f16_sdwa v84, v20 dst_sel:WORD_0 dst_unused:UNUSED_PAD src0_sel:WORD_0
	v_exp_f16_sdwa v85, v21 dst_sel:WORD_0 dst_unused:UNUSED_PAD src0_sel:WORD_0
	v_exp_f16_sdwa v82, v18 dst_sel:WORD_1 dst_unused:UNUSED_PRESERVE src0_sel:WORD_1
	v_exp_f16_sdwa v83, v19 dst_sel:WORD_1 dst_unused:UNUSED_PRESERVE src0_sel:WORD_1
	v_exp_f16_sdwa v84, v20 dst_sel:WORD_1 dst_unused:UNUSED_PRESERVE src0_sel:WORD_1
	v_exp_f16_sdwa v85, v21 dst_sel:WORD_1 dst_unused:UNUSED_PRESERVE src0_sel:WORD_1
	s_nop 0
	v_pk_add_f16 v31, v31, v79
	v_pk_add_f16 v18, v82, 0
	v_pk_add_f16 v19, v83, 0
	v_pk_add_f16 v20, v84, 0
	v_pk_add_f16 v21, v85, 0
	v_pk_fma_f16 v6, v6, v82, 0
	v_pk_fma_f16 v7, v7, v83, 0
	v_pk_fma_f16 v8, v8, v84, 0
	v_pk_fma_f16 v9, v9, v85, 0
	v_pk_add_f16 v32, v32, v80
	v_pk_add_f16 v33, v33, v81
	s_nop 0
	v_exp_f16_sdwa v82, v30 dst_sel:WORD_0 dst_unused:UNUSED_PAD src0_sel:WORD_0
	v_exp_f16_sdwa v83, v31 dst_sel:WORD_0 dst_unused:UNUSED_PAD src0_sel:WORD_0
	v_exp_f16_sdwa v84, v32 dst_sel:WORD_0 dst_unused:UNUSED_PAD src0_sel:WORD_0
	v_exp_f16_sdwa v85, v33 dst_sel:WORD_0 dst_unused:UNUSED_PAD src0_sel:WORD_0
	v_exp_f16_sdwa v82, v30 dst_sel:WORD_1 dst_unused:UNUSED_PRESERVE src0_sel:WORD_1
	v_exp_f16_sdwa v83, v31 dst_sel:WORD_1 dst_unused:UNUSED_PRESERVE src0_sel:WORD_1
	v_exp_f16_sdwa v84, v32 dst_sel:WORD_1 dst_unused:UNUSED_PRESERVE src0_sel:WORD_1
	v_exp_f16_sdwa v85, v33 dst_sel:WORD_1 dst_unused:UNUSED_PRESERVE src0_sel:WORD_1
	s_nop 0
	s_nop 0
	v_pk_add_f16 v21, v21, v85
	v_pk_add_f16 v20, v20, v84
	v_pk_add_f16 v19, v19, v83
	v_pk_add_f16 v18, v18, v82
	v_pk_fma_f16 v9, v13, v85, v9
	v_pk_fma_f16 v8, v12, v84, v8
	v_pk_fma_f16 v7, v11, v83, v7
	v_pk_fma_f16 v6, v10, v82, v6
	v_pk_add_f16 v10, v34, v78
	v_pk_add_f16 v11, v35, v79
	v_pk_add_f16 v12, v36, v80
	v_pk_add_f16 v13, v37, v81
	s_nop 0
	v_exp_f16_sdwa v30, v10 dst_sel:WORD_0 dst_unused:UNUSED_PAD src0_sel:WORD_0
	v_exp_f16_sdwa v31, v11 dst_sel:WORD_0 dst_unused:UNUSED_PAD src0_sel:WORD_0
	v_exp_f16_sdwa v32, v12 dst_sel:WORD_0 dst_unused:UNUSED_PAD src0_sel:WORD_0
	v_exp_f16_sdwa v33, v13 dst_sel:WORD_0 dst_unused:UNUSED_PAD src0_sel:WORD_0
	v_exp_f16_sdwa v30, v10 dst_sel:WORD_1 dst_unused:UNUSED_PRESERVE src0_sel:WORD_1
	v_exp_f16_sdwa v31, v11 dst_sel:WORD_1 dst_unused:UNUSED_PRESERVE src0_sel:WORD_1
	v_exp_f16_sdwa v32, v12 dst_sel:WORD_1 dst_unused:UNUSED_PRESERVE src0_sel:WORD_1
	v_exp_f16_sdwa v33, v13 dst_sel:WORD_1 dst_unused:UNUSED_PRESERVE src0_sel:WORD_1
	s_nop 0
	s_nop 0
	v_pk_add_f16 v10, v18, v30
	v_pk_add_f16 v11, v19, v31
	v_pk_add_f16 v12, v20, v32
	v_pk_add_f16 v13, v21, v33
	v_pk_fma_f16 v6, v14, v30, v6
	v_pk_fma_f16 v7, v15, v31, v7
	v_pk_fma_f16 v8, v16, v32, v8
	v_pk_fma_f16 v9, v17, v33, v9
	v_pk_add_f16 v14, v57, v78
	v_pk_add_f16 v15, v56, v79
	v_pk_add_f16 v16, v55, v80
	v_pk_add_f16 v17, v54, v81
	s_nop 0
	v_exp_f16_sdwa v18, v14 dst_sel:WORD_0 dst_unused:UNUSED_PAD src0_sel:WORD_0
	v_exp_f16_sdwa v19, v15 dst_sel:WORD_0 dst_unused:UNUSED_PAD src0_sel:WORD_0
	v_exp_f16_sdwa v20, v16 dst_sel:WORD_0 dst_unused:UNUSED_PAD src0_sel:WORD_0
	v_exp_f16_sdwa v21, v17 dst_sel:WORD_0 dst_unused:UNUSED_PAD src0_sel:WORD_0
	v_exp_f16_sdwa v18, v14 dst_sel:WORD_1 dst_unused:UNUSED_PRESERVE src0_sel:WORD_1
	v_exp_f16_sdwa v19, v15 dst_sel:WORD_1 dst_unused:UNUSED_PRESERVE src0_sel:WORD_1
	v_exp_f16_sdwa v20, v16 dst_sel:WORD_1 dst_unused:UNUSED_PRESERVE src0_sel:WORD_1
	v_exp_f16_sdwa v21, v17 dst_sel:WORD_1 dst_unused:UNUSED_PRESERVE src0_sel:WORD_1
	s_nop 0
	v_pk_add_f16 v14, v65, v78
	v_pk_add_f16 v13, v13, v21
	v_pk_add_f16 v12, v12, v20
	v_pk_add_f16 v11, v11, v19
	v_pk_add_f16 v10, v10, v18
	v_pk_fma_f16 v9, v29, v21, v9
	v_pk_fma_f16 v8, v28, v20, v8
	v_pk_fma_f16 v7, v27, v19, v7
	v_pk_fma_f16 v6, v26, v18, v6
	v_pk_add_f16 v15, v64, v79
	v_pk_add_f16 v16, v63, v80
	v_pk_add_f16 v17, v62, v81
	s_nop 0
	v_exp_f16_sdwa v18, v14 dst_sel:WORD_0 dst_unused:UNUSED_PAD src0_sel:WORD_0
	v_exp_f16_sdwa v19, v15 dst_sel:WORD_0 dst_unused:UNUSED_PAD src0_sel:WORD_0
	v_exp_f16_sdwa v20, v16 dst_sel:WORD_0 dst_unused:UNUSED_PAD src0_sel:WORD_0
	v_exp_f16_sdwa v21, v17 dst_sel:WORD_0 dst_unused:UNUSED_PAD src0_sel:WORD_0
	v_exp_f16_sdwa v18, v14 dst_sel:WORD_1 dst_unused:UNUSED_PRESERVE src0_sel:WORD_1
	v_exp_f16_sdwa v19, v15 dst_sel:WORD_1 dst_unused:UNUSED_PRESERVE src0_sel:WORD_1
	v_exp_f16_sdwa v20, v16 dst_sel:WORD_1 dst_unused:UNUSED_PRESERVE src0_sel:WORD_1
	v_exp_f16_sdwa v21, v17 dst_sel:WORD_1 dst_unused:UNUSED_PRESERVE src0_sel:WORD_1
	s_nop 0
	v_pk_add_f16 v14, v46, v78
	v_pk_add_f16 v10, v10, v18
	v_pk_add_f16 v11, v11, v19
	v_pk_add_f16 v12, v12, v20
	v_pk_add_f16 v13, v13, v21
	v_pk_fma_f16 v6, v38, v18, v6
	v_pk_fma_f16 v7, v39, v19, v7
	v_pk_fma_f16 v8, v40, v20, v8
	v_pk_fma_f16 v9, v41, v21, v9
	v_pk_add_f16 v15, v47, v79
	v_pk_add_f16 v16, v48, v80
	v_pk_add_f16 v17, v49, v81
	s_nop 0
	v_exp_f16_sdwa v18, v14 dst_sel:WORD_0 dst_unused:UNUSED_PAD src0_sel:WORD_0
	v_exp_f16_sdwa v19, v15 dst_sel:WORD_0 dst_unused:UNUSED_PAD src0_sel:WORD_0
	v_exp_f16_sdwa v20, v16 dst_sel:WORD_0 dst_unused:UNUSED_PAD src0_sel:WORD_0
	v_exp_f16_sdwa v21, v17 dst_sel:WORD_0 dst_unused:UNUSED_PAD src0_sel:WORD_0
	v_exp_f16_sdwa v18, v14 dst_sel:WORD_1 dst_unused:UNUSED_PRESERVE src0_sel:WORD_1
	v_exp_f16_sdwa v19, v15 dst_sel:WORD_1 dst_unused:UNUSED_PRESERVE src0_sel:WORD_1
	v_exp_f16_sdwa v20, v16 dst_sel:WORD_1 dst_unused:UNUSED_PRESERVE src0_sel:WORD_1
	v_exp_f16_sdwa v21, v17 dst_sel:WORD_1 dst_unused:UNUSED_PRESERVE src0_sel:WORD_1
	s_nop 0
	v_pk_add_f16 v14, v69, v78
	v_pk_add_f16 v13, v13, v21
	v_pk_add_f16 v12, v12, v20
	v_pk_add_f16 v11, v11, v19
	v_pk_add_f16 v10, v10, v18
	v_pk_fma_f16 v9, v61, v21, v9
	v_pk_fma_f16 v8, v60, v20, v8
	v_pk_fma_f16 v7, v59, v19, v7
	v_pk_fma_f16 v6, v58, v18, v6
	v_pk_add_f16 v15, v68, v79
	v_pk_add_f16 v16, v67, v80
	v_pk_add_f16 v17, v66, v81
	s_nop 0
	v_exp_f16_sdwa v18, v14 dst_sel:WORD_0 dst_unused:UNUSED_PAD src0_sel:WORD_0
	v_exp_f16_sdwa v19, v15 dst_sel:WORD_0 dst_unused:UNUSED_PAD src0_sel:WORD_0
	v_exp_f16_sdwa v20, v16 dst_sel:WORD_0 dst_unused:UNUSED_PAD src0_sel:WORD_0
	v_exp_f16_sdwa v21, v17 dst_sel:WORD_0 dst_unused:UNUSED_PAD src0_sel:WORD_0
	v_exp_f16_sdwa v18, v14 dst_sel:WORD_1 dst_unused:UNUSED_PRESERVE src0_sel:WORD_1
	v_exp_f16_sdwa v19, v15 dst_sel:WORD_1 dst_unused:UNUSED_PRESERVE src0_sel:WORD_1
	v_exp_f16_sdwa v20, v16 dst_sel:WORD_1 dst_unused:UNUSED_PRESERVE src0_sel:WORD_1
	v_exp_f16_sdwa v21, v17 dst_sel:WORD_1 dst_unused:UNUSED_PRESERVE src0_sel:WORD_1
	s_nop 0
	s_nop 0
	v_pk_add_f16 v10, v10, v18
	v_pk_add_f16 v11, v11, v19
	v_pk_add_f16 v12, v12, v20
	v_pk_add_f16 v13, v13, v21
	v_pk_fma_f16 v14, v70, v18, v6
	v_pk_fma_f16 v15, v71, v19, v7
	v_pk_fma_f16 v16, v72, v20, v8
	v_pk_fma_f16 v17, v73, v21, v9
	v_pk_add_f16 v6, v77, v78
	v_pk_add_f16 v7, v76, v79
	v_pk_add_f16 v8, v75, v80
	v_pk_add_f16 v9, v74, v81
	s_nop 0
	v_exp_f16_sdwa v18, v6 dst_sel:WORD_0 dst_unused:UNUSED_PAD src0_sel:WORD_0
	v_exp_f16_sdwa v19, v7 dst_sel:WORD_0 dst_unused:UNUSED_PAD src0_sel:WORD_0
	v_exp_f16_sdwa v20, v8 dst_sel:WORD_0 dst_unused:UNUSED_PAD src0_sel:WORD_0
	v_exp_f16_sdwa v21, v9 dst_sel:WORD_0 dst_unused:UNUSED_PAD src0_sel:WORD_0
	v_exp_f16_sdwa v18, v6 dst_sel:WORD_1 dst_unused:UNUSED_PRESERVE src0_sel:WORD_1
	v_exp_f16_sdwa v19, v7 dst_sel:WORD_1 dst_unused:UNUSED_PRESERVE src0_sel:WORD_1
	v_exp_f16_sdwa v20, v8 dst_sel:WORD_1 dst_unused:UNUSED_PRESERVE src0_sel:WORD_1
	v_exp_f16_sdwa v21, v9 dst_sel:WORD_1 dst_unused:UNUSED_PRESERVE src0_sel:WORD_1
	s_nop 0
	s_nop 0
	v_pk_add_f16 v9, v13, v21
	v_pk_add_f16 v8, v12, v20
	v_pk_add_f16 v7, v11, v19
	v_pk_add_f16 v6, v10, v18
	v_pk_fma_f16 v13, v93, v21, v17
	v_pk_fma_f16 v12, v92, v20, v16
	v_pk_fma_f16 v11, v91, v19, v15
	v_pk_fma_f16 v10, v90, v18, v14
	v_pk_add_f16 v18, v50, v78
	v_pk_add_f16 v19, v51, v79
	v_pk_add_f16 v20, v52, v80
	v_pk_add_f16 v21, v53, v81
	s_nop 0
	v_exp_f16_sdwa v14, v18 dst_sel:WORD_0 dst_unused:UNUSED_PAD src0_sel:WORD_0
	v_exp_f16_sdwa v17, v19 dst_sel:WORD_0 dst_unused:UNUSED_PAD src0_sel:WORD_0
	v_exp_f16_sdwa v15, v20 dst_sel:WORD_0 dst_unused:UNUSED_PAD src0_sel:WORD_0
	v_exp_f16_sdwa v16, v21 dst_sel:WORD_0 dst_unused:UNUSED_PAD src0_sel:WORD_0
	v_exp_f16_sdwa v14, v18 dst_sel:WORD_1 dst_unused:UNUSED_PRESERVE src0_sel:WORD_1
	v_exp_f16_sdwa v17, v19 dst_sel:WORD_1 dst_unused:UNUSED_PRESERVE src0_sel:WORD_1
	v_exp_f16_sdwa v15, v20 dst_sel:WORD_1 dst_unused:UNUSED_PRESERVE src0_sel:WORD_1
	v_exp_f16_sdwa v16, v21 dst_sel:WORD_1 dst_unused:UNUSED_PRESERVE src0_sel:WORD_1
	s_nop 0

.LBB5_4:
	v_add_u32_e32 v182, s30, v161
	v_add_u32_e32 v181, -1, v182
	v_or_b32_e32 v2, v181, v164
	v_add_u32_e32 v180, 0x18400, v171
	v_cmp_gt_u32_e64 s[0:1], 64, v2
	s_mov_b64 s[4:5], -1
	s_and_b64 vcc, exec, s[24:25]
	s_cbranch_vccz .LBB5_42
	v_cmp_lt_u32_e64 s[64:65], 0, v182
	v_cmp_gt_u32_e64 s[66:67], 63, v182
	v_cmp_lt_u32_e64 s[68:69], 0, v162
	v_cmp_gt_u32_e64 s[70:71], 60, v162
	buffer_load_dwordx4 v[186:189], v180, s[16:19], 0 offen
	v_add_u32_e32 v223, 0x18000, v180
	buffer_load_dwordx4 v[154:157], v223, s[16:19], 0 offen
	v_add_u32_e32 v222, 0x30000, v180
	buffer_load_dwordx4 v[150:153], v222, s[16:19], 0 offen
	v_add_u32_e32 v223, 0x48000, v180
	buffer_load_dwordx4 v[146:149], v223, s[16:19], 0 offen
	s_and_b64 s[72:73], s[68:69], s[64:65]
	s_and_b64 s[74:75], s[68:69], s[66:67]
	s_and_b64 s[76:77], s[70:71], s[64:65]
	s_and_b64 s[78:79], s[70:71], s[66:67]
	v_add_u32_e32 v222, 0xfffe7c00, v180
	v_add_u32_e32 v223, 0xfffe8000, v180
	v_mov_b32_e32 v110, v172
	v_mov_b32_e32 v111, v174
	v_mov_b32_e32 v112, v176
	v_mov_b32_e32 v113, v178
	v_mov_b32_e32 v70, v173
	v_mov_b32_e32 v71, v175
	v_mov_b32_e32 v72, v177
	v_mov_b32_e32 v73, v179
	v_mov_b32_e32 v126, v172
	v_mov_b32_e32 v127, v174
	v_mov_b32_e32 v128, v176
	v_mov_b32_e32 v129, v178
	v_mov_b32_e32 v98, v173
	v_mov_b32_e32 v99, v175
	v_mov_b32_e32 v100, v177
	v_mov_b32_e32 v101, v179
	v_mov_b32_e32 v134, v172
	v_mov_b32_e32 v135, v174
	v_mov_b32_e32 v136, v176
	v_mov_b32_e32 v137, v178
	v_mov_b32_e32 v114, v173
	v_mov_b32_e32 v115, v175
	v_mov_b32_e32 v116, v177
	v_mov_b32_e32 v117, v179
	s_mov_b64 exec, s[72:73]
	buffer_load_dwordx4 v[110:113], v222, s[16:19], 0 offen
	buffer_load_dwordx4 v[70:73], v222, s[16:19], 0 offen offset:512
	s_mov_b64 exec, -1
	s_mov_b64 exec, s[68:69]
	buffer_load_dwordx4 v[126:129], v223, s[16:19], 0 offen offset:512
	buffer_load_dwordx4 v[98:101], v223, s[16:19], 0 offen offset:1024
	s_mov_b64 exec, -1
	s_mov_b64 exec, s[74:75]
	buffer_load_dwordx4 v[134:137], v223, s[16:19], 0 offen offset:2048
	buffer_load_dwordx4 v[114:117], v223, s[16:19], 0 offen offset:2560
	s_mov_b64 exec, -1
	v_add_u32_e32 v222, 0xfffffc00, v180
	v_mov_b32_e32 v82, v172
	v_mov_b32_e32 v83, v174
	v_mov_b32_e32 v84, v176
	v_mov_b32_e32 v85, v178
	v_mov_b32_e32 v42, v173
	v_mov_b32_e32 v43, v175
	v_mov_b32_e32 v44, v177
	v_mov_b32_e32 v45, v179
	v_mov_b32_e32 v122, v172
	v_mov_b32_e32 v123, v174
	v_mov_b32_e32 v124, v176
	v_mov_b32_e32 v125, v178
	v_mov_b32_e32 v86, v173
	v_mov_b32_e32 v87, v175
	v_mov_b32_e32 v88, v177
	v_mov_b32_e32 v89, v179
	s_mov_b64 exec, s[64:65]
	buffer_load_dwordx4 v[82:85], v222, s[16:19], 0 offen
	buffer_load_dwordx4 v[42:45], v222, s[16:19], 0 offen offset:512
	s_mov_b64 exec, -1
	buffer_load_dwordx4 v[106:109], v180, s[16:19], 0 offen offset:512
	buffer_load_dwordx4 v[62:65], v180, s[16:19], 0 offen offset:1024
	s_mov_b64 exec, s[66:67]
	buffer_load_dwordx4 v[122:125], v180, s[16:19], 0 offen offset:2048
	buffer_load_dwordx4 v[86:89], v180, s[16:19], 0 offen offset:2560
	s_mov_b64 exec, -1
	v_add_u32_e32 v222, 0x17c00, v180
	v_add_u32_e32 v223, 0x18000, v180
	v_mov_b32_e32 v50, v172
	v_mov_b32_e32 v51, v174
	v_mov_b32_e32 v52, v176
	v_mov_b32_e32 v53, v178
	v_mov_b32_e32 v22, v173
	v_mov_b32_e32 v23, v175
	v_mov_b32_e32 v24, v177
	v_mov_b32_e32 v25, v179
	v_mov_b32_e32 v94, v172
	v_mov_b32_e32 v95, v174
	v_mov_b32_e32 v96, v176
	v_mov_b32_e32 v97, v178
	v_mov_b32_e32 v46, v173
	v_mov_b32_e32 v47, v175
	v_mov_b32_e32 v48, v177
	v_mov_b32_e32 v49, v179
	s_mov_b64 exec, s[64:65]
	buffer_load_dwordx4 v[50:53], v222, s[16:19], 0 offen
	buffer_load_dwordx4 v[22:25], v222, s[16:19], 0 offen offset:512
	s_mov_b64 exec, -1
	buffer_load_dwordx4 v[66:69], v223, s[16:19], 0 offen offset:512
	buffer_load_dwordx4 v[30:33], v223, s[16:19], 0 offen offset:1024
	s_mov_b64 exec, s[66:67]
	buffer_load_dwordx4 v[94:97], v223, s[16:19], 0 offen offset:2048
	buffer_load_dwordx4 v[46:49], v223, s[16:19], 0 offen offset:2560
	s_mov_b64 exec, -1
	v_add_u32_e32 v222, 0x2fc00, v180
	v_add_u32_e32 v223, 0x30000, v180
	v_mov_b32_e32 v18, v172
	v_mov_b32_e32 v19, v174
	v_mov_b32_e32 v20, v176
	v_mov_b32_e32 v21, v178
	v_mov_b32_e32 v6, v173
	v_mov_b32_e32 v7, v175
	v_mov_b32_e32 v8, v177
	v_mov_b32_e32 v9, v179
	v_mov_b32_e32 v54, v172
	v_mov_b32_e32 v55, v174
	v_mov_b32_e32 v56, v176
	v_mov_b32_e32 v57, v178
	v_mov_b32_e32 v14, v173
	v_mov_b32_e32 v15, v175
	v_mov_b32_e32 v16, v177
	v_mov_b32_e32 v17, v179
	s_mov_b64 exec, s[64:65]
	buffer_load_dwordx4 v[18:21], v222, s[16:19], 0 offen
	buffer_load_dwordx4 v[6:9], v222, s[16:19], 0 offen offset:512
	s_mov_b64 exec, -1
	buffer_load_dwordx4 v[34:37], v223, s[16:19], 0 offen offset:512
	buffer_load_dwordx4 v[10:13], v223, s[16:19], 0 offen offset:1024
	s_mov_b64 exec, s[66:67]
	buffer_load_dwordx4 v[54:57], v223, s[16:19], 0 offen offset:2048
	buffer_load_dwordx4 v[14:17], v223, s[16:19], 0 offen offset:2560
	s_mov_b64 exec, -1
	v_add_u32_e32 v222, 0x47c00, v180
	v_add_u32_e32 v223, 0x48000, v180
	v_mov_b32_e32 v74, v172
	v_mov_b32_e32 v75, v174
	v_mov_b32_e32 v76, v176
	v_mov_b32_e32 v77, v178
	v_mov_b32_e32 v26, v173
	v_mov_b32_e32 v27, v175
	v_mov_b32_e32 v28, v177
	v_mov_b32_e32 v29, v179
	v_mov_b32_e32 v118, v172
	v_mov_b32_e32 v119, v174
	v_mov_b32_e32 v120, v176
	v_mov_b32_e32 v121, v178
	v_mov_b32_e32 v58, v173
	v_mov_b32_e32 v59, v175
	v_mov_b32_e32 v60, v177
	v_mov_b32_e32 v61, v179
	s_mov_b64 exec, s[64:65]
	buffer_load_dwordx4 v[74:77], v222, s[16:19], 0 offen
	buffer_load_dwordx4 v[26:29], v222, s[16:19], 0 offen offset:512
	s_mov_b64 exec, -1
	buffer_load_dwordx4 v[102:105], v223, s[16:19], 0 offen offset:512
	buffer_load_dwordx4 v[38:41], v223, s[16:19], 0 offen offset:1024
	s_mov_b64 exec, s[66:67]
	buffer_load_dwordx4 v[118:121], v223, s[16:19], 0 offen offset:2048
	buffer_load_dwordx4 v[58:61], v223, s[16:19], 0 offen offset:2560
	s_mov_b64 exec, -1
	v_add_u32_e32 v222, 0x5fc00, v180
	v_add_u32_e32 v223, 0x60000, v180
	v_mov_b32_e32 v130, v172
	v_mov_b32_e32 v131, v174
	v_mov_b32_e32 v132, v176
	v_mov_b32_e32 v133, v178
	v_mov_b32_e32 v78, v173
	v_mov_b32_e32 v79, v175
	v_mov_b32_e32 v80, v177
	v_mov_b32_e32 v81, v179
	v_mov_b32_e32 v138, v172
	v_mov_b32_e32 v139, v174
	v_mov_b32_e32 v140, v176
	v_mov_b32_e32 v141, v178
	v_mov_b32_e32 v90, v173
	v_mov_b32_e32 v91, v175
	v_mov_b32_e32 v92, v177
	v_mov_b32_e32 v93, v179
	v_mov_b32_e32 v142, v172
	v_mov_b32_e32 v143, v174
	v_mov_b32_e32 v144, v176
	v_mov_b32_e32 v145, v178
	v_mov_b32_e32 v2, v173
	v_mov_b32_e32 v3, v175
	v_mov_b32_e32 v4, v177
	v_mov_b32_e32 v5, v179
	s_mov_b64 exec, s[76:77]
	buffer_load_dwordx4 v[130:133], v222, s[16:19], 0 offen
	buffer_load_dwordx4 v[78:81], v222, s[16:19], 0 offen offset:512
	s_mov_b64 exec, -1
	s_mov_b64 exec, s[70:71]
	buffer_load_dwordx4 v[138:141], v223, s[16:19], 0 offen offset:512
	buffer_load_dwordx4 v[90:93], v223, s[16:19], 0 offen offset:1024
	s_mov_b64 exec, -1
	s_mov_b64 exec, s[78:79]
	buffer_load_dwordx4 v[142:145], v223, s[16:19], 0 offen offset:2048
	buffer_load_dwordx4 v[2:5], v223, s[16:19], 0 offen offset:2560
	s_mov_b64 exec, -1
	s_load_dwordx2 s[4:5], s[22:23], 0x20
	s_waitcnt lgkmcnt(0)
	s_load_dwordx2 s[26:27], s[4:5], 0x0
	s_load_dword s31, s[4:5], 0x8
	s_waitcnt lgkmcnt(0)
	v_cvt_f16_f32_e32 v183, s27
	v_cvt_f16_f32_e32 v185, s26
	v_cvt_f16_f32_e32 v184, s31
	s_mov_b64 s[4:5], 0
	s_waitcnt vmcnt(18)
	v_pk_mul_f16 v193, v185, v189 op_sel_hi:[0,1]
	v_pk_mul_f16 v197, v183, v189 op_sel_hi:[0,1]
	v_pk_mul_f16 v201, v184, v189 op_sel_hi:[0,1]
	v_pk_mul_f16 v190, v185, v186 op_sel_hi:[0,1]
	v_pk_mul_f16 v191, v185, v187 op_sel_hi:[0,1]
	v_pk_mul_f16 v192, v185, v188 op_sel_hi:[0,1]
	v_pk_mul_f16 v194, v183, v186 op_sel_hi:[0,1]
	v_pk_mul_f16 v195, v183, v187 op_sel_hi:[0,1]
	v_pk_mul_f16 v196, v183, v188 op_sel_hi:[0,1]
	v_pk_mul_f16 v198, v184, v186 op_sel_hi:[0,1]
	v_pk_mul_f16 v199, v184, v187 op_sel_hi:[0,1]
	v_pk_mul_f16 v200, v184, v188 op_sel_hi:[0,1]
	v_pk_fma_f16 v113, v113, v189, v193
	v_pk_fma_f16 v129, v129, v189, v197
	v_pk_fma_f16 v137, v137, v189, v201
	v_pk_fma_f16 v202, v85, v189, v193
	v_pk_fma_f16 v206, v109, v189, v197
	v_pk_fma_f16 v210, v125, v189, v201
	v_pk_fma_f16 v193, v53, v189, v193
	v_pk_fma_f16 v197, v69, v189, v197
	v_pk_fma_f16 v189, v97, v189, v201
	v_pk_maximum3_f16 v201, v113, v129, v137
	v_pk_fma_f16 v112, v112, v188, v192
	v_pk_fma_f16 v111, v111, v187, v191
	v_pk_fma_f16 v110, v110, v186, v190
	v_pk_fma_f16 v128, v128, v188, v196
	v_pk_fma_f16 v127, v127, v187, v195
	v_pk_fma_f16 v126, v126, v186, v194
	v_pk_fma_f16 v136, v136, v188, v200
	v_pk_fma_f16 v135, v135, v187, v199
	v_pk_fma_f16 v134, v134, v186, v198
	v_pk_fma_f16 v203, v84, v188, v192
	v_pk_fma_f16 v204, v83, v187, v191
	v_pk_fma_f16 v205, v82, v186, v190
	v_pk_fma_f16 v207, v108, v188, v196
	v_pk_fma_f16 v208, v107, v187, v195
	v_pk_fma_f16 v209, v106, v186, v194
	v_pk_fma_f16 v211, v124, v188, v200
	v_pk_fma_f16 v212, v123, v187, v199
	v_pk_fma_f16 v213, v122, v186, v198
	v_pk_fma_f16 v192, v52, v188, v192
	v_pk_fma_f16 v191, v51, v187, v191
	v_pk_fma_f16 v190, v50, v186, v190
	v_pk_fma_f16 v196, v68, v188, v196
	v_pk_fma_f16 v195, v67, v187, v195
	v_pk_fma_f16 v194, v66, v186, v194
	v_pk_fma_f16 v188, v96, v188, v200
	v_pk_fma_f16 v187, v95, v187, v199
	v_pk_fma_f16 v186, v94, v186, v198
	v_pk_maximum3_f16 v198, v110, v126, v134
	v_pk_maximum3_f16 v199, v111, v127, v135
	v_pk_maximum3_f16 v200, v112, v128, v136
	v_pk_maximum3_f16 v217, v202, v206, v210
	v_pk_maximum3_f16 v221, v193, v197, v189
	v_pk_maximum3_f16 v214, v205, v209, v213
	v_pk_maximum3_f16 v215, v204, v208, v212
	v_pk_maximum3_f16 v216, v203, v207, v211
	s_nop 0
	v_pk_maximum3_f16 v218, v190, v194, v186
	v_pk_maximum3_f16 v219, v191, v195, v187
	v_pk_maximum3_f16 v201, v201, v217, v221
	v_pk_maximum3_f16 v220, v192, v196, v188
	s_nop 0
	v_pk_maximum3_f16 v198, v198, v214, v218
	v_pk_maximum3_f16 v199, v199, v215, v219
	v_pk_maximum3_f16 v200, v200, v216, v220
	v_xor_b32_e32 v201, 0x80008000, v201
	v_xor_b32_e32 v200, 0x80008000, v200
	v_xor_b32_e32 v199, 0x80008000, v199
	v_xor_b32_e32 v198, 0x80008000, v198
	v_pk_add_f16 v113, v113, v201
	v_pk_add_f16 v110, v110, v198
	v_pk_add_f16 v111, v111, v199
	v_pk_add_f16 v112, v112, v200
	v_pk_add_f16 v126, v126, v198
	v_exp_f16_sdwa v214, v110 dst_sel:WORD_0 dst_unused:UNUSED_PAD src0_sel:WORD_0
	v_exp_f16_sdwa v215, v111 dst_sel:WORD_0 dst_unused:UNUSED_PAD src0_sel:WORD_0
	v_exp_f16_sdwa v216, v112 dst_sel:WORD_0 dst_unused:UNUSED_PAD src0_sel:WORD_0
	v_exp_f16_sdwa v217, v113 dst_sel:WORD_0 dst_unused:UNUSED_PAD src0_sel:WORD_0
	v_exp_f16_sdwa v214, v110 dst_sel:WORD_1 dst_unused:UNUSED_PRESERVE src0_sel:WORD_1
	v_exp_f16_sdwa v215, v111 dst_sel:WORD_1 dst_unused:UNUSED_PRESERVE src0_sel:WORD_1
	v_exp_f16_sdwa v216, v112 dst_sel:WORD_1 dst_unused:UNUSED_PRESERVE src0_sel:WORD_1
	v_exp_f16_sdwa v217, v113 dst_sel:WORD_1 dst_unused:UNUSED_PRESERVE src0_sel:WORD_1
	s_nop 0
	v_pk_add_f16 v127, v127, v199
	v_pk_add_f16 v113, v214, 0
	v_pk_fma_f16 v73, v73, v217, 0
	v_pk_add_f16 v110, v217, 0
	v_pk_add_f16 v111, v216, 0
	v_pk_add_f16 v112, v215, 0
	v_pk_fma_f16 v72, v72, v216, 0
	v_pk_fma_f16 v71, v71, v215, 0
	v_pk_fma_f16 v70, v70, v214, 0
	v_pk_add_f16 v128, v128, v200
	v_pk_add_f16 v129, v129, v201
	s_nop 0
	v_exp_f16_sdwa v214, v126 dst_sel:WORD_0 dst_unused:UNUSED_PAD src0_sel:WORD_0
	v_exp_f16_sdwa v215, v127 dst_sel:WORD_0 dst_unused:UNUSED_PAD src0_sel:WORD_0
	v_exp_f16_sdwa v216, v128 dst_sel:WORD_0 dst_unused:UNUSED_PAD src0_sel:WORD_0
	v_exp_f16_sdwa v217, v129 dst_sel:WORD_0 dst_unused:UNUSED_PAD src0_sel:WORD_0
	v_exp_f16_sdwa v214, v126 dst_sel:WORD_1 dst_unused:UNUSED_PRESERVE src0_sel:WORD_1
	v_exp_f16_sdwa v215, v127 dst_sel:WORD_1 dst_unused:UNUSED_PRESERVE src0_sel:WORD_1
	v_exp_f16_sdwa v216, v128 dst_sel:WORD_1 dst_unused:UNUSED_PRESERVE src0_sel:WORD_1
	v_exp_f16_sdwa v217, v129 dst_sel:WORD_1 dst_unused:UNUSED_PRESERVE src0_sel:WORD_1
	s_nop 0
	s_nop 0
	v_pk_add_f16 v113, v113, v214
	v_pk_fma_f16 v73, v101, v217, v73
	v_pk_add_f16 v101, v137, v201
	v_pk_add_f16 v112, v112, v215
	v_pk_add_f16 v111, v111, v216
	v_pk_add_f16 v110, v110, v217
	v_pk_fma_f16 v70, v98, v214, v70
	v_pk_fma_f16 v71, v99, v215, v71
	v_pk_fma_f16 v72, v100, v216, v72
	v_pk_add_f16 v98, v134, v198
	v_pk_add_f16 v99, v135, v199
	v_pk_add_f16 v100, v136, v200
	s_nop 0
	v_exp_f16_sdwa v126, v98 dst_sel:WORD_0 dst_unused:UNUSED_PAD src0_sel:WORD_0
	v_exp_f16_sdwa v127, v99 dst_sel:WORD_0 dst_unused:UNUSED_PAD src0_sel:WORD_0
	v_exp_f16_sdwa v128, v100 dst_sel:WORD_0 dst_unused:UNUSED_PAD src0_sel:WORD_0
	v_exp_f16_sdwa v129, v101 dst_sel:WORD_0 dst_unused:UNUSED_PAD src0_sel:WORD_0
	v_exp_f16_sdwa v126, v98 dst_sel:WORD_1 dst_unused:UNUSED_PRESERVE src0_sel:WORD_1
	v_exp_f16_sdwa v127, v99 dst_sel:WORD_1 dst_unused:UNUSED_PRESERVE src0_sel:WORD_1
	v_exp_f16_sdwa v128, v100 dst_sel:WORD_1 dst_unused:UNUSED_PRESERVE src0_sel:WORD_1
	v_exp_f16_sdwa v129, v101 dst_sel:WORD_1 dst_unused:UNUSED_PRESERVE src0_sel:WORD_1
	s_nop 0
	s_nop 0
	v_pk_add_f16 v101, v113, v126
	v_pk_add_f16 v98, v110, v129
	v_pk_add_f16 v99, v111, v128
	v_pk_add_f16 v100, v112, v127
	v_pk_fma_f16 v73, v117, v129, v73
	v_pk_fma_f16 v72, v116, v128, v72
	v_pk_fma_f16 v71, v115, v127, v71
	v_pk_fma_f16 v70, v114, v126, v70
	v_pk_add_f16 v110, v205, v198
	v_pk_add_f16 v111, v204, v199
	v_pk_add_f16 v112, v203, v200
	v_pk_add_f16 v113, v202, v201
	s_nop 0
	v_exp_f16_sdwa v114, v110 dst_sel:WORD_0 dst_unused:UNUSED_PAD src0_sel:WORD_0
	v_exp_f16_sdwa v115, v111 dst_sel:WORD_0 dst_unused:UNUSED_PAD src0_sel:WORD_0
	v_exp_f16_sdwa v116, v112 dst_sel:WORD_0 dst_unused:UNUSED_PAD src0_sel:WORD_0
	v_exp_f16_sdwa v117, v113 dst_sel:WORD_0 dst_unused:UNUSED_PAD src0_sel:WORD_0
	v_exp_f16_sdwa v114, v110 dst_sel:WORD_1 dst_unused:UNUSED_PRESERVE src0_sel:WORD_1
	v_exp_f16_sdwa v115, v111 dst_sel:WORD_1 dst_unused:UNUSED_PRESERVE src0_sel:WORD_1
	v_exp_f16_sdwa v116, v112 dst_sel:WORD_1 dst_unused:UNUSED_PRESERVE src0_sel:WORD_1
	v_exp_f16_sdwa v117, v113 dst_sel:WORD_1 dst_unused:UNUSED_PRESERVE src0_sel:WORD_1
	s_nop 0
	v_pk_add_f16 v110, v209, v198
	v_pk_add_f16 v101, v101, v114
	v_pk_add_f16 v100, v100, v115
	v_pk_add_f16 v99, v99, v116
	v_pk_add_f16 v98, v98, v117
	v_pk_fma_f16 v70, v42, v114, v70
	v_pk_fma_f16 v71, v43, v115, v71
	v_pk_fma_f16 v72, v44, v116, v72
	v_pk_fma_f16 v73, v45, v117, v73
	v_pk_add_f16 v111, v208, v199
	v_pk_add_f16 v112, v207, v200
	v_pk_add_f16 v113, v206, v201
	s_nop 0
	v_exp_f16_sdwa v114, v110 dst_sel:WORD_0 dst_unused:UNUSED_PAD src0_sel:WORD_0
	v_exp_f16_sdwa v115, v111 dst_sel:WORD_0 dst_unused:UNUSED_PAD src0_sel:WORD_0
	v_exp_f16_sdwa v116, v112 dst_sel:WORD_0 dst_unused:UNUSED_PAD src0_sel:WORD_0
	v_exp_f16_sdwa v117, v113 dst_sel:WORD_0 dst_unused:UNUSED_PAD src0_sel:WORD_0
	v_exp_f16_sdwa v114, v110 dst_sel:WORD_1 dst_unused:UNUSED_PRESERVE src0_sel:WORD_1
	v_exp_f16_sdwa v115, v111 dst_sel:WORD_1 dst_unused:UNUSED_PRESERVE src0_sel:WORD_1
	v_exp_f16_sdwa v116, v112 dst_sel:WORD_1 dst_unused:UNUSED_PRESERVE src0_sel:WORD_1
	v_exp_f16_sdwa v117, v113 dst_sel:WORD_1 dst_unused:UNUSED_PRESERVE src0_sel:WORD_1
	s_nop 0
	v_pk_add_f16 v110, v213, v198
	v_pk_add_f16 v101, v101, v114
	v_pk_add_f16 v98, v98, v117
	v_pk_add_f16 v99, v99, v116
	v_pk_add_f16 v100, v100, v115
	v_pk_fma_f16 v73, v65, v117, v73
	v_pk_fma_f16 v72, v64, v116, v72
	v_pk_fma_f16 v71, v63, v115, v71
	v_pk_fma_f16 v70, v62, v114, v70
	v_pk_add_f16 v111, v212, v199
	v_pk_add_f16 v112, v211, v200
	v_pk_add_f16 v113, v210, v201
	s_nop 0
	v_exp_f16_sdwa v114, v110 dst_sel:WORD_0 dst_unused:UNUSED_PAD src0_sel:WORD_0
	v_exp_f16_sdwa v115, v111 dst_sel:WORD_0 dst_unused:UNUSED_PAD src0_sel:WORD_0
	v_exp_f16_sdwa v116, v112 dst_sel:WORD_0 dst_unused:UNUSED_PAD src0_sel:WORD_0
	v_exp_f16_sdwa v117, v113 dst_sel:WORD_0 dst_unused:UNUSED_PAD src0_sel:WORD_0
	v_exp_f16_sdwa v114, v110 dst_sel:WORD_1 dst_unused:UNUSED_PRESERVE src0_sel:WORD_1
	v_exp_f16_sdwa v115, v111 dst_sel:WORD_1 dst_unused:UNUSED_PRESERVE src0_sel:WORD_1
	v_exp_f16_sdwa v116, v112 dst_sel:WORD_1 dst_unused:UNUSED_PRESERVE src0_sel:WORD_1
	v_exp_f16_sdwa v117, v113 dst_sel:WORD_1 dst_unused:UNUSED_PRESERVE src0_sel:WORD_1
	s_nop 0
	v_pk_add_f16 v110, v190, v198
	v_pk_add_f16 v101, v101, v114
	v_pk_add_f16 v100, v100, v115
	v_pk_add_f16 v99, v99, v116
	v_pk_add_f16 v98, v98, v117
	v_pk_fma_f16 v70, v86, v114, v70
	v_pk_fma_f16 v71, v87, v115, v71
	v_pk_fma_f16 v72, v88, v116, v72
	v_pk_fma_f16 v73, v89, v117, v73
	v_pk_add_f16 v111, v191, v199
	v_pk_add_f16 v112, v192, v200
	v_pk_add_f16 v113, v193, v201
	s_nop 0
	v_exp_f16_sdwa v114, v110 dst_sel:WORD_0 dst_unused:UNUSED_PAD src0_sel:WORD_0
	v_exp_f16_sdwa v115, v111 dst_sel:WORD_0 dst_unused:UNUSED_PAD src0_sel:WORD_0
	v_exp_f16_sdwa v116, v112 dst_sel:WORD_0 dst_unused:UNUSED_PAD src0_sel:WORD_0
	v_exp_f16_sdwa v117, v113 dst_sel:WORD_0 dst_unused:UNUSED_PAD src0_sel:WORD_0
	v_exp_f16_sdwa v114, v110 dst_sel:WORD_1 dst_unused:UNUSED_PRESERVE src0_sel:WORD_1
	v_exp_f16_sdwa v115, v111 dst_sel:WORD_1 dst_unused:UNUSED_PRESERVE src0_sel:WORD_1
	v_exp_f16_sdwa v116, v112 dst_sel:WORD_1 dst_unused:UNUSED_PRESERVE src0_sel:WORD_1
	v_exp_f16_sdwa v117, v113 dst_sel:WORD_1 dst_unused:UNUSED_PRESERVE src0_sel:WORD_1
	s_nop 0
	v_pk_add_f16 v110, v194, v198
	v_pk_add_f16 v101, v101, v114
	v_pk_add_f16 v98, v98, v117
	v_pk_add_f16 v99, v99, v116
	v_pk_add_f16 v100, v100, v115
	v_pk_fma_f16 v73, v25, v117, v73
	v_pk_fma_f16 v72, v24, v116, v72
	v_pk_fma_f16 v71, v23, v115, v71
	v_pk_fma_f16 v70, v22, v114, v70
	v_pk_add_f16 v111, v195, v199
	v_pk_add_f16 v112, v196, v200
	v_pk_add_f16 v113, v197, v201
	s_nop 0
	v_exp_f16_sdwa v114, v110 dst_sel:WORD_0 dst_unused:UNUSED_PAD src0_sel:WORD_0
	v_exp_f16_sdwa v115, v111 dst_sel:WORD_0 dst_unused:UNUSED_PAD src0_sel:WORD_0
	v_exp_f16_sdwa v116, v112 dst_sel:WORD_0 dst_unused:UNUSED_PAD src0_sel:WORD_0
	v_exp_f16_sdwa v117, v113 dst_sel:WORD_0 dst_unused:UNUSED_PAD src0_sel:WORD_0
	v_exp_f16_sdwa v114, v110 dst_sel:WORD_1 dst_unused:UNUSED_PRESERVE src0_sel:WORD_1
	v_exp_f16_sdwa v115, v111 dst_sel:WORD_1 dst_unused:UNUSED_PRESERVE src0_sel:WORD_1
	v_exp_f16_sdwa v116, v112 dst_sel:WORD_1 dst_unused:UNUSED_PRESERVE src0_sel:WORD_1
	v_exp_f16_sdwa v117, v113 dst_sel:WORD_1 dst_unused:UNUSED_PRESERVE src0_sel:WORD_1
	s_nop 0
	v_pk_add_f16 v110, v186, v198
	v_pk_add_f16 v101, v101, v114
	v_pk_add_f16 v100, v100, v115
	v_pk_add_f16 v99, v99, v116
	v_pk_add_f16 v98, v98, v117
	v_pk_fma_f16 v70, v30, v114, v70
	v_pk_fma_f16 v71, v31, v115, v71
	v_pk_fma_f16 v72, v32, v116, v72
	v_pk_fma_f16 v73, v33, v117, v73
	v_pk_add_f16 v111, v187, v199
	v_pk_add_f16 v112, v188, v200
	v_pk_add_f16 v113, v189, v201
	s_nop 0
	v_exp_f16_sdwa v114, v110 dst_sel:WORD_0 dst_unused:UNUSED_PAD src0_sel:WORD_0
	v_exp_f16_sdwa v115, v111 dst_sel:WORD_0 dst_unused:UNUSED_PAD src0_sel:WORD_0
	v_exp_f16_sdwa v116, v112 dst_sel:WORD_0 dst_unused:UNUSED_PAD src0_sel:WORD_0
	v_exp_f16_sdwa v117, v113 dst_sel:WORD_0 dst_unused:UNUSED_PAD src0_sel:WORD_0
	v_exp_f16_sdwa v114, v110 dst_sel:WORD_1 dst_unused:UNUSED_PRESERVE src0_sel:WORD_1
	v_exp_f16_sdwa v115, v111 dst_sel:WORD_1 dst_unused:UNUSED_PRESERVE src0_sel:WORD_1
	v_exp_f16_sdwa v116, v112 dst_sel:WORD_1 dst_unused:UNUSED_PRESERVE src0_sel:WORD_1
	v_exp_f16_sdwa v117, v113 dst_sel:WORD_1 dst_unused:UNUSED_PRESERVE src0_sel:WORD_1
	s_nop 0
	s_nop 0
	v_pk_add_f16 v101, v101, v114
	v_pk_add_f16 v100, v100, v115
	v_rcp_f16_e32 v110, v101
	v_rcp_f16_sdwa v101, v101 dst_sel:DWORD dst_unused:UNUSED_PAD src0_sel:WORD_1
	v_pk_add_f16 v99, v99, v116
	v_rcp_f16_e32 v111, v100
	v_rcp_f16_sdwa v100, v100 dst_sel:DWORD dst_unused:UNUSED_PAD src0_sel:WORD_1
	v_pk_add_f16 v98, v98, v117
	v_rcp_f16_e32 v112, v99
	v_rcp_f16_sdwa v99, v99 dst_sel:DWORD dst_unused:UNUSED_PAD src0_sel:WORD_1
	v_rcp_f16_e32 v113, v98
	v_rcp_f16_sdwa v98, v98 dst_sel:DWORD dst_unused:UNUSED_PAD src0_sel:WORD_1
	v_pk_fma_f16 v70, v46, v114, v70
	v_pack_b32_f16 v101, v110, v101
	v_pk_fma_f16 v71, v47, v115, v71
	v_pk_mul_f16 v110, v70, v101
	v_pack_b32_f16 v70, v111, v100
	v_pk_fma_f16 v72, v48, v116, v72
	v_pk_mul_f16 v111, v71, v70
	v_pack_b32_f16 v70, v112, v99
	v_pk_fma_f16 v73, v49, v117, v73
	v_pk_mul_f16 v112, v72, v70
	v_pack_b32_f16 v70, v113, v98
	v_pk_mul_f16 v113, v73, v70
	s_waitcnt vmcnt(12)
	v_pk_mul_f16 v70, v185, v154 op_sel_hi:[0,1]
	v_pk_mul_f16 v98, v183, v154 op_sel_hi:[0,1]
	v_pk_mul_f16 v114, v184, v154 op_sel_hi:[0,1]
	v_pk_mul_f16 v71, v185, v155 op_sel_hi:[0,1]
	v_pk_mul_f16 v72, v185, v156 op_sel_hi:[0,1]
	v_pk_mul_f16 v73, v185, v157 op_sel_hi:[0,1]
	v_pk_mul_f16 v99, v183, v155 op_sel_hi:[0,1]
	v_pk_mul_f16 v100, v183, v156 op_sel_hi:[0,1]
	v_pk_mul_f16 v101, v183, v157 op_sel_hi:[0,1]
	v_pk_mul_f16 v115, v184, v155 op_sel_hi:[0,1]
	v_pk_mul_f16 v116, v184, v156 op_sel_hi:[0,1]
	v_pk_mul_f16 v117, v184, v157 op_sel_hi:[0,1]
	v_pk_fma_f16 v82, v82, v154, v70
	v_pk_fma_f16 v106, v106, v154, v98
	v_pk_fma_f16 v122, v122, v154, v114
	v_pk_fma_f16 v129, v50, v154, v70
	v_pk_fma_f16 v137, v66, v154, v98
	v_pk_fma_f16 v189, v94, v154, v114
	v_pk_fma_f16 v70, v18, v154, v70
	v_pk_fma_f16 v98, v34, v154, v98
	v_pk_fma_f16 v114, v54, v154, v114
	v_pk_maximum3_f16 v154, v82, v106, v122
	v_pk_fma_f16 v85, v85, v157, v73
	v_pk_fma_f16 v84, v84, v156, v72
	v_pk_fma_f16 v83, v83, v155, v71
	v_pk_fma_f16 v109, v109, v157, v101
	v_pk_fma_f16 v108, v108, v156, v100
	v_pk_fma_f16 v107, v107, v155, v99
	v_pk_fma_f16 v125, v125, v157, v117
	v_pk_fma_f16 v124, v124, v156, v116
	v_pk_fma_f16 v123, v123, v155, v115
	v_pk_fma_f16 v126, v53, v157, v73
	v_pk_fma_f16 v127, v52, v156, v72
	v_pk_fma_f16 v128, v51, v155, v71
	v_pk_fma_f16 v134, v69, v157, v101
	v_pk_fma_f16 v135, v68, v156, v100
	v_pk_fma_f16 v136, v67, v155, v99
	v_pk_fma_f16 v186, v97, v157, v117
	v_pk_fma_f16 v187, v96, v156, v116
	v_pk_fma_f16 v188, v95, v155, v115
	v_pk_fma_f16 v73, v21, v157, v73
	v_pk_fma_f16 v72, v20, v156, v72
	v_pk_fma_f16 v71, v19, v155, v71
	v_pk_fma_f16 v101, v37, v157, v101
	v_pk_fma_f16 v100, v36, v156, v100
	v_pk_fma_f16 v99, v35, v155, v99
	v_pk_fma_f16 v117, v57, v157, v117
	v_pk_fma_f16 v116, v56, v156, v116
	v_pk_fma_f16 v115, v55, v155, v115
	v_pk_maximum3_f16 v155, v83, v107, v123
	v_pk_maximum3_f16 v156, v84, v108, v124
	v_pk_maximum3_f16 v157, v85, v109, v125
	v_pk_maximum3_f16 v190, v129, v137, v189
	v_pk_maximum3_f16 v194, v70, v98, v114
	v_pk_maximum3_f16 v191, v128, v136, v188
	v_pk_maximum3_f16 v192, v127, v135, v187
	v_pk_maximum3_f16 v193, v126, v134, v186
	s_nop 0
	v_pk_maximum3_f16 v195, v71, v99, v115
	v_pk_maximum3_f16 v196, v72, v100, v116
	v_pk_maximum3_f16 v154, v154, v190, v194
	v_pk_maximum3_f16 v197, v73, v101, v117
	s_nop 0
	v_pk_maximum3_f16 v155, v155, v191, v195
	v_pk_maximum3_f16 v156, v156, v192, v196
	v_pk_maximum3_f16 v157, v157, v193, v197
	v_xor_b32_e32 v154, 0x80008000, v154
	v_xor_b32_e32 v157, 0x80008000, v157
	v_xor_b32_e32 v156, 0x80008000, v156
	v_xor_b32_e32 v155, 0x80008000, v155
	v_pk_add_f16 v82, v82, v154
	v_pk_add_f16 v83, v83, v155
	v_pk_add_f16 v84, v84, v156
	v_pk_add_f16 v85, v85, v157
	v_pk_add_f16 v106, v106, v154
	v_exp_f16_sdwa v190, v82 dst_sel:WORD_0 dst_unused:UNUSED_PAD src0_sel:WORD_0
	v_exp_f16_sdwa v191, v83 dst_sel:WORD_0 dst_unused:UNUSED_PAD src0_sel:WORD_0
	v_exp_f16_sdwa v192, v84 dst_sel:WORD_0 dst_unused:UNUSED_PAD src0_sel:WORD_0
	v_exp_f16_sdwa v193, v85 dst_sel:WORD_0 dst_unused:UNUSED_PAD src0_sel:WORD_0
	v_exp_f16_sdwa v190, v82 dst_sel:WORD_1 dst_unused:UNUSED_PRESERVE src0_sel:WORD_1
	v_exp_f16_sdwa v191, v83 dst_sel:WORD_1 dst_unused:UNUSED_PRESERVE src0_sel:WORD_1
	v_exp_f16_sdwa v192, v84 dst_sel:WORD_1 dst_unused:UNUSED_PRESERVE src0_sel:WORD_1
	v_exp_f16_sdwa v193, v85 dst_sel:WORD_1 dst_unused:UNUSED_PRESERVE src0_sel:WORD_1
	s_nop 0
	v_pk_add_f16 v107, v107, v155
	v_pk_add_f16 v82, v193, 0
	v_pk_fma_f16 v42, v42, v190, 0
	v_pk_add_f16 v83, v192, 0
	v_pk_add_f16 v84, v191, 0
	v_pk_add_f16 v85, v190, 0
	v_pk_fma_f16 v45, v45, v193, 0
	v_pk_fma_f16 v44, v44, v192, 0
	v_pk_fma_f16 v43, v43, v191, 0
	v_pk_add_f16 v108, v108, v156
	v_pk_add_f16 v109, v109, v157
	v_pk_add_f16 v70, v70, v154
	v_exp_f16_sdwa v190, v106 dst_sel:WORD_0 dst_unused:UNUSED_PAD src0_sel:WORD_0
	v_exp_f16_sdwa v191, v107 dst_sel:WORD_0 dst_unused:UNUSED_PAD src0_sel:WORD_0
	v_exp_f16_sdwa v192, v108 dst_sel:WORD_0 dst_unused:UNUSED_PAD src0_sel:WORD_0
	v_exp_f16_sdwa v193, v109 dst_sel:WORD_0 dst_unused:UNUSED_PAD src0_sel:WORD_0
	v_exp_f16_sdwa v190, v106 dst_sel:WORD_1 dst_unused:UNUSED_PRESERVE src0_sel:WORD_1
	v_exp_f16_sdwa v191, v107 dst_sel:WORD_1 dst_unused:UNUSED_PRESERVE src0_sel:WORD_1
	v_exp_f16_sdwa v192, v108 dst_sel:WORD_1 dst_unused:UNUSED_PRESERVE src0_sel:WORD_1
	v_exp_f16_sdwa v193, v109 dst_sel:WORD_1 dst_unused:UNUSED_PRESERVE src0_sel:WORD_1
	s_nop 0
	v_pk_add_f16 v71, v71, v155
	v_pk_add_f16 v82, v82, v193
	v_pk_fma_f16 v42, v62, v190, v42
	v_pk_add_f16 v62, v122, v154
	v_pk_add_f16 v85, v85, v190
	v_pk_add_f16 v84, v84, v191
	v_pk_add_f16 v83, v83, v192
	v_pk_fma_f16 v43, v63, v191, v43
	v_pk_fma_f16 v44, v64, v192, v44
	v_pk_fma_f16 v45, v65, v193, v45
	v_pk_add_f16 v63, v123, v155
	v_pk_add_f16 v64, v124, v156
	v_pk_add_f16 v65, v125, v157
	v_pk_add_f16 v72, v72, v156
	v_exp_f16_sdwa v106, v62 dst_sel:WORD_0 dst_unused:UNUSED_PAD src0_sel:WORD_0
	v_exp_f16_sdwa v107, v63 dst_sel:WORD_0 dst_unused:UNUSED_PAD src0_sel:WORD_0
	v_exp_f16_sdwa v108, v64 dst_sel:WORD_0 dst_unused:UNUSED_PAD src0_sel:WORD_0
	v_exp_f16_sdwa v109, v65 dst_sel:WORD_0 dst_unused:UNUSED_PAD src0_sel:WORD_0
	v_exp_f16_sdwa v106, v62 dst_sel:WORD_1 dst_unused:UNUSED_PRESERVE src0_sel:WORD_1
	v_exp_f16_sdwa v107, v63 dst_sel:WORD_1 dst_unused:UNUSED_PRESERVE src0_sel:WORD_1
	v_exp_f16_sdwa v108, v64 dst_sel:WORD_1 dst_unused:UNUSED_PRESERVE src0_sel:WORD_1
	v_exp_f16_sdwa v109, v65 dst_sel:WORD_1 dst_unused:UNUSED_PRESERVE src0_sel:WORD_1
	s_nop 0
	v_pk_add_f16 v73, v73, v157
	v_pk_add_f16 v62, v82, v109
	v_pk_add_f16 v63, v83, v108
	v_pk_add_f16 v64, v84, v107
	v_pk_add_f16 v65, v85, v106
	v_pk_fma_f16 v45, v89, v109, v45
	v_pk_fma_f16 v44, v88, v108, v44
	v_pk_fma_f16 v43, v87, v107, v43
	v_pk_fma_f16 v42, v86, v106, v42
	v_pk_add_f16 v82, v129, v154
	v_pk_add_f16 v83, v128, v155
	v_pk_add_f16 v84, v127, v156
	v_pk_add_f16 v85, v126, v157
	s_nop 0
	v_exp_f16_sdwa v86, v82 dst_sel:WORD_0 dst_unused:UNUSED_PAD src0_sel:WORD_0
	v_exp_f16_sdwa v87, v83 dst_sel:WORD_0 dst_unused:UNUSED_PAD src0_sel:WORD_0
	v_exp_f16_sdwa v88, v84 dst_sel:WORD_0 dst_unused:UNUSED_PAD src0_sel:WORD_0
	v_exp_f16_sdwa v89, v85 dst_sel:WORD_0 dst_unused:UNUSED_PAD src0_sel:WORD_0
	v_exp_f16_sdwa v86, v82 dst_sel:WORD_1 dst_unused:UNUSED_PRESERVE src0_sel:WORD_1
	v_exp_f16_sdwa v87, v83 dst_sel:WORD_1 dst_unused:UNUSED_PRESERVE src0_sel:WORD_1
	v_exp_f16_sdwa v88, v84 dst_sel:WORD_1 dst_unused:UNUSED_PRESERVE src0_sel:WORD_1
	v_exp_f16_sdwa v89, v85 dst_sel:WORD_1 dst_unused:UNUSED_PRESERVE src0_sel:WORD_1
	s_nop 0
	v_pk_add_f16 v82, v137, v154
	v_pk_add_f16 v62, v62, v89
	v_pk_add_f16 v65, v65, v86
	v_pk_add_f16 v64, v64, v87
	v_pk_add_f16 v63, v63, v88
	v_pk_fma_f16 v42, v22, v86, v42
	v_pk_fma_f16 v43, v23, v87, v43
	v_pk_fma_f16 v44, v24, v88, v44
	v_pk_fma_f16 v45, v25, v89, v45
	v_pk_add_f16 v83, v136, v155
	v_pk_add_f16 v84, v135, v156
	v_pk_add_f16 v85, v134, v157
	s_nop 0
	v_exp_f16_sdwa v86, v82 dst_sel:WORD_0 dst_unused:UNUSED_PAD src0_sel:WORD_0
	v_exp_f16_sdwa v87, v83 dst_sel:WORD_0 dst_unused:UNUSED_PAD src0_sel:WORD_0
	v_exp_f16_sdwa v88, v84 dst_sel:WORD_0 dst_unused:UNUSED_PAD src0_sel:WORD_0
	v_exp_f16_sdwa v89, v85 dst_sel:WORD_0 dst_unused:UNUSED_PAD src0_sel:WORD_0
	v_exp_f16_sdwa v86, v82 dst_sel:WORD_1 dst_unused:UNUSED_PRESERVE src0_sel:WORD_1
	v_exp_f16_sdwa v87, v83 dst_sel:WORD_1 dst_unused:UNUSED_PRESERVE src0_sel:WORD_1
	v_exp_f16_sdwa v88, v84 dst_sel:WORD_1 dst_unused:UNUSED_PRESERVE src0_sel:WORD_1
	v_exp_f16_sdwa v89, v85 dst_sel:WORD_1 dst_unused:UNUSED_PRESERVE src0_sel:WORD_1
	s_nop 0
	v_pk_add_f16 v82, v189, v154
	v_pk_add_f16 v62, v62, v89
	v_pk_add_f16 v63, v63, v88
	v_pk_add_f16 v64, v64, v87
	v_pk_add_f16 v65, v65, v86
	v_pk_fma_f16 v45, v33, v89, v45
	v_pk_fma_f16 v44, v32, v88, v44
	v_pk_fma_f16 v43, v31, v87, v43
	v_pk_fma_f16 v42, v30, v86, v42
	v_pk_add_f16 v83, v188, v155
	v_pk_add_f16 v84, v187, v156
	v_pk_add_f16 v85, v186, v157
	s_nop 0
	v_exp_f16_sdwa v86, v82 dst_sel:WORD_0 dst_unused:UNUSED_PAD src0_sel:WORD_0
	v_exp_f16_sdwa v87, v83 dst_sel:WORD_0 dst_unused:UNUSED_PAD src0_sel:WORD_0
	v_exp_f16_sdwa v88, v84 dst_sel:WORD_0 dst_unused:UNUSED_PAD src0_sel:WORD_0
	v_exp_f16_sdwa v89, v85 dst_sel:WORD_0 dst_unused:UNUSED_PAD src0_sel:WORD_0
	v_exp_f16_sdwa v86, v82 dst_sel:WORD_1 dst_unused:UNUSED_PRESERVE src0_sel:WORD_1
	v_exp_f16_sdwa v87, v83 dst_sel:WORD_1 dst_unused:UNUSED_PRESERVE src0_sel:WORD_1
	v_exp_f16_sdwa v88, v84 dst_sel:WORD_1 dst_unused:UNUSED_PRESERVE src0_sel:WORD_1
	v_exp_f16_sdwa v89, v85 dst_sel:WORD_1 dst_unused:UNUSED_PRESERVE src0_sel:WORD_1
	s_nop 0
	v_exp_f16_sdwa v82, v70 dst_sel:WORD_0 dst_unused:UNUSED_PAD src0_sel:WORD_0
	v_exp_f16_sdwa v83, v71 dst_sel:WORD_0 dst_unused:UNUSED_PAD src0_sel:WORD_0
	v_exp_f16_sdwa v84, v72 dst_sel:WORD_0 dst_unused:UNUSED_PAD src0_sel:WORD_0
	v_exp_f16_sdwa v85, v73 dst_sel:WORD_0 dst_unused:UNUSED_PAD src0_sel:WORD_0
	v_exp_f16_sdwa v82, v70 dst_sel:WORD_1 dst_unused:UNUSED_PRESERVE src0_sel:WORD_1
	v_exp_f16_sdwa v83, v71 dst_sel:WORD_1 dst_unused:UNUSED_PRESERVE src0_sel:WORD_1
	v_exp_f16_sdwa v84, v72 dst_sel:WORD_1 dst_unused:UNUSED_PRESERVE src0_sel:WORD_1
	v_exp_f16_sdwa v85, v73 dst_sel:WORD_1 dst_unused:UNUSED_PRESERVE src0_sel:WORD_1
	s_nop 0
	v_pk_add_f16 v70, v98, v154
	v_pk_add_f16 v62, v62, v89
	v_pk_add_f16 v65, v65, v86
	v_pk_add_f16 v64, v64, v87
	v_pk_add_f16 v63, v63, v88
	v_pk_fma_f16 v42, v46, v86, v42
	v_pk_fma_f16 v43, v47, v87, v43
	v_pk_fma_f16 v44, v48, v88, v44
	v_pk_fma_f16 v45, v49, v89, v45
	v_pk_add_f16 v62, v62, v85
	v_pk_add_f16 v63, v63, v84
	v_pk_add_f16 v64, v64, v83
	v_pk_add_f16 v65, v65, v82
	v_pk_fma_f16 v45, v9, v85, v45
	v_pk_fma_f16 v44, v8, v84, v44
	v_pk_fma_f16 v43, v7, v83, v43
	v_pk_fma_f16 v42, v6, v82, v42
	v_pk_add_f16 v71, v99, v155
	v_pk_add_f16 v72, v100, v156
	v_pk_add_f16 v73, v101, v157
	s_nop 0
	v_exp_f16_sdwa v82, v70 dst_sel:WORD_0 dst_unused:UNUSED_PAD src0_sel:WORD_0
	v_exp_f16_sdwa v83, v71 dst_sel:WORD_0 dst_unused:UNUSED_PAD src0_sel:WORD_0
	v_exp_f16_sdwa v84, v72 dst_sel:WORD_0 dst_unused:UNUSED_PAD src0_sel:WORD_0
	v_exp_f16_sdwa v85, v73 dst_sel:WORD_0 dst_unused:UNUSED_PAD src0_sel:WORD_0
	v_exp_f16_sdwa v82, v70 dst_sel:WORD_1 dst_unused:UNUSED_PRESERVE src0_sel:WORD_1
	v_exp_f16_sdwa v83, v71 dst_sel:WORD_1 dst_unused:UNUSED_PRESERVE src0_sel:WORD_1
	v_exp_f16_sdwa v84, v72 dst_sel:WORD_1 dst_unused:UNUSED_PRESERVE src0_sel:WORD_1
	v_exp_f16_sdwa v85, v73 dst_sel:WORD_1 dst_unused:UNUSED_PRESERVE src0_sel:WORD_1
	s_nop 0
	v_pk_add_f16 v70, v114, v154
	v_pk_add_f16 v62, v62, v85
	v_pk_add_f16 v65, v65, v82
	v_pk_add_f16 v64, v64, v83
	v_pk_add_f16 v63, v63, v84
	v_pk_fma_f16 v42, v10, v82, v42
	v_pk_fma_f16 v43, v11, v83, v43
	v_pk_fma_f16 v44, v12, v84, v44
	v_pk_fma_f16 v45, v13, v85, v45
	v_pk_add_f16 v71, v115, v155
	v_pk_add_f16 v72, v116, v156
	v_pk_add_f16 v73, v117, v157
	s_nop 0
	v_exp_f16_sdwa v82, v70 dst_sel:WORD_0 dst_unused:UNUSED_PAD src0_sel:WORD_0
	v_exp_f16_sdwa v83, v71 dst_sel:WORD_0 dst_unused:UNUSED_PAD src0_sel:WORD_0
	v_exp_f16_sdwa v84, v72 dst_sel:WORD_0 dst_unused:UNUSED_PAD src0_sel:WORD_0
	v_exp_f16_sdwa v85, v73 dst_sel:WORD_0 dst_unused:UNUSED_PAD src0_sel:WORD_0
	v_exp_f16_sdwa v82, v70 dst_sel:WORD_1 dst_unused:UNUSED_PRESERVE src0_sel:WORD_1
	v_exp_f16_sdwa v83, v71 dst_sel:WORD_1 dst_unused:UNUSED_PRESERVE src0_sel:WORD_1
	v_exp_f16_sdwa v84, v72 dst_sel:WORD_1 dst_unused:UNUSED_PRESERVE src0_sel:WORD_1
	v_exp_f16_sdwa v85, v73 dst_sel:WORD_1 dst_unused:UNUSED_PRESERVE src0_sel:WORD_1
	s_nop 0
	s_nop 0
	v_pk_add_f16 v62, v62, v85
	v_pk_add_f16 v63, v63, v84
	v_pk_add_f16 v64, v64, v83
	v_pk_add_f16 v65, v65, v82
	v_rcp_f16_e32 v73, v62
	v_rcp_f16_sdwa v62, v62 dst_sel:DWORD dst_unused:UNUSED_PAD src0_sel:WORD_1
	v_rcp_f16_e32 v70, v65
	v_rcp_f16_sdwa v65, v65 dst_sel:DWORD dst_unused:UNUSED_PAD src0_sel:WORD_1
	v_rcp_f16_e32 v71, v64
	v_rcp_f16_sdwa v64, v64 dst_sel:DWORD dst_unused:UNUSED_PAD src0_sel:WORD_1
	v_rcp_f16_e32 v72, v63
	v_rcp_f16_sdwa v63, v63 dst_sel:DWORD dst_unused:UNUSED_PAD src0_sel:WORD_1
	v_pk_fma_f16 v45, v17, v85, v45
	v_pack_b32_f16 v62, v73, v62
	v_pk_fma_f16 v44, v16, v84, v44
	v_pk_fma_f16 v43, v15, v83, v43
	v_pk_fma_f16 v42, v14, v82, v42
	v_pack_b32_f16 v65, v70, v65
	v_pack_b32_f16 v64, v71, v64
	v_pack_b32_f16 v63, v72, v63
	v_pk_mul_f16 v45, v45, v62
	s_waitcnt vmcnt(6)
	v_pk_mul_f16 v62, v185, v150 op_sel_hi:[0,1]
	v_pk_mul_f16 v70, v183, v150 op_sel_hi:[0,1]
	v_pk_mul_f16 v82, v184, v150 op_sel_hi:[0,1]
	v_pk_mul_f16 v42, v42, v65
	v_pk_mul_f16 v43, v43, v64
	v_pk_mul_f16 v44, v44, v63
	v_pk_mul_f16 v63, v185, v151 op_sel_hi:[0,1]
	v_pk_mul_f16 v64, v185, v152 op_sel_hi:[0,1]
	v_pk_mul_f16 v65, v185, v153 op_sel_hi:[0,1]
	v_pk_mul_f16 v71, v183, v151 op_sel_hi:[0,1]
	v_pk_mul_f16 v72, v183, v152 op_sel_hi:[0,1]
	v_pk_mul_f16 v73, v183, v153 op_sel_hi:[0,1]
	v_pk_mul_f16 v83, v184, v151 op_sel_hi:[0,1]
	v_pk_mul_f16 v84, v184, v152 op_sel_hi:[0,1]
	v_pk_mul_f16 v85, v184, v153 op_sel_hi:[0,1]
	v_pk_fma_f16 v50, v50, v150, v62
	v_pk_fma_f16 v66, v66, v150, v70
	v_pk_fma_f16 v89, v94, v150, v82
	v_pk_fma_f16 v53, v53, v153, v65
	v_pk_maximum3_f16 v114, v50, v66, v89
	v_pk_fma_f16 v52, v52, v152, v64
	v_pk_fma_f16 v51, v51, v151, v63
	v_pk_fma_f16 v69, v69, v153, v73
	v_pk_fma_f16 v68, v68, v152, v72
	v_pk_fma_f16 v67, v67, v151, v71
	v_pk_fma_f16 v86, v97, v153, v85
	v_pk_fma_f16 v87, v96, v152, v84
	v_pk_fma_f16 v88, v95, v151, v83
	v_pk_fma_f16 v97, v18, v150, v62
	v_pk_fma_f16 v101, v34, v150, v70
	v_pk_fma_f16 v109, v54, v150, v82
	v_pk_fma_f16 v62, v74, v150, v62
	v_pk_fma_f16 v70, v102, v150, v70
	v_pk_fma_f16 v82, v118, v150, v82
	v_pk_maximum3_f16 v115, v51, v67, v88
	v_pk_maximum3_f16 v116, v52, v68, v87
	v_pk_maximum3_f16 v117, v53, v69, v86
	v_pk_maximum3_f16 v122, v97, v101, v109
	v_pk_fma_f16 v94, v21, v153, v65
	v_pk_maximum3_f16 v126, v62, v70, v82
	v_pk_fma_f16 v95, v20, v152, v64
	v_pk_maximum3_f16 v114, v114, v122, v126
	v_pk_fma_f16 v96, v19, v151, v63
	v_pk_fma_f16 v98, v37, v153, v73
	v_pk_fma_f16 v99, v36, v152, v72
	v_pk_fma_f16 v100, v35, v151, v71
	v_pk_fma_f16 v106, v57, v153, v85
	v_pk_fma_f16 v107, v56, v152, v84
	v_pk_fma_f16 v108, v55, v151, v83
	v_pk_fma_f16 v65, v77, v153, v65
	v_pk_fma_f16 v64, v76, v152, v64
	v_pk_fma_f16 v63, v75, v151, v63
	v_pk_fma_f16 v73, v105, v153, v73
	v_pk_fma_f16 v72, v104, v152, v72
	v_pk_fma_f16 v71, v103, v151, v71
	v_pk_fma_f16 v85, v121, v153, v85
	v_pk_fma_f16 v84, v120, v152, v84
	v_pk_fma_f16 v83, v119, v151, v83
	v_pk_maximum3_f16 v123, v96, v100, v108
	v_pk_maximum3_f16 v124, v95, v99, v107
	v_pk_maximum3_f16 v125, v94, v98, v106
	v_pk_maximum3_f16 v128, v64, v72, v84
	v_pk_maximum3_f16 v129, v65, v73, v85
	s_nop 0
	v_pk_maximum3_f16 v127, v63, v71, v83
	v_xor_b32_e32 v114, 0x80008000, v114
	v_pk_maximum3_f16 v115, v115, v123, v127
	v_pk_maximum3_f16 v116, v116, v124, v128
	v_pk_maximum3_f16 v117, v117, v125, v129
	v_pk_add_f16 v50, v50, v114
	v_xor_b32_e32 v117, 0x80008000, v117
	v_xor_b32_e32 v116, 0x80008000, v116
	v_xor_b32_e32 v115, 0x80008000, v115
	v_pk_add_f16 v51, v51, v115
	v_pk_add_f16 v52, v52, v116
	v_pk_add_f16 v53, v53, v117
	v_pk_add_f16 v66, v66, v114
	v_exp_f16_sdwa v122, v50 dst_sel:WORD_0 dst_unused:UNUSED_PAD src0_sel:WORD_0
	v_exp_f16_sdwa v123, v51 dst_sel:WORD_0 dst_unused:UNUSED_PAD src0_sel:WORD_0
	v_exp_f16_sdwa v124, v52 dst_sel:WORD_0 dst_unused:UNUSED_PAD src0_sel:WORD_0
	v_exp_f16_sdwa v125, v53 dst_sel:WORD_0 dst_unused:UNUSED_PAD src0_sel:WORD_0
	v_exp_f16_sdwa v122, v50 dst_sel:WORD_1 dst_unused:UNUSED_PRESERVE src0_sel:WORD_1
	v_exp_f16_sdwa v123, v51 dst_sel:WORD_1 dst_unused:UNUSED_PRESERVE src0_sel:WORD_1
	v_exp_f16_sdwa v124, v52 dst_sel:WORD_1 dst_unused:UNUSED_PRESERVE src0_sel:WORD_1
	v_exp_f16_sdwa v125, v53 dst_sel:WORD_1 dst_unused:UNUSED_PRESERVE src0_sel:WORD_1
	s_nop 0
	v_pk_add_f16 v67, v67, v115
	v_pk_add_f16 v50, v125, 0
	v_pk_fma_f16 v22, v22, v122, 0
	v_pk_add_f16 v51, v124, 0
	v_pk_add_f16 v52, v123, 0
	v_pk_add_f16 v53, v122, 0
	v_pk_fma_f16 v23, v23, v123, 0
	v_pk_fma_f16 v24, v24, v124, 0
	v_pk_fma_f16 v25, v25, v125, 0
	v_pk_add_f16 v68, v68, v116
	v_pk_add_f16 v69, v69, v117
	s_nop 0
	v_exp_f16_sdwa v122, v66 dst_sel:WORD_0 dst_unused:UNUSED_PAD src0_sel:WORD_0
	v_exp_f16_sdwa v123, v67 dst_sel:WORD_0 dst_unused:UNUSED_PAD src0_sel:WORD_0
	v_exp_f16_sdwa v124, v68 dst_sel:WORD_0 dst_unused:UNUSED_PAD src0_sel:WORD_0
	v_exp_f16_sdwa v125, v69 dst_sel:WORD_0 dst_unused:UNUSED_PAD src0_sel:WORD_0
	v_exp_f16_sdwa v122, v66 dst_sel:WORD_1 dst_unused:UNUSED_PRESERVE src0_sel:WORD_1
	v_exp_f16_sdwa v123, v67 dst_sel:WORD_1 dst_unused:UNUSED_PRESERVE src0_sel:WORD_1
	v_exp_f16_sdwa v124, v68 dst_sel:WORD_1 dst_unused:UNUSED_PRESERVE src0_sel:WORD_1
	v_exp_f16_sdwa v125, v69 dst_sel:WORD_1 dst_unused:UNUSED_PRESERVE src0_sel:WORD_1
	s_nop 0
	s_nop 0
	v_pk_add_f16 v50, v50, v125
	v_pk_fma_f16 v22, v30, v122, v22
	v_pk_add_f16 v30, v89, v114
	v_pk_add_f16 v53, v53, v122
	v_pk_add_f16 v52, v52, v123
	v_pk_add_f16 v51, v51, v124
	v_pk_fma_f16 v25, v33, v125, v25
	v_pk_fma_f16 v24, v32, v124, v24
	v_pk_fma_f16 v23, v31, v123, v23
	v_pk_add_f16 v31, v88, v115
	v_pk_add_f16 v32, v87, v116
	v_pk_add_f16 v33, v86, v117
	s_nop 0
	v_exp_f16_sdwa v66, v30 dst_sel:WORD_0 dst_unused:UNUSED_PAD src0_sel:WORD_0
	v_exp_f16_sdwa v67, v31 dst_sel:WORD_0 dst_unused:UNUSED_PAD src0_sel:WORD_0
	v_exp_f16_sdwa v68, v32 dst_sel:WORD_0 dst_unused:UNUSED_PAD src0_sel:WORD_0
	v_exp_f16_sdwa v69, v33 dst_sel:WORD_0 dst_unused:UNUSED_PAD src0_sel:WORD_0
	v_exp_f16_sdwa v66, v30 dst_sel:WORD_1 dst_unused:UNUSED_PRESERVE src0_sel:WORD_1
	v_exp_f16_sdwa v67, v31 dst_sel:WORD_1 dst_unused:UNUSED_PRESERVE src0_sel:WORD_1
	v_exp_f16_sdwa v68, v32 dst_sel:WORD_1 dst_unused:UNUSED_PRESERVE src0_sel:WORD_1
	v_exp_f16_sdwa v69, v33 dst_sel:WORD_1 dst_unused:UNUSED_PRESERVE src0_sel:WORD_1
	s_nop 0
	s_nop 0
	v_pk_add_f16 v30, v50, v69
	v_pk_add_f16 v31, v51, v68
	v_pk_add_f16 v32, v52, v67
	v_pk_add_f16 v33, v53, v66
	v_pk_fma_f16 v22, v46, v66, v22
	v_pk_fma_f16 v23, v47, v67, v23
	v_pk_fma_f16 v24, v48, v68, v24
	v_pk_fma_f16 v25, v49, v69, v25
	v_pk_add_f16 v46, v97, v114
	v_pk_add_f16 v47, v96, v115
	v_pk_add_f16 v48, v95, v116
	v_pk_add_f16 v49, v94, v117
	s_nop 0
	v_exp_f16_sdwa v50, v46 dst_sel:WORD_0 dst_unused:UNUSED_PAD src0_sel:WORD_0
	v_exp_f16_sdwa v51, v47 dst_sel:WORD_0 dst_unused:UNUSED_PAD src0_sel:WORD_0
	v_exp_f16_sdwa v52, v48 dst_sel:WORD_0 dst_unused:UNUSED_PAD src0_sel:WORD_0
	v_exp_f16_sdwa v53, v49 dst_sel:WORD_0 dst_unused:UNUSED_PAD src0_sel:WORD_0
	v_exp_f16_sdwa v50, v46 dst_sel:WORD_1 dst_unused:UNUSED_PRESERVE src0_sel:WORD_1
	v_exp_f16_sdwa v51, v47 dst_sel:WORD_1 dst_unused:UNUSED_PRESERVE src0_sel:WORD_1
	v_exp_f16_sdwa v52, v48 dst_sel:WORD_1 dst_unused:UNUSED_PRESERVE src0_sel:WORD_1
	v_exp_f16_sdwa v53, v49 dst_sel:WORD_1 dst_unused:UNUSED_PRESERVE src0_sel:WORD_1
	s_nop 0
	v_pk_add_f16 v46, v101, v114
	v_pk_add_f16 v30, v30, v53
	v_pk_add_f16 v33, v33, v50
	v_pk_add_f16 v32, v32, v51
	v_pk_add_f16 v31, v31, v52
	v_pk_fma_f16 v25, v9, v53, v25
	v_pk_fma_f16 v24, v8, v52, v24
	v_pk_fma_f16 v23, v7, v51, v23
	v_pk_fma_f16 v22, v6, v50, v22
	v_pk_add_f16 v47, v100, v115
	v_pk_add_f16 v48, v99, v116
	v_pk_add_f16 v49, v98, v117
	s_nop 0
	v_exp_f16_sdwa v50, v46 dst_sel:WORD_0 dst_unused:UNUSED_PAD src0_sel:WORD_0
	v_exp_f16_sdwa v51, v47 dst_sel:WORD_0 dst_unused:UNUSED_PAD src0_sel:WORD_0
	v_exp_f16_sdwa v52, v48 dst_sel:WORD_0 dst_unused:UNUSED_PAD src0_sel:WORD_0
	v_exp_f16_sdwa v53, v49 dst_sel:WORD_0 dst_unused:UNUSED_PAD src0_sel:WORD_0
	v_exp_f16_sdwa v50, v46 dst_sel:WORD_1 dst_unused:UNUSED_PRESERVE src0_sel:WORD_1
	v_exp_f16_sdwa v51, v47 dst_sel:WORD_1 dst_unused:UNUSED_PRESERVE src0_sel:WORD_1
	v_exp_f16_sdwa v52, v48 dst_sel:WORD_1 dst_unused:UNUSED_PRESERVE src0_sel:WORD_1
	v_exp_f16_sdwa v53, v49 dst_sel:WORD_1 dst_unused:UNUSED_PRESERVE src0_sel:WORD_1
	s_nop 0
	v_pk_add_f16 v46, v109, v114
	v_pk_add_f16 v30, v30, v53
	v_pk_add_f16 v31, v31, v52
	v_pk_add_f16 v32, v32, v51
	v_pk_add_f16 v33, v33, v50
	v_pk_fma_f16 v22, v10, v50, v22
	v_pk_fma_f16 v23, v11, v51, v23
	v_pk_fma_f16 v24, v12, v52, v24
	v_pk_fma_f16 v25, v13, v53, v25
	v_pk_add_f16 v47, v108, v115
	v_pk_add_f16 v48, v107, v116
	v_pk_add_f16 v49, v106, v117
	s_nop 0
	v_exp_f16_sdwa v50, v46 dst_sel:WORD_0 dst_unused:UNUSED_PAD src0_sel:WORD_0
	v_exp_f16_sdwa v51, v47 dst_sel:WORD_0 dst_unused:UNUSED_PAD src0_sel:WORD_0
	v_exp_f16_sdwa v52, v48 dst_sel:WORD_0 dst_unused:UNUSED_PAD src0_sel:WORD_0
	v_exp_f16_sdwa v53, v49 dst_sel:WORD_0 dst_unused:UNUSED_PAD src0_sel:WORD_0
	v_exp_f16_sdwa v50, v46 dst_sel:WORD_1 dst_unused:UNUSED_PRESERVE src0_sel:WORD_1
	v_exp_f16_sdwa v51, v47 dst_sel:WORD_1 dst_unused:UNUSED_PRESERVE src0_sel:WORD_1
	v_exp_f16_sdwa v52, v48 dst_sel:WORD_1 dst_unused:UNUSED_PRESERVE src0_sel:WORD_1
	v_exp_f16_sdwa v53, v49 dst_sel:WORD_1 dst_unused:UNUSED_PRESERVE src0_sel:WORD_1
	s_nop 0
	v_pk_add_f16 v46, v62, v114
	v_pk_add_f16 v30, v30, v53
	v_pk_add_f16 v33, v33, v50
	v_pk_add_f16 v32, v32, v51
	v_pk_add_f16 v31, v31, v52
	v_pk_fma_f16 v25, v17, v53, v25
	v_pk_fma_f16 v24, v16, v52, v24
	v_pk_fma_f16 v23, v15, v51, v23
	v_pk_fma_f16 v22, v14, v50, v22
	v_pk_add_f16 v47, v63, v115
	v_pk_add_f16 v48, v64, v116
	v_pk_add_f16 v49, v65, v117
	s_nop 0
	v_exp_f16_sdwa v50, v46 dst_sel:WORD_0 dst_unused:UNUSED_PAD src0_sel:WORD_0
	v_exp_f16_sdwa v51, v47 dst_sel:WORD_0 dst_unused:UNUSED_PAD src0_sel:WORD_0
	v_exp_f16_sdwa v52, v48 dst_sel:WORD_0 dst_unused:UNUSED_PAD src0_sel:WORD_0
	v_exp_f16_sdwa v53, v49 dst_sel:WORD_0 dst_unused:UNUSED_PAD src0_sel:WORD_0
	v_exp_f16_sdwa v50, v46 dst_sel:WORD_1 dst_unused:UNUSED_PRESERVE src0_sel:WORD_1
	v_exp_f16_sdwa v51, v47 dst_sel:WORD_1 dst_unused:UNUSED_PRESERVE src0_sel:WORD_1
	v_exp_f16_sdwa v52, v48 dst_sel:WORD_1 dst_unused:UNUSED_PRESERVE src0_sel:WORD_1
	v_exp_f16_sdwa v53, v49 dst_sel:WORD_1 dst_unused:UNUSED_PRESERVE src0_sel:WORD_1
	s_nop 0
	v_pk_add_f16 v46, v70, v114
	v_pk_add_f16 v30, v30, v53
	v_pk_add_f16 v31, v31, v52
	v_pk_add_f16 v32, v32, v51
	v_pk_add_f16 v33, v33, v50
	v_pk_fma_f16 v22, v26, v50, v22
	v_pk_fma_f16 v23, v27, v51, v23
	v_pk_fma_f16 v24, v28, v52, v24
	v_pk_fma_f16 v25, v29, v53, v25
	v_pk_add_f16 v47, v71, v115
	v_pk_add_f16 v48, v72, v116
	v_pk_add_f16 v49, v73, v117
	s_nop 0
	v_exp_f16_sdwa v50, v46 dst_sel:WORD_0 dst_unused:UNUSED_PAD src0_sel:WORD_0
	v_exp_f16_sdwa v51, v47 dst_sel:WORD_0 dst_unused:UNUSED_PAD src0_sel:WORD_0
	v_exp_f16_sdwa v52, v48 dst_sel:WORD_0 dst_unused:UNUSED_PAD src0_sel:WORD_0
	v_exp_f16_sdwa v53, v49 dst_sel:WORD_0 dst_unused:UNUSED_PAD src0_sel:WORD_0
	v_exp_f16_sdwa v50, v46 dst_sel:WORD_1 dst_unused:UNUSED_PRESERVE src0_sel:WORD_1
	v_exp_f16_sdwa v51, v47 dst_sel:WORD_1 dst_unused:UNUSED_PRESERVE src0_sel:WORD_1
	v_exp_f16_sdwa v52, v48 dst_sel:WORD_1 dst_unused:UNUSED_PRESERVE src0_sel:WORD_1
	v_exp_f16_sdwa v53, v49 dst_sel:WORD_1 dst_unused:UNUSED_PRESERVE src0_sel:WORD_1
	s_nop 0
	v_pk_add_f16 v46, v82, v114
	v_pk_add_f16 v30, v30, v53
	v_pk_add_f16 v33, v33, v50
	v_pk_add_f16 v32, v32, v51
	v_pk_add_f16 v31, v31, v52
	v_pk_fma_f16 v25, v41, v53, v25
	v_pk_fma_f16 v24, v40, v52, v24
	v_pk_fma_f16 v23, v39, v51, v23
	v_pk_fma_f16 v22, v38, v50, v22
	v_pk_add_f16 v47, v83, v115
	v_pk_add_f16 v48, v84, v116
	v_pk_add_f16 v49, v85, v117
	s_nop 0
	v_exp_f16_sdwa v50, v46 dst_sel:WORD_0 dst_unused:UNUSED_PAD src0_sel:WORD_0
	v_exp_f16_sdwa v51, v47 dst_sel:WORD_0 dst_unused:UNUSED_PAD src0_sel:WORD_0
	v_exp_f16_sdwa v52, v48 dst_sel:WORD_0 dst_unused:UNUSED_PAD src0_sel:WORD_0
	v_exp_f16_sdwa v53, v49 dst_sel:WORD_0 dst_unused:UNUSED_PAD src0_sel:WORD_0
	v_exp_f16_sdwa v50, v46 dst_sel:WORD_1 dst_unused:UNUSED_PRESERVE src0_sel:WORD_1
	v_exp_f16_sdwa v51, v47 dst_sel:WORD_1 dst_unused:UNUSED_PRESERVE src0_sel:WORD_1
	v_exp_f16_sdwa v52, v48 dst_sel:WORD_1 dst_unused:UNUSED_PRESERVE src0_sel:WORD_1
	v_exp_f16_sdwa v53, v49 dst_sel:WORD_1 dst_unused:UNUSED_PRESERVE src0_sel:WORD_1
	s_nop 0
	s_nop 0
	v_pk_add_f16 v30, v30, v53
	v_pk_add_f16 v31, v31, v52
	v_rcp_f16_e32 v48, v30
	v_rcp_f16_sdwa v30, v30 dst_sel:DWORD dst_unused:UNUSED_PAD src0_sel:WORD_1
	v_pk_add_f16 v32, v32, v51
	v_rcp_f16_e32 v49, v31
	v_rcp_f16_sdwa v31, v31 dst_sel:DWORD dst_unused:UNUSED_PAD src0_sel:WORD_1
	v_pk_add_f16 v33, v33, v50
	v_rcp_f16_e32 v47, v32
	v_rcp_f16_sdwa v32, v32 dst_sel:DWORD dst_unused:UNUSED_PAD src0_sel:WORD_1
	v_rcp_f16_e32 v46, v33
	v_rcp_f16_sdwa v33, v33 dst_sel:DWORD dst_unused:UNUSED_PAD src0_sel:WORD_1
	v_pk_fma_f16 v25, v61, v53, v25
	v_pack_b32_f16 v30, v48, v30
	v_pk_fma_f16 v24, v60, v52, v24
	v_pk_mul_f16 v25, v25, v30
	v_pack_b32_f16 v30, v49, v31
	v_pk_fma_f16 v23, v59, v51, v23
	v_pk_mul_f16 v24, v24, v30
	v_pack_b32_f16 v30, v47, v32
	v_pk_fma_f16 v22, v58, v50, v22
	v_pk_mul_f16 v23, v23, v30
	v_pack_b32_f16 v30, v46, v33
	v_pk_mul_f16 v22, v22, v30
	s_waitcnt vmcnt(0)
	v_pk_mul_f16 v30, v185, v146 op_sel_hi:[0,1]
	v_pk_mul_f16 v31, v185, v147 op_sel_hi:[0,1]
	v_pk_mul_f16 v32, v185, v148 op_sel_hi:[0,1]
	v_pk_mul_f16 v33, v185, v149 op_sel_hi:[0,1]
	v_pk_mul_f16 v46, v183, v146 op_sel_hi:[0,1]
	v_pk_mul_f16 v47, v183, v147 op_sel_hi:[0,1]
	v_pk_mul_f16 v48, v183, v148 op_sel_hi:[0,1]
	v_pk_mul_f16 v49, v183, v149 op_sel_hi:[0,1]
	v_pk_mul_f16 v50, v184, v146 op_sel_hi:[0,1]
	v_pk_mul_f16 v51, v184, v147 op_sel_hi:[0,1]
	v_pk_mul_f16 v52, v184, v148 op_sel_hi:[0,1]
	v_pk_mul_f16 v53, v184, v149 op_sel_hi:[0,1]
	v_pk_fma_f16 v21, v21, v149, v33
	v_pk_fma_f16 v20, v20, v148, v32
	v_pk_fma_f16 v19, v19, v147, v31
	v_pk_fma_f16 v18, v18, v146, v30
	v_pk_fma_f16 v37, v37, v149, v49
	v_pk_fma_f16 v36, v36, v148, v48
	v_pk_fma_f16 v35, v35, v147, v47
	v_pk_fma_f16 v34, v34, v146, v46
	v_pk_fma_f16 v57, v57, v149, v53
	v_pk_fma_f16 v56, v56, v148, v52
	v_pk_fma_f16 v55, v55, v147, v51
	v_pk_fma_f16 v54, v54, v146, v50
	v_pk_fma_f16 v62, v77, v149, v33
	v_pk_fma_f16 v63, v76, v148, v32
	v_pk_fma_f16 v64, v75, v147, v31
	v_pk_fma_f16 v65, v74, v146, v30
	v_pk_maximum3_f16 v74, v18, v34, v54
	v_pk_maximum3_f16 v75, v19, v35, v55
	v_pk_maximum3_f16 v76, v20, v36, v56
	v_pk_maximum3_f16 v77, v21, v37, v57
	v_pk_fma_f16 v66, v105, v149, v49
	v_pk_fma_f16 v67, v104, v148, v48
	v_pk_fma_f16 v68, v103, v147, v47
	v_pk_fma_f16 v69, v102, v146, v46
	v_pk_fma_f16 v70, v121, v149, v53
	v_pk_fma_f16 v71, v120, v148, v52
	v_pk_fma_f16 v72, v119, v147, v51
	v_pk_fma_f16 v73, v118, v146, v50
	v_pk_fma_f16 v33, v133, v149, v33
	v_pk_fma_f16 v32, v132, v148, v32
	v_pk_fma_f16 v31, v131, v147, v31
	v_pk_fma_f16 v30, v130, v146, v30
	v_pk_fma_f16 v49, v141, v149, v49
	v_pk_fma_f16 v48, v140, v148, v48
	v_pk_fma_f16 v47, v139, v147, v47
	v_pk_fma_f16 v46, v138, v146, v46
	v_pk_fma_f16 v53, v145, v149, v53
	v_pk_fma_f16 v52, v144, v148, v52
	v_pk_fma_f16 v51, v143, v147, v51
	v_pk_fma_f16 v50, v142, v146, v50
	v_pk_maximum3_f16 v82, v65, v69, v73
	v_pk_maximum3_f16 v83, v64, v68, v72
	v_pk_maximum3_f16 v84, v63, v67, v71
	v_pk_maximum3_f16 v85, v62, v66, v70
	v_pk_maximum3_f16 v87, v31, v47, v51
	s_nop 0
	v_pk_maximum3_f16 v86, v30, v46, v50
	v_pk_maximum3_f16 v88, v32, v48, v52
	v_pk_maximum3_f16 v89, v33, v49, v53
	s_nop 0
	v_pk_maximum3_f16 v74, v74, v82, v86
	v_pk_maximum3_f16 v75, v75, v83, v87
	v_pk_maximum3_f16 v76, v76, v84, v88
	v_pk_maximum3_f16 v77, v77, v85, v89
	s_nop 0
	v_xor_b32_e32 v77, 0x80008000, v77
	v_xor_b32_e32 v76, 0x80008000, v76
	v_xor_b32_e32 v75, 0x80008000, v75
	v_xor_b32_e32 v74, 0x80008000, v74
	v_pk_add_f16 v18, v18, v74
	v_pk_add_f16 v19, v19, v75
	v_pk_add_f16 v20, v20, v76
	v_pk_add_f16 v21, v21, v77
	v_pk_add_f16 v34, v34, v74
	v_exp_f16_sdwa v82, v18 dst_sel:WORD_0 dst_unused:UNUSED_PAD src0_sel:WORD_0
	v_exp_f16_sdwa v83, v19 dst_sel:WORD_0 dst_unused:UNUSED_PAD src0_sel:WORD_0
	v_exp_f16_sdwa v84, v20 dst_sel:WORD_0 dst_unused:UNUSED_PAD src0_sel:WORD_0
	v_exp_f16_sdwa v85, v21 dst_sel:WORD_0 dst_unused:UNUSED_PAD src0_sel:WORD_0
	v_exp_f16_sdwa v82, v18 dst_sel:WORD_1 dst_unused:UNUSED_PRESERVE src0_sel:WORD_1
	v_exp_f16_sdwa v83, v19 dst_sel:WORD_1 dst_unused:UNUSED_PRESERVE src0_sel:WORD_1
	v_exp_f16_sdwa v84, v20 dst_sel:WORD_1 dst_unused:UNUSED_PRESERVE src0_sel:WORD_1
	v_exp_f16_sdwa v85, v21 dst_sel:WORD_1 dst_unused:UNUSED_PRESERVE src0_sel:WORD_1
	s_nop 0
	v_pk_add_f16 v35, v35, v75
	v_pk_add_f16 v18, v82, 0
	v_pk_add_f16 v19, v83, 0
	v_pk_add_f16 v20, v84, 0
	v_pk_add_f16 v21, v85, 0
	v_pk_fma_f16 v6, v6, v82, 0
	v_pk_fma_f16 v7, v7, v83, 0
	v_pk_fma_f16 v8, v8, v84, 0
	v_pk_fma_f16 v9, v9, v85, 0
	v_pk_add_f16 v36, v36, v76
	v_pk_add_f16 v37, v37, v77
	s_nop 0
	v_exp_f16_sdwa v82, v34 dst_sel:WORD_0 dst_unused:UNUSED_PAD src0_sel:WORD_0
	v_exp_f16_sdwa v83, v35 dst_sel:WORD_0 dst_unused:UNUSED_PAD src0_sel:WORD_0
	v_exp_f16_sdwa v84, v36 dst_sel:WORD_0 dst_unused:UNUSED_PAD src0_sel:WORD_0
	v_exp_f16_sdwa v85, v37 dst_sel:WORD_0 dst_unused:UNUSED_PAD src0_sel:WORD_0
	v_exp_f16_sdwa v82, v34 dst_sel:WORD_1 dst_unused:UNUSED_PRESERVE src0_sel:WORD_1
	v_exp_f16_sdwa v83, v35 dst_sel:WORD_1 dst_unused:UNUSED_PRESERVE src0_sel:WORD_1
	v_exp_f16_sdwa v84, v36 dst_sel:WORD_1 dst_unused:UNUSED_PRESERVE src0_sel:WORD_1
	v_exp_f16_sdwa v85, v37 dst_sel:WORD_1 dst_unused:UNUSED_PRESERVE src0_sel:WORD_1
	s_nop 0
	s_nop 0
	v_pk_add_f16 v21, v21, v85
	v_pk_add_f16 v20, v20, v84
	v_pk_add_f16 v19, v19, v83
	v_pk_add_f16 v18, v18, v82
	v_pk_fma_f16 v9, v13, v85, v9
	v_pk_fma_f16 v8, v12, v84, v8
	v_pk_fma_f16 v7, v11, v83, v7
	v_pk_fma_f16 v6, v10, v82, v6
	v_pk_add_f16 v10, v54, v74
	v_pk_add_f16 v11, v55, v75
	v_pk_add_f16 v12, v56, v76
	v_pk_add_f16 v13, v57, v77
	s_nop 0
	v_exp_f16_sdwa v34, v10 dst_sel:WORD_0 dst_unused:UNUSED_PAD src0_sel:WORD_0
	v_exp_f16_sdwa v35, v11 dst_sel:WORD_0 dst_unused:UNUSED_PAD src0_sel:WORD_0
	v_exp_f16_sdwa v36, v12 dst_sel:WORD_0 dst_unused:UNUSED_PAD src0_sel:WORD_0
	v_exp_f16_sdwa v37, v13 dst_sel:WORD_0 dst_unused:UNUSED_PAD src0_sel:WORD_0
	v_exp_f16_sdwa v34, v10 dst_sel:WORD_1 dst_unused:UNUSED_PRESERVE src0_sel:WORD_1
	v_exp_f16_sdwa v35, v11 dst_sel:WORD_1 dst_unused:UNUSED_PRESERVE src0_sel:WORD_1
	v_exp_f16_sdwa v36, v12 dst_sel:WORD_1 dst_unused:UNUSED_PRESERVE src0_sel:WORD_1
	v_exp_f16_sdwa v37, v13 dst_sel:WORD_1 dst_unused:UNUSED_PRESERVE src0_sel:WORD_1
	s_nop 0
	s_nop 0
	v_pk_add_f16 v10, v18, v34
	v_pk_add_f16 v11, v19, v35
	v_pk_add_f16 v12, v20, v36
	v_pk_add_f16 v13, v21, v37
	v_pk_fma_f16 v6, v14, v34, v6
	v_pk_fma_f16 v7, v15, v35, v7
	v_pk_fma_f16 v8, v16, v36, v8
	v_pk_fma_f16 v9, v17, v37, v9
	v_pk_add_f16 v14, v65, v74
	v_pk_add_f16 v15, v64, v75
	v_pk_add_f16 v16, v63, v76
	v_pk_add_f16 v17, v62, v77
	s_nop 0
	v_exp_f16_sdwa v18, v14 dst_sel:WORD_0 dst_unused:UNUSED_PAD src0_sel:WORD_0
	v_exp_f16_sdwa v19, v15 dst_sel:WORD_0 dst_unused:UNUSED_PAD src0_sel:WORD_0
	v_exp_f16_sdwa v20, v16 dst_sel:WORD_0 dst_unused:UNUSED_PAD src0_sel:WORD_0
	v_exp_f16_sdwa v21, v17 dst_sel:WORD_0 dst_unused:UNUSED_PAD src0_sel:WORD_0
	v_exp_f16_sdwa v18, v14 dst_sel:WORD_1 dst_unused:UNUSED_PRESERVE src0_sel:WORD_1
	v_exp_f16_sdwa v19, v15 dst_sel:WORD_1 dst_unused:UNUSED_PRESERVE src0_sel:WORD_1
	v_exp_f16_sdwa v20, v16 dst_sel:WORD_1 dst_unused:UNUSED_PRESERVE src0_sel:WORD_1
	v_exp_f16_sdwa v21, v17 dst_sel:WORD_1 dst_unused:UNUSED_PRESERVE src0_sel:WORD_1
	s_nop 0
	v_pk_add_f16 v14, v69, v74
	v_pk_add_f16 v13, v13, v21
	v_pk_add_f16 v12, v12, v20
	v_pk_add_f16 v11, v11, v19
	v_pk_add_f16 v10, v10, v18
	v_pk_fma_f16 v9, v29, v21, v9
	v_pk_fma_f16 v8, v28, v20, v8
	v_pk_fma_f16 v7, v27, v19, v7
	v_pk_fma_f16 v6, v26, v18, v6
	v_pk_add_f16 v15, v68, v75
	v_pk_add_f16 v16, v67, v76
	v_pk_add_f16 v17, v66, v77
	s_nop 0
	v_exp_f16_sdwa v18, v14 dst_sel:WORD_0 dst_unused:UNUSED_PAD src0_sel:WORD_0
	v_exp_f16_sdwa v19, v15 dst_sel:WORD_0 dst_unused:UNUSED_PAD src0_sel:WORD_0
	v_exp_f16_sdwa v20, v16 dst_sel:WORD_0 dst_unused:UNUSED_PAD src0_sel:WORD_0
	v_exp_f16_sdwa v21, v17 dst_sel:WORD_0 dst_unused:UNUSED_PAD src0_sel:WORD_0
	v_exp_f16_sdwa v18, v14 dst_sel:WORD_1 dst_unused:UNUSED_PRESERVE src0_sel:WORD_1
	v_exp_f16_sdwa v19, v15 dst_sel:WORD_1 dst_unused:UNUSED_PRESERVE src0_sel:WORD_1
	v_exp_f16_sdwa v20, v16 dst_sel:WORD_1 dst_unused:UNUSED_PRESERVE src0_sel:WORD_1
	v_exp_f16_sdwa v21, v17 dst_sel:WORD_1 dst_unused:UNUSED_PRESERVE src0_sel:WORD_1
	s_nop 0
	v_pk_add_f16 v14, v73, v74
	v_pk_add_f16 v10, v10, v18
	v_pk_add_f16 v11, v11, v19
	v_pk_add_f16 v12, v12, v20
	v_pk_add_f16 v13, v13, v21
	v_pk_fma_f16 v6, v38, v18, v6
	v_pk_fma_f16 v7, v39, v19, v7
	v_pk_fma_f16 v8, v40, v20, v8
	v_pk_fma_f16 v9, v41, v21, v9
	v_pk_add_f16 v15, v72, v75
	v_pk_add_f16 v16, v71, v76
	v_pk_add_f16 v17, v70, v77
	s_nop 0
	v_exp_f16_sdwa v18, v14 dst_sel:WORD_0 dst_unused:UNUSED_PAD src0_sel:WORD_0
	v_exp_f16_sdwa v19, v15 dst_sel:WORD_0 dst_unused:UNUSED_PAD src0_sel:WORD_0
	v_exp_f16_sdwa v20, v16 dst_sel:WORD_0 dst_unused:UNUSED_PAD src0_sel:WORD_0
	v_exp_f16_sdwa v21, v17 dst_sel:WORD_0 dst_unused:UNUSED_PAD src0_sel:WORD_0
	v_exp_f16_sdwa v18, v14 dst_sel:WORD_1 dst_unused:UNUSED_PRESERVE src0_sel:WORD_1
	v_exp_f16_sdwa v19, v15 dst_sel:WORD_1 dst_unused:UNUSED_PRESERVE src0_sel:WORD_1
	v_exp_f16_sdwa v20, v16 dst_sel:WORD_1 dst_unused:UNUSED_PRESERVE src0_sel:WORD_1
	v_exp_f16_sdwa v21, v17 dst_sel:WORD_1 dst_unused:UNUSED_PRESERVE src0_sel:WORD_1
	s_nop 0
	v_pk_add_f16 v14, v30, v74
	v_pk_add_f16 v13, v13, v21
	v_pk_add_f16 v12, v12, v20
	v_pk_add_f16 v11, v11, v19
	v_pk_add_f16 v10, v10, v18
	v_pk_fma_f16 v9, v61, v21, v9
	v_pk_fma_f16 v8, v60, v20, v8
	v_pk_fma_f16 v7, v59, v19, v7
	v_pk_fma_f16 v6, v58, v18, v6
	v_pk_add_f16 v15, v31, v75
	v_pk_add_f16 v16, v32, v76
	v_pk_add_f16 v17, v33, v77
	s_nop 0
	v_exp_f16_sdwa v18, v14 dst_sel:WORD_0 dst_unused:UNUSED_PAD src0_sel:WORD_0
	v_exp_f16_sdwa v19, v15 dst_sel:WORD_0 dst_unused:UNUSED_PAD src0_sel:WORD_0
	v_exp_f16_sdwa v20, v16 dst_sel:WORD_0 dst_unused:UNUSED_PAD src0_sel:WORD_0
	v_exp_f16_sdwa v21, v17 dst_sel:WORD_0 dst_unused:UNUSED_PAD src0_sel:WORD_0
	v_exp_f16_sdwa v18, v14 dst_sel:WORD_1 dst_unused:UNUSED_PRESERVE src0_sel:WORD_1
	v_exp_f16_sdwa v19, v15 dst_sel:WORD_1 dst_unused:UNUSED_PRESERVE src0_sel:WORD_1
	v_exp_f16_sdwa v20, v16 dst_sel:WORD_1 dst_unused:UNUSED_PRESERVE src0_sel:WORD_1
	v_exp_f16_sdwa v21, v17 dst_sel:WORD_1 dst_unused:UNUSED_PRESERVE src0_sel:WORD_1
	s_nop 0
	s_nop 0
	v_pk_add_f16 v10, v10, v18
	v_pk_add_f16 v11, v11, v19
	v_pk_add_f16 v12, v12, v20
	v_pk_add_f16 v13, v13, v21
	v_pk_fma_f16 v14, v78, v18, v6
	v_pk_fma_f16 v15, v79, v19, v7
	v_pk_fma_f16 v16, v80, v20, v8
	v_pk_fma_f16 v17, v81, v21, v9
	v_pk_add_f16 v6, v46, v74
	v_pk_add_f16 v7, v47, v75
	v_pk_add_f16 v8, v48, v76
	v_pk_add_f16 v9, v49, v77
	s_nop 0
	v_exp_f16_sdwa v18, v6 dst_sel:WORD_0 dst_unused:UNUSED_PAD src0_sel:WORD_0
	v_exp_f16_sdwa v19, v7 dst_sel:WORD_0 dst_unused:UNUSED_PAD src0_sel:WORD_0
	v_exp_f16_sdwa v20, v8 dst_sel:WORD_0 dst_unused:UNUSED_PAD src0_sel:WORD_0
	v_exp_f16_sdwa v21, v9 dst_sel:WORD_0 dst_unused:UNUSED_PAD src0_sel:WORD_0
	v_exp_f16_sdwa v18, v6 dst_sel:WORD_1 dst_unused:UNUSED_PRESERVE src0_sel:WORD_1
	v_exp_f16_sdwa v19, v7 dst_sel:WORD_1 dst_unused:UNUSED_PRESERVE src0_sel:WORD_1
	v_exp_f16_sdwa v20, v8 dst_sel:WORD_1 dst_unused:UNUSED_PRESERVE src0_sel:WORD_1
	v_exp_f16_sdwa v21, v9 dst_sel:WORD_1 dst_unused:UNUSED_PRESERVE src0_sel:WORD_1
	s_nop 0
	s_nop 0
	v_pk_add_f16 v9, v13, v21
	v_pk_add_f16 v8, v12, v20
	v_pk_add_f16 v7, v11, v19
	v_pk_add_f16 v6, v10, v18
	v_pk_fma_f16 v13, v93, v21, v17
	v_pk_fma_f16 v12, v92, v20, v16
	v_pk_fma_f16 v11, v91, v19, v15
	v_pk_fma_f16 v10, v90, v18, v14
	v_pk_add_f16 v18, v50, v74
	v_pk_add_f16 v19, v51, v75
	v_pk_add_f16 v20, v52, v76
	v_pk_add_f16 v21, v53, v77
	s_nop 0
	v_exp_f16_sdwa v14, v18 dst_sel:WORD_0 dst_unused:UNUSED_PAD src0_sel:WORD_0
	v_exp_f16_sdwa v17, v19 dst_sel:WORD_0 dst_unused:UNUSED_PAD src0_sel:WORD_0
	v_exp_f16_sdwa v15, v20 dst_sel:WORD_0 dst_unused:UNUSED_PAD src0_sel:WORD_0
	v_exp_f16_sdwa v16, v21 dst_sel:WORD_0 dst_unused:UNUSED_PAD src0_sel:WORD_0
	v_exp_f16_sdwa v14, v18 dst_sel:WORD_1 dst_unused:UNUSED_PRESERVE src0_sel:WORD_1
	v_exp_f16_sdwa v17, v19 dst_sel:WORD_1 dst_unused:UNUSED_PRESERVE src0_sel:WORD_1
	v_exp_f16_sdwa v15, v20 dst_sel:WORD_1 dst_unused:UNUSED_PRESERVE src0_sel:WORD_1
	v_exp_f16_sdwa v16, v21 dst_sel:WORD_1 dst_unused:UNUSED_PRESERVE src0_sel:WORD_1
	s_nop 0
.LBB5_42:
	s_and_b64 vcc, exec, s[4:5]
	s_cbranch_vccz .LBB5_3
	v_cmp_lt_u32_e64 s[64:65], 0, v182
	v_cmp_gt_u32_e64 s[66:67], 63, v182
	v_cmp_lt_u32_e64 s[68:69], 0, v162
	v_cmp_gt_u32_e64 s[70:71], 60, v162
	buffer_load_dwordx4 v[184:187], v180, s[16:19], 0 offen
	v_add_u32_e32 v223, 0x18000, v180
	buffer_load_dwordx4 v[154:157], v223, s[16:19], 0 offen
	v_add_u32_e32 v222, 0x30000, v180
	buffer_load_dwordx4 v[150:153], v222, s[16:19], 0 offen
	v_add_u32_e32 v223, 0x48000, v180
	buffer_load_dwordx4 v[146:149], v223, s[16:19], 0 offen
	s_and_b64 s[72:73], s[68:69], s[64:65]
	s_and_b64 s[74:75], s[68:69], s[66:67]
	s_and_b64 s[76:77], s[70:71], s[64:65]
	s_and_b64 s[78:79], s[70:71], s[66:67]
	v_add_u32_e32 v222, 0xfffe7c00, v180
	v_add_u32_e32 v223, 0xfffe8000, v180
	v_mov_b32_e32 v110, v172
	v_mov_b32_e32 v111, v174
	v_mov_b32_e32 v112, v176
	v_mov_b32_e32 v113, v178
	v_mov_b32_e32 v78, v173
	v_mov_b32_e32 v79, v175
	v_mov_b32_e32 v80, v177
	v_mov_b32_e32 v81, v179
	v_mov_b32_e32 v126, v172
	v_mov_b32_e32 v127, v174
	v_mov_b32_e32 v128, v176
	v_mov_b32_e32 v129, v178
	v_mov_b32_e32 v102, v173
	v_mov_b32_e32 v103, v175
	v_mov_b32_e32 v104, v177
	v_mov_b32_e32 v105, v179
	v_mov_b32_e32 v134, v172
	v_mov_b32_e32 v135, v174
	v_mov_b32_e32 v136, v176
	v_mov_b32_e32 v137, v178
	v_mov_b32_e32 v114, v173
	v_mov_b32_e32 v115, v175
	v_mov_b32_e32 v116, v177
	v_mov_b32_e32 v117, v179
	s_mov_b64 exec, s[72:73]
	buffer_load_dwordx4 v[110:113], v222, s[16:19], 0 offen
	buffer_load_dwordx4 v[78:81], v222, s[16:19], 0 offen offset:512
	s_mov_b64 exec, -1
	s_mov_b64 exec, s[68:69]
	buffer_load_dwordx4 v[126:129], v223, s[16:19], 0 offen offset:512
	buffer_load_dwordx4 v[102:105], v223, s[16:19], 0 offen offset:1024
	s_mov_b64 exec, -1
	s_mov_b64 exec, s[74:75]
	buffer_load_dwordx4 v[134:137], v223, s[16:19], 0 offen offset:2048
	buffer_load_dwordx4 v[114:117], v223, s[16:19], 0 offen offset:2560
	s_mov_b64 exec, -1
	v_add_u32_e32 v222, 0xfffffc00, v180
	v_mov_b32_e32 v82, v172
	v_mov_b32_e32 v83, v174
	v_mov_b32_e32 v84, v176
	v_mov_b32_e32 v85, v178
	v_mov_b32_e32 v42, v173
	v_mov_b32_e32 v43, v175
	v_mov_b32_e32 v44, v177
	v_mov_b32_e32 v45, v179
	v_mov_b32_e32 v122, v172
	v_mov_b32_e32 v123, v174
	v_mov_b32_e32 v124, v176
	v_mov_b32_e32 v125, v178
	v_mov_b32_e32 v86, v173
	v_mov_b32_e32 v87, v175
	v_mov_b32_e32 v88, v177
	v_mov_b32_e32 v89, v179
	s_mov_b64 exec, s[64:65]
	buffer_load_dwordx4 v[82:85], v222, s[16:19], 0 offen
	buffer_load_dwordx4 v[42:45], v222, s[16:19], 0 offen offset:512
	s_mov_b64 exec, -1
	buffer_load_dwordx4 v[106:109], v180, s[16:19], 0 offen offset:512
	buffer_load_dwordx4 v[62:65], v180, s[16:19], 0 offen offset:1024
	s_mov_b64 exec, s[66:67]
	buffer_load_dwordx4 v[122:125], v180, s[16:19], 0 offen offset:2048
	buffer_load_dwordx4 v[86:89], v180, s[16:19], 0 offen offset:2560
	s_mov_b64 exec, -1
	v_add_u32_e32 v222, 0x17c00, v180
	v_add_u32_e32 v223, 0x18000, v180
	v_mov_b32_e32 v50, v172
	v_mov_b32_e32 v51, v174
	v_mov_b32_e32 v52, v176
	v_mov_b32_e32 v53, v178
	v_mov_b32_e32 v22, v173
	v_mov_b32_e32 v23, v175
	v_mov_b32_e32 v24, v177
	v_mov_b32_e32 v25, v179
	v_mov_b32_e32 v94, v172
	v_mov_b32_e32 v95, v174
	v_mov_b32_e32 v96, v176
	v_mov_b32_e32 v97, v178
	v_mov_b32_e32 v46, v173
	v_mov_b32_e32 v47, v175
	v_mov_b32_e32 v48, v177
	v_mov_b32_e32 v49, v179
	s_mov_b64 exec, s[64:65]
	buffer_load_dwordx4 v[50:53], v222, s[16:19], 0 offen
	buffer_load_dwordx4 v[22:25], v222, s[16:19], 0 offen offset:512
	s_mov_b64 exec, -1
	buffer_load_dwordx4 v[66:69], v223, s[16:19], 0 offen offset:512
	buffer_load_dwordx4 v[34:37], v223, s[16:19], 0 offen offset:1024
	s_mov_b64 exec, s[66:67]
	buffer_load_dwordx4 v[94:97], v223, s[16:19], 0 offen offset:2048
	buffer_load_dwordx4 v[46:49], v223, s[16:19], 0 offen offset:2560
	s_mov_b64 exec, -1
	v_add_u32_e32 v222, 0x2fc00, v180
	v_add_u32_e32 v223, 0x30000, v180
	v_mov_b32_e32 v18, v172
	v_mov_b32_e32 v19, v174
	v_mov_b32_e32 v20, v176
	v_mov_b32_e32 v21, v178
	v_mov_b32_e32 v6, v173
	v_mov_b32_e32 v7, v175
	v_mov_b32_e32 v8, v177
	v_mov_b32_e32 v9, v179
	v_mov_b32_e32 v54, v172
	v_mov_b32_e32 v55, v174
	v_mov_b32_e32 v56, v176
	v_mov_b32_e32 v57, v178
	v_mov_b32_e32 v14, v173
	v_mov_b32_e32 v15, v175
	v_mov_b32_e32 v16, v177
	v_mov_b32_e32 v17, v179
	s_mov_b64 exec, s[64:65]
	buffer_load_dwordx4 v[18:21], v222, s[16:19], 0 offen
	buffer_load_dwordx4 v[6:9], v222, s[16:19], 0 offen offset:512
	s_mov_b64 exec, -1
	buffer_load_dwordx4 v[30:33], v223, s[16:19], 0 offen offset:512
	buffer_load_dwordx4 v[10:13], v223, s[16:19], 0 offen offset:1024
	s_mov_b64 exec, s[66:67]
	buffer_load_dwordx4 v[54:57], v223, s[16:19], 0 offen offset:2048
	buffer_load_dwordx4 v[14:17], v223, s[16:19], 0 offen offset:2560
	s_mov_b64 exec, -1
	v_add_u32_e32 v222, 0x47c00, v180
	v_add_u32_e32 v223, 0x48000, v180
	v_mov_b32_e32 v74, v172
	v_mov_b32_e32 v75, v174
	v_mov_b32_e32 v76, v176
	v_mov_b32_e32 v77, v178
	v_mov_b32_e32 v26, v173
	v_mov_b32_e32 v27, v175
	v_mov_b32_e32 v28, v177
	v_mov_b32_e32 v29, v179
	v_mov_b32_e32 v118, v172
	v_mov_b32_e32 v119, v174
	v_mov_b32_e32 v120, v176
	v_mov_b32_e32 v121, v178
	v_mov_b32_e32 v58, v173
	v_mov_b32_e32 v59, v175
	v_mov_b32_e32 v60, v177
	v_mov_b32_e32 v61, v179
	s_mov_b64 exec, s[64:65]
	buffer_load_dwordx4 v[74:77], v222, s[16:19], 0 offen
	buffer_load_dwordx4 v[26:29], v222, s[16:19], 0 offen offset:512
	s_mov_b64 exec, -1
	buffer_load_dwordx4 v[98:101], v223, s[16:19], 0 offen offset:512
	buffer_load_dwordx4 v[38:41], v223, s[16:19], 0 offen offset:1024
	s_mov_b64 exec, s[66:67]
	buffer_load_dwordx4 v[118:121], v223, s[16:19], 0 offen offset:2048
	buffer_load_dwordx4 v[58:61], v223, s[16:19], 0 offen offset:2560
	s_mov_b64 exec, -1
	v_add_u32_e32 v222, 0x5fc00, v180
	v_add_u32_e32 v223, 0x60000, v180
	v_mov_b32_e32 v130, v172
	v_mov_b32_e32 v131, v174
	v_mov_b32_e32 v132, v176
	v_mov_b32_e32 v133, v178
	v_mov_b32_e32 v70, v173
	v_mov_b32_e32 v71, v175
	v_mov_b32_e32 v72, v177
	v_mov_b32_e32 v73, v179
	v_mov_b32_e32 v138, v172
	v_mov_b32_e32 v139, v174
	v_mov_b32_e32 v140, v176
	v_mov_b32_e32 v141, v178
	v_mov_b32_e32 v90, v173
	v_mov_b32_e32 v91, v175
	v_mov_b32_e32 v92, v177
	v_mov_b32_e32 v93, v179
	v_mov_b32_e32 v142, v172
	v_mov_b32_e32 v143, v174
	v_mov_b32_e32 v144, v176
	v_mov_b32_e32 v145, v178
	v_mov_b32_e32 v2, v173
	v_mov_b32_e32 v3, v175
	v_mov_b32_e32 v4, v177
	v_mov_b32_e32 v5, v179
	s_mov_b64 exec, s[76:77]
	buffer_load_dwordx4 v[130:133], v222, s[16:19], 0 offen
	buffer_load_dwordx4 v[70:73], v222, s[16:19], 0 offen offset:512
	s_mov_b64 exec, -1
	s_mov_b64 exec, s[70:71]
	buffer_load_dwordx4 v[138:141], v223, s[16:19], 0 offen offset:512
	buffer_load_dwordx4 v[90:93], v223, s[16:19], 0 offen offset:1024
	s_mov_b64 exec, -1
	s_mov_b64 exec, s[78:79]
	buffer_load_dwordx4 v[142:145], v223, s[16:19], 0 offen offset:2048
	buffer_load_dwordx4 v[2:5], v223, s[16:19], 0 offen offset:2560
	s_mov_b64 exec, -1
	s_load_dwordx2 s[0:1], s[22:23], 0x18
	s_waitcnt lgkmcnt(0)
	s_load_dwordx2 s[6:7], s[0:1], 0x0
	s_load_dword s28, s[0:1], 0x8
	s_branch .LBB5_2
.LBB5_79:
	s_mul_i32 s0, s13, s3
	s_lshl_b32 s1, s15, 6
	s_add_i32 s0, s0, s12
	s_and_b32 s1, s1, 0xfffffe00
	s_or_b32 s6, s1, s2
	s_mul_i32 s2, s0, 0x60000
	s_mul_hi_i32 s1, s0, 0x60000
	s_add_u32 s2, s8, s2
	s_mulk_i32 s0, 0x300
	s_addc_u32 s7, s9, s1
	s_ashr_i32 s1, s0, 31
	s_lshl_b64 s[0:1], s[0:1], 2
	s_add_u32 s4, s10, s0
	s_addc_u32 s5, s11, s1
	s_mul_i32 s0, s3, 0x1800000
	s_mul_hi_i32 s1, s3, 0x1800000
	s_add_u32 s0, s20, s0
	v_readfirstlane_b32 s3, v0
	s_addc_u32 s1, s21, s1
	s_lshr_b32 s8, s3, 6
	s_and_b32 s1, s1, 0xffff
	s_mul_i32 s9, s8, 0x6000
	v_and_b32_e32 v2, 63, v0
	s_mul_hi_u32 s3, s8, 0x6000
	s_add_u32 s2, s2, s9
	s_addc_u32 s3, s7, s3
	v_lshlrev_b32_e32 v56, 4, v2
	v_mov_b32_e32 v57, 0
	v_lshl_add_u64 v[54:55], s[2:3], 0, v[56:57]
	s_movk_i32 s7, 0x1000
	v_add_co_u32_e32 v50, vcc, s7, v54
	s_movk_i32 s7, 0x2000
	s_nop 0
	v_addc_co_u32_e32 v51, vcc, 0, v55, vcc
	v_add_co_u32_e32 v52, vcc, s7, v54
	global_load_dwordx4 v[2:5], v56, s[2:3] offset:1024
	global_load_dwordx4 v[6:9], v56, s[2:3] offset:2048
	v_addc_co_u32_e32 v53, vcc, 0, v55, vcc
	global_load_dwordx4 v[10:13], v56, s[2:3] offset:3072
	global_load_dwordx4 v[14:17], v[52:53], off offset:-4096
	global_load_dwordx4 v[18:21], v[50:51], off offset:1024
	global_load_dwordx4 v[22:25], v[50:51], off offset:2048
	global_load_dwordx4 v[26:29], v56, s[2:3]
	global_load_dwordx4 v[30:33], v[50:51], off offset:3072
	global_load_dwordx4 v[34:37], v[52:53], off
	global_load_dwordx4 v[38:41], v[52:53], off offset:1024
	global_load_dwordx4 v[42:45], v[52:53], off offset:2048
	global_load_dwordx4 v[46:49], v[52:53], off offset:3072
	s_movk_i32 s2, 0x3000
	v_add_co_u32_e32 v58, vcc, s2, v54
	s_movk_i32 s2, 0x4000
	s_nop 0
	v_addc_co_u32_e32 v59, vcc, 0, v55, vcc
	v_add_co_u32_e32 v140, vcc, s2, v54
	s_waitcnt lgkmcnt(0)
	s_nop 0
	v_addc_co_u32_e32 v141, vcc, 0, v55, vcc
	s_barrier
	global_load_dwordx4 v[50:53], v[140:141], off offset:-4096
	global_load_dwordx4 v[62:65], v[58:59], off offset:1024
	global_load_dwordx4 v[68:71], v[58:59], off offset:2048
	v_lshlrev_b32_e32 v67, 9, v1
	v_xor_b32_e32 v61, v158, v1
	v_lshl_or_b32 v66, v61, 4, v67
	ds_read_b128 v[72:75], v66
	ds_read_b128 v[76:79], v66 offset:8192
	ds_read_b128 v[80:83], v66 offset:16384
	ds_read_b128 v[84:87], v66 offset:24576
	v_mul_u32_u24_e32 v60, 0x556, v0
	v_lshrrev_b32_e32 v60, 16, v60
	s_mul_i32 s7, s8, 48
	v_lshlrev_b32_e32 v61, 3, v60
	s_movk_i32 s9, 0x47
	v_lshl_or_b32 v56, v158, 2, s7
	s_mov_b32 s7, 0xfffffd0
	v_bitop3_b32 v61, v61, s9, v60 bitop3:0xc8
	s_mov_b32 s2, 0x1800000
	s_mov_b32 s3, 0x20000
	s_mulk_i32 s8, 0x60
	v_mul_lo_u32 v150, v60, s7
	v_or_b32_e32 v61, s6, v61
	s_waitcnt vmcnt(8) lgkmcnt(3)
	v_mfma_f32_16x16x32_f16 v[88:91], v[26:29], v[72:75], 0
	s_waitcnt lgkmcnt(2)
	v_mfma_f32_16x16x32_f16 v[92:95], v[26:29], v[76:79], 0
	s_waitcnt lgkmcnt(1)
	v_mfma_f32_16x16x32_f16 v[96:99], v[26:29], v[80:83], 0
	s_waitcnt lgkmcnt(0)
	v_mfma_f32_16x16x32_f16 v[26:29], v[26:29], v[84:87], 0
	v_mfma_f32_16x16x32_f16 v[100:103], v[2:5], v[72:75], 0
	v_mfma_f32_16x16x32_f16 v[104:107], v[2:5], v[76:79], 0
	v_mfma_f32_16x16x32_f16 v[108:111], v[2:5], v[80:83], 0
	v_mfma_f32_16x16x32_f16 v[2:5], v[2:5], v[84:87], 0
	v_mfma_f32_16x16x32_f16 v[112:115], v[6:9], v[72:75], 0
	v_mfma_f32_16x16x32_f16 v[74:77], v[6:9], v[76:79], 0
	v_mfma_f32_16x16x32_f16 v[78:81], v[6:9], v[80:83], 0
	v_mfma_f32_16x16x32_f16 v[6:9], v[6:9], v[84:87], 0
	global_load_dwordx4 v[82:85], v[58:59], off offset:3072
	global_load_dwordx4 v[116:119], v[140:141], off
	global_load_dwordx4 v[120:123], v[140:141], off offset:1024
	v_bitop3_b32 v58, v158, v1, 4 bitop3:0x36
	v_lshl_or_b32 v72, v58, 4, v67
	ds_read_b128 v[124:127], v72
	ds_read_b128 v[128:131], v72 offset:8192
	ds_read_b128 v[132:135], v72 offset:16384
	ds_read_b128 v[136:139], v72 offset:24576
	s_waitcnt lgkmcnt(3)
	v_mfma_f32_16x16x32_f16 v[86:89], v[10:13], v[124:127], v[88:91]
	s_waitcnt lgkmcnt(2)
	v_mfma_f32_16x16x32_f16 v[90:93], v[10:13], v[128:131], v[92:95]
	s_waitcnt lgkmcnt(1)
	v_mfma_f32_16x16x32_f16 v[94:97], v[10:13], v[132:135], v[96:99]
	s_waitcnt lgkmcnt(0)
	v_mfma_f32_16x16x32_f16 v[10:13], v[10:13], v[136:139], v[26:29]
	v_mfma_f32_16x16x32_f16 v[26:29], v[14:17], v[124:127], v[100:103]
	v_mfma_f32_16x16x32_f16 v[98:101], v[14:17], v[128:131], v[104:107]
	v_mfma_f32_16x16x32_f16 v[102:105], v[14:17], v[132:135], v[108:111]
	v_mfma_f32_16x16x32_f16 v[2:5], v[14:17], v[136:139], v[2:5]
	v_mfma_f32_16x16x32_f16 v[14:17], v[18:21], v[124:127], v[112:115]
	v_mfma_f32_16x16x32_f16 v[106:109], v[18:21], v[128:131], v[74:77]
	v_mfma_f32_16x16x32_f16 v[76:79], v[18:21], v[132:135], v[78:81]
	v_mfma_f32_16x16x32_f16 v[6:9], v[18:21], v[136:139], v[6:9]
	s_movk_i32 s9, 0x5000
	v_add_co_u32_e32 v58, vcc, s9, v54
	global_load_dwordx4 v[110:113], v[140:141], off offset:2048
	global_load_dwordx4 v[124:127], v[140:141], off offset:3072
	v_addc_co_u32_e32 v59, vcc, 0, v55, vcc
	global_load_dwordx4 v[128:131], v[58:59], off
	v_bitop3_b32 v18, v158, v1, 8 bitop3:0x36
	v_lshl_or_b32 v74, v18, 4, v67
	ds_read_b128 v[18:21], v74
	ds_read_b128 v[132:135], v74 offset:8192
	ds_read_b128 v[136:139], v74 offset:16384
	ds_read_b128 v[140:143], v74 offset:24576
	s_waitcnt lgkmcnt(3)
	v_mfma_f32_16x16x32_f16 v[86:89], v[22:25], v[18:21], v[86:89]
	s_waitcnt lgkmcnt(2)
	v_mfma_f32_16x16x32_f16 v[90:93], v[22:25], v[132:135], v[90:93]
	s_waitcnt lgkmcnt(1)
	v_mfma_f32_16x16x32_f16 v[94:97], v[22:25], v[136:139], v[94:97]
	s_waitcnt lgkmcnt(0)
	v_mfma_f32_16x16x32_f16 v[10:13], v[22:25], v[140:143], v[10:13]
	s_waitcnt vmcnt(13)
	v_mfma_f32_16x16x32_f16 v[22:25], v[30:33], v[18:21], v[26:29]
	v_mfma_f32_16x16x32_f16 v[26:29], v[30:33], v[132:135], v[98:101]
	v_mfma_f32_16x16x32_f16 v[98:101], v[30:33], v[136:139], v[102:105]
	v_mfma_f32_16x16x32_f16 v[2:5], v[30:33], v[140:143], v[2:5]
	s_waitcnt vmcnt(12)
	v_mfma_f32_16x16x32_f16 v[14:17], v[34:37], v[18:21], v[14:17]
	v_mfma_f32_16x16x32_f16 v[18:21], v[34:37], v[132:135], v[106:109]
	v_mfma_f32_16x16x32_f16 v[30:33], v[34:37], v[136:139], v[76:79]
	v_mfma_f32_16x16x32_f16 v[6:9], v[34:37], v[140:143], v[6:9]
	global_load_dwordx4 v[102:105], v[58:59], off offset:1024
	global_load_dwordx4 v[106:109], v[58:59], off offset:2048
	global_load_dwordx4 v[132:135], v[58:59], off offset:3072
	v_bitop3_b32 v34, v158, v1, 12 bitop3:0x36
	v_lshl_or_b32 v75, v34, 4, v67
	ds_read_b128 v[34:37], v75
	ds_read_b128 v[76:79], v75 offset:8192
	ds_read_b128 v[136:139], v75 offset:16384
	ds_read_b128 v[140:143], v75 offset:24576
	s_waitcnt vmcnt(14) lgkmcnt(3)
	v_mfma_f32_16x16x32_f16 v[86:89], v[38:41], v[34:37], v[86:89]
	s_waitcnt lgkmcnt(2)
	v_mfma_f32_16x16x32_f16 v[90:93], v[38:41], v[76:79], v[90:93]
	s_waitcnt lgkmcnt(1)
	v_mfma_f32_16x16x32_f16 v[94:97], v[38:41], v[136:139], v[94:97]
	s_waitcnt lgkmcnt(0)
	v_mfma_f32_16x16x32_f16 v[10:13], v[38:41], v[140:143], v[10:13]
	s_waitcnt vmcnt(13)
	v_mfma_f32_16x16x32_f16 v[38:41], v[42:45], v[34:37], v[22:25]
	v_mfma_f32_16x16x32_f16 v[144:147], v[42:45], v[76:79], v[26:29]
	v_mfma_f32_16x16x32_f16 v[98:101], v[42:45], v[136:139], v[98:101]
	v_mfma_f32_16x16x32_f16 v[2:5], v[42:45], v[140:143], v[2:5]
	s_waitcnt vmcnt(12)
	v_mfma_f32_16x16x32_f16 v[14:17], v[46:49], v[34:37], v[14:17]
	v_mfma_f32_16x16x32_f16 v[18:21], v[46:49], v[76:79], v[18:21]
	v_mfma_f32_16x16x32_f16 v[30:33], v[46:49], v[136:139], v[30:33]
	v_mfma_f32_16x16x32_f16 v[6:9], v[46:49], v[140:143], v[6:9]
	s_mov_b32 s9, 0x30000
	v_add_co_u32_e32 v58, vcc, s9, v54
	s_mov_b32 s9, 0x31000
	s_nop 0
	v_addc_co_u32_e32 v59, vcc, 0, v55, vcc
	v_add_co_u32_e32 v148, vcc, s9, v54
	v_bitop3_b32 v42, v158, v1, 16 bitop3:0x36
	s_nop 0
	v_addc_co_u32_e32 v149, vcc, 0, v55, vcc
	global_load_dwordx4 v[34:37], v[148:149], off offset:-4096
	global_load_dwordx4 v[26:29], v[58:59], off offset:1024
	global_load_dwordx4 v[22:25], v[58:59], off offset:2048
	v_lshl_or_b32 v76, v42, 4, v67
	ds_read_b128 v[42:45], v76
	ds_read_b128 v[46:49], v76 offset:8192
	ds_read_b128 v[78:81], v76 offset:16384
	ds_read_b128 v[136:139], v76 offset:24576
	s_waitcnt vmcnt(14) lgkmcnt(3)
	v_mfma_f32_16x16x32_f16 v[86:89], v[50:53], v[42:45], v[86:89]
	s_waitcnt lgkmcnt(2)
	v_mfma_f32_16x16x32_f16 v[90:93], v[50:53], v[46:49], v[90:93]
	s_waitcnt lgkmcnt(1)
	v_mfma_f32_16x16x32_f16 v[94:97], v[50:53], v[78:81], v[94:97]
	s_waitcnt lgkmcnt(0)
	v_mfma_f32_16x16x32_f16 v[10:13], v[50:53], v[136:139], v[10:13]
	s_waitcnt vmcnt(13)
	v_mfma_f32_16x16x32_f16 v[38:41], v[62:65], v[42:45], v[38:41]
	v_mfma_f32_16x16x32_f16 v[50:53], v[62:65], v[46:49], v[144:147]
	v_mfma_f32_16x16x32_f16 v[98:101], v[62:65], v[78:81], v[98:101]
	v_mfma_f32_16x16x32_f16 v[62:65], v[62:65], v[136:139], v[2:5]
	s_waitcnt vmcnt(12)
	v_mfma_f32_16x16x32_f16 v[42:45], v[68:71], v[42:45], v[14:17]
	v_mfma_f32_16x16x32_f16 v[18:21], v[68:71], v[46:49], v[18:21]
	v_mfma_f32_16x16x32_f16 v[30:33], v[68:71], v[78:81], v[30:33]
	v_mfma_f32_16x16x32_f16 v[46:49], v[68:71], v[136:139], v[6:9]
	global_load_dwordx4 v[14:17], v[58:59], off offset:3072
	s_nop 1
	global_load_dwordx4 v[6:9], v[148:149], off
	global_load_dwordx4 v[2:5], v[148:149], off offset:1024
	v_bitop3_b32 v58, v158, v1, 20 bitop3:0x36
	v_lshl_or_b32 v77, v58, 4, v67
	ds_read_b128 v[68:71], v77
	ds_read_b128 v[78:81], v77 offset:8192
	ds_read_b128 v[136:139], v77 offset:16384
	ds_read_b128 v[140:143], v77 offset:24576
	s_waitcnt vmcnt(14) lgkmcnt(3)
	v_mfma_f32_16x16x32_f16 v[86:89], v[82:85], v[68:71], v[86:89]
	s_waitcnt lgkmcnt(2)
	v_mfma_f32_16x16x32_f16 v[90:93], v[82:85], v[78:81], v[90:93]
	s_waitcnt lgkmcnt(1)
	v_mfma_f32_16x16x32_f16 v[94:97], v[82:85], v[136:139], v[94:97]
	s_waitcnt lgkmcnt(0)
	v_mfma_f32_16x16x32_f16 v[82:85], v[82:85], v[140:143], v[10:13]
	s_waitcnt vmcnt(13)
	v_mfma_f32_16x16x32_f16 v[38:41], v[116:119], v[68:71], v[38:41]
	v_mfma_f32_16x16x32_f16 v[50:53], v[116:119], v[78:81], v[50:53]
	v_mfma_f32_16x16x32_f16 v[98:101], v[116:119], v[136:139], v[98:101]
	v_mfma_f32_16x16x32_f16 v[62:65], v[116:119], v[140:143], v[62:65]
	s_waitcnt vmcnt(12)
	v_mfma_f32_16x16x32_f16 v[42:45], v[120:123], v[68:71], v[42:45]
	v_mfma_f32_16x16x32_f16 v[68:71], v[120:123], v[78:81], v[18:21]
	v_mfma_f32_16x16x32_f16 v[114:117], v[120:123], v[136:139], v[30:33]
	v_mfma_f32_16x16x32_f16 v[46:49], v[120:123], v[140:143], v[46:49]
	s_mov_b32 s9, 0x33000
	v_add_co_u32_e32 v58, vcc, s9, v54
	global_load_dwordx4 v[18:21], v[148:149], off offset:2048
	global_load_dwordx4 v[10:13], v[148:149], off offset:3072
	v_addc_co_u32_e32 v59, vcc, 0, v55, vcc
	global_load_dwordx4 v[30:33], v[58:59], off offset:-4096
	v_bitop3_b32 v73, v158, v1, 24 bitop3:0x36
	v_lshl_or_b32 v78, v73, 4, v67
	ds_read_b128 v[118:121], v78
	ds_read_b128 v[136:139], v78 offset:8192
	ds_read_b128 v[140:143], v78 offset:16384
	ds_read_b128 v[144:147], v78 offset:24576
	s_mov_b32 s9, 0x32000
	v_add_co_u32_e32 v148, vcc, s9, v54
	s_nop 1
	v_addc_co_u32_e32 v149, vcc, 0, v55, vcc
	s_waitcnt vmcnt(14) lgkmcnt(3)
	v_mfma_f32_16x16x32_f16 v[86:89], v[110:113], v[118:121], v[86:89]
	s_waitcnt lgkmcnt(2)
	v_mfma_f32_16x16x32_f16 v[90:93], v[110:113], v[136:139], v[90:93]
	s_waitcnt lgkmcnt(1)
	v_mfma_f32_16x16x32_f16 v[94:97], v[110:113], v[140:143], v[94:97]
	s_waitcnt lgkmcnt(0)
	v_mfma_f32_16x16x32_f16 v[80:83], v[110:113], v[144:147], v[82:85]
	s_waitcnt vmcnt(13)
	v_mfma_f32_16x16x32_f16 v[110:113], v[124:127], v[118:121], v[38:41]
	v_mfma_f32_16x16x32_f16 v[50:53], v[124:127], v[136:139], v[50:53]
	v_mfma_f32_16x16x32_f16 v[98:101], v[124:127], v[140:143], v[98:101]
	v_mfma_f32_16x16x32_f16 v[62:65], v[124:127], v[144:147], v[62:65]
	s_waitcnt vmcnt(12)
	v_mfma_f32_16x16x32_f16 v[118:121], v[128:131], v[118:121], v[42:45]
	v_mfma_f32_16x16x32_f16 v[68:71], v[128:131], v[136:139], v[68:71]
	v_mfma_f32_16x16x32_f16 v[114:117], v[128:131], v[140:143], v[114:117]
	v_mfma_f32_16x16x32_f16 v[122:125], v[128:131], v[144:147], v[46:49]
	s_nop 2
	global_load_dwordx4 v[46:49], v[148:149], off offset:1024
	global_load_dwordx4 v[42:45], v[148:149], off offset:2048
	global_load_dwordx4 v[38:41], v[148:149], off offset:3072
	v_bitop3_b32 v73, v158, v1, 28 bitop3:0x36
	v_lshl_or_b32 v79, v73, 4, v67
	ds_read_b128 v[126:129], v79
	ds_read_b128 v[136:139], v79 offset:8192
	ds_read_b128 v[140:143], v79 offset:16384
	ds_read_b128 v[144:147], v79 offset:24576
	s_waitcnt vmcnt(14) lgkmcnt(3)
	v_mfma_f32_16x16x32_f16 v[84:87], v[102:105], v[126:129], v[86:89]
	s_waitcnt lgkmcnt(2)
	v_mfma_f32_16x16x32_f16 v[88:91], v[102:105], v[136:139], v[90:93]
	s_waitcnt lgkmcnt(1)
	v_mfma_f32_16x16x32_f16 v[92:95], v[102:105], v[140:143], v[94:97]
	s_waitcnt lgkmcnt(0)
	v_mfma_f32_16x16x32_f16 v[80:83], v[102:105], v[144:147], v[80:83]
	s_waitcnt vmcnt(13)
	v_mfma_f32_16x16x32_f16 v[102:105], v[106:109], v[126:129], v[110:113]
	v_mfma_f32_16x16x32_f16 v[110:113], v[106:109], v[136:139], v[50:53]
	v_mfma_f32_16x16x32_f16 v[96:99], v[106:109], v[140:143], v[98:101]
	v_mfma_f32_16x16x32_f16 v[62:65], v[106:109], v[144:147], v[62:65]
	s_waitcnt vmcnt(12)
	v_mfma_f32_16x16x32_f16 v[106:109], v[132:135], v[126:129], v[118:121]
	v_mfma_f32_16x16x32_f16 v[118:121], v[132:135], v[136:139], v[68:71]
	v_mfma_f32_16x16x32_f16 v[114:117], v[132:135], v[140:143], v[114:117]
	v_mfma_f32_16x16x32_f16 v[50:53], v[132:135], v[144:147], v[122:125]
	v_lshl_add_u64 v[56:57], v[56:57], 2, s[4:5]
	s_nop 1
	global_load_dwordx4 v[122:125], v[56:57], off
	global_load_dwordx4 v[126:129], v[56:57], off offset:64
	global_load_dwordx4 v[130:133], v[56:57], off offset:128
	v_lshl_or_b32 v67, v158, 3, s8
	s_movk_i32 s4, 0x310
	v_mov_b32_e32 v100, v89
	v_mov_b32_e32 v101, v90
	v_mov_b32_e32 v134, v93
	v_mov_b32_e32 v135, v94
	v_mov_b32_e32 v140, v97
	v_mov_b32_e32 v141, v98
	v_mad_u32_u24 v69, v1, s4, v67
	v_mov_b32_e32 v143, v64
	v_mov_b32_e32 v136, v81
	v_mov_b32_e32 v137, v82
	v_mov_b32_e32 v138, v111
	v_mov_b32_e32 v139, v112
	v_mov_b32_e32 v142, v63
	v_add_u32_e32 v73, 0x8000, v69
	s_barrier
	v_add_u32_e32 v70, 0xb000, v69
	v_add_u32_e32 v71, 0xe000, v69
	v_add_u32_e32 v68, 0x9300, v69
	s_movk_i32 s5, 0x600
	s_movk_i32 s10, 0x1c7
	s_waitcnt vmcnt(2)
	v_pk_add_f32 v[84:85], v[84:85], v[122:123]
	v_add_f32_e32 v1, v88, v122
	v_pk_mov_b32 v[88:89], v[122:123], v[124:125] op_sel:[1,0]
	v_add_f32_e32 v67, v91, v125
	v_add_f32_e32 v92, v92, v122
	v_add_f32_e32 v93, v95, v125
	v_add_f32_e32 v94, v80, v122
	v_add_f32_e32 v95, v83, v125
	s_waitcnt vmcnt(1)
	v_add_f32_e32 v97, v110, v126
	v_add_f32_e32 v98, v113, v129
	v_add_f32_e32 v96, v96, v126
	v_add_f32_e32 v99, v99, v129
	v_cvt_pk_f16_f32 v64, v84, v85
	v_cvt_f16_f32_e32 v1, v1
	v_pk_add_f32 v[84:85], v[100:101], v[88:89]
	v_cvt_f16_f32_e32 v67, v67
	v_cvt_f16_f32_e32 v100, v92
	v_cvt_f16_f32_e32 v101, v93
	v_cvt_f16_f32_e32 v94, v94
	v_cvt_f16_f32_e32 v95, v95
	v_cvt_f16_f32_e32 v97, v97
	v_cvt_f16_f32_e32 v98, v98
	v_pk_add_f32 v[86:87], v[86:87], v[124:125]
	v_pk_add_f32 v[80:81], v[102:103], v[126:127]
	v_pk_add_f32 v[82:83], v[104:105], v[128:129]
	v_pk_mov_b32 v[90:91], v[126:127], v[128:129] op_sel:[1,0]
	v_cvt_f16_f32_e32 v96, v96
	v_cvt_f16_f32_e32 v99, v99
	v_add_f32_e32 v102, v62, v126
	v_add_f32_e32 v103, v65, v129
	s_waitcnt vmcnt(0)
	v_pk_add_f32 v[62:63], v[106:107], v[130:131]
	v_cvt_pk_f16_f32 v65, v86, v87
	v_pk_add_f32 v[86:87], v[134:135], v[88:89]
	v_pk_add_f32 v[88:89], v[136:137], v[88:89]
	v_cvt_pk_f16_f32 v80, v80, v81
	v_cvt_pk_f16_f32 v81, v82, v83
	v_pk_add_f32 v[82:83], v[138:139], v[90:91]
	v_pk_add_f32 v[92:93], v[140:141], v[90:91]
	v_cvt_pk_f16_f32 v62, v62, v63
	v_cvt_pk_f16_f32 v63, v84, v85
	v_cvt_pk_f16_f32 v84, v86, v87
	v_cvt_pk_f16_f32 v85, v88, v89
	v_cvt_pk_f16_f32 v86, v82, v83
	v_cvt_pk_f16_f32 v87, v92, v93
	ds_write2_b64 v73, v[64:65], v[80:81] offset1:4
	v_pack_b32_f16 v64, v1, v63
	v_alignbit_b32 v65, v67, v63, 16
	v_pack_b32_f16 v80, v100, v84
	v_alignbit_b32 v81, v101, v84, 16
	v_pack_b32_f16 v82, v94, v85
	v_alignbit_b32 v83, v95, v85, 16
	v_pack_b32_f16 v84, v97, v86
	v_alignbit_b32 v85, v98, v86, 16
	v_pack_b32_f16 v86, v96, v87
	v_alignbit_b32 v87, v99, v87, 16
	ds_write2_b64 v70, v[64:65], v[84:85] offset0:32 offset1:36
	ds_write2_b64 v71, v[80:81], v[86:87] offset0:64 offset1:68
	v_pk_add_f32 v[64:65], v[108:109], v[132:133]
	v_add_f32_e32 v1, v118, v130
	v_cvt_pk_f16_f32 v63, v64, v65
	v_cvt_f16_f32_e32 v1, v1
	v_add_f32_e32 v67, v121, v133
	ds_write_b64 v69, v[62:63] offset:32832
	v_mov_b32_e32 v62, v119
	v_mov_b32_e32 v63, v120
	v_pk_mov_b32 v[64:65], v[130:131], v[132:133] op_sel:[1,0]
	v_cvt_f16_f32_e32 v67, v67
	v_pk_add_f32 v[62:63], v[62:63], v[64:65]
	v_cvt_f16_f32_e32 v102, v102
	v_cvt_pk_f16_f32 v63, v62, v63
	v_pack_b32_f16 v62, v1, v63
	v_add_f32_e32 v1, v114, v130
	v_alignbit_b32 v63, v67, v63, 16
	v_cvt_f16_f32_e32 v1, v1
	ds_write_b64 v69, v[62:63] offset:45376
	v_mov_b32_e32 v62, v115
	v_mov_b32_e32 v63, v116
	v_pk_add_f32 v[62:63], v[62:63], v[64:65]
	v_add_f32_e32 v67, v117, v133
	v_cvt_pk_f16_f32 v63, v62, v63
	v_pack_b32_f16 v62, v1, v63
	v_add_f32_e32 v1, v50, v130
	v_mov_b32_e32 v50, v51
	v_mov_b32_e32 v51, v52
	v_add_f32_e32 v52, v53, v133
	v_cvt_f16_f32_e32 v103, v103
	v_cvt_f16_f32_e32 v67, v67
	v_cvt_f16_f32_e32 v1, v1
	v_cvt_f16_f32_e32 v52, v52
	v_pk_add_f32 v[90:91], v[142:143], v[90:91]
	v_pk_add_f32 v[50:51], v[50:51], v[64:65]
	v_cvt_pk_f16_f32 v89, v90, v91
	v_cvt_pk_f16_f32 v51, v50, v51
	v_pack_b32_f16 v88, v102, v89
	v_alignbit_b32 v89, v103, v89, 16
	v_add_u32_e32 v80, 0x8000, v68
	v_alignbit_b32 v63, v67, v63, 16
	v_pack_b32_f16 v50, v1, v51
	v_alignbit_b32 v51, v52, v51, 16
	ds_write2_b64 v80, v[82:83], v[88:89] offset1:4
	ds_write_b64 v69, v[62:63] offset:57920
	ds_write_b64 v68, v[50:51] offset:32832
	s_waitcnt lgkmcnt(0)
	s_barrier
	global_load_dwordx4 v[82:85], v[58:59], off
	global_load_dwordx4 v[86:89], v[58:59], off offset:1024
	global_load_dwordx4 v[90:93], v[58:59], off offset:2048
	v_add_lshl_u32 v52, v150, v0, 4
	v_mad_u64_u32 v[50:51], s[8:9], v61, s5, v[52:53]
	v_or_b32_e32 v1, 0x200, v0
	v_mad_u32_u24 v51, v60, s4, v52
	v_mul_u32_u24_e32 v52, 0x556, v1
	v_lshrrev_b32_e32 v53, 16, v52
	v_mul_lo_u32 v52, v53, s7
	v_add_lshl_u32 v52, v52, v1, 4
	v_lshlrev_b32_e32 v1, 3, v53
	s_movk_i32 s8, 0xc7
	ds_read_b128 v[60:63], v51 offset:32768
	v_bitop3_b32 v1, v1, s8, v53 bitop3:0xc8
	v_or_b32_e32 v1, s6, v1
	v_mad_u32_u24 v81, v53, s4, v52
	v_mad_u64_u32 v[52:53], s[8:9], v1, s5, v[52:53]
	v_or_b32_e32 v1, 0x400, v0
	v_mul_u32_u24_e32 v53, 0x556, v1
	v_lshrrev_b32_e32 v53, 16, v53
	ds_read_b128 v[94:97], v81 offset:32768
	s_waitcnt lgkmcnt(1)
	buffer_store_dwordx4 v[60:63], v50, s[0:3], 0 offen sc1
	s_waitcnt lgkmcnt(0)
	buffer_store_dwordx4 v[94:97], v52, s[0:3], 0 offen sc1
	v_lshlrev_b32_e32 v61, 3, v53
	v_mul_lo_u32 v60, v53, s7
	v_bitop3_b32 v61, v61, s10, v53 bitop3:0xc8
	v_or_b32_e32 v61, s6, v61
	v_add_lshl_u32 v62, v60, v1, 4
	v_mad_u64_u32 v[60:61], s[8:9], v61, s5, v[62:63]
	v_or_b32_e32 v1, 0x600, v0
	v_mad_u32_u24 v53, v53, s4, v62
	v_mul_u32_u24_e32 v61, 0x556, v1
	ds_read_b128 v[62:65], v53 offset:32768
	v_lshrrev_b32_e32 v67, 16, v61
	v_mul_lo_u32 v94, v67, s7
	v_add_lshl_u32 v98, v94, v1, 4
	v_lshrrev_b32_e32 v1, 13, v61
	v_mad_u32_u24 v160, v67, s4, v98
	v_and_b32_e32 v1, 0x1c0, v1
	v_bfe_u32 v61, v61, 16, 3
	ds_read_b128 v[94:97], v160 offset:32768
	v_or3_b32 v1, s6, v61, v1
	s_waitcnt lgkmcnt(1)
	buffer_store_dwordx4 v[62:65], v60, s[0:3], 0 offen sc1
	s_nop 1
	v_mad_u64_u32 v[62:63], s[8:9], v1, s5, v[98:99]
	v_or_b32_e32 v1, 0x800, v0
	v_mul_u32_u24_e32 v61, 0xaab, v1
	v_lshrrev_b32_e32 v61, 17, v61
	v_mul_lo_u32 v63, v61, s7
	v_lshlrev_b32_e32 v64, 3, v61
	s_waitcnt lgkmcnt(0)
	buffer_store_dwordx4 v[94:97], v62, s[0:3], 0 offen sc1
	v_bitop3_b32 v64, v64, s10, v61 bitop3:0xc8
	v_or_b32_e32 v64, s6, v64
	v_add_lshl_u32 v94, v63, v1, 4
	v_mad_u32_u24 v61, v61, s4, v94
	v_or_b32_e32 v0, 0xa00, v0
	v_mad_u64_u32 v[64:65], s[8:9], v64, s5, v[94:95]
	ds_read_b128 v[94:97], v61 offset:32768
	v_mul_u32_u24_e32 v1, 0xaab, v0
	v_lshrrev_b32_e32 v63, 17, v1
	v_mul_lo_u32 v65, v63, s7
	v_add_lshl_u32 v0, v65, v0, 4
	v_mad_u32_u24 v63, v63, s4, v0
	ds_read_b128 v[98:101], v63 offset:32768
	s_waitcnt lgkmcnt(1)
	buffer_store_dwordx4 v[94:97], v64, s[0:3], 0 offen sc1
	ds_read_b128 v[94:97], v66
	ds_read_b128 v[102:105], v66 offset:8192
	ds_read_b128 v[106:109], v66 offset:16384
	ds_read_b128 v[110:113], v66 offset:24576
	v_lshrrev_b32_e32 v65, 14, v1
	v_and_b32_e32 v65, 0x1c0, v65
	v_bfe_u32 v1, v1, 17, 3
	v_or3_b32 v1, s6, v1, v65
	v_mad_u64_u32 v[66:67], s[4:5], v1, s5, v[0:1]
	s_waitcnt lgkmcnt(4)
	buffer_store_dwordx4 v[98:101], v66, s[0:3], 0 offen sc1
	s_waitcnt lgkmcnt(3)
	s_nop 0
	v_mfma_f32_16x16x32_f16 v[98:101], v[34:37], v[94:97], 0
	s_waitcnt lgkmcnt(2)
	v_mfma_f32_16x16x32_f16 v[114:117], v[34:37], v[102:105], 0
	s_waitcnt lgkmcnt(1)
	v_mfma_f32_16x16x32_f16 v[118:121], v[34:37], v[106:109], 0
	s_waitcnt lgkmcnt(0)
	v_mfma_f32_16x16x32_f16 v[34:37], v[34:37], v[110:113], 0
	v_mfma_f32_16x16x32_f16 v[122:125], v[26:29], v[94:97], 0
	v_mfma_f32_16x16x32_f16 v[126:129], v[26:29], v[102:105], 0
	v_mfma_f32_16x16x32_f16 v[130:133], v[26:29], v[106:109], 0
	v_mfma_f32_16x16x32_f16 v[26:29], v[26:29], v[110:113], 0
	v_mfma_f32_16x16x32_f16 v[94:97], v[22:25], v[94:97], 0
	v_mfma_f32_16x16x32_f16 v[102:105], v[22:25], v[102:105], 0
	v_mfma_f32_16x16x32_f16 v[106:109], v[22:25], v[106:109], 0
	v_mfma_f32_16x16x32_f16 v[22:25], v[22:25], v[110:113], 0
	s_mov_b32 s4, 0x34000
	v_add_co_u32_e32 v158, vcc, s4, v54
	s_mov_b32 s4, 0x35000
	s_nop 0
	v_addc_co_u32_e32 v159, vcc, 0, v55, vcc
	v_add_co_u32_e32 v54, vcc, s4, v54
	s_nop 1
	v_addc_co_u32_e32 v55, vcc, 0, v55, vcc
	global_load_dwordx4 v[110:113], v[54:55], off offset:-4096
	global_load_dwordx4 v[134:137], v[58:59], off offset:3072
	global_load_dwordx4 v[138:141], v[158:159], off offset:1024
	ds_read_b128 v[142:145], v72
	ds_read_b128 v[146:149], v72 offset:8192
	ds_read_b128 v[150:153], v72 offset:16384
	ds_read_b128 v[154:157], v72 offset:24576
	s_waitcnt lgkmcnt(3)
	v_mfma_f32_16x16x32_f16 v[98:101], v[14:17], v[142:145], v[98:101]
	s_waitcnt lgkmcnt(2)
	v_mfma_f32_16x16x32_f16 v[114:117], v[14:17], v[146:149], v[114:117]
	s_waitcnt lgkmcnt(1)
	v_mfma_f32_16x16x32_f16 v[118:121], v[14:17], v[150:153], v[118:121]
	s_waitcnt lgkmcnt(0)
	v_mfma_f32_16x16x32_f16 v[14:17], v[14:17], v[154:157], v[34:37]
	v_mfma_f32_16x16x32_f16 v[34:37], v[6:9], v[142:145], v[122:125]
	v_mfma_f32_16x16x32_f16 v[122:125], v[6:9], v[146:149], v[126:129]
	v_mfma_f32_16x16x32_f16 v[126:129], v[6:9], v[150:153], v[130:133]
	v_mfma_f32_16x16x32_f16 v[6:9], v[6:9], v[154:157], v[26:29]
	v_mfma_f32_16x16x32_f16 v[26:29], v[2:5], v[142:145], v[94:97]
	v_mfma_f32_16x16x32_f16 v[94:97], v[2:5], v[146:149], v[102:105]
	v_mfma_f32_16x16x32_f16 v[102:105], v[2:5], v[150:153], v[106:109]
	v_mfma_f32_16x16x32_f16 v[0:3], v[2:5], v[154:157], v[22:25]
	s_nop 2
	global_load_dwordx4 v[22:25], v[158:159], off offset:2048
	global_load_dwordx4 v[106:109], v[158:159], off offset:3072
	global_load_dwordx4 v[130:133], v[54:55], off
	ds_read_b128 v[142:145], v74
	ds_read_b128 v[146:149], v74 offset:8192
	ds_read_b128 v[150:153], v74 offset:16384
	ds_read_b128 v[154:157], v74 offset:24576
	s_waitcnt lgkmcnt(3)
	v_mfma_f32_16x16x32_f16 v[98:101], v[18:21], v[142:145], v[98:101]
	s_waitcnt lgkmcnt(2)
	v_mfma_f32_16x16x32_f16 v[114:117], v[18:21], v[146:149], v[114:117]
	s_waitcnt lgkmcnt(1)
	v_mfma_f32_16x16x32_f16 v[118:121], v[18:21], v[150:153], v[118:121]
	s_waitcnt lgkmcnt(0)
	v_mfma_f32_16x16x32_f16 v[14:17], v[18:21], v[154:157], v[14:17]
	v_mfma_f32_16x16x32_f16 v[18:21], v[10:13], v[142:145], v[34:37]
	v_mfma_f32_16x16x32_f16 v[34:37], v[10:13], v[146:149], v[122:125]
	v_mfma_f32_16x16x32_f16 v[122:125], v[10:13], v[150:153], v[126:129]
	v_mfma_f32_16x16x32_f16 v[4:7], v[10:13], v[154:157], v[6:9]
	v_mfma_f32_16x16x32_f16 v[8:11], v[30:33], v[142:145], v[26:29]
	v_mfma_f32_16x16x32_f16 v[26:29], v[30:33], v[146:149], v[94:97]
	v_mfma_f32_16x16x32_f16 v[94:97], v[30:33], v[150:153], v[102:105]
	v_mfma_f32_16x16x32_f16 v[0:3], v[30:33], v[154:157], v[0:3]
	global_load_dwordx4 v[30:33], v[54:55], off offset:1024
	s_nop 0
	global_load_dwordx4 v[102:105], v[54:55], off offset:2048
	global_load_dwordx4 v[126:129], v[54:55], off offset:3072
	ds_read_b128 v[142:145], v75
	ds_read_b128 v[146:149], v75 offset:8192
	ds_read_b128 v[150:153], v75 offset:16384
	ds_read_b128 v[154:157], v75 offset:24576
	s_waitcnt lgkmcnt(3)
	v_mfma_f32_16x16x32_f16 v[98:101], v[46:49], v[142:145], v[98:101]
	s_waitcnt lgkmcnt(2)
	v_mfma_f32_16x16x32_f16 v[114:117], v[46:49], v[146:149], v[114:117]
	s_waitcnt lgkmcnt(1)
	v_mfma_f32_16x16x32_f16 v[118:121], v[46:49], v[150:153], v[118:121]
	s_waitcnt lgkmcnt(0)
	v_mfma_f32_16x16x32_f16 v[12:15], v[46:49], v[154:157], v[14:17]
	v_mfma_f32_16x16x32_f16 v[16:19], v[42:45], v[142:145], v[18:21]
	v_mfma_f32_16x16x32_f16 v[34:37], v[42:45], v[146:149], v[34:37]
	v_mfma_f32_16x16x32_f16 v[46:49], v[42:45], v[150:153], v[122:125]
	v_mfma_f32_16x16x32_f16 v[4:7], v[42:45], v[154:157], v[4:7]
	v_mfma_f32_16x16x32_f16 v[8:11], v[38:41], v[142:145], v[8:11]
	v_mfma_f32_16x16x32_f16 v[26:29], v[38:41], v[146:149], v[26:29]
	v_mfma_f32_16x16x32_f16 v[42:45], v[38:41], v[150:153], v[94:97]
	v_mfma_f32_16x16x32_f16 v[0:3], v[38:41], v[154:157], v[0:3]
	ds_read_b128 v[38:41], v76
	s_nop 0
	ds_read_b128 v[94:97], v76 offset:8192
	ds_read_b128 v[122:125], v76 offset:16384
	ds_read_b128 v[142:145], v76 offset:24576
	s_waitcnt vmcnt(17) lgkmcnt(3)
	v_mfma_f32_16x16x32_f16 v[98:101], v[82:85], v[38:41], v[98:101]
	s_waitcnt lgkmcnt(2)
	v_mfma_f32_16x16x32_f16 v[114:117], v[82:85], v[94:97], v[114:117]
	s_waitcnt lgkmcnt(1)
	v_mfma_f32_16x16x32_f16 v[118:121], v[82:85], v[122:125], v[118:121]
	s_waitcnt lgkmcnt(0)
	v_mfma_f32_16x16x32_f16 v[12:15], v[82:85], v[142:145], v[12:15]
	s_waitcnt vmcnt(16)
	v_mfma_f32_16x16x32_f16 v[16:19], v[86:89], v[38:41], v[16:19]
	v_mfma_f32_16x16x32_f16 v[34:37], v[86:89], v[94:97], v[34:37]
	v_mfma_f32_16x16x32_f16 v[46:49], v[86:89], v[122:125], v[46:49]
	v_mfma_f32_16x16x32_f16 v[4:7], v[86:89], v[142:145], v[4:7]
	s_waitcnt vmcnt(15)
	v_mfma_f32_16x16x32_f16 v[8:11], v[90:93], v[38:41], v[8:11]
	v_mfma_f32_16x16x32_f16 v[26:29], v[90:93], v[94:97], v[26:29]
	v_mfma_f32_16x16x32_f16 v[38:41], v[90:93], v[122:125], v[42:45]
	v_mfma_f32_16x16x32_f16 v[0:3], v[90:93], v[142:145], v[0:3]
	s_nop 1
	ds_read_b128 v[42:45], v77
	ds_read_b128 v[82:85], v77 offset:8192
	ds_read_b128 v[86:89], v77 offset:16384
	ds_read_b128 v[74:77], v77 offset:24576
	s_waitcnt vmcnt(7) lgkmcnt(3)
	v_mfma_f32_16x16x32_f16 v[90:93], v[134:137], v[42:45], v[98:101]
	s_waitcnt lgkmcnt(2)
	v_mfma_f32_16x16x32_f16 v[94:97], v[134:137], v[82:85], v[114:117]
	s_waitcnt lgkmcnt(1)
	v_mfma_f32_16x16x32_f16 v[98:101], v[134:137], v[86:89], v[118:121]
	s_waitcnt lgkmcnt(0)
	v_mfma_f32_16x16x32_f16 v[12:15], v[134:137], v[74:77], v[12:15]
	v_mfma_f32_16x16x32_f16 v[16:19], v[110:113], v[42:45], v[16:19]
	v_mfma_f32_16x16x32_f16 v[34:37], v[110:113], v[82:85], v[34:37]
	v_mfma_f32_16x16x32_f16 v[46:49], v[110:113], v[86:89], v[46:49]
	v_mfma_f32_16x16x32_f16 v[4:7], v[110:113], v[74:77], v[4:7]
	s_waitcnt vmcnt(6)
	v_mfma_f32_16x16x32_f16 v[8:11], v[138:141], v[42:45], v[8:11]
	v_mfma_f32_16x16x32_f16 v[26:29], v[138:141], v[82:85], v[26:29]
	v_mfma_f32_16x16x32_f16 v[38:41], v[138:141], v[86:89], v[38:41]
	v_mfma_f32_16x16x32_f16 v[0:3], v[138:141], v[74:77], v[0:3]
	ds_read_b128 v[42:45], v78
	ds_read_b128 v[74:77], v78 offset:8192
	ds_read_b128 v[82:85], v78 offset:16384
	ds_read_b128 v[86:89], v78 offset:24576
	s_waitcnt vmcnt(5) lgkmcnt(3)
	v_mfma_f32_16x16x32_f16 v[90:93], v[22:25], v[42:45], v[90:93]
	s_waitcnt lgkmcnt(2)
	v_mfma_f32_16x16x32_f16 v[94:97], v[22:25], v[74:77], v[94:97]
	s_waitcnt lgkmcnt(1)
	v_mfma_f32_16x16x32_f16 v[98:101], v[22:25], v[82:85], v[98:101]
	s_waitcnt lgkmcnt(0)
	v_mfma_f32_16x16x32_f16 v[12:15], v[22:25], v[86:89], v[12:15]
	s_waitcnt vmcnt(4)
	v_mfma_f32_16x16x32_f16 v[16:19], v[106:109], v[42:45], v[16:19]
	v_mfma_f32_16x16x32_f16 v[20:23], v[106:109], v[74:77], v[34:37]
	v_mfma_f32_16x16x32_f16 v[34:37], v[106:109], v[82:85], v[46:49]
	v_mfma_f32_16x16x32_f16 v[4:7], v[106:109], v[86:89], v[4:7]
	s_waitcnt vmcnt(3)
	v_mfma_f32_16x16x32_f16 v[8:11], v[130:133], v[42:45], v[8:11]
	v_mfma_f32_16x16x32_f16 v[24:27], v[130:133], v[74:77], v[26:29]
	v_mfma_f32_16x16x32_f16 v[38:41], v[130:133], v[82:85], v[38:41]
	v_mfma_f32_16x16x32_f16 v[0:3], v[130:133], v[86:89], v[0:3]
	ds_read_b128 v[42:45], v79
	ds_read_b128 v[46:49], v79 offset:8192
	ds_read_b128 v[74:77], v79 offset:16384
	ds_read_b128 v[82:85], v79 offset:24576
	s_waitcnt vmcnt(2) lgkmcnt(3)
	v_mfma_f32_16x16x32_f16 v[86:89], v[30:33], v[42:45], v[90:93]
	s_waitcnt lgkmcnt(2)
	v_mfma_f32_16x16x32_f16 v[90:93], v[30:33], v[46:49], v[94:97]
	s_waitcnt lgkmcnt(1)
	v_mfma_f32_16x16x32_f16 v[94:97], v[30:33], v[74:77], v[98:101]
	s_waitcnt lgkmcnt(0)
	v_mfma_f32_16x16x32_f16 v[12:15], v[30:33], v[82:85], v[12:15]
	s_waitcnt vmcnt(1)
	v_mfma_f32_16x16x32_f16 v[16:19], v[102:105], v[42:45], v[16:19]
	v_mfma_f32_16x16x32_f16 v[20:23], v[102:105], v[46:49], v[20:23]
	v_mfma_f32_16x16x32_f16 v[28:31], v[102:105], v[74:77], v[34:37]
	v_mfma_f32_16x16x32_f16 v[4:7], v[102:105], v[82:85], v[4:7]
	s_waitcnt vmcnt(0)
	v_mfma_f32_16x16x32_f16 v[8:11], v[126:129], v[42:45], v[8:11]
	v_mfma_f32_16x16x32_f16 v[24:27], v[126:129], v[46:49], v[24:27]
	v_mfma_f32_16x16x32_f16 v[32:35], v[126:129], v[74:77], v[38:41]
	v_mfma_f32_16x16x32_f16 v[0:3], v[126:129], v[82:85], v[0:3]
	s_nop 1
	global_load_dwordx4 v[36:39], v[56:57], off offset:1536
	global_load_dwordx4 v[40:43], v[56:57], off offset:1600
	global_load_dwordx4 v[44:47], v[56:57], off offset:1664
	v_mov_b32_e32 v58, v21
	v_mov_b32_e32 v59, v22
	v_mov_b32_e32 v74, v29
	v_mov_b32_e32 v56, v13
	v_mov_b32_e32 v57, v14
	v_mov_b32_e32 v75, v30
	v_mov_b32_e32 v48, v91
	v_mov_b32_e32 v49, v92
	v_mov_b32_e32 v54, v95
	v_mov_b32_e32 v55, v96
	v_mov_b32_e32 v76, v5
	v_mov_b32_e32 v77, v6
	s_barrier
	s_waitcnt vmcnt(2)
	v_pk_add_f32 v[78:79], v[86:87], v[36:37]
	v_pk_add_f32 v[82:83], v[88:89], v[38:39]
	v_add_f32_e32 v21, v90, v36
	v_pk_mov_b32 v[84:85], v[36:37], v[38:39] op_sel:[1,0]
	v_add_f32_e32 v22, v93, v39
	v_add_f32_e32 v29, v94, v36
	v_add_f32_e32 v36, v12, v36
	v_add_f32_e32 v37, v15, v39
	s_waitcnt vmcnt(1)
	v_add_f32_e32 v38, v20, v40
	v_add_f32_e32 v23, v23, v43
	v_add_f32_e32 v30, v97, v39
	v_pk_add_f32 v[12:13], v[16:17], v[40:41]
	v_pk_add_f32 v[14:15], v[18:19], v[42:43]
	v_pk_mov_b32 v[16:17], v[40:41], v[42:43] op_sel:[1,0]
	v_add_f32_e32 v28, v28, v40
	v_add_f32_e32 v31, v31, v43
	v_add_f32_e32 v39, v4, v40
	v_add_f32_e32 v40, v7, v43
	v_cvt_f16_f32_e32 v41, v21
	v_cvt_f16_f32_e32 v42, v22
	v_cvt_f16_f32_e32 v36, v36
	v_cvt_f16_f32_e32 v37, v37
	v_cvt_f16_f32_e32 v38, v38
	v_cvt_f16_f32_e32 v43, v23
	v_cvt_f16_f32_e32 v29, v29
	v_cvt_f16_f32_e32 v30, v30
	v_cvt_f16_f32_e32 v28, v28
	v_cvt_f16_f32_e32 v31, v31
	v_cvt_f16_f32_e32 v39, v39
	v_cvt_f16_f32_e32 v40, v40
	s_waitcnt vmcnt(0)
	v_pk_add_f32 v[4:5], v[8:9], v[44:45]
	v_pk_add_f32 v[6:7], v[10:11], v[46:47]
	v_pk_add_f32 v[10:11], v[48:49], v[84:85]
	v_pk_add_f32 v[20:21], v[56:57], v[84:85]
	v_cvt_pk_f16_f32 v12, v12, v13
	v_cvt_pk_f16_f32 v13, v14, v15
	v_pk_add_f32 v[14:15], v[58:59], v[16:17]
	v_cvt_pk_f16_f32 v8, v78, v79
	v_cvt_pk_f16_f32 v9, v82, v83
	v_pk_add_f32 v[18:19], v[54:55], v[84:85]
	v_pk_add_f32 v[22:23], v[74:75], v[16:17]
	v_pk_add_f32 v[16:17], v[76:77], v[16:17]
	v_cvt_pk_f16_f32 v4, v4, v5
	v_cvt_pk_f16_f32 v5, v6, v7
	v_cvt_pk_f16_f32 v6, v10, v11
	v_cvt_pk_f16_f32 v10, v20, v21
	v_cvt_pk_f16_f32 v11, v14, v15
	v_cvt_pk_f16_f32 v7, v18, v19
	v_cvt_pk_f16_f32 v14, v22, v23
	v_cvt_pk_f16_f32 v15, v16, v17
	ds_write2_b64 v73, v[8:9], v[12:13] offset1:4
	ds_write_b64 v69, v[4:5] offset:32832
	v_pack_b32_f16 v4, v41, v6
	v_alignbit_b32 v5, v42, v6, 16
	v_pack_b32_f16 v8, v36, v10
	v_alignbit_b32 v9, v37, v10, 16
	v_pack_b32_f16 v10, v38, v11
	v_alignbit_b32 v11, v43, v11, 16
	v_add_f32_e32 v24, v24, v44
	v_pack_b32_f16 v6, v29, v7
	v_alignbit_b32 v7, v30, v7, 16
	v_pack_b32_f16 v12, v28, v14
	v_alignbit_b32 v13, v31, v14, 16
	v_pack_b32_f16 v14, v39, v15
	v_alignbit_b32 v15, v40, v15, 16
	ds_write2_b64 v70, v[4:5], v[10:11] offset0:32 offset1:36
	ds_write2_b64 v71, v[6:7], v[12:13] offset0:64 offset1:68
	ds_write2_b64 v80, v[8:9], v[14:15] offset1:4
	v_add_f32_e32 v8, v27, v47
	v_cvt_f16_f32_e32 v24, v24
	v_cvt_f16_f32_e32 v8, v8
	v_mov_b32_e32 v4, v25
	v_mov_b32_e32 v5, v26
	v_pk_mov_b32 v[6:7], v[44:45], v[46:47] op_sel:[1,0]
	v_add_f32_e32 v9, v35, v47
	v_pk_add_f32 v[4:5], v[4:5], v[6:7]
	v_cvt_f16_f32_e32 v9, v9
	v_cvt_pk_f16_f32 v5, v4, v5
	v_pack_b32_f16 v4, v24, v5
	v_alignbit_b32 v5, v8, v5, 16
	ds_write_b64 v69, v[4:5] offset:45376
	v_add_f32_e32 v4, v32, v44
	v_cvt_f16_f32_e32 v8, v4
	v_mov_b32_e32 v4, v33
	v_mov_b32_e32 v5, v34
	v_pk_add_f32 v[4:5], v[4:5], v[6:7]
	v_add_f32_e32 v0, v0, v44
	v_cvt_pk_f16_f32 v5, v4, v5
	v_pack_b32_f16 v4, v8, v5
	v_alignbit_b32 v5, v9, v5, 16
	ds_write_b64 v69, v[4:5] offset:57920
	v_cvt_f16_f32_e32 v4, v0
	v_mov_b32_e32 v0, v1
	v_mov_b32_e32 v1, v2
	v_add_f32_e32 v2, v3, v47
	v_cvt_f16_f32_e32 v2, v2
	v_pk_add_f32 v[0:1], v[0:1], v[6:7]
	s_nop 0
	v_cvt_pk_f16_f32 v1, v0, v1
	v_pack_b32_f16 v0, v4, v1
	v_alignbit_b32 v1, v2, v1, 16
	ds_write_b64 v68, v[0:1] offset:32832
	s_waitcnt lgkmcnt(0)
	s_barrier
	ds_read_b128 v[0:3], v51 offset:32768
	ds_read_b128 v[4:7], v81 offset:32768
	s_waitcnt lgkmcnt(1)
	buffer_store_dwordx4 v[0:3], v50, s[0:3], 0 offen offset:768 sc1
	ds_read_b128 v[0:3], v53 offset:32768
	ds_read_b128 v[8:11], v160 offset:32768
	ds_read_b128 v[12:15], v61 offset:32768
	ds_read_b128 v[16:19], v63 offset:32768
	s_waitcnt lgkmcnt(4)
	buffer_store_dwordx4 v[4:7], v52, s[0:3], 0 offen offset:768 sc1
	s_waitcnt lgkmcnt(3)
	buffer_store_dwordx4 v[0:3], v60, s[0:3], 0 offen offset:768 sc1
	s_waitcnt lgkmcnt(2)
	buffer_store_dwordx4 v[8:11], v62, s[0:3], 0 offen offset:768 sc1
	s_waitcnt lgkmcnt(1)
	buffer_store_dwordx4 v[12:15], v64, s[0:3], 0 offen offset:768 sc1
	s_waitcnt lgkmcnt(0)
	buffer_store_dwordx4 v[16:19], v66, s[0:3], 0 offen offset:768 sc1
	s_endpgm
	.p2alignl 8, 3212836864

	.amdhsa_kernel _Z7k_stageILi0ELi4EEv8AttnArgsPKDF16_PKfPDF16_iii
		.amdhsa_group_segment_fixed_size 82944
		.amdhsa_private_segment_fixed_size 0
		.amdhsa_kernarg_size 148
		.amdhsa_user_sgpr_count 2
		.amdhsa_user_sgpr_dispatch_ptr 0
		.amdhsa_user_sgpr_queue_ptr 0
		.amdhsa_user_sgpr_kernarg_segment_ptr 1
		.amdhsa_user_sgpr_dispatch_id 0
		.amdhsa_user_sgpr_kernarg_preload_length 0
		.amdhsa_user_sgpr_kernarg_preload_offset 0
		.amdhsa_user_sgpr_private_segment_size 0
		.amdhsa_uses_dynamic_stack 0
		.amdhsa_enable_private_segment 0
		.amdhsa_system_sgpr_workgroup_id_x 1
		.amdhsa_system_sgpr_workgroup_id_y 1
		.amdhsa_system_sgpr_workgroup_id_z 0
		.amdhsa_system_sgpr_workgroup_info 0
		.amdhsa_system_vgpr_workitem_id 0
		.amdhsa_next_free_vgpr 224
		.amdhsa_next_free_sgpr 96
		.amdhsa_accum_offset 224
		.amdhsa_reserve_vcc 1
		.amdhsa_float_round_mode_32 0
		.amdhsa_float_round_mode_16_64 0
		.amdhsa_float_denorm_mode_32 3
		.amdhsa_float_denorm_mode_16_64 3
		.amdhsa_dx10_clamp 1
		.amdhsa_ieee_mode 1
		.amdhsa_fp16_overflow 0
		.amdhsa_tg_split 0
		.amdhsa_exception_fp_ieee_invalid_op 0
		.amdhsa_exception_fp_denorm_src 0
		.amdhsa_exception_fp_ieee_div_zero 0
		.amdhsa_exception_fp_ieee_overflow 0
		.amdhsa_exception_fp_ieee_underflow 0
		.amdhsa_exception_fp_ieee_inexact 0
		.amdhsa_exception_int_div_zero 0
	.end_amdhsa_kernel

_Z7k_attn2ILi2EEv8AttnArgs:
	v_readfirstlane_b32 s3, v0
	s_lshl_b32 s12, s3, 1
	v_lshlrev_b32_e32 v3, 3, v0
	s_and_b32 s12, s12, 0x80
	v_and_b32_e32 v3, 0x78, v3
	s_load_dwordx4 s[8:11], s[0:1], 0x0
	s_load_dwordx2 s[4:5], s[0:1], 0x10
	s_load_dwordx2 s[6:7], s[0:1], 0x50
	v_or_b32_e32 v180, s12, v3
	s_lshl_b32 s12, s2, 5
	v_lshrrev_b32_e32 v1, 5, v0
	v_bfe_u32 v2, v0, 4, 2
	s_and_b32 s14, s12, 0xe0
	s_lshr_b32 s12, s2, 3
	v_lshrrev_b32_e32 v0, 6, v0
	v_and_b32_e32 v1, 4, v1
	s_add_i32 s14, s14, s12
	s_and_b32 s2, s2, 56
	v_and_b32_e32 v0, 4, v0
	v_and_or_b32 v181, s14, 56, v0
	v_or3_b32 v182, v2, s2, v1
	s_and_b32 s2, s14, 0x3ffffc0
	v_or_b32_e32 v4, s2, v181
	v_lshlrev_b32_e32 v0, 1, v180
	v_mov_b32_e32 v1, 0
	s_waitcnt lgkmcnt(0)
	v_lshl_add_u64 v[2:3], s[6:7], 0, v[0:1]
	v_lshl_or_b32 v0, v4, 6, v182
	v_lshlrev_b64 v[4:5], 9, v[0:1]
	v_lshl_add_u64 v[8:9], v[2:3], 0, v[4:5]
	v_or_b32_e32 v4, 64, v0
	v_mov_b32_e32 v5, v1
	v_lshlrev_b64 v[4:5], 9, v[4:5]
	v_lshlrev_b32_e32 v20, 2, v180
	v_lshl_add_u64 v[10:11], v[2:3], 0, v[4:5]
	global_load_dwordx4 v[22:25], v20, s[10:11] offset:16
	global_load_dwordx4 v[16:19], v20, s[10:11]
	global_load_dwordx4 v[26:29], v20, s[4:5] offset:16
	global_load_dwordx4 v[30:33], v20, s[4:5]
	global_load_dwordx4 v[12:15], v[8:9], off nt
	global_load_dwordx4 v[4:7], v[10:11], off nt
	v_or_b32_e32 v8, 0x80, v0
	v_mov_b32_e32 v9, v1
	v_lshlrev_b64 v[8:9], 9, v[8:9]
	v_or_b32_e32 v0, 0xc0, v0
	v_lshl_add_u64 v[20:21], v[2:3], 0, v[8:9]
	v_lshlrev_b64 v[0:1], 9, v[0:1]
	v_lshl_add_u64 v[34:35], v[2:3], 0, v[0:1]
	global_load_dwordx4 v[8:11], v[20:21], off nt
	global_load_dwordx4 v[0:3], v[34:35], off nt
	s_bitcmp1_b32 s3, 6
	s_cselect_b64 s[4:5], -1, 0
	s_and_b32 s2, s14, 0x3ffc0
	v_or_b32_e32 v20, s2, v181
	v_lshl_or_b32 v20, v20, 6, v182
	v_add_u32_e32 v184, -1, v182
	v_add_u32_e32 v185, -1, v181
	v_mul_u32_u24_e32 v20, 0x300, v20
	v_or_b32_e32 v34, v185, v184
	v_or_b32_e32 v20, v180, v20
	s_mov_b32 s11, 0x20000
	s_mov_b32 s10, 0x1800000
	s_and_b32 s9, s9, 0xffff
	v_lshlrev_b32_e32 v183, 1, v20
	v_cmp_gt_u32_e64 s[2:3], 64, v34
	s_and_b64 vcc, exec, s[4:5]
	s_waitcnt vmcnt(7)
	v_cvt_pk_f16_f32 v22, v22, v23
	s_waitcnt vmcnt(6)
	v_cvt_pk_f16_f32 v20, v16, v17
	v_cvt_pk_f16_f32 v21, v18, v19
	s_waitcnt vmcnt(4)
	v_cvt_pk_f16_f32 v16, v30, v31
	v_cvt_pk_f16_f32 v17, v32, v33
	v_cvt_pk_f16_f32 v18, v26, v27
	v_cvt_pk_f16_f32 v23, v24, v25
	v_cvt_pk_f16_f32 v19, v28, v29
	s_cbranch_vccz .LBB6_38
	v_cmp_lt_u32_e64 s[64:65], 0, v182
	v_cmp_gt_u32_e64 s[66:67], 63, v182
	v_cmp_lt_u32_e64 s[68:69], 0, v181
	v_cmp_gt_u32_e64 s[70:71], 60, v181
	buffer_load_dwordx4 v[190:193], v183, s[8:11], 0 offen
	v_add_u32_e32 v227, 0x18000, v183
	buffer_load_dwordx4 v[176:179], v227, s[8:11], 0 offen
	v_add_u32_e32 v226, 0x30000, v183
	buffer_load_dwordx4 v[172:175], v226, s[8:11], 0 offen
	v_add_u32_e32 v227, 0x48000, v183
	buffer_load_dwordx4 v[168:171], v227, s[8:11], 0 offen
	s_and_b64 s[72:73], s[68:69], s[64:65]
	s_and_b64 s[74:75], s[68:69], s[66:67]
	s_and_b64 s[76:77], s[70:71], s[64:65]
	s_and_b64 s[78:79], s[70:71], s[66:67]
	v_add_u32_e32 v226, 0xfffe7c00, v183
	v_add_u32_e32 v227, 0xfffe8000, v183
	v_mov_b32_e32 v136, v20
	v_mov_b32_e32 v137, v21
	v_mov_b32_e32 v138, v22
	v_mov_b32_e32 v139, v23
	v_mov_b32_e32 v96, v16
	v_mov_b32_e32 v97, v17
	v_mov_b32_e32 v98, v18
	v_mov_b32_e32 v99, v19
	v_mov_b32_e32 v152, v20
	v_mov_b32_e32 v153, v21
	v_mov_b32_e32 v154, v22
	v_mov_b32_e32 v155, v23
	v_mov_b32_e32 v124, v16
	v_mov_b32_e32 v125, v17
	v_mov_b32_e32 v126, v18
	v_mov_b32_e32 v127, v19
	v_mov_b32_e32 v160, v20
	v_mov_b32_e32 v161, v21
	v_mov_b32_e32 v162, v22
	v_mov_b32_e32 v163, v23
	v_mov_b32_e32 v140, v16
	v_mov_b32_e32 v141, v17
	v_mov_b32_e32 v142, v18
	v_mov_b32_e32 v143, v19
	s_mov_b64 exec, s[72:73]
	buffer_load_dwordx4 v[136:139], v226, s[8:11], 0 offen
	buffer_load_dwordx4 v[96:99], v226, s[8:11], 0 offen offset:512
	s_mov_b64 exec, -1
	s_mov_b64 exec, s[68:69]
	buffer_load_dwordx4 v[152:155], v227, s[8:11], 0 offen offset:512
	buffer_load_dwordx4 v[124:127], v227, s[8:11], 0 offen offset:1024
	s_mov_b64 exec, -1
	s_mov_b64 exec, s[74:75]
	buffer_load_dwordx4 v[160:163], v227, s[8:11], 0 offen offset:2048
	buffer_load_dwordx4 v[140:143], v227, s[8:11], 0 offen offset:2560
	s_mov_b64 exec, -1
	v_add_u32_e32 v226, 0xfffffc00, v183
	v_mov_b32_e32 v112, v20
	v_mov_b32_e32 v113, v21
	v_mov_b32_e32 v114, v22
	v_mov_b32_e32 v115, v23
	v_mov_b32_e32 v68, v16
	v_mov_b32_e32 v69, v17
	v_mov_b32_e32 v70, v18
	v_mov_b32_e32 v71, v19
	v_mov_b32_e32 v148, v20
	v_mov_b32_e32 v149, v21
	v_mov_b32_e32 v150, v22
	v_mov_b32_e32 v151, v23
	v_mov_b32_e32 v108, v16
	v_mov_b32_e32 v109, v17
	v_mov_b32_e32 v110, v18
	v_mov_b32_e32 v111, v19
	s_mov_b64 exec, s[64:65]
	buffer_load_dwordx4 v[112:115], v226, s[8:11], 0 offen
	buffer_load_dwordx4 v[68:71], v226, s[8:11], 0 offen offset:512
	s_mov_b64 exec, -1
	buffer_load_dwordx4 v[132:135], v183, s[8:11], 0 offen offset:512
	buffer_load_dwordx4 v[88:91], v183, s[8:11], 0 offen offset:1024
	s_mov_b64 exec, s[66:67]
	buffer_load_dwordx4 v[148:151], v183, s[8:11], 0 offen offset:2048
	buffer_load_dwordx4 v[108:111], v183, s[8:11], 0 offen offset:2560
	s_mov_b64 exec, -1
	v_add_u32_e32 v226, 0x17c00, v183
	v_add_u32_e32 v227, 0x18000, v183
	v_mov_b32_e32 v76, v20
	v_mov_b32_e32 v77, v21
	v_mov_b32_e32 v78, v22
	v_mov_b32_e32 v79, v23
	v_mov_b32_e32 v48, v16
	v_mov_b32_e32 v49, v17
	v_mov_b32_e32 v50, v18
	v_mov_b32_e32 v51, v19
	v_mov_b32_e32 v116, v20
	v_mov_b32_e32 v117, v21
	v_mov_b32_e32 v118, v22
	v_mov_b32_e32 v119, v23
	v_mov_b32_e32 v72, v16
	v_mov_b32_e32 v73, v17
	v_mov_b32_e32 v74, v18
	v_mov_b32_e32 v75, v19
	s_mov_b64 exec, s[64:65]
	buffer_load_dwordx4 v[76:79], v226, s[8:11], 0 offen
	buffer_load_dwordx4 v[48:51], v226, s[8:11], 0 offen offset:512
	s_mov_b64 exec, -1
	buffer_load_dwordx4 v[92:95], v227, s[8:11], 0 offen offset:512
	buffer_load_dwordx4 v[56:59], v227, s[8:11], 0 offen offset:1024
	s_mov_b64 exec, s[66:67]
	buffer_load_dwordx4 v[116:119], v227, s[8:11], 0 offen offset:2048
	buffer_load_dwordx4 v[72:75], v227, s[8:11], 0 offen offset:2560
	s_mov_b64 exec, -1
	v_add_u32_e32 v226, 0x2fc00, v183
	v_add_u32_e32 v227, 0x30000, v183
	v_mov_b32_e32 v44, v20
	v_mov_b32_e32 v45, v21
	v_mov_b32_e32 v46, v22
	v_mov_b32_e32 v47, v23
	v_mov_b32_e32 v32, v16
	v_mov_b32_e32 v33, v17
	v_mov_b32_e32 v34, v18
	v_mov_b32_e32 v35, v19
	v_mov_b32_e32 v80, v20
	v_mov_b32_e32 v81, v21
	v_mov_b32_e32 v82, v22
	v_mov_b32_e32 v83, v23
	v_mov_b32_e32 v40, v16
	v_mov_b32_e32 v41, v17
	v_mov_b32_e32 v42, v18
	v_mov_b32_e32 v43, v19
	s_mov_b64 exec, s[64:65]
	buffer_load_dwordx4 v[44:47], v226, s[8:11], 0 offen
	buffer_load_dwordx4 v[32:35], v226, s[8:11], 0 offen offset:512
	s_mov_b64 exec, -1
	buffer_load_dwordx4 v[60:63], v227, s[8:11], 0 offen offset:512
	buffer_load_dwordx4 v[36:39], v227, s[8:11], 0 offen offset:1024
	s_mov_b64 exec, s[66:67]
	buffer_load_dwordx4 v[80:83], v227, s[8:11], 0 offen offset:2048
	buffer_load_dwordx4 v[40:43], v227, s[8:11], 0 offen offset:2560
	s_mov_b64 exec, -1
	v_add_u32_e32 v226, 0x47c00, v183
	v_add_u32_e32 v227, 0x48000, v183
	v_mov_b32_e32 v100, v20
	v_mov_b32_e32 v101, v21
	v_mov_b32_e32 v102, v22
	v_mov_b32_e32 v103, v23
	v_mov_b32_e32 v52, v16
	v_mov_b32_e32 v53, v17
	v_mov_b32_e32 v54, v18
	v_mov_b32_e32 v55, v19
	v_mov_b32_e32 v144, v20
	v_mov_b32_e32 v145, v21
	v_mov_b32_e32 v146, v22
	v_mov_b32_e32 v147, v23
	v_mov_b32_e32 v84, v16
	v_mov_b32_e32 v85, v17
	v_mov_b32_e32 v86, v18
	v_mov_b32_e32 v87, v19
	s_mov_b64 exec, s[64:65]
	buffer_load_dwordx4 v[100:103], v226, s[8:11], 0 offen
	buffer_load_dwordx4 v[52:55], v226, s[8:11], 0 offen offset:512
	s_mov_b64 exec, -1
	buffer_load_dwordx4 v[128:131], v227, s[8:11], 0 offen offset:512
	buffer_load_dwordx4 v[64:67], v227, s[8:11], 0 offen offset:1024
	s_mov_b64 exec, s[66:67]
	buffer_load_dwordx4 v[144:147], v227, s[8:11], 0 offen offset:2048
	buffer_load_dwordx4 v[84:87], v227, s[8:11], 0 offen offset:2560
	s_mov_b64 exec, -1
	v_add_u32_e32 v226, 0x5fc00, v183
	v_add_u32_e32 v227, 0x60000, v183
	v_mov_b32_e32 v156, v20
	v_mov_b32_e32 v157, v21
	v_mov_b32_e32 v158, v22
	v_mov_b32_e32 v159, v23
	v_mov_b32_e32 v104, v16
	v_mov_b32_e32 v105, v17
	v_mov_b32_e32 v106, v18
	v_mov_b32_e32 v107, v19
	v_mov_b32_e32 v164, v20
	v_mov_b32_e32 v165, v21
	v_mov_b32_e32 v166, v22
	v_mov_b32_e32 v167, v23
	v_mov_b32_e32 v120, v16
	v_mov_b32_e32 v121, v17
	v_mov_b32_e32 v122, v18
	v_mov_b32_e32 v123, v19
	v_mov_b32_e32 v28, v20
	v_mov_b32_e32 v29, v21
	v_mov_b32_e32 v30, v22
	v_mov_b32_e32 v31, v23
	v_mov_b32_e32 v24, v16
	v_mov_b32_e32 v25, v17
	v_mov_b32_e32 v26, v18
	v_mov_b32_e32 v27, v19
	s_mov_b64 exec, s[76:77]
	buffer_load_dwordx4 v[156:159], v226, s[8:11], 0 offen
	buffer_load_dwordx4 v[104:107], v226, s[8:11], 0 offen offset:512
	s_mov_b64 exec, -1
	s_mov_b64 exec, s[70:71]
	buffer_load_dwordx4 v[164:167], v227, s[8:11], 0 offen offset:512
	buffer_load_dwordx4 v[120:123], v227, s[8:11], 0 offen offset:1024
	s_mov_b64 exec, -1
	s_mov_b64 exec, s[78:79]
	buffer_load_dwordx4 v[28:31], v227, s[8:11], 0 offen offset:2048
	buffer_load_dwordx4 v[24:27], v227, s[8:11], 0 offen offset:2560
	s_mov_b64 exec, -1
	s_load_dwordx2 s[12:13], s[0:1], 0x20
	s_waitcnt lgkmcnt(0)
	s_load_dwordx2 s[4:5], s[12:13], 0x0
	s_load_dword s12, s[12:13], 0x8
	s_waitcnt lgkmcnt(0)
	v_cvt_f16_f32_e32 v186, s5
	v_cvt_f16_f32_e32 v188, s4
	v_cvt_f16_f32_e32 v187, s12
	s_waitcnt vmcnt(18)
	v_pk_mul_f16 v196, v188, v193 op_sel_hi:[0,1]
	v_pk_mul_f16 v200, v186, v193 op_sel_hi:[0,1]
	v_pk_mul_f16 v204, v187, v193 op_sel_hi:[0,1]
	v_pk_mul_f16 v189, v188, v190 op_sel_hi:[0,1]
	v_pk_mul_f16 v194, v188, v191 op_sel_hi:[0,1]
	v_pk_mul_f16 v195, v188, v192 op_sel_hi:[0,1]
	v_pk_mul_f16 v197, v186, v190 op_sel_hi:[0,1]
	v_pk_mul_f16 v198, v186, v191 op_sel_hi:[0,1]
	v_pk_mul_f16 v199, v186, v192 op_sel_hi:[0,1]
	v_pk_mul_f16 v201, v187, v190 op_sel_hi:[0,1]
	v_pk_mul_f16 v202, v187, v191 op_sel_hi:[0,1]
	v_pk_mul_f16 v203, v187, v192 op_sel_hi:[0,1]
	v_pk_fma_f16 v139, v139, v193, v196
	v_pk_fma_f16 v155, v155, v193, v200
	v_pk_fma_f16 v163, v163, v193, v204
	v_pk_fma_f16 v205, v115, v193, v196
	v_pk_fma_f16 v209, v135, v193, v200
	v_pk_fma_f16 v213, v151, v193, v204
	v_pk_fma_f16 v196, v79, v193, v196
	v_pk_fma_f16 v200, v95, v193, v200
	v_pk_fma_f16 v193, v119, v193, v204
	v_pk_maximum3_f16 v204, v139, v155, v163
	v_pk_fma_f16 v138, v138, v192, v195
	v_pk_fma_f16 v137, v137, v191, v194
	v_pk_fma_f16 v136, v136, v190, v189
	v_pk_fma_f16 v154, v154, v192, v199
	v_pk_fma_f16 v153, v153, v191, v198
	v_pk_fma_f16 v152, v152, v190, v197
	v_pk_fma_f16 v162, v162, v192, v203
	v_pk_fma_f16 v161, v161, v191, v202
	v_pk_fma_f16 v160, v160, v190, v201
	v_pk_fma_f16 v206, v114, v192, v195
	v_pk_fma_f16 v207, v113, v191, v194
	v_pk_fma_f16 v208, v112, v190, v189
	v_pk_fma_f16 v210, v134, v192, v199
	v_pk_fma_f16 v211, v133, v191, v198
	v_pk_fma_f16 v212, v132, v190, v197
	v_pk_fma_f16 v214, v150, v192, v203
	v_pk_fma_f16 v215, v149, v191, v202
	v_pk_fma_f16 v216, v148, v190, v201
	v_pk_fma_f16 v195, v78, v192, v195
	v_pk_fma_f16 v194, v77, v191, v194
	v_pk_fma_f16 v189, v76, v190, v189
	v_pk_fma_f16 v199, v94, v192, v199
	v_pk_fma_f16 v198, v93, v191, v198
	v_pk_fma_f16 v197, v92, v190, v197
	v_pk_fma_f16 v192, v118, v192, v203
	v_pk_fma_f16 v191, v117, v191, v202
	v_pk_fma_f16 v190, v116, v190, v201
	v_pk_maximum3_f16 v201, v136, v152, v160
	v_pk_maximum3_f16 v202, v137, v153, v161
	v_pk_maximum3_f16 v203, v138, v154, v162
	v_pk_maximum3_f16 v220, v205, v209, v213
	v_pk_maximum3_f16 v224, v196, v200, v193
	v_pk_maximum3_f16 v217, v208, v212, v216
	v_pk_maximum3_f16 v218, v207, v211, v215
	v_pk_maximum3_f16 v219, v206, v210, v214
	s_nop 0
	v_pk_maximum3_f16 v221, v189, v197, v190
	v_pk_maximum3_f16 v222, v194, v198, v191
	v_pk_maximum3_f16 v204, v204, v220, v224
	v_pk_maximum3_f16 v223, v195, v199, v192
	s_nop 0
	v_pk_maximum3_f16 v201, v201, v217, v221
	v_pk_maximum3_f16 v202, v202, v218, v222
	v_pk_maximum3_f16 v203, v203, v219, v223
	v_xor_b32_e32 v204, 0x80008000, v204
	v_xor_b32_e32 v203, 0x80008000, v203
	v_xor_b32_e32 v202, 0x80008000, v202
	v_xor_b32_e32 v201, 0x80008000, v201
	v_pk_add_f16 v139, v139, v204
	v_pk_add_f16 v136, v136, v201
	v_pk_add_f16 v137, v137, v202
	v_pk_add_f16 v138, v138, v203
	v_pk_add_f16 v152, v152, v201
	v_exp_f16_sdwa v217, v136 dst_sel:WORD_0 dst_unused:UNUSED_PAD src0_sel:WORD_0
	v_exp_f16_sdwa v218, v137 dst_sel:WORD_0 dst_unused:UNUSED_PAD src0_sel:WORD_0
	v_exp_f16_sdwa v219, v138 dst_sel:WORD_0 dst_unused:UNUSED_PAD src0_sel:WORD_0
	v_exp_f16_sdwa v220, v139 dst_sel:WORD_0 dst_unused:UNUSED_PAD src0_sel:WORD_0
	v_exp_f16_sdwa v217, v136 dst_sel:WORD_1 dst_unused:UNUSED_PRESERVE src0_sel:WORD_1
	v_exp_f16_sdwa v218, v137 dst_sel:WORD_1 dst_unused:UNUSED_PRESERVE src0_sel:WORD_1
	v_exp_f16_sdwa v219, v138 dst_sel:WORD_1 dst_unused:UNUSED_PRESERVE src0_sel:WORD_1
	v_exp_f16_sdwa v220, v139 dst_sel:WORD_1 dst_unused:UNUSED_PRESERVE src0_sel:WORD_1
	s_nop 0
	v_pk_add_f16 v153, v153, v202
	v_pk_add_f16 v139, v217, 0
	v_pk_fma_f16 v99, v99, v220, 0
	v_pk_add_f16 v136, v220, 0
	v_pk_add_f16 v137, v219, 0
	v_pk_add_f16 v138, v218, 0
	v_pk_fma_f16 v98, v98, v219, 0
	v_pk_fma_f16 v97, v97, v218, 0
	v_pk_fma_f16 v96, v96, v217, 0
	v_pk_add_f16 v154, v154, v203
	v_pk_add_f16 v155, v155, v204
	s_nop 0
	v_exp_f16_sdwa v217, v152 dst_sel:WORD_0 dst_unused:UNUSED_PAD src0_sel:WORD_0
	v_exp_f16_sdwa v218, v153 dst_sel:WORD_0 dst_unused:UNUSED_PAD src0_sel:WORD_0
	v_exp_f16_sdwa v219, v154 dst_sel:WORD_0 dst_unused:UNUSED_PAD src0_sel:WORD_0
	v_exp_f16_sdwa v220, v155 dst_sel:WORD_0 dst_unused:UNUSED_PAD src0_sel:WORD_0
	v_exp_f16_sdwa v217, v152 dst_sel:WORD_1 dst_unused:UNUSED_PRESERVE src0_sel:WORD_1
	v_exp_f16_sdwa v218, v153 dst_sel:WORD_1 dst_unused:UNUSED_PRESERVE src0_sel:WORD_1
	v_exp_f16_sdwa v219, v154 dst_sel:WORD_1 dst_unused:UNUSED_PRESERVE src0_sel:WORD_1
	v_exp_f16_sdwa v220, v155 dst_sel:WORD_1 dst_unused:UNUSED_PRESERVE src0_sel:WORD_1
	s_nop 0
	s_nop 0
	v_pk_add_f16 v139, v139, v217
	v_pk_fma_f16 v99, v127, v220, v99
	v_pk_add_f16 v127, v163, v204
	v_pk_add_f16 v138, v138, v218
	v_pk_add_f16 v137, v137, v219
	v_pk_add_f16 v136, v136, v220
	v_pk_fma_f16 v96, v124, v217, v96
	v_pk_fma_f16 v97, v125, v218, v97
	v_pk_fma_f16 v98, v126, v219, v98
	v_pk_add_f16 v124, v160, v201
	v_pk_add_f16 v125, v161, v202
	v_pk_add_f16 v126, v162, v203
	s_nop 0
	v_exp_f16_sdwa v152, v124 dst_sel:WORD_0 dst_unused:UNUSED_PAD src0_sel:WORD_0
	v_exp_f16_sdwa v153, v125 dst_sel:WORD_0 dst_unused:UNUSED_PAD src0_sel:WORD_0
	v_exp_f16_sdwa v154, v126 dst_sel:WORD_0 dst_unused:UNUSED_PAD src0_sel:WORD_0
	v_exp_f16_sdwa v155, v127 dst_sel:WORD_0 dst_unused:UNUSED_PAD src0_sel:WORD_0
	v_exp_f16_sdwa v152, v124 dst_sel:WORD_1 dst_unused:UNUSED_PRESERVE src0_sel:WORD_1
	v_exp_f16_sdwa v153, v125 dst_sel:WORD_1 dst_unused:UNUSED_PRESERVE src0_sel:WORD_1
	v_exp_f16_sdwa v154, v126 dst_sel:WORD_1 dst_unused:UNUSED_PRESERVE src0_sel:WORD_1
	v_exp_f16_sdwa v155, v127 dst_sel:WORD_1 dst_unused:UNUSED_PRESERVE src0_sel:WORD_1
	s_nop 0
	s_nop 0
	v_pk_add_f16 v127, v139, v152
	v_pk_add_f16 v124, v136, v155
	v_pk_add_f16 v125, v137, v154
	v_pk_add_f16 v126, v138, v153
	v_pk_fma_f16 v99, v143, v155, v99
	v_pk_fma_f16 v98, v142, v154, v98
	v_pk_fma_f16 v97, v141, v153, v97
	v_pk_fma_f16 v96, v140, v152, v96
	v_pk_add_f16 v136, v208, v201
	v_pk_add_f16 v137, v207, v202
	v_pk_add_f16 v138, v206, v203
	v_pk_add_f16 v139, v205, v204
	s_nop 0
	v_exp_f16_sdwa v140, v136 dst_sel:WORD_0 dst_unused:UNUSED_PAD src0_sel:WORD_0
	v_exp_f16_sdwa v141, v137 dst_sel:WORD_0 dst_unused:UNUSED_PAD src0_sel:WORD_0
	v_exp_f16_sdwa v142, v138 dst_sel:WORD_0 dst_unused:UNUSED_PAD src0_sel:WORD_0
	v_exp_f16_sdwa v143, v139 dst_sel:WORD_0 dst_unused:UNUSED_PAD src0_sel:WORD_0
	v_exp_f16_sdwa v140, v136 dst_sel:WORD_1 dst_unused:UNUSED_PRESERVE src0_sel:WORD_1
	v_exp_f16_sdwa v141, v137 dst_sel:WORD_1 dst_unused:UNUSED_PRESERVE src0_sel:WORD_1
	v_exp_f16_sdwa v142, v138 dst_sel:WORD_1 dst_unused:UNUSED_PRESERVE src0_sel:WORD_1
	v_exp_f16_sdwa v143, v139 dst_sel:WORD_1 dst_unused:UNUSED_PRESERVE src0_sel:WORD_1
	s_nop 0
	v_pk_add_f16 v136, v212, v201
	v_pk_add_f16 v127, v127, v140
	v_pk_add_f16 v126, v126, v141
	v_pk_add_f16 v125, v125, v142
	v_pk_add_f16 v124, v124, v143
	v_pk_fma_f16 v96, v68, v140, v96
	v_pk_fma_f16 v97, v69, v141, v97
	v_pk_fma_f16 v98, v70, v142, v98
	v_pk_fma_f16 v99, v71, v143, v99
	v_pk_add_f16 v137, v211, v202
	v_pk_add_f16 v138, v210, v203
	v_pk_add_f16 v139, v209, v204
	s_nop 0
	v_exp_f16_sdwa v140, v136 dst_sel:WORD_0 dst_unused:UNUSED_PAD src0_sel:WORD_0
	v_exp_f16_sdwa v141, v137 dst_sel:WORD_0 dst_unused:UNUSED_PAD src0_sel:WORD_0
	v_exp_f16_sdwa v142, v138 dst_sel:WORD_0 dst_unused:UNUSED_PAD src0_sel:WORD_0
	v_exp_f16_sdwa v143, v139 dst_sel:WORD_0 dst_unused:UNUSED_PAD src0_sel:WORD_0
	v_exp_f16_sdwa v140, v136 dst_sel:WORD_1 dst_unused:UNUSED_PRESERVE src0_sel:WORD_1
	v_exp_f16_sdwa v141, v137 dst_sel:WORD_1 dst_unused:UNUSED_PRESERVE src0_sel:WORD_1
	v_exp_f16_sdwa v142, v138 dst_sel:WORD_1 dst_unused:UNUSED_PRESERVE src0_sel:WORD_1
	v_exp_f16_sdwa v143, v139 dst_sel:WORD_1 dst_unused:UNUSED_PRESERVE src0_sel:WORD_1
	s_nop 0
	v_pk_add_f16 v136, v216, v201
	v_pk_add_f16 v127, v127, v140
	v_pk_add_f16 v124, v124, v143
	v_pk_add_f16 v125, v125, v142
	v_pk_add_f16 v126, v126, v141
	v_pk_fma_f16 v99, v91, v143, v99
	v_pk_fma_f16 v98, v90, v142, v98
	v_pk_fma_f16 v97, v89, v141, v97
	v_pk_fma_f16 v96, v88, v140, v96
	v_pk_add_f16 v137, v215, v202
	v_pk_add_f16 v138, v214, v203
	v_pk_add_f16 v139, v213, v204
	s_nop 0
	v_exp_f16_sdwa v140, v136 dst_sel:WORD_0 dst_unused:UNUSED_PAD src0_sel:WORD_0
	v_exp_f16_sdwa v141, v137 dst_sel:WORD_0 dst_unused:UNUSED_PAD src0_sel:WORD_0
	v_exp_f16_sdwa v142, v138 dst_sel:WORD_0 dst_unused:UNUSED_PAD src0_sel:WORD_0
	v_exp_f16_sdwa v143, v139 dst_sel:WORD_0 dst_unused:UNUSED_PAD src0_sel:WORD_0
	v_exp_f16_sdwa v140, v136 dst_sel:WORD_1 dst_unused:UNUSED_PRESERVE src0_sel:WORD_1
	v_exp_f16_sdwa v141, v137 dst_sel:WORD_1 dst_unused:UNUSED_PRESERVE src0_sel:WORD_1
	v_exp_f16_sdwa v142, v138 dst_sel:WORD_1 dst_unused:UNUSED_PRESERVE src0_sel:WORD_1
	v_exp_f16_sdwa v143, v139 dst_sel:WORD_1 dst_unused:UNUSED_PRESERVE src0_sel:WORD_1
	s_nop 0
	v_pk_add_f16 v136, v189, v201
	v_pk_add_f16 v127, v127, v140
	v_pk_add_f16 v126, v126, v141
	v_pk_add_f16 v125, v125, v142
	v_pk_add_f16 v124, v124, v143
	v_pk_fma_f16 v96, v108, v140, v96
	v_pk_fma_f16 v97, v109, v141, v97
	v_pk_fma_f16 v98, v110, v142, v98
	v_pk_fma_f16 v99, v111, v143, v99
	v_pk_add_f16 v137, v194, v202
	v_pk_add_f16 v138, v195, v203
	v_pk_add_f16 v139, v196, v204
	s_nop 0
	v_exp_f16_sdwa v140, v136 dst_sel:WORD_0 dst_unused:UNUSED_PAD src0_sel:WORD_0
	v_exp_f16_sdwa v141, v137 dst_sel:WORD_0 dst_unused:UNUSED_PAD src0_sel:WORD_0
	v_exp_f16_sdwa v142, v138 dst_sel:WORD_0 dst_unused:UNUSED_PAD src0_sel:WORD_0
	v_exp_f16_sdwa v143, v139 dst_sel:WORD_0 dst_unused:UNUSED_PAD src0_sel:WORD_0
	v_exp_f16_sdwa v140, v136 dst_sel:WORD_1 dst_unused:UNUSED_PRESERVE src0_sel:WORD_1
	v_exp_f16_sdwa v141, v137 dst_sel:WORD_1 dst_unused:UNUSED_PRESERVE src0_sel:WORD_1
	v_exp_f16_sdwa v142, v138 dst_sel:WORD_1 dst_unused:UNUSED_PRESERVE src0_sel:WORD_1
	v_exp_f16_sdwa v143, v139 dst_sel:WORD_1 dst_unused:UNUSED_PRESERVE src0_sel:WORD_1
	s_nop 0
	v_pk_add_f16 v136, v197, v201
	v_pk_add_f16 v127, v127, v140
	v_pk_add_f16 v124, v124, v143
	v_pk_add_f16 v125, v125, v142
	v_pk_add_f16 v126, v126, v141
	v_pk_fma_f16 v99, v51, v143, v99
	v_pk_fma_f16 v98, v50, v142, v98
	v_pk_fma_f16 v97, v49, v141, v97
	v_pk_fma_f16 v96, v48, v140, v96
	v_pk_add_f16 v137, v198, v202
	v_pk_add_f16 v138, v199, v203
	v_pk_add_f16 v139, v200, v204
	s_nop 0
	v_exp_f16_sdwa v140, v136 dst_sel:WORD_0 dst_unused:UNUSED_PAD src0_sel:WORD_0
	v_exp_f16_sdwa v141, v137 dst_sel:WORD_0 dst_unused:UNUSED_PAD src0_sel:WORD_0
	v_exp_f16_sdwa v142, v138 dst_sel:WORD_0 dst_unused:UNUSED_PAD src0_sel:WORD_0
	v_exp_f16_sdwa v143, v139 dst_sel:WORD_0 dst_unused:UNUSED_PAD src0_sel:WORD_0
	v_exp_f16_sdwa v140, v136 dst_sel:WORD_1 dst_unused:UNUSED_PRESERVE src0_sel:WORD_1
	v_exp_f16_sdwa v141, v137 dst_sel:WORD_1 dst_unused:UNUSED_PRESERVE src0_sel:WORD_1
	v_exp_f16_sdwa v142, v138 dst_sel:WORD_1 dst_unused:UNUSED_PRESERVE src0_sel:WORD_1
	v_exp_f16_sdwa v143, v139 dst_sel:WORD_1 dst_unused:UNUSED_PRESERVE src0_sel:WORD_1
	s_nop 0
	v_pk_add_f16 v136, v190, v201
	v_pk_add_f16 v127, v127, v140
	v_pk_add_f16 v126, v126, v141
	v_pk_add_f16 v125, v125, v142
	v_pk_add_f16 v124, v124, v143
	v_pk_fma_f16 v96, v56, v140, v96
	v_pk_fma_f16 v97, v57, v141, v97
	v_pk_fma_f16 v98, v58, v142, v98
	v_pk_fma_f16 v99, v59, v143, v99
	v_pk_add_f16 v137, v191, v202
	v_pk_add_f16 v138, v192, v203
	v_pk_add_f16 v139, v193, v204
	s_nop 0
	v_exp_f16_sdwa v140, v136 dst_sel:WORD_0 dst_unused:UNUSED_PAD src0_sel:WORD_0
	v_exp_f16_sdwa v141, v137 dst_sel:WORD_0 dst_unused:UNUSED_PAD src0_sel:WORD_0
	v_exp_f16_sdwa v142, v138 dst_sel:WORD_0 dst_unused:UNUSED_PAD src0_sel:WORD_0
	v_exp_f16_sdwa v143, v139 dst_sel:WORD_0 dst_unused:UNUSED_PAD src0_sel:WORD_0
	v_exp_f16_sdwa v140, v136 dst_sel:WORD_1 dst_unused:UNUSED_PRESERVE src0_sel:WORD_1
	v_exp_f16_sdwa v141, v137 dst_sel:WORD_1 dst_unused:UNUSED_PRESERVE src0_sel:WORD_1
	v_exp_f16_sdwa v142, v138 dst_sel:WORD_1 dst_unused:UNUSED_PRESERVE src0_sel:WORD_1
	v_exp_f16_sdwa v143, v139 dst_sel:WORD_1 dst_unused:UNUSED_PRESERVE src0_sel:WORD_1
	s_nop 0
	s_nop 0
	v_pk_add_f16 v127, v127, v140
	v_pk_add_f16 v126, v126, v141
	v_rcp_f16_e32 v136, v127
	v_rcp_f16_sdwa v127, v127 dst_sel:DWORD dst_unused:UNUSED_PAD src0_sel:WORD_1
	v_pk_add_f16 v125, v125, v142
	v_rcp_f16_e32 v137, v126
	v_rcp_f16_sdwa v126, v126 dst_sel:DWORD dst_unused:UNUSED_PAD src0_sel:WORD_1
	v_pk_add_f16 v124, v124, v143
	v_rcp_f16_e32 v138, v125
	v_rcp_f16_sdwa v139, v125 dst_sel:DWORD dst_unused:UNUSED_PAD src0_sel:WORD_1
	v_pk_fma_f16 v97, v73, v141, v97
	v_pk_fma_f16 v96, v72, v140, v96
	v_rcp_f16_e32 v140, v124
	v_rcp_f16_sdwa v141, v124 dst_sel:DWORD dst_unused:UNUSED_PAD src0_sel:WORD_1
	v_pack_b32_f16 v124, v136, v127
	v_pk_mul_f16 v124, v96, v124
	v_pack_b32_f16 v96, v137, v126
	v_pk_fma_f16 v98, v74, v142, v98
	v_pk_mul_f16 v125, v97, v96
	v_pack_b32_f16 v96, v138, v139
	v_pk_fma_f16 v99, v75, v143, v99
	v_pk_mul_f16 v126, v98, v96
	v_pack_b32_f16 v96, v140, v141
	v_pk_mul_f16 v127, v99, v96
	s_waitcnt vmcnt(12)
	v_pk_mul_f16 v99, v188, v179 op_sel_hi:[0,1]
	v_pk_mul_f16 v139, v186, v179 op_sel_hi:[0,1]
	v_pk_mul_f16 v143, v187, v179 op_sel_hi:[0,1]
	v_pk_mul_f16 v96, v188, v176 op_sel_hi:[0,1]
	v_pk_mul_f16 v97, v188, v177 op_sel_hi:[0,1]
	v_pk_mul_f16 v98, v188, v178 op_sel_hi:[0,1]
	v_pk_mul_f16 v136, v186, v176 op_sel_hi:[0,1]
	v_pk_mul_f16 v137, v186, v177 op_sel_hi:[0,1]
	v_pk_mul_f16 v138, v186, v178 op_sel_hi:[0,1]
	v_pk_mul_f16 v140, v187, v176 op_sel_hi:[0,1]
	v_pk_mul_f16 v141, v187, v177 op_sel_hi:[0,1]
	v_pk_mul_f16 v142, v187, v178 op_sel_hi:[0,1]
	v_pk_fma_f16 v115, v115, v179, v99
	v_pk_fma_f16 v135, v135, v179, v139
	v_pk_fma_f16 v151, v151, v179, v143
	v_pk_fma_f16 v152, v79, v179, v99
	v_pk_fma_f16 v160, v95, v179, v139
	v_pk_fma_f16 v189, v119, v179, v143
	v_pk_fma_f16 v99, v47, v179, v99
	v_pk_fma_f16 v139, v63, v179, v139
	v_pk_fma_f16 v143, v83, v179, v143
	v_pk_maximum3_f16 v179, v115, v135, v151
	v_pk_fma_f16 v114, v114, v178, v98
	v_pk_fma_f16 v113, v113, v177, v97
	v_pk_fma_f16 v112, v112, v176, v96
	v_pk_fma_f16 v134, v134, v178, v138
	v_pk_fma_f16 v133, v133, v177, v137
	v_pk_fma_f16 v132, v132, v176, v136
	v_pk_fma_f16 v150, v150, v178, v142
	v_pk_fma_f16 v149, v149, v177, v141
	v_pk_fma_f16 v148, v148, v176, v140
	v_pk_fma_f16 v153, v78, v178, v98
	v_pk_fma_f16 v154, v77, v177, v97
	v_pk_fma_f16 v155, v76, v176, v96
	v_pk_fma_f16 v161, v94, v178, v138
	v_pk_fma_f16 v162, v93, v177, v137
	v_pk_fma_f16 v163, v92, v176, v136
	v_pk_fma_f16 v190, v118, v178, v142
	v_pk_fma_f16 v191, v117, v177, v141
	v_pk_fma_f16 v192, v116, v176, v140
	v_pk_fma_f16 v98, v46, v178, v98
	v_pk_fma_f16 v97, v45, v177, v97
	v_pk_fma_f16 v96, v44, v176, v96
	v_pk_fma_f16 v138, v62, v178, v138
	v_pk_fma_f16 v137, v61, v177, v137
	v_pk_fma_f16 v136, v60, v176, v136
	v_pk_fma_f16 v142, v82, v178, v142
	v_pk_fma_f16 v141, v81, v177, v141
	v_pk_fma_f16 v140, v80, v176, v140
	v_pk_maximum3_f16 v176, v112, v132, v148
	v_pk_maximum3_f16 v177, v113, v133, v149
	v_pk_maximum3_f16 v178, v114, v134, v150
	v_pk_maximum3_f16 v196, v152, v160, v189
	v_pk_maximum3_f16 v200, v99, v139, v143
	v_pk_maximum3_f16 v193, v155, v163, v192
	v_pk_maximum3_f16 v194, v154, v162, v191
	v_pk_maximum3_f16 v195, v153, v161, v190
	s_nop 0
	v_pk_maximum3_f16 v197, v96, v136, v140
	v_pk_maximum3_f16 v198, v97, v137, v141
	v_pk_maximum3_f16 v179, v179, v196, v200
	v_pk_maximum3_f16 v199, v98, v138, v142
	s_nop 0
	v_pk_maximum3_f16 v176, v176, v193, v197
	v_pk_maximum3_f16 v177, v177, v194, v198
	v_pk_maximum3_f16 v178, v178, v195, v199
	v_xor_b32_e32 v179, 0x80008000, v179
	v_xor_b32_e32 v178, 0x80008000, v178
	v_xor_b32_e32 v177, 0x80008000, v177
	v_xor_b32_e32 v176, 0x80008000, v176
	v_pk_add_f16 v115, v115, v179
	v_pk_add_f16 v112, v112, v176
	v_pk_add_f16 v113, v113, v177
	v_pk_add_f16 v114, v114, v178
	v_pk_add_f16 v132, v132, v176
	v_exp_f16_sdwa v193, v112 dst_sel:WORD_0 dst_unused:UNUSED_PAD src0_sel:WORD_0
	v_exp_f16_sdwa v194, v113 dst_sel:WORD_0 dst_unused:UNUSED_PAD src0_sel:WORD_0
	v_exp_f16_sdwa v195, v114 dst_sel:WORD_0 dst_unused:UNUSED_PAD src0_sel:WORD_0
	v_exp_f16_sdwa v196, v115 dst_sel:WORD_0 dst_unused:UNUSED_PAD src0_sel:WORD_0
	v_exp_f16_sdwa v193, v112 dst_sel:WORD_1 dst_unused:UNUSED_PRESERVE src0_sel:WORD_1
	v_exp_f16_sdwa v194, v113 dst_sel:WORD_1 dst_unused:UNUSED_PRESERVE src0_sel:WORD_1
	v_exp_f16_sdwa v195, v114 dst_sel:WORD_1 dst_unused:UNUSED_PRESERVE src0_sel:WORD_1
	v_exp_f16_sdwa v196, v115 dst_sel:WORD_1 dst_unused:UNUSED_PRESERVE src0_sel:WORD_1
	s_nop 0
	v_pk_add_f16 v133, v133, v177
	v_pk_add_f16 v115, v193, 0
	v_pk_fma_f16 v71, v71, v196, 0
	v_pk_add_f16 v112, v196, 0
	v_pk_add_f16 v113, v195, 0
	v_pk_add_f16 v114, v194, 0
	v_pk_fma_f16 v70, v70, v195, 0
	v_pk_fma_f16 v69, v69, v194, 0
	v_pk_fma_f16 v68, v68, v193, 0
	v_pk_add_f16 v134, v134, v178
	v_pk_add_f16 v135, v135, v179
	v_pk_add_f16 v96, v96, v176
	v_exp_f16_sdwa v193, v132 dst_sel:WORD_0 dst_unused:UNUSED_PAD src0_sel:WORD_0
	v_exp_f16_sdwa v194, v133 dst_sel:WORD_0 dst_unused:UNUSED_PAD src0_sel:WORD_0
	v_exp_f16_sdwa v195, v134 dst_sel:WORD_0 dst_unused:UNUSED_PAD src0_sel:WORD_0
	v_exp_f16_sdwa v196, v135 dst_sel:WORD_0 dst_unused:UNUSED_PAD src0_sel:WORD_0
	v_exp_f16_sdwa v193, v132 dst_sel:WORD_1 dst_unused:UNUSED_PRESERVE src0_sel:WORD_1
	v_exp_f16_sdwa v194, v133 dst_sel:WORD_1 dst_unused:UNUSED_PRESERVE src0_sel:WORD_1
	v_exp_f16_sdwa v195, v134 dst_sel:WORD_1 dst_unused:UNUSED_PRESERVE src0_sel:WORD_1
	v_exp_f16_sdwa v196, v135 dst_sel:WORD_1 dst_unused:UNUSED_PRESERVE src0_sel:WORD_1
	s_nop 0
	v_pk_add_f16 v97, v97, v177
	v_pk_add_f16 v115, v115, v193
	v_pk_fma_f16 v71, v91, v196, v71
	v_pk_add_f16 v91, v151, v179
	v_pk_add_f16 v114, v114, v194
	v_pk_add_f16 v113, v113, v195
	v_pk_add_f16 v112, v112, v196
	v_pk_fma_f16 v68, v88, v193, v68
	v_pk_fma_f16 v69, v89, v194, v69
	v_pk_fma_f16 v70, v90, v195, v70
	v_pk_add_f16 v88, v148, v176
	v_pk_add_f16 v89, v149, v177
	v_pk_add_f16 v90, v150, v178
	v_pk_add_f16 v98, v98, v178
	v_exp_f16_sdwa v132, v88 dst_sel:WORD_0 dst_unused:UNUSED_PAD src0_sel:WORD_0
	v_exp_f16_sdwa v133, v89 dst_sel:WORD_0 dst_unused:UNUSED_PAD src0_sel:WORD_0
	v_exp_f16_sdwa v134, v90 dst_sel:WORD_0 dst_unused:UNUSED_PAD src0_sel:WORD_0
	v_exp_f16_sdwa v135, v91 dst_sel:WORD_0 dst_unused:UNUSED_PAD src0_sel:WORD_0
	v_exp_f16_sdwa v132, v88 dst_sel:WORD_1 dst_unused:UNUSED_PRESERVE src0_sel:WORD_1
	v_exp_f16_sdwa v133, v89 dst_sel:WORD_1 dst_unused:UNUSED_PRESERVE src0_sel:WORD_1
	v_exp_f16_sdwa v134, v90 dst_sel:WORD_1 dst_unused:UNUSED_PRESERVE src0_sel:WORD_1
	v_exp_f16_sdwa v135, v91 dst_sel:WORD_1 dst_unused:UNUSED_PRESERVE src0_sel:WORD_1
	s_nop 0
	v_pk_add_f16 v99, v99, v179
	v_pk_add_f16 v91, v115, v132
	v_pk_add_f16 v88, v112, v135
	v_pk_add_f16 v89, v113, v134
	v_pk_add_f16 v90, v114, v133
	v_pk_fma_f16 v71, v111, v135, v71
	v_pk_fma_f16 v70, v110, v134, v70
	v_pk_fma_f16 v69, v109, v133, v69
	v_pk_fma_f16 v68, v108, v132, v68
	v_pk_add_f16 v108, v155, v176
	v_pk_add_f16 v109, v154, v177
	v_pk_add_f16 v110, v153, v178
	v_pk_add_f16 v111, v152, v179
	s_nop 0
	v_exp_f16_sdwa v112, v108 dst_sel:WORD_0 dst_unused:UNUSED_PAD src0_sel:WORD_0
	v_exp_f16_sdwa v113, v109 dst_sel:WORD_0 dst_unused:UNUSED_PAD src0_sel:WORD_0
	v_exp_f16_sdwa v114, v110 dst_sel:WORD_0 dst_unused:UNUSED_PAD src0_sel:WORD_0
	v_exp_f16_sdwa v115, v111 dst_sel:WORD_0 dst_unused:UNUSED_PAD src0_sel:WORD_0
	v_exp_f16_sdwa v112, v108 dst_sel:WORD_1 dst_unused:UNUSED_PRESERVE src0_sel:WORD_1
	v_exp_f16_sdwa v113, v109 dst_sel:WORD_1 dst_unused:UNUSED_PRESERVE src0_sel:WORD_1
	v_exp_f16_sdwa v114, v110 dst_sel:WORD_1 dst_unused:UNUSED_PRESERVE src0_sel:WORD_1
	v_exp_f16_sdwa v115, v111 dst_sel:WORD_1 dst_unused:UNUSED_PRESERVE src0_sel:WORD_1
	s_nop 0
	v_pk_add_f16 v108, v163, v176
	v_pk_add_f16 v91, v91, v112
	v_pk_add_f16 v90, v90, v113
	v_pk_add_f16 v89, v89, v114
	v_pk_add_f16 v88, v88, v115
	v_pk_fma_f16 v68, v48, v112, v68
	v_pk_fma_f16 v69, v49, v113, v69
	v_pk_fma_f16 v70, v50, v114, v70
	v_pk_fma_f16 v71, v51, v115, v71
	v_pk_add_f16 v109, v162, v177
	v_pk_add_f16 v110, v161, v178
	v_pk_add_f16 v111, v160, v179
	s_nop 0
	v_exp_f16_sdwa v112, v108 dst_sel:WORD_0 dst_unused:UNUSED_PAD src0_sel:WORD_0
	v_exp_f16_sdwa v113, v109 dst_sel:WORD_0 dst_unused:UNUSED_PAD src0_sel:WORD_0
	v_exp_f16_sdwa v114, v110 dst_sel:WORD_0 dst_unused:UNUSED_PAD src0_sel:WORD_0
	v_exp_f16_sdwa v115, v111 dst_sel:WORD_0 dst_unused:UNUSED_PAD src0_sel:WORD_0
	v_exp_f16_sdwa v112, v108 dst_sel:WORD_1 dst_unused:UNUSED_PRESERVE src0_sel:WORD_1
	v_exp_f16_sdwa v113, v109 dst_sel:WORD_1 dst_unused:UNUSED_PRESERVE src0_sel:WORD_1
	v_exp_f16_sdwa v114, v110 dst_sel:WORD_1 dst_unused:UNUSED_PRESERVE src0_sel:WORD_1
	v_exp_f16_sdwa v115, v111 dst_sel:WORD_1 dst_unused:UNUSED_PRESERVE src0_sel:WORD_1
	s_nop 0
	v_pk_add_f16 v108, v192, v176
	v_pk_add_f16 v91, v91, v112
	v_pk_add_f16 v88, v88, v115
	v_pk_add_f16 v89, v89, v114
	v_pk_add_f16 v90, v90, v113
	v_pk_fma_f16 v71, v59, v115, v71
	v_pk_fma_f16 v70, v58, v114, v70
	v_pk_fma_f16 v69, v57, v113, v69
	v_pk_fma_f16 v68, v56, v112, v68
	v_pk_add_f16 v109, v191, v177
	v_pk_add_f16 v110, v190, v178
	v_pk_add_f16 v111, v189, v179
	s_nop 0
	v_exp_f16_sdwa v112, v108 dst_sel:WORD_0 dst_unused:UNUSED_PAD src0_sel:WORD_0
	v_exp_f16_sdwa v113, v109 dst_sel:WORD_0 dst_unused:UNUSED_PAD src0_sel:WORD_0
	v_exp_f16_sdwa v114, v110 dst_sel:WORD_0 dst_unused:UNUSED_PAD src0_sel:WORD_0
	v_exp_f16_sdwa v115, v111 dst_sel:WORD_0 dst_unused:UNUSED_PAD src0_sel:WORD_0
	v_exp_f16_sdwa v112, v108 dst_sel:WORD_1 dst_unused:UNUSED_PRESERVE src0_sel:WORD_1
	v_exp_f16_sdwa v113, v109 dst_sel:WORD_1 dst_unused:UNUSED_PRESERVE src0_sel:WORD_1
	v_exp_f16_sdwa v114, v110 dst_sel:WORD_1 dst_unused:UNUSED_PRESERVE src0_sel:WORD_1
	v_exp_f16_sdwa v115, v111 dst_sel:WORD_1 dst_unused:UNUSED_PRESERVE src0_sel:WORD_1
	s_nop 0
	v_exp_f16_sdwa v108, v96 dst_sel:WORD_0 dst_unused:UNUSED_PAD src0_sel:WORD_0
	v_exp_f16_sdwa v109, v97 dst_sel:WORD_0 dst_unused:UNUSED_PAD src0_sel:WORD_0
	v_exp_f16_sdwa v110, v98 dst_sel:WORD_0 dst_unused:UNUSED_PAD src0_sel:WORD_0
	v_exp_f16_sdwa v111, v99 dst_sel:WORD_0 dst_unused:UNUSED_PAD src0_sel:WORD_0
	v_exp_f16_sdwa v108, v96 dst_sel:WORD_1 dst_unused:UNUSED_PRESERVE src0_sel:WORD_1
	v_exp_f16_sdwa v109, v97 dst_sel:WORD_1 dst_unused:UNUSED_PRESERVE src0_sel:WORD_1
	v_exp_f16_sdwa v110, v98 dst_sel:WORD_1 dst_unused:UNUSED_PRESERVE src0_sel:WORD_1
	v_exp_f16_sdwa v111, v99 dst_sel:WORD_1 dst_unused:UNUSED_PRESERVE src0_sel:WORD_1
	s_nop 0
	v_pk_add_f16 v96, v136, v176
	v_pk_add_f16 v91, v91, v112
	v_pk_add_f16 v90, v90, v113
	v_pk_add_f16 v89, v89, v114
	v_pk_add_f16 v88, v88, v115
	v_pk_fma_f16 v68, v72, v112, v68
	v_pk_fma_f16 v69, v73, v113, v69
	v_pk_fma_f16 v70, v74, v114, v70
	v_pk_fma_f16 v71, v75, v115, v71
	v_pk_add_f16 v91, v91, v108
	v_pk_add_f16 v88, v88, v111
	v_pk_add_f16 v89, v89, v110
	v_pk_add_f16 v90, v90, v109
	v_pk_fma_f16 v71, v35, v111, v71
	v_pk_fma_f16 v70, v34, v110, v70
	v_pk_fma_f16 v69, v33, v109, v69
	v_pk_fma_f16 v68, v32, v108, v68
	v_pk_add_f16 v97, v137, v177
	v_pk_add_f16 v98, v138, v178
	v_pk_add_f16 v99, v139, v179
	s_nop 0
	v_exp_f16_sdwa v108, v96 dst_sel:WORD_0 dst_unused:UNUSED_PAD src0_sel:WORD_0
	v_exp_f16_sdwa v109, v97 dst_sel:WORD_0 dst_unused:UNUSED_PAD src0_sel:WORD_0
	v_exp_f16_sdwa v110, v98 dst_sel:WORD_0 dst_unused:UNUSED_PAD src0_sel:WORD_0
	v_exp_f16_sdwa v111, v99 dst_sel:WORD_0 dst_unused:UNUSED_PAD src0_sel:WORD_0
	v_exp_f16_sdwa v108, v96 dst_sel:WORD_1 dst_unused:UNUSED_PRESERVE src0_sel:WORD_1
	v_exp_f16_sdwa v109, v97 dst_sel:WORD_1 dst_unused:UNUSED_PRESERVE src0_sel:WORD_1
	v_exp_f16_sdwa v110, v98 dst_sel:WORD_1 dst_unused:UNUSED_PRESERVE src0_sel:WORD_1
	v_exp_f16_sdwa v111, v99 dst_sel:WORD_1 dst_unused:UNUSED_PRESERVE src0_sel:WORD_1
	s_nop 0
	v_pk_add_f16 v96, v140, v176
	v_pk_add_f16 v91, v91, v108
	v_pk_add_f16 v90, v90, v109
	v_pk_add_f16 v89, v89, v110
	v_pk_add_f16 v88, v88, v111
	v_pk_fma_f16 v68, v36, v108, v68
	v_pk_fma_f16 v69, v37, v109, v69
	v_pk_fma_f16 v70, v38, v110, v70
	v_pk_fma_f16 v71, v39, v111, v71
	v_pk_add_f16 v97, v141, v177
	v_pk_add_f16 v98, v142, v178
	v_pk_add_f16 v99, v143, v179
	s_nop 0
	v_exp_f16_sdwa v108, v96 dst_sel:WORD_0 dst_unused:UNUSED_PAD src0_sel:WORD_0
	v_exp_f16_sdwa v109, v97 dst_sel:WORD_0 dst_unused:UNUSED_PAD src0_sel:WORD_0
	v_exp_f16_sdwa v110, v98 dst_sel:WORD_0 dst_unused:UNUSED_PAD src0_sel:WORD_0
	v_exp_f16_sdwa v111, v99 dst_sel:WORD_0 dst_unused:UNUSED_PAD src0_sel:WORD_0
	v_exp_f16_sdwa v108, v96 dst_sel:WORD_1 dst_unused:UNUSED_PRESERVE src0_sel:WORD_1
	v_exp_f16_sdwa v109, v97 dst_sel:WORD_1 dst_unused:UNUSED_PRESERVE src0_sel:WORD_1
	v_exp_f16_sdwa v110, v98 dst_sel:WORD_1 dst_unused:UNUSED_PRESERVE src0_sel:WORD_1
	v_exp_f16_sdwa v111, v99 dst_sel:WORD_1 dst_unused:UNUSED_PRESERVE src0_sel:WORD_1
	s_nop 0
	s_nop 0
	v_pk_add_f16 v91, v91, v108
	v_pk_add_f16 v90, v90, v109
	v_rcp_f16_e32 v96, v91
	v_rcp_f16_sdwa v91, v91 dst_sel:DWORD dst_unused:UNUSED_PAD src0_sel:WORD_1
	v_pk_add_f16 v89, v89, v110
	v_rcp_f16_e32 v97, v90
	v_rcp_f16_sdwa v90, v90 dst_sel:DWORD dst_unused:UNUSED_PAD src0_sel:WORD_1
	v_pk_add_f16 v88, v88, v111
	v_rcp_f16_e32 v98, v89
	v_rcp_f16_sdwa v99, v89 dst_sel:DWORD dst_unused:UNUSED_PAD src0_sel:WORD_1
	v_pk_fma_f16 v69, v41, v109, v69
	v_pk_fma_f16 v68, v40, v108, v68
	v_rcp_f16_e32 v108, v88
	v_rcp_f16_sdwa v109, v88 dst_sel:DWORD dst_unused:UNUSED_PAD src0_sel:WORD_1
	v_pack_b32_f16 v88, v96, v91
	v_pk_mul_f16 v88, v68, v88
	v_pack_b32_f16 v68, v97, v90
	v_pk_fma_f16 v70, v42, v110, v70
	v_pk_mul_f16 v89, v69, v68
	v_pack_b32_f16 v68, v98, v99
	v_pk_fma_f16 v71, v43, v111, v71
	v_pk_mul_f16 v90, v70, v68
	v_pack_b32_f16 v68, v108, v109
	v_pk_mul_f16 v91, v71, v68
	s_waitcnt vmcnt(6)
	v_pk_mul_f16 v68, v188, v172 op_sel_hi:[0,1]
	v_pk_mul_f16 v96, v186, v172 op_sel_hi:[0,1]
	v_pk_mul_f16 v108, v187, v172 op_sel_hi:[0,1]
	v_pk_mul_f16 v69, v188, v173 op_sel_hi:[0,1]
	v_pk_mul_f16 v70, v188, v174 op_sel_hi:[0,1]
	v_pk_mul_f16 v71, v188, v175 op_sel_hi:[0,1]
	v_pk_mul_f16 v97, v186, v173 op_sel_hi:[0,1]
	v_pk_mul_f16 v98, v186, v174 op_sel_hi:[0,1]
	v_pk_mul_f16 v99, v186, v175 op_sel_hi:[0,1]
	v_pk_mul_f16 v109, v187, v173 op_sel_hi:[0,1]
	v_pk_mul_f16 v110, v187, v174 op_sel_hi:[0,1]
	v_pk_mul_f16 v111, v187, v175 op_sel_hi:[0,1]
	v_pk_fma_f16 v76, v76, v172, v68
	v_pk_fma_f16 v92, v92, v172, v96
	v_pk_fma_f16 v115, v116, v172, v108
	v_pk_fma_f16 v79, v79, v175, v71
	v_pk_maximum3_f16 v140, v76, v92, v115
	v_pk_fma_f16 v78, v78, v174, v70
	v_pk_fma_f16 v77, v77, v173, v69
	v_pk_fma_f16 v95, v95, v175, v99
	v_pk_fma_f16 v94, v94, v174, v98
	v_pk_fma_f16 v93, v93, v173, v97
	v_pk_fma_f16 v112, v119, v175, v111
	v_pk_fma_f16 v113, v118, v174, v110
	v_pk_fma_f16 v114, v117, v173, v109
	v_pk_fma_f16 v119, v44, v172, v68
	v_pk_fma_f16 v135, v60, v172, v96
	v_pk_fma_f16 v139, v80, v172, v108
	v_pk_fma_f16 v68, v100, v172, v68
	v_pk_fma_f16 v96, v128, v172, v96
	v_pk_fma_f16 v108, v144, v172, v108
	v_pk_maximum3_f16 v141, v77, v93, v114
	v_pk_maximum3_f16 v142, v78, v94, v113
	v_pk_maximum3_f16 v143, v79, v95, v112
	v_pk_maximum3_f16 v148, v119, v135, v139
	v_pk_fma_f16 v116, v47, v175, v71
	v_pk_maximum3_f16 v152, v68, v96, v108
	v_pk_fma_f16 v117, v46, v174, v70
	v_pk_maximum3_f16 v140, v140, v148, v152
	v_pk_fma_f16 v118, v45, v173, v69
	v_pk_fma_f16 v132, v63, v175, v99
	v_pk_fma_f16 v133, v62, v174, v98
	v_pk_fma_f16 v134, v61, v173, v97
	v_pk_fma_f16 v136, v83, v175, v111
	v_pk_fma_f16 v137, v82, v174, v110
	v_pk_fma_f16 v138, v81, v173, v109
	v_pk_fma_f16 v71, v103, v175, v71
	v_pk_fma_f16 v70, v102, v174, v70
	v_pk_fma_f16 v69, v101, v173, v69
	v_pk_fma_f16 v99, v131, v175, v99
	v_pk_fma_f16 v98, v130, v174, v98
	v_pk_fma_f16 v97, v129, v173, v97
	v_pk_fma_f16 v111, v147, v175, v111
	v_pk_fma_f16 v110, v146, v174, v110
	v_pk_fma_f16 v109, v145, v173, v109
	v_pk_maximum3_f16 v149, v118, v134, v138
	v_pk_maximum3_f16 v150, v117, v133, v137
	v_pk_maximum3_f16 v151, v116, v132, v136
	v_pk_maximum3_f16 v154, v70, v98, v110
	v_pk_maximum3_f16 v155, v71, v99, v111
	s_nop 0
	v_pk_maximum3_f16 v153, v69, v97, v109
	v_xor_b32_e32 v140, 0x80008000, v140
	v_pk_maximum3_f16 v141, v141, v149, v153
	v_pk_maximum3_f16 v142, v142, v150, v154
	v_pk_maximum3_f16 v143, v143, v151, v155
	v_pk_add_f16 v76, v76, v140
	v_xor_b32_e32 v143, 0x80008000, v143
	v_xor_b32_e32 v142, 0x80008000, v142
	v_xor_b32_e32 v141, 0x80008000, v141
	v_pk_add_f16 v77, v77, v141
	v_pk_add_f16 v78, v78, v142
	v_pk_add_f16 v79, v79, v143
	v_pk_add_f16 v92, v92, v140
	v_exp_f16_sdwa v148, v76 dst_sel:WORD_0 dst_unused:UNUSED_PAD src0_sel:WORD_0
	v_exp_f16_sdwa v149, v77 dst_sel:WORD_0 dst_unused:UNUSED_PAD src0_sel:WORD_0
	v_exp_f16_sdwa v150, v78 dst_sel:WORD_0 dst_unused:UNUSED_PAD src0_sel:WORD_0
	v_exp_f16_sdwa v151, v79 dst_sel:WORD_0 dst_unused:UNUSED_PAD src0_sel:WORD_0
	v_exp_f16_sdwa v148, v76 dst_sel:WORD_1 dst_unused:UNUSED_PRESERVE src0_sel:WORD_1
	v_exp_f16_sdwa v149, v77 dst_sel:WORD_1 dst_unused:UNUSED_PRESERVE src0_sel:WORD_1
	v_exp_f16_sdwa v150, v78 dst_sel:WORD_1 dst_unused:UNUSED_PRESERVE src0_sel:WORD_1
	v_exp_f16_sdwa v151, v79 dst_sel:WORD_1 dst_unused:UNUSED_PRESERVE src0_sel:WORD_1
	s_nop 0
	v_pk_add_f16 v93, v93, v141
	v_pk_add_f16 v76, v151, 0
	v_pk_fma_f16 v48, v48, v148, 0
	v_pk_add_f16 v77, v150, 0
	v_pk_add_f16 v78, v149, 0
	v_pk_add_f16 v79, v148, 0
	v_pk_fma_f16 v49, v49, v149, 0
	v_pk_fma_f16 v50, v50, v150, 0
	v_pk_fma_f16 v51, v51, v151, 0
	v_pk_add_f16 v94, v94, v142
	v_pk_add_f16 v95, v95, v143
	v_pk_add_f16 v68, v68, v140
	v_exp_f16_sdwa v148, v92 dst_sel:WORD_0 dst_unused:UNUSED_PAD src0_sel:WORD_0
	v_exp_f16_sdwa v149, v93 dst_sel:WORD_0 dst_unused:UNUSED_PAD src0_sel:WORD_0
	v_exp_f16_sdwa v150, v94 dst_sel:WORD_0 dst_unused:UNUSED_PAD src0_sel:WORD_0
	v_exp_f16_sdwa v151, v95 dst_sel:WORD_0 dst_unused:UNUSED_PAD src0_sel:WORD_0
	v_exp_f16_sdwa v148, v92 dst_sel:WORD_1 dst_unused:UNUSED_PRESERVE src0_sel:WORD_1
	v_exp_f16_sdwa v149, v93 dst_sel:WORD_1 dst_unused:UNUSED_PRESERVE src0_sel:WORD_1
	v_exp_f16_sdwa v150, v94 dst_sel:WORD_1 dst_unused:UNUSED_PRESERVE src0_sel:WORD_1
	v_exp_f16_sdwa v151, v95 dst_sel:WORD_1 dst_unused:UNUSED_PRESERVE src0_sel:WORD_1
	s_nop 0
	v_pk_add_f16 v69, v69, v141
	v_pk_add_f16 v76, v76, v151
	v_pk_fma_f16 v48, v56, v148, v48
	v_pk_add_f16 v56, v115, v140
	v_pk_add_f16 v79, v79, v148
	v_pk_add_f16 v78, v78, v149
	v_pk_add_f16 v77, v77, v150
	v_pk_fma_f16 v51, v59, v151, v51
	v_pk_fma_f16 v50, v58, v150, v50
	v_pk_fma_f16 v49, v57, v149, v49
	v_pk_add_f16 v57, v114, v141
	v_pk_add_f16 v58, v113, v142
	v_pk_add_f16 v59, v112, v143
	v_pk_add_f16 v70, v70, v142
	v_exp_f16_sdwa v92, v56 dst_sel:WORD_0 dst_unused:UNUSED_PAD src0_sel:WORD_0
	v_exp_f16_sdwa v93, v57 dst_sel:WORD_0 dst_unused:UNUSED_PAD src0_sel:WORD_0
	v_exp_f16_sdwa v94, v58 dst_sel:WORD_0 dst_unused:UNUSED_PAD src0_sel:WORD_0
	v_exp_f16_sdwa v95, v59 dst_sel:WORD_0 dst_unused:UNUSED_PAD src0_sel:WORD_0
	v_exp_f16_sdwa v92, v56 dst_sel:WORD_1 dst_unused:UNUSED_PRESERVE src0_sel:WORD_1
	v_exp_f16_sdwa v93, v57 dst_sel:WORD_1 dst_unused:UNUSED_PRESERVE src0_sel:WORD_1
	v_exp_f16_sdwa v94, v58 dst_sel:WORD_1 dst_unused:UNUSED_PRESERVE src0_sel:WORD_1
	v_exp_f16_sdwa v95, v59 dst_sel:WORD_1 dst_unused:UNUSED_PRESERVE src0_sel:WORD_1
	s_nop 0
	v_pk_add_f16 v71, v71, v143
	v_pk_add_f16 v56, v76, v95
	v_pk_add_f16 v57, v77, v94
	v_pk_add_f16 v58, v78, v93
	v_pk_add_f16 v59, v79, v92
	v_pk_fma_f16 v48, v72, v92, v48
	v_pk_fma_f16 v49, v73, v93, v49
	v_pk_fma_f16 v50, v74, v94, v50
	v_pk_fma_f16 v51, v75, v95, v51
	v_pk_add_f16 v72, v119, v140
	v_pk_add_f16 v73, v118, v141
	v_pk_add_f16 v74, v117, v142
	v_pk_add_f16 v75, v116, v143
	s_nop 0
	v_exp_f16_sdwa v76, v72 dst_sel:WORD_0 dst_unused:UNUSED_PAD src0_sel:WORD_0
	v_exp_f16_sdwa v77, v73 dst_sel:WORD_0 dst_unused:UNUSED_PAD src0_sel:WORD_0
	v_exp_f16_sdwa v78, v74 dst_sel:WORD_0 dst_unused:UNUSED_PAD src0_sel:WORD_0
	v_exp_f16_sdwa v79, v75 dst_sel:WORD_0 dst_unused:UNUSED_PAD src0_sel:WORD_0
	v_exp_f16_sdwa v76, v72 dst_sel:WORD_1 dst_unused:UNUSED_PRESERVE src0_sel:WORD_1
	v_exp_f16_sdwa v77, v73 dst_sel:WORD_1 dst_unused:UNUSED_PRESERVE src0_sel:WORD_1
	v_exp_f16_sdwa v78, v74 dst_sel:WORD_1 dst_unused:UNUSED_PRESERVE src0_sel:WORD_1
	v_exp_f16_sdwa v79, v75 dst_sel:WORD_1 dst_unused:UNUSED_PRESERVE src0_sel:WORD_1
	s_nop 0
	v_pk_add_f16 v72, v135, v140
	v_pk_add_f16 v56, v56, v79
	v_pk_add_f16 v59, v59, v76
	v_pk_add_f16 v58, v58, v77
	v_pk_add_f16 v57, v57, v78
	v_pk_fma_f16 v51, v35, v79, v51
	v_pk_fma_f16 v50, v34, v78, v50
	v_pk_fma_f16 v49, v33, v77, v49
	v_pk_fma_f16 v48, v32, v76, v48
	v_pk_add_f16 v73, v134, v141
	v_pk_add_f16 v74, v133, v142
	v_pk_add_f16 v75, v132, v143
	s_nop 0
	v_exp_f16_sdwa v76, v72 dst_sel:WORD_0 dst_unused:UNUSED_PAD src0_sel:WORD_0
	v_exp_f16_sdwa v77, v73 dst_sel:WORD_0 dst_unused:UNUSED_PAD src0_sel:WORD_0
	v_exp_f16_sdwa v78, v74 dst_sel:WORD_0 dst_unused:UNUSED_PAD src0_sel:WORD_0
	v_exp_f16_sdwa v79, v75 dst_sel:WORD_0 dst_unused:UNUSED_PAD src0_sel:WORD_0
	v_exp_f16_sdwa v76, v72 dst_sel:WORD_1 dst_unused:UNUSED_PRESERVE src0_sel:WORD_1
	v_exp_f16_sdwa v77, v73 dst_sel:WORD_1 dst_unused:UNUSED_PRESERVE src0_sel:WORD_1
	v_exp_f16_sdwa v78, v74 dst_sel:WORD_1 dst_unused:UNUSED_PRESERVE src0_sel:WORD_1
	v_exp_f16_sdwa v79, v75 dst_sel:WORD_1 dst_unused:UNUSED_PRESERVE src0_sel:WORD_1
	s_nop 0
	v_pk_add_f16 v72, v139, v140
	v_pk_add_f16 v56, v56, v79
	v_pk_add_f16 v57, v57, v78
	v_pk_add_f16 v58, v58, v77
	v_pk_add_f16 v59, v59, v76
	v_pk_fma_f16 v48, v36, v76, v48
	v_pk_fma_f16 v49, v37, v77, v49
	v_pk_fma_f16 v50, v38, v78, v50
	v_pk_fma_f16 v51, v39, v79, v51
	v_pk_add_f16 v73, v138, v141
	v_pk_add_f16 v74, v137, v142
	v_pk_add_f16 v75, v136, v143
	s_nop 0
	v_exp_f16_sdwa v76, v72 dst_sel:WORD_0 dst_unused:UNUSED_PAD src0_sel:WORD_0
	v_exp_f16_sdwa v77, v73 dst_sel:WORD_0 dst_unused:UNUSED_PAD src0_sel:WORD_0
	v_exp_f16_sdwa v78, v74 dst_sel:WORD_0 dst_unused:UNUSED_PAD src0_sel:WORD_0
	v_exp_f16_sdwa v79, v75 dst_sel:WORD_0 dst_unused:UNUSED_PAD src0_sel:WORD_0
	v_exp_f16_sdwa v76, v72 dst_sel:WORD_1 dst_unused:UNUSED_PRESERVE src0_sel:WORD_1
	v_exp_f16_sdwa v77, v73 dst_sel:WORD_1 dst_unused:UNUSED_PRESERVE src0_sel:WORD_1
	v_exp_f16_sdwa v78, v74 dst_sel:WORD_1 dst_unused:UNUSED_PRESERVE src0_sel:WORD_1
	v_exp_f16_sdwa v79, v75 dst_sel:WORD_1 dst_unused:UNUSED_PRESERVE src0_sel:WORD_1
	s_nop 0
	v_exp_f16_sdwa v72, v68 dst_sel:WORD_0 dst_unused:UNUSED_PAD src0_sel:WORD_0
	v_exp_f16_sdwa v73, v69 dst_sel:WORD_0 dst_unused:UNUSED_PAD src0_sel:WORD_0
	v_exp_f16_sdwa v74, v70 dst_sel:WORD_0 dst_unused:UNUSED_PAD src0_sel:WORD_0
	v_exp_f16_sdwa v75, v71 dst_sel:WORD_0 dst_unused:UNUSED_PAD src0_sel:WORD_0
	v_exp_f16_sdwa v72, v68 dst_sel:WORD_1 dst_unused:UNUSED_PRESERVE src0_sel:WORD_1
	v_exp_f16_sdwa v73, v69 dst_sel:WORD_1 dst_unused:UNUSED_PRESERVE src0_sel:WORD_1
	v_exp_f16_sdwa v74, v70 dst_sel:WORD_1 dst_unused:UNUSED_PRESERVE src0_sel:WORD_1
	v_exp_f16_sdwa v75, v71 dst_sel:WORD_1 dst_unused:UNUSED_PRESERVE src0_sel:WORD_1
	s_nop 0
	v_pk_add_f16 v68, v96, v140
	v_pk_add_f16 v56, v56, v79
	v_pk_add_f16 v59, v59, v76
	v_pk_add_f16 v58, v58, v77
	v_pk_add_f16 v57, v57, v78
	v_pk_fma_f16 v51, v43, v79, v51
	v_pk_fma_f16 v50, v42, v78, v50
	v_pk_fma_f16 v49, v41, v77, v49
	v_pk_fma_f16 v48, v40, v76, v48
	v_pk_add_f16 v56, v56, v75
	v_pk_add_f16 v57, v57, v74
	v_pk_add_f16 v58, v58, v73
	v_pk_add_f16 v59, v59, v72
	v_pk_fma_f16 v48, v52, v72, v48
	v_pk_fma_f16 v49, v53, v73, v49
	v_pk_fma_f16 v50, v54, v74, v50
	v_pk_fma_f16 v51, v55, v75, v51
	v_pk_add_f16 v69, v97, v141
	v_pk_add_f16 v70, v98, v142
	v_pk_add_f16 v71, v99, v143
	s_nop 0
	v_exp_f16_sdwa v72, v68 dst_sel:WORD_0 dst_unused:UNUSED_PAD src0_sel:WORD_0
	v_exp_f16_sdwa v73, v69 dst_sel:WORD_0 dst_unused:UNUSED_PAD src0_sel:WORD_0
	v_exp_f16_sdwa v74, v70 dst_sel:WORD_0 dst_unused:UNUSED_PAD src0_sel:WORD_0
	v_exp_f16_sdwa v75, v71 dst_sel:WORD_0 dst_unused:UNUSED_PAD src0_sel:WORD_0
	v_exp_f16_sdwa v72, v68 dst_sel:WORD_1 dst_unused:UNUSED_PRESERVE src0_sel:WORD_1
	v_exp_f16_sdwa v73, v69 dst_sel:WORD_1 dst_unused:UNUSED_PRESERVE src0_sel:WORD_1
	v_exp_f16_sdwa v74, v70 dst_sel:WORD_1 dst_unused:UNUSED_PRESERVE src0_sel:WORD_1
	v_exp_f16_sdwa v75, v71 dst_sel:WORD_1 dst_unused:UNUSED_PRESERVE src0_sel:WORD_1
	s_nop 0
	v_pk_add_f16 v68, v108, v140
	v_pk_add_f16 v56, v56, v75
	v_pk_add_f16 v59, v59, v72
	v_pk_add_f16 v58, v58, v73
	v_pk_add_f16 v57, v57, v74
	v_pk_fma_f16 v51, v67, v75, v51
	v_pk_fma_f16 v50, v66, v74, v50
	v_pk_fma_f16 v49, v65, v73, v49
	v_pk_fma_f16 v48, v64, v72, v48
	v_pk_add_f16 v69, v109, v141
	v_pk_add_f16 v70, v110, v142
	v_pk_add_f16 v71, v111, v143
	s_nop 0
	v_exp_f16_sdwa v72, v68 dst_sel:WORD_0 dst_unused:UNUSED_PAD src0_sel:WORD_0
	v_exp_f16_sdwa v73, v69 dst_sel:WORD_0 dst_unused:UNUSED_PAD src0_sel:WORD_0
	v_exp_f16_sdwa v74, v70 dst_sel:WORD_0 dst_unused:UNUSED_PAD src0_sel:WORD_0
	v_exp_f16_sdwa v75, v71 dst_sel:WORD_0 dst_unused:UNUSED_PAD src0_sel:WORD_0
	v_exp_f16_sdwa v72, v68 dst_sel:WORD_1 dst_unused:UNUSED_PRESERVE src0_sel:WORD_1
	v_exp_f16_sdwa v73, v69 dst_sel:WORD_1 dst_unused:UNUSED_PRESERVE src0_sel:WORD_1
	v_exp_f16_sdwa v74, v70 dst_sel:WORD_1 dst_unused:UNUSED_PRESERVE src0_sel:WORD_1
	v_exp_f16_sdwa v75, v71 dst_sel:WORD_1 dst_unused:UNUSED_PRESERVE src0_sel:WORD_1
	s_nop 0
	s_nop 0
	v_pk_add_f16 v56, v56, v75
	v_pk_add_f16 v57, v57, v74
	v_rcp_f16_e32 v70, v56
	v_rcp_f16_sdwa v56, v56 dst_sel:DWORD dst_unused:UNUSED_PAD src0_sel:WORD_1
	v_pk_add_f16 v58, v58, v73
	v_rcp_f16_e32 v71, v57
	v_rcp_f16_sdwa v57, v57 dst_sel:DWORD dst_unused:UNUSED_PAD src0_sel:WORD_1
	v_pk_add_f16 v59, v59, v72
	v_rcp_f16_e32 v69, v58
	v_rcp_f16_sdwa v58, v58 dst_sel:DWORD dst_unused:UNUSED_PAD src0_sel:WORD_1
	v_rcp_f16_e32 v68, v59
	v_rcp_f16_sdwa v59, v59 dst_sel:DWORD dst_unused:UNUSED_PAD src0_sel:WORD_1
	v_pk_fma_f16 v51, v87, v75, v51
	v_pack_b32_f16 v56, v70, v56
	v_pk_fma_f16 v50, v86, v74, v50
	v_pk_mul_f16 v51, v51, v56
	v_pack_b32_f16 v56, v71, v57
	v_pk_fma_f16 v49, v85, v73, v49
	v_pk_mul_f16 v50, v50, v56
	v_pack_b32_f16 v56, v69, v58
	v_pk_fma_f16 v48, v84, v72, v48
	v_pk_mul_f16 v49, v49, v56
	v_pack_b32_f16 v56, v68, v59
	v_pk_mul_f16 v48, v48, v56
	s_waitcnt vmcnt(0)
	v_pk_mul_f16 v56, v188, v168 op_sel_hi:[0,1]
	v_pk_mul_f16 v57, v188, v169 op_sel_hi:[0,1]
	v_pk_mul_f16 v58, v188, v170 op_sel_hi:[0,1]
	v_pk_mul_f16 v59, v188, v171 op_sel_hi:[0,1]
	v_pk_mul_f16 v68, v186, v168 op_sel_hi:[0,1]
	v_pk_mul_f16 v69, v186, v169 op_sel_hi:[0,1]
	v_pk_mul_f16 v70, v186, v170 op_sel_hi:[0,1]
	v_pk_mul_f16 v71, v186, v171 op_sel_hi:[0,1]
	v_pk_mul_f16 v72, v187, v168 op_sel_hi:[0,1]
	v_pk_mul_f16 v73, v187, v169 op_sel_hi:[0,1]
	v_pk_mul_f16 v74, v187, v170 op_sel_hi:[0,1]
	v_pk_mul_f16 v75, v187, v171 op_sel_hi:[0,1]
	v_pk_fma_f16 v47, v47, v171, v59
	v_pk_fma_f16 v46, v46, v170, v58
	v_pk_fma_f16 v45, v45, v169, v57
	v_pk_fma_f16 v44, v44, v168, v56
	v_pk_fma_f16 v63, v63, v171, v71
	v_pk_fma_f16 v62, v62, v170, v70
	v_pk_fma_f16 v61, v61, v169, v69
	v_pk_fma_f16 v60, v60, v168, v68
	v_pk_fma_f16 v76, v83, v171, v75
	v_pk_fma_f16 v77, v82, v170, v74
	v_pk_fma_f16 v78, v81, v169, v73
	v_pk_fma_f16 v79, v80, v168, v72
	v_pk_fma_f16 v80, v103, v171, v59
	v_pk_fma_f16 v81, v102, v170, v58
	v_pk_fma_f16 v82, v101, v169, v57
	v_pk_fma_f16 v83, v100, v168, v56
	v_pk_fma_f16 v92, v131, v171, v71
	v_pk_fma_f16 v93, v130, v170, v70
	v_pk_fma_f16 v94, v129, v169, v69
	v_pk_fma_f16 v95, v128, v168, v68
	v_pk_fma_f16 v96, v147, v171, v75
	v_pk_fma_f16 v97, v146, v170, v74
	v_pk_fma_f16 v98, v145, v169, v73
	v_pk_fma_f16 v99, v144, v168, v72
	v_pk_fma_f16 v75, v31, v171, v75
	v_pk_fma_f16 v74, v30, v170, v74
	v_pk_fma_f16 v73, v29, v169, v73
	v_pk_fma_f16 v72, v28, v168, v72
	v_pk_maximum3_f16 v28, v44, v60, v79
	v_pk_maximum3_f16 v29, v45, v61, v78
	v_pk_maximum3_f16 v30, v46, v62, v77
	v_pk_maximum3_f16 v31, v47, v63, v76
	v_pk_maximum3_f16 v100, v83, v95, v99
	v_pk_maximum3_f16 v101, v82, v94, v98
	v_pk_maximum3_f16 v102, v81, v93, v97
	v_pk_maximum3_f16 v103, v80, v92, v96
	v_pk_fma_f16 v59, v159, v171, v59
	v_pk_fma_f16 v58, v158, v170, v58
	v_pk_fma_f16 v57, v157, v169, v57
	v_pk_fma_f16 v56, v156, v168, v56
	v_pk_fma_f16 v71, v167, v171, v71
	v_pk_fma_f16 v70, v166, v170, v70
	v_pk_fma_f16 v69, v165, v169, v69
	v_pk_fma_f16 v68, v164, v168, v68
	v_pk_maximum3_f16 v109, v57, v69, v73
	v_pk_maximum3_f16 v110, v58, v70, v74
	v_pk_maximum3_f16 v111, v59, v71, v75
	s_nop 0
	v_pk_maximum3_f16 v108, v56, v68, v72
	v_pk_maximum3_f16 v29, v29, v101, v109
	v_pk_maximum3_f16 v30, v30, v102, v110
	v_pk_maximum3_f16 v31, v31, v103, v111
	s_nop 0
	v_pk_maximum3_f16 v28, v28, v100, v108
	v_xor_b32_e32 v100, 0x80008000, v31
	v_xor_b32_e32 v101, 0x80008000, v30
	v_xor_b32_e32 v102, 0x80008000, v29
	v_xor_b32_e32 v103, 0x80008000, v28
	v_pk_add_f16 v28, v44, v103
	v_pk_add_f16 v29, v45, v102
	v_pk_add_f16 v30, v46, v101
	v_pk_add_f16 v31, v47, v100
	s_nop 0
	v_exp_f16_sdwa v44, v28 dst_sel:WORD_0 dst_unused:UNUSED_PAD src0_sel:WORD_0
	v_exp_f16_sdwa v45, v29 dst_sel:WORD_0 dst_unused:UNUSED_PAD src0_sel:WORD_0
	v_exp_f16_sdwa v46, v30 dst_sel:WORD_0 dst_unused:UNUSED_PAD src0_sel:WORD_0
	v_exp_f16_sdwa v47, v31 dst_sel:WORD_0 dst_unused:UNUSED_PAD src0_sel:WORD_0
	v_exp_f16_sdwa v44, v28 dst_sel:WORD_1 dst_unused:UNUSED_PRESERVE src0_sel:WORD_1
	v_exp_f16_sdwa v45, v29 dst_sel:WORD_1 dst_unused:UNUSED_PRESERVE src0_sel:WORD_1
	v_exp_f16_sdwa v46, v30 dst_sel:WORD_1 dst_unused:UNUSED_PRESERVE src0_sel:WORD_1
	v_exp_f16_sdwa v47, v31 dst_sel:WORD_1 dst_unused:UNUSED_PRESERVE src0_sel:WORD_1
	s_nop 0
	s_nop 0
	v_pk_add_f16 v28, v44, 0
	v_pk_add_f16 v29, v45, 0
	v_pk_add_f16 v30, v46, 0
	v_pk_add_f16 v31, v47, 0
	v_pk_fma_f16 v32, v32, v44, 0
	v_pk_fma_f16 v33, v33, v45, 0
	v_pk_fma_f16 v34, v34, v46, 0
	v_pk_fma_f16 v35, v35, v47, 0
	v_pk_add_f16 v44, v60, v103
	v_pk_add_f16 v45, v61, v102
	v_pk_add_f16 v46, v62, v101
	v_pk_add_f16 v47, v63, v100
	s_nop 0
	v_exp_f16_sdwa v60, v44 dst_sel:WORD_0 dst_unused:UNUSED_PAD src0_sel:WORD_0
	v_exp_f16_sdwa v61, v45 dst_sel:WORD_0 dst_unused:UNUSED_PAD src0_sel:WORD_0
	v_exp_f16_sdwa v62, v46 dst_sel:WORD_0 dst_unused:UNUSED_PAD src0_sel:WORD_0
	v_exp_f16_sdwa v63, v47 dst_sel:WORD_0 dst_unused:UNUSED_PAD src0_sel:WORD_0
	v_exp_f16_sdwa v60, v44 dst_sel:WORD_1 dst_unused:UNUSED_PRESERVE src0_sel:WORD_1
	v_exp_f16_sdwa v61, v45 dst_sel:WORD_1 dst_unused:UNUSED_PRESERVE src0_sel:WORD_1
	v_exp_f16_sdwa v62, v46 dst_sel:WORD_1 dst_unused:UNUSED_PRESERVE src0_sel:WORD_1
	v_exp_f16_sdwa v63, v47 dst_sel:WORD_1 dst_unused:UNUSED_PRESERVE src0_sel:WORD_1
	s_nop 0
	s_nop 0
	v_pk_add_f16 v31, v31, v63
	v_pk_add_f16 v30, v30, v62
	v_pk_add_f16 v29, v29, v61
	v_pk_add_f16 v28, v28, v60
	v_pk_fma_f16 v35, v39, v63, v35
	v_pk_fma_f16 v34, v38, v62, v34
	v_pk_fma_f16 v33, v37, v61, v33
	v_pk_fma_f16 v32, v36, v60, v32
	v_pk_add_f16 v36, v79, v103
	v_pk_add_f16 v37, v78, v102
	v_pk_add_f16 v38, v77, v101
	v_pk_add_f16 v39, v76, v100
	s_nop 0
	v_exp_f16_sdwa v44, v36 dst_sel:WORD_0 dst_unused:UNUSED_PAD src0_sel:WORD_0
	v_exp_f16_sdwa v45, v37 dst_sel:WORD_0 dst_unused:UNUSED_PAD src0_sel:WORD_0
	v_exp_f16_sdwa v46, v38 dst_sel:WORD_0 dst_unused:UNUSED_PAD src0_sel:WORD_0
	v_exp_f16_sdwa v47, v39 dst_sel:WORD_0 dst_unused:UNUSED_PAD src0_sel:WORD_0
	v_exp_f16_sdwa v44, v36 dst_sel:WORD_1 dst_unused:UNUSED_PRESERVE src0_sel:WORD_1
	v_exp_f16_sdwa v45, v37 dst_sel:WORD_1 dst_unused:UNUSED_PRESERVE src0_sel:WORD_1
	v_exp_f16_sdwa v46, v38 dst_sel:WORD_1 dst_unused:UNUSED_PRESERVE src0_sel:WORD_1
	v_exp_f16_sdwa v47, v39 dst_sel:WORD_1 dst_unused:UNUSED_PRESERVE src0_sel:WORD_1
	s_nop 0
	v_pk_add_f16 v36, v83, v103
	v_pk_add_f16 v28, v28, v44
	v_pk_add_f16 v29, v29, v45
	v_pk_add_f16 v30, v30, v46
	v_pk_add_f16 v31, v31, v47
	v_pk_fma_f16 v32, v40, v44, v32
	v_pk_fma_f16 v33, v41, v45, v33
	v_pk_fma_f16 v34, v42, v46, v34
	v_pk_fma_f16 v35, v43, v47, v35
	v_pk_add_f16 v37, v82, v102
	v_pk_add_f16 v38, v81, v101
	v_pk_add_f16 v39, v80, v100
	s_nop 0
	v_exp_f16_sdwa v40, v36 dst_sel:WORD_0 dst_unused:UNUSED_PAD src0_sel:WORD_0
	v_exp_f16_sdwa v41, v37 dst_sel:WORD_0 dst_unused:UNUSED_PAD src0_sel:WORD_0
	v_exp_f16_sdwa v42, v38 dst_sel:WORD_0 dst_unused:UNUSED_PAD src0_sel:WORD_0
	v_exp_f16_sdwa v43, v39 dst_sel:WORD_0 dst_unused:UNUSED_PAD src0_sel:WORD_0
	v_exp_f16_sdwa v40, v36 dst_sel:WORD_1 dst_unused:UNUSED_PRESERVE src0_sel:WORD_1
	v_exp_f16_sdwa v41, v37 dst_sel:WORD_1 dst_unused:UNUSED_PRESERVE src0_sel:WORD_1
	v_exp_f16_sdwa v42, v38 dst_sel:WORD_1 dst_unused:UNUSED_PRESERVE src0_sel:WORD_1
	v_exp_f16_sdwa v43, v39 dst_sel:WORD_1 dst_unused:UNUSED_PRESERVE src0_sel:WORD_1
	s_nop 0
	v_pk_add_f16 v36, v95, v103
	v_pk_add_f16 v31, v31, v43
	v_pk_add_f16 v30, v30, v42
	v_pk_add_f16 v29, v29, v41
	v_pk_add_f16 v28, v28, v40
	v_pk_fma_f16 v35, v55, v43, v35
	v_pk_fma_f16 v34, v54, v42, v34
	v_pk_fma_f16 v33, v53, v41, v33
	v_pk_fma_f16 v32, v52, v40, v32
	v_pk_add_f16 v37, v94, v102
	v_pk_add_f16 v38, v93, v101
	v_pk_add_f16 v39, v92, v100
	s_nop 0
	v_exp_f16_sdwa v40, v36 dst_sel:WORD_0 dst_unused:UNUSED_PAD src0_sel:WORD_0
	v_exp_f16_sdwa v41, v37 dst_sel:WORD_0 dst_unused:UNUSED_PAD src0_sel:WORD_0
	v_exp_f16_sdwa v42, v38 dst_sel:WORD_0 dst_unused:UNUSED_PAD src0_sel:WORD_0
	v_exp_f16_sdwa v43, v39 dst_sel:WORD_0 dst_unused:UNUSED_PAD src0_sel:WORD_0
	v_exp_f16_sdwa v40, v36 dst_sel:WORD_1 dst_unused:UNUSED_PRESERVE src0_sel:WORD_1
	v_exp_f16_sdwa v41, v37 dst_sel:WORD_1 dst_unused:UNUSED_PRESERVE src0_sel:WORD_1
	v_exp_f16_sdwa v42, v38 dst_sel:WORD_1 dst_unused:UNUSED_PRESERVE src0_sel:WORD_1
	v_exp_f16_sdwa v43, v39 dst_sel:WORD_1 dst_unused:UNUSED_PRESERVE src0_sel:WORD_1
	s_nop 0
	v_pk_add_f16 v36, v99, v103
	v_pk_add_f16 v28, v28, v40
	v_pk_add_f16 v29, v29, v41
	v_pk_add_f16 v30, v30, v42
	v_pk_add_f16 v31, v31, v43
	v_pk_fma_f16 v32, v64, v40, v32
	v_pk_fma_f16 v33, v65, v41, v33
	v_pk_fma_f16 v34, v66, v42, v34
	v_pk_fma_f16 v35, v67, v43, v35
	v_pk_add_f16 v37, v98, v102
	v_pk_add_f16 v38, v97, v101
	v_pk_add_f16 v39, v96, v100
	s_nop 0
	v_exp_f16_sdwa v40, v36 dst_sel:WORD_0 dst_unused:UNUSED_PAD src0_sel:WORD_0
	v_exp_f16_sdwa v41, v37 dst_sel:WORD_0 dst_unused:UNUSED_PAD src0_sel:WORD_0
	v_exp_f16_sdwa v42, v38 dst_sel:WORD_0 dst_unused:UNUSED_PAD src0_sel:WORD_0
	v_exp_f16_sdwa v43, v39 dst_sel:WORD_0 dst_unused:UNUSED_PAD src0_sel:WORD_0
	v_exp_f16_sdwa v40, v36 dst_sel:WORD_1 dst_unused:UNUSED_PRESERVE src0_sel:WORD_1
	v_exp_f16_sdwa v41, v37 dst_sel:WORD_1 dst_unused:UNUSED_PRESERVE src0_sel:WORD_1
	v_exp_f16_sdwa v42, v38 dst_sel:WORD_1 dst_unused:UNUSED_PRESERVE src0_sel:WORD_1
	v_exp_f16_sdwa v43, v39 dst_sel:WORD_1 dst_unused:UNUSED_PRESERVE src0_sel:WORD_1
	s_nop 0
	v_pk_add_f16 v36, v56, v103
	v_pk_add_f16 v31, v31, v43
	v_pk_add_f16 v30, v30, v42
	v_pk_add_f16 v29, v29, v41
	v_pk_add_f16 v28, v28, v40
	v_pk_fma_f16 v35, v87, v43, v35
	v_pk_fma_f16 v34, v86, v42, v34
	v_pk_fma_f16 v33, v85, v41, v33
	v_pk_fma_f16 v32, v84, v40, v32
	v_pk_add_f16 v37, v57, v102
	v_pk_add_f16 v38, v58, v101
	v_pk_add_f16 v39, v59, v100
	s_nop 0
	v_exp_f16_sdwa v40, v36 dst_sel:WORD_0 dst_unused:UNUSED_PAD src0_sel:WORD_0
	v_exp_f16_sdwa v41, v37 dst_sel:WORD_0 dst_unused:UNUSED_PAD src0_sel:WORD_0
	v_exp_f16_sdwa v42, v38 dst_sel:WORD_0 dst_unused:UNUSED_PAD src0_sel:WORD_0
	v_exp_f16_sdwa v43, v39 dst_sel:WORD_0 dst_unused:UNUSED_PAD src0_sel:WORD_0
	v_exp_f16_sdwa v40, v36 dst_sel:WORD_1 dst_unused:UNUSED_PRESERVE src0_sel:WORD_1
	v_exp_f16_sdwa v41, v37 dst_sel:WORD_1 dst_unused:UNUSED_PRESERVE src0_sel:WORD_1
	v_exp_f16_sdwa v42, v38 dst_sel:WORD_1 dst_unused:UNUSED_PRESERVE src0_sel:WORD_1
	v_exp_f16_sdwa v43, v39 dst_sel:WORD_1 dst_unused:UNUSED_PRESERVE src0_sel:WORD_1
	s_nop 0
	v_pk_add_f16 v36, v68, v103
	v_pk_add_f16 v28, v28, v40
	v_pk_add_f16 v29, v29, v41
	v_pk_add_f16 v30, v30, v42
	v_pk_add_f16 v31, v31, v43
	v_pk_fma_f16 v32, v104, v40, v32
	v_pk_fma_f16 v33, v105, v41, v33
	v_pk_fma_f16 v34, v106, v42, v34
	v_pk_fma_f16 v35, v107, v43, v35
	v_pk_add_f16 v37, v69, v102
	v_pk_add_f16 v38, v70, v101
	v_pk_add_f16 v39, v71, v100
	s_nop 0
	v_exp_f16_sdwa v40, v36 dst_sel:WORD_0 dst_unused:UNUSED_PAD src0_sel:WORD_0
	v_exp_f16_sdwa v41, v37 dst_sel:WORD_0 dst_unused:UNUSED_PAD src0_sel:WORD_0
	v_exp_f16_sdwa v42, v38 dst_sel:WORD_0 dst_unused:UNUSED_PAD src0_sel:WORD_0
	v_exp_f16_sdwa v43, v39 dst_sel:WORD_0 dst_unused:UNUSED_PAD src0_sel:WORD_0
	v_exp_f16_sdwa v40, v36 dst_sel:WORD_1 dst_unused:UNUSED_PRESERVE src0_sel:WORD_1
	v_exp_f16_sdwa v41, v37 dst_sel:WORD_1 dst_unused:UNUSED_PRESERVE src0_sel:WORD_1
	v_exp_f16_sdwa v42, v38 dst_sel:WORD_1 dst_unused:UNUSED_PRESERVE src0_sel:WORD_1
	v_exp_f16_sdwa v43, v39 dst_sel:WORD_1 dst_unused:UNUSED_PRESERVE src0_sel:WORD_1
	s_nop 0
	s_nop 0
	v_pk_add_f16 v31, v31, v43
	v_pk_add_f16 v30, v30, v42
	v_pk_add_f16 v29, v29, v41
	v_pk_add_f16 v28, v28, v40
	v_pk_fma_f16 v35, v123, v43, v35
	v_pk_fma_f16 v34, v122, v42, v34
	v_pk_fma_f16 v33, v121, v41, v33
	v_pk_fma_f16 v32, v120, v40, v32
	v_pk_add_f16 v40, v72, v103
	v_pk_add_f16 v41, v73, v102
	v_pk_add_f16 v42, v74, v101
	v_pk_add_f16 v43, v75, v100
	s_nop 0
	v_exp_f16_sdwa v36, v40 dst_sel:WORD_0 dst_unused:UNUSED_PAD src0_sel:WORD_0
	v_exp_f16_sdwa v37, v41 dst_sel:WORD_0 dst_unused:UNUSED_PAD src0_sel:WORD_0
	v_exp_f16_sdwa v38, v42 dst_sel:WORD_0 dst_unused:UNUSED_PAD src0_sel:WORD_0
	v_exp_f16_sdwa v39, v43 dst_sel:WORD_0 dst_unused:UNUSED_PAD src0_sel:WORD_0
	v_exp_f16_sdwa v36, v40 dst_sel:WORD_1 dst_unused:UNUSED_PRESERVE src0_sel:WORD_1
	v_exp_f16_sdwa v37, v41 dst_sel:WORD_1 dst_unused:UNUSED_PRESERVE src0_sel:WORD_1
	v_exp_f16_sdwa v38, v42 dst_sel:WORD_1 dst_unused:UNUSED_PRESERVE src0_sel:WORD_1
	v_exp_f16_sdwa v39, v43 dst_sel:WORD_1 dst_unused:UNUSED_PRESERVE src0_sel:WORD_1
	s_nop 0
	s_load_dwordx2 s[12:13], s[0:1], 0x60
	s_branch .LBB6_76
.LBB6_38:
	s_load_dwordx2 s[12:13], s[0:1], 0x60
	s_cbranch_execz .LBB6_76
	v_cmp_lt_u32_e64 s[64:65], 0, v182
	v_cmp_gt_u32_e64 s[66:67], 63, v182
	v_cmp_lt_u32_e64 s[68:69], 0, v181
	v_cmp_gt_u32_e64 s[70:71], 60, v181
	buffer_load_dwordx4 v[168:171], v183, s[8:11], 0 offen
	v_add_u32_e32 v227, 0x18000, v183
	buffer_load_dwordx4 v[160:163], v227, s[8:11], 0 offen
	s_and_b64 s[72:73], s[68:69], s[64:65]
	s_and_b64 s[74:75], s[68:69], s[66:67]
	s_and_b64 s[76:77], s[70:71], s[64:65]
	s_and_b64 s[78:79], s[70:71], s[66:67]
	v_add_u32_e32 v226, 0xfffe7c00, v183
	v_add_u32_e32 v227, 0xfffe8000, v183
	v_mov_b32_e32 v140, v20
	v_mov_b32_e32 v141, v21
	v_mov_b32_e32 v142, v22
	v_mov_b32_e32 v143, v23
	v_mov_b32_e32 v120, v16
	v_mov_b32_e32 v121, v17
	v_mov_b32_e32 v122, v18
	v_mov_b32_e32 v123, v19
	v_mov_b32_e32 v152, v20
	v_mov_b32_e32 v153, v21
	v_mov_b32_e32 v154, v22
	v_mov_b32_e32 v155, v23
	v_mov_b32_e32 v132, v16
	v_mov_b32_e32 v133, v17
	v_mov_b32_e32 v134, v18
	v_mov_b32_e32 v135, v19
	v_mov_b32_e32 v156, v20
	v_mov_b32_e32 v157, v21
	v_mov_b32_e32 v158, v22
	v_mov_b32_e32 v159, v23
	v_mov_b32_e32 v144, v16
	v_mov_b32_e32 v145, v17
	v_mov_b32_e32 v146, v18
	v_mov_b32_e32 v147, v19
	s_mov_b64 exec, s[72:73]
	buffer_load_dwordx4 v[140:143], v226, s[8:11], 0 offen
	buffer_load_dwordx4 v[120:123], v226, s[8:11], 0 offen offset:512
	s_mov_b64 exec, -1
	s_mov_b64 exec, s[68:69]
	buffer_load_dwordx4 v[152:155], v227, s[8:11], 0 offen offset:512
	buffer_load_dwordx4 v[132:135], v227, s[8:11], 0 offen offset:1024
	s_mov_b64 exec, -1
	s_mov_b64 exec, s[74:75]
	buffer_load_dwordx4 v[156:159], v227, s[8:11], 0 offen offset:2048
	buffer_load_dwordx4 v[144:147], v227, s[8:11], 0 offen offset:2560
	s_mov_b64 exec, -1
	v_add_u32_e32 v226, 0xfffffc00, v183
	v_mov_b32_e32 v124, v20
	v_mov_b32_e32 v125, v21
	v_mov_b32_e32 v126, v22
	v_mov_b32_e32 v127, v23
	v_mov_b32_e32 v104, v16
	v_mov_b32_e32 v105, v17
	v_mov_b32_e32 v106, v18
	v_mov_b32_e32 v107, v19
	v_mov_b32_e32 v148, v20
	v_mov_b32_e32 v149, v21
	v_mov_b32_e32 v150, v22
	v_mov_b32_e32 v151, v23
	v_mov_b32_e32 v88, v16
	v_mov_b32_e32 v89, v17
	v_mov_b32_e32 v90, v18
	v_mov_b32_e32 v91, v19
	s_mov_b64 exec, s[64:65]
	buffer_load_dwordx4 v[124:127], v226, s[8:11], 0 offen
	buffer_load_dwordx4 v[104:107], v226, s[8:11], 0 offen offset:512
	s_mov_b64 exec, -1
	buffer_load_dwordx4 v[136:139], v183, s[8:11], 0 offen offset:512
	buffer_load_dwordx4 v[108:111], v183, s[8:11], 0 offen offset:1024
	s_mov_b64 exec, s[66:67]
	buffer_load_dwordx4 v[148:151], v183, s[8:11], 0 offen offset:2048
	buffer_load_dwordx4 v[88:91], v183, s[8:11], 0 offen offset:2560
	s_mov_b64 exec, -1
	v_add_u32_e32 v226, 0x17c00, v183
	v_add_u32_e32 v227, 0x18000, v183
	v_mov_b32_e32 v64, v20
	v_mov_b32_e32 v65, v21
	v_mov_b32_e32 v66, v22
	v_mov_b32_e32 v67, v23
	v_mov_b32_e32 v40, v16
	v_mov_b32_e32 v41, v17
	v_mov_b32_e32 v42, v18
	v_mov_b32_e32 v43, v19
	v_mov_b32_e32 v92, v20
	v_mov_b32_e32 v93, v21
	v_mov_b32_e32 v94, v22
	v_mov_b32_e32 v95, v23
	v_mov_b32_e32 v60, v16
	v_mov_b32_e32 v61, v17
	v_mov_b32_e32 v62, v18
	v_mov_b32_e32 v63, v19
	s_mov_b64 exec, s[64:65]
	buffer_load_dwordx4 v[64:67], v226, s[8:11], 0 offen
	buffer_load_dwordx4 v[40:43], v226, s[8:11], 0 offen offset:512
	s_mov_b64 exec, -1
	buffer_load_dwordx4 v[76:79], v227, s[8:11], 0 offen offset:512
	buffer_load_dwordx4 v[48:51], v227, s[8:11], 0 offen offset:1024
	s_mov_b64 exec, s[66:67]
	buffer_load_dwordx4 v[92:95], v227, s[8:11], 0 offen offset:2048
	buffer_load_dwordx4 v[60:63], v227, s[8:11], 0 offen offset:2560
	s_mov_b64 exec, -1
	v_add_u32_e32 v226, 0x2fc00, v183
	v_add_u32_e32 v227, 0x30000, v183
	v_mov_b32_e32 v36, v20
	v_mov_b32_e32 v37, v21
	v_mov_b32_e32 v38, v22
	v_mov_b32_e32 v39, v23
	v_mov_b32_e32 v24, v16
	v_mov_b32_e32 v25, v17
	v_mov_b32_e32 v26, v18
	v_mov_b32_e32 v27, v19
	v_mov_b32_e32 v68, v20
	v_mov_b32_e32 v69, v21
	v_mov_b32_e32 v70, v22
	v_mov_b32_e32 v71, v23
	v_mov_b32_e32 v32, v16
	v_mov_b32_e32 v33, v17
	v_mov_b32_e32 v34, v18
	v_mov_b32_e32 v35, v19
	s_mov_b64 exec, s[64:65]
	buffer_load_dwordx4 v[36:39], v226, s[8:11], 0 offen
	buffer_load_dwordx4 v[24:27], v226, s[8:11], 0 offen offset:512
	s_mov_b64 exec, -1
	buffer_load_dwordx4 v[52:55], v227, s[8:11], 0 offen offset:512
	buffer_load_dwordx4 v[28:31], v227, s[8:11], 0 offen offset:1024
	s_mov_b64 exec, s[66:67]
	buffer_load_dwordx4 v[68:71], v227, s[8:11], 0 offen offset:2048
	buffer_load_dwordx4 v[32:35], v227, s[8:11], 0 offen offset:2560
	s_mov_b64 exec, -1
	v_add_u32_e32 v226, 0x47c00, v183
	v_add_u32_e32 v227, 0x48000, v183
	v_mov_b32_e32 v80, v20
	v_mov_b32_e32 v81, v21
	v_mov_b32_e32 v82, v22
	v_mov_b32_e32 v83, v23
	v_mov_b32_e32 v44, v16
	v_mov_b32_e32 v45, v17
	v_mov_b32_e32 v46, v18
	v_mov_b32_e32 v47, v19
	v_mov_b32_e32 v112, v20
	v_mov_b32_e32 v113, v21
	v_mov_b32_e32 v114, v22
	v_mov_b32_e32 v115, v23
	v_mov_b32_e32 v72, v16
	v_mov_b32_e32 v73, v17
	v_mov_b32_e32 v74, v18
	v_mov_b32_e32 v75, v19
	s_mov_b64 exec, s[64:65]
	buffer_load_dwordx4 v[80:83], v226, s[8:11], 0 offen
	buffer_load_dwordx4 v[44:47], v226, s[8:11], 0 offen offset:512
	s_mov_b64 exec, -1
	buffer_load_dwordx4 v[100:103], v227, s[8:11], 0 offen offset:512
	buffer_load_dwordx4 v[56:59], v227, s[8:11], 0 offen offset:1024
	s_mov_b64 exec, s[66:67]
	buffer_load_dwordx4 v[112:115], v227, s[8:11], 0 offen offset:2048
	buffer_load_dwordx4 v[72:75], v227, s[8:11], 0 offen offset:2560
	s_mov_b64 exec, -1
	v_add_u32_e32 v226, 0x5fc00, v183
	v_add_u32_e32 v227, 0x60000, v183
	v_mov_b32_e32 v116, v20
	v_mov_b32_e32 v117, v21
	v_mov_b32_e32 v118, v22
	v_mov_b32_e32 v119, v23
	v_mov_b32_e32 v84, v16
	v_mov_b32_e32 v85, v17
	v_mov_b32_e32 v86, v18
	v_mov_b32_e32 v87, v19
	v_mov_b32_e32 v128, v20
	v_mov_b32_e32 v129, v21
	v_mov_b32_e32 v130, v22
	v_mov_b32_e32 v131, v23
	v_mov_b32_e32 v96, v16
	v_mov_b32_e32 v97, v17
	v_mov_b32_e32 v98, v18
	v_mov_b32_e32 v99, v19
	s_mov_b64 exec, s[76:77]
	buffer_load_dwordx4 v[116:119], v226, s[8:11], 0 offen
	buffer_load_dwordx4 v[84:87], v226, s[8:11], 0 offen offset:512
	s_mov_b64 exec, -1
	s_mov_b64 exec, s[70:71]
	buffer_load_dwordx4 v[128:131], v227, s[8:11], 0 offen offset:512
	buffer_load_dwordx4 v[96:99], v227, s[8:11], 0 offen offset:1024
	s_mov_b64 exec, -1
	s_mov_b64 exec, s[78:79]
	buffer_load_dwordx4 v[20:23], v227, s[8:11], 0 offen offset:2048
	buffer_load_dwordx4 v[16:19], v227, s[8:11], 0 offen offset:2560
	s_mov_b64 exec, -1
	s_load_dwordx2 s[2:3], s[0:1], 0x18
	s_waitcnt lgkmcnt(0)
	s_load_dwordx2 s[0:1], s[2:3], 0x0
	s_load_dword s4, s[2:3], 0x8
	s_waitcnt lgkmcnt(0)
	v_cvt_f16_f32_e32 v164, s0
	v_cvt_f16_f32_e32 v165, s1
	v_cvt_f16_f32_e32 v166, s4
	s_waitcnt vmcnt(18)
	v_pk_mul_f16 v167, v164, v168 op_sel_hi:[0,1]
	v_pk_mul_f16 v172, v164, v169 op_sel_hi:[0,1]
	v_pk_mul_f16 v173, v164, v170 op_sel_hi:[0,1]
	v_pk_mul_f16 v174, v164, v171 op_sel_hi:[0,1]
	v_pk_mul_f16 v175, v165, v170 op_sel_hi:[0,1]
	v_pk_mul_f16 v176, v165, v171 op_sel_hi:[0,1]
	v_pk_mul_f16 v177, v165, v169 op_sel_hi:[0,1]
	v_pk_mul_f16 v178, v165, v168 op_sel_hi:[0,1]
	v_pk_mul_f16 v179, v166, v171 op_sel_hi:[0,1]
	v_pk_mul_f16 v184, v166, v170 op_sel_hi:[0,1]
	v_pk_mul_f16 v185, v166, v169 op_sel_hi:[0,1]
	v_pk_mul_f16 v186, v166, v168 op_sel_hi:[0,1]
	v_pk_fma_f16 v143, v143, v171, v174
	v_pk_fma_f16 v142, v142, v170, v173
	v_pk_fma_f16 v141, v141, v169, v172
	v_pk_fma_f16 v140, v140, v168, v167
	v_pk_fma_f16 v155, v155, v171, v174
	v_pk_fma_f16 v154, v154, v170, v173
	v_pk_fma_f16 v153, v153, v169, v172
	v_pk_fma_f16 v152, v152, v168, v167
	v_pk_fma_f16 v159, v159, v171, v174
	v_pk_fma_f16 v158, v158, v170, v173
	v_pk_fma_f16 v157, v157, v169, v172
	v_pk_fma_f16 v156, v156, v168, v167
	v_pk_fma_f16 v167, v127, v171, v176
	v_pk_fma_f16 v172, v126, v170, v175
	v_pk_fma_f16 v173, v139, v171, v176
	v_pk_fma_f16 v174, v138, v170, v175
	v_pk_fma_f16 v176, v151, v171, v176
	v_pk_fma_f16 v175, v150, v170, v175
	v_pk_fma_f16 v187, v125, v169, v177
	v_pk_fma_f16 v188, v137, v169, v177
	v_pk_fma_f16 v177, v149, v169, v177
	v_pk_fma_f16 v189, v124, v168, v178
	v_pk_fma_f16 v190, v136, v168, v178
	v_pk_fma_f16 v178, v148, v168, v178
	v_pk_fma_f16 v191, v67, v171, v179
	v_pk_fma_f16 v192, v79, v171, v179
	v_pk_fma_f16 v171, v95, v171, v179
	v_pk_fma_f16 v179, v66, v170, v184
	v_pk_fma_f16 v193, v78, v170, v184
	v_pk_fma_f16 v170, v94, v170, v184
	v_pk_fma_f16 v184, v65, v169, v185
	v_pk_fma_f16 v194, v77, v169, v185
	v_pk_fma_f16 v169, v93, v169, v185
	v_pk_fma_f16 v185, v64, v168, v186
	v_pk_fma_f16 v195, v76, v168, v186
	v_pk_fma_f16 v168, v92, v168, v186
	v_pk_maximum3_f16 v186, v140, v152, v156
	v_pk_maximum3_f16 v196, v189, v190, v178
	v_pk_maximum3_f16 v198, v141, v153, v157
	v_pk_maximum3_f16 v199, v187, v188, v177
	v_pk_maximum3_f16 v200, v184, v194, v169
	s_nop 0
	v_pk_maximum3_f16 v197, v185, v195, v168
	v_pk_maximum3_f16 v201, v142, v154, v158
	v_pk_maximum3_f16 v202, v172, v174, v175
	v_pk_maximum3_f16 v203, v179, v193, v170
	v_pk_maximum3_f16 v204, v143, v155, v159
	v_pk_maximum3_f16 v205, v167, v173, v176
	v_pk_maximum3_f16 v206, v191, v192, v171
	s_nop 0
	v_pk_maximum3_f16 v186, v186, v196, v197
	v_pk_maximum3_f16 v196, v198, v199, v200
	v_pk_maximum3_f16 v197, v201, v202, v203
	s_waitcnt vmcnt(12)
	v_pk_mul_f16 v203, v166, v163 op_sel_hi:[0,1]
	v_pk_maximum3_f16 v198, v204, v205, v206
	v_xor_b32_e32 v197, 0x80008000, v197
	v_xor_b32_e32 v198, 0x80008000, v198
	v_xor_b32_e32 v196, 0x80008000, v196
	v_xor_b32_e32 v186, 0x80008000, v186
	v_pk_add_f16 v140, v140, v186
	v_pk_add_f16 v141, v141, v196
	v_pk_add_f16 v142, v142, v197
	v_pk_add_f16 v143, v143, v198
	v_pk_add_f16 v152, v152, v186
	v_exp_f16_sdwa v199, v140 dst_sel:WORD_0 dst_unused:UNUSED_PAD src0_sel:WORD_0
	v_exp_f16_sdwa v200, v141 dst_sel:WORD_0 dst_unused:UNUSED_PAD src0_sel:WORD_0
	v_exp_f16_sdwa v201, v142 dst_sel:WORD_0 dst_unused:UNUSED_PAD src0_sel:WORD_0
	v_exp_f16_sdwa v202, v143 dst_sel:WORD_0 dst_unused:UNUSED_PAD src0_sel:WORD_0
	v_exp_f16_sdwa v199, v140 dst_sel:WORD_1 dst_unused:UNUSED_PRESERVE src0_sel:WORD_1
	v_exp_f16_sdwa v200, v141 dst_sel:WORD_1 dst_unused:UNUSED_PRESERVE src0_sel:WORD_1
	v_exp_f16_sdwa v201, v142 dst_sel:WORD_1 dst_unused:UNUSED_PRESERVE src0_sel:WORD_1
	v_exp_f16_sdwa v202, v143 dst_sel:WORD_1 dst_unused:UNUSED_PRESERVE src0_sel:WORD_1
	s_nop 0
	v_pk_add_f16 v153, v153, v196
	v_pk_fma_f16 v123, v123, v202, 0
	v_pk_fma_f16 v120, v120, v199, 0
	v_pk_add_f16 v154, v154, v197
	v_pk_add_f16 v155, v155, v198
	v_pk_fma_f16 v122, v122, v201, 0
	v_exp_f16_sdwa v140, v152 dst_sel:WORD_0 dst_unused:UNUSED_PAD src0_sel:WORD_0
	v_exp_f16_sdwa v141, v153 dst_sel:WORD_0 dst_unused:UNUSED_PAD src0_sel:WORD_0
	v_exp_f16_sdwa v142, v154 dst_sel:WORD_0 dst_unused:UNUSED_PAD src0_sel:WORD_0
	v_exp_f16_sdwa v143, v155 dst_sel:WORD_0 dst_unused:UNUSED_PAD src0_sel:WORD_0
	v_exp_f16_sdwa v140, v152 dst_sel:WORD_1 dst_unused:UNUSED_PRESERVE src0_sel:WORD_1
	v_exp_f16_sdwa v141, v153 dst_sel:WORD_1 dst_unused:UNUSED_PRESERVE src0_sel:WORD_1
	v_exp_f16_sdwa v142, v154 dst_sel:WORD_1 dst_unused:UNUSED_PRESERVE src0_sel:WORD_1
	v_exp_f16_sdwa v143, v155 dst_sel:WORD_1 dst_unused:UNUSED_PRESERVE src0_sel:WORD_1
	s_nop 0
	v_pk_fma_f16 v121, v121, v200, 0
	v_pk_fma_f16 v120, v132, v140, v120
	v_pk_fma_f16 v123, v135, v143, v123
	v_pk_add_f16 v135, v159, v198
	v_pk_fma_f16 v121, v133, v141, v121
	v_pk_fma_f16 v122, v134, v142, v122
	v_pk_add_f16 v132, v156, v186
	v_pk_add_f16 v133, v157, v196
	v_pk_add_f16 v134, v158, v197
	v_pk_fma_f16 v204, v39, v163, v203
	v_exp_f16_sdwa v152, v132 dst_sel:WORD_0 dst_unused:UNUSED_PAD src0_sel:WORD_0
	v_exp_f16_sdwa v153, v133 dst_sel:WORD_0 dst_unused:UNUSED_PAD src0_sel:WORD_0
	v_exp_f16_sdwa v154, v134 dst_sel:WORD_0 dst_unused:UNUSED_PAD src0_sel:WORD_0
	v_exp_f16_sdwa v155, v135 dst_sel:WORD_0 dst_unused:UNUSED_PAD src0_sel:WORD_0
	v_exp_f16_sdwa v152, v132 dst_sel:WORD_1 dst_unused:UNUSED_PRESERVE src0_sel:WORD_1
	v_exp_f16_sdwa v153, v133 dst_sel:WORD_1 dst_unused:UNUSED_PRESERVE src0_sel:WORD_1
	v_exp_f16_sdwa v154, v134 dst_sel:WORD_1 dst_unused:UNUSED_PRESERVE src0_sel:WORD_1
	v_exp_f16_sdwa v155, v135 dst_sel:WORD_1 dst_unused:UNUSED_PRESERVE src0_sel:WORD_1
	s_nop 0
	v_pk_mul_f16 v135, v164, v163 op_sel_hi:[0,1]
	v_pk_fma_f16 v120, v144, v152, v120
	v_pk_mul_f16 v144, v165, v163 op_sel_hi:[0,1]
	v_pk_fma_f16 v123, v147, v155, v123
	v_pk_fma_f16 v122, v146, v154, v122
	v_pk_fma_f16 v121, v145, v153, v121
	v_pk_mul_f16 v132, v164, v160 op_sel_hi:[0,1]
	v_pk_mul_f16 v133, v164, v161 op_sel_hi:[0,1]
	v_pk_mul_f16 v134, v164, v162 op_sel_hi:[0,1]
	v_pk_fma_f16 v127, v127, v163, v135
	v_pk_fma_f16 v139, v139, v163, v135
	v_pk_fma_f16 v135, v151, v163, v135
	v_pk_fma_f16 v145, v67, v163, v144
	v_pk_fma_f16 v146, v79, v163, v144
	v_pk_fma_f16 v144, v95, v163, v144
	v_pk_mul_f16 v147, v165, v162 op_sel_hi:[0,1]
	v_pk_fma_f16 v205, v55, v163, v203
	v_pk_fma_f16 v163, v71, v163, v203
	v_pk_mul_f16 v203, v166, v162 op_sel_hi:[0,1]
	v_pk_fma_f16 v126, v126, v162, v134
	v_pk_fma_f16 v125, v125, v161, v133
	v_pk_fma_f16 v124, v124, v160, v132
	v_pk_fma_f16 v138, v138, v162, v134
	v_pk_fma_f16 v137, v137, v161, v133
	v_pk_fma_f16 v136, v136, v160, v132
	v_pk_fma_f16 v134, v150, v162, v134
	v_pk_fma_f16 v133, v149, v161, v133
	v_pk_fma_f16 v132, v148, v160, v132
	v_pk_fma_f16 v148, v66, v162, v147
	v_pk_fma_f16 v149, v78, v162, v147
	v_pk_fma_f16 v147, v94, v162, v147
	v_pk_mul_f16 v150, v165, v161 op_sel_hi:[0,1]
	v_pk_fma_f16 v206, v38, v162, v203
	v_pk_fma_f16 v207, v54, v162, v203
	v_pk_fma_f16 v162, v70, v162, v203
	v_pk_mul_f16 v203, v166, v161 op_sel_hi:[0,1]
	v_pk_fma_f16 v151, v65, v161, v150
	v_pk_fma_f16 v156, v77, v161, v150
	v_pk_fma_f16 v150, v93, v161, v150
	v_pk_mul_f16 v157, v165, v160 op_sel_hi:[0,1]
	v_pk_fma_f16 v208, v37, v161, v203
	v_pk_fma_f16 v209, v53, v161, v203
	v_pk_fma_f16 v161, v69, v161, v203
	v_pk_mul_f16 v203, v166, v160 op_sel_hi:[0,1]
	v_pk_fma_f16 v158, v64, v160, v157
	v_pk_fma_f16 v159, v76, v160, v157
	v_pk_fma_f16 v157, v92, v160, v157
	v_pk_fma_f16 v210, v36, v160, v203
	v_pk_fma_f16 v211, v52, v160, v203
	v_pk_fma_f16 v160, v68, v160, v203
	v_pk_maximum3_f16 v203, v124, v136, v132
	v_pk_maximum3_f16 v212, v158, v159, v157
	v_pk_maximum3_f16 v214, v208, v209, v161
	v_pk_maximum3_f16 v215, v206, v207, v162
	v_pk_maximum3_f16 v216, v204, v205, v163
	s_nop 0
	v_pk_maximum3_f16 v213, v210, v211, v160
	v_pk_add_f16 v189, v189, v186
	v_pk_maximum3_f16 v203, v203, v212, v213
	v_pk_maximum3_f16 v212, v125, v137, v133
	v_pk_maximum3_f16 v213, v151, v156, v150
	v_pk_add_f16 v187, v187, v196
	v_pk_maximum3_f16 v212, v212, v213, v214
	v_pk_maximum3_f16 v213, v126, v138, v134
	v_pk_maximum3_f16 v214, v148, v149, v147
	v_pk_add_f16 v172, v172, v197
	v_pk_maximum3_f16 v213, v213, v214, v215
	v_pk_maximum3_f16 v214, v127, v139, v135
	v_pk_maximum3_f16 v215, v145, v146, v144
	v_pk_add_f16 v167, v167, v198
	v_pk_maximum3_f16 v214, v214, v215, v216
	s_nop 0
	v_exp_f16_sdwa v215, v189 dst_sel:WORD_0 dst_unused:UNUSED_PAD src0_sel:WORD_0
	v_exp_f16_sdwa v216, v187 dst_sel:WORD_0 dst_unused:UNUSED_PAD src0_sel:WORD_0
	v_exp_f16_sdwa v217, v172 dst_sel:WORD_0 dst_unused:UNUSED_PAD src0_sel:WORD_0
	v_exp_f16_sdwa v218, v167 dst_sel:WORD_0 dst_unused:UNUSED_PAD src0_sel:WORD_0
	v_exp_f16_sdwa v215, v189 dst_sel:WORD_1 dst_unused:UNUSED_PRESERVE src0_sel:WORD_1
	v_exp_f16_sdwa v216, v187 dst_sel:WORD_1 dst_unused:UNUSED_PRESERVE src0_sel:WORD_1
	v_exp_f16_sdwa v217, v172 dst_sel:WORD_1 dst_unused:UNUSED_PRESERVE src0_sel:WORD_1
	v_exp_f16_sdwa v218, v167 dst_sel:WORD_1 dst_unused:UNUSED_PRESERVE src0_sel:WORD_1
	s_nop 0
	v_xor_b32_e32 v167, 0x80008000, v214
	v_xor_b32_e32 v172, 0x80008000, v213
	v_xor_b32_e32 v187, 0x80008000, v212
	v_xor_b32_e32 v189, 0x80008000, v203
	v_pk_add_f16 v124, v124, v189
	v_pk_add_f16 v125, v125, v187
	v_pk_add_f16 v126, v126, v172
	v_pk_add_f16 v127, v127, v167
	v_pk_fma_f16 v120, v104, v215, v120
	v_pk_fma_f16 v121, v105, v216, v121
	v_exp_f16_sdwa v203, v124 dst_sel:WORD_0 dst_unused:UNUSED_PAD src0_sel:WORD_0
	v_exp_f16_sdwa v212, v125 dst_sel:WORD_0 dst_unused:UNUSED_PAD src0_sel:WORD_0
	v_exp_f16_sdwa v213, v126 dst_sel:WORD_0 dst_unused:UNUSED_PAD src0_sel:WORD_0
	v_exp_f16_sdwa v214, v127 dst_sel:WORD_0 dst_unused:UNUSED_PAD src0_sel:WORD_0
	v_exp_f16_sdwa v203, v124 dst_sel:WORD_1 dst_unused:UNUSED_PRESERVE src0_sel:WORD_1
	v_exp_f16_sdwa v212, v125 dst_sel:WORD_1 dst_unused:UNUSED_PRESERVE src0_sel:WORD_1
	v_exp_f16_sdwa v213, v126 dst_sel:WORD_1 dst_unused:UNUSED_PRESERVE src0_sel:WORD_1
	v_exp_f16_sdwa v214, v127 dst_sel:WORD_1 dst_unused:UNUSED_PRESERVE src0_sel:WORD_1
	s_nop 0
	v_pk_add_f16 v124, v190, v186
	v_pk_fma_f16 v105, v105, v212, 0
	v_pk_fma_f16 v104, v104, v203, 0
	v_pk_add_f16 v125, v188, v196
	v_pk_add_f16 v126, v174, v197
	v_pk_add_f16 v127, v173, v198
	v_pk_fma_f16 v122, v106, v217, v122
	v_pk_fma_f16 v123, v107, v218, v123
	v_pk_fma_f16 v107, v107, v214, 0
	v_pk_fma_f16 v106, v106, v213, 0
	v_exp_f16_sdwa v173, v124 dst_sel:WORD_0 dst_unused:UNUSED_PAD src0_sel:WORD_0
	v_exp_f16_sdwa v174, v125 dst_sel:WORD_0 dst_unused:UNUSED_PAD src0_sel:WORD_0
	v_exp_f16_sdwa v188, v126 dst_sel:WORD_0 dst_unused:UNUSED_PAD src0_sel:WORD_0
	v_exp_f16_sdwa v190, v127 dst_sel:WORD_0 dst_unused:UNUSED_PAD src0_sel:WORD_0
	v_exp_f16_sdwa v173, v124 dst_sel:WORD_1 dst_unused:UNUSED_PRESERVE src0_sel:WORD_1
	v_exp_f16_sdwa v174, v125 dst_sel:WORD_1 dst_unused:UNUSED_PRESERVE src0_sel:WORD_1
	v_exp_f16_sdwa v188, v126 dst_sel:WORD_1 dst_unused:UNUSED_PRESERVE src0_sel:WORD_1
	v_exp_f16_sdwa v190, v127 dst_sel:WORD_1 dst_unused:UNUSED_PRESERVE src0_sel:WORD_1
	s_nop 0
	v_pk_add_f16 v124, v136, v189
	v_pk_add_f16 v125, v137, v187
	v_pk_add_f16 v126, v138, v172
	v_pk_add_f16 v127, v139, v167
	v_pk_fma_f16 v123, v111, v190, v123
	v_exp_f16_sdwa v136, v124 dst_sel:WORD_0 dst_unused:UNUSED_PAD src0_sel:WORD_0
	v_exp_f16_sdwa v137, v125 dst_sel:WORD_0 dst_unused:UNUSED_PAD src0_sel:WORD_0
	v_exp_f16_sdwa v138, v126 dst_sel:WORD_0 dst_unused:UNUSED_PAD src0_sel:WORD_0
	v_exp_f16_sdwa v139, v127 dst_sel:WORD_0 dst_unused:UNUSED_PAD src0_sel:WORD_0
	v_exp_f16_sdwa v136, v124 dst_sel:WORD_1 dst_unused:UNUSED_PRESERVE src0_sel:WORD_1
	v_exp_f16_sdwa v137, v125 dst_sel:WORD_1 dst_unused:UNUSED_PRESERVE src0_sel:WORD_1
	v_exp_f16_sdwa v138, v126 dst_sel:WORD_1 dst_unused:UNUSED_PRESERVE src0_sel:WORD_1
	v_exp_f16_sdwa v139, v127 dst_sel:WORD_1 dst_unused:UNUSED_PRESERVE src0_sel:WORD_1
	s_nop 0
	v_pk_fma_f16 v122, v110, v188, v122
	v_pk_fma_f16 v219, v108, v136, v104
	v_pk_fma_f16 v220, v109, v137, v105
	v_pk_add_f16 v104, v199, 0
	v_pk_add_f16 v105, v200, 0
	v_pk_fma_f16 v221, v110, v138, v106
	v_pk_fma_f16 v222, v111, v139, v107
	v_pk_add_f16 v104, v104, v140
	v_pk_add_f16 v105, v105, v141
	v_pk_add_f16 v106, v201, 0
	v_pk_add_f16 v107, v202, 0
	v_pk_add_f16 v106, v106, v142
	v_pk_add_f16 v107, v107, v143
	v_pk_add_f16 v105, v105, v153
	v_pk_add_f16 v104, v104, v152
	v_pk_add_f16 v107, v107, v155
	v_pk_add_f16 v106, v106, v154
	v_pk_add_f16 v104, v104, v215
	v_pk_add_f16 v105, v105, v216
	v_pk_add_f16 v106, v106, v217
	v_pk_add_f16 v107, v107, v218
	v_pk_add_f16 v105, v105, v174
	v_pk_add_f16 v104, v104, v173
	v_pk_fma_f16 v121, v109, v174, v121
	v_pk_fma_f16 v120, v108, v173, v120
	v_pk_add_f16 v107, v107, v190
	v_pk_add_f16 v106, v106, v188
	v_pk_add_f16 v108, v178, v186
	v_pk_add_f16 v109, v177, v196
	v_pk_add_f16 v110, v175, v197
	v_pk_add_f16 v111, v176, v198
	v_pk_add_f16 v132, v132, v189
	v_exp_f16_sdwa v124, v108 dst_sel:WORD_0 dst_unused:UNUSED_PAD src0_sel:WORD_0
	v_exp_f16_sdwa v125, v109 dst_sel:WORD_0 dst_unused:UNUSED_PAD src0_sel:WORD_0
	v_exp_f16_sdwa v126, v110 dst_sel:WORD_0 dst_unused:UNUSED_PAD src0_sel:WORD_0
	v_exp_f16_sdwa v127, v111 dst_sel:WORD_0 dst_unused:UNUSED_PAD src0_sel:WORD_0
	v_exp_f16_sdwa v124, v108 dst_sel:WORD_1 dst_unused:UNUSED_PRESERVE src0_sel:WORD_1
	v_exp_f16_sdwa v125, v109 dst_sel:WORD_1 dst_unused:UNUSED_PRESERVE src0_sel:WORD_1
	v_exp_f16_sdwa v126, v110 dst_sel:WORD_1 dst_unused:UNUSED_PRESERVE src0_sel:WORD_1
	v_exp_f16_sdwa v127, v111 dst_sel:WORD_1 dst_unused:UNUSED_PRESERVE src0_sel:WORD_1
	s_nop 0
	v_pk_add_f16 v133, v133, v187
	v_pk_add_f16 v104, v104, v124
	v_pk_add_f16 v105, v105, v125
	v_pk_fma_f16 v108, v88, v124, v120
	v_pk_fma_f16 v109, v89, v125, v121
	v_pk_add_f16 v106, v106, v126
	v_pk_fma_f16 v110, v90, v126, v122
	v_pk_add_f16 v107, v107, v127
	v_pk_fma_f16 v111, v91, v127, v123
	v_pk_add_f16 v120, v185, v186
	v_pk_add_f16 v121, v184, v196
	v_pk_add_f16 v122, v179, v197
	v_pk_add_f16 v123, v191, v198
	v_pk_add_f16 v134, v134, v172
	v_exp_f16_sdwa v124, v120 dst_sel:WORD_0 dst_unused:UNUSED_PAD src0_sel:WORD_0
	v_exp_f16_sdwa v125, v121 dst_sel:WORD_0 dst_unused:UNUSED_PAD src0_sel:WORD_0
	v_exp_f16_sdwa v126, v122 dst_sel:WORD_0 dst_unused:UNUSED_PAD src0_sel:WORD_0
	v_exp_f16_sdwa v127, v123 dst_sel:WORD_0 dst_unused:UNUSED_PAD src0_sel:WORD_0
	v_exp_f16_sdwa v124, v120 dst_sel:WORD_1 dst_unused:UNUSED_PRESERVE src0_sel:WORD_1
	v_exp_f16_sdwa v125, v121 dst_sel:WORD_1 dst_unused:UNUSED_PRESERVE src0_sel:WORD_1
	v_exp_f16_sdwa v126, v122 dst_sel:WORD_1 dst_unused:UNUSED_PRESERVE src0_sel:WORD_1
	v_exp_f16_sdwa v127, v123 dst_sel:WORD_1 dst_unused:UNUSED_PRESERVE src0_sel:WORD_1
	s_nop 0
	v_pk_add_f16 v120, v195, v186
	v_pk_add_f16 v105, v105, v125
	v_pk_add_f16 v104, v104, v124
	v_pk_add_f16 v107, v107, v127
	v_pk_fma_f16 v111, v43, v127, v111
	v_pk_add_f16 v106, v106, v126
	v_pk_fma_f16 v110, v42, v126, v110
	v_pk_fma_f16 v109, v41, v125, v109
	v_pk_fma_f16 v108, v40, v124, v108
	v_pk_add_f16 v121, v194, v196
	v_pk_add_f16 v122, v193, v197
	v_pk_add_f16 v123, v192, v198
	v_pk_add_f16 v135, v135, v167
	v_exp_f16_sdwa v124, v120 dst_sel:WORD_0 dst_unused:UNUSED_PAD src0_sel:WORD_0
	v_exp_f16_sdwa v125, v121 dst_sel:WORD_0 dst_unused:UNUSED_PAD src0_sel:WORD_0
	v_exp_f16_sdwa v126, v122 dst_sel:WORD_0 dst_unused:UNUSED_PAD src0_sel:WORD_0
	v_exp_f16_sdwa v127, v123 dst_sel:WORD_0 dst_unused:UNUSED_PAD src0_sel:WORD_0
	v_exp_f16_sdwa v124, v120 dst_sel:WORD_1 dst_unused:UNUSED_PRESERVE src0_sel:WORD_1
	v_exp_f16_sdwa v125, v121 dst_sel:WORD_1 dst_unused:UNUSED_PRESERVE src0_sel:WORD_1
	v_exp_f16_sdwa v126, v122 dst_sel:WORD_1 dst_unused:UNUSED_PRESERVE src0_sel:WORD_1
	v_exp_f16_sdwa v127, v123 dst_sel:WORD_1 dst_unused:UNUSED_PRESERVE src0_sel:WORD_1
	s_nop 0
	v_pk_add_f16 v120, v168, v186
	v_pk_add_f16 v104, v104, v124
	v_pk_add_f16 v105, v105, v125
	v_pk_fma_f16 v108, v48, v124, v108
	v_pk_fma_f16 v109, v49, v125, v109
	v_pk_add_f16 v106, v106, v126
	v_pk_fma_f16 v110, v50, v126, v110
	v_pk_add_f16 v107, v107, v127
	v_pk_fma_f16 v111, v51, v127, v111
	v_pk_add_f16 v121, v169, v196
	v_pk_add_f16 v122, v170, v197
	v_pk_add_f16 v123, v171, v198
	s_nop 0
	v_exp_f16_sdwa v124, v120 dst_sel:WORD_0 dst_unused:UNUSED_PAD src0_sel:WORD_0
	v_exp_f16_sdwa v125, v121 dst_sel:WORD_0 dst_unused:UNUSED_PAD src0_sel:WORD_0
	v_exp_f16_sdwa v126, v122 dst_sel:WORD_0 dst_unused:UNUSED_PAD src0_sel:WORD_0
	v_exp_f16_sdwa v127, v123 dst_sel:WORD_0 dst_unused:UNUSED_PAD src0_sel:WORD_0
	v_exp_f16_sdwa v124, v120 dst_sel:WORD_1 dst_unused:UNUSED_PRESERVE src0_sel:WORD_1
	v_exp_f16_sdwa v125, v121 dst_sel:WORD_1 dst_unused:UNUSED_PRESERVE src0_sel:WORD_1
	v_exp_f16_sdwa v126, v122 dst_sel:WORD_1 dst_unused:UNUSED_PRESERVE src0_sel:WORD_1
	v_exp_f16_sdwa v127, v123 dst_sel:WORD_1 dst_unused:UNUSED_PRESERVE src0_sel:WORD_1
	s_nop 0
	v_pk_add_f16 v123, v213, 0
	v_pk_add_f16 v105, v105, v125
	v_pk_add_f16 v104, v104, v124
	v_rcp_f16_e32 v121, v105
	v_rcp_f16_e32 v120, v104
	v_rcp_f16_sdwa v104, v104 dst_sel:DWORD dst_unused:UNUSED_PAD src0_sel:WORD_1
	v_rcp_f16_sdwa v105, v105 dst_sel:DWORD dst_unused:UNUSED_PAD src0_sel:WORD_1
	v_pk_add_f16 v107, v107, v127
	v_pk_add_f16 v106, v106, v126
	v_pk_fma_f16 v109, v61, v125, v109
	v_pk_fma_f16 v108, v60, v124, v108
	v_pack_b32_f16 v104, v120, v104
	v_pack_b32_f16 v105, v121, v105
	v_pk_mul_f16 v124, v108, v104
	v_rcp_f16_e32 v108, v106
	v_rcp_f16_sdwa v106, v106 dst_sel:DWORD dst_unused:UNUSED_PAD src0_sel:WORD_1
	v_pk_mul_f16 v125, v109, v105
	v_rcp_f16_e32 v105, v107
	v_rcp_f16_sdwa v107, v107 dst_sel:DWORD dst_unused:UNUSED_PAD src0_sel:WORD_1
	v_pk_fma_f16 v111, v63, v127, v111
	v_pk_fma_f16 v110, v62, v126, v110
	v_pack_b32_f16 v106, v108, v106
	v_pack_b32_f16 v105, v105, v107
	v_add_u32_e32 v104, 0x30000, v183
	v_pk_mul_f16 v126, v110, v106
	v_pk_mul_f16 v127, v111, v105
	v_pk_add_f16 v105, v212, 0
	v_pk_add_f16 v106, v203, 0
	v_add_u32_e32 v120, 0x48000, v183
	v_pk_add_f16 v121, v106, v136
	v_pk_add_f16 v122, v105, v137
	buffer_load_dwordx4 v[108:111], v104, s[8:11], 0 offen
	s_nop 0
	buffer_load_dwordx4 v[104:107], v120, s[8:11], 0 offen
	v_pk_add_f16 v120, v214, 0
	v_pk_add_f16 v123, v123, v138
	v_pk_add_f16 v120, v120, v139
	v_exp_f16_sdwa v136, v132 dst_sel:WORD_0 dst_unused:UNUSED_PAD src0_sel:WORD_0
	v_exp_f16_sdwa v137, v133 dst_sel:WORD_0 dst_unused:UNUSED_PAD src0_sel:WORD_0
	v_exp_f16_sdwa v138, v134 dst_sel:WORD_0 dst_unused:UNUSED_PAD src0_sel:WORD_0
	v_exp_f16_sdwa v139, v135 dst_sel:WORD_0 dst_unused:UNUSED_PAD src0_sel:WORD_0
	v_exp_f16_sdwa v136, v132 dst_sel:WORD_1 dst_unused:UNUSED_PRESERVE src0_sel:WORD_1
	v_exp_f16_sdwa v137, v133 dst_sel:WORD_1 dst_unused:UNUSED_PRESERVE src0_sel:WORD_1
	v_exp_f16_sdwa v138, v134 dst_sel:WORD_1 dst_unused:UNUSED_PRESERVE src0_sel:WORD_1
	v_exp_f16_sdwa v139, v135 dst_sel:WORD_1 dst_unused:UNUSED_PRESERVE src0_sel:WORD_1
	s_nop 0
	v_pk_add_f16 v132, v158, v189
	v_pk_add_f16 v121, v121, v136
	v_pk_add_f16 v120, v120, v139
	v_pk_add_f16 v123, v123, v138
	v_pk_add_f16 v122, v122, v137
	v_pk_fma_f16 v91, v91, v139, v222
	v_pk_fma_f16 v90, v90, v138, v221
	v_pk_fma_f16 v89, v89, v137, v220
	v_pk_fma_f16 v88, v88, v136, v219
	v_pk_add_f16 v133, v151, v187
	v_pk_add_f16 v134, v148, v172
	v_pk_add_f16 v135, v145, v167
	s_nop 0
	v_exp_f16_sdwa v136, v132 dst_sel:WORD_0 dst_unused:UNUSED_PAD src0_sel:WORD_0
	v_exp_f16_sdwa v137, v133 dst_sel:WORD_0 dst_unused:UNUSED_PAD src0_sel:WORD_0
	v_exp_f16_sdwa v138, v134 dst_sel:WORD_0 dst_unused:UNUSED_PAD src0_sel:WORD_0
	v_exp_f16_sdwa v139, v135 dst_sel:WORD_0 dst_unused:UNUSED_PAD src0_sel:WORD_0
	v_exp_f16_sdwa v136, v132 dst_sel:WORD_1 dst_unused:UNUSED_PRESERVE src0_sel:WORD_1
	v_exp_f16_sdwa v137, v133 dst_sel:WORD_1 dst_unused:UNUSED_PRESERVE src0_sel:WORD_1
	v_exp_f16_sdwa v138, v134 dst_sel:WORD_1 dst_unused:UNUSED_PRESERVE src0_sel:WORD_1
	v_exp_f16_sdwa v139, v135 dst_sel:WORD_1 dst_unused:UNUSED_PRESERVE src0_sel:WORD_1
	s_nop 0
	v_pk_add_f16 v132, v159, v189
	v_pk_add_f16 v121, v121, v136
	v_pk_add_f16 v122, v122, v137
	v_pk_add_f16 v123, v123, v138
	v_pk_add_f16 v120, v120, v139
	v_pk_fma_f16 v88, v40, v136, v88
	v_pk_fma_f16 v89, v41, v137, v89
	v_pk_fma_f16 v90, v42, v138, v90
	v_pk_fma_f16 v91, v43, v139, v91
	v_pk_add_f16 v133, v156, v187
	v_pk_add_f16 v134, v149, v172
	v_pk_add_f16 v135, v146, v167
	s_nop 0
	v_exp_f16_sdwa v136, v132 dst_sel:WORD_0 dst_unused:UNUSED_PAD src0_sel:WORD_0
	v_exp_f16_sdwa v137, v133 dst_sel:WORD_0 dst_unused:UNUSED_PAD src0_sel:WORD_0
	v_exp_f16_sdwa v138, v134 dst_sel:WORD_0 dst_unused:UNUSED_PAD src0_sel:WORD_0
	v_exp_f16_sdwa v139, v135 dst_sel:WORD_0 dst_unused:UNUSED_PAD src0_sel:WORD_0
	v_exp_f16_sdwa v136, v132 dst_sel:WORD_1 dst_unused:UNUSED_PRESERVE src0_sel:WORD_1
	v_exp_f16_sdwa v137, v133 dst_sel:WORD_1 dst_unused:UNUSED_PRESERVE src0_sel:WORD_1
	v_exp_f16_sdwa v138, v134 dst_sel:WORD_1 dst_unused:UNUSED_PRESERVE src0_sel:WORD_1
	v_exp_f16_sdwa v139, v135 dst_sel:WORD_1 dst_unused:UNUSED_PRESERVE src0_sel:WORD_1
	s_nop 0
	v_pk_add_f16 v132, v157, v189
	v_pk_add_f16 v121, v121, v136
	v_pk_add_f16 v120, v120, v139
	v_pk_add_f16 v123, v123, v138
	v_pk_add_f16 v122, v122, v137
	v_pk_fma_f16 v91, v51, v139, v91
	v_pk_fma_f16 v90, v50, v138, v90
	v_pk_fma_f16 v89, v49, v137, v89
	v_pk_fma_f16 v88, v48, v136, v88
	v_pk_add_f16 v133, v150, v187
	v_pk_add_f16 v134, v147, v172
	v_pk_add_f16 v135, v144, v167
	s_nop 0
	v_exp_f16_sdwa v136, v132 dst_sel:WORD_0 dst_unused:UNUSED_PAD src0_sel:WORD_0
	v_exp_f16_sdwa v137, v133 dst_sel:WORD_0 dst_unused:UNUSED_PAD src0_sel:WORD_0
	v_exp_f16_sdwa v138, v134 dst_sel:WORD_0 dst_unused:UNUSED_PAD src0_sel:WORD_0
	v_exp_f16_sdwa v139, v135 dst_sel:WORD_0 dst_unused:UNUSED_PAD src0_sel:WORD_0
	v_exp_f16_sdwa v136, v132 dst_sel:WORD_1 dst_unused:UNUSED_PRESERVE src0_sel:WORD_1
	v_exp_f16_sdwa v137, v133 dst_sel:WORD_1 dst_unused:UNUSED_PRESERVE src0_sel:WORD_1
	v_exp_f16_sdwa v138, v134 dst_sel:WORD_1 dst_unused:UNUSED_PRESERVE src0_sel:WORD_1
	v_exp_f16_sdwa v139, v135 dst_sel:WORD_1 dst_unused:UNUSED_PRESERVE src0_sel:WORD_1
	s_nop 0
	v_pk_add_f16 v132, v210, v189
	v_pk_add_f16 v121, v121, v136
	v_pk_add_f16 v122, v122, v137
	v_pk_add_f16 v123, v123, v138
	v_pk_add_f16 v120, v120, v139
	v_pk_fma_f16 v88, v60, v136, v88
	v_pk_fma_f16 v89, v61, v137, v89
	v_pk_fma_f16 v90, v62, v138, v90
	v_pk_fma_f16 v91, v63, v139, v91
	v_pk_add_f16 v133, v208, v187
	v_pk_add_f16 v134, v206, v172
	v_pk_add_f16 v135, v204, v167
	s_nop 0
	v_exp_f16_sdwa v136, v132 dst_sel:WORD_0 dst_unused:UNUSED_PAD src0_sel:WORD_0
	v_exp_f16_sdwa v137, v133 dst_sel:WORD_0 dst_unused:UNUSED_PAD src0_sel:WORD_0
	v_exp_f16_sdwa v138, v134 dst_sel:WORD_0 dst_unused:UNUSED_PAD src0_sel:WORD_0
	v_exp_f16_sdwa v139, v135 dst_sel:WORD_0 dst_unused:UNUSED_PAD src0_sel:WORD_0
	v_exp_f16_sdwa v136, v132 dst_sel:WORD_1 dst_unused:UNUSED_PRESERVE src0_sel:WORD_1
	v_exp_f16_sdwa v137, v133 dst_sel:WORD_1 dst_unused:UNUSED_PRESERVE src0_sel:WORD_1
	v_exp_f16_sdwa v138, v134 dst_sel:WORD_1 dst_unused:UNUSED_PRESERVE src0_sel:WORD_1
	v_exp_f16_sdwa v139, v135 dst_sel:WORD_1 dst_unused:UNUSED_PRESERVE src0_sel:WORD_1
	s_nop 0
	v_pk_add_f16 v132, v211, v189
	v_pk_add_f16 v121, v121, v136
	v_pk_add_f16 v120, v120, v139
	v_pk_add_f16 v123, v123, v138
	v_pk_add_f16 v122, v122, v137
	v_pk_fma_f16 v91, v27, v139, v91
	v_pk_fma_f16 v90, v26, v138, v90
	v_pk_fma_f16 v89, v25, v137, v89
	v_pk_fma_f16 v88, v24, v136, v88
	v_pk_add_f16 v133, v209, v187
	v_pk_add_f16 v134, v207, v172
	v_pk_add_f16 v135, v205, v167
	s_nop 0
	v_exp_f16_sdwa v136, v132 dst_sel:WORD_0 dst_unused:UNUSED_PAD src0_sel:WORD_0
	v_exp_f16_sdwa v137, v133 dst_sel:WORD_0 dst_unused:UNUSED_PAD src0_sel:WORD_0
	v_exp_f16_sdwa v138, v134 dst_sel:WORD_0 dst_unused:UNUSED_PAD src0_sel:WORD_0
	v_exp_f16_sdwa v139, v135 dst_sel:WORD_0 dst_unused:UNUSED_PAD src0_sel:WORD_0
	v_exp_f16_sdwa v136, v132 dst_sel:WORD_1 dst_unused:UNUSED_PRESERVE src0_sel:WORD_1
	v_exp_f16_sdwa v137, v133 dst_sel:WORD_1 dst_unused:UNUSED_PRESERVE src0_sel:WORD_1
	v_exp_f16_sdwa v138, v134 dst_sel:WORD_1 dst_unused:UNUSED_PRESERVE src0_sel:WORD_1
	v_exp_f16_sdwa v139, v135 dst_sel:WORD_1 dst_unused:UNUSED_PRESERVE src0_sel:WORD_1
	s_nop 0
	v_pk_add_f16 v132, v160, v189
	v_pk_add_f16 v121, v121, v136
	v_pk_add_f16 v122, v122, v137
	v_pk_add_f16 v123, v123, v138
	v_pk_add_f16 v120, v120, v139
	v_pk_fma_f16 v88, v28, v136, v88
	v_pk_fma_f16 v89, v29, v137, v89
	v_pk_fma_f16 v90, v30, v138, v90
	v_pk_fma_f16 v91, v31, v139, v91
	v_pk_add_f16 v133, v161, v187
	v_pk_add_f16 v134, v162, v172
	v_pk_add_f16 v135, v163, v167
	s_nop 0
	v_exp_f16_sdwa v136, v132 dst_sel:WORD_0 dst_unused:UNUSED_PAD src0_sel:WORD_0
	v_exp_f16_sdwa v137, v133 dst_sel:WORD_0 dst_unused:UNUSED_PAD src0_sel:WORD_0
	v_exp_f16_sdwa v138, v134 dst_sel:WORD_0 dst_unused:UNUSED_PAD src0_sel:WORD_0
	v_exp_f16_sdwa v139, v135 dst_sel:WORD_0 dst_unused:UNUSED_PAD src0_sel:WORD_0
	v_exp_f16_sdwa v136, v132 dst_sel:WORD_1 dst_unused:UNUSED_PRESERVE src0_sel:WORD_1
	v_exp_f16_sdwa v137, v133 dst_sel:WORD_1 dst_unused:UNUSED_PRESERVE src0_sel:WORD_1
	v_exp_f16_sdwa v138, v134 dst_sel:WORD_1 dst_unused:UNUSED_PRESERVE src0_sel:WORD_1
	v_exp_f16_sdwa v139, v135 dst_sel:WORD_1 dst_unused:UNUSED_PRESERVE src0_sel:WORD_1
	s_nop 0
	s_nop 0
	v_pk_add_f16 v121, v121, v136
	v_pk_add_f16 v120, v120, v139
	v_pk_add_f16 v122, v122, v137
	v_rcp_f16_e32 v132, v121
	v_rcp_f16_sdwa v121, v121 dst_sel:DWORD dst_unused:UNUSED_PAD src0_sel:WORD_1
	v_pk_add_f16 v123, v123, v138
	v_rcp_f16_e32 v133, v122
	v_rcp_f16_sdwa v122, v122 dst_sel:DWORD dst_unused:UNUSED_PAD src0_sel:WORD_1
	v_rcp_f16_e32 v135, v120
	v_rcp_f16_sdwa v120, v120 dst_sel:DWORD dst_unused:UNUSED_PAD src0_sel:WORD_1
	v_rcp_f16_e32 v134, v123
	v_rcp_f16_sdwa v123, v123 dst_sel:DWORD dst_unused:UNUSED_PAD src0_sel:WORD_1
	v_pk_fma_f16 v88, v32, v136, v88
	v_pack_b32_f16 v121, v132, v121
	v_pk_fma_f16 v91, v35, v139, v91
	v_pk_fma_f16 v89, v33, v137, v89
	v_pk_mul_f16 v88, v88, v121
	v_pack_b32_f16 v121, v133, v122
	v_pack_b32_f16 v120, v135, v120
	v_pk_fma_f16 v90, v34, v138, v90
	v_pk_mul_f16 v89, v89, v121
	v_pack_b32_f16 v121, v134, v123
	v_pk_mul_f16 v91, v91, v120
	s_waitcnt vmcnt(1)
	v_pk_mul_f16 v120, v164, v108 op_sel_hi:[0,1]
	v_pk_mul_f16 v123, v164, v111 op_sel_hi:[0,1]
	v_pk_mul_f16 v132, v165, v108 op_sel_hi:[0,1]
	v_pk_mul_f16 v135, v165, v111 op_sel_hi:[0,1]
	v_pk_mul_f16 v136, v166, v108 op_sel_hi:[0,1]
	v_pk_mul_f16 v139, v166, v111 op_sel_hi:[0,1]
	v_pk_mul_f16 v90, v90, v121
	v_pk_mul_f16 v121, v164, v109 op_sel_hi:[0,1]
	v_pk_mul_f16 v122, v164, v110 op_sel_hi:[0,1]
	v_pk_mul_f16 v133, v165, v109 op_sel_hi:[0,1]
	v_pk_mul_f16 v134, v165, v110 op_sel_hi:[0,1]
	v_pk_mul_f16 v137, v166, v109 op_sel_hi:[0,1]
	v_pk_mul_f16 v138, v166, v110 op_sel_hi:[0,1]
	v_pk_fma_f16 v67, v67, v111, v123
	v_pk_fma_f16 v64, v64, v108, v120
	v_pk_fma_f16 v79, v79, v111, v123
	v_pk_fma_f16 v76, v76, v108, v120
	v_pk_fma_f16 v95, v95, v111, v123
	v_pk_fma_f16 v92, v92, v108, v120
	v_pk_fma_f16 v120, v39, v111, v135
	v_pk_fma_f16 v123, v36, v108, v132
	v_pk_fma_f16 v140, v55, v111, v135
	v_pk_fma_f16 v143, v52, v108, v132
	v_pk_fma_f16 v135, v71, v111, v135
	v_pk_fma_f16 v132, v68, v108, v132
	v_pk_fma_f16 v144, v83, v111, v139
	v_pk_fma_f16 v147, v80, v108, v136
	v_pk_fma_f16 v148, v103, v111, v139
	v_pk_fma_f16 v151, v100, v108, v136
	v_pk_fma_f16 v111, v115, v111, v139
	v_pk_fma_f16 v108, v112, v108, v136
	v_pk_maximum3_f16 v136, v64, v76, v92
	v_pk_maximum3_f16 v139, v67, v79, v95
	v_pk_fma_f16 v66, v66, v110, v122
	v_pk_fma_f16 v65, v65, v109, v121
	v_pk_fma_f16 v78, v78, v110, v122
	v_pk_fma_f16 v77, v77, v109, v121
	v_pk_fma_f16 v94, v94, v110, v122
	v_pk_fma_f16 v93, v93, v109, v121
	v_pk_fma_f16 v121, v38, v110, v134
	v_pk_fma_f16 v122, v37, v109, v133
	v_pk_fma_f16 v141, v54, v110, v134
	v_pk_fma_f16 v142, v53, v109, v133
	v_pk_fma_f16 v134, v70, v110, v134
	v_pk_fma_f16 v133, v69, v109, v133
	v_pk_fma_f16 v145, v82, v110, v138
	v_pk_fma_f16 v146, v81, v109, v137
	v_pk_fma_f16 v149, v102, v110, v138
	v_pk_fma_f16 v150, v101, v109, v137
	v_pk_fma_f16 v110, v114, v110, v138
	v_pk_fma_f16 v109, v113, v109, v137
	v_pk_maximum3_f16 v137, v65, v77, v93
	v_pk_maximum3_f16 v138, v66, v78, v94
	v_pk_maximum3_f16 v152, v123, v143, v132
	v_pk_maximum3_f16 v155, v120, v140, v135
	v_pk_maximum3_f16 v156, v147, v151, v108
	v_pk_maximum3_f16 v159, v144, v148, v111
	v_pk_maximum3_f16 v153, v122, v142, v133
	v_pk_maximum3_f16 v154, v121, v141, v134
	s_nop 0
	v_pk_maximum3_f16 v157, v146, v150, v109
	v_pk_maximum3_f16 v158, v145, v149, v110
	v_pk_maximum3_f16 v136, v136, v152, v156
	v_pk_maximum3_f16 v139, v139, v155, v159
	s_nop 0
	v_pk_maximum3_f16 v137, v137, v153, v157
	v_pk_maximum3_f16 v138, v138, v154, v158
	v_xor_b32_e32 v139, 0x80008000, v139
	v_xor_b32_e32 v136, 0x80008000, v136
	v_xor_b32_e32 v138, 0x80008000, v138
	v_xor_b32_e32 v137, 0x80008000, v137
	v_pk_add_f16 v64, v64, v136
	v_pk_add_f16 v67, v67, v139
	v_pk_add_f16 v65, v65, v137
	v_pk_add_f16 v66, v66, v138
	v_pk_add_f16 v76, v76, v136
	v_exp_f16_sdwa v152, v64 dst_sel:WORD_0 dst_unused:UNUSED_PAD src0_sel:WORD_0
	v_exp_f16_sdwa v153, v65 dst_sel:WORD_0 dst_unused:UNUSED_PAD src0_sel:WORD_0
	v_exp_f16_sdwa v154, v66 dst_sel:WORD_0 dst_unused:UNUSED_PAD src0_sel:WORD_0
	v_exp_f16_sdwa v155, v67 dst_sel:WORD_0 dst_unused:UNUSED_PAD src0_sel:WORD_0
	v_exp_f16_sdwa v152, v64 dst_sel:WORD_1 dst_unused:UNUSED_PRESERVE src0_sel:WORD_1
	v_exp_f16_sdwa v153, v65 dst_sel:WORD_1 dst_unused:UNUSED_PRESERVE src0_sel:WORD_1
	v_exp_f16_sdwa v154, v66 dst_sel:WORD_1 dst_unused:UNUSED_PRESERVE src0_sel:WORD_1
	v_exp_f16_sdwa v155, v67 dst_sel:WORD_1 dst_unused:UNUSED_PRESERVE src0_sel:WORD_1
	s_nop 0
	v_pk_add_f16 v77, v77, v137
	v_pk_add_f16 v64, v155, 0
	v_pk_add_f16 v67, v152, 0
	v_pk_fma_f16 v40, v40, v152, 0
	v_pk_fma_f16 v43, v43, v155, 0
	v_pk_add_f16 v65, v154, 0
	v_pk_add_f16 v66, v153, 0
	v_pk_fma_f16 v41, v41, v153, 0
	v_pk_fma_f16 v42, v42, v154, 0
	v_pk_add_f16 v78, v78, v138
	v_pk_add_f16 v79, v79, v139
	s_nop 0
	v_exp_f16_sdwa v152, v76 dst_sel:WORD_0 dst_unused:UNUSED_PAD src0_sel:WORD_0
	v_exp_f16_sdwa v153, v77 dst_sel:WORD_0 dst_unused:UNUSED_PAD src0_sel:WORD_0
	v_exp_f16_sdwa v154, v78 dst_sel:WORD_0 dst_unused:UNUSED_PAD src0_sel:WORD_0
	v_exp_f16_sdwa v155, v79 dst_sel:WORD_0 dst_unused:UNUSED_PAD src0_sel:WORD_0
	v_exp_f16_sdwa v152, v76 dst_sel:WORD_1 dst_unused:UNUSED_PRESERVE src0_sel:WORD_1
	v_exp_f16_sdwa v153, v77 dst_sel:WORD_1 dst_unused:UNUSED_PRESERVE src0_sel:WORD_1
	v_exp_f16_sdwa v154, v78 dst_sel:WORD_1 dst_unused:UNUSED_PRESERVE src0_sel:WORD_1
	v_exp_f16_sdwa v155, v79 dst_sel:WORD_1 dst_unused:UNUSED_PRESERVE src0_sel:WORD_1
	s_nop 0
	s_nop 0
	v_pk_add_f16 v67, v67, v152
	v_pk_add_f16 v64, v64, v155
	v_pk_fma_f16 v43, v51, v155, v43
	v_pk_fma_f16 v40, v48, v152, v40
	v_pk_add_f16 v48, v92, v136
	v_pk_add_f16 v51, v95, v139
	v_pk_add_f16 v66, v66, v153
	v_pk_add_f16 v65, v65, v154
	v_pk_fma_f16 v42, v50, v154, v42
	v_pk_fma_f16 v41, v49, v153, v41
	v_pk_add_f16 v49, v93, v137
	v_pk_add_f16 v50, v94, v138
	s_nop 0
	v_exp_f16_sdwa v76, v48 dst_sel:WORD_0 dst_unused:UNUSED_PAD src0_sel:WORD_0
	v_exp_f16_sdwa v77, v49 dst_sel:WORD_0 dst_unused:UNUSED_PAD src0_sel:WORD_0
	v_exp_f16_sdwa v78, v50 dst_sel:WORD_0 dst_unused:UNUSED_PAD src0_sel:WORD_0
	v_exp_f16_sdwa v79, v51 dst_sel:WORD_0 dst_unused:UNUSED_PAD src0_sel:WORD_0
	v_exp_f16_sdwa v76, v48 dst_sel:WORD_1 dst_unused:UNUSED_PRESERVE src0_sel:WORD_1
	v_exp_f16_sdwa v77, v49 dst_sel:WORD_1 dst_unused:UNUSED_PRESERVE src0_sel:WORD_1
	v_exp_f16_sdwa v78, v50 dst_sel:WORD_1 dst_unused:UNUSED_PRESERVE src0_sel:WORD_1
	v_exp_f16_sdwa v79, v51 dst_sel:WORD_1 dst_unused:UNUSED_PRESERVE src0_sel:WORD_1
	s_nop 0
	s_nop 0
	v_pk_add_f16 v48, v64, v79
	v_pk_add_f16 v51, v67, v76
	v_pk_add_f16 v49, v65, v78
	v_pk_add_f16 v50, v66, v77
	v_pk_fma_f16 v40, v60, v76, v40
	v_pk_fma_f16 v41, v61, v77, v41
	v_pk_fma_f16 v42, v62, v78, v42
	v_pk_fma_f16 v43, v63, v79, v43
	v_pk_add_f16 v60, v123, v136
	v_pk_add_f16 v61, v122, v137
	v_pk_add_f16 v62, v121, v138
	v_pk_add_f16 v63, v120, v139
	s_nop 0
	v_exp_f16_sdwa v64, v60 dst_sel:WORD_0 dst_unused:UNUSED_PAD src0_sel:WORD_0
	v_exp_f16_sdwa v65, v61 dst_sel:WORD_0 dst_unused:UNUSED_PAD src0_sel:WORD_0
	v_exp_f16_sdwa v66, v62 dst_sel:WORD_0 dst_unused:UNUSED_PAD src0_sel:WORD_0
	v_exp_f16_sdwa v67, v63 dst_sel:WORD_0 dst_unused:UNUSED_PAD src0_sel:WORD_0
	v_exp_f16_sdwa v64, v60 dst_sel:WORD_1 dst_unused:UNUSED_PRESERVE src0_sel:WORD_1
	v_exp_f16_sdwa v65, v61 dst_sel:WORD_1 dst_unused:UNUSED_PRESERVE src0_sel:WORD_1
	v_exp_f16_sdwa v66, v62 dst_sel:WORD_1 dst_unused:UNUSED_PRESERVE src0_sel:WORD_1
	v_exp_f16_sdwa v67, v63 dst_sel:WORD_1 dst_unused:UNUSED_PRESERVE src0_sel:WORD_1
	s_nop 0
	v_pk_add_f16 v60, v143, v136
	v_pk_add_f16 v51, v51, v64
	v_pk_add_f16 v48, v48, v67
	v_pk_add_f16 v50, v50, v65
	v_pk_add_f16 v49, v49, v66
	v_pk_fma_f16 v43, v27, v67, v43
	v_pk_fma_f16 v42, v26, v66, v42
	v_pk_fma_f16 v41, v25, v65, v41
	v_pk_fma_f16 v40, v24, v64, v40
	v_pk_add_f16 v61, v142, v137
	v_pk_add_f16 v62, v141, v138
	v_pk_add_f16 v63, v140, v139
	s_nop 0
	v_exp_f16_sdwa v64, v60 dst_sel:WORD_0 dst_unused:UNUSED_PAD src0_sel:WORD_0
	v_exp_f16_sdwa v65, v61 dst_sel:WORD_0 dst_unused:UNUSED_PAD src0_sel:WORD_0
	v_exp_f16_sdwa v66, v62 dst_sel:WORD_0 dst_unused:UNUSED_PAD src0_sel:WORD_0
	v_exp_f16_sdwa v67, v63 dst_sel:WORD_0 dst_unused:UNUSED_PAD src0_sel:WORD_0
	v_exp_f16_sdwa v64, v60 dst_sel:WORD_1 dst_unused:UNUSED_PRESERVE src0_sel:WORD_1
	v_exp_f16_sdwa v65, v61 dst_sel:WORD_1 dst_unused:UNUSED_PRESERVE src0_sel:WORD_1
	v_exp_f16_sdwa v66, v62 dst_sel:WORD_1 dst_unused:UNUSED_PRESERVE src0_sel:WORD_1
	v_exp_f16_sdwa v67, v63 dst_sel:WORD_1 dst_unused:UNUSED_PRESERVE src0_sel:WORD_1
	s_nop 0
	v_pk_add_f16 v60, v132, v136
	v_pk_add_f16 v48, v48, v67
	v_pk_add_f16 v51, v51, v64
	v_pk_add_f16 v49, v49, v66
	v_pk_add_f16 v50, v50, v65
	v_pk_fma_f16 v40, v28, v64, v40
	v_pk_fma_f16 v41, v29, v65, v41
	v_pk_fma_f16 v42, v30, v66, v42
	v_pk_fma_f16 v43, v31, v67, v43
	v_pk_add_f16 v61, v133, v137
	v_pk_add_f16 v62, v134, v138
	v_pk_add_f16 v63, v135, v139
	s_nop 0
	v_exp_f16_sdwa v64, v60 dst_sel:WORD_0 dst_unused:UNUSED_PAD src0_sel:WORD_0
	v_exp_f16_sdwa v65, v61 dst_sel:WORD_0 dst_unused:UNUSED_PAD src0_sel:WORD_0
	v_exp_f16_sdwa v66, v62 dst_sel:WORD_0 dst_unused:UNUSED_PAD src0_sel:WORD_0
	v_exp_f16_sdwa v67, v63 dst_sel:WORD_0 dst_unused:UNUSED_PAD src0_sel:WORD_0
	v_exp_f16_sdwa v64, v60 dst_sel:WORD_1 dst_unused:UNUSED_PRESERVE src0_sel:WORD_1
	v_exp_f16_sdwa v65, v61 dst_sel:WORD_1 dst_unused:UNUSED_PRESERVE src0_sel:WORD_1
	v_exp_f16_sdwa v66, v62 dst_sel:WORD_1 dst_unused:UNUSED_PRESERVE src0_sel:WORD_1
	v_exp_f16_sdwa v67, v63 dst_sel:WORD_1 dst_unused:UNUSED_PRESERVE src0_sel:WORD_1
	s_nop 0
	v_pk_add_f16 v60, v147, v136
	v_pk_add_f16 v51, v51, v64
	v_pk_add_f16 v48, v48, v67
	v_pk_add_f16 v50, v50, v65
	v_pk_add_f16 v49, v49, v66
	v_pk_fma_f16 v43, v35, v67, v43
	v_pk_fma_f16 v42, v34, v66, v42
	v_pk_fma_f16 v41, v33, v65, v41
	v_pk_fma_f16 v40, v32, v64, v40
	v_pk_add_f16 v61, v146, v137
	v_pk_add_f16 v62, v145, v138
	v_pk_add_f16 v63, v144, v139
	s_nop 0
	v_exp_f16_sdwa v64, v60 dst_sel:WORD_0 dst_unused:UNUSED_PAD src0_sel:WORD_0
	v_exp_f16_sdwa v65, v61 dst_sel:WORD_0 dst_unused:UNUSED_PAD src0_sel:WORD_0
	v_exp_f16_sdwa v66, v62 dst_sel:WORD_0 dst_unused:UNUSED_PAD src0_sel:WORD_0
	v_exp_f16_sdwa v67, v63 dst_sel:WORD_0 dst_unused:UNUSED_PAD src0_sel:WORD_0
	v_exp_f16_sdwa v64, v60 dst_sel:WORD_1 dst_unused:UNUSED_PRESERVE src0_sel:WORD_1
	v_exp_f16_sdwa v65, v61 dst_sel:WORD_1 dst_unused:UNUSED_PRESERVE src0_sel:WORD_1
	v_exp_f16_sdwa v66, v62 dst_sel:WORD_1 dst_unused:UNUSED_PRESERVE src0_sel:WORD_1
	v_exp_f16_sdwa v67, v63 dst_sel:WORD_1 dst_unused:UNUSED_PRESERVE src0_sel:WORD_1
	s_nop 0
	v_pk_add_f16 v60, v151, v136
	v_pk_add_f16 v48, v48, v67
	v_pk_add_f16 v51, v51, v64
	v_pk_add_f16 v49, v49, v66
	v_pk_add_f16 v50, v50, v65
	v_pk_fma_f16 v40, v44, v64, v40
	v_pk_fma_f16 v41, v45, v65, v41
	v_pk_fma_f16 v42, v46, v66, v42
	v_pk_fma_f16 v43, v47, v67, v43
	v_pk_add_f16 v61, v150, v137
	v_pk_add_f16 v62, v149, v138
	v_pk_add_f16 v63, v148, v139
	s_nop 0
	v_exp_f16_sdwa v64, v60 dst_sel:WORD_0 dst_unused:UNUSED_PAD src0_sel:WORD_0
	v_exp_f16_sdwa v65, v61 dst_sel:WORD_0 dst_unused:UNUSED_PAD src0_sel:WORD_0
	v_exp_f16_sdwa v66, v62 dst_sel:WORD_0 dst_unused:UNUSED_PAD src0_sel:WORD_0
	v_exp_f16_sdwa v67, v63 dst_sel:WORD_0 dst_unused:UNUSED_PAD src0_sel:WORD_0
	v_exp_f16_sdwa v64, v60 dst_sel:WORD_1 dst_unused:UNUSED_PRESERVE src0_sel:WORD_1
	v_exp_f16_sdwa v65, v61 dst_sel:WORD_1 dst_unused:UNUSED_PRESERVE src0_sel:WORD_1
	v_exp_f16_sdwa v66, v62 dst_sel:WORD_1 dst_unused:UNUSED_PRESERVE src0_sel:WORD_1
	v_exp_f16_sdwa v67, v63 dst_sel:WORD_1 dst_unused:UNUSED_PRESERVE src0_sel:WORD_1
	s_nop 0
	v_pk_add_f16 v60, v108, v136
	v_pk_add_f16 v51, v51, v64
	v_pk_add_f16 v48, v48, v67
	v_pk_add_f16 v50, v50, v65
	v_pk_add_f16 v49, v49, v66
	v_pk_fma_f16 v43, v59, v67, v43
	v_pk_fma_f16 v42, v58, v66, v42
	v_pk_fma_f16 v41, v57, v65, v41
	v_pk_fma_f16 v40, v56, v64, v40
	v_pk_add_f16 v61, v109, v137
	v_pk_add_f16 v62, v110, v138
	v_pk_add_f16 v63, v111, v139
	s_nop 0
	v_exp_f16_sdwa v64, v60 dst_sel:WORD_0 dst_unused:UNUSED_PAD src0_sel:WORD_0
	v_exp_f16_sdwa v65, v61 dst_sel:WORD_0 dst_unused:UNUSED_PAD src0_sel:WORD_0
	v_exp_f16_sdwa v66, v62 dst_sel:WORD_0 dst_unused:UNUSED_PAD src0_sel:WORD_0
	v_exp_f16_sdwa v67, v63 dst_sel:WORD_0 dst_unused:UNUSED_PAD src0_sel:WORD_0
	v_exp_f16_sdwa v64, v60 dst_sel:WORD_1 dst_unused:UNUSED_PRESERVE src0_sel:WORD_1
	v_exp_f16_sdwa v65, v61 dst_sel:WORD_1 dst_unused:UNUSED_PRESERVE src0_sel:WORD_1
	v_exp_f16_sdwa v66, v62 dst_sel:WORD_1 dst_unused:UNUSED_PRESERVE src0_sel:WORD_1
	v_exp_f16_sdwa v67, v63 dst_sel:WORD_1 dst_unused:UNUSED_PRESERVE src0_sel:WORD_1
	s_nop 0
	s_nop 0
	v_pk_add_f16 v48, v48, v67
	v_pk_add_f16 v51, v51, v64
	v_pk_add_f16 v49, v49, v66
	v_rcp_f16_e32 v60, v51
	v_rcp_f16_sdwa v61, v51 dst_sel:DWORD dst_unused:UNUSED_PAD src0_sel:WORD_1
	v_rcp_f16_e32 v51, v48
	v_rcp_f16_sdwa v48, v48 dst_sel:DWORD dst_unused:UNUSED_PAD src0_sel:WORD_1
	v_pk_add_f16 v50, v50, v65
	v_rcp_f16_e32 v63, v49
	v_rcp_f16_sdwa v49, v49 dst_sel:DWORD dst_unused:UNUSED_PAD src0_sel:WORD_1
	v_pk_fma_f16 v40, v72, v64, v40
	v_rcp_f16_e32 v62, v50
	v_rcp_f16_sdwa v64, v50 dst_sel:DWORD dst_unused:UNUSED_PAD src0_sel:WORD_1
	v_pk_fma_f16 v43, v75, v67, v43
	v_pack_b32_f16 v48, v51, v48
	v_pk_fma_f16 v42, v74, v66, v42
	v_pk_mul_f16 v51, v43, v48
	v_pack_b32_f16 v43, v63, v49
	v_pk_fma_f16 v41, v73, v65, v41
	v_pk_mul_f16 v50, v42, v43
	v_pack_b32_f16 v42, v62, v64
	v_pk_mul_f16 v49, v41, v42
	v_pack_b32_f16 v41, v60, v61
	v_pk_mul_f16 v48, v40, v41
	s_waitcnt vmcnt(0)
	v_pk_mul_f16 v40, v164, v104 op_sel_hi:[0,1]
	v_pk_mul_f16 v41, v164, v105 op_sel_hi:[0,1]
	v_pk_mul_f16 v42, v164, v106 op_sel_hi:[0,1]
	v_pk_mul_f16 v43, v164, v107 op_sel_hi:[0,1]
	v_pk_mul_f16 v60, v165, v104 op_sel_hi:[0,1]
	v_pk_mul_f16 v61, v165, v105 op_sel_hi:[0,1]
	v_pk_mul_f16 v62, v165, v106 op_sel_hi:[0,1]
	v_pk_mul_f16 v63, v165, v107 op_sel_hi:[0,1]
	v_pk_mul_f16 v64, v166, v104 op_sel_hi:[0,1]
	v_pk_mul_f16 v65, v166, v105 op_sel_hi:[0,1]
	v_pk_mul_f16 v66, v166, v106 op_sel_hi:[0,1]
	v_pk_mul_f16 v67, v166, v107 op_sel_hi:[0,1]
	v_pk_fma_f16 v39, v39, v107, v43
	v_pk_fma_f16 v38, v38, v106, v42
	v_pk_fma_f16 v37, v37, v105, v41
	v_pk_fma_f16 v36, v36, v104, v40
	v_pk_fma_f16 v55, v55, v107, v43
	v_pk_fma_f16 v54, v54, v106, v42
	v_pk_fma_f16 v53, v53, v105, v41
	v_pk_fma_f16 v52, v52, v104, v40
	v_pk_fma_f16 v43, v71, v107, v43
	v_pk_fma_f16 v42, v70, v106, v42
	v_pk_fma_f16 v41, v69, v105, v41
	v_pk_fma_f16 v40, v68, v104, v40
	v_pk_fma_f16 v68, v83, v107, v63
	v_pk_fma_f16 v69, v82, v106, v62
	v_pk_fma_f16 v70, v81, v105, v61
	v_pk_fma_f16 v71, v80, v104, v60
	v_pk_fma_f16 v80, v119, v107, v67
	v_pk_fma_f16 v81, v118, v106, v66
	v_pk_fma_f16 v82, v117, v105, v65
	v_pk_fma_f16 v83, v116, v104, v64
	v_pk_fma_f16 v92, v131, v107, v67
	v_pk_fma_f16 v93, v130, v106, v66
	v_pk_fma_f16 v94, v129, v105, v65
	v_pk_fma_f16 v95, v128, v104, v64
	v_pk_fma_f16 v23, v23, v107, v67
	v_pk_fma_f16 v22, v22, v106, v66
	v_pk_fma_f16 v21, v21, v105, v65
	v_pk_fma_f16 v20, v20, v104, v64
	v_pk_maximum3_f16 v64, v36, v52, v40
	v_pk_maximum3_f16 v65, v37, v53, v41
	v_pk_maximum3_f16 v66, v38, v54, v42
	v_pk_maximum3_f16 v67, v39, v55, v43
	v_pk_fma_f16 v76, v103, v107, v63
	v_pk_fma_f16 v77, v102, v106, v62
	v_pk_fma_f16 v78, v101, v105, v61
	v_pk_fma_f16 v79, v100, v104, v60
	v_pk_fma_f16 v63, v115, v107, v63
	v_pk_fma_f16 v62, v114, v106, v62
	v_pk_fma_f16 v61, v113, v105, v61
	v_pk_fma_f16 v60, v112, v104, v60
	v_pk_maximum3_f16 v101, v70, v78, v61
	v_pk_maximum3_f16 v102, v69, v77, v62
	v_pk_maximum3_f16 v103, v68, v76, v63
	v_pk_maximum3_f16 v104, v83, v95, v20
	v_pk_maximum3_f16 v105, v82, v94, v21
	s_nop 0
	v_pk_maximum3_f16 v100, v71, v79, v60
	v_pk_maximum3_f16 v106, v81, v93, v22
	v_pk_maximum3_f16 v107, v80, v92, v23
	s_nop 0
	v_pk_maximum3_f16 v64, v64, v100, v104
	v_pk_maximum3_f16 v65, v65, v101, v105
	v_pk_maximum3_f16 v66, v66, v102, v106
	v_pk_maximum3_f16 v67, v67, v103, v107
	s_nop 0
	v_xor_b32_e32 v67, 0x80008000, v67
	v_xor_b32_e32 v66, 0x80008000, v66
	v_xor_b32_e32 v65, 0x80008000, v65
	v_xor_b32_e32 v64, 0x80008000, v64
	v_pk_add_f16 v36, v36, v64
	v_pk_add_f16 v37, v37, v65
	v_pk_add_f16 v38, v38, v66
	v_pk_add_f16 v39, v39, v67
	v_pk_add_f16 v52, v52, v64
	v_exp_f16_sdwa v100, v36 dst_sel:WORD_0 dst_unused:UNUSED_PAD src0_sel:WORD_0
	v_exp_f16_sdwa v101, v37 dst_sel:WORD_0 dst_unused:UNUSED_PAD src0_sel:WORD_0
	v_exp_f16_sdwa v102, v38 dst_sel:WORD_0 dst_unused:UNUSED_PAD src0_sel:WORD_0
	v_exp_f16_sdwa v103, v39 dst_sel:WORD_0 dst_unused:UNUSED_PAD src0_sel:WORD_0
	v_exp_f16_sdwa v100, v36 dst_sel:WORD_1 dst_unused:UNUSED_PRESERVE src0_sel:WORD_1
	v_exp_f16_sdwa v101, v37 dst_sel:WORD_1 dst_unused:UNUSED_PRESERVE src0_sel:WORD_1
	v_exp_f16_sdwa v102, v38 dst_sel:WORD_1 dst_unused:UNUSED_PRESERVE src0_sel:WORD_1
	v_exp_f16_sdwa v103, v39 dst_sel:WORD_1 dst_unused:UNUSED_PRESERVE src0_sel:WORD_1
	s_nop 0
	v_pk_add_f16 v53, v53, v65
	v_pk_add_f16 v36, v100, 0
	v_pk_add_f16 v37, v101, 0
	v_pk_add_f16 v38, v102, 0
	v_pk_add_f16 v39, v103, 0
	v_pk_fma_f16 v24, v24, v100, 0
	v_pk_fma_f16 v25, v25, v101, 0
	v_pk_fma_f16 v26, v26, v102, 0
	v_pk_fma_f16 v27, v27, v103, 0
	v_pk_add_f16 v54, v54, v66
	v_pk_add_f16 v55, v55, v67
	v_pk_add_f16 v20, v20, v64
	v_exp_f16_sdwa v100, v52 dst_sel:WORD_0 dst_unused:UNUSED_PAD src0_sel:WORD_0
	v_exp_f16_sdwa v101, v53 dst_sel:WORD_0 dst_unused:UNUSED_PAD src0_sel:WORD_0
	v_exp_f16_sdwa v102, v54 dst_sel:WORD_0 dst_unused:UNUSED_PAD src0_sel:WORD_0
	v_exp_f16_sdwa v103, v55 dst_sel:WORD_0 dst_unused:UNUSED_PAD src0_sel:WORD_0
	v_exp_f16_sdwa v100, v52 dst_sel:WORD_1 dst_unused:UNUSED_PRESERVE src0_sel:WORD_1
	v_exp_f16_sdwa v101, v53 dst_sel:WORD_1 dst_unused:UNUSED_PRESERVE src0_sel:WORD_1
	v_exp_f16_sdwa v102, v54 dst_sel:WORD_1 dst_unused:UNUSED_PRESERVE src0_sel:WORD_1
	v_exp_f16_sdwa v103, v55 dst_sel:WORD_1 dst_unused:UNUSED_PRESERVE src0_sel:WORD_1
	s_nop 0
	v_pk_add_f16 v21, v21, v65
	v_pk_add_f16 v39, v39, v103
	v_pk_add_f16 v38, v38, v102
	v_pk_add_f16 v37, v37, v101
	v_pk_add_f16 v36, v36, v100
	v_pk_fma_f16 v27, v31, v103, v27
	v_pk_fma_f16 v26, v30, v102, v26
	v_pk_fma_f16 v25, v29, v101, v25
	v_pk_fma_f16 v24, v28, v100, v24
	v_pk_add_f16 v28, v40, v64
	v_pk_add_f16 v29, v41, v65
	v_pk_add_f16 v30, v42, v66
	v_pk_add_f16 v31, v43, v67
	v_pk_add_f16 v22, v22, v66
	v_exp_f16_sdwa v40, v28 dst_sel:WORD_0 dst_unused:UNUSED_PAD src0_sel:WORD_0
	v_exp_f16_sdwa v41, v29 dst_sel:WORD_0 dst_unused:UNUSED_PAD src0_sel:WORD_0
	v_exp_f16_sdwa v42, v30 dst_sel:WORD_0 dst_unused:UNUSED_PAD src0_sel:WORD_0
	v_exp_f16_sdwa v43, v31 dst_sel:WORD_0 dst_unused:UNUSED_PAD src0_sel:WORD_0
	v_exp_f16_sdwa v40, v28 dst_sel:WORD_1 dst_unused:UNUSED_PRESERVE src0_sel:WORD_1
	v_exp_f16_sdwa v41, v29 dst_sel:WORD_1 dst_unused:UNUSED_PRESERVE src0_sel:WORD_1
	v_exp_f16_sdwa v42, v30 dst_sel:WORD_1 dst_unused:UNUSED_PRESERVE src0_sel:WORD_1
	v_exp_f16_sdwa v43, v31 dst_sel:WORD_1 dst_unused:UNUSED_PRESERVE src0_sel:WORD_1
	s_nop 0
	v_pk_add_f16 v23, v23, v67
	v_pk_add_f16 v28, v36, v40
	v_pk_add_f16 v29, v37, v41
	v_pk_add_f16 v30, v38, v42
	v_pk_add_f16 v31, v39, v43
	v_pk_fma_f16 v24, v32, v40, v24
	v_pk_fma_f16 v25, v33, v41, v25
	v_pk_fma_f16 v26, v34, v42, v26
	v_pk_fma_f16 v27, v35, v43, v27
	v_pk_add_f16 v32, v71, v64
	v_pk_add_f16 v33, v70, v65
	v_pk_add_f16 v34, v69, v66
	v_pk_add_f16 v35, v68, v67
	s_nop 0
	v_exp_f16_sdwa v36, v32 dst_sel:WORD_0 dst_unused:UNUSED_PAD src0_sel:WORD_0
	v_exp_f16_sdwa v37, v33 dst_sel:WORD_0 dst_unused:UNUSED_PAD src0_sel:WORD_0
	v_exp_f16_sdwa v38, v34 dst_sel:WORD_0 dst_unused:UNUSED_PAD src0_sel:WORD_0
	v_exp_f16_sdwa v39, v35 dst_sel:WORD_0 dst_unused:UNUSED_PAD src0_sel:WORD_0
	v_exp_f16_sdwa v36, v32 dst_sel:WORD_1 dst_unused:UNUSED_PRESERVE src0_sel:WORD_1
	v_exp_f16_sdwa v37, v33 dst_sel:WORD_1 dst_unused:UNUSED_PRESERVE src0_sel:WORD_1
	v_exp_f16_sdwa v38, v34 dst_sel:WORD_1 dst_unused:UNUSED_PRESERVE src0_sel:WORD_1
	v_exp_f16_sdwa v39, v35 dst_sel:WORD_1 dst_unused:UNUSED_PRESERVE src0_sel:WORD_1
	s_nop 0
	v_pk_add_f16 v32, v79, v64
	v_pk_add_f16 v31, v31, v39
	v_pk_add_f16 v30, v30, v38
	v_pk_add_f16 v29, v29, v37
	v_pk_add_f16 v28, v28, v36
	v_pk_fma_f16 v27, v47, v39, v27
	v_pk_fma_f16 v26, v46, v38, v26
	v_pk_fma_f16 v25, v45, v37, v25
	v_pk_fma_f16 v24, v44, v36, v24
	v_pk_add_f16 v33, v78, v65
	v_pk_add_f16 v34, v77, v66
	v_pk_add_f16 v35, v76, v67
	s_nop 0
	v_exp_f16_sdwa v36, v32 dst_sel:WORD_0 dst_unused:UNUSED_PAD src0_sel:WORD_0
	v_exp_f16_sdwa v37, v33 dst_sel:WORD_0 dst_unused:UNUSED_PAD src0_sel:WORD_0
	v_exp_f16_sdwa v38, v34 dst_sel:WORD_0 dst_unused:UNUSED_PAD src0_sel:WORD_0
	v_exp_f16_sdwa v39, v35 dst_sel:WORD_0 dst_unused:UNUSED_PAD src0_sel:WORD_0
	v_exp_f16_sdwa v36, v32 dst_sel:WORD_1 dst_unused:UNUSED_PRESERVE src0_sel:WORD_1
	v_exp_f16_sdwa v37, v33 dst_sel:WORD_1 dst_unused:UNUSED_PRESERVE src0_sel:WORD_1
	v_exp_f16_sdwa v38, v34 dst_sel:WORD_1 dst_unused:UNUSED_PRESERVE src0_sel:WORD_1
	v_exp_f16_sdwa v39, v35 dst_sel:WORD_1 dst_unused:UNUSED_PRESERVE src0_sel:WORD_1
	s_nop 0
	v_pk_add_f16 v32, v60, v64
	v_pk_add_f16 v28, v28, v36
	v_pk_add_f16 v29, v29, v37
	v_pk_add_f16 v30, v30, v38
	v_pk_add_f16 v31, v31, v39
	v_pk_fma_f16 v24, v56, v36, v24
	v_pk_fma_f16 v25, v57, v37, v25
	v_pk_fma_f16 v26, v58, v38, v26
	v_pk_fma_f16 v27, v59, v39, v27
	v_pk_add_f16 v33, v61, v65
	v_pk_add_f16 v34, v62, v66
	v_pk_add_f16 v35, v63, v67
	s_nop 0
	v_exp_f16_sdwa v36, v32 dst_sel:WORD_0 dst_unused:UNUSED_PAD src0_sel:WORD_0
	v_exp_f16_sdwa v37, v33 dst_sel:WORD_0 dst_unused:UNUSED_PAD src0_sel:WORD_0
	v_exp_f16_sdwa v38, v34 dst_sel:WORD_0 dst_unused:UNUSED_PAD src0_sel:WORD_0
	v_exp_f16_sdwa v39, v35 dst_sel:WORD_0 dst_unused:UNUSED_PAD src0_sel:WORD_0
	v_exp_f16_sdwa v36, v32 dst_sel:WORD_1 dst_unused:UNUSED_PRESERVE src0_sel:WORD_1
	v_exp_f16_sdwa v37, v33 dst_sel:WORD_1 dst_unused:UNUSED_PRESERVE src0_sel:WORD_1
	v_exp_f16_sdwa v38, v34 dst_sel:WORD_1 dst_unused:UNUSED_PRESERVE src0_sel:WORD_1
	v_exp_f16_sdwa v39, v35 dst_sel:WORD_1 dst_unused:UNUSED_PRESERVE src0_sel:WORD_1
	s_nop 0
	v_pk_add_f16 v32, v83, v64
	v_pk_add_f16 v31, v31, v39
	v_pk_add_f16 v30, v30, v38
	v_pk_add_f16 v29, v29, v37
	v_pk_add_f16 v28, v28, v36
	v_pk_fma_f16 v27, v75, v39, v27
	v_pk_fma_f16 v26, v74, v38, v26
	v_pk_fma_f16 v25, v73, v37, v25
	v_pk_fma_f16 v24, v72, v36, v24
	v_pk_add_f16 v33, v82, v65
	v_pk_add_f16 v34, v81, v66
	v_pk_add_f16 v35, v80, v67
	s_nop 0
	v_exp_f16_sdwa v36, v32 dst_sel:WORD_0 dst_unused:UNUSED_PAD src0_sel:WORD_0
	v_exp_f16_sdwa v37, v33 dst_sel:WORD_0 dst_unused:UNUSED_PAD src0_sel:WORD_0
	v_exp_f16_sdwa v38, v34 dst_sel:WORD_0 dst_unused:UNUSED_PAD src0_sel:WORD_0
	v_exp_f16_sdwa v39, v35 dst_sel:WORD_0 dst_unused:UNUSED_PAD src0_sel:WORD_0
	v_exp_f16_sdwa v36, v32 dst_sel:WORD_1 dst_unused:UNUSED_PRESERVE src0_sel:WORD_1
	v_exp_f16_sdwa v37, v33 dst_sel:WORD_1 dst_unused:UNUSED_PRESERVE src0_sel:WORD_1
	v_exp_f16_sdwa v38, v34 dst_sel:WORD_1 dst_unused:UNUSED_PRESERVE src0_sel:WORD_1
	v_exp_f16_sdwa v39, v35 dst_sel:WORD_1 dst_unused:UNUSED_PRESERVE src0_sel:WORD_1
	s_nop 0
	v_pk_add_f16 v32, v95, v64
	v_pk_add_f16 v28, v28, v36
	v_pk_add_f16 v29, v29, v37
	v_pk_add_f16 v30, v30, v38
	v_pk_add_f16 v31, v31, v39
	v_pk_fma_f16 v24, v84, v36, v24
	v_pk_fma_f16 v25, v85, v37, v25
	v_pk_fma_f16 v26, v86, v38, v26
	v_pk_fma_f16 v27, v87, v39, v27
	v_pk_add_f16 v33, v94, v65
	v_pk_add_f16 v34, v93, v66
	v_pk_add_f16 v35, v92, v67
	s_nop 0
	v_exp_f16_sdwa v36, v32 dst_sel:WORD_0 dst_unused:UNUSED_PAD src0_sel:WORD_0
	v_exp_f16_sdwa v37, v33 dst_sel:WORD_0 dst_unused:UNUSED_PAD src0_sel:WORD_0
	v_exp_f16_sdwa v38, v34 dst_sel:WORD_0 dst_unused:UNUSED_PAD src0_sel:WORD_0
	v_exp_f16_sdwa v39, v35 dst_sel:WORD_0 dst_unused:UNUSED_PAD src0_sel:WORD_0
	v_exp_f16_sdwa v36, v32 dst_sel:WORD_1 dst_unused:UNUSED_PRESERVE src0_sel:WORD_1
	v_exp_f16_sdwa v37, v33 dst_sel:WORD_1 dst_unused:UNUSED_PRESERVE src0_sel:WORD_1
	v_exp_f16_sdwa v38, v34 dst_sel:WORD_1 dst_unused:UNUSED_PRESERVE src0_sel:WORD_1
	v_exp_f16_sdwa v39, v35 dst_sel:WORD_1 dst_unused:UNUSED_PRESERVE src0_sel:WORD_1
	s_nop 0
	s_nop 0
	v_pk_add_f16 v31, v31, v39
	v_pk_add_f16 v30, v30, v38
	v_pk_add_f16 v29, v29, v37
	v_pk_add_f16 v28, v28, v36
	v_pk_fma_f16 v35, v99, v39, v27
	v_pk_fma_f16 v34, v98, v38, v26
	v_pk_fma_f16 v33, v97, v37, v25
	v_pk_fma_f16 v32, v96, v36, v24
	v_exp_f16_sdwa v36, v20 dst_sel:WORD_0 dst_unused:UNUSED_PAD src0_sel:WORD_0
	v_exp_f16_sdwa v37, v21 dst_sel:WORD_0 dst_unused:UNUSED_PAD src0_sel:WORD_0
	v_exp_f16_sdwa v38, v22 dst_sel:WORD_0 dst_unused:UNUSED_PAD src0_sel:WORD_0
	v_exp_f16_sdwa v39, v23 dst_sel:WORD_0 dst_unused:UNUSED_PAD src0_sel:WORD_0
	v_exp_f16_sdwa v36, v20 dst_sel:WORD_1 dst_unused:UNUSED_PRESERVE src0_sel:WORD_1
	v_exp_f16_sdwa v37, v21 dst_sel:WORD_1 dst_unused:UNUSED_PRESERVE src0_sel:WORD_1
	v_exp_f16_sdwa v38, v22 dst_sel:WORD_1 dst_unused:UNUSED_PRESERVE src0_sel:WORD_1
	v_exp_f16_sdwa v39, v23 dst_sel:WORD_1 dst_unused:UNUSED_PRESERVE src0_sel:WORD_1
	s_nop 0
	v_mov_b32_e32 v27, v19
	v_mov_b32_e32 v26, v18
	v_mov_b32_e32 v25, v17
	v_mov_b32_e32 v24, v16

	.amdhsa_kernel _Z7k_attn2ILi2EEv8AttnArgs
		.amdhsa_group_segment_fixed_size 0
		.amdhsa_private_segment_fixed_size 0
		.amdhsa_kernarg_size 112
		.amdhsa_user_sgpr_count 2
		.amdhsa_user_sgpr_dispatch_ptr 0
		.amdhsa_user_sgpr_queue_ptr 0
		.amdhsa_user_sgpr_kernarg_segment_ptr 1
		.amdhsa_user_sgpr_dispatch_id 0
		.amdhsa_user_sgpr_kernarg_preload_length 0
		.amdhsa_user_sgpr_kernarg_preload_offset 0
		.amdhsa_user_sgpr_private_segment_size 0
		.amdhsa_uses_dynamic_stack 0
		.amdhsa_enable_private_segment 0
		.amdhsa_system_sgpr_workgroup_id_x 1
		.amdhsa_system_sgpr_workgroup_id_y 0
		.amdhsa_system_sgpr_workgroup_id_z 0
		.amdhsa_system_sgpr_workgroup_info 0
		.amdhsa_system_vgpr_workitem_id 0
		.amdhsa_next_free_vgpr 228
		.amdhsa_next_free_sgpr 80
		.amdhsa_accum_offset 228
		.amdhsa_reserve_vcc 1
		.amdhsa_float_round_mode_32 0
		.amdhsa_float_round_mode_16_64 0
		.amdhsa_float_denorm_mode_32 3
		.amdhsa_float_denorm_mode_16_64 3
		.amdhsa_dx10_clamp 1
		.amdhsa_ieee_mode 1
		.amdhsa_fp16_overflow 0
		.amdhsa_tg_split 0
		.amdhsa_exception_fp_ieee_invalid_op 0
		.amdhsa_exception_fp_denorm_src 0
		.amdhsa_exception_fp_ieee_div_zero 0
		.amdhsa_exception_fp_ieee_overflow 0
		.amdhsa_exception_fp_ieee_underflow 0
		.amdhsa_exception_fp_ieee_inexact 0
		.amdhsa_exception_int_div_zero 0
	.end_amdhsa_kernel

	.text
	.p2alignl 8, 3212836864
	.fill 256, 4, 3212836864

amdhsa.kernels:
  - .agpr_count:     0
    .args:
      - .actual_access:  read_only
        .address_space:  global
        .offset:         0
        .size:           8
        .value_kind:     global_buffer
      - .actual_access:  read_only
        .address_space:  global
        .offset:         8
        .size:           8
        .value_kind:     global_buffer
      - .actual_access:  read_only
        .address_space:  global
        .offset:         16
        .size:           8
        .value_kind:     global_buffer
      - .actual_access:  read_only
        .address_space:  global
        .offset:         24
        .size:           8
        .value_kind:     global_buffer
      - .actual_access:  read_only
        .address_space:  global
        .offset:         32
        .size:           8
        .value_kind:     global_buffer
      - .actual_access:  read_only
        .address_space:  global
        .offset:         40
        .size:           8
        .value_kind:     global_buffer
      - .actual_access:  read_only
        .address_space:  global
        .offset:         48
        .size:           8
        .value_kind:     global_buffer
      - .actual_access:  read_only
        .address_space:  global
        .offset:         56
        .size:           8
        .value_kind:     global_buffer
      - .actual_access:  write_only
        .address_space:  global
        .offset:         64
        .size:           8
        .value_kind:     global_buffer
      - .actual_access:  write_only
        .address_space:  global
        .offset:         72
        .size:           8
        .value_kind:     global_buffer
      - .actual_access:  write_only
        .address_space:  global
        .offset:         80
        .size:           8
        .value_kind:     global_buffer
      - .actual_access:  write_only
        .address_space:  global
        .offset:         88
        .size:           8
        .value_kind:     global_buffer
    .group_segment_fixed_size: 0
    .kernarg_segment_align: 8
    .kernarg_segment_size: 96
    .language:       OpenCL C
    .language_version:
      - 2
      - 0
    .max_flat_workgroup_size: 256
    .name:           _Z8k_prep_wPKfS0_S0_S0_S0_S0_S0_S0_PDF16_PfS1_S1_
    .private_segment_fixed_size: 0
    .sgpr_count:     23
    .sgpr_spill_count: 0
    .symbol:         _Z8k_prep_wPKfS0_S0_S0_S0_S0_S0_S0_PDF16_PfS1_S1_.kd
    .uniform_work_group_size: 1
    .uses_dynamic_stack: false
    .vgpr_count:     15
    .vgpr_spill_count: 0
    .wavefront_size: 64
  - .agpr_count:     0
    .args:
      - .actual_access:  read_only
        .address_space:  global
        .offset:         0
        .size:           8
        .value_kind:     global_buffer
      - .actual_access:  read_only
        .address_space:  global
        .offset:         8
        .size:           8
        .value_kind:     global_buffer
      - .actual_access:  read_only
        .address_space:  global
        .offset:         16
        .size:           8
        .value_kind:     global_buffer
      - .actual_access:  read_only
        .address_space:  global
        .offset:         24
        .size:           8
        .value_kind:     global_buffer
      - .actual_access:  write_only
        .address_space:  global
        .offset:         32
        .size:           8
        .value_kind:     global_buffer
      - .actual_access:  read_only
        .address_space:  global
        .offset:         40
        .size:           8
        .value_kind:     global_buffer
      - .actual_access:  read_only
        .address_space:  global
        .offset:         48
        .size:           8
        .value_kind:     global_buffer
      - .actual_access:  write_only
        .address_space:  global
        .offset:         56
        .size:           8
        .value_kind:     global_buffer
      - .offset:         64
        .size:           4
        .value_kind:     by_value
      - .offset:         68
        .size:           4
        .value_kind:     by_value
    .group_segment_fixed_size: 115712
    .kernarg_segment_align: 8
    .kernarg_segment_size: 72
    .language:       OpenCL C
    .language_version:
      - 2
      - 0
    .max_flat_workgroup_size: 512
    .name:           _Z8k_stageAPKfS0_S0_S0_PDF16_PKDF16_S0_S1_ii
    .private_segment_fixed_size: 0
    .sgpr_count:     28
    .sgpr_spill_count: 0
    .symbol:         _Z8k_stageAPKfS0_S0_S0_PDF16_PKDF16_S0_S1_ii.kd
    .uniform_work_group_size: 1
    .uses_dynamic_stack: false
    .vgpr_count:     251
    .vgpr_spill_count: 0
    .wavefront_size: 64
  - .agpr_count:     112
    .args:
      - .actual_access:  read_only
        .address_space:  global
        .offset:         0
        .size:           8
        .value_kind:     global_buffer
      - .actual_access:  read_only
        .address_space:  global
        .offset:         8
        .size:           8
        .value_kind:     global_buffer
      - .actual_access:  read_only
        .address_space:  global
        .offset:         16
        .size:           8
        .value_kind:     global_buffer
      - .actual_access:  read_only
        .address_space:  global
        .offset:         24
        .size:           8
        .value_kind:     global_buffer
      - .actual_access:  read_only
        .address_space:  global
        .offset:         32
        .size:           8
        .value_kind:     global_buffer
      - .actual_access:  write_only
        .address_space:  global
        .offset:         40
        .size:           8
        .value_kind:     global_buffer
    .group_segment_fixed_size: 107712
    .kernarg_segment_align: 8
    .kernarg_segment_size: 48
    .language:       OpenCL C
    .language_version:
      - 2
      - 0
    .max_flat_workgroup_size: 256
    .name:           _Z7k_conv4PKDF16_S0_S0_PKfS2_Pf
    .private_segment_fixed_size: 0
    .sgpr_count:     36
    .sgpr_spill_count: 0
    .symbol:         _Z7k_conv4PKDF16_S0_S0_PKfS2_Pf.kd
    .uniform_work_group_size: 1
    .uses_dynamic_stack: false
    .vgpr_count:     328
    .vgpr_spill_count: 0
    .wavefront_size: 64
  - .agpr_count:     0
    .args:
      - .offset:         0
        .size:           112
        .value_kind:     by_value
      - .actual_access:  read_only
        .address_space:  global
        .offset:         112
        .size:           8
        .value_kind:     global_buffer
      - .actual_access:  read_only
        .address_space:  global
        .offset:         120
        .size:           8
        .value_kind:     global_buffer
      - .actual_access:  write_only
        .address_space:  global
        .offset:         128
        .size:           8
        .value_kind:     global_buffer
      - .offset:         136
        .size:           4
        .value_kind:     by_value
      - .offset:         140
        .size:           4
        .value_kind:     by_value
      - .offset:         144
        .size:           4
        .value_kind:     by_value
    .group_segment_fixed_size: 115712
    .kernarg_segment_align: 8
    .kernarg_segment_size: 148
    .language:       OpenCL C
    .language_version:
      - 2
      - 0
    .max_flat_workgroup_size: 512
    .name:           _Z7k_stageILi0ELi8EEv8AttnArgsPKDF16_PKfPDF16_iii
    .private_segment_fixed_size: 0
    .sgpr_count:     41
    .sgpr_spill_count: 0
    .symbol:         _Z7k_stageILi0ELi8EEv8AttnArgsPKDF16_PKfPDF16_iii.kd
    .uniform_work_group_size: 1
    .uses_dynamic_stack: false
    .vgpr_count:     251
    .vgpr_spill_count: 0
    .wavefront_size: 64
  - .agpr_count:     0
    .args:
      - .offset:         0
        .size:           112
        .value_kind:     by_value
      - .actual_access:  read_only
        .address_space:  global
        .offset:         112
        .size:           8
        .value_kind:     global_buffer
      - .actual_access:  read_only
        .address_space:  global
        .offset:         120
        .size:           8
        .value_kind:     global_buffer
      - .actual_access:  write_only
        .address_space:  global
        .offset:         128
        .size:           8
        .value_kind:     global_buffer
      - .offset:         136
        .size:           4
        .value_kind:     by_value
      - .offset:         140
        .size:           4
        .value_kind:     by_value
      - .offset:         144
        .size:           4
        .value_kind:     by_value
    .group_segment_fixed_size: 82944
    .kernarg_segment_align: 8
    .kernarg_segment_size: 148
    .language:       OpenCL C
    .language_version:
      - 2
      - 0
    .max_flat_workgroup_size: 512
    .name:           _Z7k_stageILi1ELi4EEv8AttnArgsPKDF16_PKfPDF16_iii
    .private_segment_fixed_size: 0
    .sgpr_count:     55
    .sgpr_spill_count: 0
    .symbol:         _Z7k_stageILi1ELi4EEv8AttnArgsPKDF16_PKfPDF16_iii.kd
    .uniform_work_group_size: 1
    .uses_dynamic_stack: false
    .vgpr_count:     247
    .vgpr_spill_count: 0
    .wavefront_size: 64
  - .agpr_count:     0
    .args:
      - .offset:         0
        .size:           112
        .value_kind:     by_value
      - .actual_access:  read_only
        .address_space:  global
        .offset:         112
        .size:           8
        .value_kind:     global_buffer
      - .actual_access:  read_only
        .address_space:  global
        .offset:         120
        .size:           8
        .value_kind:     global_buffer
      - .actual_access:  write_only
        .address_space:  global
        .offset:         128
        .size:           8
        .value_kind:     global_buffer
      - .offset:         136
        .size:           4
        .value_kind:     by_value
      - .offset:         140
        .size:           4
        .value_kind:     by_value
      - .offset:         144
        .size:           4
        .value_kind:     by_value
    .group_segment_fixed_size: 82944
    .kernarg_segment_align: 8
    .kernarg_segment_size: 148
    .language:       OpenCL C
    .language_version:
      - 2
      - 0
    .max_flat_workgroup_size: 512
    .name:           _Z7k_stageILi0ELi4EEv8AttnArgsPKDF16_PKfPDF16_iii
    .private_segment_fixed_size: 0
    .sgpr_count:     38
    .sgpr_spill_count: 0
    .symbol:         _Z7k_stageILi0ELi4EEv8AttnArgsPKDF16_PKfPDF16_iii.kd
    .uniform_work_group_size: 1
    .uses_dynamic_stack: false
    .vgpr_count:     224
    .vgpr_spill_count: 0
    .wavefront_size: 64
  - .agpr_count:     0
    .args:
      - .offset:         0
        .size:           112
        .value_kind:     by_value
    .group_segment_fixed_size: 0
    .kernarg_segment_align: 8
    .kernarg_segment_size: 112
    .language:       OpenCL C
    .language_version:
      - 2
      - 0
    .max_flat_workgroup_size: 512
    .name:           _Z7k_attn2ILi2EEv8AttnArgs
    .private_segment_fixed_size: 0
    .sgpr_count:     86
    .sgpr_spill_count: 0
    .symbol:         _Z7k_attn2ILi2EEv8AttnArgs.kd
    .uniform_work_group_size: 1
    .uses_dynamic_stack: false
    .vgpr_count:     228
    .vgpr_spill_count: 0
    .wavefront_size: 64
